# drop compiler vmcnt(0) in first trips; split packed f32 VALU ops in GEMM epilogues into scalar pairs
# baseline (speedup 1.0000x reference)
; #define PG8_TRIP_HEAD(T) const int t = (T); const bool last = (t == nt - 2); \
;             const char* a1 = cA + (size_t)(t + 1) * kstep; \
;             const char* a2 = last ? nA : cA + (size_t)(t + 2) * kstep; const char* b2 = last ? nB : cB + (size_t)(t + 2) * kstep; \
;             const char* a3 = a2 + kstep; const char* b3 = b2 + kstep; \
;             if (last && has_next) S.a_ready(nxt);
; template <class Epi, class Sched, bool ALIGN_EPI = false, bool SP2 = false>
; __device__ __forceinline__ void gemm_phase(PG8_LAS unsigned char* lds, const Gemm g, const Sched& S, const Epi& E) {
;     ...
;             { PG8_TRIP_HEAD(0) PG8_TRIP_SP2(asm volatile("s_waitcnt vmcnt(%0)" :: "n"(8 + Epi::NST) : "memory"), PG8_MMAZ) }
.LBB0_129:
	s_ashr_i32 s23, s22, 31
	s_lshl_b64 s[4:5], s[22:23], 20
	s_add_u32 s26, s34, s4
	s_addc_u32 s27, s35, s5
	s_add_i32 s45, 0, 0x10000
	s_add_i32 s47, 0, 0x14000
	v_add_u32_e32 v140, s45, v160
	v_add_u32_e32 v141, s47, v160
	ds_read_b128 v[4:7], v140
	ds_read_b128 v[8:11], v140 offset:1024
	ds_read_b128 v[12:15], v140 offset:2048
	ds_read_b128 v[16:19], v140 offset:3072
	ds_read_b128 v[20:23], v141
	ds_read_b128 v[24:27], v141 offset:1024
	ds_read_b128 v[28:31], v141 offset:2048
	ds_read_b128 v[32:35], v141 offset:3072
	s_and_b64 s[4:5], s[10:11], exec
	s_cselect_b32 s4, s27, s29
	s_cselect_b32 s5, s26, s28
	v_lshl_add_u64 v[184:185], s[30:31], 0, v[134:135]
	s_mov_b64 s[10:11], 0x84080
	s_add_i32 s23, s37, 0xc000
	v_lshl_add_u64 v[68:69], v[184:185], 0, s[10:11]
	s_mov_b32 m0, s23
	s_mov_b64 s[10:11], 0xc6080
	s_add_i32 s33, s37, 0xe000
	ds_read_b128 v[36:39], v163
	ds_read_b128 v[40:43], v163 offset:1024
	ds_read_b128 v[44:47], v163 offset:2048
	ds_read_b128 v[48:51], v163 offset:3072
	ds_read_b128 v[52:55], v163 offset:4096
	ds_read_b128 v[56:59], v163 offset:5120
	ds_read_b128 v[60:63], v163 offset:6144
	ds_read_b128 v[64:67], v163 offset:7168
	global_load_lds_dwordx4 v[68:69], off
	v_lshl_add_u64 v[68:69], v[184:185], 0, s[10:11]
	s_mov_b32 m0, s33
	s_nop 0
	global_load_lds_dwordx4 v[68:69], off
	s_waitcnt vmcnt(16)
	s_waitcnt lgkmcnt(0)
	s_barrier
	s_setprio 1
	s_waitcnt lgkmcnt(0)
	v_mfma_f32_16x16x32_bf16 v[88:91], v[12:15], v[52:55], 0
	v_mfma_f32_16x16x32_bf16 v[92:95], v[16:19], v[56:59], v[88:91]
	v_mfma_f32_16x16x32_bf16 v[88:91], v[4:7], v[60:63], 0
	v_mfma_f32_16x16x32_bf16 v[68:71], v[4:7], v[36:39], 0
	v_mfma_f32_16x16x32_bf16 v[72:75], v[12:15], v[36:39], 0
	v_mfma_f32_16x16x32_bf16 v[76:79], v[4:7], v[44:47], 0
	v_mfma_f32_16x16x32_bf16 v[80:83], v[12:15], v[44:47], 0
	v_mfma_f32_16x16x32_bf16 v[84:87], v[4:7], v[52:55], 0
	v_mfma_f32_16x16x32_bf16 v[96:99], v[8:11], v[64:67], v[88:91]
	v_mfma_f32_16x16x32_bf16 v[88:91], v[12:15], v[60:63], 0
	v_mfma_f32_16x16x32_bf16 v[68:71], v[8:11], v[40:43], v[68:71]
	v_mfma_f32_16x16x32_bf16 v[72:75], v[16:19], v[40:43], v[72:75]
	v_mfma_f32_16x16x32_bf16 v[76:79], v[8:11], v[48:51], v[76:79]
	v_mfma_f32_16x16x32_bf16 v[80:83], v[16:19], v[48:51], v[80:83]
	v_mfma_f32_16x16x32_bf16 v[84:87], v[8:11], v[56:59], v[84:87]
	v_mfma_f32_16x16x32_bf16 v[108:111], v[16:19], v[64:67], v[88:91]
	s_setprio 0
	s_setprio 1
	v_mfma_f32_16x16x32_bf16 v[88:91], v[20:23], v[36:39], 0
	v_mfma_f32_16x16x32_bf16 v[36:39], v[28:31], v[36:39], 0
	v_mfma_f32_16x16x32_bf16 v[112:115], v[24:27], v[40:43], v[88:91]
	v_mfma_f32_16x16x32_bf16 v[36:39], v[32:35], v[40:43], v[36:39]
	v_mfma_f32_16x16x32_bf16 v[40:43], v[20:23], v[44:47], 0
	v_mfma_f32_16x16x32_bf16 v[44:47], v[28:31], v[44:47], 0
	v_mfma_f32_16x16x32_bf16 v[40:43], v[24:27], v[48:51], v[40:43]
	v_mfma_f32_16x16x32_bf16 v[44:47], v[32:35], v[48:51], v[44:47]
	v_mfma_f32_16x16x32_bf16 v[48:51], v[20:23], v[52:55], 0
	v_mfma_f32_16x16x32_bf16 v[52:55], v[28:31], v[52:55], 0
	v_mfma_f32_16x16x32_bf16 v[48:51], v[24:27], v[56:59], v[48:51]
	v_mfma_f32_16x16x32_bf16 v[52:55], v[32:35], v[56:59], v[52:55]
	v_mfma_f32_16x16x32_bf16 v[56:59], v[20:23], v[60:63], 0
	v_mfma_f32_16x16x32_bf16 v[60:63], v[28:31], v[60:63], 0
	v_mfma_f32_16x16x32_bf16 v[56:59], v[24:27], v[64:67], v[56:59]
	v_mfma_f32_16x16x32_bf16 v[60:63], v[32:35], v[64:67], v[60:63]
	s_setprio 0
	s_barrier
	v_lshl_add_u64 v[186:187], s[28:29], 0, v[132:133]
	s_mov_b64 s[10:11], 0x100
	s_add_i32 s45, s45, s36
	v_lshl_add_u64 v[142:143], v[186:187], 0, s[10:11]
	s_mov_b32 m0, s45
	s_mov_b64 s[48:49], 0x40100
	s_add_i32 s46, s45, 0x2000
	ds_read_b128 v[64:67], v163 offset:16384
	ds_read_b128 v[88:91], v163 offset:17408
	ds_read_b128 v[100:103], v163 offset:18432
	ds_read_b128 v[104:107], v163 offset:19456
	ds_read_b128 v[116:119], v163 offset:20480
	ds_read_b128 v[120:123], v163 offset:21504
	ds_read_b128 v[124:127], v163 offset:22528
	ds_read_b128 v[128:131], v163 offset:23552
	global_load_lds_dwordx4 v[142:143], off
	v_lshl_add_u64 v[142:143], v[186:187], 0, s[48:49]
	s_mov_b32 m0, s46
	s_mov_b64 s[48:49], 0x80100
	s_add_i32 s47, s47, s36
	global_load_lds_dwordx4 v[142:143], off
	v_lshl_add_u64 v[142:143], v[186:187], 0, s[48:49]
	s_mov_b32 m0, s47
	s_mov_b64 s[48:49], 0xc0100
	global_load_lds_dwordx4 v[142:143], off
	v_lshl_add_u64 v[142:143], v[186:187], 0, s[48:49]
	s_add_i32 s48, s47, 0x2000
	s_mov_b32 m0, s48
	s_nop 0
	global_load_lds_dwordx4 v[142:143], off
	v_lshl_add_u64 v[142:143], v[184:185], 0, s[10:11]
	s_mov_b32 m0, s37
	s_mov_b64 s[10:11], 0x42100
	global_load_lds_dwordx4 v[142:143], off
	v_lshl_add_u64 v[142:143], v[184:185], 0, s[10:11]
	s_mov_b32 m0, s38
	s_nop 0
	global_load_lds_dwordx4 v[142:143], off
	s_waitcnt vmcnt(16)
	s_waitcnt lgkmcnt(0)
	s_barrier
	s_setprio 1
	s_waitcnt lgkmcnt(0)
	v_mfma_f32_16x16x32_bf16 v[142:145], v[4:7], v[64:67], 0
	v_mfma_f32_16x16x32_bf16 v[152:155], v[4:7], v[100:103], 0
	v_mfma_f32_16x16x32_bf16 v[164:167], v[4:7], v[116:119], 0
	v_mfma_f32_16x16x32_bf16 v[4:7], v[4:7], v[124:127], 0
	v_mfma_f32_16x16x32_bf16 v[144:147], v[8:11], v[88:91], v[142:145]
	v_mfma_f32_16x16x32_bf16 v[152:155], v[8:11], v[104:107], v[152:155]
	v_mfma_f32_16x16x32_bf16 v[164:167], v[8:11], v[120:123], v[164:167]
	v_mfma_f32_16x16x32_bf16 v[4:7], v[8:11], v[128:131], v[4:7]
	v_mfma_f32_16x16x32_bf16 v[8:11], v[12:15], v[124:127], 0
	v_mfma_f32_16x16x32_bf16 v[148:151], v[12:15], v[64:67], 0
	v_mfma_f32_16x16x32_bf16 v[156:159], v[12:15], v[100:103], 0
	v_mfma_f32_16x16x32_bf16 v[168:171], v[12:15], v[116:119], 0
	v_mfma_f32_16x16x32_bf16 v[12:15], v[16:19], v[128:131], v[8:11]
	v_mfma_f32_16x16x32_bf16 v[148:151], v[16:19], v[88:91], v[148:151]
	v_mfma_f32_16x16x32_bf16 v[156:159], v[16:19], v[104:107], v[156:159]
	v_mfma_f32_16x16x32_bf16 v[168:171], v[16:19], v[120:123], v[168:171]
	s_setprio 0
	s_setprio 1
	v_mfma_f32_16x16x32_bf16 v[8:11], v[20:23], v[64:67], 0
	v_mfma_f32_16x16x32_bf16 v[16:19], v[24:27], v[88:91], v[8:11]
	v_mfma_f32_16x16x32_bf16 v[8:11], v[28:31], v[64:67], 0
	v_mfma_f32_16x16x32_bf16 v[172:175], v[32:35], v[88:91], v[8:11]
	v_mfma_f32_16x16x32_bf16 v[8:11], v[20:23], v[100:103], 0
	v_mfma_f32_16x16x32_bf16 v[176:179], v[24:27], v[104:107], v[8:11]
	v_mfma_f32_16x16x32_bf16 v[8:11], v[28:31], v[100:103], 0
	v_mfma_f32_16x16x32_bf16 v[194:197], v[32:35], v[104:107], v[8:11]
	v_mfma_f32_16x16x32_bf16 v[8:11], v[20:23], v[116:119], 0
	v_mfma_f32_16x16x32_bf16 v[198:201], v[24:27], v[120:123], v[8:11]
	v_mfma_f32_16x16x32_bf16 v[8:11], v[28:31], v[116:119], 0
	v_mfma_f32_16x16x32_bf16 v[202:205], v[32:35], v[120:123], v[8:11]
	v_mfma_f32_16x16x32_bf16 v[8:11], v[20:23], v[124:127], 0
	v_mfma_f32_16x16x32_bf16 v[206:209], v[24:27], v[128:131], v[8:11]
	v_mfma_f32_16x16x32_bf16 v[8:11], v[28:31], v[124:127], 0
	v_mfma_f32_16x16x32_bf16 v[220:223], v[32:35], v[128:131], v[8:11]
	s_setprio 0
	s_barrier
	s_add_i32 s49, 0, 0x18000
	s_add_i32 s51, 0, 0x1c000
	v_add_u32_e32 v142, s49, v160
	v_add_u32_e32 v143, s51, v160
	s_nop 0
	ds_read_b128 v[8:11], v142
	ds_read_b128 v[28:31], v142 offset:1024
	ds_read_b128 v[32:35], v142 offset:2048
	ds_read_b128 v[64:67], v142 offset:3072
	ds_read_b128 v[224:227], v143
	ds_read_b128 v[228:231], v143 offset:1024
	ds_read_b128 v[232:235], v143 offset:2048
	ds_read_b128 v[236:239], v143 offset:3072
	s_mov_b64 s[10:11], 0x84100
	s_mov_b32 m0, s39
	v_lshl_add_u64 v[88:89], v[184:185], 0, s[10:11]
	s_mov_b64 s[10:11], 0xc6100
	ds_read_b128 v[20:23], v163 offset:32768
	ds_read_b128 v[24:27], v163 offset:33792
	ds_read_b128 v[240:243], v163 offset:34816
	ds_read_b128 v[244:247], v163 offset:35840
	ds_read_b128 v[248:251], v163 offset:36864
	ds_read_b128 v[216:219], v163 offset:37888
	ds_read_b128 v[190:193], v163 offset:38912
	ds_read_b128 v[180:183], v163 offset:39936
	global_load_lds_dwordx4 v[88:89], off
	v_lshl_add_u64 v[88:89], v[184:185], 0, s[10:11]
	s_mov_b32 m0, s40
	s_nop 0
	global_load_lds_dwordx4 v[88:89], off
	s_waitcnt vmcnt(8)
	s_waitcnt lgkmcnt(0)
	s_barrier
	s_setprio 1
	s_waitcnt lgkmcnt(0)
	v_mfma_f32_16x16x32_bf16 v[68:71], v[8:11], v[20:23], v[68:71]
	v_mfma_f32_16x16x32_bf16 v[120:123], v[28:31], v[24:27], v[68:71]
	v_mfma_f32_16x16x32_bf16 v[68:71], v[32:35], v[20:23], v[72:75]
	v_mfma_f32_16x16x32_bf16 v[116:119], v[64:67], v[24:27], v[68:71]
	v_mfma_f32_16x16x32_bf16 v[68:71], v[8:11], v[240:243], v[76:79]
	v_mfma_f32_16x16x32_bf16 v[104:107], v[28:31], v[244:247], v[68:71]
	v_mfma_f32_16x16x32_bf16 v[68:71], v[32:35], v[240:243], v[80:83]
	v_mfma_f32_16x16x32_bf16 v[100:103], v[64:67], v[244:247], v[68:71]
	v_mfma_f32_16x16x32_bf16 v[68:71], v[8:11], v[248:251], v[84:87]
	v_mfma_f32_16x16x32_bf16 v[88:91], v[28:31], v[216:219], v[68:71]
	v_mfma_f32_16x16x32_bf16 v[68:71], v[32:35], v[248:251], v[92:95]
	v_mfma_f32_16x16x32_bf16 v[84:87], v[64:67], v[216:219], v[68:71]
	v_mfma_f32_16x16x32_bf16 v[68:71], v[8:11], v[190:193], v[96:99]
	v_mfma_f32_16x16x32_bf16 v[72:75], v[28:31], v[180:183], v[68:71]
	v_mfma_f32_16x16x32_bf16 v[68:71], v[32:35], v[190:193], v[108:111]
	v_mfma_f32_16x16x32_bf16 v[68:71], v[64:67], v[180:183], v[68:71]
	s_setprio 0
	s_setprio 1
	v_mfma_f32_16x16x32_bf16 v[76:79], v[224:227], v[20:23], v[112:115]
	v_mfma_f32_16x16x32_bf16 v[20:23], v[232:235], v[20:23], v[36:39]
	v_mfma_f32_16x16x32_bf16 v[124:127], v[236:239], v[24:27], v[20:23]
	v_mfma_f32_16x16x32_bf16 v[20:23], v[224:227], v[240:243], v[40:43]
	v_mfma_f32_16x16x32_bf16 v[112:115], v[228:231], v[244:247], v[20:23]
	v_mfma_f32_16x16x32_bf16 v[20:23], v[232:235], v[240:243], v[44:47]
	v_mfma_f32_16x16x32_bf16 v[108:111], v[236:239], v[244:247], v[20:23]
	v_mfma_f32_16x16x32_bf16 v[20:23], v[224:227], v[248:251], v[48:51]
	v_mfma_f32_16x16x32_bf16 v[96:99], v[228:231], v[216:219], v[20:23]
	v_mfma_f32_16x16x32_bf16 v[20:23], v[232:235], v[248:251], v[52:55]
	v_mfma_f32_16x16x32_bf16 v[92:95], v[236:239], v[216:219], v[20:23]
	v_mfma_f32_16x16x32_bf16 v[20:23], v[224:227], v[190:193], v[56:59]
	v_mfma_f32_16x16x32_bf16 v[80:83], v[228:231], v[180:183], v[20:23]
	v_mfma_f32_16x16x32_bf16 v[20:23], v[232:235], v[190:193], v[60:63]
	v_mfma_f32_16x16x32_bf16 v[128:131], v[228:231], v[24:27], v[76:79]
	v_mfma_f32_16x16x32_bf16 v[76:79], v[236:239], v[180:183], v[20:23]
	s_setprio 0
	s_barrier
; #define PG8_MMA(ai, bj, At, Bt) do { __builtin_amdgcn_s_setprio(1); _Pragma("unroll") for (int m = 0; m < 4; ++m) _Pragma("unroll") for (int n = 0; n < 2; ++n) _Pragma("unroll") for (int k = 0; k < 2; ++k) \
;         acc[ai][bj][m][n] = __builtin_amdgcn_mfma_f32_16x16x32_bf16(Bt[n][k], At[m][k], acc[ai][bj][m][n], 0, 0, 0); __builtin_amdgcn_s_setprio(0); } while (0)
; #define PG8_WAIT_V(n) asm volatile("s_waitcnt vmcnt(" #n ")" ::: "memory")
; #define PG8_TRIP_HEAD(T) const int t = (T); const bool last = (t == nt - 2); \
;             const char* a1 = cA + (size_t)(t + 1) * kstep; \
;             const char* a2 = last ? nA : cA + (size_t)(t + 2) * kstep; const char* b2 = last ? nB : cB + (size_t)(t + 2) * kstep; \
;             const char* a3 = a2 + kstep; const char* b3 = b2 + kstep; \
;             if (last && has_next) S.a_ready(nxt);
; template <class Epi, class Sched, bool ALIGN_EPI = false, bool SP2 = false>
; __device__ __forceinline__ void gemm_phase(PG8_LAS unsigned char* lds, const Gemm g, const Sched& S, const Epi& E) {
;     ...
;         if constexpr (SP2) {
;             { PG8_TRIP_HEAD(0) PG8_TRIP_SP2(asm volatile("s_waitcnt vmcnt(%0)" :: "n"(8 + Epi::NST) : "memory"), PG8_MMAZ) }
;             for (int tt = 2; tt < nt; tt += 2) { PG8_TRIP_HEAD(tt) PG8_TRIP_SP2(PG8_WAIT_V(8), PG8_MMA) }
	s_mov_b64 s[10:11], 0x180
	s_add_i32 s49, s49, s36
	s_nop 1
	v_lshl_add_u64 v[20:21], v[186:187], 0, s[10:11]
	s_mov_b32 m0, s49
	s_mov_b64 s[52:53], 0x40180
	s_add_i32 s50, s49, 0x2000
	ds_read_b128 v[44:47], v163 offset:49152
	ds_read_b128 v[48:51], v163 offset:50176
	ds_read_b128 v[180:183], v163 offset:51200
	ds_read_b128 v[190:193], v163 offset:52224
	ds_read_b128 v[216:219], v163 offset:53248
	ds_read_b128 v[240:243], v163 offset:54272
	ds_read_b128 v[244:247], v163 offset:55296
	ds_read_b128 v[248:251], v163 offset:56320
	global_load_lds_dwordx4 v[20:21], off
	v_lshl_add_u64 v[20:21], v[186:187], 0, s[52:53]
	s_mov_b32 m0, s50
	s_mov_b64 s[52:53], 0x80180
	s_add_i32 s51, s51, s36
	global_load_lds_dwordx4 v[20:21], off
	v_lshl_add_u64 v[20:21], v[186:187], 0, s[52:53]
	s_mov_b32 m0, s51
	s_mov_b64 s[52:53], 0xc0180
	global_load_lds_dwordx4 v[20:21], off
	v_lshl_add_u64 v[20:21], v[186:187], 0, s[52:53]
	s_add_i32 s52, s51, 0x2000
	s_mov_b32 m0, s52
	s_nop 0
	global_load_lds_dwordx4 v[20:21], off
	v_lshl_add_u64 v[20:21], v[184:185], 0, s[10:11]
	s_mov_b32 m0, s0
	s_mov_b64 s[10:11], 0x42180
	global_load_lds_dwordx4 v[20:21], off
	v_lshl_add_u64 v[20:21], v[184:185], 0, s[10:11]
	s_mov_b32 m0, s41
	s_nop 0
	global_load_lds_dwordx4 v[20:21], off
	s_waitcnt vmcnt(8)
	s_waitcnt lgkmcnt(0)
	s_barrier
	s_setprio 1
	s_waitcnt lgkmcnt(0)
	v_mfma_f32_16x16x32_bf16 v[20:23], v[8:11], v[44:47], v[144:147]
	v_mfma_f32_16x16x32_bf16 v[56:59], v[28:31], v[48:51], v[20:23]
	v_mfma_f32_16x16x32_bf16 v[20:23], v[32:35], v[44:47], v[148:151]
	v_mfma_f32_16x16x32_bf16 v[52:55], v[64:67], v[48:51], v[20:23]
	v_mfma_f32_16x16x32_bf16 v[20:23], v[8:11], v[180:183], v[152:155]
	v_mfma_f32_16x16x32_bf16 v[40:43], v[28:31], v[190:193], v[20:23]
	v_mfma_f32_16x16x32_bf16 v[20:23], v[32:35], v[180:183], v[156:159]
	v_mfma_f32_16x16x32_bf16 v[36:39], v[64:67], v[190:193], v[20:23]
	v_mfma_f32_16x16x32_bf16 v[20:23], v[8:11], v[216:219], v[164:167]
	v_mfma_f32_16x16x32_bf16 v[4:7], v[8:11], v[244:247], v[4:7]
	v_mfma_f32_16x16x32_bf16 v[24:27], v[28:31], v[240:243], v[20:23]
	v_mfma_f32_16x16x32_bf16 v[20:23], v[32:35], v[216:219], v[168:171]
	v_mfma_f32_16x16x32_bf16 v[8:11], v[28:31], v[248:251], v[4:7]
	v_mfma_f32_16x16x32_bf16 v[4:7], v[32:35], v[244:247], v[12:15]
	v_mfma_f32_16x16x32_bf16 v[20:23], v[64:67], v[240:243], v[20:23]
	v_mfma_f32_16x16x32_bf16 v[4:7], v[64:67], v[248:251], v[4:7]
	s_setprio 0
	s_setprio 1
	v_mfma_f32_16x16x32_bf16 v[12:15], v[224:227], v[44:47], v[16:19]
	v_mfma_f32_16x16x32_bf16 v[64:67], v[228:231], v[48:51], v[12:15]
	v_mfma_f32_16x16x32_bf16 v[12:15], v[232:235], v[44:47], v[172:175]
	v_mfma_f32_16x16x32_bf16 v[60:63], v[236:239], v[48:51], v[12:15]
	v_mfma_f32_16x16x32_bf16 v[12:15], v[224:227], v[180:183], v[176:179]
	v_mfma_f32_16x16x32_bf16 v[48:51], v[228:231], v[190:193], v[12:15]
	v_mfma_f32_16x16x32_bf16 v[12:15], v[232:235], v[180:183], v[194:197]
	v_mfma_f32_16x16x32_bf16 v[44:47], v[236:239], v[190:193], v[12:15]
	v_mfma_f32_16x16x32_bf16 v[12:15], v[224:227], v[216:219], v[198:201]
	v_mfma_f32_16x16x32_bf16 v[32:35], v[228:231], v[240:243], v[12:15]
	v_mfma_f32_16x16x32_bf16 v[12:15], v[232:235], v[216:219], v[202:205]
	v_mfma_f32_16x16x32_bf16 v[28:31], v[236:239], v[240:243], v[12:15]
	v_mfma_f32_16x16x32_bf16 v[12:15], v[224:227], v[244:247], v[206:209]
	v_mfma_f32_16x16x32_bf16 v[16:19], v[228:231], v[248:251], v[12:15]
	v_mfma_f32_16x16x32_bf16 v[12:15], v[232:235], v[244:247], v[220:223]
	v_mfma_f32_16x16x32_bf16 v[12:15], v[236:239], v[248:251], v[12:15]
	s_setprio 0
	s_barrier
	s_add_u32 s10, s30, 0x84180
	s_addc_u32 s11, s31, 0
	s_add_u32 s28, s28, 0x200
	s_addc_u32 s29, s29, 0
	s_mov_b32 s30, 0
	s_mov_b64 s[60:61], 0x80000
	s_mov_b64 s[62:63], 0x80080
	s_mov_b64 s[64:65], 0xc0000
	s_mov_b64 s[66:67], 0xc0080
	s_mov_b64 s[68:69], 0xc6000

; __device__ __forceinline__ unsigned cvt_pk_bf16(float lo, float hi) { f32x2_c v = {lo, hi}; bf16x2_c b = __builtin_convertvector(v, bf16x2_c); return __builtin_bit_cast(unsigned, b); }
; __device__ __forceinline__ float silu_f(float g) { return g * __builtin_amdgcn_rcpf(1.0f + __builtin_amdgcn_exp2f(-1.44269504f * g)); }
;     __device__ __forceinline__ void operator()(const f32x4 (&acc)[2][2][4][2], const Unit& u, int wr, int wc, int fr, int fq) const {
;     ...
;             for (int m = 0; m < 4; ++m) { bf16_t* rowp = O + (size_t)(row0 + ai * HALF + m * 16) * ldc + col0;
;                 const float rs = my[(ai * 4 + m) * 16];
;                 const f32x4 a0 = acc[ai][0][m][0] * rs, a1 = acc[ai][0][m][1] * rs, g0 = acc[ai][1][m][0] * rs, g1 = acc[ai][1][m][1] * rs;
;                 u32x4 w; w.x = cvt_pk_bf16(a0[0] * silu_f(g0[0]), a0[1] * silu_f(g0[1])); w.y = cvt_pk_bf16(a0[2] * silu_f(g0[2]), a0[3] * silu_f(g0[3]));
;                 w.z = cvt_pk_bf16(a1[0] * silu_f(g1[0]), a1[1] * silu_f(g1[1])); w.w = cvt_pk_bf16(a1[2] * silu_f(g1[2]), a1[3] * silu_f(g1[3]));
;                 *(u32x4*)rowp = w; }
.LBB0_153:
	s_waitcnt lgkmcnt(0)
	v_mov_b64_e32 v[142:143], s[94:95]
	s_movk_i32 s4, 0x2c00
	v_lshl_or_b32 v158, s2, 7, v162
	v_mad_u64_u32 v[164:165], s[2:3], v144, s4, v[142:143]
	v_mov_b32_e32 v144, v165
	v_ashrrev_i32_e32 v159, 31, v158
	v_mad_u64_u32 v[144:145], s[2:3], v145, s4, v[144:145]
	v_mov_b32_e32 v165, v144
	v_lshlrev_b64 v[144:145], 1, v[158:159]
	v_lshl_add_u64 v[158:159], v[164:165], 0, v[144:145]
	ds_read2_b32 v[164:165], v161 offset1:16
	s_and_b64 vcc, exec, s[8:9]
	s_waitcnt lgkmcnt(0)
	v_mul_f32_e64 v166, v118, v164
	v_mul_f32_e64 v167, v119, v164
	v_mul_f32_e64 v118, v116, v164
	v_mul_f32_e64 v119, v117, v164
	v_mul_f32_e64 v116, v128, v164
	v_mul_f32_e64 v117, v129, v164
	v_mul_f32_e64 v120, v120, v164
	v_mul_f32_e64 v121, v121, v164
	v_mul_f32_e32 v128, 0xbfb8aa3b, v116
	v_mul_f32_e32 v129, 0xbfb8aa3b, v117
	v_exp_f32_e32 v128, v128
	v_exp_f32_e32 v129, v129
	v_mul_f32_e64 v130, v130, v164
	v_mul_f32_e64 v131, v131, v164
	v_mul_f32_e64 v122, v122, v164
	v_mul_f32_e64 v123, v123, v164
	v_add_f32_e32 v128, 1.0, v128
	v_add_f32_e32 v129, 1.0, v129
	v_rcp_f32_e32 v128, v128
	v_rcp_f32_e32 v129, v129
	v_mul_f32_e64 v124, v124, v164
	v_mul_f32_e64 v125, v125, v164
	v_mul_f32_e64 v126, v126, v164
	v_mul_f32_e64 v127, v127, v164
	v_mul_f32_e64 v116, v116, v128
	v_mul_f32_e64 v117, v117, v129
	s_nop 0
	v_mul_f32_e64 v116, v120, v116
	v_mul_f32_e64 v117, v121, v117
	s_nop 0
	v_cvt_pk_bf16_f32 v116, v116, v117
	v_mul_f32_e32 v117, 0xbfb8aa3b, v130
	v_exp_f32_e32 v117, v117
	s_nop 0
	v_add_f32_e32 v117, 1.0, v117
	v_rcp_f32_e32 v120, v117
	v_mul_f32_e32 v117, 0xbfb8aa3b, v131
	v_exp_f32_e32 v117, v117
	s_nop 0
	v_add_f32_e32 v117, 1.0, v117
	v_rcp_f32_e32 v121, v117
	s_nop 0
	v_mul_f32_e64 v120, v130, v120
	v_mul_f32_e64 v121, v131, v121
	s_nop 0
	v_mul_f32_e64 v120, v122, v120
	v_mul_f32_e64 v121, v123, v121
	s_nop 0
	v_cvt_pk_bf16_f32 v117, v120, v121
	v_mul_f32_e32 v120, 0xbfb8aa3b, v124
	v_mul_f32_e32 v121, 0xbfb8aa3b, v125
	v_exp_f32_e32 v120, v120
	v_exp_f32_e32 v121, v121
	v_add_f32_e32 v120, 1.0, v120
	v_add_f32_e32 v121, 1.0, v121
	v_rcp_f32_e32 v120, v120
	v_rcp_f32_e32 v121, v121
	s_nop 0
	v_mul_f32_e64 v120, v124, v120
	v_mul_f32_e64 v121, v125, v121
	s_nop 0
	v_mul_f32_e64 v118, v118, v120
	v_mul_f32_e64 v119, v119, v121
	s_nop 0
	v_cvt_pk_bf16_f32 v118, v118, v119
	v_mul_f32_e32 v119, 0xbfb8aa3b, v126
	v_exp_f32_e32 v119, v119
	s_nop 0
	v_add_f32_e32 v119, 1.0, v119
	v_rcp_f32_e32 v120, v119
	v_mul_f32_e32 v119, 0xbfb8aa3b, v127
	v_exp_f32_e32 v119, v119
	s_nop 0
	v_add_f32_e32 v119, 1.0, v119
	v_rcp_f32_e32 v121, v119
	s_nop 0
	v_mul_f32_e64 v120, v126, v120
	v_mul_f32_e64 v121, v127, v121
	s_nop 0
	v_mul_f32_e64 v120, v166, v120
	v_mul_f32_e64 v121, v167, v121
	s_nop 0
	v_cvt_pk_bf16_f32 v119, v120, v121
	global_store_dwordx4 v[158:159], v[116:119], off
	s_nop 1
	v_mad_u64_u32 v[116:117], s[2:3], v156, s4, v[142:143]
	v_mov_b32_e32 v118, v117
	v_mad_u64_u32 v[118:119], s[2:3], v157, s4, v[118:119]
	v_mov_b32_e32 v117, v118
	v_mov_b32_e32 v118, v165
	v_mul_f32_e64 v120, v102, v118
	v_mul_f32_e64 v121, v103, v118
	v_mul_f32_e64 v102, v100, v118
	v_mul_f32_e64 v103, v101, v118
	v_mul_f32_e64 v100, v112, v118
	v_mul_f32_e64 v101, v113, v118
	v_mul_f32_e64 v104, v104, v118
	v_mul_f32_e64 v105, v105, v118
	v_mul_f32_e32 v112, 0xbfb8aa3b, v100
	v_mul_f32_e32 v113, 0xbfb8aa3b, v101
	v_exp_f32_e32 v112, v112
	v_exp_f32_e32 v113, v113
	v_mul_f32_e64 v114, v114, v118
	v_mul_f32_e64 v115, v115, v118
	v_mul_f32_e64 v106, v106, v118
	v_mul_f32_e64 v107, v107, v118
	v_add_f32_e32 v112, 1.0, v112
	v_add_f32_e32 v113, 1.0, v113
	v_rcp_f32_e32 v112, v112
	v_rcp_f32_e32 v113, v113
	v_mul_f32_e64 v108, v108, v118
	v_mul_f32_e64 v109, v109, v118
	v_mul_f32_e64 v110, v110, v118
	v_mul_f32_e64 v111, v111, v118
	v_lshl_add_u64 v[116:117], v[116:117], 0, v[144:145]
	v_mul_f32_e64 v100, v100, v112
	v_mul_f32_e64 v101, v101, v113
	s_nop 0
	v_mul_f32_e64 v100, v104, v100
	v_mul_f32_e64 v101, v105, v101
	s_nop 0
	v_cvt_pk_bf16_f32 v100, v100, v101
	v_mul_f32_e32 v101, 0xbfb8aa3b, v114
	v_exp_f32_e32 v101, v101
	s_nop 0
	v_add_f32_e32 v101, 1.0, v101
	v_rcp_f32_e32 v104, v101
	v_mul_f32_e32 v101, 0xbfb8aa3b, v115
	v_exp_f32_e32 v101, v101
	s_nop 0
	v_add_f32_e32 v101, 1.0, v101
	v_rcp_f32_e32 v105, v101
	s_nop 0
	v_mul_f32_e64 v104, v114, v104
	v_mul_f32_e64 v105, v115, v105
	s_nop 0
	v_mul_f32_e64 v104, v106, v104
	v_mul_f32_e64 v105, v107, v105
	s_nop 0
	v_cvt_pk_bf16_f32 v101, v104, v105
	v_mul_f32_e32 v104, 0xbfb8aa3b, v108
	v_mul_f32_e32 v105, 0xbfb8aa3b, v109
	v_exp_f32_e32 v104, v104
	v_exp_f32_e32 v105, v105
	v_add_f32_e32 v104, 1.0, v104
	v_add_f32_e32 v105, 1.0, v105
	v_rcp_f32_e32 v104, v104
	v_rcp_f32_e32 v105, v105
	s_nop 0
	v_mul_f32_e64 v104, v108, v104
	v_mul_f32_e64 v105, v109, v105
	s_nop 0
	v_mul_f32_e64 v102, v102, v104
	v_mul_f32_e64 v103, v103, v105
	s_nop 0
	v_cvt_pk_bf16_f32 v102, v102, v103
	v_mul_f32_e32 v103, 0xbfb8aa3b, v110
	v_exp_f32_e32 v103, v103
	s_nop 0
	v_add_f32_e32 v103, 1.0, v103
	v_rcp_f32_e32 v104, v103
	v_mul_f32_e32 v103, 0xbfb8aa3b, v111
	v_exp_f32_e32 v103, v103
	s_nop 0
	v_add_f32_e32 v103, 1.0, v103
	v_rcp_f32_e32 v105, v103
	s_nop 0
	v_mul_f32_e64 v104, v110, v104
	v_mul_f32_e64 v105, v111, v105
	s_nop 0
	v_mul_f32_e64 v104, v120, v104
	v_mul_f32_e64 v105, v121, v105
	s_nop 0
	v_cvt_pk_bf16_f32 v103, v104, v105
	global_store_dwordx4 v[116:117], v[100:103], off
	s_nop 1
	v_mad_u64_u32 v[100:101], s[2:3], v154, s4, v[142:143]
	v_mov_b32_e32 v102, v101
	v_mad_u64_u32 v[102:103], s[2:3], v155, s4, v[102:103]
	v_mov_b32_e32 v101, v102
	ds_read2_b32 v[102:103], v161 offset0:32 offset1:48
	v_lshl_add_u64 v[100:101], v[100:101], 0, v[144:145]
	s_waitcnt lgkmcnt(0)
; __device__ __forceinline__ unsigned cvt_pk_bf16(float lo, float hi) { f32x2_c v = {lo, hi}; bf16x2_c b = __builtin_convertvector(v, bf16x2_c); return __builtin_bit_cast(unsigned, b); }
; __device__ __forceinline__ float silu_f(float g) { return g * __builtin_amdgcn_rcpf(1.0f + __builtin_amdgcn_exp2f(-1.44269504f * g)); }
;     __device__ __forceinline__ void operator()(const f32x4 (&acc)[2][2][4][2], const Unit& u, int wr, int wc, int fr, int fq) const {
;     ...
;             for (int m = 0; m < 4; ++m) { bf16_t* rowp = O + (size_t)(row0 + ai * HALF + m * 16) * ldc + col0;
;                 const float rs = my[(ai * 4 + m) * 16];
;                 const f32x4 a0 = acc[ai][0][m][0] * rs, a1 = acc[ai][0][m][1] * rs, g0 = acc[ai][1][m][0] * rs, g1 = acc[ai][1][m][1] * rs;
;                 u32x4 w; w.x = cvt_pk_bf16(a0[0] * silu_f(g0[0]), a0[1] * silu_f(g0[1])); w.y = cvt_pk_bf16(a0[2] * silu_f(g0[2]), a0[3] * silu_f(g0[3]));
;                 w.z = cvt_pk_bf16(a1[0] * silu_f(g1[0]), a1[1] * silu_f(g1[1])); w.w = cvt_pk_bf16(a1[2] * silu_f(g1[2]), a1[3] * silu_f(g1[3]));
;                 *(u32x4*)rowp = w; }
	v_mul_f32_e64 v104, v86, v102
	v_mul_f32_e64 v105, v87, v102
	v_mul_f32_e64 v86, v84, v102
	v_mul_f32_e64 v87, v85, v102
	v_mul_f32_e64 v84, v96, v102
	v_mul_f32_e64 v85, v97, v102
	v_mul_f32_e64 v88, v88, v102
	v_mul_f32_e64 v89, v89, v102
	v_mul_f32_e32 v96, 0xbfb8aa3b, v84
	v_mul_f32_e32 v97, 0xbfb8aa3b, v85
	v_exp_f32_e32 v96, v96
	v_exp_f32_e32 v97, v97
	v_mul_f32_e64 v98, v98, v102
	v_mul_f32_e64 v99, v99, v102
	v_mul_f32_e64 v90, v90, v102
	v_mul_f32_e64 v91, v91, v102
	v_add_f32_e32 v96, 1.0, v96
	v_add_f32_e32 v97, 1.0, v97
	v_rcp_f32_e32 v96, v96
	v_rcp_f32_e32 v97, v97
	v_mul_f32_e64 v92, v92, v102
	v_mul_f32_e64 v93, v93, v102
	v_mul_f32_e64 v94, v94, v102
	v_mul_f32_e64 v95, v95, v102
	v_mul_f32_e64 v84, v84, v96
	v_mul_f32_e64 v85, v85, v97
	s_nop 0
	v_mul_f32_e64 v84, v88, v84
	v_mul_f32_e64 v85, v89, v85
	s_nop 0
	v_cvt_pk_bf16_f32 v84, v84, v85
	v_mul_f32_e32 v85, 0xbfb8aa3b, v98
	v_exp_f32_e32 v85, v85
	s_nop 0
	v_add_f32_e32 v85, 1.0, v85
	v_rcp_f32_e32 v88, v85
	v_mul_f32_e32 v85, 0xbfb8aa3b, v99
	v_exp_f32_e32 v85, v85
	s_nop 0
	v_add_f32_e32 v85, 1.0, v85
	v_rcp_f32_e32 v89, v85
	s_nop 0
	v_mul_f32_e64 v88, v98, v88
	v_mul_f32_e64 v89, v99, v89
	s_nop 0
	v_mul_f32_e64 v88, v90, v88
	v_mul_f32_e64 v89, v91, v89
	s_nop 0
	v_cvt_pk_bf16_f32 v85, v88, v89
	v_mul_f32_e32 v88, 0xbfb8aa3b, v92
	v_mul_f32_e32 v89, 0xbfb8aa3b, v93
	v_exp_f32_e32 v88, v88
	v_exp_f32_e32 v89, v89
	v_add_f32_e32 v88, 1.0, v88
	v_add_f32_e32 v89, 1.0, v89
	v_rcp_f32_e32 v88, v88
	v_rcp_f32_e32 v89, v89
	s_nop 0
	v_mul_f32_e64 v88, v92, v88
	v_mul_f32_e64 v89, v93, v89
	s_nop 0
	v_mul_f32_e64 v86, v86, v88
	v_mul_f32_e64 v87, v87, v89
	s_nop 0
	v_cvt_pk_bf16_f32 v86, v86, v87
	v_mul_f32_e32 v87, 0xbfb8aa3b, v94
	v_exp_f32_e32 v87, v87
	s_nop 0
	v_add_f32_e32 v87, 1.0, v87
	v_rcp_f32_e32 v88, v87
	v_mul_f32_e32 v87, 0xbfb8aa3b, v95
	v_exp_f32_e32 v87, v87
	s_nop 0
	v_add_f32_e32 v87, 1.0, v87
	v_rcp_f32_e32 v89, v87
	s_nop 0
	v_mul_f32_e64 v88, v94, v88
	v_mul_f32_e64 v89, v95, v89
	s_nop 0
	v_mul_f32_e64 v88, v104, v88
	v_mul_f32_e64 v89, v105, v89
	s_nop 0
	v_cvt_pk_bf16_f32 v87, v88, v89
	global_store_dwordx4 v[100:101], v[84:87], off
	s_nop 1
	v_mad_u64_u32 v[84:85], s[2:3], v152, s4, v[142:143]
	v_mov_b32_e32 v86, v85
	v_mad_u64_u32 v[86:87], s[2:3], v153, s4, v[86:87]
	v_mov_b32_e32 v85, v86
	v_mov_b32_e32 v86, v103
	v_mul_f32_e64 v88, v70, v86
	v_mul_f32_e64 v89, v71, v86
	v_mul_f32_e64 v70, v68, v86
	v_mul_f32_e64 v71, v69, v86
	v_mul_f32_e64 v68, v80, v86
	v_mul_f32_e64 v69, v81, v86
	v_mul_f32_e64 v72, v72, v86
	v_mul_f32_e64 v73, v73, v86
	v_mul_f32_e32 v80, 0xbfb8aa3b, v68
	v_mul_f32_e32 v81, 0xbfb8aa3b, v69
	v_exp_f32_e32 v80, v80
	v_exp_f32_e32 v81, v81
	v_mul_f32_e64 v82, v82, v86
	v_mul_f32_e64 v83, v83, v86
	v_mul_f32_e64 v74, v74, v86
	v_mul_f32_e64 v75, v75, v86
	v_add_f32_e32 v80, 1.0, v80
	v_add_f32_e32 v81, 1.0, v81
	v_rcp_f32_e32 v80, v80
	v_rcp_f32_e32 v81, v81
	v_mul_f32_e64 v76, v76, v86
	v_mul_f32_e64 v77, v77, v86
	v_mul_f32_e64 v78, v78, v86
	v_mul_f32_e64 v79, v79, v86
	v_lshl_add_u64 v[84:85], v[84:85], 0, v[144:145]
	v_mul_f32_e64 v68, v68, v80
	v_mul_f32_e64 v69, v69, v81
	s_nop 0
	v_mul_f32_e64 v68, v72, v68
	v_mul_f32_e64 v69, v73, v69
	s_nop 0
	v_cvt_pk_bf16_f32 v68, v68, v69
	v_mul_f32_e32 v69, 0xbfb8aa3b, v82
	v_exp_f32_e32 v69, v69
	s_nop 0
	v_add_f32_e32 v69, 1.0, v69
	v_rcp_f32_e32 v72, v69
	v_mul_f32_e32 v69, 0xbfb8aa3b, v83
	v_exp_f32_e32 v69, v69
	s_nop 0
	v_add_f32_e32 v69, 1.0, v69
	v_rcp_f32_e32 v73, v69
	s_nop 0
	v_mul_f32_e64 v72, v82, v72
	v_mul_f32_e64 v73, v83, v73
	s_nop 0
	v_mul_f32_e64 v72, v74, v72
	v_mul_f32_e64 v73, v75, v73
	s_nop 0
	v_cvt_pk_bf16_f32 v69, v72, v73
	v_mul_f32_e32 v72, 0xbfb8aa3b, v76
	v_mul_f32_e32 v73, 0xbfb8aa3b, v77
	v_exp_f32_e32 v72, v72
	v_exp_f32_e32 v73, v73
	v_add_f32_e32 v72, 1.0, v72
	v_add_f32_e32 v73, 1.0, v73
	v_rcp_f32_e32 v72, v72
	v_rcp_f32_e32 v73, v73
	s_nop 0
	v_mul_f32_e64 v72, v76, v72
	v_mul_f32_e64 v73, v77, v73
	s_nop 0
	v_mul_f32_e64 v70, v70, v72
	v_mul_f32_e64 v71, v71, v73
	s_nop 0
	v_cvt_pk_bf16_f32 v70, v70, v71
	v_mul_f32_e32 v71, 0xbfb8aa3b, v78
	v_exp_f32_e32 v71, v71
	s_nop 0
	v_add_f32_e32 v71, 1.0, v71
	v_rcp_f32_e32 v72, v71
	v_mul_f32_e32 v71, 0xbfb8aa3b, v79
	v_exp_f32_e32 v71, v71
	s_nop 0
	v_add_f32_e32 v71, 1.0, v71
	v_rcp_f32_e32 v73, v71
	s_nop 0
	v_mul_f32_e64 v72, v78, v72
	v_mul_f32_e64 v73, v79, v73
	s_nop 0
	v_mul_f32_e64 v72, v88, v72
	v_mul_f32_e64 v73, v89, v73
	s_nop 0
	v_cvt_pk_bf16_f32 v71, v72, v73
	global_store_dwordx4 v[84:85], v[68:71], off
	s_nop 1
	v_mad_u64_u32 v[68:69], s[2:3], v150, s4, v[142:143]
	v_mov_b32_e32 v70, v69
	v_mad_u64_u32 v[70:71], s[2:3], v151, s4, v[70:71]
	v_mov_b32_e32 v69, v70
	ds_read2_b32 v[70:71], v161 offset0:64 offset1:80
	v_lshl_add_u64 v[68:69], v[68:69], 0, v[144:145]
	s_waitcnt lgkmcnt(0)
; __device__ __forceinline__ unsigned cvt_pk_bf16(float lo, float hi) { f32x2_c v = {lo, hi}; bf16x2_c b = __builtin_convertvector(v, bf16x2_c); return __builtin_bit_cast(unsigned, b); }
; __device__ __forceinline__ float silu_f(float g) { return g * __builtin_amdgcn_rcpf(1.0f + __builtin_amdgcn_exp2f(-1.44269504f * g)); }
;     __device__ __forceinline__ void operator()(const f32x4 (&acc)[2][2][4][2], const Unit& u, int wr, int wc, int fr, int fq) const {
;     ...
;             for (int m = 0; m < 4; ++m) { bf16_t* rowp = O + (size_t)(row0 + ai * HALF + m * 16) * ldc + col0;
;                 const float rs = my[(ai * 4 + m) * 16];
;                 const f32x4 a0 = acc[ai][0][m][0] * rs, a1 = acc[ai][0][m][1] * rs, g0 = acc[ai][1][m][0] * rs, g1 = acc[ai][1][m][1] * rs;
;                 u32x4 w; w.x = cvt_pk_bf16(a0[0] * silu_f(g0[0]), a0[1] * silu_f(g0[1])); w.y = cvt_pk_bf16(a0[2] * silu_f(g0[2]), a0[3] * silu_f(g0[3]));
;                 w.z = cvt_pk_bf16(a1[0] * silu_f(g1[0]), a1[1] * silu_f(g1[1])); w.w = cvt_pk_bf16(a1[2] * silu_f(g1[2]), a1[3] * silu_f(g1[3]));
;                 *(u32x4*)rowp = w; }
	v_mul_f32_e64 v72, v54, v70
	v_mul_f32_e64 v73, v55, v70
	v_mul_f32_e64 v54, v52, v70
	v_mul_f32_e64 v55, v53, v70
	v_mul_f32_e64 v52, v64, v70
	v_mul_f32_e64 v53, v65, v70
	v_mul_f32_e64 v56, v56, v70
	v_mul_f32_e64 v57, v57, v70
	v_mul_f32_e32 v64, 0xbfb8aa3b, v52
	v_mul_f32_e32 v65, 0xbfb8aa3b, v53
	v_exp_f32_e32 v64, v64
	v_exp_f32_e32 v65, v65
	v_mul_f32_e64 v66, v66, v70
	v_mul_f32_e64 v67, v67, v70
	v_mul_f32_e64 v58, v58, v70
	v_mul_f32_e64 v59, v59, v70
	v_add_f32_e32 v64, 1.0, v64
	v_add_f32_e32 v65, 1.0, v65
	v_rcp_f32_e32 v64, v64
	v_rcp_f32_e32 v65, v65
	v_mul_f32_e64 v60, v60, v70
	v_mul_f32_e64 v61, v61, v70
	v_mul_f32_e64 v62, v62, v70
	v_mul_f32_e64 v63, v63, v70
	v_mul_f32_e64 v52, v52, v64
	v_mul_f32_e64 v53, v53, v65
	s_nop 0
	v_mul_f32_e64 v52, v56, v52
	v_mul_f32_e64 v53, v57, v53
	s_nop 0
	v_cvt_pk_bf16_f32 v52, v52, v53
	v_mul_f32_e32 v53, 0xbfb8aa3b, v66
	v_exp_f32_e32 v53, v53
	s_nop 0
	v_add_f32_e32 v53, 1.0, v53
	v_rcp_f32_e32 v56, v53
	v_mul_f32_e32 v53, 0xbfb8aa3b, v67
	v_exp_f32_e32 v53, v53
	s_nop 0
	v_add_f32_e32 v53, 1.0, v53
	v_rcp_f32_e32 v57, v53
	s_nop 0
	v_mul_f32_e64 v56, v66, v56
	v_mul_f32_e64 v57, v67, v57
	s_nop 0
	v_mul_f32_e64 v56, v58, v56
	v_mul_f32_e64 v57, v59, v57
	s_nop 0
	v_cvt_pk_bf16_f32 v53, v56, v57
	v_mul_f32_e32 v56, 0xbfb8aa3b, v60
	v_mul_f32_e32 v57, 0xbfb8aa3b, v61
	v_exp_f32_e32 v56, v56
	v_exp_f32_e32 v57, v57
	v_add_f32_e32 v56, 1.0, v56
	v_add_f32_e32 v57, 1.0, v57
	v_rcp_f32_e32 v56, v56
	v_rcp_f32_e32 v57, v57
	s_nop 0
	v_mul_f32_e64 v56, v60, v56
	v_mul_f32_e64 v57, v61, v57
	s_nop 0
	v_mul_f32_e64 v54, v54, v56
	v_mul_f32_e64 v55, v55, v57
	s_nop 0
	v_cvt_pk_bf16_f32 v54, v54, v55
	v_mul_f32_e32 v55, 0xbfb8aa3b, v62
	v_exp_f32_e32 v55, v55
	s_nop 0
	v_add_f32_e32 v55, 1.0, v55
	v_rcp_f32_e32 v56, v55
	v_mul_f32_e32 v55, 0xbfb8aa3b, v63
	v_exp_f32_e32 v55, v55
	s_nop 0
	v_add_f32_e32 v55, 1.0, v55
	v_rcp_f32_e32 v57, v55
	s_nop 0
	v_mul_f32_e64 v56, v62, v56
	v_mul_f32_e64 v57, v63, v57
	s_nop 0
	v_mul_f32_e64 v56, v72, v56
	v_mul_f32_e64 v57, v73, v57
	s_nop 0
	v_cvt_pk_bf16_f32 v55, v56, v57
	global_store_dwordx4 v[68:69], v[52:55], off
	s_nop 1
	v_mad_u64_u32 v[52:53], s[2:3], v148, s4, v[142:143]
	v_mov_b32_e32 v54, v53
	v_mad_u64_u32 v[54:55], s[2:3], v149, s4, v[54:55]
	v_mov_b32_e32 v53, v54
	v_mov_b32_e32 v54, v71
	v_mul_f32_e64 v56, v38, v54
	v_mul_f32_e64 v57, v39, v54
	v_mul_f32_e64 v38, v36, v54
	v_mul_f32_e64 v39, v37, v54
	v_mul_f32_e64 v36, v48, v54
	v_mul_f32_e64 v37, v49, v54
	v_mul_f32_e64 v40, v40, v54
	v_mul_f32_e64 v41, v41, v54
	v_mul_f32_e32 v48, 0xbfb8aa3b, v36
	v_mul_f32_e32 v49, 0xbfb8aa3b, v37
	v_exp_f32_e32 v48, v48
	v_exp_f32_e32 v49, v49
	v_mul_f32_e64 v50, v50, v54
	v_mul_f32_e64 v51, v51, v54
	v_mul_f32_e64 v42, v42, v54
	v_mul_f32_e64 v43, v43, v54
	v_add_f32_e32 v48, 1.0, v48
	v_add_f32_e32 v49, 1.0, v49
	v_rcp_f32_e32 v48, v48
	v_rcp_f32_e32 v49, v49
	v_mul_f32_e64 v44, v44, v54
	v_mul_f32_e64 v45, v45, v54
	v_mul_f32_e64 v46, v46, v54
	v_mul_f32_e64 v47, v47, v54
	v_lshl_add_u64 v[52:53], v[52:53], 0, v[144:145]
	v_mul_f32_e64 v36, v36, v48
	v_mul_f32_e64 v37, v37, v49
	s_nop 0
	v_mul_f32_e64 v36, v40, v36
	v_mul_f32_e64 v37, v41, v37
	s_nop 0
	v_cvt_pk_bf16_f32 v36, v36, v37
	v_mul_f32_e32 v37, 0xbfb8aa3b, v50
	v_exp_f32_e32 v37, v37
	s_nop 0
	v_add_f32_e32 v37, 1.0, v37
	v_rcp_f32_e32 v40, v37
	v_mul_f32_e32 v37, 0xbfb8aa3b, v51
	v_exp_f32_e32 v37, v37
	s_nop 0
	v_add_f32_e32 v37, 1.0, v37
	v_rcp_f32_e32 v41, v37
	s_nop 0
	v_mul_f32_e64 v40, v50, v40
	v_mul_f32_e64 v41, v51, v41
	s_nop 0
	v_mul_f32_e64 v40, v42, v40
	v_mul_f32_e64 v41, v43, v41
	s_nop 0
	v_cvt_pk_bf16_f32 v37, v40, v41
	v_mul_f32_e32 v40, 0xbfb8aa3b, v44
	v_mul_f32_e32 v41, 0xbfb8aa3b, v45
	v_exp_f32_e32 v40, v40
	v_exp_f32_e32 v41, v41
	v_add_f32_e32 v40, 1.0, v40
	v_add_f32_e32 v41, 1.0, v41
	v_rcp_f32_e32 v40, v40
	v_rcp_f32_e32 v41, v41
	s_nop 0
	v_mul_f32_e64 v40, v44, v40
	v_mul_f32_e64 v41, v45, v41
	s_nop 0
	v_mul_f32_e64 v38, v38, v40
	v_mul_f32_e64 v39, v39, v41
	s_nop 0
	v_cvt_pk_bf16_f32 v38, v38, v39
	v_mul_f32_e32 v39, 0xbfb8aa3b, v46
	v_exp_f32_e32 v39, v39
	s_nop 0
	v_add_f32_e32 v39, 1.0, v39
	v_rcp_f32_e32 v40, v39
	v_mul_f32_e32 v39, 0xbfb8aa3b, v47
	v_exp_f32_e32 v39, v39
	s_nop 0
	v_add_f32_e32 v39, 1.0, v39
	v_rcp_f32_e32 v41, v39
	s_nop 0
	v_mul_f32_e64 v40, v46, v40
	v_mul_f32_e64 v41, v47, v41
	s_nop 0
	v_mul_f32_e64 v40, v56, v40
	v_mul_f32_e64 v41, v57, v41
	s_nop 0
	v_cvt_pk_bf16_f32 v39, v40, v41
	global_store_dwordx4 v[52:53], v[36:39], off
	s_nop 1
	v_mad_u64_u32 v[36:37], s[2:3], v146, s4, v[142:143]
	v_mov_b32_e32 v38, v37
	v_mad_u64_u32 v[38:39], s[2:3], v147, s4, v[38:39]
	v_mov_b32_e32 v37, v38
	ds_read2_b32 v[38:39], v161 offset0:96 offset1:112
	v_lshl_add_u64 v[36:37], v[36:37], 0, v[144:145]
	s_waitcnt lgkmcnt(0)
; __device__ __forceinline__ unsigned cvt_pk_bf16(float lo, float hi) { f32x2_c v = {lo, hi}; bf16x2_c b = __builtin_convertvector(v, bf16x2_c); return __builtin_bit_cast(unsigned, b); }
; __device__ __forceinline__ float silu_f(float g) { return g * __builtin_amdgcn_rcpf(1.0f + __builtin_amdgcn_exp2f(-1.44269504f * g)); }
; #define PG8_BAR __builtin_amdgcn_s_barrier()
;     __device__ __forceinline__ void operator()(const f32x4 (&acc)[2][2][4][2], const Unit& u, int wr, int wc, int fr, int fq) const {
;     ...
;             for (int m = 0; m < 4; ++m) { bf16_t* rowp = O + (size_t)(row0 + ai * HALF + m * 16) * ldc + col0;
;                 const float rs = my[(ai * 4 + m) * 16];
;                 const f32x4 a0 = acc[ai][0][m][0] * rs, a1 = acc[ai][0][m][1] * rs, g0 = acc[ai][1][m][0] * rs, g1 = acc[ai][1][m][1] * rs;
;                 u32x4 w; w.x = cvt_pk_bf16(a0[0] * silu_f(g0[0]), a0[1] * silu_f(g0[1])); w.y = cvt_pk_bf16(a0[2] * silu_f(g0[2]), a0[3] * silu_f(g0[3]));
;                 w.z = cvt_pk_bf16(a1[0] * silu_f(g1[0]), a1[1] * silu_f(g1[1])); w.w = cvt_pk_bf16(a1[2] * silu_f(g1[2]), a1[3] * silu_f(g1[3]));
;                 *(u32x4*)rowp = w; }
; template <class Epi, class Sched, bool ALIGN_EPI = false, bool SP2 = false>
; __device__ __forceinline__ void gemm_phase(PG8_LAS unsigned char* lds, const Gemm g, const Sched& S, const Epi& E) {
;     ...
;         if (!has_next) break;
;         if constexpr (!SP2) {
; #pragma unroll
;         for (int a = 0; a < 2; ++a)
; #pragma unroll
;             for (int b = 0; b < 2; ++b)
; #pragma unroll
;                 for (int m = 0; m < 4; ++m)
; #pragma unroll
;                     for (int n = 0; n < 2; ++n) acc[a][b][m][n] = (f32x4){0.f, 0.f, 0.f, 0.f};
;         }
;         cur = nxt; cA = nA; cB = nB; ++ui;
;         if constexpr (ALIGN_EPI) { if (wr == 1) PG8_BAR; }
	v_mul_f32_e64 v40, v22, v38
	v_mul_f32_e64 v41, v23, v38
	v_mul_f32_e64 v22, v20, v38
	v_mul_f32_e64 v23, v21, v38
	v_mul_f32_e64 v20, v32, v38
	v_mul_f32_e64 v21, v33, v38
	v_mul_f32_e64 v24, v24, v38
	v_mul_f32_e64 v25, v25, v38
	v_mul_f32_e32 v32, 0xbfb8aa3b, v20
	v_mul_f32_e32 v33, 0xbfb8aa3b, v21
	v_exp_f32_e32 v32, v32
	v_exp_f32_e32 v33, v33
	v_mul_f32_e64 v34, v34, v38
	v_mul_f32_e64 v35, v35, v38
	v_mul_f32_e64 v26, v26, v38
	v_mul_f32_e64 v27, v27, v38
	v_add_f32_e32 v32, 1.0, v32
	v_add_f32_e32 v33, 1.0, v33
	v_rcp_f32_e32 v32, v32
	v_rcp_f32_e32 v33, v33
	v_mul_f32_e64 v28, v28, v38
	v_mul_f32_e64 v29, v29, v38
	v_mul_f32_e64 v30, v30, v38
	v_mul_f32_e64 v31, v31, v38
	v_mul_f32_e64 v20, v20, v32
	v_mul_f32_e64 v21, v21, v33
	s_nop 0
	v_mul_f32_e64 v20, v24, v20
	v_mul_f32_e64 v21, v25, v21
	s_nop 0
	v_cvt_pk_bf16_f32 v20, v20, v21
	v_mul_f32_e32 v21, 0xbfb8aa3b, v34
	v_exp_f32_e32 v21, v21
	s_nop 0
	v_add_f32_e32 v21, 1.0, v21
	v_rcp_f32_e32 v24, v21
	v_mul_f32_e32 v21, 0xbfb8aa3b, v35
	v_exp_f32_e32 v21, v21
	s_nop 0
	v_add_f32_e32 v21, 1.0, v21
	v_rcp_f32_e32 v25, v21
	s_nop 0
	v_mul_f32_e64 v24, v34, v24
	v_mul_f32_e64 v25, v35, v25
	s_nop 0
	v_mul_f32_e64 v24, v26, v24
	v_mul_f32_e64 v25, v27, v25
	s_nop 0
	v_cvt_pk_bf16_f32 v21, v24, v25
	v_mul_f32_e32 v24, 0xbfb8aa3b, v28
	v_mul_f32_e32 v25, 0xbfb8aa3b, v29
	v_exp_f32_e32 v24, v24
	v_exp_f32_e32 v25, v25
	v_add_f32_e32 v24, 1.0, v24
	v_add_f32_e32 v25, 1.0, v25
	v_rcp_f32_e32 v24, v24
	v_rcp_f32_e32 v25, v25
	s_nop 0
	v_mul_f32_e64 v24, v28, v24
	v_mul_f32_e64 v25, v29, v25
	s_nop 0
	v_mul_f32_e64 v22, v22, v24
	v_mul_f32_e64 v23, v23, v25
	s_nop 0
	v_cvt_pk_bf16_f32 v22, v22, v23
	v_mul_f32_e32 v23, 0xbfb8aa3b, v30
	v_exp_f32_e32 v23, v23
	s_nop 0
	v_add_f32_e32 v23, 1.0, v23
	v_rcp_f32_e32 v24, v23
	v_mul_f32_e32 v23, 0xbfb8aa3b, v31
	v_exp_f32_e32 v23, v23
	s_nop 0
	v_add_f32_e32 v23, 1.0, v23
	v_rcp_f32_e32 v25, v23
	s_nop 0
	v_mul_f32_e64 v24, v30, v24
	v_mul_f32_e64 v25, v31, v25
	s_nop 0
	v_mul_f32_e64 v24, v40, v24
	v_mul_f32_e64 v25, v41, v25
	s_nop 0
	v_cvt_pk_bf16_f32 v23, v24, v25
	global_store_dwordx4 v[36:37], v[20:23], off
	s_nop 1
	v_mad_u64_u32 v[20:21], s[2:3], v140, s4, v[142:143]
	v_mov_b32_e32 v22, v21
	v_mad_u64_u32 v[22:23], s[2:3], v141, s4, v[22:23]
	v_mov_b32_e32 v21, v22
	v_mov_b32_e32 v22, v39
	v_mul_f32_e64 v24, v6, v22
	v_mul_f32_e64 v25, v7, v22
	v_mul_f32_e64 v6, v4, v22
	v_mul_f32_e64 v7, v5, v22
	v_mul_f32_e64 v4, v16, v22
	v_mul_f32_e64 v5, v17, v22
	v_mul_f32_e64 v8, v8, v22
	v_mul_f32_e64 v9, v9, v22
	v_mul_f32_e32 v16, 0xbfb8aa3b, v4
	v_mul_f32_e32 v17, 0xbfb8aa3b, v5
	v_exp_f32_e32 v16, v16
	v_exp_f32_e32 v17, v17
	v_mul_f32_e64 v18, v18, v22
	v_mul_f32_e64 v19, v19, v22
	v_mul_f32_e64 v10, v10, v22
	v_mul_f32_e64 v11, v11, v22
	v_add_f32_e32 v16, 1.0, v16
	v_add_f32_e32 v17, 1.0, v17
	v_rcp_f32_e32 v16, v16
	v_rcp_f32_e32 v17, v17
	v_mul_f32_e64 v12, v12, v22
	v_mul_f32_e64 v13, v13, v22
	v_mul_f32_e64 v14, v14, v22
	v_mul_f32_e64 v15, v15, v22
	v_lshl_add_u64 v[20:21], v[20:21], 0, v[144:145]
	v_mul_f32_e64 v4, v4, v16
	v_mul_f32_e64 v5, v5, v17
	s_mov_b64 s[4:5], -1
	v_mul_f32_e64 v4, v8, v4
	v_mul_f32_e64 v5, v9, v5
	s_nop 0
	v_cvt_pk_bf16_f32 v4, v4, v5
	v_mul_f32_e32 v5, 0xbfb8aa3b, v18
	v_exp_f32_e32 v5, v5
	s_nop 0
	v_add_f32_e32 v5, 1.0, v5
	v_rcp_f32_e32 v8, v5
	v_mul_f32_e32 v5, 0xbfb8aa3b, v19
	v_exp_f32_e32 v5, v5
	s_nop 0
	v_add_f32_e32 v5, 1.0, v5
	v_rcp_f32_e32 v9, v5
	s_nop 0
	v_mul_f32_e64 v8, v18, v8
	v_mul_f32_e64 v9, v19, v9
	s_nop 0
	v_mul_f32_e64 v8, v10, v8
	v_mul_f32_e64 v9, v11, v9
	s_nop 0
	v_cvt_pk_bf16_f32 v5, v8, v9
	v_mul_f32_e32 v8, 0xbfb8aa3b, v12
	v_mul_f32_e32 v9, 0xbfb8aa3b, v13
	v_exp_f32_e32 v8, v8
	v_exp_f32_e32 v9, v9
	v_add_f32_e32 v8, 1.0, v8
	v_add_f32_e32 v9, 1.0, v9
	v_rcp_f32_e32 v8, v8
	v_rcp_f32_e32 v9, v9
	s_nop 0
	v_mul_f32_e64 v8, v12, v8
	v_mul_f32_e64 v9, v13, v9
	s_nop 0
	v_mul_f32_e64 v6, v6, v8
	v_mul_f32_e64 v7, v7, v9
	s_nop 0
	v_cvt_pk_bf16_f32 v6, v6, v7
	v_mul_f32_e32 v7, 0xbfb8aa3b, v14
	v_exp_f32_e32 v7, v7
	s_nop 0
	v_add_f32_e32 v7, 1.0, v7
	v_rcp_f32_e32 v8, v7
	v_mul_f32_e32 v7, 0xbfb8aa3b, v15
	v_exp_f32_e32 v7, v7
	s_nop 0
	v_add_f32_e32 v7, 1.0, v7
	v_rcp_f32_e32 v9, v7
	s_nop 0
	v_mul_f32_e64 v8, v14, v8
	v_mul_f32_e64 v9, v15, v9
	s_nop 0
	v_mul_f32_e64 v8, v24, v8
	v_mul_f32_e64 v9, v25, v9
	s_nop 0
	v_cvt_pk_bf16_f32 v7, v8, v9
	global_store_dwordx4 v[20:21], v[4:7], off
	s_cbranch_vccnz .LBB0_124
	s_andn2_b64 vcc, exec, s[18:19]
	s_cbranch_vccnz .LBB0_123
	s_barrier
	s_branch .LBB0_123

; __device__ __forceinline__ unsigned cvt_pk_bf16(float lo, float hi) { f32x2_c v = {lo, hi}; bf16x2_c b = __builtin_convertvector(v, bf16x2_c); return __builtin_bit_cast(unsigned, b); }
; __device__ __forceinline__ float bf_lo(unsigned u) { return __uint_as_float(u << 16); }
; __device__ __forceinline__ float bf_hi(unsigned u) { return __uint_as_float(u & 0xffff0000u); }
;     __device__ __forceinline__ void operator()(const f32x4 (&acc)[2][2][4][2], const Unit& u, int wr, int wc, int fr, int fq) const {
;     ...
;                 for (int bj = 0; bj < 2; ++bj) xv[m][bj] = *(const u32x4*)(Hx + (size_t)(row0 + ai * HALF + m * 16) * LDT + col0 + bj * HALF);
;             float ssm[4];
; #pragma unroll
;             for (int m = 0; m < 4; ++m) { const int row = row0 + ai * HALF + m * 16; bf16_t* hp = Hx + (size_t)row * LDT + col0;
;                 float ss = 0.f;
; #pragma unroll
;                 for (int bj = 0; bj < 2; ++bj) { const u32x4 x = xv[m][bj]; const f32x4 a0 = acc[ai][bj][m][0], a1 = acc[ai][bj][m][1];
;                     const float y0 = bf_lo(x.x) + a0[0] * scale, y1 = bf_hi(x.x) + a0[1] * scale, y2 = bf_lo(x.y) + a0[2] * scale, y3 = bf_hi(x.y) + a0[3] * scale;
;                     const float y4 = bf_lo(x.z) + a1[0] * scale, y5 = bf_hi(x.z) + a1[1] * scale, y6 = bf_lo(x.w) + a1[2] * scale, y7 = bf_hi(x.w) + a1[3] * scale;
;                     ss += ((y0 * y0 + y1 * y1) + (y2 * y2 + y3 * y3)) + ((y4 * y4 + y5 * y5) + (y6 * y6 + y7 * y7));
;                     u32x4 w; w.x = cvt_pk_bf16(y0, y1); w.y = cvt_pk_bf16(y2, y3); w.z = cvt_pk_bf16(y4, y5); w.w = cvt_pk_bf16(y6, y7);
;                     *(u32x4*)(hp + bj * HALF) = w; }
;                 ss += __shfl_xor(ss, 16); ss += __shfl_xor(ss, 32); ssm[m] = ss; }
.LBB0_236:
	v_lshl_or_b32 v116, s2, 8, v177
	v_ashrrev_i32_e32 v117, 31, v116
	v_readlane_b32 s24, v254, 23
	v_lshlrev_b64 v[166:167], 1, v[116:117]
	v_readlane_b32 s25, v254, 24
	v_lshl_add_u32 v181, s3, 8, v174
	v_or_b32_e32 v196, 16, v181
	v_lshl_add_u64 v[168:169], s[24:25], 0, v[166:167]
	v_mad_i64_i32 v[116:117], s[4:5], v181, s81, v[168:169]
	global_load_dwordx4 v[182:185], v[116:117], off
	global_load_dwordx4 v[156:159], v[116:117], off offset:256
	v_mad_i64_i32 v[116:117], s[4:5], v196, s81, v[168:169]
	global_load_dwordx4 v[152:155], v[116:117], off
	global_load_dwordx4 v[148:151], v[116:117], off offset:256
	v_or_b32_e32 v195, 32, v181
	v_mad_i64_i32 v[116:117], s[4:5], v195, s81, v[168:169]
	global_load_dwordx4 v[144:147], v[116:117], off
	global_load_dwordx4 v[132:135], v[116:117], off offset:256
	v_and_b32_e32 v119, 64, v210
	v_xor_b32_e32 v118, 16, v210
	v_add_u32_e32 v119, 64, v119
	v_cmp_lt_i32_e32 vcc, v118, v119
	v_or_b32_e32 v194, 48, v181
	v_mad_i64_i32 v[116:117], s[4:5], v194, s81, v[168:169]
	v_cndmask_b32_e32 v118, v210, v118, vcc
	v_lshlrev_b32_e32 v180, 2, v118
	v_xor_b32_e32 v118, 32, v210
	v_cmp_lt_i32_e32 vcc, v118, v119
	v_mov_b64_e32 v[170:171], s[24:25]
	v_mad_i64_i32 v[172:173], s[4:5], v181, s81, v[170:171]
	v_cndmask_b32_e32 v118, v210, v118, vcc
	v_lshlrev_b32_e32 v179, 2, v118
	global_load_dwordx4 v[120:123], v[116:117], off
	s_nop 0
	global_load_dwordx4 v[116:119], v[116:117], off offset:256
	v_lshl_add_u64 v[172:173], v[172:173], 0, v[166:167]
	v_cmp_lt_i32_e32 vcc, 0, v3
	s_waitcnt vmcnt(0)
	v_lshlrev_b32_e32 v186, 16, v182
	v_and_b32_e32 v187, 0xffff0000, v182
	v_lshlrev_b32_e32 v182, 16, v183
	v_and_b32_e32 v183, 0xffff0000, v183
	v_fma_f32 v142, v142, 0.5, v182
	v_fma_f32 v143, v143, 0.5, v183
	v_lshlrev_b32_e32 v182, 16, v184
	v_and_b32_e32 v183, 0xffff0000, v184
	v_fma_f32 v182, v136, 0.5, v182
	v_fma_f32 v183, v137, 0.5, v183
	v_lshlrev_b32_e32 v136, 16, v185
	v_and_b32_e32 v137, 0xffff0000, v185
	v_fma_f32 v140, v140, 0.5, v186
	v_fma_f32 v141, v141, 0.5, v187
	v_fma_f32 v184, v138, 0.5, v136
	v_fma_f32 v185, v139, 0.5, v137
	v_cvt_pk_bf16_f32 v136, v140, v141
	v_cvt_pk_bf16_f32 v137, v142, v143
	v_cvt_pk_bf16_f32 v138, v182, v183
	v_cvt_pk_bf16_f32 v139, v184, v185
	global_store_dwordx4 v[172:173], v[136:139], off
	v_mul_f32_e64 v190, v182, v182
	v_mul_f32_e64 v191, v183, v183
	v_mul_f32_e64 v192, v184, v184
	v_mul_f32_e64 v193, v185, v185
	v_lshlrev_b32_e32 v136, 16, v156
	v_and_b32_e32 v137, 0xffff0000, v156
	v_fma_f32 v128, v128, 0.5, v136
	v_fma_f32 v129, v129, 0.5, v137
	v_lshlrev_b32_e32 v136, 16, v157
	v_and_b32_e32 v137, 0xffff0000, v157
	v_fma_f32 v130, v130, 0.5, v136
	v_fma_f32 v131, v131, 0.5, v137
	v_lshlrev_b32_e32 v136, 16, v158
	v_and_b32_e32 v137, 0xffff0000, v158
	v_fma_f32 v136, v124, 0.5, v136
	v_fma_f32 v137, v125, 0.5, v137
	v_lshlrev_b32_e32 v124, 16, v159
	v_and_b32_e32 v125, 0xffff0000, v159
	v_fma_f32 v138, v126, 0.5, v124
	v_fma_f32 v139, v127, 0.5, v125
	v_mul_f32_e64 v124, v128, v128
	v_mul_f32_e64 v125, v129, v129
	v_mul_f32_e64 v126, v130, v130
	v_mul_f32_e64 v127, v131, v131
	v_add_f32_e32 v124, v124, v125
	v_add_f32_e32 v126, v126, v127
	v_mul_f32_e64 v186, v140, v140
	v_mul_f32_e64 v187, v141, v141
	v_mul_f32_e64 v188, v142, v142
	v_mul_f32_e64 v189, v143, v143
	v_mul_f32_e64 v140, v136, v136
	v_mul_f32_e64 v141, v137, v137
	v_mul_f32_e64 v142, v138, v138
	v_mul_f32_e64 v143, v139, v139
	v_add_f32_e32 v124, v124, v126
	v_add_f32_e32 v125, v192, v193
	v_add_f32_e32 v126, v190, v191
	v_add_f32_e32 v142, v142, v143
	v_add_f32_e32 v140, v140, v141
	v_add_f32_e32 v125, v126, v125
	v_add_f32_e32 v126, v188, v189
	v_add_f32_e32 v127, v186, v187
	v_add_f32_e32 v140, v140, v142
	v_add_f32_e32 v126, v127, v126
	v_add_f32_e32 v124, v124, v140
	v_add_f32_e32 v125, v126, v125
	v_add_f32_e32 v140, v125, v124
	v_cvt_pk_bf16_f32 v124, v128, v129
	v_lshlrev_b32_e32 v128, 16, v152
	v_and_b32_e32 v129, 0xffff0000, v152
	v_fma_f32 v112, v112, 0.5, v128
	v_fma_f32 v113, v113, 0.5, v129
	v_lshlrev_b32_e32 v128, 16, v153
	v_and_b32_e32 v129, 0xffff0000, v153
	v_fma_f32 v114, v114, 0.5, v128
	v_fma_f32 v115, v115, 0.5, v129
	v_lshlrev_b32_e32 v128, 16, v154
	v_and_b32_e32 v129, 0xffff0000, v154
	v_cvt_pk_bf16_f32 v125, v130, v131
	v_cvt_pk_bf16_f32 v126, v136, v137
	v_cvt_pk_bf16_f32 v127, v138, v139
	v_fma_f32 v128, v108, 0.5, v128
	v_fma_f32 v129, v109, 0.5, v129
	v_lshlrev_b32_e32 v108, 16, v155
	v_and_b32_e32 v109, 0xffff0000, v155
	global_store_dwordx4 v[172:173], v[124:127], off offset:256
	v_fma_f32 v130, v110, 0.5, v108
	v_fma_f32 v131, v111, 0.5, v109
	v_cvt_pk_bf16_f32 v108, v112, v113
	v_mad_i64_i32 v[126:127], s[4:5], v196, s81, v[170:171]
	v_lshl_add_u64 v[126:127], v[126:127], 0, v[166:167]
	v_cvt_pk_bf16_f32 v109, v114, v115
	v_cvt_pk_bf16_f32 v110, v128, v129
	v_cvt_pk_bf16_f32 v111, v130, v131
	ds_bpermute_b32 v124, v180, v140
	global_store_dwordx4 v[126:127], v[108:111], off
	v_mul_f32_e64 v142, v130, v130
	v_mul_f32_e64 v143, v131, v131
	v_mul_f32_e64 v136, v112, v112
	v_mul_f32_e64 v137, v113, v113
	v_lshlrev_b32_e32 v108, 16, v148
	v_and_b32_e32 v109, 0xffff0000, v148
	v_fma_f32 v104, v104, 0.5, v108
	v_fma_f32 v105, v105, 0.5, v109
	v_lshlrev_b32_e32 v108, 16, v149
	v_and_b32_e32 v109, 0xffff0000, v149
	v_fma_f32 v106, v106, 0.5, v108
	v_fma_f32 v107, v107, 0.5, v109
	v_lshlrev_b32_e32 v108, 16, v150
	v_and_b32_e32 v109, 0xffff0000, v150
	v_fma_f32 v108, v100, 0.5, v108
	v_fma_f32 v109, v101, 0.5, v109
	v_lshlrev_b32_e32 v100, 16, v151
	v_and_b32_e32 v101, 0xffff0000, v151
	v_fma_f32 v110, v102, 0.5, v100
	v_fma_f32 v111, v103, 0.5, v101
	v_mul_f32_e64 v100, v104, v104
	v_mul_f32_e64 v101, v105, v105
	v_mul_f32_e64 v102, v106, v106
	v_mul_f32_e64 v103, v107, v107
	s_waitcnt lgkmcnt(0)
; __device__ __forceinline__ unsigned cvt_pk_bf16(float lo, float hi) { f32x2_c v = {lo, hi}; bf16x2_c b = __builtin_convertvector(v, bf16x2_c); return __builtin_bit_cast(unsigned, b); }
; __device__ __forceinline__ float bf_lo(unsigned u) { return __uint_as_float(u << 16); }
; __device__ __forceinline__ float bf_hi(unsigned u) { return __uint_as_float(u & 0xffff0000u); }
;     __device__ __forceinline__ void operator()(const f32x4 (&acc)[2][2][4][2], const Unit& u, int wr, int wc, int fr, int fq) const {
;     ...
;             for (int m = 0; m < 4; ++m) { const int row = row0 + ai * HALF + m * 16; bf16_t* hp = Hx + (size_t)row * LDT + col0;
;                 float ss = 0.f;
; #pragma unroll
;                 for (int bj = 0; bj < 2; ++bj) { const u32x4 x = xv[m][bj]; const f32x4 a0 = acc[ai][bj][m][0], a1 = acc[ai][bj][m][1];
;                     const float y0 = bf_lo(x.x) + a0[0] * scale, y1 = bf_hi(x.x) + a0[1] * scale, y2 = bf_lo(x.y) + a0[2] * scale, y3 = bf_hi(x.y) + a0[3] * scale;
;                     const float y4 = bf_lo(x.z) + a1[0] * scale, y5 = bf_hi(x.z) + a1[1] * scale, y6 = bf_lo(x.w) + a1[2] * scale, y7 = bf_hi(x.w) + a1[3] * scale;
;                     ss += ((y0 * y0 + y1 * y1) + (y2 * y2 + y3 * y3)) + ((y4 * y4 + y5 * y5) + (y6 * y6 + y7 * y7));
;                     u32x4 w; w.x = cvt_pk_bf16(y0, y1); w.y = cvt_pk_bf16(y2, y3); w.z = cvt_pk_bf16(y4, y5); w.w = cvt_pk_bf16(y6, y7);
;                     *(u32x4*)(hp + bj * HALF) = w; }
;                 ss += __shfl_xor(ss, 16); ss += __shfl_xor(ss, 32); ssm[m] = ss; }
;             { const float sv = (fq == 0) ? ssm[0] : (fq == 1) ? ssm[1] : (fq == 2) ? ssm[2] : ssm[3];
	v_add_f32_e32 v124, v140, v124
	v_mul_f32_e64 v140, v128, v128
	v_mul_f32_e64 v141, v129, v129
	v_add_f32_e32 v102, v102, v103
	v_add_f32_e32 v100, v100, v101
	v_mul_f32_e64 v138, v114, v114
	v_mul_f32_e64 v139, v115, v115
	v_mul_f32_e64 v112, v108, v108
	v_mul_f32_e64 v113, v109, v109
	v_mul_f32_e64 v114, v110, v110
	v_mul_f32_e64 v115, v111, v111
	v_add_f32_e32 v100, v100, v102
	v_add_f32_e32 v101, v142, v143
	v_add_f32_e32 v102, v140, v141
	v_add_f32_e32 v114, v114, v115
	v_add_f32_e32 v112, v112, v113
	v_add_f32_e32 v101, v102, v101
	v_add_f32_e32 v102, v138, v139
	v_add_f32_e32 v103, v136, v137
	v_add_f32_e32 v112, v112, v114
	v_add_f32_e32 v102, v103, v102
	v_add_f32_e32 v100, v100, v112
	v_add_f32_e32 v101, v102, v101
	v_add_f32_e32 v112, v101, v100
	v_cvt_pk_bf16_f32 v100, v104, v105
	v_lshlrev_b32_e32 v104, 16, v144
	v_and_b32_e32 v105, 0xffff0000, v144
	v_fma_f32 v96, v96, 0.5, v104
	v_fma_f32 v97, v97, 0.5, v105
	v_lshlrev_b32_e32 v104, 16, v145
	v_and_b32_e32 v105, 0xffff0000, v145
	v_fma_f32 v98, v98, 0.5, v104
	v_fma_f32 v99, v99, 0.5, v105
	v_lshlrev_b32_e32 v104, 16, v146
	v_and_b32_e32 v105, 0xffff0000, v146
	v_cvt_pk_bf16_f32 v101, v106, v107
	v_cvt_pk_bf16_f32 v102, v108, v109
	v_cvt_pk_bf16_f32 v103, v110, v111
	v_fma_f32 v104, v92, 0.5, v104
	v_fma_f32 v105, v93, 0.5, v105
	v_lshlrev_b32_e32 v92, 16, v147
	v_and_b32_e32 v93, 0xffff0000, v147
	global_store_dwordx4 v[126:127], v[100:103], off offset:256
	v_fma_f32 v106, v94, 0.5, v92
	v_fma_f32 v107, v95, 0.5, v93
	v_cvt_pk_bf16_f32 v92, v96, v97
	v_mad_i64_i32 v[102:103], s[4:5], v195, s81, v[170:171]
	v_lshl_add_u64 v[102:103], v[102:103], 0, v[166:167]
	v_cvt_pk_bf16_f32 v93, v98, v99
	v_cvt_pk_bf16_f32 v94, v104, v105
	v_cvt_pk_bf16_f32 v95, v106, v107
	ds_bpermute_b32 v100, v180, v112
	global_store_dwordx4 v[102:103], v[92:95], off
	v_mul_f32_e64 v114, v106, v106
	v_mul_f32_e64 v115, v107, v107
	v_mul_f32_e64 v108, v96, v96
	v_mul_f32_e64 v109, v97, v97
	v_lshlrev_b32_e32 v92, 16, v132
	v_and_b32_e32 v93, 0xffff0000, v132
	v_fma_f32 v88, v88, 0.5, v92
	v_fma_f32 v89, v89, 0.5, v93
	v_lshlrev_b32_e32 v92, 16, v133
	v_and_b32_e32 v93, 0xffff0000, v133
	v_fma_f32 v90, v90, 0.5, v92
	v_fma_f32 v91, v91, 0.5, v93
	v_lshlrev_b32_e32 v92, 16, v134
	v_and_b32_e32 v93, 0xffff0000, v134
	v_fma_f32 v92, v84, 0.5, v92
	v_fma_f32 v93, v85, 0.5, v93
	v_lshlrev_b32_e32 v84, 16, v135
	v_and_b32_e32 v85, 0xffff0000, v135
	v_fma_f32 v94, v86, 0.5, v84
	v_fma_f32 v95, v87, 0.5, v85
	v_mul_f32_e64 v84, v88, v88
	v_mul_f32_e64 v85, v89, v89
	v_mul_f32_e64 v86, v90, v90
	v_mul_f32_e64 v87, v91, v91
	s_waitcnt lgkmcnt(0)
	v_add_f32_e32 v100, v112, v100
	v_mul_f32_e64 v112, v104, v104
	v_mul_f32_e64 v113, v105, v105
	v_add_f32_e32 v86, v86, v87
	v_add_f32_e32 v84, v84, v85
	v_mul_f32_e64 v110, v98, v98
	v_mul_f32_e64 v111, v99, v99
	v_mul_f32_e64 v96, v92, v92
	v_mul_f32_e64 v97, v93, v93
	v_mul_f32_e64 v98, v94, v94
	v_mul_f32_e64 v99, v95, v95
	v_add_f32_e32 v84, v84, v86
	v_add_f32_e32 v85, v114, v115
	v_add_f32_e32 v86, v112, v113
	v_add_f32_e32 v98, v98, v99
	v_add_f32_e32 v96, v96, v97
	v_add_f32_e32 v85, v86, v85
	v_add_f32_e32 v86, v110, v111
	v_add_f32_e32 v87, v108, v109
	v_add_f32_e32 v96, v96, v98
	v_add_f32_e32 v86, v87, v86
	v_add_f32_e32 v84, v84, v96
	v_add_f32_e32 v85, v86, v85
	v_add_f32_e32 v96, v85, v84
	v_cvt_pk_bf16_f32 v84, v88, v89
	v_lshlrev_b32_e32 v88, 16, v120
	v_and_b32_e32 v89, 0xffff0000, v120
	v_fma_f32 v80, v80, 0.5, v88
	v_fma_f32 v81, v81, 0.5, v89
	v_lshlrev_b32_e32 v88, 16, v121
	v_and_b32_e32 v89, 0xffff0000, v121
	v_fma_f32 v82, v82, 0.5, v88
	v_fma_f32 v83, v83, 0.5, v89
	v_lshlrev_b32_e32 v88, 16, v122
	v_and_b32_e32 v89, 0xffff0000, v122
	v_cvt_pk_bf16_f32 v85, v90, v91
	v_cvt_pk_bf16_f32 v86, v92, v93
	v_cvt_pk_bf16_f32 v87, v94, v95
	v_fma_f32 v88, v76, 0.5, v88
	v_fma_f32 v89, v77, 0.5, v89
	v_lshlrev_b32_e32 v76, 16, v123
	v_and_b32_e32 v77, 0xffff0000, v123
	global_store_dwordx4 v[102:103], v[84:87], off offset:256
	v_fma_f32 v90, v78, 0.5, v76
	v_fma_f32 v91, v79, 0.5, v77
	v_cvt_pk_bf16_f32 v76, v80, v81
	v_mad_i64_i32 v[86:87], s[4:5], v194, s81, v[170:171]
	v_lshl_add_u64 v[86:87], v[86:87], 0, v[166:167]
	v_cvt_pk_bf16_f32 v77, v82, v83
	v_cvt_pk_bf16_f32 v78, v88, v89
	v_cvt_pk_bf16_f32 v79, v90, v91
	ds_bpermute_b32 v84, v180, v96
	global_store_dwordx4 v[86:87], v[76:79], off
	v_mul_f32_e64 v98, v90, v90
	v_mul_f32_e64 v99, v91, v91
	v_mul_f32_e64 v92, v80, v80
	v_mul_f32_e64 v93, v81, v81
	v_lshlrev_b32_e32 v76, 16, v116
	v_and_b32_e32 v77, 0xffff0000, v116
	v_fma_f32 v72, v72, 0.5, v76
	v_fma_f32 v73, v73, 0.5, v77
	v_lshlrev_b32_e32 v76, 16, v117
	v_and_b32_e32 v77, 0xffff0000, v117
	v_fma_f32 v74, v74, 0.5, v76
	v_fma_f32 v75, v75, 0.5, v77
	v_lshlrev_b32_e32 v76, 16, v118
	v_and_b32_e32 v77, 0xffff0000, v118
	v_fma_f32 v76, v68, 0.5, v76
	v_fma_f32 v77, v69, 0.5, v77
	v_lshlrev_b32_e32 v68, 16, v119
	v_and_b32_e32 v69, 0xffff0000, v119
	v_fma_f32 v78, v70, 0.5, v68
	v_fma_f32 v79, v71, 0.5, v69
	v_mul_f32_e64 v68, v72, v72
	v_mul_f32_e64 v69, v73, v73
	v_mul_f32_e64 v70, v74, v74
	v_mul_f32_e64 v71, v75, v75
	s_waitcnt lgkmcnt(0)
	v_add_f32_e32 v84, v96, v84
	v_mul_f32_e64 v96, v88, v88
	v_mul_f32_e64 v97, v89, v89
	v_add_f32_e32 v70, v70, v71
	v_add_f32_e32 v68, v68, v69
	v_mul_f32_e64 v94, v82, v82
	v_mul_f32_e64 v95, v83, v83
	v_mul_f32_e64 v80, v76, v76
	v_mul_f32_e64 v81, v77, v77
	v_mul_f32_e64 v82, v78, v78
	v_mul_f32_e64 v83, v79, v79
	v_add_f32_e32 v68, v68, v70
	v_add_f32_e32 v69, v98, v99
	v_add_f32_e32 v70, v96, v97
	v_add_f32_e32 v82, v82, v83
	v_add_f32_e32 v80, v80, v81
	v_add_f32_e32 v69, v70, v69
	v_add_f32_e32 v70, v94, v95
	v_add_f32_e32 v71, v92, v93
	v_add_f32_e32 v80, v80, v82
	v_add_f32_e32 v70, v71, v70
	v_add_f32_e32 v68, v68, v80
	v_add_f32_e32 v69, v70, v69
	v_add_f32_e32 v80, v69, v68
	v_cvt_pk_bf16_f32 v68, v72, v73
	v_cvt_pk_bf16_f32 v69, v74, v75
	v_cvt_pk_bf16_f32 v70, v76, v77
	v_cvt_pk_bf16_f32 v71, v78, v79
	global_store_dwordx4 v[86:87], v[68:71], off offset:256
	ds_bpermute_b32 v68, v180, v80
	ds_bpermute_b32 v125, v179, v124
	ds_bpermute_b32 v101, v179, v100
	ds_bpermute_b32 v85, v179, v84
	s_waitcnt lgkmcnt(3)
	v_add_f32_e32 v69, v80, v68
	ds_bpermute_b32 v70, v179, v69
	s_and_saveexec_b64 s[4:5], vcc
	s_xor_b64 s[4:5], exec, s[4:5]
	s_cbranch_execz .LBB0_242
	v_cmp_ne_u32_e32 vcc, 1, v3
	s_and_saveexec_b64 s[24:25], vcc
	s_xor_b64 s[24:25], exec, s[24:25]
	s_cbranch_execz .LBB0_239
	s_waitcnt lgkmcnt(0)
	v_add_f32_e32 v68, v69, v70
	v_add_f32_e32 v69, v84, v85
	v_cndmask_b32_e64 v68, v68, v69, s[6:7]

; __device__ __forceinline__ unsigned cvt_pk_bf16(float lo, float hi) { f32x2_c v = {lo, hi}; bf16x2_c b = __builtin_convertvector(v, bf16x2_c); return __builtin_bit_cast(unsigned, b); }
; __device__ __forceinline__ float bf_lo(unsigned u) { return __uint_as_float(u << 16); }
; __device__ __forceinline__ float bf_hi(unsigned u) { return __uint_as_float(u & 0xffff0000u); }
;     __device__ __forceinline__ void operator()(const f32x4 (&acc)[2][2][4][2], const Unit& u, int wr, int wc, int fr, int fq) const {
;     ...
;                 for (int bj = 0; bj < 2; ++bj) xv[m][bj] = *(const u32x4*)(Hx + (size_t)(row0 + ai * HALF + m * 16) * LDT + col0 + bj * HALF);
;             float ssm[4];
; #pragma unroll
;             for (int m = 0; m < 4; ++m) { const int row = row0 + ai * HALF + m * 16; bf16_t* hp = Hx + (size_t)row * LDT + col0;
;                 float ss = 0.f;
; #pragma unroll
;                 for (int bj = 0; bj < 2; ++bj) { const u32x4 x = xv[m][bj]; const f32x4 a0 = acc[ai][bj][m][0], a1 = acc[ai][bj][m][1];
;                     const float y0 = bf_lo(x.x) + a0[0] * scale, y1 = bf_hi(x.x) + a0[1] * scale, y2 = bf_lo(x.y) + a0[2] * scale, y3 = bf_hi(x.y) + a0[3] * scale;
;                     const float y4 = bf_lo(x.z) + a1[0] * scale, y5 = bf_hi(x.z) + a1[1] * scale, y6 = bf_lo(x.w) + a1[2] * scale, y7 = bf_hi(x.w) + a1[3] * scale;
;                     ss += ((y0 * y0 + y1 * y1) + (y2 * y2 + y3 * y3)) + ((y4 * y4 + y5 * y5) + (y6 * y6 + y7 * y7));
;                     u32x4 w; w.x = cvt_pk_bf16(y0, y1); w.y = cvt_pk_bf16(y2, y3); w.z = cvt_pk_bf16(y4, y5); w.w = cvt_pk_bf16(y6, y7);
;                     *(u32x4*)(hp + bj * HALF) = w; }
;                 ss += __shfl_xor(ss, 16); ss += __shfl_xor(ss, 32); ssm[m] = ss; }
;             { const float sv = (fq == 0) ? ssm[0] : (fq == 1) ? ssm[1] : (fq == 2) ? ssm[2] : ssm[3];
;               ssq[(size_t)(row0 + ai * HALF + fq * 16) * 32 + u.pn * 4 + wc] = sv; }
.LBB0_244:
	s_or_b64 exec, exec, s[4:5]
	v_or_b32_e32 v92, v181, v175
	v_ashrrev_i32_e32 v93, 31, v92
	s_lshl_b32 s24, s2, 2
	s_waitcnt lgkmcnt(0)
	v_lshlrev_b64 v[70:71], 7, v[92:93]
	s_ashr_i32 s25, s24, 31
	v_lshl_add_u64 v[70:71], s[16:17], 0, v[70:71]
	v_lshl_add_u64 v[70:71], s[24:25], 2, v[70:71]
	s_lshl_b32 s0, s15, 2
	v_lshl_add_u64 v[70:71], v[70:71], 0, s[0:1]
	global_store_dword v[70:71], v68, off
	v_add_u32_e32 v97, 0x80, v181
	v_mad_i64_i32 v[68:69], s[2:3], v97, s81, v[168:169]
	global_load_dwordx4 v[98:101], v[68:69], off
	global_load_dwordx4 v[102:105], v[68:69], off offset:256
	v_add_u32_e32 v116, 0x90, v181
	v_mad_i64_i32 v[68:69], s[2:3], v116, s81, v[168:169]
	global_load_dwordx4 v[88:91], v[68:69], off
	global_load_dwordx4 v[84:87], v[68:69], off offset:256
	v_add_u32_e32 v96, 0xa0, v181
	v_mad_i64_i32 v[68:69], s[2:3], v96, s81, v[168:169]
	global_load_dwordx4 v[80:83], v[68:69], off
	global_load_dwordx4 v[76:79], v[68:69], off offset:256
	v_add_u32_e32 v93, 0xb0, v181
	v_mad_i64_i32 v[68:69], s[2:3], v93, s81, v[168:169]
	global_load_dwordx4 v[72:75], v[68:69], off
	s_nop 0
	global_load_dwordx4 v[68:71], v[68:69], off offset:256
	v_readlane_b32 s2, v254, 23
	v_readlane_b32 s3, v254, 24
	v_cmp_lt_i32_e32 vcc, 0, v3
	s_waitcnt vmcnt(7)
	v_lshlrev_b32_e32 v108, 16, v98
	v_and_b32_e32 v109, 0xffff0000, v98
	v_lshlrev_b32_e32 v98, 16, v99
	v_and_b32_e32 v99, 0xffff0000, v99
	v_fma_f32 v58, v58, 0.5, v98
	v_fma_f32 v59, v59, 0.5, v99
	v_lshlrev_b32_e32 v98, 16, v100
	v_and_b32_e32 v99, 0xffff0000, v100
	v_mov_b64_e32 v[94:95], s[2:3]
	v_fma_f32 v98, v52, 0.5, v98
	v_fma_f32 v99, v53, 0.5, v99
	v_lshlrev_b32_e32 v52, 16, v101
	v_and_b32_e32 v53, 0xffff0000, v101
	v_mad_i64_i32 v[106:107], s[2:3], v97, s81, v[94:95]
	v_fma_f32 v56, v56, 0.5, v108
	v_fma_f32 v57, v57, 0.5, v109
	v_fma_f32 v100, v54, 0.5, v52
	v_fma_f32 v101, v55, 0.5, v53
	v_lshl_add_u64 v[106:107], v[106:107], 0, v[166:167]
	v_cvt_pk_bf16_f32 v52, v56, v57
	v_cvt_pk_bf16_f32 v53, v58, v59
	v_cvt_pk_bf16_f32 v54, v98, v99
	v_cvt_pk_bf16_f32 v55, v100, v101
	global_store_dwordx4 v[106:107], v[52:55], off
	v_mul_f32_e64 v108, v56, v56
	v_mul_f32_e64 v109, v57, v57
	v_mul_f32_e64 v110, v58, v58
	v_mul_f32_e64 v111, v59, v59
	s_waitcnt vmcnt(7)
	v_lshlrev_b32_e32 v52, 16, v102
	v_and_b32_e32 v53, 0xffff0000, v102
	v_lshlrev_b32_e32 v54, 16, v103
	v_and_b32_e32 v55, 0xffff0000, v103
	v_fma_f32 v52, v64, 0.5, v52
	v_fma_f32 v53, v65, 0.5, v53
	v_fma_f32 v54, v66, 0.5, v54
	v_fma_f32 v55, v67, 0.5, v55
	v_lshlrev_b32_e32 v56, 16, v104
	v_and_b32_e32 v57, 0xffff0000, v104
	v_lshlrev_b32_e32 v58, 16, v105
	v_and_b32_e32 v59, 0xffff0000, v105
	v_fma_f32 v56, v60, 0.5, v56
	v_fma_f32 v57, v61, 0.5, v57
	v_fma_f32 v58, v62, 0.5, v58
	v_fma_f32 v59, v63, 0.5, v59
	v_mul_f32_e64 v60, v52, v52
	v_mul_f32_e64 v61, v53, v53
	v_mul_f32_e64 v62, v54, v54
	v_mul_f32_e64 v63, v55, v55
	v_mul_f32_e64 v112, v98, v98
	v_mul_f32_e64 v113, v99, v99
	v_mul_f32_e64 v114, v100, v100
	v_mul_f32_e64 v115, v101, v101
	v_add_f32_e32 v62, v62, v63
	v_add_f32_e32 v60, v60, v61
	v_mul_f32_e64 v64, v56, v56
	v_mul_f32_e64 v65, v57, v57
	v_mul_f32_e64 v66, v58, v58
	v_mul_f32_e64 v67, v59, v59
	v_add_f32_e32 v60, v60, v62
	v_add_f32_e32 v61, v114, v115
	v_add_f32_e32 v62, v112, v113
	v_add_f32_e32 v66, v66, v67
	v_add_f32_e32 v64, v64, v65
	v_add_f32_e32 v61, v62, v61
	v_add_f32_e32 v62, v110, v111
	v_add_f32_e32 v63, v108, v109
	v_add_f32_e32 v64, v64, v66
	v_add_f32_e32 v62, v63, v62
	v_add_f32_e32 v60, v60, v64
	v_add_f32_e32 v61, v62, v61
	v_add_f32_e32 v60, v61, v60
	v_cvt_pk_bf16_f32 v52, v52, v53
	v_cvt_pk_bf16_f32 v53, v54, v55
	v_cvt_pk_bf16_f32 v54, v56, v57
	v_cvt_pk_bf16_f32 v55, v58, v59
	global_store_dwordx4 v[106:107], v[52:55], off offset:256
	ds_bpermute_b32 v52, v180, v60
	s_waitcnt vmcnt(7)
	v_lshlrev_b32_e32 v56, 16, v88
	v_and_b32_e32 v57, 0xffff0000, v88
	v_fma_f32 v48, v48, 0.5, v56
	v_fma_f32 v49, v49, 0.5, v57
	v_lshlrev_b32_e32 v56, 16, v89
	v_and_b32_e32 v57, 0xffff0000, v89
	v_fma_f32 v50, v50, 0.5, v56
	v_fma_f32 v51, v51, 0.5, v57
	v_lshlrev_b32_e32 v56, 16, v90
	v_and_b32_e32 v57, 0xffff0000, v90
	v_fma_f32 v56, v44, 0.5, v56
	v_fma_f32 v57, v45, 0.5, v57
	v_lshlrev_b32_e32 v44, 16, v91
	v_and_b32_e32 v45, 0xffff0000, v91
	s_waitcnt lgkmcnt(0)
	v_add_f32_e32 v54, v60, v52
	v_mad_i64_i32 v[52:53], s[2:3], v116, s81, v[94:95]
	v_fma_f32 v58, v46, 0.5, v44
	v_fma_f32 v59, v47, 0.5, v45
	v_lshl_add_u64 v[52:53], v[52:53], 0, v[166:167]
	v_cvt_pk_bf16_f32 v44, v48, v49
	v_cvt_pk_bf16_f32 v45, v50, v51
	v_cvt_pk_bf16_f32 v46, v56, v57
	v_cvt_pk_bf16_f32 v47, v58, v59
	global_store_dwordx4 v[52:53], v[44:47], off
	v_mul_f32_e64 v64, v56, v56
	v_mul_f32_e64 v65, v57, v57
	v_mul_f32_e64 v66, v58, v58
	v_mul_f32_e64 v67, v59, v59
	s_waitcnt vmcnt(7)
	v_lshlrev_b32_e32 v44, 16, v84
	v_and_b32_e32 v45, 0xffff0000, v84
	v_fma_f32 v40, v40, 0.5, v44
	v_fma_f32 v41, v41, 0.5, v45
	v_lshlrev_b32_e32 v44, 16, v85
	v_and_b32_e32 v45, 0xffff0000, v85
	v_fma_f32 v42, v42, 0.5, v44
	v_fma_f32 v43, v43, 0.5, v45
	v_lshlrev_b32_e32 v44, 16, v86
	v_and_b32_e32 v45, 0xffff0000, v86
	v_fma_f32 v44, v36, 0.5, v44
	v_fma_f32 v45, v37, 0.5, v45
	v_lshlrev_b32_e32 v36, 16, v87
	v_and_b32_e32 v37, 0xffff0000, v87
	v_fma_f32 v46, v38, 0.5, v36
	v_fma_f32 v47, v39, 0.5, v37
	v_mul_f32_e64 v36, v40, v40
	v_mul_f32_e64 v37, v41, v41
	v_mul_f32_e64 v38, v42, v42
	v_mul_f32_e64 v39, v43, v43
	v_add_f32_e32 v36, v36, v37
	v_add_f32_e32 v38, v38, v39
	v_mul_f32_e64 v60, v48, v48
	v_mul_f32_e64 v61, v49, v49
	v_mul_f32_e64 v62, v50, v50
	v_mul_f32_e64 v63, v51, v51
	v_mul_f32_e64 v48, v44, v44
	v_mul_f32_e64 v49, v45, v45
	v_mul_f32_e64 v50, v46, v46
	v_mul_f32_e64 v51, v47, v47
	v_add_f32_e32 v36, v36, v38
	v_add_f32_e32 v37, v66, v67
	v_add_f32_e32 v38, v64, v65
	v_add_f32_e32 v50, v50, v51
	v_add_f32_e32 v48, v48, v49
	v_add_f32_e32 v37, v38, v37
	v_add_f32_e32 v38, v62, v63
	v_add_f32_e32 v39, v60, v61
	v_add_f32_e32 v48, v48, v50
	v_add_f32_e32 v38, v39, v38
	v_add_f32_e32 v36, v36, v48
	v_add_f32_e32 v37, v38, v37
	v_add_f32_e32 v48, v37, v36
	v_cvt_pk_bf16_f32 v36, v40, v41
	s_waitcnt vmcnt(6)
; __device__ __forceinline__ unsigned cvt_pk_bf16(float lo, float hi) { f32x2_c v = {lo, hi}; bf16x2_c b = __builtin_convertvector(v, bf16x2_c); return __builtin_bit_cast(unsigned, b); }
; __device__ __forceinline__ float bf_lo(unsigned u) { return __uint_as_float(u << 16); }
; __device__ __forceinline__ float bf_hi(unsigned u) { return __uint_as_float(u & 0xffff0000u); }
;     __device__ __forceinline__ void operator()(const f32x4 (&acc)[2][2][4][2], const Unit& u, int wr, int wc, int fr, int fq) const {
;     ...
;             for (int m = 0; m < 4; ++m) { const int row = row0 + ai * HALF + m * 16; bf16_t* hp = Hx + (size_t)row * LDT + col0;
;                 float ss = 0.f;
; #pragma unroll
;                 for (int bj = 0; bj < 2; ++bj) { const u32x4 x = xv[m][bj]; const f32x4 a0 = acc[ai][bj][m][0], a1 = acc[ai][bj][m][1];
;                     const float y0 = bf_lo(x.x) + a0[0] * scale, y1 = bf_hi(x.x) + a0[1] * scale, y2 = bf_lo(x.y) + a0[2] * scale, y3 = bf_hi(x.y) + a0[3] * scale;
;                     const float y4 = bf_lo(x.z) + a1[0] * scale, y5 = bf_hi(x.z) + a1[1] * scale, y6 = bf_lo(x.w) + a1[2] * scale, y7 = bf_hi(x.w) + a1[3] * scale;
;                     ss += ((y0 * y0 + y1 * y1) + (y2 * y2 + y3 * y3)) + ((y4 * y4 + y5 * y5) + (y6 * y6 + y7 * y7));
;                     u32x4 w; w.x = cvt_pk_bf16(y0, y1); w.y = cvt_pk_bf16(y2, y3); w.z = cvt_pk_bf16(y4, y5); w.w = cvt_pk_bf16(y6, y7);
;                     *(u32x4*)(hp + bj * HALF) = w; }
;                 ss += __shfl_xor(ss, 16); ss += __shfl_xor(ss, 32); ssm[m] = ss; }
;             { const float sv = (fq == 0) ? ssm[0] : (fq == 1) ? ssm[1] : (fq == 2) ? ssm[2] : ssm[3];
	v_lshlrev_b32_e32 v40, 16, v80
	v_and_b32_e32 v41, 0xffff0000, v80
	v_fma_f32 v32, v32, 0.5, v40
	v_fma_f32 v33, v33, 0.5, v41
	v_lshlrev_b32_e32 v40, 16, v81
	v_and_b32_e32 v41, 0xffff0000, v81
	v_fma_f32 v34, v34, 0.5, v40
	v_fma_f32 v35, v35, 0.5, v41
	v_lshlrev_b32_e32 v40, 16, v82
	v_and_b32_e32 v41, 0xffff0000, v82
	v_cvt_pk_bf16_f32 v37, v42, v43
	v_cvt_pk_bf16_f32 v38, v44, v45
	v_cvt_pk_bf16_f32 v39, v46, v47
	v_fma_f32 v40, v28, 0.5, v40
	v_fma_f32 v41, v29, 0.5, v41
	v_lshlrev_b32_e32 v28, 16, v83
	v_and_b32_e32 v29, 0xffff0000, v83
	global_store_dwordx4 v[52:53], v[36:39], off offset:256
	v_fma_f32 v42, v30, 0.5, v28
	v_fma_f32 v43, v31, 0.5, v29
	v_cvt_pk_bf16_f32 v28, v32, v33
	v_mad_i64_i32 v[38:39], s[2:3], v96, s81, v[94:95]
	v_lshl_add_u64 v[38:39], v[38:39], 0, v[166:167]
	v_cvt_pk_bf16_f32 v29, v34, v35
	v_cvt_pk_bf16_f32 v30, v40, v41
	v_cvt_pk_bf16_f32 v31, v42, v43
	ds_bpermute_b32 v36, v180, v48
	global_store_dwordx4 v[38:39], v[28:31], off
	v_mul_f32_e64 v50, v42, v42
	v_mul_f32_e64 v51, v43, v43
	v_mul_f32_e64 v44, v32, v32
	v_mul_f32_e64 v45, v33, v33
	s_waitcnt vmcnt(7)
	v_lshlrev_b32_e32 v28, 16, v76
	v_and_b32_e32 v29, 0xffff0000, v76
	v_fma_f32 v24, v24, 0.5, v28
	v_fma_f32 v25, v25, 0.5, v29
	v_lshlrev_b32_e32 v28, 16, v77
	v_and_b32_e32 v29, 0xffff0000, v77
	v_fma_f32 v26, v26, 0.5, v28
	v_fma_f32 v27, v27, 0.5, v29
	v_lshlrev_b32_e32 v28, 16, v78
	v_and_b32_e32 v29, 0xffff0000, v78
	v_fma_f32 v28, v20, 0.5, v28
	v_fma_f32 v29, v21, 0.5, v29
	v_lshlrev_b32_e32 v20, 16, v79
	v_and_b32_e32 v21, 0xffff0000, v79
	v_fma_f32 v30, v22, 0.5, v20
	v_fma_f32 v31, v23, 0.5, v21
	v_mul_f32_e64 v20, v24, v24
	v_mul_f32_e64 v21, v25, v25
	v_mul_f32_e64 v22, v26, v26
	v_mul_f32_e64 v23, v27, v27
	s_waitcnt lgkmcnt(0)
	v_add_f32_e32 v36, v48, v36
	v_mul_f32_e64 v48, v40, v40
	v_mul_f32_e64 v49, v41, v41
	v_add_f32_e32 v22, v22, v23
	v_add_f32_e32 v20, v20, v21
	v_mul_f32_e64 v46, v34, v34
	v_mul_f32_e64 v47, v35, v35
	v_mul_f32_e64 v32, v28, v28
	v_mul_f32_e64 v33, v29, v29
	v_mul_f32_e64 v34, v30, v30
	v_mul_f32_e64 v35, v31, v31
	v_add_f32_e32 v20, v20, v22
	v_add_f32_e32 v21, v50, v51
	v_add_f32_e32 v22, v48, v49
	v_add_f32_e32 v34, v34, v35
	v_add_f32_e32 v32, v32, v33
	v_add_f32_e32 v21, v22, v21
	v_add_f32_e32 v22, v46, v47
	v_add_f32_e32 v23, v44, v45
	v_add_f32_e32 v32, v32, v34
	v_add_f32_e32 v22, v23, v22
	v_add_f32_e32 v20, v20, v32
	v_add_f32_e32 v21, v22, v21
	v_add_f32_e32 v32, v21, v20
	v_cvt_pk_bf16_f32 v20, v24, v25
	s_waitcnt vmcnt(6)
	v_lshlrev_b32_e32 v24, 16, v72
	v_and_b32_e32 v25, 0xffff0000, v72
	v_fma_f32 v16, v16, 0.5, v24
	v_fma_f32 v17, v17, 0.5, v25
	v_lshlrev_b32_e32 v24, 16, v73
	v_and_b32_e32 v25, 0xffff0000, v73
	v_fma_f32 v18, v18, 0.5, v24
	v_fma_f32 v19, v19, 0.5, v25
	v_lshlrev_b32_e32 v24, 16, v74
	v_and_b32_e32 v25, 0xffff0000, v74
	v_cvt_pk_bf16_f32 v21, v26, v27
	v_cvt_pk_bf16_f32 v22, v28, v29
	v_cvt_pk_bf16_f32 v23, v30, v31
	v_fma_f32 v24, v12, 0.5, v24
	v_fma_f32 v25, v13, 0.5, v25
	v_lshlrev_b32_e32 v12, 16, v75
	v_and_b32_e32 v13, 0xffff0000, v75
	global_store_dwordx4 v[38:39], v[20:23], off offset:256
	v_fma_f32 v26, v14, 0.5, v12
	v_fma_f32 v27, v15, 0.5, v13
	v_cvt_pk_bf16_f32 v12, v16, v17
	v_mad_i64_i32 v[22:23], s[2:3], v93, s81, v[94:95]
	v_lshl_add_u64 v[22:23], v[22:23], 0, v[166:167]
	v_cvt_pk_bf16_f32 v13, v18, v19
	v_cvt_pk_bf16_f32 v14, v24, v25
	v_cvt_pk_bf16_f32 v15, v26, v27
	ds_bpermute_b32 v20, v180, v32
	global_store_dwordx4 v[22:23], v[12:15], off
	v_mul_f32_e64 v34, v26, v26
	v_mul_f32_e64 v35, v27, v27
	v_mul_f32_e64 v28, v16, v16
	v_mul_f32_e64 v29, v17, v17
	s_waitcnt vmcnt(7)
	v_lshlrev_b32_e32 v12, 16, v68
	v_and_b32_e32 v13, 0xffff0000, v68
	v_fma_f32 v8, v8, 0.5, v12
	v_fma_f32 v9, v9, 0.5, v13
	v_lshlrev_b32_e32 v12, 16, v69
	v_and_b32_e32 v13, 0xffff0000, v69
	v_fma_f32 v10, v10, 0.5, v12
	v_fma_f32 v11, v11, 0.5, v13
	v_lshlrev_b32_e32 v12, 16, v70
	v_and_b32_e32 v13, 0xffff0000, v70
	v_fma_f32 v12, v4, 0.5, v12
	v_fma_f32 v13, v5, 0.5, v13
	v_lshlrev_b32_e32 v4, 16, v71
	v_and_b32_e32 v5, 0xffff0000, v71
	v_fma_f32 v14, v6, 0.5, v4
	v_fma_f32 v15, v7, 0.5, v5
	v_mul_f32_e64 v4, v8, v8
	v_mul_f32_e64 v5, v9, v9
	v_mul_f32_e64 v6, v10, v10
	v_mul_f32_e64 v7, v11, v11
	s_waitcnt lgkmcnt(0)
	v_add_f32_e32 v20, v32, v20
	v_mul_f32_e64 v32, v24, v24
	v_mul_f32_e64 v33, v25, v25
	v_add_f32_e32 v6, v6, v7
	v_add_f32_e32 v4, v4, v5
	v_mul_f32_e64 v30, v18, v18
	v_mul_f32_e64 v31, v19, v19
	v_mul_f32_e64 v16, v12, v12
	v_mul_f32_e64 v17, v13, v13
	v_mul_f32_e64 v18, v14, v14
	v_mul_f32_e64 v19, v15, v15
	v_add_f32_e32 v4, v4, v6
	v_add_f32_e32 v5, v34, v35
	v_add_f32_e32 v6, v32, v33
	v_add_f32_e32 v18, v18, v19
	v_add_f32_e32 v16, v16, v17
	v_add_f32_e32 v5, v6, v5
	v_add_f32_e32 v6, v30, v31
	v_add_f32_e32 v7, v28, v29
	v_add_f32_e32 v16, v16, v18
	v_add_f32_e32 v6, v7, v6
	v_add_f32_e32 v4, v4, v16
	v_add_f32_e32 v5, v6, v5
	v_add_f32_e32 v16, v5, v4
	v_cvt_pk_bf16_f32 v4, v8, v9
	v_cvt_pk_bf16_f32 v5, v10, v11
	v_cvt_pk_bf16_f32 v6, v12, v13
	v_cvt_pk_bf16_f32 v7, v14, v15
	global_store_dwordx4 v[22:23], v[4:7], off offset:256
	ds_bpermute_b32 v4, v180, v16
	ds_bpermute_b32 v55, v179, v54
	ds_bpermute_b32 v37, v179, v36
	ds_bpermute_b32 v21, v179, v20
	s_waitcnt lgkmcnt(3)
	v_add_f32_e32 v5, v16, v4
	ds_bpermute_b32 v6, v179, v5
	s_and_saveexec_b64 s[2:3], vcc
	s_xor_b64 s[4:5], exec, s[2:3]
	s_cbranch_execz .LBB0_250
	v_cmp_ne_u32_e32 vcc, 1, v3
	s_and_saveexec_b64 s[2:3], vcc
	s_xor_b64 s[26:27], exec, s[2:3]
	s_cbranch_execz .LBB0_247
	s_waitcnt lgkmcnt(0)
	v_add_f32_e32 v4, v5, v6
	v_add_f32_e32 v5, v20, v21
	v_cndmask_b32_e64 v4, v4, v5, s[6:7]

; __device__ __forceinline__ unsigned cvt_pk_bf16(float lo, float hi) { f32x2_c v = {lo, hi}; bf16x2_c b = __builtin_convertvector(v, bf16x2_c); return __builtin_bit_cast(unsigned, b); }
;     template <int TT> __device__ __forceinline__ void other(const f32x4 (&acc)[2][2][4][2], bf16_t* base, int row0, int col0, PG8_LAS float* my, int t, int hh, int wc, int fq) const {
;     ...
;             for (int m = 0; m < 4; ++m) { bf16_t* rowp = base + (size_t)(row0 + ai * HALF + m * 16) * LDT + col0;
;                 const float rs = my[(ai * 4 + m) * 16]; float ps = 0.f, pq = 0.f; u32x4 gq = {0u, 0u, 0u, 0u};
; #pragma unroll
;                 for (int bj = 0; bj < 2; ++bj) { f32x4 v0 = acc[ai][bj][m][0] * rs + bv[bj][0], v1 = acc[ai][bj][m][1] * rs + bv[bj][1];
;                     if (TT == 3) {
; #pragma unroll
;                         for (int j = 0; j < 4; ++j) { v0[j] = silu_f(v0[j]); v1[j] = silu_f(v1[j]); } }
;                     else if (TT == 4 || TT == 5) { f32x2 a = gelu_pk((f32x2){v0[0], v0[1]}), b = gelu_pk((f32x2){v0[2], v0[3]}), c = gelu_pk((f32x2){v1[0], v1[1]}), d = gelu_pk((f32x2){v1[2], v1[3]});
;                         v0 = (f32x4){a.x, a.y, b.x, b.y}; v1 = (f32x4){c.x, c.y, d.x, d.y};
;                         if (TT == 5) { ps += ((v0[0] + v0[1]) + (v0[2] + v0[3])) + ((v1[0] + v1[1]) + (v1[2] + v1[3]));
;                             pq += ((v0[0] * v0[0] + v0[1] * v0[1]) + (v0[2] * v0[2] + v0[3] * v0[3])) + ((v1[0] * v1[0] + v1[1] * v1[1]) + (v1[2] * v1[2] + v1[3] * v1[3])); } }
;                     else if (TT >= 6) {
; #pragma unroll
;                         for (int j = 0; j < 4; ++j) { v0[j] = sigmoid_f(v0[j]); v1[j] = sigmoid_f(v1[j]); } }
;                     if (TT >= 6) { unsigned b0 = 0u, b1 = 0u;
; #pragma unroll
;                         for (int j = 0; j < 4; ++j) { b0 = __builtin_amdgcn_cvt_pk_u8_f32(__builtin_rintf(v0[j] * 255.0f), j, b0); b1 = __builtin_amdgcn_cvt_pk_u8_f32(__builtin_rintf(v1[j] * 255.0f), j, b1); }
;                         if (bj == 0) { gq.x = b0; gq.y = b1; } else { gq.z = b0; gq.w = b1; } }
;                     else { u32x4 w; w.x = cvt_pk_bf16(v0[0], v0[1]); w.y = cvt_pk_bf16(v0[2], v0[3]); w.z = cvt_pk_bf16(v1[0], v1[1]); w.w = cvt_pk_bf16(v1[2], v1[3]);
;                         *(u32x4*)(rowp + bj * HALF) = w; } }
.LBB0_348:
	s_bfe_u32 s45, s44, 0x30003
	s_cmp_lt_i32 s45, 2
	s_cbranch_scc1 .LBB0_357
	s_cmp_gt_i32 s45, 6
	s_cbranch_scc0 .LBB0_351
	v_mov_b32_e32 v132, v158
	v_mov_b32_e32 v146, v174
	s_waitcnt lgkmcnt(0)
	v_mov_b32_e32 v133, v3
	ds_read2_b32 v[138:139], v199 offset1:16
	v_ashrrev_i32_e32 v133, 31, v132
	v_lshl_add_u64 v[132:133], v[132:133], 1, s[28:29]
	v_mad_i64_i32 v[140:141], s[4:5], v146, s81, v[132:133]
	s_waitcnt lgkmcnt(0)
	v_fma_f32 v136, v122, v138, 0
	v_fma_f32 v137, v123, v138, 0
	v_fma_f32 v134, v120, v138, 0
	v_fma_f32 v135, v121, v138, 0
	v_fma_f32 v142, v118, v138, 0
	v_fma_f32 v143, v119, v138, 0
	v_fma_f32 v144, v116, v138, 0
	v_fma_f32 v145, v117, v138, 0
	v_cvt_pk_bf16_f32 v134, v134, v135
	v_cvt_pk_bf16_f32 v135, v136, v137
	v_cvt_pk_bf16_f32 v136, v144, v145
	v_cvt_pk_bf16_f32 v137, v142, v143
	global_store_dwordx4 v[140:141], v[134:137], off
	v_fma_f32 v142, v126, v138, 0
	v_fma_f32 v143, v127, v138, 0
	v_fma_f32 v144, v124, v138, 0
	v_fma_f32 v145, v125, v138, 0
	v_fma_f32 v136, v130, v138, 0
	v_fma_f32 v137, v131, v138, 0
	v_fma_f32 v134, v128, v138, 0
	v_fma_f32 v135, v129, v138, 0
	v_mov_b32_e32 v138, v139
	v_cvt_pk_bf16_f32 v134, v134, v135
	v_cvt_pk_bf16_f32 v135, v136, v137
	v_cvt_pk_bf16_f32 v136, v144, v145
	v_cvt_pk_bf16_f32 v137, v142, v143
	global_store_dwordx4 v[140:141], v[134:137], off offset:256
	v_fma_f32 v142, v102, v138, 0
	v_fma_f32 v143, v103, v138, 0
	v_fma_f32 v144, v100, v138, 0
	v_fma_f32 v145, v101, v138, 0
	v_add_u32_e32 v134, 16, v146
	v_mad_i64_i32 v[140:141], s[4:5], v134, s81, v[132:133]
	v_fma_f32 v136, v106, v138, 0
	v_fma_f32 v137, v107, v138, 0
	v_fma_f32 v134, v104, v138, 0
	v_fma_f32 v135, v105, v138, 0
	s_nop 0
	v_cvt_pk_bf16_f32 v134, v134, v135
	v_cvt_pk_bf16_f32 v135, v136, v137
	v_cvt_pk_bf16_f32 v136, v144, v145
	v_cvt_pk_bf16_f32 v137, v142, v143
	global_store_dwordx4 v[140:141], v[134:137], off
	v_fma_f32 v142, v110, v138, 0
	v_fma_f32 v143, v111, v138, 0
	s_nop 0
	v_fma_f32 v136, v114, v138, 0
	v_fma_f32 v137, v115, v138, 0
	v_fma_f32 v134, v112, v138, 0
	v_fma_f32 v135, v113, v138, 0
	v_fma_f32 v139, v109, v138, 0
	v_fma_f32 v138, v108, v138, 0
	v_cvt_pk_bf16_f32 v134, v134, v135
	v_cvt_pk_bf16_f32 v135, v136, v137
	v_cvt_pk_bf16_f32 v136, v138, v139
	ds_read2_b32 v[138:139], v199 offset0:32 offset1:48
	v_cvt_pk_bf16_f32 v137, v142, v143
	global_store_dwordx4 v[140:141], v[134:137], off offset:256
	s_waitcnt lgkmcnt(0)
	v_fma_f32 v142, v86, v138, 0
	v_fma_f32 v143, v87, v138, 0
	v_add_u32_e32 v134, 32, v146
	v_mad_i64_i32 v[140:141], s[4:5], v134, s81, v[132:133]
	v_fma_f32 v136, v90, v138, 0
	v_fma_f32 v137, v91, v138, 0
	v_fma_f32 v134, v88, v138, 0
	v_fma_f32 v135, v89, v138, 0
	v_fma_f32 v144, v84, v138, 0
	v_fma_f32 v145, v85, v138, 0
	v_cvt_pk_bf16_f32 v134, v134, v135
	v_cvt_pk_bf16_f32 v135, v136, v137
	v_cvt_pk_bf16_f32 v136, v144, v145
	v_cvt_pk_bf16_f32 v137, v142, v143
	global_store_dwordx4 v[140:141], v[134:137], off
	v_fma_f32 v142, v94, v138, 0
	v_fma_f32 v143, v95, v138, 0
	v_fma_f32 v144, v92, v138, 0
	v_fma_f32 v145, v93, v138, 0
	v_fma_f32 v136, v98, v138, 0
	v_fma_f32 v137, v99, v138, 0
	v_fma_f32 v134, v96, v138, 0
	v_fma_f32 v135, v97, v138, 0
	v_mov_b32_e32 v138, v139
	v_cvt_pk_bf16_f32 v134, v134, v135
	v_cvt_pk_bf16_f32 v135, v136, v137
	v_cvt_pk_bf16_f32 v136, v144, v145
	v_cvt_pk_bf16_f32 v137, v142, v143
	global_store_dwordx4 v[140:141], v[134:137], off offset:256
	v_fma_f32 v142, v70, v138, 0
	v_fma_f32 v143, v71, v138, 0
	v_fma_f32 v144, v68, v138, 0
	v_fma_f32 v145, v69, v138, 0
	v_add_u32_e32 v134, 48, v146
	v_mad_i64_i32 v[140:141], s[4:5], v134, s81, v[132:133]
	v_fma_f32 v136, v74, v138, 0
	v_fma_f32 v137, v75, v138, 0
	v_fma_f32 v134, v72, v138, 0
	v_fma_f32 v135, v73, v138, 0
	s_nop 0
	v_cvt_pk_bf16_f32 v134, v134, v135
	v_cvt_pk_bf16_f32 v135, v136, v137
	v_cvt_pk_bf16_f32 v136, v144, v145
	v_cvt_pk_bf16_f32 v137, v142, v143
	global_store_dwordx4 v[140:141], v[134:137], off
	v_fma_f32 v142, v78, v138, 0
	v_fma_f32 v143, v79, v138, 0
	s_nop 0
	v_fma_f32 v136, v82, v138, 0
	v_fma_f32 v137, v83, v138, 0
	v_fma_f32 v134, v80, v138, 0
	v_fma_f32 v135, v81, v138, 0
	v_fma_f32 v139, v77, v138, 0
	v_fma_f32 v138, v76, v138, 0
	v_cvt_pk_bf16_f32 v134, v134, v135
	v_cvt_pk_bf16_f32 v135, v136, v137
	v_cvt_pk_bf16_f32 v136, v138, v139
	ds_read2_b32 v[138:139], v199 offset0:64 offset1:80
	v_cvt_pk_bf16_f32 v137, v142, v143
	global_store_dwordx4 v[140:141], v[134:137], off offset:256
	s_waitcnt lgkmcnt(0)
	v_fma_f32 v142, v54, v138, 0
	v_fma_f32 v143, v55, v138, 0
	v_add_u32_e32 v134, 0x80, v146
	v_mad_i64_i32 v[140:141], s[4:5], v134, s81, v[132:133]
	v_fma_f32 v136, v58, v138, 0
	v_fma_f32 v137, v59, v138, 0
	v_fma_f32 v134, v56, v138, 0
	v_fma_f32 v135, v57, v138, 0
	v_fma_f32 v144, v52, v138, 0
	v_fma_f32 v145, v53, v138, 0
	v_cvt_pk_bf16_f32 v134, v134, v135
	v_cvt_pk_bf16_f32 v135, v136, v137
	v_cvt_pk_bf16_f32 v136, v144, v145
	v_cvt_pk_bf16_f32 v137, v142, v143
	global_store_dwordx4 v[140:141], v[134:137], off
	v_fma_f32 v142, v62, v138, 0
	v_fma_f32 v143, v63, v138, 0
	v_fma_f32 v144, v60, v138, 0
	v_fma_f32 v145, v61, v138, 0
	v_fma_f32 v136, v66, v138, 0
	v_fma_f32 v137, v67, v138, 0
	v_fma_f32 v134, v64, v138, 0
	v_fma_f32 v135, v65, v138, 0
	v_mov_b32_e32 v138, v139
	v_cvt_pk_bf16_f32 v134, v134, v135
	v_cvt_pk_bf16_f32 v135, v136, v137
	v_cvt_pk_bf16_f32 v136, v144, v145
	v_cvt_pk_bf16_f32 v137, v142, v143
	global_store_dwordx4 v[140:141], v[134:137], off offset:256
	v_fma_f32 v142, v38, v138, 0
	v_fma_f32 v143, v39, v138, 0
	v_fma_f32 v144, v36, v138, 0
	v_fma_f32 v145, v37, v138, 0
	v_add_u32_e32 v134, 0x90, v146
	v_mad_i64_i32 v[140:141], s[4:5], v134, s81, v[132:133]
	v_fma_f32 v136, v42, v138, 0
	v_fma_f32 v137, v43, v138, 0
	v_fma_f32 v134, v40, v138, 0
	v_fma_f32 v135, v41, v138, 0
	s_nop 0
	v_cvt_pk_bf16_f32 v134, v134, v135
	v_cvt_pk_bf16_f32 v135, v136, v137
	v_cvt_pk_bf16_f32 v136, v144, v145
	v_cvt_pk_bf16_f32 v137, v142, v143
	global_store_dwordx4 v[140:141], v[134:137], off
	v_fma_f32 v142, v46, v138, 0
	v_fma_f32 v143, v47, v138, 0
	s_nop 0
	v_fma_f32 v136, v50, v138, 0
	v_fma_f32 v137, v51, v138, 0
	v_fma_f32 v134, v48, v138, 0
	v_fma_f32 v135, v49, v138, 0
	v_fma_f32 v139, v45, v138, 0
	v_fma_f32 v138, v44, v138, 0
	v_cvt_pk_bf16_f32 v134, v134, v135
	v_cvt_pk_bf16_f32 v135, v136, v137
	v_cvt_pk_bf16_f32 v136, v138, v139
	ds_read2_b32 v[138:139], v199 offset0:96 offset1:112
	v_cvt_pk_bf16_f32 v137, v142, v143
	global_store_dwordx4 v[140:141], v[134:137], off offset:256
	s_waitcnt lgkmcnt(0)
;     template <int TT> __device__ __forceinline__ void other(const f32x4 (&acc)[2][2][4][2], bf16_t* base, int row0, int col0, PG8_LAS float* my, int t, int hh, int wc, int fq) const {
;     ...
;             for (int n = 0; n < 2; ++n) bv[bj][n] = (TT >= 6) ? *(const f32x4*)(bgate + (t - 6) * 2048 + col0 + bj * HALF + 4 * n) : (f32x4){0.f, 0.f, 0.f, 0.f};
;         float psm = 0.f, pqm = 0.f;
; #pragma unroll
;         for (int ai = 0; ai < 2; ++ai)
; #pragma unroll
;             for (int m = 0; m < 4; ++m) { bf16_t* rowp = base + (size_t)(row0 + ai * HALF + m * 16) * LDT + col0;
;                 const float rs = my[(ai * 4 + m) * 16]; float ps = 0.f, pq = 0.f; u32x4 gq = {0u, 0u, 0u, 0u};
; #pragma unroll
;                 for (int bj = 0; bj < 2; ++bj) { f32x4 v0 = acc[ai][bj][m][0] * rs + bv[bj][0], v1 = acc[ai][bj][m][1] * rs + bv[bj][1];
;                     if (TT == 3) {
; #pragma unroll
;                         for (int j = 0; j < 4; ++j) { v0[j] = silu_f(v0[j]); v1[j] = silu_f(v1[j]); } }
;                     else if (TT == 4 || TT == 5) { f32x2 a = gelu_pk((f32x2){v0[0], v0[1]}), b = gelu_pk((f32x2){v0[2], v0[3]}), c = gelu_pk((f32x2){v1[0], v1[1]}), d = gelu_pk((f32x2){v1[2], v1[3]});
;                         v0 = (f32x4){a.x, a.y, b.x, b.y}; v1 = (f32x4){c.x, c.y, d.x, d.y};
;                         if (TT == 5) { ps += ((v0[0] + v0[1]) + (v0[2] + v0[3])) + ((v1[0] + v1[1]) + (v1[2] + v1[3]));
;                             pq += ((v0[0] * v0[0] + v0[1] * v0[1]) + (v0[2] * v0[2] + v0[3] * v0[3])) + ((v1[0] * v1[0] + v1[1] * v1[1]) + (v1[2] * v1[2] + v1[3] * v1[3])); } }
;                     else if (TT >= 6) {
; #pragma unroll
;                         for (int j = 0; j < 4; ++j) { v0[j] = sigmoid_f(v0[j]); v1[j] = sigmoid_f(v1[j]); } }
;                     if (TT >= 6) { unsigned b0 = 0u, b1 = 0u;
; #pragma unroll
;                         for (int j = 0; j < 4; ++j) { b0 = __builtin_amdgcn_cvt_pk_u8_f32(__builtin_rintf(v0[j] * 255.0f), j, b0); b1 = __builtin_amdgcn_cvt_pk_u8_f32(__builtin_rintf(v1[j] * 255.0f), j, b1); }
;                         if (bj == 0) { gq.x = b0; gq.y = b1; } else { gq.z = b0; gq.w = b1; } }
;                     else { u32x4 w; w.x = cvt_pk_bf16(v0[0], v0[1]); w.y = cvt_pk_bf16(v0[2], v0[3]); w.z = cvt_pk_bf16(v1[0], v1[1]); w.w = cvt_pk_bf16(v1[2], v1[3]);
	v_fma_f32 v142, v22, v138, 0
	v_fma_f32 v143, v23, v138, 0
	v_add_u32_e32 v134, 0xa0, v146
	v_mad_i64_i32 v[140:141], s[4:5], v134, s81, v[132:133]
	v_fma_f32 v136, v26, v138, 0
	v_fma_f32 v137, v27, v138, 0
	v_fma_f32 v134, v24, v138, 0
	v_fma_f32 v135, v25, v138, 0
	v_fma_f32 v144, v20, v138, 0
	v_fma_f32 v145, v21, v138, 0
	v_cvt_pk_bf16_f32 v134, v134, v135
	v_cvt_pk_bf16_f32 v135, v136, v137
	v_cvt_pk_bf16_f32 v136, v144, v145
	v_cvt_pk_bf16_f32 v137, v142, v143
	global_store_dwordx4 v[140:141], v[134:137], off
	v_fma_f32 v142, v30, v138, 0
	v_fma_f32 v143, v31, v138, 0
	v_fma_f32 v144, v28, v138, 0
	v_fma_f32 v145, v29, v138, 0
	v_fma_f32 v136, v34, v138, 0
	v_fma_f32 v137, v35, v138, 0
	v_fma_f32 v134, v32, v138, 0
	v_fma_f32 v135, v33, v138, 0
	v_mov_b32_e32 v138, v139
	v_cvt_pk_bf16_f32 v134, v134, v135
	v_cvt_pk_bf16_f32 v135, v136, v137
	v_cvt_pk_bf16_f32 v136, v144, v145
	v_cvt_pk_bf16_f32 v137, v142, v143
	global_store_dwordx4 v[140:141], v[134:137], off offset:256
	v_fma_f32 v140, v6, v138, 0
	v_fma_f32 v141, v7, v138, 0
	v_fma_f32 v142, v4, v138, 0
	v_fma_f32 v143, v5, v138, 0
	v_add_u32_e32 v134, 0xb0, v146
	v_mad_i64_i32 v[136:137], s[4:5], v134, s81, v[132:133]
	v_fma_f32 v134, v10, v138, 0
	v_fma_f32 v135, v11, v138, 0
	v_fma_f32 v132, v8, v138, 0
	v_fma_f32 v133, v9, v138, 0
	s_mov_b64 s[4:5], 0
	v_cvt_pk_bf16_f32 v132, v132, v133
	v_cvt_pk_bf16_f32 v133, v134, v135
	v_cvt_pk_bf16_f32 v134, v142, v143
	v_cvt_pk_bf16_f32 v135, v140, v141
	global_store_dwordx4 v[136:137], v[132:135], off
	v_fma_f32 v140, v14, v138, 0
	v_fma_f32 v141, v15, v138, 0
	s_nop 0
	v_fma_f32 v134, v18, v138, 0
	v_fma_f32 v135, v19, v138, 0
	v_fma_f32 v132, v16, v138, 0
	v_fma_f32 v133, v17, v138, 0
	v_fma_f32 v139, v13, v138, 0
	v_fma_f32 v138, v12, v138, 0
	v_cvt_pk_bf16_f32 v132, v132, v133
	v_cvt_pk_bf16_f32 v133, v134, v135
	v_cvt_pk_bf16_f32 v134, v138, v139
	v_cvt_pk_bf16_f32 v135, v140, v141
	global_store_dwordx4 v[136:137], v[132:135], off offset:256
.LBB0_351:
	s_andn2_b64 vcc, exec, s[4:5]
	s_cbranch_vccnz .LBB0_356
	s_cmp_lg_u32 s45, 2
	s_mov_b64 s[4:5], -1
	s_cbranch_scc0 .LBB0_354
	s_lshl_b32 s3, s3, 13
	v_mov_b32_e32 v148, v3
	v_mov_b32_e32 v132, v158
	v_mov_b32_e32 v159, v174
	s_add_u32 s4, s36, s3
	s_addc_u32 s5, s37, 0
	s_waitcnt lgkmcnt(0)
	v_ashrrev_i32_e32 v133, 31, v132
	v_lshl_add_u64 v[132:133], v[132:133], 2, s[4:5]
	s_mov_b32 s4, 0xffff4000
	s_mov_b32 s5, -1
	s_mov_b32 s3, 0xffff4000
	v_lshl_add_u64 v[136:137], v[132:133], 0, s[4:5]
	v_add_co_u32_e32 v132, vcc, s3, v132
	s_add_u32 s2, s28, s2
	s_nop 0
	v_addc_co_u32_e32 v133, vcc, -1, v133, vcc
	global_load_dwordx4 v[140:143], v[132:133], off
	global_load_dwordx4 v[144:147], v[136:137], off offset:16
	s_nop 0
	global_load_dwordx4 v[132:135], v[136:137], off offset:528
	s_nop 0
	global_load_dwordx4 v[136:139], v[136:137], off offset:512
	ds_read2_b32 v[154:155], v199 offset1:16
	v_lshl_add_u32 v148, v148, 4, s41
	s_addc_u32 s3, s29, 0
	v_ashrrev_i32_e32 v149, 31, v148
	v_lshl_add_u64 v[152:153], s[2:3], 0, v[148:149]
	s_movk_i32 s4, 0x840
	v_add_u32_e32 v176, 32, v159
	s_waitcnt vmcnt(0) lgkmcnt(0)
	v_fma_f32 v150, v120, v154, v140
	v_fma_f32 v151, v121, v154, v141
	s_nop 0
	v_mul_f32_e32 v150, 0xbfb8aa3b, v150
	v_fma_f32 v148, v122, v154, v142
	v_fma_f32 v149, v123, v154, v143
	v_fma_f32 v160, v116, v154, v144
	v_fma_f32 v161, v117, v154, v145
	v_exp_f32_e32 v150, v150
	v_mul_f32_e32 v151, 0xbfb8aa3b, v151
	v_mul_f32_e32 v160, 0xbfb8aa3b, v160
	v_exp_f32_e32 v151, v151
	v_mul_f32_e32 v148, 0xbfb8aa3b, v148
	v_fma_f32 v156, v118, v154, v146
	v_fma_f32 v157, v119, v154, v147
	v_exp_f32_e32 v160, v160
	v_mul_f32_e32 v161, 0xbfb8aa3b, v161
	v_exp_f32_e32 v148, v148
	v_mul_f32_e32 v149, 0xbfb8aa3b, v149
	v_exp_f32_e32 v161, v161
	v_mul_f32_e32 v156, 0xbfb8aa3b, v156
	v_exp_f32_e32 v149, v149
	v_add_f32_e32 v150, 1.0, v150
	v_exp_f32_e32 v156, v156
	v_mul_f32_e32 v157, 0xbfb8aa3b, v157
	v_rcp_f32_e32 v150, v150
	v_add_f32_e32 v151, 1.0, v151
	v_exp_f32_e32 v157, v157
	v_add_f32_e32 v160, 1.0, v160
	v_rcp_f32_e32 v151, v151
	v_add_f32_e32 v148, 1.0, v148
	v_rcp_f32_e32 v160, v160
	v_add_f32_e32 v161, 1.0, v161
	v_rcp_f32_e32 v148, v148
	v_add_f32_e32 v149, 1.0, v149
	v_rcp_f32_e32 v161, v161
	v_add_f32_e32 v156, 1.0, v156
	v_rcp_f32_e32 v149, v149
	v_rcp_f32_e32 v156, v156
	v_add_f32_e32 v157, 1.0, v157
	v_mul_f32_e32 v150, 0x437f0000, v150
	v_rcp_f32_e32 v157, v157
	v_rndne_f32_e32 v150, v150
	v_mul_f32_e32 v151, 0x437f0000, v151
	v_cvt_pk_u8_f32 v150, v150, 0, 0
	v_mul_f32_e32 v160, 0x437f0000, v160
	v_rndne_f32_e32 v151, v151
	v_mul_f32_e32 v148, 0x437f0000, v148
	v_rndne_f32_e32 v160, v160
	v_cvt_pk_u8_f32 v150, v151, 1, v150
	v_mul_f32_e32 v151, 0x437f0000, v161
	v_rndne_f32_e32 v148, v148
	v_mul_f32_e32 v149, 0x437f0000, v149
	v_cvt_pk_u8_f32 v160, v160, 0, 0
	v_rndne_f32_e32 v151, v151
	v_cvt_pk_u8_f32 v148, v148, 2, v150
	v_mul_f32_e32 v150, 0x437f0000, v156
	v_rndne_f32_e32 v149, v149
	v_cvt_pk_u8_f32 v151, v151, 1, v160
	v_rndne_f32_e32 v150, v150
	v_cvt_pk_u8_f32 v148, v149, 3, v148
	v_mul_f32_e32 v149, 0x437f0000, v157
	v_cvt_pk_u8_f32 v150, v150, 2, v151
	v_rndne_f32_e32 v149, v149
	v_fma_f32 v160, v128, v154, v136
	v_fma_f32 v161, v129, v154, v137
	v_cvt_pk_u8_f32 v149, v149, 3, v150
	v_fma_f32 v150, v130, v154, v138
	v_fma_f32 v151, v131, v154, v139
	v_fma_f32 v156, v126, v154, v134
	v_fma_f32 v157, v127, v154, v135
	v_fma_f32 v162, v124, v154, v132
	v_fma_f32 v163, v125, v154, v133
	v_mul_f32_e32 v154, 0xbfb8aa3b, v160
	v_exp_f32_e32 v154, v154
	v_mul_f32_e32 v161, 0xbfb8aa3b, v161
	v_mul_f32_e32 v160, 0xbfb8aa3b, v162
	v_exp_f32_e32 v161, v161
; __device__ __forceinline__ unsigned cvt_pk_bf16(float lo, float hi) { f32x2_c v = {lo, hi}; bf16x2_c b = __builtin_convertvector(v, bf16x2_c); return __builtin_bit_cast(unsigned, b); }
; __device__ __forceinline__ float silu_f(float g) { return g * __builtin_amdgcn_rcpf(1.0f + __builtin_amdgcn_exp2f(-1.44269504f * g)); }
;     template <int TT> __device__ __forceinline__ void other(const f32x4 (&acc)[2][2][4][2], bf16_t* base, int row0, int col0, PG8_LAS float* my, int t, int hh, int wc, int fq) const {
;     ...
;                 for (int bj = 0; bj < 2; ++bj) { f32x4 v0 = acc[ai][bj][m][0] * rs + bv[bj][0], v1 = acc[ai][bj][m][1] * rs + bv[bj][1];
;                     if (TT == 3) {
; #pragma unroll
;                         for (int j = 0; j < 4; ++j) { v0[j] = silu_f(v0[j]); v1[j] = silu_f(v1[j]); } }
;                     else if (TT == 4 || TT == 5) { f32x2 a = gelu_pk((f32x2){v0[0], v0[1]}), b = gelu_pk((f32x2){v0[2], v0[3]}), c = gelu_pk((f32x2){v1[0], v1[1]}), d = gelu_pk((f32x2){v1[2], v1[3]});
;                         v0 = (f32x4){a.x, a.y, b.x, b.y}; v1 = (f32x4){c.x, c.y, d.x, d.y};
;                         if (TT == 5) { ps += ((v0[0] + v0[1]) + (v0[2] + v0[3])) + ((v1[0] + v1[1]) + (v1[2] + v1[3]));
;                             pq += ((v0[0] * v0[0] + v0[1] * v0[1]) + (v0[2] * v0[2] + v0[3] * v0[3])) + ((v1[0] * v1[0] + v1[1] * v1[1]) + (v1[2] * v1[2] + v1[3] * v1[3])); } }
;                     else if (TT >= 6) {
; #pragma unroll
;                         for (int j = 0; j < 4; ++j) { v0[j] = sigmoid_f(v0[j]); v1[j] = sigmoid_f(v1[j]); } }
;                     if (TT >= 6) { unsigned b0 = 0u, b1 = 0u;
; #pragma unroll
;                         for (int j = 0; j < 4; ++j) { b0 = __builtin_amdgcn_cvt_pk_u8_f32(__builtin_rintf(v0[j] * 255.0f), j, b0); b1 = __builtin_amdgcn_cvt_pk_u8_f32(__builtin_rintf(v1[j] * 255.0f), j, b1); }
;                         if (bj == 0) { gq.x = b0; gq.y = b1; } else { gq.z = b0; gq.w = b1; } }
;                     else { u32x4 w; w.x = cvt_pk_bf16(v0[0], v0[1]); w.y = cvt_pk_bf16(v0[2], v0[3]); w.z = cvt_pk_bf16(v1[0], v1[1]); w.w = cvt_pk_bf16(v1[2], v1[3]);
;                         *(u32x4*)(rowp + bj * HALF) = w; } }
;                 if (TT >= 6) *(u32x4*)((unsigned char*)base + (size_t)(row0 + ai * HALF + m * 16) * GATE_PITCH + hh * 256 + (wc * 4 + fq) * 16) = gq;
	v_mul_f32_e32 v150, 0xbfb8aa3b, v150
	v_exp_f32_e32 v160, v160
	v_mul_f32_e32 v162, 0xbfb8aa3b, v163
	v_exp_f32_e32 v150, v150
	v_mul_f32_e32 v151, 0xbfb8aa3b, v151
	v_exp_f32_e32 v162, v162
	v_mul_f32_e32 v156, 0xbfb8aa3b, v156
	v_exp_f32_e32 v151, v151
	v_add_f32_e32 v154, 1.0, v154
	v_exp_f32_e32 v156, v156
	v_mul_f32_e32 v157, 0xbfb8aa3b, v157
	v_rcp_f32_e32 v154, v154
	v_add_f32_e32 v161, 1.0, v161
	v_exp_f32_e32 v157, v157
	v_add_f32_e32 v160, 1.0, v160
	v_rcp_f32_e32 v161, v161
	v_add_f32_e32 v150, 1.0, v150
	v_rcp_f32_e32 v160, v160
	v_add_f32_e32 v162, 1.0, v162
	v_rcp_f32_e32 v150, v150
	v_add_f32_e32 v151, 1.0, v151
	v_rcp_f32_e32 v162, v162
	v_add_f32_e32 v156, 1.0, v156
	v_rcp_f32_e32 v151, v151
	v_rcp_f32_e32 v156, v156
	v_add_f32_e32 v157, 1.0, v157
	v_mul_f32_e32 v154, 0x437f0000, v154
	v_rcp_f32_e32 v157, v157
	v_rndne_f32_e32 v154, v154
	v_mul_f32_e32 v161, 0x437f0000, v161
	v_cvt_pk_u8_f32 v154, v154, 0, 0
	v_mul_f32_e32 v160, 0x437f0000, v160
	v_rndne_f32_e32 v161, v161
	v_mul_f32_e32 v150, 0x437f0000, v150
	v_rndne_f32_e32 v160, v160
	v_cvt_pk_u8_f32 v154, v161, 1, v154
	v_mul_f32_e32 v161, 0x437f0000, v162
	v_rndne_f32_e32 v150, v150
	v_mul_f32_e32 v151, 0x437f0000, v151
	v_cvt_pk_u8_f32 v160, v160, 0, 0
	v_rndne_f32_e32 v161, v161
	v_cvt_pk_u8_f32 v150, v150, 2, v154
	v_mul_f32_e32 v154, 0x437f0000, v156
	v_rndne_f32_e32 v151, v151
	v_cvt_pk_u8_f32 v160, v161, 1, v160
	v_rndne_f32_e32 v154, v154
	v_cvt_pk_u8_f32 v150, v151, 3, v150
	v_mul_f32_e32 v151, 0x437f0000, v157
	v_cvt_pk_u8_f32 v154, v154, 2, v160
	v_rndne_f32_e32 v151, v151
	v_cvt_pk_u8_f32 v151, v151, 3, v154
	v_mad_i64_i32 v[156:157], s[2:3], v159, s4, v[152:153]
	global_store_dwordx4 v[156:157], v[148:151], off
	v_add_u32_e32 v162, 16, v159
	s_nop 0
	v_mov_b32_e32 v150, v155
	v_fma_f32 v154, v104, v150, v140
	v_fma_f32 v155, v105, v150, v141
	v_fma_f32 v148, v106, v150, v142
	v_fma_f32 v149, v107, v150, v143
	v_fma_f32 v156, v102, v150, v146
	v_fma_f32 v157, v103, v150, v147
	v_fma_f32 v160, v100, v150, v144
	v_fma_f32 v161, v101, v150, v145
	v_mul_f32_e32 v151, 0xbfb8aa3b, v154
	v_exp_f32_e32 v151, v151
	v_mul_f32_e32 v155, 0xbfb8aa3b, v155
	v_mul_f32_e32 v154, 0xbfb8aa3b, v160
	v_exp_f32_e32 v155, v155
	v_mul_f32_e32 v148, 0xbfb8aa3b, v148
	v_exp_f32_e32 v154, v154
	v_mul_f32_e32 v160, 0xbfb8aa3b, v161
	v_exp_f32_e32 v148, v148
	v_mul_f32_e32 v149, 0xbfb8aa3b, v149
	v_exp_f32_e32 v160, v160
	v_mul_f32_e32 v156, 0xbfb8aa3b, v156
	v_exp_f32_e32 v149, v149
	v_add_f32_e32 v151, 1.0, v151
	v_exp_f32_e32 v156, v156
	v_mul_f32_e32 v157, 0xbfb8aa3b, v157
	v_rcp_f32_e32 v151, v151
	v_add_f32_e32 v155, 1.0, v155
	v_exp_f32_e32 v157, v157
	v_add_f32_e32 v154, 1.0, v154
	v_rcp_f32_e32 v155, v155
	v_add_f32_e32 v148, 1.0, v148
	v_rcp_f32_e32 v154, v154
	v_add_f32_e32 v160, 1.0, v160
	v_rcp_f32_e32 v148, v148
	v_add_f32_e32 v149, 1.0, v149
	v_rcp_f32_e32 v160, v160
	v_add_f32_e32 v156, 1.0, v156
	v_rcp_f32_e32 v149, v149
	v_rcp_f32_e32 v156, v156
	v_add_f32_e32 v157, 1.0, v157
	v_mul_f32_e32 v151, 0x437f0000, v151
	v_rcp_f32_e32 v157, v157
	v_rndne_f32_e32 v151, v151
	v_mul_f32_e32 v155, 0x437f0000, v155
	v_cvt_pk_u8_f32 v151, v151, 0, 0
	v_mul_f32_e32 v154, 0x437f0000, v154
	v_rndne_f32_e32 v155, v155
	v_mul_f32_e32 v148, 0x437f0000, v148
	v_rndne_f32_e32 v154, v154
	v_cvt_pk_u8_f32 v151, v155, 1, v151
	v_mul_f32_e32 v155, 0x437f0000, v160
	v_rndne_f32_e32 v148, v148
	v_mul_f32_e32 v149, 0x437f0000, v149
	v_cvt_pk_u8_f32 v154, v154, 0, 0
	v_rndne_f32_e32 v155, v155
	v_cvt_pk_u8_f32 v148, v148, 2, v151
	v_mul_f32_e32 v151, 0x437f0000, v156
	v_rndne_f32_e32 v149, v149
	v_cvt_pk_u8_f32 v154, v155, 1, v154
	v_rndne_f32_e32 v151, v151
	v_cvt_pk_u8_f32 v148, v149, 3, v148
	v_mul_f32_e32 v149, 0x437f0000, v157
	v_cvt_pk_u8_f32 v151, v151, 2, v154
	v_rndne_f32_e32 v149, v149
	v_cvt_pk_u8_f32 v149, v149, 3, v151
	v_fma_f32 v154, v114, v150, v138
	v_fma_f32 v155, v115, v150, v139
	v_fma_f32 v156, v112, v150, v136
	v_fma_f32 v157, v113, v150, v137
	v_fma_f32 v160, v110, v150, v134
	v_fma_f32 v161, v111, v150, v135
	v_fma_f32 v151, v109, v150, v133
	v_fma_f32 v150, v108, v150, v132
	v_mul_f32_e32 v156, 0xbfb8aa3b, v156
	v_mul_f32_e32 v150, 0xbfb8aa3b, v150
	v_exp_f32_e32 v150, v150
	v_mul_f32_e32 v151, 0xbfb8aa3b, v151
	v_exp_f32_e32 v151, v151
	v_exp_f32_e32 v156, v156
	v_mul_f32_e32 v157, 0xbfb8aa3b, v157
	v_mul_f32_e32 v154, 0xbfb8aa3b, v154
	v_mul_f32_e32 v160, 0xbfb8aa3b, v160
	v_exp_f32_e32 v157, v157
	v_exp_f32_e32 v154, v154
	v_exp_f32_e32 v160, v160
	v_add_f32_e32 v150, 1.0, v150
	v_mul_f32_e32 v155, 0xbfb8aa3b, v155
	v_rcp_f32_e32 v150, v150
	v_add_f32_e32 v151, 1.0, v151
	v_exp_f32_e32 v155, v155
	v_add_f32_e32 v156, 1.0, v156
	v_rcp_f32_e32 v151, v151
	v_mul_f32_e32 v161, 0xbfb8aa3b, v161
	v_rcp_f32_e32 v156, v156
	v_add_f32_e32 v157, 1.0, v157
	v_add_f32_e32 v154, 1.0, v154
	v_add_f32_e32 v160, 1.0, v160
	v_exp_f32_e32 v161, v161
	v_rcp_f32_e32 v157, v157
	v_rcp_f32_e32 v154, v154
	v_rcp_f32_e32 v160, v160
	v_add_f32_e32 v155, 1.0, v155
	v_mul_f32_e32 v150, 0x437f0000, v150
	v_rcp_f32_e32 v155, v155
	v_rndne_f32_e32 v150, v150
	v_mul_f32_e32 v151, 0x437f0000, v151
	v_add_f32_e32 v161, 1.0, v161
	v_mul_f32_e32 v156, 0x437f0000, v156
	v_cvt_pk_u8_f32 v150, v150, 0, 0
	v_rndne_f32_e32 v151, v151
	v_rcp_f32_e32 v161, v161
	v_rndne_f32_e32 v156, v156
	v_mul_f32_e32 v157, 0x437f0000, v157
	v_cvt_pk_u8_f32 v150, v151, 1, v150
	v_mul_f32_e32 v151, 0x437f0000, v154
	v_mul_f32_e32 v154, 0x437f0000, v160
	v_cvt_pk_u8_f32 v156, v156, 0, 0
	v_rndne_f32_e32 v157, v157
	v_rndne_f32_e32 v154, v154
	v_cvt_pk_u8_f32 v156, v157, 1, v156
	v_rndne_f32_e32 v151, v151
	v_cvt_pk_u8_f32 v154, v154, 2, v150
	v_mul_f32_e32 v150, 0x437f0000, v155
	v_cvt_pk_u8_f32 v151, v151, 2, v156
	v_rndne_f32_e32 v150, v150
	v_cvt_pk_u8_f32 v150, v150, 3, v151
	v_mul_f32_e32 v151, 0x437f0000, v161
	v_rndne_f32_e32 v151, v151
	v_cvt_pk_u8_f32 v151, v151, 3, v154
	v_mad_i64_i32 v[154:155], s[2:3], v162, s4, v[152:153]
	global_store_dwordx4 v[154:155], v[148:151], off
	ds_read2_b32 v[148:149], v199 offset0:32 offset1:48
	s_waitcnt lgkmcnt(0)
; __device__ __forceinline__ unsigned cvt_pk_bf16(float lo, float hi) { f32x2_c v = {lo, hi}; bf16x2_c b = __builtin_convertvector(v, bf16x2_c); return __builtin_bit_cast(unsigned, b); }
; __device__ __forceinline__ float silu_f(float g) { return g * __builtin_amdgcn_rcpf(1.0f + __builtin_amdgcn_exp2f(-1.44269504f * g)); }
;     template <int TT> __device__ __forceinline__ void other(const f32x4 (&acc)[2][2][4][2], bf16_t* base, int row0, int col0, PG8_LAS float* my, int t, int hh, int wc, int fq) const {
;     ...
;                 for (int bj = 0; bj < 2; ++bj) { f32x4 v0 = acc[ai][bj][m][0] * rs + bv[bj][0], v1 = acc[ai][bj][m][1] * rs + bv[bj][1];
;                     if (TT == 3) {
; #pragma unroll
;                         for (int j = 0; j < 4; ++j) { v0[j] = silu_f(v0[j]); v1[j] = silu_f(v1[j]); } }
;                     else if (TT == 4 || TT == 5) { f32x2 a = gelu_pk((f32x2){v0[0], v0[1]}), b = gelu_pk((f32x2){v0[2], v0[3]}), c = gelu_pk((f32x2){v1[0], v1[1]}), d = gelu_pk((f32x2){v1[2], v1[3]});
;                         v0 = (f32x4){a.x, a.y, b.x, b.y}; v1 = (f32x4){c.x, c.y, d.x, d.y};
;                         if (TT == 5) { ps += ((v0[0] + v0[1]) + (v0[2] + v0[3])) + ((v1[0] + v1[1]) + (v1[2] + v1[3]));
;                             pq += ((v0[0] * v0[0] + v0[1] * v0[1]) + (v0[2] * v0[2] + v0[3] * v0[3])) + ((v1[0] * v1[0] + v1[1] * v1[1]) + (v1[2] * v1[2] + v1[3] * v1[3])); } }
;                     else if (TT >= 6) {
; #pragma unroll
;                         for (int j = 0; j < 4; ++j) { v0[j] = sigmoid_f(v0[j]); v1[j] = sigmoid_f(v1[j]); } }
;                     if (TT >= 6) { unsigned b0 = 0u, b1 = 0u;
; #pragma unroll
;                         for (int j = 0; j < 4; ++j) { b0 = __builtin_amdgcn_cvt_pk_u8_f32(__builtin_rintf(v0[j] * 255.0f), j, b0); b1 = __builtin_amdgcn_cvt_pk_u8_f32(__builtin_rintf(v1[j] * 255.0f), j, b1); }
;                         if (bj == 0) { gq.x = b0; gq.y = b1; } else { gq.z = b0; gq.w = b1; } }
;                     else { u32x4 w; w.x = cvt_pk_bf16(v0[0], v0[1]); w.y = cvt_pk_bf16(v0[2], v0[3]); w.z = cvt_pk_bf16(v1[0], v1[1]); w.w = cvt_pk_bf16(v1[2], v1[3]);
;                         *(u32x4*)(rowp + bj * HALF) = w; } }
;                 if (TT >= 6) *(u32x4*)((unsigned char*)base + (size_t)(row0 + ai * HALF + m * 16) * GATE_PITCH + hh * 256 + (wc * 4 + fq) * 16) = gq;
	v_fma_f32 v154, v88, v148, v140
	v_fma_f32 v155, v89, v148, v141
	s_nop 0
	v_mul_f32_e32 v154, 0xbfb8aa3b, v154
	v_fma_f32 v150, v90, v148, v142
	v_fma_f32 v151, v91, v148, v143
	v_fma_f32 v160, v84, v148, v144
	v_fma_f32 v161, v85, v148, v145
	v_exp_f32_e32 v154, v154
	v_mul_f32_e32 v155, 0xbfb8aa3b, v155
	v_mul_f32_e32 v160, 0xbfb8aa3b, v160
	v_exp_f32_e32 v155, v155
	v_mul_f32_e32 v150, 0xbfb8aa3b, v150
	v_fma_f32 v156, v86, v148, v146
	v_fma_f32 v157, v87, v148, v147
	v_exp_f32_e32 v160, v160
	v_mul_f32_e32 v161, 0xbfb8aa3b, v161
	v_exp_f32_e32 v150, v150
	v_exp_f32_e32 v161, v161
	v_mul_f32_e32 v156, 0xbfb8aa3b, v156
	v_mul_f32_e32 v151, 0xbfb8aa3b, v151
	v_add_f32_e32 v154, 1.0, v154
	v_exp_f32_e32 v156, v156
	v_exp_f32_e32 v151, v151
	v_rcp_f32_e32 v154, v154
	v_add_f32_e32 v155, 1.0, v155
	v_mul_f32_e32 v157, 0xbfb8aa3b, v157
	v_add_f32_e32 v160, 1.0, v160
	v_rcp_f32_e32 v155, v155
	v_add_f32_e32 v150, 1.0, v150
	v_exp_f32_e32 v157, v157
	v_rcp_f32_e32 v160, v160
	v_add_f32_e32 v161, 1.0, v161
	v_rcp_f32_e32 v150, v150
	v_rcp_f32_e32 v161, v161
	v_add_f32_e32 v156, 1.0, v156
	v_add_f32_e32 v151, 1.0, v151
	v_rcp_f32_e32 v156, v156
	v_rcp_f32_e32 v151, v151
	v_mul_f32_e32 v154, 0x437f0000, v154
	v_add_f32_e32 v157, 1.0, v157
	v_rndne_f32_e32 v154, v154
	v_mul_f32_e32 v155, 0x437f0000, v155
	v_rcp_f32_e32 v157, v157
	v_cvt_pk_u8_f32 v154, v154, 0, 0
	v_mul_f32_e32 v160, 0x437f0000, v160
	v_rndne_f32_e32 v155, v155
	v_mul_f32_e32 v150, 0x437f0000, v150
	v_rndne_f32_e32 v160, v160
	v_cvt_pk_u8_f32 v154, v155, 1, v154
	v_mul_f32_e32 v155, 0x437f0000, v161
	v_rndne_f32_e32 v150, v150
	v_cvt_pk_u8_f32 v160, v160, 0, 0
	v_rndne_f32_e32 v155, v155
	v_cvt_pk_u8_f32 v150, v150, 2, v154
	v_mul_f32_e32 v154, 0x437f0000, v156
	v_mul_f32_e32 v151, 0x437f0000, v151
	v_cvt_pk_u8_f32 v155, v155, 1, v160
	v_rndne_f32_e32 v154, v154
	v_rndne_f32_e32 v151, v151
	v_cvt_pk_u8_f32 v155, v154, 2, v155
	v_cvt_pk_u8_f32 v154, v151, 3, v150
	v_mul_f32_e32 v150, 0x437f0000, v157
	v_rndne_f32_e32 v150, v150
	v_fma_f32 v156, v96, v148, v136
	v_fma_f32 v157, v97, v148, v137
	v_cvt_pk_u8_f32 v155, v150, 3, v155
	v_fma_f32 v150, v98, v148, v138
	v_fma_f32 v151, v99, v148, v139
	v_fma_f32 v160, v94, v148, v134
	v_fma_f32 v161, v95, v148, v135
	v_fma_f32 v162, v92, v148, v132
	v_fma_f32 v163, v93, v148, v133
	v_mul_f32_e32 v148, 0xbfb8aa3b, v156
	v_exp_f32_e32 v148, v148
	v_mul_f32_e32 v157, 0xbfb8aa3b, v157
	v_mul_f32_e32 v156, 0xbfb8aa3b, v162
	v_exp_f32_e32 v157, v157
	v_mul_f32_e32 v150, 0xbfb8aa3b, v150
	v_exp_f32_e32 v156, v156
	v_mul_f32_e32 v162, 0xbfb8aa3b, v163
	v_exp_f32_e32 v150, v150
	v_exp_f32_e32 v162, v162
	v_mul_f32_e32 v160, 0xbfb8aa3b, v160
	v_mul_f32_e32 v151, 0xbfb8aa3b, v151
	v_add_f32_e32 v148, 1.0, v148
	v_exp_f32_e32 v160, v160
	v_exp_f32_e32 v151, v151
	v_rcp_f32_e32 v148, v148
	v_add_f32_e32 v157, 1.0, v157
	v_mul_f32_e32 v161, 0xbfb8aa3b, v161
	v_add_f32_e32 v156, 1.0, v156
	v_rcp_f32_e32 v157, v157
	v_add_f32_e32 v150, 1.0, v150
	v_exp_f32_e32 v161, v161
	v_rcp_f32_e32 v156, v156
	v_add_f32_e32 v162, 1.0, v162
	v_rcp_f32_e32 v150, v150
	v_rcp_f32_e32 v162, v162
	v_add_f32_e32 v160, 1.0, v160
	v_add_f32_e32 v151, 1.0, v151
	v_rcp_f32_e32 v160, v160
	v_rcp_f32_e32 v151, v151
	v_mul_f32_e32 v148, 0x437f0000, v148
	v_add_f32_e32 v161, 1.0, v161
	v_rndne_f32_e32 v148, v148
	v_mul_f32_e32 v157, 0x437f0000, v157
	v_rcp_f32_e32 v161, v161
	v_cvt_pk_u8_f32 v148, v148, 0, 0
	v_mul_f32_e32 v156, 0x437f0000, v156
	v_rndne_f32_e32 v157, v157
	v_mul_f32_e32 v150, 0x437f0000, v150
	v_rndne_f32_e32 v156, v156
	v_cvt_pk_u8_f32 v148, v157, 1, v148
	v_mul_f32_e32 v157, 0x437f0000, v162
	v_rndne_f32_e32 v150, v150
	v_cvt_pk_u8_f32 v156, v156, 0, 0
	v_rndne_f32_e32 v157, v157
	v_cvt_pk_u8_f32 v148, v150, 2, v148
	v_mul_f32_e32 v150, 0x437f0000, v160
	v_mul_f32_e32 v151, 0x437f0000, v151
	v_cvt_pk_u8_f32 v156, v157, 1, v156
	v_rndne_f32_e32 v150, v150
	v_rndne_f32_e32 v151, v151
	v_cvt_pk_u8_f32 v150, v150, 2, v156
	v_cvt_pk_u8_f32 v156, v151, 3, v148
	v_mul_f32_e32 v148, 0x437f0000, v161
	v_rndne_f32_e32 v148, v148
	v_cvt_pk_u8_f32 v157, v148, 3, v150
	v_mad_i64_i32 v[150:151], s[2:3], v176, s4, v[152:153]
	global_store_dwordx4 v[150:151], v[154:157], off
	v_mov_b32_e32 v150, v149
	v_fma_f32 v148, v74, v150, v142
	v_fma_f32 v149, v75, v150, v143
	v_fma_f32 v154, v72, v150, v140
	v_fma_f32 v155, v73, v150, v141
	v_fma_f32 v156, v70, v150, v146
	v_fma_f32 v157, v71, v150, v147
	v_fma_f32 v160, v68, v150, v144
	v_fma_f32 v161, v69, v150, v145
	v_mul_f32_e32 v151, 0xbfb8aa3b, v154
	v_exp_f32_e32 v151, v151
	v_mul_f32_e32 v155, 0xbfb8aa3b, v155
	v_mul_f32_e32 v154, 0xbfb8aa3b, v160
	v_exp_f32_e32 v155, v155
	v_mul_f32_e32 v148, 0xbfb8aa3b, v148
	v_exp_f32_e32 v154, v154
	v_mul_f32_e32 v160, 0xbfb8aa3b, v161
	v_exp_f32_e32 v148, v148
	v_mul_f32_e32 v149, 0xbfb8aa3b, v149
	v_exp_f32_e32 v160, v160
	v_mul_f32_e32 v156, 0xbfb8aa3b, v156
	v_exp_f32_e32 v149, v149
	v_add_f32_e32 v151, 1.0, v151
	v_exp_f32_e32 v156, v156
	v_mul_f32_e32 v157, 0xbfb8aa3b, v157
	v_rcp_f32_e32 v151, v151
	v_add_f32_e32 v155, 1.0, v155
	v_exp_f32_e32 v157, v157
	v_add_f32_e32 v154, 1.0, v154
	v_rcp_f32_e32 v155, v155
	v_add_f32_e32 v148, 1.0, v148
	v_rcp_f32_e32 v154, v154
	v_add_f32_e32 v160, 1.0, v160
	v_rcp_f32_e32 v148, v148
	v_add_f32_e32 v149, 1.0, v149
	v_rcp_f32_e32 v160, v160
	v_add_f32_e32 v156, 1.0, v156
	v_rcp_f32_e32 v149, v149
	v_rcp_f32_e32 v156, v156
	v_add_f32_e32 v157, 1.0, v157
	v_mul_f32_e32 v151, 0x437f0000, v151
	v_rcp_f32_e32 v157, v157
	v_rndne_f32_e32 v151, v151
	v_mul_f32_e32 v155, 0x437f0000, v155
	v_cvt_pk_u8_f32 v151, v151, 0, 0
	v_mul_f32_e32 v154, 0x437f0000, v154
; __device__ __forceinline__ unsigned cvt_pk_bf16(float lo, float hi) { f32x2_c v = {lo, hi}; bf16x2_c b = __builtin_convertvector(v, bf16x2_c); return __builtin_bit_cast(unsigned, b); }
; __device__ __forceinline__ float silu_f(float g) { return g * __builtin_amdgcn_rcpf(1.0f + __builtin_amdgcn_exp2f(-1.44269504f * g)); }
;     template <int TT> __device__ __forceinline__ void other(const f32x4 (&acc)[2][2][4][2], bf16_t* base, int row0, int col0, PG8_LAS float* my, int t, int hh, int wc, int fq) const {
;     ...
;                 for (int bj = 0; bj < 2; ++bj) { f32x4 v0 = acc[ai][bj][m][0] * rs + bv[bj][0], v1 = acc[ai][bj][m][1] * rs + bv[bj][1];
;                     if (TT == 3) {
; #pragma unroll
;                         for (int j = 0; j < 4; ++j) { v0[j] = silu_f(v0[j]); v1[j] = silu_f(v1[j]); } }
;                     else if (TT == 4 || TT == 5) { f32x2 a = gelu_pk((f32x2){v0[0], v0[1]}), b = gelu_pk((f32x2){v0[2], v0[3]}), c = gelu_pk((f32x2){v1[0], v1[1]}), d = gelu_pk((f32x2){v1[2], v1[3]});
;                         v0 = (f32x4){a.x, a.y, b.x, b.y}; v1 = (f32x4){c.x, c.y, d.x, d.y};
;                         if (TT == 5) { ps += ((v0[0] + v0[1]) + (v0[2] + v0[3])) + ((v1[0] + v1[1]) + (v1[2] + v1[3]));
;                             pq += ((v0[0] * v0[0] + v0[1] * v0[1]) + (v0[2] * v0[2] + v0[3] * v0[3])) + ((v1[0] * v1[0] + v1[1] * v1[1]) + (v1[2] * v1[2] + v1[3] * v1[3])); } }
;                     else if (TT >= 6) {
; #pragma unroll
;                         for (int j = 0; j < 4; ++j) { v0[j] = sigmoid_f(v0[j]); v1[j] = sigmoid_f(v1[j]); } }
;                     if (TT >= 6) { unsigned b0 = 0u, b1 = 0u;
; #pragma unroll
;                         for (int j = 0; j < 4; ++j) { b0 = __builtin_amdgcn_cvt_pk_u8_f32(__builtin_rintf(v0[j] * 255.0f), j, b0); b1 = __builtin_amdgcn_cvt_pk_u8_f32(__builtin_rintf(v1[j] * 255.0f), j, b1); }
;                         if (bj == 0) { gq.x = b0; gq.y = b1; } else { gq.z = b0; gq.w = b1; } }
;                     else { u32x4 w; w.x = cvt_pk_bf16(v0[0], v0[1]); w.y = cvt_pk_bf16(v0[2], v0[3]); w.z = cvt_pk_bf16(v1[0], v1[1]); w.w = cvt_pk_bf16(v1[2], v1[3]);
;                         *(u32x4*)(rowp + bj * HALF) = w; } }
;                 if (TT >= 6) *(u32x4*)((unsigned char*)base + (size_t)(row0 + ai * HALF + m * 16) * GATE_PITCH + hh * 256 + (wc * 4 + fq) * 16) = gq;
	v_rndne_f32_e32 v155, v155
	v_mul_f32_e32 v148, 0x437f0000, v148
	v_rndne_f32_e32 v154, v154
	v_cvt_pk_u8_f32 v151, v155, 1, v151
	v_mul_f32_e32 v155, 0x437f0000, v160
	v_rndne_f32_e32 v148, v148
	v_mul_f32_e32 v149, 0x437f0000, v149
	v_cvt_pk_u8_f32 v154, v154, 0, 0
	v_rndne_f32_e32 v155, v155
	v_cvt_pk_u8_f32 v148, v148, 2, v151
	v_mul_f32_e32 v151, 0x437f0000, v156
	v_rndne_f32_e32 v149, v149
	v_cvt_pk_u8_f32 v154, v155, 1, v154
	v_rndne_f32_e32 v151, v151
	v_cvt_pk_u8_f32 v148, v149, 3, v148
	v_mul_f32_e32 v149, 0x437f0000, v157
	v_cvt_pk_u8_f32 v151, v151, 2, v154
	v_rndne_f32_e32 v149, v149
	v_cvt_pk_u8_f32 v149, v149, 3, v151
	v_fma_f32 v154, v82, v150, v138
	v_fma_f32 v155, v83, v150, v139
	v_fma_f32 v156, v80, v150, v136
	v_fma_f32 v157, v81, v150, v137
	v_fma_f32 v160, v78, v150, v134
	v_fma_f32 v161, v79, v150, v135
	v_fma_f32 v151, v77, v150, v133
	v_fma_f32 v150, v76, v150, v132
	v_mul_f32_e32 v156, 0xbfb8aa3b, v156
	v_mul_f32_e32 v150, 0xbfb8aa3b, v150
	v_exp_f32_e32 v150, v150
	v_mul_f32_e32 v151, 0xbfb8aa3b, v151
	v_exp_f32_e32 v151, v151
	v_exp_f32_e32 v156, v156
	v_mul_f32_e32 v157, 0xbfb8aa3b, v157
	v_mul_f32_e32 v154, 0xbfb8aa3b, v154
	v_mul_f32_e32 v160, 0xbfb8aa3b, v160
	v_exp_f32_e32 v157, v157
	v_exp_f32_e32 v154, v154
	v_exp_f32_e32 v160, v160
	v_add_f32_e32 v150, 1.0, v150
	v_mul_f32_e32 v155, 0xbfb8aa3b, v155
	v_rcp_f32_e32 v150, v150
	v_add_f32_e32 v151, 1.0, v151
	v_exp_f32_e32 v155, v155
	v_add_f32_e32 v156, 1.0, v156
	v_rcp_f32_e32 v151, v151
	v_mul_f32_e32 v161, 0xbfb8aa3b, v161
	v_rcp_f32_e32 v156, v156
	v_add_f32_e32 v157, 1.0, v157
	v_add_f32_e32 v154, 1.0, v154
	v_add_f32_e32 v160, 1.0, v160
	v_exp_f32_e32 v161, v161
	v_rcp_f32_e32 v157, v157
	v_rcp_f32_e32 v154, v154
	v_rcp_f32_e32 v160, v160
	v_add_f32_e32 v155, 1.0, v155
	v_mul_f32_e32 v150, 0x437f0000, v150
	v_rcp_f32_e32 v155, v155
	v_rndne_f32_e32 v150, v150
	v_mul_f32_e32 v151, 0x437f0000, v151
	v_add_f32_e32 v161, 1.0, v161
	v_mul_f32_e32 v156, 0x437f0000, v156
	v_cvt_pk_u8_f32 v150, v150, 0, 0
	v_rndne_f32_e32 v151, v151
	v_rcp_f32_e32 v161, v161
	v_rndne_f32_e32 v156, v156
	v_mul_f32_e32 v157, 0x437f0000, v157
	v_cvt_pk_u8_f32 v150, v151, 1, v150
	v_mul_f32_e32 v151, 0x437f0000, v154
	v_mul_f32_e32 v154, 0x437f0000, v160
	v_cvt_pk_u8_f32 v156, v156, 0, 0
	v_rndne_f32_e32 v157, v157
	v_rndne_f32_e32 v154, v154
	v_cvt_pk_u8_f32 v156, v157, 1, v156
	v_rndne_f32_e32 v151, v151
	v_cvt_pk_u8_f32 v154, v154, 2, v150
	v_mul_f32_e32 v150, 0x437f0000, v155
	v_cvt_pk_u8_f32 v151, v151, 2, v156
	v_rndne_f32_e32 v150, v150
	v_cvt_pk_u8_f32 v150, v150, 3, v151
	v_mul_f32_e32 v151, 0x437f0000, v161
	v_add_u32_e32 v162, 48, v159
	v_rndne_f32_e32 v151, v151
	v_cvt_pk_u8_f32 v151, v151, 3, v154
	v_mad_i64_i32 v[154:155], s[2:3], v162, s4, v[152:153]
	global_store_dwordx4 v[154:155], v[148:151], off
	ds_read2_b32 v[148:149], v199 offset0:64 offset1:80
	v_add_u32_e32 v176, 0x80, v159
	s_waitcnt lgkmcnt(0)
	v_fma_f32 v154, v56, v148, v140
	v_fma_f32 v155, v57, v148, v141
	s_nop 0
	v_mul_f32_e32 v154, 0xbfb8aa3b, v154
	v_fma_f32 v150, v58, v148, v142
	v_fma_f32 v151, v59, v148, v143
	v_fma_f32 v160, v52, v148, v144
	v_fma_f32 v161, v53, v148, v145
	v_exp_f32_e32 v154, v154
	v_mul_f32_e32 v155, 0xbfb8aa3b, v155
	v_mul_f32_e32 v160, 0xbfb8aa3b, v160
	v_exp_f32_e32 v155, v155
	v_mul_f32_e32 v150, 0xbfb8aa3b, v150
	v_fma_f32 v156, v54, v148, v146
	v_fma_f32 v157, v55, v148, v147
	v_exp_f32_e32 v160, v160
	v_mul_f32_e32 v161, 0xbfb8aa3b, v161
	v_exp_f32_e32 v150, v150
	v_exp_f32_e32 v161, v161
	v_mul_f32_e32 v156, 0xbfb8aa3b, v156
	v_mul_f32_e32 v151, 0xbfb8aa3b, v151
	v_add_f32_e32 v154, 1.0, v154
	v_exp_f32_e32 v156, v156
	v_exp_f32_e32 v151, v151
	v_rcp_f32_e32 v154, v154
	v_add_f32_e32 v155, 1.0, v155
	v_mul_f32_e32 v157, 0xbfb8aa3b, v157
	v_add_f32_e32 v160, 1.0, v160
	v_rcp_f32_e32 v155, v155
	v_add_f32_e32 v150, 1.0, v150
	v_exp_f32_e32 v157, v157
	v_rcp_f32_e32 v160, v160
	v_add_f32_e32 v161, 1.0, v161
	v_rcp_f32_e32 v150, v150
	v_rcp_f32_e32 v161, v161
	v_add_f32_e32 v156, 1.0, v156
	v_add_f32_e32 v151, 1.0, v151
	v_rcp_f32_e32 v156, v156
	v_rcp_f32_e32 v151, v151
	v_mul_f32_e32 v154, 0x437f0000, v154
	v_add_f32_e32 v157, 1.0, v157
	v_rndne_f32_e32 v154, v154
	v_mul_f32_e32 v155, 0x437f0000, v155
	v_rcp_f32_e32 v157, v157
	v_cvt_pk_u8_f32 v154, v154, 0, 0
	v_mul_f32_e32 v160, 0x437f0000, v160
	v_rndne_f32_e32 v155, v155
	v_mul_f32_e32 v150, 0x437f0000, v150
	v_rndne_f32_e32 v160, v160
	v_cvt_pk_u8_f32 v154, v155, 1, v154
	v_mul_f32_e32 v155, 0x437f0000, v161
	v_rndne_f32_e32 v150, v150
	v_cvt_pk_u8_f32 v160, v160, 0, 0
	v_rndne_f32_e32 v155, v155
	v_cvt_pk_u8_f32 v150, v150, 2, v154
	v_mul_f32_e32 v154, 0x437f0000, v156
	v_mul_f32_e32 v151, 0x437f0000, v151
	v_cvt_pk_u8_f32 v155, v155, 1, v160
	v_rndne_f32_e32 v154, v154
	v_rndne_f32_e32 v151, v151
	v_cvt_pk_u8_f32 v155, v154, 2, v155
	v_cvt_pk_u8_f32 v154, v151, 3, v150
	v_mul_f32_e32 v150, 0x437f0000, v157
	v_rndne_f32_e32 v150, v150
	v_fma_f32 v156, v64, v148, v136
	v_fma_f32 v157, v65, v148, v137
	v_cvt_pk_u8_f32 v155, v150, 3, v155
	v_fma_f32 v150, v66, v148, v138
	v_fma_f32 v151, v67, v148, v139
	v_fma_f32 v160, v62, v148, v134
	v_fma_f32 v161, v63, v148, v135
	v_fma_f32 v162, v60, v148, v132
	v_fma_f32 v163, v61, v148, v133
	v_mul_f32_e32 v148, 0xbfb8aa3b, v156
	v_exp_f32_e32 v148, v148
	v_mul_f32_e32 v157, 0xbfb8aa3b, v157
	v_mul_f32_e32 v156, 0xbfb8aa3b, v162
	v_exp_f32_e32 v157, v157
	v_mul_f32_e32 v150, 0xbfb8aa3b, v150
	v_exp_f32_e32 v156, v156
	v_mul_f32_e32 v162, 0xbfb8aa3b, v163
	v_exp_f32_e32 v150, v150
	v_exp_f32_e32 v162, v162
	v_mul_f32_e32 v160, 0xbfb8aa3b, v160
	v_mul_f32_e32 v151, 0xbfb8aa3b, v151
; __device__ __forceinline__ unsigned cvt_pk_bf16(float lo, float hi) { f32x2_c v = {lo, hi}; bf16x2_c b = __builtin_convertvector(v, bf16x2_c); return __builtin_bit_cast(unsigned, b); }
; __device__ __forceinline__ float silu_f(float g) { return g * __builtin_amdgcn_rcpf(1.0f + __builtin_amdgcn_exp2f(-1.44269504f * g)); }
;     template <int TT> __device__ __forceinline__ void other(const f32x4 (&acc)[2][2][4][2], bf16_t* base, int row0, int col0, PG8_LAS float* my, int t, int hh, int wc, int fq) const {
;     ...
;                 for (int bj = 0; bj < 2; ++bj) { f32x4 v0 = acc[ai][bj][m][0] * rs + bv[bj][0], v1 = acc[ai][bj][m][1] * rs + bv[bj][1];
;                     if (TT == 3) {
; #pragma unroll
;                         for (int j = 0; j < 4; ++j) { v0[j] = silu_f(v0[j]); v1[j] = silu_f(v1[j]); } }
;                     else if (TT == 4 || TT == 5) { f32x2 a = gelu_pk((f32x2){v0[0], v0[1]}), b = gelu_pk((f32x2){v0[2], v0[3]}), c = gelu_pk((f32x2){v1[0], v1[1]}), d = gelu_pk((f32x2){v1[2], v1[3]});
;                         v0 = (f32x4){a.x, a.y, b.x, b.y}; v1 = (f32x4){c.x, c.y, d.x, d.y};
;                         if (TT == 5) { ps += ((v0[0] + v0[1]) + (v0[2] + v0[3])) + ((v1[0] + v1[1]) + (v1[2] + v1[3]));
;                             pq += ((v0[0] * v0[0] + v0[1] * v0[1]) + (v0[2] * v0[2] + v0[3] * v0[3])) + ((v1[0] * v1[0] + v1[1] * v1[1]) + (v1[2] * v1[2] + v1[3] * v1[3])); } }
;                     else if (TT >= 6) {
; #pragma unroll
;                         for (int j = 0; j < 4; ++j) { v0[j] = sigmoid_f(v0[j]); v1[j] = sigmoid_f(v1[j]); } }
;                     if (TT >= 6) { unsigned b0 = 0u, b1 = 0u;
; #pragma unroll
;                         for (int j = 0; j < 4; ++j) { b0 = __builtin_amdgcn_cvt_pk_u8_f32(__builtin_rintf(v0[j] * 255.0f), j, b0); b1 = __builtin_amdgcn_cvt_pk_u8_f32(__builtin_rintf(v1[j] * 255.0f), j, b1); }
;                         if (bj == 0) { gq.x = b0; gq.y = b1; } else { gq.z = b0; gq.w = b1; } }
;                     else { u32x4 w; w.x = cvt_pk_bf16(v0[0], v0[1]); w.y = cvt_pk_bf16(v0[2], v0[3]); w.z = cvt_pk_bf16(v1[0], v1[1]); w.w = cvt_pk_bf16(v1[2], v1[3]);
;                         *(u32x4*)(rowp + bj * HALF) = w; } }
;                 if (TT >= 6) *(u32x4*)((unsigned char*)base + (size_t)(row0 + ai * HALF + m * 16) * GATE_PITCH + hh * 256 + (wc * 4 + fq) * 16) = gq;
	v_add_f32_e32 v148, 1.0, v148
	v_exp_f32_e32 v160, v160
	v_exp_f32_e32 v151, v151
	v_rcp_f32_e32 v148, v148
	v_add_f32_e32 v157, 1.0, v157
	v_mul_f32_e32 v161, 0xbfb8aa3b, v161
	v_add_f32_e32 v156, 1.0, v156
	v_rcp_f32_e32 v157, v157
	v_add_f32_e32 v150, 1.0, v150
	v_exp_f32_e32 v161, v161
	v_rcp_f32_e32 v156, v156
	v_add_f32_e32 v162, 1.0, v162
	v_rcp_f32_e32 v150, v150
	v_rcp_f32_e32 v162, v162
	v_add_f32_e32 v160, 1.0, v160
	v_add_f32_e32 v151, 1.0, v151
	v_rcp_f32_e32 v160, v160
	v_rcp_f32_e32 v151, v151
	v_mul_f32_e32 v148, 0x437f0000, v148
	v_add_f32_e32 v161, 1.0, v161
	v_rndne_f32_e32 v148, v148
	v_mul_f32_e32 v157, 0x437f0000, v157
	v_rcp_f32_e32 v161, v161
	v_cvt_pk_u8_f32 v148, v148, 0, 0
	v_mul_f32_e32 v156, 0x437f0000, v156
	v_rndne_f32_e32 v157, v157
	v_mul_f32_e32 v150, 0x437f0000, v150
	v_rndne_f32_e32 v156, v156
	v_cvt_pk_u8_f32 v148, v157, 1, v148
	v_mul_f32_e32 v157, 0x437f0000, v162
	v_rndne_f32_e32 v150, v150
	v_cvt_pk_u8_f32 v156, v156, 0, 0
	v_rndne_f32_e32 v157, v157
	v_cvt_pk_u8_f32 v148, v150, 2, v148
	v_mul_f32_e32 v150, 0x437f0000, v160
	v_mul_f32_e32 v151, 0x437f0000, v151
	v_cvt_pk_u8_f32 v156, v157, 1, v156
	v_rndne_f32_e32 v150, v150
	v_rndne_f32_e32 v151, v151
	v_cvt_pk_u8_f32 v150, v150, 2, v156
	v_cvt_pk_u8_f32 v156, v151, 3, v148
	v_mul_f32_e32 v148, 0x437f0000, v161
	v_rndne_f32_e32 v148, v148
	v_cvt_pk_u8_f32 v157, v148, 3, v150
	v_mad_i64_i32 v[150:151], s[2:3], v176, s4, v[152:153]
	global_store_dwordx4 v[150:151], v[154:157], off
	v_mov_b32_e32 v150, v149
	v_fma_f32 v148, v42, v150, v142
	v_fma_f32 v149, v43, v150, v143
	v_fma_f32 v154, v40, v150, v140
	v_fma_f32 v155, v41, v150, v141
	v_fma_f32 v156, v38, v150, v146
	v_fma_f32 v157, v39, v150, v147
	v_fma_f32 v160, v36, v150, v144
	v_fma_f32 v161, v37, v150, v145
	v_mul_f32_e32 v151, 0xbfb8aa3b, v154
	v_exp_f32_e32 v151, v151
	v_mul_f32_e32 v155, 0xbfb8aa3b, v155
	v_mul_f32_e32 v154, 0xbfb8aa3b, v160
	v_exp_f32_e32 v155, v155
	v_mul_f32_e32 v148, 0xbfb8aa3b, v148
	v_exp_f32_e32 v154, v154
	v_mul_f32_e32 v160, 0xbfb8aa3b, v161
	v_exp_f32_e32 v148, v148
	v_mul_f32_e32 v149, 0xbfb8aa3b, v149
	v_exp_f32_e32 v160, v160
	v_mul_f32_e32 v156, 0xbfb8aa3b, v156
	v_exp_f32_e32 v149, v149
	v_add_f32_e32 v151, 1.0, v151
	v_exp_f32_e32 v156, v156
	v_mul_f32_e32 v157, 0xbfb8aa3b, v157
	v_rcp_f32_e32 v151, v151
	v_add_f32_e32 v155, 1.0, v155
	v_exp_f32_e32 v157, v157
	v_add_f32_e32 v154, 1.0, v154
	v_rcp_f32_e32 v155, v155
	v_add_f32_e32 v148, 1.0, v148
	v_rcp_f32_e32 v154, v154
	v_add_f32_e32 v160, 1.0, v160
	v_rcp_f32_e32 v148, v148
	v_add_f32_e32 v149, 1.0, v149
	v_rcp_f32_e32 v160, v160
	v_add_f32_e32 v156, 1.0, v156
	v_rcp_f32_e32 v149, v149
	v_rcp_f32_e32 v156, v156
	v_add_f32_e32 v157, 1.0, v157
	v_mul_f32_e32 v151, 0x437f0000, v151
	v_rcp_f32_e32 v157, v157
	v_rndne_f32_e32 v151, v151
	v_mul_f32_e32 v155, 0x437f0000, v155
	v_cvt_pk_u8_f32 v151, v151, 0, 0
	v_mul_f32_e32 v154, 0x437f0000, v154
	v_rndne_f32_e32 v155, v155
	v_mul_f32_e32 v148, 0x437f0000, v148
	v_rndne_f32_e32 v154, v154
	v_cvt_pk_u8_f32 v151, v155, 1, v151
	v_mul_f32_e32 v155, 0x437f0000, v160
	v_rndne_f32_e32 v148, v148
	v_mul_f32_e32 v149, 0x437f0000, v149
	v_cvt_pk_u8_f32 v154, v154, 0, 0
	v_rndne_f32_e32 v155, v155
	v_cvt_pk_u8_f32 v148, v148, 2, v151
	v_mul_f32_e32 v151, 0x437f0000, v156
	v_rndne_f32_e32 v149, v149
	v_cvt_pk_u8_f32 v154, v155, 1, v154
	v_rndne_f32_e32 v151, v151
	v_cvt_pk_u8_f32 v148, v149, 3, v148
	v_mul_f32_e32 v149, 0x437f0000, v157
	v_cvt_pk_u8_f32 v151, v151, 2, v154
	v_rndne_f32_e32 v149, v149
	v_cvt_pk_u8_f32 v149, v149, 3, v151
	v_fma_f32 v154, v50, v150, v138
	v_fma_f32 v155, v51, v150, v139
	v_fma_f32 v156, v48, v150, v136
	v_fma_f32 v157, v49, v150, v137
	v_fma_f32 v160, v46, v150, v134
	v_fma_f32 v161, v47, v150, v135
	v_fma_f32 v151, v45, v150, v133
	v_fma_f32 v150, v44, v150, v132
	v_mul_f32_e32 v156, 0xbfb8aa3b, v156
	v_mul_f32_e32 v150, 0xbfb8aa3b, v150
	v_exp_f32_e32 v150, v150
	v_mul_f32_e32 v151, 0xbfb8aa3b, v151
	v_exp_f32_e32 v151, v151
	v_exp_f32_e32 v156, v156
	v_mul_f32_e32 v157, 0xbfb8aa3b, v157
	v_mul_f32_e32 v154, 0xbfb8aa3b, v154
	v_mul_f32_e32 v160, 0xbfb8aa3b, v160
	v_exp_f32_e32 v157, v157
	v_exp_f32_e32 v154, v154
	v_exp_f32_e32 v160, v160
	v_add_f32_e32 v150, 1.0, v150
	v_mul_f32_e32 v155, 0xbfb8aa3b, v155
	v_rcp_f32_e32 v150, v150
	v_add_f32_e32 v151, 1.0, v151
	v_exp_f32_e32 v155, v155
	v_add_f32_e32 v156, 1.0, v156
	v_rcp_f32_e32 v151, v151
	v_mul_f32_e32 v161, 0xbfb8aa3b, v161
	v_rcp_f32_e32 v156, v156
	v_add_f32_e32 v157, 1.0, v157
	v_add_f32_e32 v154, 1.0, v154
	v_add_f32_e32 v160, 1.0, v160
	v_exp_f32_e32 v161, v161
	v_rcp_f32_e32 v157, v157
	v_rcp_f32_e32 v154, v154
	v_rcp_f32_e32 v160, v160
	v_add_f32_e32 v155, 1.0, v155
	v_mul_f32_e32 v150, 0x437f0000, v150
	v_rcp_f32_e32 v155, v155
	v_rndne_f32_e32 v150, v150
	v_mul_f32_e32 v151, 0x437f0000, v151
	v_add_f32_e32 v161, 1.0, v161
	v_mul_f32_e32 v156, 0x437f0000, v156
	v_cvt_pk_u8_f32 v150, v150, 0, 0
	v_rndne_f32_e32 v151, v151
	v_rcp_f32_e32 v161, v161
	v_rndne_f32_e32 v156, v156
	v_mul_f32_e32 v157, 0x437f0000, v157
	v_cvt_pk_u8_f32 v150, v151, 1, v150
	v_mul_f32_e32 v151, 0x437f0000, v154
	v_mul_f32_e32 v154, 0x437f0000, v160
	v_cvt_pk_u8_f32 v156, v156, 0, 0
	v_rndne_f32_e32 v157, v157
	v_rndne_f32_e32 v154, v154
	v_cvt_pk_u8_f32 v156, v157, 1, v156
	v_rndne_f32_e32 v151, v151
	v_cvt_pk_u8_f32 v154, v154, 2, v150
	v_mul_f32_e32 v150, 0x437f0000, v155
	v_cvt_pk_u8_f32 v151, v151, 2, v156
	v_rndne_f32_e32 v150, v150
	v_cvt_pk_u8_f32 v150, v150, 3, v151
	v_mul_f32_e32 v151, 0x437f0000, v161
	v_add_u32_e32 v162, 0x90, v159
	v_rndne_f32_e32 v151, v151
	v_cvt_pk_u8_f32 v151, v151, 3, v154
	v_mad_i64_i32 v[154:155], s[2:3], v162, s4, v[152:153]
	global_store_dwordx4 v[154:155], v[148:151], off
	ds_read2_b32 v[148:149], v199 offset0:96 offset1:112
	v_add_u32_e32 v176, 0xa0, v159
	s_waitcnt lgkmcnt(0)
; __device__ __forceinline__ unsigned cvt_pk_bf16(float lo, float hi) { f32x2_c v = {lo, hi}; bf16x2_c b = __builtin_convertvector(v, bf16x2_c); return __builtin_bit_cast(unsigned, b); }
; __device__ __forceinline__ float silu_f(float g) { return g * __builtin_amdgcn_rcpf(1.0f + __builtin_amdgcn_exp2f(-1.44269504f * g)); }
;     template <int TT> __device__ __forceinline__ void other(const f32x4 (&acc)[2][2][4][2], bf16_t* base, int row0, int col0, PG8_LAS float* my, int t, int hh, int wc, int fq) const {
;     ...
;                 for (int bj = 0; bj < 2; ++bj) { f32x4 v0 = acc[ai][bj][m][0] * rs + bv[bj][0], v1 = acc[ai][bj][m][1] * rs + bv[bj][1];
;                     if (TT == 3) {
; #pragma unroll
;                         for (int j = 0; j < 4; ++j) { v0[j] = silu_f(v0[j]); v1[j] = silu_f(v1[j]); } }
;                     else if (TT == 4 || TT == 5) { f32x2 a = gelu_pk((f32x2){v0[0], v0[1]}), b = gelu_pk((f32x2){v0[2], v0[3]}), c = gelu_pk((f32x2){v1[0], v1[1]}), d = gelu_pk((f32x2){v1[2], v1[3]});
;                         v0 = (f32x4){a.x, a.y, b.x, b.y}; v1 = (f32x4){c.x, c.y, d.x, d.y};
;                         if (TT == 5) { ps += ((v0[0] + v0[1]) + (v0[2] + v0[3])) + ((v1[0] + v1[1]) + (v1[2] + v1[3]));
;                             pq += ((v0[0] * v0[0] + v0[1] * v0[1]) + (v0[2] * v0[2] + v0[3] * v0[3])) + ((v1[0] * v1[0] + v1[1] * v1[1]) + (v1[2] * v1[2] + v1[3] * v1[3])); } }
;                     else if (TT >= 6) {
; #pragma unroll
;                         for (int j = 0; j < 4; ++j) { v0[j] = sigmoid_f(v0[j]); v1[j] = sigmoid_f(v1[j]); } }
;                     if (TT >= 6) { unsigned b0 = 0u, b1 = 0u;
; #pragma unroll
;                         for (int j = 0; j < 4; ++j) { b0 = __builtin_amdgcn_cvt_pk_u8_f32(__builtin_rintf(v0[j] * 255.0f), j, b0); b1 = __builtin_amdgcn_cvt_pk_u8_f32(__builtin_rintf(v1[j] * 255.0f), j, b1); }
;                         if (bj == 0) { gq.x = b0; gq.y = b1; } else { gq.z = b0; gq.w = b1; } }
;                     else { u32x4 w; w.x = cvt_pk_bf16(v0[0], v0[1]); w.y = cvt_pk_bf16(v0[2], v0[3]); w.z = cvt_pk_bf16(v1[0], v1[1]); w.w = cvt_pk_bf16(v1[2], v1[3]);
;                         *(u32x4*)(rowp + bj * HALF) = w; } }
;                 if (TT >= 6) *(u32x4*)((unsigned char*)base + (size_t)(row0 + ai * HALF + m * 16) * GATE_PITCH + hh * 256 + (wc * 4 + fq) * 16) = gq;
	v_fma_f32 v154, v24, v148, v140
	v_fma_f32 v155, v25, v148, v141
	s_nop 0
	v_mul_f32_e32 v154, 0xbfb8aa3b, v154
	v_fma_f32 v150, v26, v148, v142
	v_fma_f32 v151, v27, v148, v143
	v_fma_f32 v160, v20, v148, v144
	v_fma_f32 v161, v21, v148, v145
	v_exp_f32_e32 v154, v154
	v_mul_f32_e32 v155, 0xbfb8aa3b, v155
	v_mul_f32_e32 v160, 0xbfb8aa3b, v160
	v_exp_f32_e32 v155, v155
	v_mul_f32_e32 v150, 0xbfb8aa3b, v150
	v_fma_f32 v156, v22, v148, v146
	v_fma_f32 v157, v23, v148, v147
	v_exp_f32_e32 v160, v160
	v_mul_f32_e32 v161, 0xbfb8aa3b, v161
	v_exp_f32_e32 v150, v150
	v_exp_f32_e32 v161, v161
	v_mul_f32_e32 v156, 0xbfb8aa3b, v156
	v_mul_f32_e32 v151, 0xbfb8aa3b, v151
	v_add_f32_e32 v154, 1.0, v154
	v_exp_f32_e32 v156, v156
	v_exp_f32_e32 v151, v151
	v_rcp_f32_e32 v154, v154
	v_add_f32_e32 v155, 1.0, v155
	v_mul_f32_e32 v157, 0xbfb8aa3b, v157
	v_add_f32_e32 v160, 1.0, v160
	v_rcp_f32_e32 v155, v155
	v_add_f32_e32 v150, 1.0, v150
	v_exp_f32_e32 v157, v157
	v_rcp_f32_e32 v160, v160
	v_add_f32_e32 v161, 1.0, v161
	v_rcp_f32_e32 v150, v150
	v_rcp_f32_e32 v161, v161
	v_add_f32_e32 v156, 1.0, v156
	v_add_f32_e32 v151, 1.0, v151
	v_rcp_f32_e32 v156, v156
	v_rcp_f32_e32 v151, v151
	v_mul_f32_e32 v154, 0x437f0000, v154
	v_add_f32_e32 v157, 1.0, v157
	v_rndne_f32_e32 v154, v154
	v_mul_f32_e32 v155, 0x437f0000, v155
	v_rcp_f32_e32 v157, v157
	v_cvt_pk_u8_f32 v154, v154, 0, 0
	v_mul_f32_e32 v160, 0x437f0000, v160
	v_rndne_f32_e32 v155, v155
	v_mul_f32_e32 v150, 0x437f0000, v150
	v_rndne_f32_e32 v160, v160
	v_cvt_pk_u8_f32 v154, v155, 1, v154
	v_mul_f32_e32 v155, 0x437f0000, v161
	v_rndne_f32_e32 v150, v150
	v_cvt_pk_u8_f32 v160, v160, 0, 0
	v_rndne_f32_e32 v155, v155
	v_cvt_pk_u8_f32 v150, v150, 2, v154
	v_mul_f32_e32 v154, 0x437f0000, v156
	v_mul_f32_e32 v151, 0x437f0000, v151
	v_cvt_pk_u8_f32 v155, v155, 1, v160
	v_rndne_f32_e32 v154, v154
	v_rndne_f32_e32 v151, v151
	v_cvt_pk_u8_f32 v155, v154, 2, v155
	v_cvt_pk_u8_f32 v154, v151, 3, v150
	v_mul_f32_e32 v150, 0x437f0000, v157
	v_rndne_f32_e32 v150, v150
	v_fma_f32 v156, v32, v148, v136
	v_fma_f32 v157, v33, v148, v137
	v_cvt_pk_u8_f32 v155, v150, 3, v155
	v_fma_f32 v150, v34, v148, v138
	v_fma_f32 v151, v35, v148, v139
	v_fma_f32 v160, v30, v148, v134
	v_fma_f32 v161, v31, v148, v135
	v_fma_f32 v162, v28, v148, v132
	v_fma_f32 v163, v29, v148, v133
	v_mul_f32_e32 v148, 0xbfb8aa3b, v156
	v_exp_f32_e32 v148, v148
	v_mul_f32_e32 v157, 0xbfb8aa3b, v157
	v_mul_f32_e32 v156, 0xbfb8aa3b, v162
	v_exp_f32_e32 v157, v157
	v_mul_f32_e32 v150, 0xbfb8aa3b, v150
	v_exp_f32_e32 v156, v156
	v_mul_f32_e32 v162, 0xbfb8aa3b, v163
	v_exp_f32_e32 v150, v150
	v_exp_f32_e32 v162, v162
	v_mul_f32_e32 v160, 0xbfb8aa3b, v160
	v_mul_f32_e32 v151, 0xbfb8aa3b, v151
	v_add_f32_e32 v148, 1.0, v148
	v_exp_f32_e32 v160, v160
	v_exp_f32_e32 v151, v151
	v_rcp_f32_e32 v148, v148
	v_add_f32_e32 v157, 1.0, v157
	v_mul_f32_e32 v161, 0xbfb8aa3b, v161
	v_add_f32_e32 v156, 1.0, v156
	v_rcp_f32_e32 v157, v157
	v_add_f32_e32 v150, 1.0, v150
	v_exp_f32_e32 v161, v161
	v_rcp_f32_e32 v156, v156
	v_add_f32_e32 v162, 1.0, v162
	v_rcp_f32_e32 v150, v150
	v_rcp_f32_e32 v162, v162
	v_add_f32_e32 v160, 1.0, v160
	v_add_f32_e32 v151, 1.0, v151
	v_rcp_f32_e32 v160, v160
	v_rcp_f32_e32 v151, v151
	v_mul_f32_e32 v148, 0x437f0000, v148
	v_add_f32_e32 v161, 1.0, v161
	v_rndne_f32_e32 v148, v148
	v_mul_f32_e32 v157, 0x437f0000, v157
	v_rcp_f32_e32 v161, v161
	v_cvt_pk_u8_f32 v148, v148, 0, 0
	v_mul_f32_e32 v156, 0x437f0000, v156
	v_rndne_f32_e32 v157, v157
	v_mul_f32_e32 v150, 0x437f0000, v150
	v_rndne_f32_e32 v156, v156
	v_cvt_pk_u8_f32 v148, v157, 1, v148
	v_mul_f32_e32 v157, 0x437f0000, v162
	v_rndne_f32_e32 v150, v150
	v_cvt_pk_u8_f32 v156, v156, 0, 0
	v_rndne_f32_e32 v157, v157
	v_cvt_pk_u8_f32 v148, v150, 2, v148
	v_mul_f32_e32 v150, 0x437f0000, v160
	v_mul_f32_e32 v151, 0x437f0000, v151
	v_cvt_pk_u8_f32 v156, v157, 1, v156
	v_rndne_f32_e32 v150, v150
	v_rndne_f32_e32 v151, v151
	v_cvt_pk_u8_f32 v150, v150, 2, v156
	v_cvt_pk_u8_f32 v156, v151, 3, v148
	v_mul_f32_e32 v148, 0x437f0000, v161
	v_rndne_f32_e32 v148, v148
	v_cvt_pk_u8_f32 v157, v148, 3, v150
	v_mov_b32_e32 v148, v149
	v_fma_f32 v140, v8, v148, v140
	v_fma_f32 v141, v9, v148, v141
	v_fma_f32 v142, v10, v148, v142
	v_fma_f32 v143, v11, v148, v143
	v_mul_f32_e32 v140, 0xbfb8aa3b, v140
	v_fma_f32 v144, v4, v148, v144
	v_fma_f32 v145, v5, v148, v145
	v_exp_f32_e32 v140, v140
	v_mul_f32_e32 v141, 0xbfb8aa3b, v141
	v_mul_f32_e32 v144, 0xbfb8aa3b, v144
	v_exp_f32_e32 v141, v141
	v_mul_f32_e32 v142, 0xbfb8aa3b, v142
	v_fma_f32 v146, v6, v148, v146
	v_fma_f32 v147, v7, v148, v147
	v_exp_f32_e32 v144, v144
	v_mul_f32_e32 v145, 0xbfb8aa3b, v145
	v_exp_f32_e32 v142, v142
	v_fma_f32 v132, v12, v148, v132
	v_fma_f32 v133, v13, v148, v133
	v_exp_f32_e32 v145, v145
	v_mul_f32_e32 v146, 0xbfb8aa3b, v146
	v_fma_f32 v136, v16, v148, v136
	v_fma_f32 v137, v17, v148, v137
	v_mul_f32_e32 v132, 0xbfb8aa3b, v132
	v_add_f32_e32 v140, 1.0, v140
	v_exp_f32_e32 v146, v146
	v_fma_f32 v134, v14, v148, v134
	v_fma_f32 v135, v15, v148, v135
	v_mul_f32_e32 v136, 0xbfb8aa3b, v136
	v_exp_f32_e32 v132, v132
	v_mul_f32_e32 v133, 0xbfb8aa3b, v133
	v_rcp_f32_e32 v140, v140
	v_add_f32_e32 v141, 1.0, v141
	v_mul_f32_e32 v143, 0xbfb8aa3b, v143
	v_fma_f32 v138, v18, v148, v138
	v_fma_f32 v139, v19, v148, v139
	v_exp_f32_e32 v136, v136
	v_mul_f32_e32 v137, 0xbfb8aa3b, v137
	v_exp_f32_e32 v133, v133
	v_mul_f32_e32 v134, 0xbfb8aa3b, v134
	v_add_f32_e32 v144, 1.0, v144
	v_rcp_f32_e32 v141, v141
	v_add_f32_e32 v142, 1.0, v142
	v_exp_f32_e32 v143, v143
	v_exp_f32_e32 v137, v137
	v_mul_f32_e32 v138, 0xbfb8aa3b, v138
	v_exp_f32_e32 v134, v134
; __device__ __forceinline__ unsigned cvt_pk_bf16(float lo, float hi) { f32x2_c v = {lo, hi}; bf16x2_c b = __builtin_convertvector(v, bf16x2_c); return __builtin_bit_cast(unsigned, b); }
; __device__ __forceinline__ float silu_f(float g) { return g * __builtin_amdgcn_rcpf(1.0f + __builtin_amdgcn_exp2f(-1.44269504f * g)); }
; __device__ __forceinline__ float sigmoid_f(float g) { return __builtin_amdgcn_rcpf(1.0f + __builtin_amdgcn_exp2f(-1.44269504f * g)); }
;     template <int TT> __device__ __forceinline__ void other(const f32x4 (&acc)[2][2][4][2], bf16_t* base, int row0, int col0, PG8_LAS float* my, int t, int hh, int wc, int fq) const {
;     ...
;             for (int m = 0; m < 4; ++m) { bf16_t* rowp = base + (size_t)(row0 + ai * HALF + m * 16) * LDT + col0;
;                 const float rs = my[(ai * 4 + m) * 16]; float ps = 0.f, pq = 0.f; u32x4 gq = {0u, 0u, 0u, 0u};
; #pragma unroll
;                 for (int bj = 0; bj < 2; ++bj) { f32x4 v0 = acc[ai][bj][m][0] * rs + bv[bj][0], v1 = acc[ai][bj][m][1] * rs + bv[bj][1];
;                     if (TT == 3) {
; #pragma unroll
;                         for (int j = 0; j < 4; ++j) { v0[j] = silu_f(v0[j]); v1[j] = silu_f(v1[j]); } }
;                     else if (TT == 4 || TT == 5) { f32x2 a = gelu_pk((f32x2){v0[0], v0[1]}), b = gelu_pk((f32x2){v0[2], v0[3]}), c = gelu_pk((f32x2){v1[0], v1[1]}), d = gelu_pk((f32x2){v1[2], v1[3]});
;     ...
;                     else if (TT >= 6) {
; #pragma unroll
;                         for (int j = 0; j < 4; ++j) { v0[j] = sigmoid_f(v0[j]); v1[j] = sigmoid_f(v1[j]); } }
;                     if (TT >= 6) { unsigned b0 = 0u, b1 = 0u;
; #pragma unroll
;                         for (int j = 0; j < 4; ++j) { b0 = __builtin_amdgcn_cvt_pk_u8_f32(__builtin_rintf(v0[j] * 255.0f), j, b0); b1 = __builtin_amdgcn_cvt_pk_u8_f32(__builtin_rintf(v1[j] * 255.0f), j, b1); }
;                         if (bj == 0) { gq.x = b0; gq.y = b1; } else { gq.z = b0; gq.w = b1; } }
;                     else { u32x4 w; w.x = cvt_pk_bf16(v0[0], v0[1]); w.y = cvt_pk_bf16(v0[2], v0[3]); w.z = cvt_pk_bf16(v1[0], v1[1]); w.w = cvt_pk_bf16(v1[2], v1[3]);
;                         *(u32x4*)(rowp + bj * HALF) = w; } }
;                 if (TT >= 6) *(u32x4*)((unsigned char*)base + (size_t)(row0 + ai * HALF + m * 16) * GATE_PITCH + hh * 256 + (wc * 4 + fq) * 16) = gq;
	v_rcp_f32_e32 v144, v144
	v_add_f32_e32 v145, 1.0, v145
	v_rcp_f32_e32 v142, v142
	v_mul_f32_e32 v147, 0xbfb8aa3b, v147
	v_exp_f32_e32 v138, v138
	v_mul_f32_e32 v139, 0xbfb8aa3b, v139
	v_rcp_f32_e32 v145, v145
	v_add_f32_e32 v146, 1.0, v146
	v_exp_f32_e32 v147, v147
	v_add_f32_e32 v132, 1.0, v132
	v_exp_f32_e32 v139, v139
	v_rcp_f32_e32 v146, v146
	v_mul_f32_e32 v140, 0x437f0000, v140
	v_add_f32_e32 v136, 1.0, v136
	v_rcp_f32_e32 v132, v132
	v_add_f32_e32 v133, 1.0, v133
	v_mul_f32_e32 v135, 0xbfb8aa3b, v135
	v_add_f32_e32 v143, 1.0, v143
	v_rndne_f32_e32 v140, v140
	v_mul_f32_e32 v141, 0x437f0000, v141
	v_rcp_f32_e32 v136, v136
	v_add_f32_e32 v137, 1.0, v137
	v_rcp_f32_e32 v133, v133
	v_add_f32_e32 v134, 1.0, v134
	v_exp_f32_e32 v135, v135
	v_rcp_f32_e32 v143, v143
	v_cvt_pk_u8_f32 v140, v140, 0, 0
	v_mul_f32_e32 v144, 0x437f0000, v144
	v_rndne_f32_e32 v141, v141
	v_mul_f32_e32 v142, 0x437f0000, v142
	v_rcp_f32_e32 v137, v137
	v_add_f32_e32 v138, 1.0, v138
	v_rcp_f32_e32 v134, v134
	v_add_f32_e32 v147, 1.0, v147
	v_rndne_f32_e32 v144, v144
	v_cvt_pk_u8_f32 v140, v141, 1, v140
	v_mul_f32_e32 v141, 0x437f0000, v145
	v_rndne_f32_e32 v142, v142
	v_rcp_f32_e32 v138, v138
	v_add_f32_e32 v139, 1.0, v139
	v_rcp_f32_e32 v147, v147
	v_cvt_pk_u8_f32 v144, v144, 0, 0
	v_rndne_f32_e32 v141, v141
	v_cvt_pk_u8_f32 v140, v142, 2, v140
	v_mul_f32_e32 v142, 0x437f0000, v146
	v_rcp_f32_e32 v139, v139
	v_mul_f32_e32 v132, 0x437f0000, v132
	v_cvt_pk_u8_f32 v141, v141, 1, v144
	v_rndne_f32_e32 v142, v142
	v_add_f32_e32 v135, 1.0, v135
	v_mul_f32_e32 v136, 0x437f0000, v136
	v_rndne_f32_e32 v132, v132
	v_mul_f32_e32 v133, 0x437f0000, v133
	v_cvt_pk_u8_f32 v141, v142, 2, v141
	v_mul_f32_e32 v142, 0x437f0000, v143
	v_rcp_f32_e32 v135, v135
	v_rndne_f32_e32 v136, v136
	v_cvt_pk_u8_f32 v132, v132, 0, 0
	v_mul_f32_e32 v137, 0x437f0000, v137
	v_rndne_f32_e32 v133, v133
	v_mul_f32_e32 v134, 0x437f0000, v134
	v_rndne_f32_e32 v142, v142
	v_cvt_pk_u8_f32 v136, v136, 0, 0
	v_rndne_f32_e32 v137, v137
	v_cvt_pk_u8_f32 v132, v133, 1, v132
	v_mul_f32_e32 v133, 0x437f0000, v138
	v_rndne_f32_e32 v134, v134
	v_cvt_pk_u8_f32 v140, v142, 3, v140
	v_mul_f32_e32 v142, 0x437f0000, v147
	v_cvt_pk_u8_f32 v136, v137, 1, v136
	v_rndne_f32_e32 v133, v133
	v_cvt_pk_u8_f32 v132, v134, 2, v132
	v_mul_f32_e32 v134, 0x437f0000, v139
	v_rndne_f32_e32 v142, v142
	v_cvt_pk_u8_f32 v133, v133, 2, v136
	v_rndne_f32_e32 v134, v134
	v_mad_i64_i32 v[150:151], s[2:3], v176, s4, v[152:153]
	v_cvt_pk_u8_f32 v141, v142, 3, v141
	v_cvt_pk_u8_f32 v142, v134, 3, v133
	v_mul_f32_e32 v133, 0x437f0000, v135
	global_store_dwordx4 v[150:151], v[154:157], off
	v_add_u32_e32 v150, 0xb0, v159
	v_rndne_f32_e32 v133, v133
	v_cvt_pk_u8_f32 v143, v133, 3, v132
	v_mad_i64_i32 v[132:133], s[2:3], v150, s4, v[152:153]
	global_store_dwordx4 v[132:133], v[140:143], off
	s_mov_b64 s[4:5], 0
.LBB0_354:
	s_andn2_b64 vcc, exec, s[4:5]
	s_cbranch_vccnz .LBB0_356
	v_mov_b32_e32 v150, v174
	v_mov_b32_e32 v151, v3
	v_mov_b32_e32 v132, v158
	ds_read2_b32 v[138:139], v199 offset1:16
	s_waitcnt lgkmcnt(0)
	v_ashrrev_i32_e32 v133, 31, v132
	v_lshl_add_u64 v[134:135], v[132:133], 1, s[28:29]
	v_and_b32_e32 v133, 64, v210
	v_xor_b32_e32 v132, 16, v210
	v_add_u32_e32 v133, 64, v133
	v_cmp_lt_i32_e32 vcc, v132, v133
	v_fma_f32 v142, v118, v138, 0
	v_fma_f32 v143, v119, v138, 0
	v_lshl_or_b32 v152, v151, 7, s23
	v_cndmask_b32_e32 v132, v210, v132, vcc
	v_lshlrev_b32_e32 v149, 2, v132
	v_xor_b32_e32 v132, 32, v210
	v_cmp_lt_i32_e32 vcc, v132, v133
	s_mov_b32 s4, 0x3e6d3388
	v_and_b32_e32 v185, 0x7fffffff, v143
	v_cndmask_b32_e32 v132, v210, v132, vcc
	v_and_b32_e32 v184, 0x7fffffff, v142
	v_lshlrev_b32_e32 v148, 2, v132
	v_lshl_add_u32 v132, v150, 3, v152
	v_fma_f32 v184, v184, s4, 1.0
	v_fma_f32 v185, v185, s4, 1.0
	v_ashrrev_i32_e32 v133, 31, v132
	v_fma_f32 v154, v120, v138, 0
	v_fma_f32 v155, v121, v138, 0
	v_rcp_f32_e32 v184, v184
	v_rcp_f32_e32 v185, v185
	v_lshlrev_b64 v[136:137], 5, v[132:133]
	v_mad_i64_i32 v[140:141], s[2:3], v150, s81, v[134:135]
	v_and_b32_e32 v133, 0x7fffffff, v155
	v_and_b32_e32 v132, 0x7fffffff, v154
	v_fma_f32 v132, v132, s4, 1.0
	v_fma_f32 v133, v133, s4, 1.0
	s_mov_b32 s2, 0xbf3a00e3
	v_rcp_f32_e32 v156, v132
	v_rcp_f32_e32 v157, v133
	v_mov_b64_e32 v[132:133], s[2:3]
	s_mov_b32 s46, 0x3f07dc22
	s_mov_b32 s48, 0x3f35f0e3
	v_fma_f32 v186, v184, s46, v132
	v_fma_f32 v187, v185, s46, v132
	s_mov_b32 s50, 0xbe11a98e
	v_fma_f32 v186, v184, v186, s48
	v_fma_f32 v187, v185, v187, s48
	s_mov_b32 s52, 0x3e027906
	v_fma_f32 v186, v184, v186, s50
	v_fma_f32 v187, v185, v187, s50
	v_fma_f32 v190, v130, v138, 0
	v_fma_f32 v191, v131, v138, 0
	v_fma_f32 v144, v122, v138, 0
	v_fma_f32 v145, v123, v138, 0
	v_fma_f32 v186, v184, v186, s52
	v_fma_f32 v187, v185, v187, s52
	v_and_b32_e32 v207, 0x7fffffff, v191
	v_and_b32_e32 v206, 0x7fffffff, v190
	v_and_b32_e32 v177, 0x7fffffff, v145
	v_and_b32_e32 v176, 0x7fffffff, v144
	v_mul_f32_e64 v184, v184, v186
	v_mul_f32_e64 v185, v185, v187
	v_fma_f32 v186, v128, v138, 0
	v_fma_f32 v187, v129, v138, 0
	v_fma_f32 v206, v206, s4, 1.0
	v_fma_f32 v207, v207, s4, 1.0
	v_fma_f32 v176, v176, s4, 1.0
	v_fma_f32 v177, v177, s4, 1.0
	v_and_b32_e32 v189, 0x7fffffff, v187
	v_and_b32_e32 v188, 0x7fffffff, v186
	v_rcp_f32_e32 v206, v206
	v_rcp_f32_e32 v207, v207
	v_rcp_f32_e32 v176, v176
	v_rcp_f32_e32 v177, v177
	v_fma_f32 v188, v188, s4, 1.0
	v_fma_f32 v189, v189, s4, 1.0
	v_fma_f32 v192, v126, v138, 0
	v_fma_f32 v193, v127, v138, 0
	v_rcp_f32_e32 v188, v188
	v_rcp_f32_e32 v189, v189
	v_fma_f32 v208, v206, s46, v132
	v_fma_f32 v209, v207, s46, v132
	v_and_b32_e32 v219, 0x7fffffff, v193
; __device__ __forceinline__ f32x2 gelu_pk(f32x2 v) {
;     const f32x2 av = __builtin_elementwise_abs(v), d = av * 0.2316418882f + 1.0f;
;     f32x2 t; t.x = __builtin_amdgcn_rcpf(d.x); t.y = __builtin_amdgcn_rcpf(d.y);
;     f32x2 q = t * 0.5307027145f + (-0.7265760135f); q = q * t + 0.7107068705f; q = q * t + (-0.142248368f); q = q * t + 0.127414796f; q = q * t;
;     const f32x2 s = (v * v) * (-0.72134752044f);
;     f32x2 e; e.x = __builtin_amdgcn_exp2f(s.x); e.y = __builtin_amdgcn_exp2f(s.y);
;     const f32x2 m = v * (q * e), r = v - m;
;     f32x2 o; o.x = v.x < 0.f ? m.x : r.x; o.y = v.y < 0.f ? m.y : r.y; return o;
; }
	v_and_b32_e32 v218, 0x7fffffff, v192
	v_fma_f32 v178, v176, s46, v132
	v_fma_f32 v179, v177, s46, v132
	v_fma_f32 v208, v206, v208, s48
	v_fma_f32 v209, v207, v209, s48
	v_fma_f32 v218, v218, s4, 1.0
	v_fma_f32 v219, v219, s4, 1.0
	s_mov_b32 s54, 0xbf38aa3b
	v_fma_f32 v178, v176, v178, s48
	v_fma_f32 v179, v177, v179, s48
	v_fma_f32 v202, v188, s46, v132
	v_fma_f32 v203, v189, s46, v132
	v_mul_f32_e64 v204, v186, v186
	v_mul_f32_e64 v205, v187, v187
	v_fma_f32 v208, v206, v208, s50
	v_fma_f32 v209, v207, v209, s50
	v_rcp_f32_e32 v218, v218
	v_rcp_f32_e32 v219, v219
	v_fma_f32 v160, v156, s46, v132
	v_fma_f32 v161, v157, s46, v132
	v_mul_f32_e64 v162, v154, v154
	v_mul_f32_e64 v163, v155, v155
	v_fma_f32 v178, v176, v178, s50
	v_fma_f32 v179, v177, v179, s50
	v_fma_f32 v194, v124, v138, 0
	v_fma_f32 v195, v125, v138, 0
	v_fma_f32 v202, v188, v202, s48
	v_fma_f32 v203, v189, v203, s48
	v_mul_f32_e64 v204, v204, s54
	v_mul_f32_e64 v205, v205, s54
	v_fma_f32 v208, v206, v208, s52
	v_fma_f32 v209, v207, v209, s52
	v_fma_f32 v146, v116, v138, 0
	v_fma_f32 v147, v117, v138, 0
	v_fma_f32 v160, v156, v160, s48
	v_fma_f32 v161, v157, v161, s48
	v_mul_f32_e64 v162, v162, s54
	v_mul_f32_e64 v163, v163, s54
	v_fma_f32 v178, v176, v178, s52
	v_fma_f32 v179, v177, v179, s52
	v_fma_f32 v202, v188, v202, s50
	v_fma_f32 v203, v189, v203, s50
	v_exp_f32_e32 v204, v204
	v_exp_f32_e32 v205, v205
	v_mul_f32_e64 v206, v206, v208
	v_mul_f32_e64 v207, v207, v209
	v_and_b32_e32 v209, 0x7fffffff, v195
	v_and_b32_e32 v208, 0x7fffffff, v194
	v_fma_f32 v160, v156, v160, s50
	v_fma_f32 v161, v157, v161, s50
	v_exp_f32_e32 v162, v162
	v_exp_f32_e32 v163, v163
	v_mul_f32_e64 v176, v176, v178
	v_mul_f32_e64 v177, v177, v179
	v_and_b32_e32 v179, 0x7fffffff, v147
	v_and_b32_e32 v178, 0x7fffffff, v146
	v_fma_f32 v202, v188, v202, s52
	v_fma_f32 v203, v189, v203, s52
	v_fma_f32 v208, v208, s4, 1.0
	v_fma_f32 v209, v209, s4, 1.0
	v_fma_f32 v160, v156, v160, s52
	v_fma_f32 v161, v157, v161, s52
	v_fma_f32 v178, v178, s4, 1.0
	v_fma_f32 v179, v179, s4, 1.0
	v_mul_f32_e64 v188, v188, v202
	v_mul_f32_e64 v189, v189, v203
	v_mul_f32_e64 v202, v190, v190
	v_mul_f32_e64 v203, v191, v191
	v_rcp_f32_e32 v208, v208
	v_rcp_f32_e32 v209, v209
	v_fma_f32 v220, v218, s46, v132
	v_fma_f32 v221, v219, s46, v132
	v_mul_f32_e64 v156, v156, v160
	v_mul_f32_e64 v157, v157, v161
	v_mul_f32_e64 v160, v144, v144
	v_mul_f32_e64 v161, v145, v145
	v_rcp_f32_e32 v178, v178
	v_rcp_f32_e32 v179, v179
	v_mul_f32_e64 v202, v202, s54
	v_mul_f32_e64 v203, v203, s54
	v_fma_f32 v220, v218, v220, s48
	v_fma_f32 v221, v219, v221, s48
	v_mul_f32_e64 v160, v160, s54
	v_mul_f32_e64 v161, v161, s54
	v_mul_f32_e64 v188, v204, v188
	v_mul_f32_e64 v189, v205, v189
	v_exp_f32_e32 v202, v202
	v_exp_f32_e32 v203, v203
	v_fma_f32 v220, v218, v220, s50
	v_fma_f32 v221, v219, v221, s50
	v_mul_f32_e64 v156, v162, v156
	v_mul_f32_e64 v157, v163, v157
	v_exp_f32_e32 v160, v160
	v_exp_f32_e32 v161, v161
	v_mul_f32_e64 v204, v186, v188
	v_mul_f32_e64 v205, v187, v189
	v_fma_f32 v188, -v186, v188, v186
	v_fma_f32 v189, -v187, v189, v187
	v_fma_f32 v220, v218, v220, s52
	v_fma_f32 v221, v219, v221, s52
	v_cmp_gt_f32_e32 vcc, 0, v186
	v_mul_f32_e64 v162, v154, v156
	v_mul_f32_e64 v163, v155, v157
	v_fma_f32 v156, -v154, v156, v154
	v_fma_f32 v157, -v155, v157, v155
	v_fma_f32 v214, v208, s46, v132
	v_fma_f32 v215, v209, s46, v132
	v_mul_f32_e64 v216, v194, v194
	v_mul_f32_e64 v217, v195, v195
	v_mul_f32_e64 v218, v218, v220
	v_mul_f32_e64 v219, v219, v221
	v_cndmask_b32_e32 v221, v188, v204, vcc
	v_cmp_gt_f32_e32 vcc, 0, v154
	v_fma_f32 v180, v178, s46, v132
	v_fma_f32 v181, v179, s46, v132
	v_mul_f32_e64 v182, v146, v146
	v_mul_f32_e64 v183, v147, v147
	v_fma_f32 v214, v208, v214, s48
	v_fma_f32 v215, v209, v215, s48
	v_mul_f32_e64 v216, v216, s54
	v_mul_f32_e64 v217, v217, s54
	v_cndmask_b32_e32 v220, v156, v162, vcc
	v_cmp_gt_f32_e32 vcc, 0, v187
	v_fma_f32 v180, v178, v180, s48
	v_fma_f32 v181, v179, v181, s48
	v_mul_f32_e64 v182, v182, s54
	v_mul_f32_e64 v183, v183, s54
	v_mul_f32_e64 v202, v202, v206
	v_mul_f32_e64 v203, v203, v207
	v_fma_f32 v214, v208, v214, s50
	v_fma_f32 v215, v209, v215, s50
	v_exp_f32_e32 v216, v216
	v_exp_f32_e32 v217, v217
	v_cndmask_b32_e32 v187, v189, v205, vcc
	v_cmp_gt_f32_e32 vcc, 0, v155
	v_mul_f32_e64 v160, v160, v176
	v_mul_f32_e64 v161, v161, v177
	v_fma_f32 v180, v178, v180, s50
	v_fma_f32 v181, v179, v181, s50
	v_exp_f32_e32 v182, v182
	v_exp_f32_e32 v183, v183
	v_mul_f32_e64 v206, v190, v202
	v_mul_f32_e64 v207, v191, v203
	v_fma_f32 v202, -v190, v202, v190
	v_fma_f32 v203, -v191, v203, v191
	v_fma_f32 v214, v208, v214, s52
	v_fma_f32 v215, v209, v215, s52
	v_cndmask_b32_e32 v186, v157, v163, vcc
	v_cmp_gt_f32_e32 vcc, 0, v190
	v_mul_f32_e64 v176, v144, v160
	v_mul_f32_e64 v177, v145, v161
	v_fma_f32 v160, -v144, v160, v144
	v_fma_f32 v161, -v145, v161, v145
	v_fma_f32 v180, v178, v180, s52
	v_fma_f32 v181, v179, v181, s52
	v_mul_f32_e64 v208, v208, v214
	v_mul_f32_e64 v209, v209, v215
	v_mul_f32_e64 v214, v192, v192
	v_mul_f32_e64 v215, v193, v193
	v_cndmask_b32_e32 v155, v202, v206, vcc
	v_cmp_gt_f32_e32 vcc, 0, v144
	v_mul_f32_e64 v178, v178, v180
	v_mul_f32_e64 v179, v179, v181
	v_mul_f32_e64 v180, v142, v142
	v_mul_f32_e64 v181, v143, v143
	v_mul_f32_e64 v214, v214, s54
	v_mul_f32_e64 v215, v215, s54
	v_cndmask_b32_e32 v154, v160, v176, vcc
	v_cmp_gt_f32_e32 vcc, 0, v191
	v_mul_f32_e64 v180, v180, s54
	v_mul_f32_e64 v181, v181, s54
	v_mul_f32_e64 v208, v216, v208
	v_mul_f32_e64 v209, v217, v209
	v_exp_f32_e32 v214, v214
	v_exp_f32_e32 v215, v215
	v_cndmask_b32_e32 v157, v203, v207, vcc
;     template <int TT> __device__ __forceinline__ void other(const f32x4 (&acc)[2][2][4][2], bf16_t* base, int row0, int col0, PG8_LAS float* my, int t, int hh, int wc, int fq) const {
;     ...
;                 for (int bj = 0; bj < 2; ++bj) { f32x4 v0 = acc[ai][bj][m][0] * rs + bv[bj][0], v1 = acc[ai][bj][m][1] * rs + bv[bj][1];
;                     if (TT == 3) {
; #pragma unroll
;                         for (int j = 0; j < 4; ++j) { v0[j] = silu_f(v0[j]); v1[j] = silu_f(v1[j]); } }
;                     else if (TT == 4 || TT == 5) { f32x2 a = gelu_pk((f32x2){v0[0], v0[1]}), b = gelu_pk((f32x2){v0[2], v0[3]}), c = gelu_pk((f32x2){v1[0], v1[1]}), d = gelu_pk((f32x2){v1[2], v1[3]});
;                         v0 = (f32x4){a.x, a.y, b.x, b.y}; v1 = (f32x4){c.x, c.y, d.x, d.y};
;                         if (TT == 5) { ps += ((v0[0] + v0[1]) + (v0[2] + v0[3])) + ((v1[0] + v1[1]) + (v1[2] + v1[3]));
;                             pq += ((v0[0] * v0[0] + v0[1] * v0[1]) + (v0[2] * v0[2] + v0[3] * v0[3])) + ((v1[0] * v1[0] + v1[1] * v1[1]) + (v1[2] * v1[2] + v1[3] * v1[3])); } }
;                     else if (TT >= 6) {
; #pragma unroll
;                         for (int j = 0; j < 4; ++j) { v0[j] = sigmoid_f(v0[j]); v1[j] = sigmoid_f(v1[j]); } }
;                     if (TT >= 6) { unsigned b0 = 0u, b1 = 0u;
; #pragma unroll
;                         for (int j = 0; j < 4; ++j) { b0 = __builtin_amdgcn_cvt_pk_u8_f32(__builtin_rintf(v0[j] * 255.0f), j, b0); b1 = __builtin_amdgcn_cvt_pk_u8_f32(__builtin_rintf(v1[j] * 255.0f), j, b1); }
;                         if (bj == 0) { gq.x = b0; gq.y = b1; } else { gq.z = b0; gq.w = b1; } }
;                     else { u32x4 w; w.x = cvt_pk_bf16(v0[0], v0[1]); w.y = cvt_pk_bf16(v0[2], v0[3]); w.z = cvt_pk_bf16(v1[0], v1[1]); w.w = cvt_pk_bf16(v1[2], v1[3]);
;                         *(u32x4*)(rowp + bj * HALF) = w; } }
;                 if (TT >= 6) *(u32x4*)((unsigned char*)base + (size_t)(row0 + ai * HALF + m * 16) * GATE_PITCH + hh * 256 + (wc * 4 + fq) * 16) = gq;
;                 if (TT == 5) { ps += __shfl_xor(ps, 16); pq += __shfl_xor(pq, 16); ps += __shfl_xor(ps, 32); pq += __shfl_xor(pq, 32);
;                     if (m == 0 || fq == m) { psm = ps; pqm = pq; }
;                     if (m == 3) *(f32x2*)(sgst + ((size_t)((row0 + ai * HALF + fq * 16) * 8 + hh) * 4 + wc) * 2) = (f32x2){psm, pqm}; } }
	v_cmp_gt_f32_e32 vcc, 0, v145
	v_mul_f32_e64 v178, v182, v178
	v_mul_f32_e64 v179, v183, v179
	v_exp_f32_e32 v180, v180
	v_exp_f32_e32 v181, v181
	v_mul_f32_e64 v216, v194, v208
	v_mul_f32_e64 v217, v195, v209
	v_fma_f32 v208, -v194, v208, v194
	v_fma_f32 v209, -v195, v209, v195
	v_cndmask_b32_e32 v156, v161, v177, vcc
	v_cmp_gt_f32_e32 vcc, 0, v194
	v_mul_f32_e64 v182, v146, v178
	v_mul_f32_e64 v183, v147, v179
	v_fma_f32 v178, -v146, v178, v146
	v_fma_f32 v179, -v147, v179, v147
	v_cndmask_b32_e32 v161, v208, v216, vcc
	v_cmp_gt_f32_e32 vcc, 0, v146
	v_mul_f32_e64 v214, v214, v218
	v_mul_f32_e64 v215, v215, v219
	v_mul_f32_e64 v180, v180, v184
	v_mul_f32_e64 v181, v181, v185
	v_cndmask_b32_e32 v160, v178, v182, vcc
	v_cmp_gt_f32_e32 vcc, 0, v195
	v_mul_f32_e64 v218, v192, v214
	v_mul_f32_e64 v219, v193, v215
	v_fma_f32 v214, -v192, v214, v192
	v_fma_f32 v215, -v193, v215, v193
	v_cndmask_b32_e32 v163, v209, v217, vcc
	v_cmp_gt_f32_e32 vcc, 0, v147
	v_mul_f32_e64 v184, v142, v180
	v_mul_f32_e64 v185, v143, v181
	v_fma_f32 v180, -v142, v180, v142
	v_fma_f32 v181, -v143, v181, v143
	v_cndmask_b32_e32 v162, v179, v183, vcc
	v_cmp_gt_f32_e32 vcc, 0, v192
	v_add_f32_e64 v178, v220, v186
	v_add_f32_e64 v179, v221, v187
	v_cvt_pk_bf16_f32 v144, v160, v162
	v_cndmask_b32_e32 v147, v214, v218, vcc
	v_cmp_gt_f32_e32 vcc, 0, v142
	v_cvt_pk_bf16_f32 v142, v220, v186
	v_lshl_add_u64 v[136:137], s[20:21], 0, v[136:137]
	v_cndmask_b32_e32 v146, v180, v184, vcc
	v_cmp_gt_f32_e32 vcc, 0, v193
	s_nop 1
	v_cndmask_b32_e32 v177, v215, v219, vcc
	v_cmp_gt_f32_e32 vcc, 0, v143
	v_cvt_pk_bf16_f32 v143, v154, v156
	s_nop 0
	v_cndmask_b32_e32 v176, v181, v185, vcc
	v_add_f32_e64 v180, v154, v156
	v_add_f32_e64 v181, v155, v157
	v_add_f32_e64 v182, v146, v176
	v_add_f32_e64 v183, v147, v177
	v_add_f32_e64 v178, v178, v180
	v_add_f32_e64 v179, v179, v181
	v_add_f32_e64 v180, v160, v162
	v_add_f32_e64 v181, v161, v163
	v_cvt_pk_bf16_f32 v145, v146, v176
	v_add_f32_e64 v180, v180, v182
	v_add_f32_e64 v181, v181, v183
	v_mul_f32_e64 v182, v176, v176
	v_mul_f32_e64 v183, v177, v177
	v_add_f32_e64 v178, v178, v180
	v_add_f32_e64 v179, v179, v181
	v_mul_f32_e64 v180, v156, v156
	v_mul_f32_e64 v181, v157, v157
	v_add_f32_e32 v138, 0, v178
	v_add_f32_e32 v138, v179, v138
	v_mul_f32_e64 v178, v186, v186
	v_mul_f32_e64 v179, v187, v187
	v_fma_f32 v180, v154, v154, v180
	v_fma_f32 v181, v155, v155, v181
	v_fma_f32 v178, v220, v220, v178
	v_fma_f32 v179, v221, v221, v179
	v_fma_f32 v182, v146, v146, v182
	v_fma_f32 v183, v147, v147, v183
	v_add_f32_e64 v178, v178, v180
	v_add_f32_e64 v179, v179, v181
	v_mul_f32_e64 v180, v162, v162
	v_mul_f32_e64 v181, v163, v163
	ds_bpermute_b32 v153, v149, v138
	v_fma_f32 v180, v160, v160, v180
	v_fma_f32 v181, v161, v161, v181
	global_store_dwordx4 v[140:141], v[142:145], off
	v_add_f32_e64 v180, v180, v182
	v_add_f32_e64 v181, v181, v183
	s_waitcnt lgkmcnt(0)
	v_add_f32_e32 v138, v138, v153
	v_add_f32_e64 v178, v178, v180
	v_add_f32_e64 v179, v179, v181
	ds_bpermute_b32 v153, v148, v138
	v_add_f32_e32 v146, v178, v179
	ds_bpermute_b32 v154, v149, v146
	v_cvt_pk_bf16_f32 v142, v221, v187
	v_cvt_pk_bf16_f32 v143, v155, v157
	v_cvt_pk_bf16_f32 v144, v161, v163
	v_cvt_pk_bf16_f32 v145, v147, v177
	s_waitcnt lgkmcnt(0)
	v_add_f32_e32 v146, v146, v154
	ds_bpermute_b32 v154, v148, v146
	global_store_dwordx4 v[140:141], v[142:145], off offset:256
	v_add_f32_e32 v153, v138, v153
	v_add_u32_e32 v138, 16, v150
	v_mov_b32_e32 v142, v139
	v_fma_f32 v144, v104, v142, 0
	v_fma_f32 v145, v105, v142, 0
	v_mad_i64_i32 v[140:141], s[2:3], v138, s81, v[134:135]
	v_and_b32_e32 v139, 0x7fffffff, v145
	v_and_b32_e32 v138, 0x7fffffff, v144
	v_fma_f32 v138, v138, s4, 1.0
	v_fma_f32 v139, v139, s4, 1.0
	s_waitcnt lgkmcnt(0)
	v_add_f32_e32 v159, v146, v154
	v_rcp_f32_e32 v146, v138
	v_rcp_f32_e32 v147, v139
	v_fma_f32 v138, v102, v142, 0
	v_fma_f32 v139, v103, v142, 0
	v_fma_f32 v190, v114, v142, 0
	v_fma_f32 v191, v115, v142, 0
	v_and_b32_e32 v185, 0x7fffffff, v139
	v_and_b32_e32 v184, 0x7fffffff, v138
	v_fma_f32 v184, v184, s4, 1.0
	v_fma_f32 v185, v185, s4, 1.0
	v_fma_f32 v154, v106, v142, 0
	v_fma_f32 v155, v107, v142, 0
	v_rcp_f32_e32 v184, v184
	v_rcp_f32_e32 v185, v185
	v_and_b32_e32 v205, 0x7fffffff, v191
	v_and_b32_e32 v204, 0x7fffffff, v190
	v_and_b32_e32 v177, 0x7fffffff, v155
	v_fma_f32 v186, v184, s46, v132
	v_fma_f32 v187, v185, s46, v132
	v_and_b32_e32 v176, 0x7fffffff, v154
	v_fma_f32 v186, v184, v186, s48
	v_fma_f32 v187, v185, v187, s48
	v_fma_f32 v204, v204, s4, 1.0
	v_fma_f32 v205, v205, s4, 1.0
	v_fma_f32 v186, v184, v186, s50
	v_fma_f32 v187, v185, v187, s50
	v_fma_f32 v176, v176, s4, 1.0
	v_fma_f32 v177, v177, s4, 1.0
	v_fma_f32 v186, v184, v186, s52
	v_fma_f32 v187, v185, v187, s52
	v_rcp_f32_e32 v204, v204
	v_mul_f32_e64 v184, v184, v186
	v_mul_f32_e64 v185, v185, v187
	v_fma_f32 v186, v112, v142, 0
	v_fma_f32 v187, v113, v142, 0
	v_rcp_f32_e32 v205, v205
	v_and_b32_e32 v189, 0x7fffffff, v187
	v_and_b32_e32 v188, 0x7fffffff, v186
	v_rcp_f32_e32 v176, v176
	v_rcp_f32_e32 v177, v177
	v_fma_f32 v188, v188, s4, 1.0
	v_fma_f32 v189, v189, s4, 1.0
	v_fma_f32 v192, v110, v142, 0
	v_fma_f32 v193, v111, v142, 0
	v_rcp_f32_e32 v188, v188
	v_rcp_f32_e32 v189, v189
	v_fma_f32 v206, v204, s46, v132
	v_fma_f32 v207, v205, s46, v132
	v_and_b32_e32 v217, 0x7fffffff, v193
	v_and_b32_e32 v216, 0x7fffffff, v192
	v_fma_f32 v178, v176, s46, v132
	v_fma_f32 v179, v177, s46, v132
	v_fma_f32 v206, v204, v206, s48
	v_fma_f32 v207, v205, v207, s48
	v_fma_f32 v216, v216, s4, 1.0
	v_fma_f32 v217, v217, s4, 1.0
	v_fma_f32 v178, v176, v178, s48
	v_fma_f32 v179, v177, v179, s48
; __device__ __forceinline__ float silu_f(float g) { return g * __builtin_amdgcn_rcpf(1.0f + __builtin_amdgcn_exp2f(-1.44269504f * g)); }
; __device__ __forceinline__ f32x2 gelu_pk(f32x2 v) {
;     const f32x2 av = __builtin_elementwise_abs(v), d = av * 0.2316418882f + 1.0f;
;     f32x2 t; t.x = __builtin_amdgcn_rcpf(d.x); t.y = __builtin_amdgcn_rcpf(d.y);
;     f32x2 q = t * 0.5307027145f + (-0.7265760135f); q = q * t + 0.7107068705f; q = q * t + (-0.142248368f); q = q * t + 0.127414796f; q = q * t;
;     const f32x2 s = (v * v) * (-0.72134752044f);
;     f32x2 e; e.x = __builtin_amdgcn_exp2f(s.x); e.y = __builtin_amdgcn_exp2f(s.y);
;     const f32x2 m = v * (q * e), r = v - m;
;     f32x2 o; o.x = v.x < 0.f ? m.x : r.x; o.y = v.y < 0.f ? m.y : r.y; return o;
; }
;     template <int TT> __device__ __forceinline__ void other(const f32x4 (&acc)[2][2][4][2], bf16_t* base, int row0, int col0, PG8_LAS float* my, int t, int hh, int wc, int fq) const {
;     ...
;                 for (int bj = 0; bj < 2; ++bj) { f32x4 v0 = acc[ai][bj][m][0] * rs + bv[bj][0], v1 = acc[ai][bj][m][1] * rs + bv[bj][1];
;                     if (TT == 3) {
; #pragma unroll
;                         for (int j = 0; j < 4; ++j) { v0[j] = silu_f(v0[j]); v1[j] = silu_f(v1[j]); } }
;                     else if (TT == 4 || TT == 5) { f32x2 a = gelu_pk((f32x2){v0[0], v0[1]}), b = gelu_pk((f32x2){v0[2], v0[3]}), c = gelu_pk((f32x2){v1[0], v1[1]}), d = gelu_pk((f32x2){v1[2], v1[3]});
;                         v0 = (f32x4){a.x, a.y, b.x, b.y}; v1 = (f32x4){c.x, c.y, d.x, d.y};
	v_fma_f32 v194, v188, s46, v132
	v_fma_f32 v195, v189, s46, v132
	v_mul_f32_e64 v202, v186, v186
	v_mul_f32_e64 v203, v187, v187
	v_fma_f32 v206, v204, v206, s50
	v_fma_f32 v207, v205, v207, s50
	v_rcp_f32_e32 v216, v216
	v_rcp_f32_e32 v217, v217
	v_fma_f32 v156, v100, v142, 0
	v_fma_f32 v157, v101, v142, 0
	v_fma_f32 v160, v146, s46, v132
	v_fma_f32 v161, v147, s46, v132
	v_mul_f32_e64 v162, v144, v144
	v_mul_f32_e64 v163, v145, v145
	v_fma_f32 v178, v176, v178, s50
	v_fma_f32 v179, v177, v179, s50
	v_fma_f32 v143, v109, v142, 0
	v_fma_f32 v142, v108, v142, 0
	v_fma_f32 v194, v188, v194, s48
	v_fma_f32 v195, v189, v195, s48
	v_mul_f32_e64 v202, v202, s54
	v_mul_f32_e64 v203, v203, s54
	v_fma_f32 v206, v204, v206, s52
	v_fma_f32 v207, v205, v207, s52
	v_fma_f32 v160, v146, v160, s48
	v_fma_f32 v161, v147, v161, s48
	v_mul_f32_e64 v162, v162, s54
	v_mul_f32_e64 v163, v163, s54
	v_fma_f32 v178, v176, v178, s52
	v_fma_f32 v179, v177, v179, s52
	v_fma_f32 v194, v188, v194, s50
	v_fma_f32 v195, v189, v195, s50
	v_exp_f32_e32 v202, v202
	v_exp_f32_e32 v203, v203
	v_mul_f32_e64 v204, v204, v206
	v_mul_f32_e64 v205, v205, v207
	v_and_b32_e32 v207, 0x7fffffff, v143
	v_and_b32_e32 v206, 0x7fffffff, v142
	v_fma_f32 v160, v146, v160, s50
	v_fma_f32 v161, v147, v161, s50
	v_exp_f32_e32 v162, v162
	v_exp_f32_e32 v163, v163
	v_mul_f32_e64 v176, v176, v178
	v_mul_f32_e64 v177, v177, v179
	v_and_b32_e32 v179, 0x7fffffff, v157
	v_and_b32_e32 v178, 0x7fffffff, v156
	v_fma_f32 v194, v188, v194, s52
	v_fma_f32 v195, v189, v195, s52
	v_fma_f32 v206, v206, s4, 1.0
	v_fma_f32 v207, v207, s4, 1.0
	v_fma_f32 v160, v146, v160, s52
	v_fma_f32 v161, v147, v161, s52
	v_fma_f32 v178, v178, s4, 1.0
	v_fma_f32 v179, v179, s4, 1.0
	v_mul_f32_e64 v188, v188, v194
	v_mul_f32_e64 v189, v189, v195
	v_mul_f32_e64 v194, v190, v190
	v_mul_f32_e64 v195, v191, v191
	v_rcp_f32_e32 v206, v206
	v_rcp_f32_e32 v207, v207
	v_fma_f32 v218, v216, s46, v132
	v_fma_f32 v219, v217, s46, v132
	v_mul_f32_e64 v146, v146, v160
	v_mul_f32_e64 v147, v147, v161
	v_mul_f32_e64 v160, v154, v154
	v_mul_f32_e64 v161, v155, v155
	v_rcp_f32_e32 v178, v178
	v_rcp_f32_e32 v179, v179
	v_mul_f32_e64 v194, v194, s54
	v_mul_f32_e64 v195, v195, s54
	v_fma_f32 v218, v216, v218, s48
	v_fma_f32 v219, v217, v219, s48
	v_mul_f32_e64 v160, v160, s54
	v_mul_f32_e64 v161, v161, s54
	v_mul_f32_e64 v188, v202, v188
	v_mul_f32_e64 v189, v203, v189
	v_exp_f32_e32 v194, v194
	v_exp_f32_e32 v195, v195
	v_fma_f32 v218, v216, v218, s50
	v_fma_f32 v219, v217, v219, s50
	v_mul_f32_e64 v146, v162, v146
	v_mul_f32_e64 v147, v163, v147
	v_exp_f32_e32 v160, v160
	v_exp_f32_e32 v161, v161
	v_mul_f32_e64 v202, v186, v188
	v_mul_f32_e64 v203, v187, v189
	v_fma_f32 v188, -v186, v188, v186
	v_fma_f32 v189, -v187, v189, v187
	v_fma_f32 v218, v216, v218, s52
	v_fma_f32 v219, v217, v219, s52
	v_cmp_gt_f32_e32 vcc, 0, v186
	v_mul_f32_e64 v162, v144, v146
	v_mul_f32_e64 v163, v145, v147
	v_fma_f32 v146, -v144, v146, v144
	v_fma_f32 v147, -v145, v147, v145
	v_fma_f32 v208, v206, s46, v132
	v_fma_f32 v209, v207, s46, v132
	v_mul_f32_e64 v214, v142, v142
	v_mul_f32_e64 v215, v143, v143
	v_mul_f32_e64 v216, v216, v218
	v_mul_f32_e64 v217, v217, v219
	v_cndmask_b32_e32 v219, v188, v202, vcc
	v_cmp_gt_f32_e32 vcc, 0, v144
	v_fma_f32 v180, v178, s46, v132
	v_fma_f32 v181, v179, s46, v132
	v_mul_f32_e64 v182, v156, v156
	v_mul_f32_e64 v183, v157, v157
	v_fma_f32 v208, v206, v208, s48
	v_fma_f32 v209, v207, v209, s48
	v_mul_f32_e64 v214, v214, s54
	v_mul_f32_e64 v215, v215, s54
	v_cndmask_b32_e32 v218, v146, v162, vcc
	v_cmp_gt_f32_e32 vcc, 0, v187
	v_fma_f32 v180, v178, v180, s48
	v_fma_f32 v181, v179, v181, s48
	v_mul_f32_e64 v182, v182, s54
	v_mul_f32_e64 v183, v183, s54
	v_mul_f32_e64 v194, v194, v204
	v_mul_f32_e64 v195, v195, v205
	v_fma_f32 v208, v206, v208, s50
	v_fma_f32 v209, v207, v209, s50
	v_exp_f32_e32 v214, v214
	v_exp_f32_e32 v215, v215
	v_cndmask_b32_e32 v187, v189, v203, vcc
	v_cmp_gt_f32_e32 vcc, 0, v145
	v_mul_f32_e64 v160, v160, v176
	v_mul_f32_e64 v161, v161, v177
	v_fma_f32 v180, v178, v180, s50
	v_fma_f32 v181, v179, v181, s50
	v_exp_f32_e32 v182, v182
	v_exp_f32_e32 v183, v183
	v_mul_f32_e64 v204, v190, v194
	v_mul_f32_e64 v205, v191, v195
	v_fma_f32 v194, -v190, v194, v190
	v_fma_f32 v195, -v191, v195, v191
	v_fma_f32 v208, v206, v208, s52
	v_fma_f32 v209, v207, v209, s52
	v_cndmask_b32_e32 v186, v147, v163, vcc
	v_cmp_gt_f32_e32 vcc, 0, v190
	v_mul_f32_e64 v176, v154, v160
	v_mul_f32_e64 v177, v155, v161
	v_fma_f32 v160, -v154, v160, v154
	v_fma_f32 v161, -v155, v161, v155
	v_fma_f32 v180, v178, v180, s52
	v_fma_f32 v181, v179, v181, s52
	v_mul_f32_e64 v206, v206, v208
	v_mul_f32_e64 v207, v207, v209
	v_mul_f32_e64 v208, v192, v192
	v_mul_f32_e64 v209, v193, v193
	v_cndmask_b32_e32 v147, v194, v204, vcc
	v_cmp_gt_f32_e32 vcc, 0, v154
	v_mul_f32_e64 v178, v178, v180
	v_mul_f32_e64 v179, v179, v181
	v_mul_f32_e64 v180, v138, v138
	v_mul_f32_e64 v181, v139, v139
	v_mul_f32_e64 v208, v208, s54
	v_mul_f32_e64 v209, v209, s54
	v_cndmask_b32_e32 v146, v160, v176, vcc
	v_cmp_gt_f32_e32 vcc, 0, v191
	v_mul_f32_e64 v180, v180, s54
	v_mul_f32_e64 v181, v181, s54
	v_mul_f32_e64 v206, v214, v206
	v_mul_f32_e64 v207, v215, v207
	v_exp_f32_e32 v208, v208
	v_exp_f32_e32 v209, v209
	v_cndmask_b32_e32 v163, v195, v205, vcc
	v_cmp_gt_f32_e32 vcc, 0, v155
	v_mul_f32_e64 v178, v182, v178
	v_mul_f32_e64 v179, v183, v179
	v_exp_f32_e32 v180, v180
	v_exp_f32_e32 v181, v181
	v_mul_f32_e64 v214, v142, v206
	v_mul_f32_e64 v215, v143, v207
	v_fma_f32 v206, -v142, v206, v142
	v_fma_f32 v207, -v143, v207, v143
	v_cndmask_b32_e32 v162, v161, v177, vcc
;     template <int TT> __device__ __forceinline__ void other(const f32x4 (&acc)[2][2][4][2], bf16_t* base, int row0, int col0, PG8_LAS float* my, int t, int hh, int wc, int fq) const {
;     ...
;                 for (int bj = 0; bj < 2; ++bj) { f32x4 v0 = acc[ai][bj][m][0] * rs + bv[bj][0], v1 = acc[ai][bj][m][1] * rs + bv[bj][1];
;                     if (TT == 3) {
; #pragma unroll
;                         for (int j = 0; j < 4; ++j) { v0[j] = silu_f(v0[j]); v1[j] = silu_f(v1[j]); } }
;                     else if (TT == 4 || TT == 5) { f32x2 a = gelu_pk((f32x2){v0[0], v0[1]}), b = gelu_pk((f32x2){v0[2], v0[3]}), c = gelu_pk((f32x2){v1[0], v1[1]}), d = gelu_pk((f32x2){v1[2], v1[3]});
;                         v0 = (f32x4){a.x, a.y, b.x, b.y}; v1 = (f32x4){c.x, c.y, d.x, d.y};
;                         if (TT == 5) { ps += ((v0[0] + v0[1]) + (v0[2] + v0[3])) + ((v1[0] + v1[1]) + (v1[2] + v1[3]));
;                             pq += ((v0[0] * v0[0] + v0[1] * v0[1]) + (v0[2] * v0[2] + v0[3] * v0[3])) + ((v1[0] * v1[0] + v1[1] * v1[1]) + (v1[2] * v1[2] + v1[3] * v1[3])); } }
;                     else if (TT >= 6) {
; #pragma unroll
;                         for (int j = 0; j < 4; ++j) { v0[j] = sigmoid_f(v0[j]); v1[j] = sigmoid_f(v1[j]); } }
;                     if (TT >= 6) { unsigned b0 = 0u, b1 = 0u;
; #pragma unroll
;                         for (int j = 0; j < 4; ++j) { b0 = __builtin_amdgcn_cvt_pk_u8_f32(__builtin_rintf(v0[j] * 255.0f), j, b0); b1 = __builtin_amdgcn_cvt_pk_u8_f32(__builtin_rintf(v1[j] * 255.0f), j, b1); }
;                         if (bj == 0) { gq.x = b0; gq.y = b1; } else { gq.z = b0; gq.w = b1; } }
;                     else { u32x4 w; w.x = cvt_pk_bf16(v0[0], v0[1]); w.y = cvt_pk_bf16(v0[2], v0[3]); w.z = cvt_pk_bf16(v1[0], v1[1]); w.w = cvt_pk_bf16(v1[2], v1[3]);
;                         *(u32x4*)(rowp + bj * HALF) = w; } }
;                 if (TT >= 6) *(u32x4*)((unsigned char*)base + (size_t)(row0 + ai * HALF + m * 16) * GATE_PITCH + hh * 256 + (wc * 4 + fq) * 16) = gq;
;                 if (TT == 5) { ps += __shfl_xor(ps, 16); pq += __shfl_xor(pq, 16); ps += __shfl_xor(ps, 32); pq += __shfl_xor(pq, 32);
;                     if (m == 0 || fq == m) { psm = ps; pqm = pq; }
;                     if (m == 3) *(f32x2*)(sgst + ((size_t)((row0 + ai * HALF + fq * 16) * 8 + hh) * 4 + wc) * 2) = (f32x2){psm, pqm}; } }
	v_cmp_gt_f32_e32 vcc, 0, v142
	v_mul_f32_e64 v182, v156, v178
	v_mul_f32_e64 v183, v157, v179
	v_fma_f32 v178, -v156, v178, v156
	v_fma_f32 v179, -v157, v179, v157
	v_cndmask_b32_e32 v155, v206, v214, vcc
	v_cmp_gt_f32_e32 vcc, 0, v156
	v_mul_f32_e64 v208, v208, v216
	v_mul_f32_e64 v209, v209, v217
	v_mul_f32_e64 v180, v180, v184
	v_mul_f32_e64 v181, v181, v185
	v_cndmask_b32_e32 v154, v178, v182, vcc
	v_cmp_gt_f32_e32 vcc, 0, v143
	v_mul_f32_e64 v216, v192, v208
	v_mul_f32_e64 v217, v193, v209
	v_fma_f32 v208, -v192, v208, v192
	v_fma_f32 v209, -v193, v209, v193
	v_cndmask_b32_e32 v161, v207, v215, vcc
	v_cmp_gt_f32_e32 vcc, 0, v157
	v_mul_f32_e64 v184, v138, v180
	v_mul_f32_e64 v185, v139, v181
	v_fma_f32 v180, -v138, v180, v138
	v_fma_f32 v181, -v139, v181, v139
	v_cndmask_b32_e32 v160, v179, v183, vcc
	v_cmp_gt_f32_e32 vcc, 0, v192
	v_add_f32_e64 v178, v146, v162
	v_add_f32_e64 v179, v147, v163
	v_cvt_pk_bf16_f32 v143, v146, v162
	v_cndmask_b32_e32 v157, v208, v216, vcc
	v_cmp_gt_f32_e32 vcc, 0, v138
	v_cvt_pk_bf16_f32 v142, v218, v186
	v_cvt_pk_bf16_f32 v144, v154, v160
	v_cndmask_b32_e32 v156, v180, v184, vcc
	v_cmp_gt_f32_e32 vcc, 0, v193
	s_nop 1
	v_cndmask_b32_e32 v177, v209, v217, vcc
	v_cmp_gt_f32_e32 vcc, 0, v139
	v_add_f32_e64 v138, v218, v186
	v_add_f32_e64 v139, v219, v187
	s_nop 0
	v_cndmask_b32_e32 v176, v181, v185, vcc
	v_add_f32_e64 v138, v138, v178
	v_add_f32_e64 v139, v139, v179
	v_add_f32_e64 v178, v154, v160
	v_add_f32_e64 v179, v155, v161
	v_add_f32_e64 v180, v156, v176
	v_add_f32_e64 v181, v157, v177
	v_cvt_pk_bf16_f32 v145, v156, v176
	v_add_f32_e64 v178, v178, v180
	v_add_f32_e64 v179, v179, v181
	v_mul_f32_e64 v180, v176, v176
	v_mul_f32_e64 v181, v177, v177
	v_add_f32_e64 v138, v138, v178
	v_add_f32_e64 v139, v139, v179
	v_mul_f32_e64 v178, v162, v162
	v_mul_f32_e64 v179, v163, v163
	v_add_f32_e32 v138, 0, v138
	v_add_f32_e32 v182, v139, v138
	v_mul_f32_e64 v138, v186, v186
	v_mul_f32_e64 v139, v187, v187
	v_fma_f32 v178, v146, v146, v178
	v_fma_f32 v179, v147, v147, v179
	v_fma_f32 v138, v218, v218, v138
	v_fma_f32 v139, v219, v219, v139
	v_fma_f32 v180, v156, v156, v180
	v_fma_f32 v181, v157, v157, v181
	v_add_f32_e64 v138, v138, v178
	v_add_f32_e64 v139, v139, v179
	v_mul_f32_e64 v178, v160, v160
	v_mul_f32_e64 v179, v161, v161
	global_store_dwordx4 v[140:141], v[142:145], off
	v_fma_f32 v178, v154, v154, v178
	v_fma_f32 v179, v155, v155, v179
	v_cmp_eq_u32_e32 vcc, 1, v151
	v_add_f32_e64 v178, v178, v180
	v_add_f32_e64 v179, v179, v181
	v_cvt_pk_bf16_f32 v143, v147, v163
	v_add_f32_e64 v138, v138, v178
	v_add_f32_e64 v139, v139, v179
	v_cvt_pk_bf16_f32 v142, v219, v187
	v_add_f32_e32 v138, v138, v139
	ds_bpermute_b32 v146, v149, v138
	ds_bpermute_b32 v139, v149, v182
	v_cvt_pk_bf16_f32 v144, v155, v161
	v_cvt_pk_bf16_f32 v145, v157, v177
	global_store_dwordx4 v[140:141], v[142:145], off offset:256
	s_waitcnt lgkmcnt(0)
	v_add_f32_e32 v138, v138, v146
	v_add_f32_e32 v139, v182, v139
	ds_bpermute_b32 v147, v148, v138
	ds_bpermute_b32 v146, v148, v139
	s_waitcnt lgkmcnt(0)
	v_add_f32_e32 v138, v138, v147
	v_add_f32_e32 v140, v139, v146
	v_cndmask_b32_e32 v159, v159, v138, vcc
	ds_read2_b32 v[138:139], v199 offset0:32 offset1:48
	v_cndmask_b32_e32 v153, v153, v140, vcc
	v_add_u32_e32 v140, 32, v150
	v_mad_i64_i32 v[140:141], s[2:3], v140, s81, v[134:135]
	s_waitcnt lgkmcnt(0)
	v_fma_f32 v144, v88, v138, 0
	v_fma_f32 v145, v89, v138, 0
	v_fma_f32 v190, v98, v138, 0
	v_fma_f32 v191, v99, v138, 0
	v_and_b32_e32 v143, 0x7fffffff, v145
	v_and_b32_e32 v142, 0x7fffffff, v144
	v_fma_f32 v142, v142, s4, 1.0
	v_fma_f32 v143, v143, s4, 1.0
	v_fma_f32 v154, v90, v138, 0
	v_fma_f32 v155, v91, v138, 0
	v_rcp_f32_e32 v146, v142
	v_rcp_f32_e32 v147, v143
	v_fma_f32 v142, v86, v138, 0
	v_fma_f32 v143, v87, v138, 0
	v_and_b32_e32 v207, 0x7fffffff, v191
	v_and_b32_e32 v185, 0x7fffffff, v143
	v_and_b32_e32 v184, 0x7fffffff, v142
	v_fma_f32 v184, v184, s4, 1.0
	v_fma_f32 v185, v185, s4, 1.0
	v_and_b32_e32 v206, 0x7fffffff, v190
	v_rcp_f32_e32 v184, v184
	v_rcp_f32_e32 v185, v185
	v_and_b32_e32 v177, 0x7fffffff, v155
	v_and_b32_e32 v176, 0x7fffffff, v154
	v_fma_f32 v206, v206, s4, 1.0
	v_fma_f32 v207, v207, s4, 1.0
	v_fma_f32 v186, v184, s46, v132
	v_fma_f32 v187, v185, s46, v132
	v_fma_f32 v176, v176, s4, 1.0
	v_fma_f32 v177, v177, s4, 1.0
	v_fma_f32 v186, v184, v186, s48
	v_fma_f32 v187, v185, v187, s48
	v_rcp_f32_e32 v206, v206
	v_fma_f32 v186, v184, v186, s50
	v_fma_f32 v187, v185, v187, s50
	v_rcp_f32_e32 v207, v207
	v_fma_f32 v186, v184, v186, s52
	v_fma_f32 v187, v185, v187, s52
	v_rcp_f32_e32 v176, v176
	v_mul_f32_e64 v184, v184, v186
	v_mul_f32_e64 v185, v185, v187
	v_fma_f32 v186, v96, v138, 0
	v_fma_f32 v187, v97, v138, 0
	v_rcp_f32_e32 v177, v177
	v_and_b32_e32 v189, 0x7fffffff, v187
	v_and_b32_e32 v188, 0x7fffffff, v186
	v_fma_f32 v188, v188, s4, 1.0
	v_fma_f32 v189, v189, s4, 1.0
	v_fma_f32 v192, v94, v138, 0
	v_fma_f32 v193, v95, v138, 0
	v_rcp_f32_e32 v188, v188
	v_rcp_f32_e32 v189, v189
	v_fma_f32 v208, v206, s46, v132
	v_fma_f32 v209, v207, s46, v132
	v_and_b32_e32 v219, 0x7fffffff, v193
	v_and_b32_e32 v218, 0x7fffffff, v192
	v_fma_f32 v178, v176, s46, v132
	v_fma_f32 v179, v177, s46, v132
	v_fma_f32 v208, v206, v208, s48
	v_fma_f32 v209, v207, v209, s48
	v_fma_f32 v218, v218, s4, 1.0
	v_fma_f32 v219, v219, s4, 1.0
	v_fma_f32 v178, v176, v178, s48
	v_fma_f32 v179, v177, v179, s48
	v_fma_f32 v202, v188, s46, v132
	v_fma_f32 v203, v189, s46, v132
	v_mul_f32_e64 v204, v186, v186
	v_mul_f32_e64 v205, v187, v187
	v_fma_f32 v208, v206, v208, s50
	v_fma_f32 v209, v207, v209, s50
	v_rcp_f32_e32 v218, v218
; __device__ __forceinline__ f32x2 gelu_pk(f32x2 v) {
;     const f32x2 av = __builtin_elementwise_abs(v), d = av * 0.2316418882f + 1.0f;
;     f32x2 t; t.x = __builtin_amdgcn_rcpf(d.x); t.y = __builtin_amdgcn_rcpf(d.y);
;     f32x2 q = t * 0.5307027145f + (-0.7265760135f); q = q * t + 0.7107068705f; q = q * t + (-0.142248368f); q = q * t + 0.127414796f; q = q * t;
;     const f32x2 s = (v * v) * (-0.72134752044f);
;     f32x2 e; e.x = __builtin_amdgcn_exp2f(s.x); e.y = __builtin_amdgcn_exp2f(s.y);
;     const f32x2 m = v * (q * e), r = v - m;
;     f32x2 o; o.x = v.x < 0.f ? m.x : r.x; o.y = v.y < 0.f ? m.y : r.y; return o;
; }
	v_rcp_f32_e32 v219, v219
	v_fma_f32 v160, v146, s46, v132
	v_fma_f32 v161, v147, s46, v132
	v_mul_f32_e64 v162, v144, v144
	v_mul_f32_e64 v163, v145, v145
	v_fma_f32 v178, v176, v178, s50
	v_fma_f32 v179, v177, v179, s50
	v_fma_f32 v194, v92, v138, 0
	v_fma_f32 v195, v93, v138, 0
	v_fma_f32 v202, v188, v202, s48
	v_fma_f32 v203, v189, v203, s48
	v_mul_f32_e64 v204, v204, s54
	v_mul_f32_e64 v205, v205, s54
	v_fma_f32 v208, v206, v208, s52
	v_fma_f32 v209, v207, v209, s52
	v_fma_f32 v156, v84, v138, 0
	v_fma_f32 v157, v85, v138, 0
	v_fma_f32 v160, v146, v160, s48
	v_fma_f32 v161, v147, v161, s48
	v_mul_f32_e64 v162, v162, s54
	v_mul_f32_e64 v163, v163, s54
	v_fma_f32 v178, v176, v178, s52
	v_fma_f32 v179, v177, v179, s52
	v_fma_f32 v202, v188, v202, s50
	v_fma_f32 v203, v189, v203, s50
	v_exp_f32_e32 v204, v204
	v_exp_f32_e32 v205, v205
	v_mul_f32_e64 v206, v206, v208
	v_mul_f32_e64 v207, v207, v209
	v_and_b32_e32 v209, 0x7fffffff, v195
	v_and_b32_e32 v208, 0x7fffffff, v194
	v_fma_f32 v160, v146, v160, s50
	v_fma_f32 v161, v147, v161, s50
	v_exp_f32_e32 v162, v162
	v_exp_f32_e32 v163, v163
	v_mul_f32_e64 v176, v176, v178
	v_mul_f32_e64 v177, v177, v179
	v_and_b32_e32 v179, 0x7fffffff, v157
	v_and_b32_e32 v178, 0x7fffffff, v156
	v_fma_f32 v202, v188, v202, s52
	v_fma_f32 v203, v189, v203, s52
	v_fma_f32 v208, v208, s4, 1.0
	v_fma_f32 v209, v209, s4, 1.0
	v_fma_f32 v160, v146, v160, s52
	v_fma_f32 v161, v147, v161, s52
	v_fma_f32 v178, v178, s4, 1.0
	v_fma_f32 v179, v179, s4, 1.0
	v_mul_f32_e64 v188, v188, v202
	v_mul_f32_e64 v189, v189, v203
	v_mul_f32_e64 v202, v190, v190
	v_mul_f32_e64 v203, v191, v191
	v_rcp_f32_e32 v208, v208
	v_rcp_f32_e32 v209, v209
	v_fma_f32 v220, v218, s46, v132
	v_fma_f32 v221, v219, s46, v132
	v_mul_f32_e64 v146, v146, v160
	v_mul_f32_e64 v147, v147, v161
	v_mul_f32_e64 v160, v154, v154
	v_mul_f32_e64 v161, v155, v155
	v_rcp_f32_e32 v178, v178
	v_rcp_f32_e32 v179, v179
	v_mul_f32_e64 v202, v202, s54
	v_mul_f32_e64 v203, v203, s54
	v_fma_f32 v220, v218, v220, s48
	v_fma_f32 v221, v219, v221, s48
	v_mul_f32_e64 v160, v160, s54
	v_mul_f32_e64 v161, v161, s54
	v_mul_f32_e64 v188, v204, v188
	v_mul_f32_e64 v189, v205, v189
	v_exp_f32_e32 v202, v202
	v_exp_f32_e32 v203, v203
	v_fma_f32 v220, v218, v220, s50
	v_fma_f32 v221, v219, v221, s50
	v_mul_f32_e64 v146, v162, v146
	v_mul_f32_e64 v147, v163, v147
	v_exp_f32_e32 v160, v160
	v_exp_f32_e32 v161, v161
	v_mul_f32_e64 v204, v186, v188
	v_mul_f32_e64 v205, v187, v189
	v_fma_f32 v188, -v186, v188, v186
	v_fma_f32 v189, -v187, v189, v187
	v_fma_f32 v220, v218, v220, s52
	v_fma_f32 v221, v219, v221, s52
	v_cmp_gt_f32_e64 s[10:11], 0, v186
	v_mul_f32_e64 v162, v144, v146
	v_mul_f32_e64 v163, v145, v147
	v_fma_f32 v146, -v144, v146, v144
	v_fma_f32 v147, -v145, v147, v145
	v_fma_f32 v214, v208, s46, v132
	v_fma_f32 v215, v209, s46, v132
	v_mul_f32_e64 v216, v194, v194
	v_mul_f32_e64 v217, v195, v195
	v_mul_f32_e64 v218, v218, v220
	v_mul_f32_e64 v219, v219, v221
	v_cndmask_b32_e64 v221, v188, v204, s[10:11]
	v_cmp_gt_f32_e64 s[10:11], 0, v144
	v_fma_f32 v180, v178, s46, v132
	v_fma_f32 v181, v179, s46, v132
	v_mul_f32_e64 v182, v156, v156
	v_mul_f32_e64 v183, v157, v157
	v_fma_f32 v214, v208, v214, s48
	v_fma_f32 v215, v209, v215, s48
	v_mul_f32_e64 v216, v216, s54
	v_mul_f32_e64 v217, v217, s54
	v_cndmask_b32_e64 v220, v146, v162, s[10:11]
	v_cmp_gt_f32_e64 s[10:11], 0, v187
	v_fma_f32 v180, v178, v180, s48
	v_fma_f32 v181, v179, v181, s48
	v_mul_f32_e64 v182, v182, s54
	v_mul_f32_e64 v183, v183, s54
	v_mul_f32_e64 v202, v202, v206
	v_mul_f32_e64 v203, v203, v207
	v_fma_f32 v214, v208, v214, s50
	v_fma_f32 v215, v209, v215, s50
	v_exp_f32_e32 v216, v216
	v_exp_f32_e32 v217, v217
	v_cndmask_b32_e64 v187, v189, v205, s[10:11]
	v_cmp_gt_f32_e64 s[10:11], 0, v145
	v_mul_f32_e64 v160, v160, v176
	v_mul_f32_e64 v161, v161, v177
	v_fma_f32 v180, v178, v180, s50
	v_fma_f32 v181, v179, v181, s50
	v_exp_f32_e32 v182, v182
	v_exp_f32_e32 v183, v183
	v_mul_f32_e64 v206, v190, v202
	v_mul_f32_e64 v207, v191, v203
	v_fma_f32 v202, -v190, v202, v190
	v_fma_f32 v203, -v191, v203, v191
	v_fma_f32 v214, v208, v214, s52
	v_fma_f32 v215, v209, v215, s52
	v_cndmask_b32_e64 v186, v147, v163, s[10:11]
	v_cmp_gt_f32_e64 s[10:11], 0, v190
	v_mul_f32_e64 v176, v154, v160
	v_mul_f32_e64 v177, v155, v161
	v_fma_f32 v160, -v154, v160, v154
	v_fma_f32 v161, -v155, v161, v155
	v_fma_f32 v180, v178, v180, s52
	v_fma_f32 v181, v179, v181, s52
	v_mul_f32_e64 v208, v208, v214
	v_mul_f32_e64 v209, v209, v215
	v_mul_f32_e64 v214, v192, v192
	v_mul_f32_e64 v215, v193, v193
	v_cndmask_b32_e64 v147, v202, v206, s[10:11]
	v_cmp_gt_f32_e64 s[10:11], 0, v154
	v_mul_f32_e64 v178, v178, v180
	v_mul_f32_e64 v179, v179, v181
	v_mul_f32_e64 v180, v142, v142
	v_mul_f32_e64 v181, v143, v143
	v_mul_f32_e64 v214, v214, s54
	v_mul_f32_e64 v215, v215, s54
	v_cndmask_b32_e64 v146, v160, v176, s[10:11]
	v_cmp_gt_f32_e64 s[10:11], 0, v191
	v_mul_f32_e64 v180, v180, s54
	v_mul_f32_e64 v181, v181, s54
	v_mul_f32_e64 v208, v216, v208
	v_mul_f32_e64 v209, v217, v209
	v_exp_f32_e32 v214, v214
	v_exp_f32_e32 v215, v215
	v_cndmask_b32_e64 v163, v203, v207, s[10:11]
	v_cmp_gt_f32_e64 s[10:11], 0, v155
	v_mul_f32_e64 v178, v182, v178
	v_mul_f32_e64 v179, v183, v179
	v_exp_f32_e32 v180, v180
	v_exp_f32_e32 v181, v181
	v_mul_f32_e64 v216, v194, v208
	v_mul_f32_e64 v217, v195, v209
	v_fma_f32 v208, -v194, v208, v194
	v_fma_f32 v209, -v195, v209, v195
	v_cndmask_b32_e64 v162, v161, v177, s[10:11]
	v_cmp_gt_f32_e64 s[10:11], 0, v194
	v_mul_f32_e64 v182, v156, v178
	v_mul_f32_e64 v183, v157, v179
	v_fma_f32 v178, -v156, v178, v156
;     template <int TT> __device__ __forceinline__ void other(const f32x4 (&acc)[2][2][4][2], bf16_t* base, int row0, int col0, PG8_LAS float* my, int t, int hh, int wc, int fq) const {
;     ...
;                 for (int bj = 0; bj < 2; ++bj) { f32x4 v0 = acc[ai][bj][m][0] * rs + bv[bj][0], v1 = acc[ai][bj][m][1] * rs + bv[bj][1];
;                     if (TT == 3) {
; #pragma unroll
;                         for (int j = 0; j < 4; ++j) { v0[j] = silu_f(v0[j]); v1[j] = silu_f(v1[j]); } }
;                     else if (TT == 4 || TT == 5) { f32x2 a = gelu_pk((f32x2){v0[0], v0[1]}), b = gelu_pk((f32x2){v0[2], v0[3]}), c = gelu_pk((f32x2){v1[0], v1[1]}), d = gelu_pk((f32x2){v1[2], v1[3]});
;                         v0 = (f32x4){a.x, a.y, b.x, b.y}; v1 = (f32x4){c.x, c.y, d.x, d.y};
;                         if (TT == 5) { ps += ((v0[0] + v0[1]) + (v0[2] + v0[3])) + ((v1[0] + v1[1]) + (v1[2] + v1[3]));
;                             pq += ((v0[0] * v0[0] + v0[1] * v0[1]) + (v0[2] * v0[2] + v0[3] * v0[3])) + ((v1[0] * v1[0] + v1[1] * v1[1]) + (v1[2] * v1[2] + v1[3] * v1[3])); } }
;                     else if (TT >= 6) {
; #pragma unroll
;                         for (int j = 0; j < 4; ++j) { v0[j] = sigmoid_f(v0[j]); v1[j] = sigmoid_f(v1[j]); } }
;                     if (TT >= 6) { unsigned b0 = 0u, b1 = 0u;
; #pragma unroll
;                         for (int j = 0; j < 4; ++j) { b0 = __builtin_amdgcn_cvt_pk_u8_f32(__builtin_rintf(v0[j] * 255.0f), j, b0); b1 = __builtin_amdgcn_cvt_pk_u8_f32(__builtin_rintf(v1[j] * 255.0f), j, b1); }
;                         if (bj == 0) { gq.x = b0; gq.y = b1; } else { gq.z = b0; gq.w = b1; } }
;                     else { u32x4 w; w.x = cvt_pk_bf16(v0[0], v0[1]); w.y = cvt_pk_bf16(v0[2], v0[3]); w.z = cvt_pk_bf16(v1[0], v1[1]); w.w = cvt_pk_bf16(v1[2], v1[3]);
;                         *(u32x4*)(rowp + bj * HALF) = w; } }
;                 if (TT >= 6) *(u32x4*)((unsigned char*)base + (size_t)(row0 + ai * HALF + m * 16) * GATE_PITCH + hh * 256 + (wc * 4 + fq) * 16) = gq;
;                 if (TT == 5) { ps += __shfl_xor(ps, 16); pq += __shfl_xor(pq, 16); ps += __shfl_xor(ps, 32); pq += __shfl_xor(pq, 32);
;                     if (m == 0 || fq == m) { psm = ps; pqm = pq; }
;                     if (m == 3) *(f32x2*)(sgst + ((size_t)((row0 + ai * HALF + fq * 16) * 8 + hh) * 4 + wc) * 2) = (f32x2){psm, pqm}; } }
	v_fma_f32 v179, -v157, v179, v157
	v_cndmask_b32_e64 v155, v208, v216, s[10:11]
	v_cmp_gt_f32_e64 s[10:11], 0, v156
	v_mul_f32_e64 v214, v214, v218
	v_mul_f32_e64 v215, v215, v219
	v_mul_f32_e64 v180, v180, v184
	v_mul_f32_e64 v181, v181, v185
	v_cndmask_b32_e64 v154, v178, v182, s[10:11]
	v_cmp_gt_f32_e64 s[10:11], 0, v195
	v_mul_f32_e64 v218, v192, v214
	v_mul_f32_e64 v219, v193, v215
	v_fma_f32 v214, -v192, v214, v192
	v_fma_f32 v215, -v193, v215, v193
	v_cndmask_b32_e64 v161, v209, v217, s[10:11]
	v_cmp_gt_f32_e64 s[10:11], 0, v157
	v_mul_f32_e64 v184, v142, v180
	v_mul_f32_e64 v185, v143, v181
	v_fma_f32 v180, -v142, v180, v142
	v_fma_f32 v181, -v143, v181, v143
	v_cndmask_b32_e64 v160, v179, v183, s[10:11]
	v_cmp_gt_f32_e64 s[10:11], 0, v192
	v_add_f32_e64 v178, v220, v186
	v_add_f32_e64 v179, v221, v187
	v_cvt_pk_bf16_f32 v144, v154, v160
	v_cndmask_b32_e64 v157, v214, v218, s[10:11]
	v_cmp_gt_f32_e64 s[10:11], 0, v142
	v_cvt_pk_bf16_f32 v142, v220, v186
	s_nop 0
	v_cndmask_b32_e64 v156, v180, v184, s[10:11]
	v_cmp_gt_f32_e64 s[10:11], 0, v193
	s_nop 1
	v_cndmask_b32_e64 v177, v215, v219, s[10:11]
	v_cmp_gt_f32_e64 s[10:11], 0, v143
	v_cvt_pk_bf16_f32 v143, v146, v162
	s_nop 0
	v_cndmask_b32_e64 v176, v181, v185, s[10:11]
	v_add_f32_e64 v180, v146, v162
	v_add_f32_e64 v181, v147, v163
	v_add_f32_e64 v182, v156, v176
	v_add_f32_e64 v183, v157, v177
	v_add_f32_e64 v178, v178, v180
	v_add_f32_e64 v179, v179, v181
	v_add_f32_e64 v180, v154, v160
	v_add_f32_e64 v181, v155, v161
	v_cvt_pk_bf16_f32 v145, v156, v176
	v_add_f32_e64 v180, v180, v182
	v_add_f32_e64 v181, v181, v183
	v_mul_f32_e64 v182, v176, v176
	v_mul_f32_e64 v183, v177, v177
	v_add_f32_e64 v178, v178, v180
	v_add_f32_e64 v179, v179, v181
	v_mul_f32_e64 v180, v162, v162
	v_mul_f32_e64 v181, v163, v163
	v_add_f32_e32 v138, 0, v178
	v_add_f32_e32 v138, v179, v138
	v_mul_f32_e64 v178, v186, v186
	v_mul_f32_e64 v179, v187, v187
	v_fma_f32 v180, v146, v146, v180
	v_fma_f32 v181, v147, v147, v181
	v_fma_f32 v178, v220, v220, v178
	v_fma_f32 v179, v221, v221, v179
	v_fma_f32 v182, v156, v156, v182
	v_fma_f32 v183, v157, v157, v183
	v_add_f32_e64 v178, v178, v180
	v_add_f32_e64 v179, v179, v181
	v_mul_f32_e64 v180, v160, v160
	v_mul_f32_e64 v181, v161, v161
	global_store_dwordx4 v[140:141], v[142:145], off
	v_fma_f32 v180, v154, v154, v180
	v_fma_f32 v181, v155, v155, v181
	ds_bpermute_b32 v154, v149, v138
	v_add_f32_e64 v180, v180, v182
	v_add_f32_e64 v181, v181, v183
	v_cvt_pk_bf16_f32 v143, v147, v163
	v_add_f32_e64 v178, v178, v180
	v_add_f32_e64 v179, v179, v181
	v_cvt_pk_bf16_f32 v142, v221, v187
	v_add_f32_e32 v146, v178, v179
	ds_bpermute_b32 v156, v149, v146
	s_waitcnt lgkmcnt(0)
	v_add_f32_e32 v138, v138, v154
	ds_bpermute_b32 v147, v148, v138
	v_cvt_pk_bf16_f32 v144, v155, v161
	v_cvt_pk_bf16_f32 v145, v157, v177
	v_add_f32_e32 v146, v146, v156
	ds_bpermute_b32 v154, v148, v146
	global_store_dwordx4 v[140:141], v[142:145], off offset:256
	s_waitcnt lgkmcnt(0)
	v_add_f32_e32 v138, v138, v147
	v_cmp_eq_u32_e64 s[10:11], 2, v151
	v_mov_b32_e32 v142, v139
	v_add_f32_e32 v140, v146, v154
	v_cndmask_b32_e64 v153, v153, v138, s[10:11]
	v_add_u32_e32 v138, 48, v150
	v_fma_f32 v144, v72, v142, 0
	v_fma_f32 v145, v73, v142, 0
	v_cndmask_b32_e64 v159, v159, v140, s[10:11]
	v_mad_i64_i32 v[140:141], s[2:3], v138, s81, v[134:135]
	v_and_b32_e32 v139, 0x7fffffff, v145
	v_and_b32_e32 v138, 0x7fffffff, v144
	v_fma_f32 v138, v138, s4, 1.0
	v_fma_f32 v139, v139, s4, 1.0
	v_fma_f32 v190, v82, v142, 0
	v_fma_f32 v191, v83, v142, 0
	v_rcp_f32_e32 v146, v138
	v_rcp_f32_e32 v147, v139
	v_fma_f32 v138, v70, v142, 0
	v_fma_f32 v139, v71, v142, 0
	v_fma_f32 v154, v74, v142, 0
	v_fma_f32 v155, v75, v142, 0
	v_and_b32_e32 v185, 0x7fffffff, v139
	v_and_b32_e32 v184, 0x7fffffff, v138
	v_fma_f32 v184, v184, s4, 1.0
	v_fma_f32 v185, v185, s4, 1.0
	v_and_b32_e32 v205, 0x7fffffff, v191
	v_rcp_f32_e32 v184, v184
	v_rcp_f32_e32 v185, v185
	v_and_b32_e32 v204, 0x7fffffff, v190
	v_and_b32_e32 v177, 0x7fffffff, v155
	v_and_b32_e32 v176, 0x7fffffff, v154
	v_fma_f32 v186, v184, s46, v132
	v_fma_f32 v187, v185, s46, v132
	v_fma_f32 v204, v204, s4, 1.0
	v_fma_f32 v205, v205, s4, 1.0
	v_fma_f32 v186, v184, v186, s48
	v_fma_f32 v187, v185, v187, s48
	v_fma_f32 v176, v176, s4, 1.0
	v_fma_f32 v177, v177, s4, 1.0
	v_fma_f32 v186, v184, v186, s50
	v_fma_f32 v187, v185, v187, s50
	v_rcp_f32_e32 v204, v204
	v_fma_f32 v186, v184, v186, s52
	v_fma_f32 v187, v185, v187, s52
	v_rcp_f32_e32 v205, v205
	v_mul_f32_e64 v184, v184, v186
	v_mul_f32_e64 v185, v185, v187
	v_fma_f32 v186, v80, v142, 0
	v_fma_f32 v187, v81, v142, 0
	v_rcp_f32_e32 v176, v176
	v_and_b32_e32 v189, 0x7fffffff, v187
	v_and_b32_e32 v188, 0x7fffffff, v186
	v_rcp_f32_e32 v177, v177
	v_fma_f32 v188, v188, s4, 1.0
	v_fma_f32 v189, v189, s4, 1.0
	v_fma_f32 v192, v78, v142, 0
	v_fma_f32 v193, v79, v142, 0
	v_rcp_f32_e32 v188, v188
	v_rcp_f32_e32 v189, v189
	v_fma_f32 v206, v204, s46, v132
	v_fma_f32 v207, v205, s46, v132
	v_and_b32_e32 v217, 0x7fffffff, v193
	v_and_b32_e32 v216, 0x7fffffff, v192
	v_fma_f32 v178, v176, s46, v132
	v_fma_f32 v179, v177, s46, v132
	v_fma_f32 v206, v204, v206, s48
	v_fma_f32 v207, v205, v207, s48
	v_fma_f32 v216, v216, s4, 1.0
	v_fma_f32 v217, v217, s4, 1.0
	v_fma_f32 v178, v176, v178, s48
	v_fma_f32 v179, v177, v179, s48
	v_fma_f32 v194, v188, s46, v132
	v_fma_f32 v195, v189, s46, v132
	v_mul_f32_e64 v202, v186, v186
	v_mul_f32_e64 v203, v187, v187
	v_fma_f32 v206, v204, v206, s50
	v_fma_f32 v207, v205, v207, s50
	v_rcp_f32_e32 v216, v216
	v_rcp_f32_e32 v217, v217
	v_fma_f32 v156, v68, v142, 0
	v_fma_f32 v157, v69, v142, 0
; __device__ __forceinline__ f32x2 gelu_pk(f32x2 v) {
;     const f32x2 av = __builtin_elementwise_abs(v), d = av * 0.2316418882f + 1.0f;
;     f32x2 t; t.x = __builtin_amdgcn_rcpf(d.x); t.y = __builtin_amdgcn_rcpf(d.y);
;     f32x2 q = t * 0.5307027145f + (-0.7265760135f); q = q * t + 0.7107068705f; q = q * t + (-0.142248368f); q = q * t + 0.127414796f; q = q * t;
;     const f32x2 s = (v * v) * (-0.72134752044f);
;     f32x2 e; e.x = __builtin_amdgcn_exp2f(s.x); e.y = __builtin_amdgcn_exp2f(s.y);
;     const f32x2 m = v * (q * e), r = v - m;
;     f32x2 o; o.x = v.x < 0.f ? m.x : r.x; o.y = v.y < 0.f ? m.y : r.y; return o;
; }
	v_fma_f32 v160, v146, s46, v132
	v_fma_f32 v161, v147, s46, v132
	v_mul_f32_e64 v162, v144, v144
	v_mul_f32_e64 v163, v145, v145
	v_fma_f32 v178, v176, v178, s50
	v_fma_f32 v179, v177, v179, s50
	v_fma_f32 v143, v77, v142, 0
	v_fma_f32 v142, v76, v142, 0
	v_fma_f32 v194, v188, v194, s48
	v_fma_f32 v195, v189, v195, s48
	v_mul_f32_e64 v202, v202, s54
	v_mul_f32_e64 v203, v203, s54
	v_fma_f32 v206, v204, v206, s52
	v_fma_f32 v207, v205, v207, s52
	v_fma_f32 v160, v146, v160, s48
	v_fma_f32 v161, v147, v161, s48
	v_mul_f32_e64 v162, v162, s54
	v_mul_f32_e64 v163, v163, s54
	v_fma_f32 v178, v176, v178, s52
	v_fma_f32 v179, v177, v179, s52
	v_fma_f32 v194, v188, v194, s50
	v_fma_f32 v195, v189, v195, s50
	v_exp_f32_e32 v202, v202
	v_exp_f32_e32 v203, v203
	v_mul_f32_e64 v204, v204, v206
	v_mul_f32_e64 v205, v205, v207
	v_and_b32_e32 v207, 0x7fffffff, v143
	v_and_b32_e32 v206, 0x7fffffff, v142
	v_fma_f32 v160, v146, v160, s50
	v_fma_f32 v161, v147, v161, s50
	v_exp_f32_e32 v162, v162
	v_exp_f32_e32 v163, v163
	v_mul_f32_e64 v176, v176, v178
	v_mul_f32_e64 v177, v177, v179
	v_and_b32_e32 v179, 0x7fffffff, v157
	v_and_b32_e32 v178, 0x7fffffff, v156
	v_fma_f32 v194, v188, v194, s52
	v_fma_f32 v195, v189, v195, s52
	v_fma_f32 v206, v206, s4, 1.0
	v_fma_f32 v207, v207, s4, 1.0
	v_fma_f32 v160, v146, v160, s52
	v_fma_f32 v161, v147, v161, s52
	v_fma_f32 v178, v178, s4, 1.0
	v_fma_f32 v179, v179, s4, 1.0
	v_mul_f32_e64 v188, v188, v194
	v_mul_f32_e64 v189, v189, v195
	v_mul_f32_e64 v194, v190, v190
	v_mul_f32_e64 v195, v191, v191
	v_rcp_f32_e32 v206, v206
	v_rcp_f32_e32 v207, v207
	v_fma_f32 v218, v216, s46, v132
	v_fma_f32 v219, v217, s46, v132
	v_mul_f32_e64 v146, v146, v160
	v_mul_f32_e64 v147, v147, v161
	v_mul_f32_e64 v160, v154, v154
	v_mul_f32_e64 v161, v155, v155
	v_rcp_f32_e32 v178, v178
	v_rcp_f32_e32 v179, v179
	v_mul_f32_e64 v194, v194, s54
	v_mul_f32_e64 v195, v195, s54
	v_fma_f32 v218, v216, v218, s48
	v_fma_f32 v219, v217, v219, s48
	v_mul_f32_e64 v160, v160, s54
	v_mul_f32_e64 v161, v161, s54
	v_mul_f32_e64 v188, v202, v188
	v_mul_f32_e64 v189, v203, v189
	v_exp_f32_e32 v194, v194
	v_exp_f32_e32 v195, v195
	v_fma_f32 v218, v216, v218, s50
	v_fma_f32 v219, v217, v219, s50
	v_mul_f32_e64 v146, v162, v146
	v_mul_f32_e64 v147, v163, v147
	v_exp_f32_e32 v160, v160
	v_exp_f32_e32 v161, v161
	v_mul_f32_e64 v202, v186, v188
	v_mul_f32_e64 v203, v187, v189
	v_fma_f32 v188, -v186, v188, v186
	v_fma_f32 v189, -v187, v189, v187
	v_fma_f32 v218, v216, v218, s52
	v_fma_f32 v219, v217, v219, s52
	v_cmp_gt_f32_e64 s[12:13], 0, v186
	v_mul_f32_e64 v162, v144, v146
	v_mul_f32_e64 v163, v145, v147
	v_fma_f32 v146, -v144, v146, v144
	v_fma_f32 v147, -v145, v147, v145
	v_fma_f32 v208, v206, s46, v132
	v_fma_f32 v209, v207, s46, v132
	v_mul_f32_e64 v214, v142, v142
	v_mul_f32_e64 v215, v143, v143
	v_mul_f32_e64 v216, v216, v218
	v_mul_f32_e64 v217, v217, v219
	v_cndmask_b32_e64 v219, v188, v202, s[12:13]
	v_cmp_gt_f32_e64 s[12:13], 0, v144
	v_fma_f32 v180, v178, s46, v132
	v_fma_f32 v181, v179, s46, v132
	v_mul_f32_e64 v182, v156, v156
	v_mul_f32_e64 v183, v157, v157
	v_fma_f32 v208, v206, v208, s48
	v_fma_f32 v209, v207, v209, s48
	v_mul_f32_e64 v214, v214, s54
	v_mul_f32_e64 v215, v215, s54
	v_cndmask_b32_e64 v218, v146, v162, s[12:13]
	v_cmp_gt_f32_e64 s[12:13], 0, v187
	v_fma_f32 v180, v178, v180, s48
	v_fma_f32 v181, v179, v181, s48
	v_mul_f32_e64 v182, v182, s54
	v_mul_f32_e64 v183, v183, s54
	v_mul_f32_e64 v194, v194, v204
	v_mul_f32_e64 v195, v195, v205
	v_fma_f32 v208, v206, v208, s50
	v_fma_f32 v209, v207, v209, s50
	v_exp_f32_e32 v214, v214
	v_exp_f32_e32 v215, v215
	v_cndmask_b32_e64 v187, v189, v203, s[12:13]
	v_cmp_gt_f32_e64 s[12:13], 0, v145
	v_mul_f32_e64 v160, v160, v176
	v_mul_f32_e64 v161, v161, v177
	v_fma_f32 v180, v178, v180, s50
	v_fma_f32 v181, v179, v181, s50
	v_exp_f32_e32 v182, v182
	v_exp_f32_e32 v183, v183
	v_mul_f32_e64 v204, v190, v194
	v_mul_f32_e64 v205, v191, v195
	v_fma_f32 v194, -v190, v194, v190
	v_fma_f32 v195, -v191, v195, v191
	v_fma_f32 v208, v206, v208, s52
	v_fma_f32 v209, v207, v209, s52
	v_cndmask_b32_e64 v186, v147, v163, s[12:13]
	v_cmp_gt_f32_e64 s[12:13], 0, v190
	v_mul_f32_e64 v176, v154, v160
	v_mul_f32_e64 v177, v155, v161
	v_fma_f32 v160, -v154, v160, v154
	v_fma_f32 v161, -v155, v161, v155
	v_fma_f32 v180, v178, v180, s52
	v_fma_f32 v181, v179, v181, s52
	v_mul_f32_e64 v206, v206, v208
	v_mul_f32_e64 v207, v207, v209
	v_mul_f32_e64 v208, v192, v192
	v_mul_f32_e64 v209, v193, v193
	v_cndmask_b32_e64 v147, v194, v204, s[12:13]
	v_cmp_gt_f32_e64 s[12:13], 0, v154
	v_mul_f32_e64 v178, v178, v180
	v_mul_f32_e64 v179, v179, v181
	v_mul_f32_e64 v180, v138, v138
	v_mul_f32_e64 v181, v139, v139
	v_mul_f32_e64 v208, v208, s54
	v_mul_f32_e64 v209, v209, s54
	v_cndmask_b32_e64 v146, v160, v176, s[12:13]
	v_cmp_gt_f32_e64 s[12:13], 0, v191
	v_mul_f32_e64 v180, v180, s54
	v_mul_f32_e64 v181, v181, s54
	v_mul_f32_e64 v206, v214, v206
	v_mul_f32_e64 v207, v215, v207
	v_exp_f32_e32 v208, v208
	v_exp_f32_e32 v209, v209
	v_cndmask_b32_e64 v163, v195, v205, s[12:13]
	v_cmp_gt_f32_e64 s[12:13], 0, v155
	v_mul_f32_e64 v178, v182, v178
	v_mul_f32_e64 v179, v183, v179
	v_exp_f32_e32 v180, v180
	v_exp_f32_e32 v181, v181
	v_mul_f32_e64 v214, v142, v206
	v_mul_f32_e64 v215, v143, v207
	v_fma_f32 v206, -v142, v206, v142
	v_fma_f32 v207, -v143, v207, v143
	v_cndmask_b32_e64 v162, v161, v177, s[12:13]
	v_cmp_gt_f32_e64 s[12:13], 0, v142
	v_mul_f32_e64 v182, v156, v178
	v_mul_f32_e64 v183, v157, v179
	v_fma_f32 v178, -v156, v178, v156
	v_fma_f32 v179, -v157, v179, v157
	v_cndmask_b32_e64 v155, v206, v214, s[12:13]
; __device__ __forceinline__ unsigned cvt_pk_bf16(float lo, float hi) { f32x2_c v = {lo, hi}; bf16x2_c b = __builtin_convertvector(v, bf16x2_c); return __builtin_bit_cast(unsigned, b); }
; __device__ __forceinline__ float silu_f(float g) { return g * __builtin_amdgcn_rcpf(1.0f + __builtin_amdgcn_exp2f(-1.44269504f * g)); }
;     template <int TT> __device__ __forceinline__ void other(const f32x4 (&acc)[2][2][4][2], bf16_t* base, int row0, int col0, PG8_LAS float* my, int t, int hh, int wc, int fq) const {
;     ...
;             for (int m = 0; m < 4; ++m) { bf16_t* rowp = base + (size_t)(row0 + ai * HALF + m * 16) * LDT + col0;
;                 const float rs = my[(ai * 4 + m) * 16]; float ps = 0.f, pq = 0.f; u32x4 gq = {0u, 0u, 0u, 0u};
; #pragma unroll
;                 for (int bj = 0; bj < 2; ++bj) { f32x4 v0 = acc[ai][bj][m][0] * rs + bv[bj][0], v1 = acc[ai][bj][m][1] * rs + bv[bj][1];
;                     if (TT == 3) {
; #pragma unroll
;                         for (int j = 0; j < 4; ++j) { v0[j] = silu_f(v0[j]); v1[j] = silu_f(v1[j]); } }
;                     else if (TT == 4 || TT == 5) { f32x2 a = gelu_pk((f32x2){v0[0], v0[1]}), b = gelu_pk((f32x2){v0[2], v0[3]}), c = gelu_pk((f32x2){v1[0], v1[1]}), d = gelu_pk((f32x2){v1[2], v1[3]});
;     ...
;                     else { u32x4 w; w.x = cvt_pk_bf16(v0[0], v0[1]); w.y = cvt_pk_bf16(v0[2], v0[3]); w.z = cvt_pk_bf16(v1[0], v1[1]); w.w = cvt_pk_bf16(v1[2], v1[3]);
;                         *(u32x4*)(rowp + bj * HALF) = w; } }
;                 if (TT >= 6) *(u32x4*)((unsigned char*)base + (size_t)(row0 + ai * HALF + m * 16) * GATE_PITCH + hh * 256 + (wc * 4 + fq) * 16) = gq;
;                 if (TT == 5) { ps += __shfl_xor(ps, 16); pq += __shfl_xor(pq, 16); ps += __shfl_xor(ps, 32); pq += __shfl_xor(pq, 32);
;                     if (m == 0 || fq == m) { psm = ps; pqm = pq; }
;                     if (m == 3) *(f32x2*)(sgst + ((size_t)((row0 + ai * HALF + fq * 16) * 8 + hh) * 4 + wc) * 2) = (f32x2){psm, pqm}; } }
	v_cmp_gt_f32_e64 s[12:13], 0, v156
	v_mul_f32_e64 v208, v208, v216
	v_mul_f32_e64 v209, v209, v217
	v_mul_f32_e64 v180, v180, v184
	v_mul_f32_e64 v181, v181, v185
	v_cndmask_b32_e64 v154, v178, v182, s[12:13]
	v_cmp_gt_f32_e64 s[12:13], 0, v143
	v_mul_f32_e64 v216, v192, v208
	v_mul_f32_e64 v217, v193, v209
	v_fma_f32 v208, -v192, v208, v192
	v_fma_f32 v209, -v193, v209, v193
	v_cndmask_b32_e64 v161, v207, v215, s[12:13]
	v_cmp_gt_f32_e64 s[12:13], 0, v157
	v_mul_f32_e64 v184, v138, v180
	v_mul_f32_e64 v185, v139, v181
	v_fma_f32 v180, -v138, v180, v138
	v_fma_f32 v181, -v139, v181, v139
	v_cndmask_b32_e64 v160, v179, v183, s[12:13]
	v_cmp_gt_f32_e64 s[12:13], 0, v192
	v_cvt_pk_bf16_f32 v142, v218, v186
	v_cvt_pk_bf16_f32 v143, v146, v162
	v_cndmask_b32_e64 v157, v208, v216, s[12:13]
	v_cmp_gt_f32_e64 s[12:13], 0, v138
	v_cvt_pk_bf16_f32 v144, v154, v160
	s_nop 0
	v_cndmask_b32_e64 v156, v180, v184, s[12:13]
	v_cmp_gt_f32_e64 s[12:13], 0, v193
	s_nop 1
	v_cndmask_b32_e64 v177, v209, v217, s[12:13]
	v_cmp_gt_f32_e64 s[12:13], 0, v139
	v_add_f32_e64 v138, v218, v186
	v_add_f32_e64 v139, v219, v187
	s_nop 0
	v_cndmask_b32_e64 v176, v181, v185, s[12:13]
	v_cvt_pk_bf16_f32 v145, v156, v176
	global_store_dwordx4 v[140:141], v[142:145], off
	v_cmp_eq_u32_e64 s[12:13], 3, v151
	s_nop 0
	v_add_f32_e64 v142, v146, v162
	v_add_f32_e64 v143, v147, v163
	v_add_f32_e64 v144, v156, v176
	v_add_f32_e64 v145, v157, v177
	v_add_f32_e64 v138, v138, v142
	v_add_f32_e64 v139, v139, v143
	v_add_f32_e64 v142, v154, v160
	v_add_f32_e64 v143, v155, v161
	s_nop 0
	v_add_f32_e64 v142, v142, v144
	v_add_f32_e64 v143, v143, v145
	v_mul_f32_e64 v144, v176, v176
	v_mul_f32_e64 v145, v177, v177
	v_add_f32_e64 v138, v138, v142
	v_add_f32_e64 v139, v139, v143
	v_mul_f32_e64 v142, v162, v162
	v_mul_f32_e64 v143, v163, v163
	v_add_f32_e32 v138, 0, v138
	v_add_f32_e32 v178, v139, v138
	v_mul_f32_e64 v138, v186, v186
	v_mul_f32_e64 v139, v187, v187
	v_fma_f32 v142, v146, v146, v142
	v_fma_f32 v143, v147, v147, v143
	v_fma_f32 v138, v218, v218, v138
	v_fma_f32 v139, v219, v219, v139
	v_fma_f32 v144, v156, v156, v144
	v_fma_f32 v145, v157, v157, v145
	v_add_f32_e64 v138, v138, v142
	v_add_f32_e64 v139, v139, v143
	v_mul_f32_e64 v142, v160, v160
	v_mul_f32_e64 v143, v161, v161
	s_nop 0
	v_fma_f32 v142, v154, v154, v142
	v_fma_f32 v143, v155, v155, v143
	s_nop 0
	v_add_f32_e64 v142, v142, v144
	v_add_f32_e64 v143, v143, v145
	v_cvt_pk_bf16_f32 v144, v155, v161
	v_add_f32_e64 v138, v138, v142
	v_add_f32_e64 v139, v139, v143
	v_cvt_pk_bf16_f32 v143, v147, v163
	v_add_f32_e32 v138, v138, v139
	ds_bpermute_b32 v139, v149, v178
	ds_bpermute_b32 v146, v149, v138
	v_cvt_pk_bf16_f32 v142, v219, v187
	v_cvt_pk_bf16_f32 v145, v157, v177
	global_store_dwordx4 v[140:141], v[142:145], off offset:256
	s_waitcnt lgkmcnt(0)
	v_add_f32_e32 v139, v178, v139
	v_add_f32_e32 v146, v138, v146
	ds_bpermute_b32 v147, v148, v139
	ds_bpermute_b32 v154, v148, v146
	v_add_u32_e32 v140, 0x80, v150
	s_waitcnt lgkmcnt(0)
	v_add_f32_e32 v138, v139, v147
	v_add_f32_e32 v139, v146, v154
	v_cndmask_b32_e64 v138, v153, v138, s[12:13]
	v_cndmask_b32_e64 v139, v159, v139, s[12:13]
	global_store_dwordx2 v[136:137], v[138:139], off
	ds_read2_b32 v[138:139], v199 offset0:64 offset1:80
	v_lshl_add_u32 v136, v140, 3, v152
	v_mad_i64_i32 v[140:141], s[2:3], v140, s81, v[134:135]
	v_ashrrev_i32_e32 v137, 31, v136
	s_waitcnt lgkmcnt(0)
	v_fma_f32 v144, v56, v138, 0
	v_fma_f32 v145, v57, v138, 0
	v_fma_f32 v188, v66, v138, 0
	v_fma_f32 v189, v67, v138, 0
	v_and_b32_e32 v143, 0x7fffffff, v145
	v_and_b32_e32 v142, 0x7fffffff, v144
	v_fma_f32 v142, v142, s4, 1.0
	v_fma_f32 v143, v143, s4, 1.0
	v_fma_f32 v152, v58, v138, 0
	v_fma_f32 v153, v59, v138, 0
	v_rcp_f32_e32 v146, v142
	v_rcp_f32_e32 v147, v143
	v_fma_f32 v142, v54, v138, 0
	v_fma_f32 v143, v55, v138, 0
	v_and_b32_e32 v205, 0x7fffffff, v189
	v_and_b32_e32 v183, 0x7fffffff, v143
	v_and_b32_e32 v182, 0x7fffffff, v142
	v_fma_f32 v182, v182, s4, 1.0
	v_fma_f32 v183, v183, s4, 1.0
	v_and_b32_e32 v204, 0x7fffffff, v188
	v_rcp_f32_e32 v182, v182
	v_rcp_f32_e32 v183, v183
	v_and_b32_e32 v163, 0x7fffffff, v153
	v_and_b32_e32 v162, 0x7fffffff, v152
	v_fma_f32 v204, v204, s4, 1.0
	v_fma_f32 v205, v205, s4, 1.0
	v_fma_f32 v184, v182, s46, v132
	v_fma_f32 v185, v183, s46, v132
	v_fma_f32 v162, v162, s4, 1.0
	v_fma_f32 v163, v163, s4, 1.0
	v_fma_f32 v184, v182, v184, s48
	v_fma_f32 v185, v183, v185, s48
	v_rcp_f32_e32 v204, v204
	v_fma_f32 v184, v182, v184, s50
	v_fma_f32 v185, v183, v185, s50
	v_rcp_f32_e32 v205, v205
	v_fma_f32 v184, v182, v184, s52
	v_fma_f32 v185, v183, v185, s52
	v_rcp_f32_e32 v162, v162
	v_mul_f32_e64 v182, v182, v184
	v_mul_f32_e64 v183, v183, v185
	v_fma_f32 v184, v64, v138, 0
	v_fma_f32 v185, v65, v138, 0
	v_rcp_f32_e32 v163, v163
	v_and_b32_e32 v187, 0x7fffffff, v185
	v_and_b32_e32 v186, 0x7fffffff, v184
	v_fma_f32 v186, v186, s4, 1.0
	v_fma_f32 v187, v187, s4, 1.0
	v_fma_f32 v190, v62, v138, 0
	v_fma_f32 v191, v63, v138, 0
	v_rcp_f32_e32 v186, v186
	v_rcp_f32_e32 v187, v187
	v_fma_f32 v206, v204, s46, v132
	v_fma_f32 v207, v205, s46, v132
	v_and_b32_e32 v217, 0x7fffffff, v191
	v_and_b32_e32 v216, 0x7fffffff, v190
	v_fma_f32 v176, v162, s46, v132
	v_fma_f32 v177, v163, s46, v132
	v_fma_f32 v206, v204, v206, s48
	v_fma_f32 v207, v205, v207, s48
	v_fma_f32 v216, v216, s4, 1.0
	v_fma_f32 v217, v217, s4, 1.0
	v_fma_f32 v176, v162, v176, s48
	v_fma_f32 v177, v163, v177, s48
	v_fma_f32 v194, v186, s46, v132
	v_fma_f32 v195, v187, s46, v132
	v_mul_f32_e64 v202, v184, v184
	v_mul_f32_e64 v203, v185, v185
	v_fma_f32 v206, v204, v206, s50
	v_fma_f32 v207, v205, v207, s50
; __device__ __forceinline__ f32x2 gelu_pk(f32x2 v) {
;     const f32x2 av = __builtin_elementwise_abs(v), d = av * 0.2316418882f + 1.0f;
;     f32x2 t; t.x = __builtin_amdgcn_rcpf(d.x); t.y = __builtin_amdgcn_rcpf(d.y);
;     f32x2 q = t * 0.5307027145f + (-0.7265760135f); q = q * t + 0.7107068705f; q = q * t + (-0.142248368f); q = q * t + 0.127414796f; q = q * t;
;     const f32x2 s = (v * v) * (-0.72134752044f);
;     f32x2 e; e.x = __builtin_amdgcn_exp2f(s.x); e.y = __builtin_amdgcn_exp2f(s.y);
;     const f32x2 m = v * (q * e), r = v - m;
;     f32x2 o; o.x = v.x < 0.f ? m.x : r.x; o.y = v.y < 0.f ? m.y : r.y; return o;
; }
	v_rcp_f32_e32 v216, v216
	v_rcp_f32_e32 v217, v217
	v_fma_f32 v156, v146, s46, v132
	v_fma_f32 v157, v147, s46, v132
	v_mul_f32_e64 v160, v144, v144
	v_mul_f32_e64 v161, v145, v145
	v_fma_f32 v176, v162, v176, s50
	v_fma_f32 v177, v163, v177, s50
	v_fma_f32 v192, v60, v138, 0
	v_fma_f32 v193, v61, v138, 0
	v_fma_f32 v194, v186, v194, s48
	v_fma_f32 v195, v187, v195, s48
	v_mul_f32_e64 v202, v202, s54
	v_mul_f32_e64 v203, v203, s54
	v_fma_f32 v206, v204, v206, s52
	v_fma_f32 v207, v205, v207, s52
	v_fma_f32 v154, v52, v138, 0
	v_fma_f32 v155, v53, v138, 0
	v_fma_f32 v156, v146, v156, s48
	v_fma_f32 v157, v147, v157, s48
	v_mul_f32_e64 v160, v160, s54
	v_mul_f32_e64 v161, v161, s54
	v_fma_f32 v176, v162, v176, s52
	v_fma_f32 v177, v163, v177, s52
	v_fma_f32 v194, v186, v194, s50
	v_fma_f32 v195, v187, v195, s50
	v_exp_f32_e32 v202, v202
	v_exp_f32_e32 v203, v203
	v_mul_f32_e64 v204, v204, v206
	v_mul_f32_e64 v205, v205, v207
	v_and_b32_e32 v207, 0x7fffffff, v193
	v_and_b32_e32 v206, 0x7fffffff, v192
	v_fma_f32 v156, v146, v156, s50
	v_fma_f32 v157, v147, v157, s50
	v_exp_f32_e32 v160, v160
	v_exp_f32_e32 v161, v161
	v_mul_f32_e64 v162, v162, v176
	v_mul_f32_e64 v163, v163, v177
	v_and_b32_e32 v177, 0x7fffffff, v155
	v_and_b32_e32 v176, 0x7fffffff, v154
	v_fma_f32 v194, v186, v194, s52
	v_fma_f32 v195, v187, v195, s52
	v_fma_f32 v206, v206, s4, 1.0
	v_fma_f32 v207, v207, s4, 1.0
	v_fma_f32 v156, v146, v156, s52
	v_fma_f32 v157, v147, v157, s52
	v_fma_f32 v176, v176, s4, 1.0
	v_fma_f32 v177, v177, s4, 1.0
	v_mul_f32_e64 v186, v186, v194
	v_mul_f32_e64 v187, v187, v195
	v_mul_f32_e64 v194, v188, v188
	v_mul_f32_e64 v195, v189, v189
	v_rcp_f32_e32 v206, v206
	v_rcp_f32_e32 v207, v207
	v_fma_f32 v218, v216, s46, v132
	v_fma_f32 v219, v217, s46, v132
	v_mul_f32_e64 v146, v146, v156
	v_mul_f32_e64 v147, v147, v157
	v_mul_f32_e64 v156, v152, v152
	v_mul_f32_e64 v157, v153, v153
	v_rcp_f32_e32 v176, v176
	v_rcp_f32_e32 v177, v177
	v_mul_f32_e64 v194, v194, s54
	v_mul_f32_e64 v195, v195, s54
	v_fma_f32 v218, v216, v218, s48
	v_fma_f32 v219, v217, v219, s48
	v_mul_f32_e64 v156, v156, s54
	v_mul_f32_e64 v157, v157, s54
	v_mul_f32_e64 v186, v202, v186
	v_mul_f32_e64 v187, v203, v187
	v_exp_f32_e32 v194, v194
	v_exp_f32_e32 v195, v195
	v_fma_f32 v218, v216, v218, s50
	v_fma_f32 v219, v217, v219, s50
	v_mul_f32_e64 v146, v160, v146
	v_mul_f32_e64 v147, v161, v147
	v_exp_f32_e32 v156, v156
	v_exp_f32_e32 v157, v157
	v_mul_f32_e64 v202, v184, v186
	v_mul_f32_e64 v203, v185, v187
	v_fma_f32 v186, -v184, v186, v184
	v_fma_f32 v187, -v185, v187, v185
	v_fma_f32 v218, v216, v218, s52
	v_fma_f32 v219, v217, v219, s52
	v_cmp_gt_f32_e64 s[14:15], 0, v184
	v_mul_f32_e64 v160, v144, v146
	v_mul_f32_e64 v161, v145, v147
	v_fma_f32 v146, -v144, v146, v144
	v_fma_f32 v147, -v145, v147, v145
	v_fma_f32 v208, v206, s46, v132
	v_fma_f32 v209, v207, s46, v132
	v_mul_f32_e64 v214, v192, v192
	v_mul_f32_e64 v215, v193, v193
	v_mul_f32_e64 v216, v216, v218
	v_mul_f32_e64 v217, v217, v219
	v_cndmask_b32_e64 v219, v186, v202, s[14:15]
	v_cmp_gt_f32_e64 s[14:15], 0, v144
	v_fma_f32 v178, v176, s46, v132
	v_fma_f32 v179, v177, s46, v132
	v_mul_f32_e64 v180, v154, v154
	v_mul_f32_e64 v181, v155, v155
	v_fma_f32 v208, v206, v208, s48
	v_fma_f32 v209, v207, v209, s48
	v_mul_f32_e64 v214, v214, s54
	v_mul_f32_e64 v215, v215, s54
	v_cndmask_b32_e64 v218, v146, v160, s[14:15]
	v_cmp_gt_f32_e64 s[14:15], 0, v185
	v_fma_f32 v178, v176, v178, s48
	v_fma_f32 v179, v177, v179, s48
	v_mul_f32_e64 v180, v180, s54
	v_mul_f32_e64 v181, v181, s54
	v_mul_f32_e64 v194, v194, v204
	v_mul_f32_e64 v195, v195, v205
	v_fma_f32 v208, v206, v208, s50
	v_fma_f32 v209, v207, v209, s50
	v_exp_f32_e32 v214, v214
	v_exp_f32_e32 v215, v215
	v_cndmask_b32_e64 v185, v187, v203, s[14:15]
	v_cmp_gt_f32_e64 s[14:15], 0, v145
	v_mul_f32_e64 v156, v156, v162
	v_mul_f32_e64 v157, v157, v163
	v_fma_f32 v178, v176, v178, s50
	v_fma_f32 v179, v177, v179, s50
	v_exp_f32_e32 v180, v180
	v_exp_f32_e32 v181, v181
	v_mul_f32_e64 v204, v188, v194
	v_mul_f32_e64 v205, v189, v195
	v_fma_f32 v194, -v188, v194, v188
	v_fma_f32 v195, -v189, v195, v189
	v_fma_f32 v208, v206, v208, s52
	v_fma_f32 v209, v207, v209, s52
	v_cndmask_b32_e64 v184, v147, v161, s[14:15]
	v_cmp_gt_f32_e64 s[14:15], 0, v188
	v_mul_f32_e64 v162, v152, v156
	v_mul_f32_e64 v163, v153, v157
	v_fma_f32 v156, -v152, v156, v152
	v_fma_f32 v157, -v153, v157, v153
	v_fma_f32 v178, v176, v178, s52
	v_fma_f32 v179, v177, v179, s52
	v_mul_f32_e64 v206, v206, v208
	v_mul_f32_e64 v207, v207, v209
	v_mul_f32_e64 v208, v190, v190
	v_mul_f32_e64 v209, v191, v191
	v_cndmask_b32_e64 v147, v194, v204, s[14:15]
	v_cmp_gt_f32_e64 s[14:15], 0, v152
	v_mul_f32_e64 v176, v176, v178
	v_mul_f32_e64 v177, v177, v179
	v_mul_f32_e64 v178, v142, v142
	v_mul_f32_e64 v179, v143, v143
	v_mul_f32_e64 v208, v208, s54
	v_mul_f32_e64 v209, v209, s54
	v_cndmask_b32_e64 v146, v156, v162, s[14:15]
	v_cmp_gt_f32_e64 s[14:15], 0, v189
	v_mul_f32_e64 v178, v178, s54
	v_mul_f32_e64 v179, v179, s54
	v_mul_f32_e64 v206, v214, v206
	v_mul_f32_e64 v207, v215, v207
	v_exp_f32_e32 v208, v208
	v_exp_f32_e32 v209, v209
	v_cndmask_b32_e64 v161, v195, v205, s[14:15]
	v_cmp_gt_f32_e64 s[14:15], 0, v153
	v_mul_f32_e64 v176, v180, v176
	v_mul_f32_e64 v177, v181, v177
	v_exp_f32_e32 v178, v178
	v_exp_f32_e32 v179, v179
	v_mul_f32_e64 v214, v192, v206
	v_mul_f32_e64 v215, v193, v207
	v_fma_f32 v206, -v192, v206, v192
	v_fma_f32 v207, -v193, v207, v193
	v_cndmask_b32_e64 v160, v157, v163, s[14:15]
	v_cmp_gt_f32_e64 s[14:15], 0, v192
	v_mul_f32_e64 v180, v154, v176
	v_mul_f32_e64 v181, v155, v177
	v_fma_f32 v176, -v154, v176, v154
;     template <int TT> __device__ __forceinline__ void other(const f32x4 (&acc)[2][2][4][2], bf16_t* base, int row0, int col0, PG8_LAS float* my, int t, int hh, int wc, int fq) const {
;     ...
;                 for (int bj = 0; bj < 2; ++bj) { f32x4 v0 = acc[ai][bj][m][0] * rs + bv[bj][0], v1 = acc[ai][bj][m][1] * rs + bv[bj][1];
;                     if (TT == 3) {
; #pragma unroll
;                         for (int j = 0; j < 4; ++j) { v0[j] = silu_f(v0[j]); v1[j] = silu_f(v1[j]); } }
;                     else if (TT == 4 || TT == 5) { f32x2 a = gelu_pk((f32x2){v0[0], v0[1]}), b = gelu_pk((f32x2){v0[2], v0[3]}), c = gelu_pk((f32x2){v1[0], v1[1]}), d = gelu_pk((f32x2){v1[2], v1[3]});
;                         v0 = (f32x4){a.x, a.y, b.x, b.y}; v1 = (f32x4){c.x, c.y, d.x, d.y};
;                         if (TT == 5) { ps += ((v0[0] + v0[1]) + (v0[2] + v0[3])) + ((v1[0] + v1[1]) + (v1[2] + v1[3]));
;                             pq += ((v0[0] * v0[0] + v0[1] * v0[1]) + (v0[2] * v0[2] + v0[3] * v0[3])) + ((v1[0] * v1[0] + v1[1] * v1[1]) + (v1[2] * v1[2] + v1[3] * v1[3])); } }
;                     else if (TT >= 6) {
; #pragma unroll
;                         for (int j = 0; j < 4; ++j) { v0[j] = sigmoid_f(v0[j]); v1[j] = sigmoid_f(v1[j]); } }
;                     if (TT >= 6) { unsigned b0 = 0u, b1 = 0u;
; #pragma unroll
;                         for (int j = 0; j < 4; ++j) { b0 = __builtin_amdgcn_cvt_pk_u8_f32(__builtin_rintf(v0[j] * 255.0f), j, b0); b1 = __builtin_amdgcn_cvt_pk_u8_f32(__builtin_rintf(v1[j] * 255.0f), j, b1); }
;                         if (bj == 0) { gq.x = b0; gq.y = b1; } else { gq.z = b0; gq.w = b1; } }
;                     else { u32x4 w; w.x = cvt_pk_bf16(v0[0], v0[1]); w.y = cvt_pk_bf16(v0[2], v0[3]); w.z = cvt_pk_bf16(v1[0], v1[1]); w.w = cvt_pk_bf16(v1[2], v1[3]);
;                         *(u32x4*)(rowp + bj * HALF) = w; } }
;                 if (TT >= 6) *(u32x4*)((unsigned char*)base + (size_t)(row0 + ai * HALF + m * 16) * GATE_PITCH + hh * 256 + (wc * 4 + fq) * 16) = gq;
;                 if (TT == 5) { ps += __shfl_xor(ps, 16); pq += __shfl_xor(pq, 16); ps += __shfl_xor(ps, 32); pq += __shfl_xor(pq, 32);
;                     if (m == 0 || fq == m) { psm = ps; pqm = pq; }
;                     if (m == 3) *(f32x2*)(sgst + ((size_t)((row0 + ai * HALF + fq * 16) * 8 + hh) * 4 + wc) * 2) = (f32x2){psm, pqm}; } }
	v_fma_f32 v177, -v155, v177, v155
	v_cndmask_b32_e64 v153, v206, v214, s[14:15]
	v_cmp_gt_f32_e64 s[14:15], 0, v154
	v_mul_f32_e64 v208, v208, v216
	v_mul_f32_e64 v209, v209, v217
	v_mul_f32_e64 v178, v178, v182
	v_mul_f32_e64 v179, v179, v183
	v_cndmask_b32_e64 v152, v176, v180, s[14:15]
	v_cmp_gt_f32_e64 s[14:15], 0, v193
	v_mul_f32_e64 v216, v190, v208
	v_mul_f32_e64 v217, v191, v209
	v_fma_f32 v208, -v190, v208, v190
	v_fma_f32 v209, -v191, v209, v191
	v_cndmask_b32_e64 v157, v207, v215, s[14:15]
	v_cmp_gt_f32_e64 s[14:15], 0, v155
	v_mul_f32_e64 v182, v142, v178
	v_mul_f32_e64 v183, v143, v179
	v_fma_f32 v178, -v142, v178, v142
	v_fma_f32 v179, -v143, v179, v143
	v_cndmask_b32_e64 v156, v177, v181, s[14:15]
	v_cmp_gt_f32_e64 s[14:15], 0, v190
	v_add_f32_e64 v176, v218, v184
	v_add_f32_e64 v177, v219, v185
	v_cvt_pk_bf16_f32 v144, v152, v156
	v_cndmask_b32_e64 v155, v208, v216, s[14:15]
	v_cmp_gt_f32_e64 s[14:15], 0, v142
	v_cvt_pk_bf16_f32 v142, v218, v184
	v_lshlrev_b64 v[136:137], 5, v[136:137]
	v_cndmask_b32_e64 v154, v178, v182, s[14:15]
	v_cmp_gt_f32_e64 s[14:15], 0, v191
	s_nop 1
	v_cndmask_b32_e64 v163, v209, v217, s[14:15]
	v_cmp_gt_f32_e64 s[14:15], 0, v143
	v_cvt_pk_bf16_f32 v143, v146, v160
	s_nop 0
	v_cndmask_b32_e64 v162, v179, v183, s[14:15]
	v_add_f32_e64 v178, v146, v160
	v_add_f32_e64 v179, v147, v161
	v_add_f32_e64 v180, v154, v162
	v_add_f32_e64 v181, v155, v163
	v_add_f32_e64 v176, v176, v178
	v_add_f32_e64 v177, v177, v179
	v_add_f32_e64 v178, v152, v156
	v_add_f32_e64 v179, v153, v157
	v_cvt_pk_bf16_f32 v145, v154, v162
	v_add_f32_e64 v178, v178, v180
	v_add_f32_e64 v179, v179, v181
	v_mul_f32_e64 v180, v162, v162
	v_mul_f32_e64 v181, v163, v163
	v_add_f32_e64 v176, v176, v178
	v_add_f32_e64 v177, v177, v179
	v_mul_f32_e64 v178, v160, v160
	v_mul_f32_e64 v179, v161, v161
	v_add_f32_e32 v138, 0, v176
	v_add_f32_e32 v138, v177, v138
	v_mul_f32_e64 v176, v184, v184
	v_mul_f32_e64 v177, v185, v185
	v_fma_f32 v178, v146, v146, v178
	v_fma_f32 v179, v147, v147, v179
	v_fma_f32 v176, v218, v218, v176
	v_fma_f32 v177, v219, v219, v177
	v_fma_f32 v180, v154, v154, v180
	v_fma_f32 v181, v155, v155, v181
	v_add_f32_e64 v176, v176, v178
	v_add_f32_e64 v177, v177, v179
	v_mul_f32_e64 v178, v156, v156
	v_mul_f32_e64 v179, v157, v157
	ds_bpermute_b32 v151, v149, v138
	v_fma_f32 v178, v152, v152, v178
	v_fma_f32 v179, v153, v153, v179
	global_store_dwordx4 v[140:141], v[142:145], off
	v_add_f32_e64 v178, v178, v180
	v_add_f32_e64 v179, v179, v181
	s_waitcnt lgkmcnt(0)
	v_add_f32_e32 v138, v138, v151
	v_add_f32_e64 v176, v176, v178
	v_add_f32_e64 v177, v177, v179
	v_cvt_pk_bf16_f32 v143, v147, v161
	v_add_f32_e32 v146, v176, v177
	ds_bpermute_b32 v152, v149, v146
	ds_bpermute_b32 v147, v148, v138
	v_cvt_pk_bf16_f32 v142, v219, v185
	v_cvt_pk_bf16_f32 v144, v153, v157
	v_cvt_pk_bf16_f32 v145, v155, v163
	s_waitcnt lgkmcnt(0)
	v_add_f32_e32 v146, v146, v152
	ds_bpermute_b32 v151, v148, v146
	global_store_dwordx4 v[140:141], v[142:145], off offset:256
	v_add_f32_e32 v159, v138, v147
	v_add_u32_e32 v138, 0x90, v150
	v_mov_b32_e32 v142, v139
	v_fma_f32 v144, v40, v142, 0
	v_fma_f32 v145, v41, v142, 0
	v_mad_i64_i32 v[140:141], s[2:3], v138, s81, v[134:135]
	v_and_b32_e32 v139, 0x7fffffff, v145
	v_and_b32_e32 v138, 0x7fffffff, v144
	v_fma_f32 v138, v138, s4, 1.0
	v_fma_f32 v139, v139, s4, 1.0
	s_waitcnt lgkmcnt(0)
	v_add_f32_e32 v151, v146, v151
	v_rcp_f32_e32 v146, v138
	v_rcp_f32_e32 v147, v139
	v_fma_f32 v138, v38, v142, 0
	v_fma_f32 v139, v39, v142, 0
	v_fma_f32 v188, v50, v142, 0
	v_fma_f32 v189, v51, v142, 0
	v_and_b32_e32 v183, 0x7fffffff, v139
	v_and_b32_e32 v182, 0x7fffffff, v138
	v_fma_f32 v182, v182, s4, 1.0
	v_fma_f32 v183, v183, s4, 1.0
	v_fma_f32 v152, v42, v142, 0
	v_fma_f32 v153, v43, v142, 0
	v_rcp_f32_e32 v182, v182
	v_rcp_f32_e32 v183, v183
	v_and_b32_e32 v203, 0x7fffffff, v189
	v_and_b32_e32 v202, 0x7fffffff, v188
	v_and_b32_e32 v163, 0x7fffffff, v153
	v_fma_f32 v184, v182, s46, v132
	v_fma_f32 v185, v183, s46, v132
	v_and_b32_e32 v162, 0x7fffffff, v152
	v_fma_f32 v184, v182, v184, s48
	v_fma_f32 v185, v183, v185, s48
	v_fma_f32 v202, v202, s4, 1.0
	v_fma_f32 v203, v203, s4, 1.0
	v_fma_f32 v184, v182, v184, s50
	v_fma_f32 v185, v183, v185, s50
	v_fma_f32 v162, v162, s4, 1.0
	v_fma_f32 v163, v163, s4, 1.0
	v_fma_f32 v184, v182, v184, s52
	v_fma_f32 v185, v183, v185, s52
	v_rcp_f32_e32 v202, v202
	v_mul_f32_e64 v182, v182, v184
	v_mul_f32_e64 v183, v183, v185
	v_fma_f32 v184, v48, v142, 0
	v_fma_f32 v185, v49, v142, 0
	v_rcp_f32_e32 v203, v203
	v_and_b32_e32 v187, 0x7fffffff, v185
	v_and_b32_e32 v186, 0x7fffffff, v184
	v_rcp_f32_e32 v162, v162
	v_rcp_f32_e32 v163, v163
	v_fma_f32 v186, v186, s4, 1.0
	v_fma_f32 v187, v187, s4, 1.0
	v_fma_f32 v190, v46, v142, 0
	v_fma_f32 v191, v47, v142, 0
	v_rcp_f32_e32 v186, v186
	v_rcp_f32_e32 v187, v187
	v_fma_f32 v204, v202, s46, v132
	v_fma_f32 v205, v203, s46, v132
	v_and_b32_e32 v215, 0x7fffffff, v191
	v_and_b32_e32 v214, 0x7fffffff, v190
	v_fma_f32 v176, v162, s46, v132
	v_fma_f32 v177, v163, s46, v132
	v_fma_f32 v204, v202, v204, s48
	v_fma_f32 v205, v203, v205, s48
	v_fma_f32 v214, v214, s4, 1.0
	v_fma_f32 v215, v215, s4, 1.0
	v_fma_f32 v176, v162, v176, s48
	v_fma_f32 v177, v163, v177, s48
	v_fma_f32 v192, v186, s46, v132
	v_fma_f32 v193, v187, s46, v132
	v_mul_f32_e64 v194, v184, v184
	v_mul_f32_e64 v195, v185, v185
	v_fma_f32 v204, v202, v204, s50
	v_fma_f32 v205, v203, v205, s50
	v_rcp_f32_e32 v214, v214
	v_rcp_f32_e32 v215, v215
	v_fma_f32 v154, v36, v142, 0
	v_fma_f32 v155, v37, v142, 0
	v_fma_f32 v156, v146, s46, v132
	v_fma_f32 v157, v147, s46, v132
; __device__ __forceinline__ f32x2 gelu_pk(f32x2 v) {
;     const f32x2 av = __builtin_elementwise_abs(v), d = av * 0.2316418882f + 1.0f;
;     f32x2 t; t.x = __builtin_amdgcn_rcpf(d.x); t.y = __builtin_amdgcn_rcpf(d.y);
;     f32x2 q = t * 0.5307027145f + (-0.7265760135f); q = q * t + 0.7107068705f; q = q * t + (-0.142248368f); q = q * t + 0.127414796f; q = q * t;
;     const f32x2 s = (v * v) * (-0.72134752044f);
;     f32x2 e; e.x = __builtin_amdgcn_exp2f(s.x); e.y = __builtin_amdgcn_exp2f(s.y);
;     const f32x2 m = v * (q * e), r = v - m;
;     f32x2 o; o.x = v.x < 0.f ? m.x : r.x; o.y = v.y < 0.f ? m.y : r.y; return o;
; }
	v_mul_f32_e64 v160, v144, v144
	v_mul_f32_e64 v161, v145, v145
	v_fma_f32 v176, v162, v176, s50
	v_fma_f32 v177, v163, v177, s50
	v_fma_f32 v143, v45, v142, 0
	v_fma_f32 v142, v44, v142, 0
	v_fma_f32 v192, v186, v192, s48
	v_fma_f32 v193, v187, v193, s48
	v_mul_f32_e64 v194, v194, s54
	v_mul_f32_e64 v195, v195, s54
	v_fma_f32 v204, v202, v204, s52
	v_fma_f32 v205, v203, v205, s52
	v_fma_f32 v156, v146, v156, s48
	v_fma_f32 v157, v147, v157, s48
	v_mul_f32_e64 v160, v160, s54
	v_mul_f32_e64 v161, v161, s54
	v_fma_f32 v176, v162, v176, s52
	v_fma_f32 v177, v163, v177, s52
	v_fma_f32 v192, v186, v192, s50
	v_fma_f32 v193, v187, v193, s50
	v_exp_f32_e32 v194, v194
	v_exp_f32_e32 v195, v195
	v_mul_f32_e64 v202, v202, v204
	v_mul_f32_e64 v203, v203, v205
	v_and_b32_e32 v205, 0x7fffffff, v143
	v_and_b32_e32 v204, 0x7fffffff, v142
	v_fma_f32 v156, v146, v156, s50
	v_fma_f32 v157, v147, v157, s50
	v_exp_f32_e32 v160, v160
	v_exp_f32_e32 v161, v161
	v_mul_f32_e64 v162, v162, v176
	v_mul_f32_e64 v163, v163, v177
	v_and_b32_e32 v177, 0x7fffffff, v155
	v_and_b32_e32 v176, 0x7fffffff, v154
	v_fma_f32 v192, v186, v192, s52
	v_fma_f32 v193, v187, v193, s52
	v_fma_f32 v204, v204, s4, 1.0
	v_fma_f32 v205, v205, s4, 1.0
	v_fma_f32 v156, v146, v156, s52
	v_fma_f32 v157, v147, v157, s52
	v_fma_f32 v176, v176, s4, 1.0
	v_fma_f32 v177, v177, s4, 1.0
	v_mul_f32_e64 v186, v186, v192
	v_mul_f32_e64 v187, v187, v193
	v_mul_f32_e64 v192, v188, v188
	v_mul_f32_e64 v193, v189, v189
	v_rcp_f32_e32 v204, v204
	v_rcp_f32_e32 v205, v205
	v_fma_f32 v216, v214, s46, v132
	v_fma_f32 v217, v215, s46, v132
	v_mul_f32_e64 v146, v146, v156
	v_mul_f32_e64 v147, v147, v157
	v_mul_f32_e64 v156, v152, v152
	v_mul_f32_e64 v157, v153, v153
	v_rcp_f32_e32 v176, v176
	v_rcp_f32_e32 v177, v177
	v_mul_f32_e64 v192, v192, s54
	v_mul_f32_e64 v193, v193, s54
	v_fma_f32 v216, v214, v216, s48
	v_fma_f32 v217, v215, v217, s48
	v_mul_f32_e64 v156, v156, s54
	v_mul_f32_e64 v157, v157, s54
	v_mul_f32_e64 v186, v194, v186
	v_mul_f32_e64 v187, v195, v187
	v_exp_f32_e32 v192, v192
	v_exp_f32_e32 v193, v193
	v_fma_f32 v216, v214, v216, s50
	v_fma_f32 v217, v215, v217, s50
	v_mul_f32_e64 v146, v160, v146
	v_mul_f32_e64 v147, v161, v147
	v_exp_f32_e32 v156, v156
	v_exp_f32_e32 v157, v157
	v_mul_f32_e64 v194, v184, v186
	v_mul_f32_e64 v195, v185, v187
	v_fma_f32 v186, -v184, v186, v184
	v_fma_f32 v187, -v185, v187, v185
	v_fma_f32 v216, v214, v216, s52
	v_fma_f32 v217, v215, v217, s52
	v_cmp_gt_f32_e64 s[14:15], 0, v184
	v_mul_f32_e64 v160, v144, v146
	v_mul_f32_e64 v161, v145, v147
	v_fma_f32 v146, -v144, v146, v144
	v_fma_f32 v147, -v145, v147, v145
	v_fma_f32 v206, v204, s46, v132
	v_fma_f32 v207, v205, s46, v132
	v_mul_f32_e64 v208, v142, v142
	v_mul_f32_e64 v209, v143, v143
	v_mul_f32_e64 v214, v214, v216
	v_mul_f32_e64 v215, v215, v217
	v_cndmask_b32_e64 v217, v186, v194, s[14:15]
	v_cmp_gt_f32_e64 s[14:15], 0, v144
	v_fma_f32 v178, v176, s46, v132
	v_fma_f32 v179, v177, s46, v132
	v_mul_f32_e64 v180, v154, v154
	v_mul_f32_e64 v181, v155, v155
	v_fma_f32 v206, v204, v206, s48
	v_fma_f32 v207, v205, v207, s48
	v_mul_f32_e64 v208, v208, s54
	v_mul_f32_e64 v209, v209, s54
	v_cndmask_b32_e64 v216, v146, v160, s[14:15]
	v_cmp_gt_f32_e64 s[14:15], 0, v185
	v_fma_f32 v178, v176, v178, s48
	v_fma_f32 v179, v177, v179, s48
	v_mul_f32_e64 v180, v180, s54
	v_mul_f32_e64 v181, v181, s54
	v_mul_f32_e64 v192, v192, v202
	v_mul_f32_e64 v193, v193, v203
	v_fma_f32 v206, v204, v206, s50
	v_fma_f32 v207, v205, v207, s50
	v_exp_f32_e32 v208, v208
	v_exp_f32_e32 v209, v209
	v_cndmask_b32_e64 v185, v187, v195, s[14:15]
	v_cmp_gt_f32_e64 s[14:15], 0, v145
	v_mul_f32_e64 v156, v156, v162
	v_mul_f32_e64 v157, v157, v163
	v_fma_f32 v178, v176, v178, s50
	v_fma_f32 v179, v177, v179, s50
	v_exp_f32_e32 v180, v180
	v_exp_f32_e32 v181, v181
	v_mul_f32_e64 v202, v188, v192
	v_mul_f32_e64 v203, v189, v193
	v_fma_f32 v192, -v188, v192, v188
	v_fma_f32 v193, -v189, v193, v189
	v_fma_f32 v206, v204, v206, s52
	v_fma_f32 v207, v205, v207, s52
	v_cndmask_b32_e64 v184, v147, v161, s[14:15]
	v_cmp_gt_f32_e64 s[14:15], 0, v188
	v_mul_f32_e64 v162, v152, v156
	v_mul_f32_e64 v163, v153, v157
	v_fma_f32 v156, -v152, v156, v152
	v_fma_f32 v157, -v153, v157, v153
	v_fma_f32 v178, v176, v178, s52
	v_fma_f32 v179, v177, v179, s52
	v_mul_f32_e64 v204, v204, v206
	v_mul_f32_e64 v205, v205, v207
	v_mul_f32_e64 v206, v190, v190
	v_mul_f32_e64 v207, v191, v191
	v_cndmask_b32_e64 v147, v192, v202, s[14:15]
	v_cmp_gt_f32_e64 s[14:15], 0, v152
	v_mul_f32_e64 v176, v176, v178
	v_mul_f32_e64 v177, v177, v179
	v_mul_f32_e64 v178, v138, v138
	v_mul_f32_e64 v179, v139, v139
	v_mul_f32_e64 v206, v206, s54
	v_mul_f32_e64 v207, v207, s54
	v_cndmask_b32_e64 v146, v156, v162, s[14:15]
	v_cmp_gt_f32_e64 s[14:15], 0, v189
	v_mul_f32_e64 v178, v178, s54
	v_mul_f32_e64 v179, v179, s54
	v_mul_f32_e64 v204, v208, v204
	v_mul_f32_e64 v205, v209, v205
	v_exp_f32_e32 v206, v206
	v_exp_f32_e32 v207, v207
	v_cndmask_b32_e64 v161, v193, v203, s[14:15]
	v_cmp_gt_f32_e64 s[14:15], 0, v153
	v_mul_f32_e64 v176, v180, v176
	v_mul_f32_e64 v177, v181, v177
	v_exp_f32_e32 v178, v178
	v_exp_f32_e32 v179, v179
	v_mul_f32_e64 v208, v142, v204
	v_mul_f32_e64 v209, v143, v205
	v_fma_f32 v204, -v142, v204, v142
	v_fma_f32 v205, -v143, v205, v143
	v_cndmask_b32_e64 v160, v157, v163, s[14:15]
	v_cmp_gt_f32_e64 s[14:15], 0, v142
	v_mul_f32_e64 v180, v154, v176
	v_mul_f32_e64 v181, v155, v177
	v_fma_f32 v176, -v154, v176, v154
	v_fma_f32 v177, -v155, v177, v155
	v_cndmask_b32_e64 v153, v204, v208, s[14:15]
	v_cmp_gt_f32_e64 s[14:15], 0, v154
	v_mul_f32_e64 v206, v206, v214
;     template <int TT> __device__ __forceinline__ void other(const f32x4 (&acc)[2][2][4][2], bf16_t* base, int row0, int col0, PG8_LAS float* my, int t, int hh, int wc, int fq) const {
;     ...
;                 for (int bj = 0; bj < 2; ++bj) { f32x4 v0 = acc[ai][bj][m][0] * rs + bv[bj][0], v1 = acc[ai][bj][m][1] * rs + bv[bj][1];
;                     if (TT == 3) {
; #pragma unroll
;                         for (int j = 0; j < 4; ++j) { v0[j] = silu_f(v0[j]); v1[j] = silu_f(v1[j]); } }
;                     else if (TT == 4 || TT == 5) { f32x2 a = gelu_pk((f32x2){v0[0], v0[1]}), b = gelu_pk((f32x2){v0[2], v0[3]}), c = gelu_pk((f32x2){v1[0], v1[1]}), d = gelu_pk((f32x2){v1[2], v1[3]});
;                         v0 = (f32x4){a.x, a.y, b.x, b.y}; v1 = (f32x4){c.x, c.y, d.x, d.y};
;                         if (TT == 5) { ps += ((v0[0] + v0[1]) + (v0[2] + v0[3])) + ((v1[0] + v1[1]) + (v1[2] + v1[3]));
;                             pq += ((v0[0] * v0[0] + v0[1] * v0[1]) + (v0[2] * v0[2] + v0[3] * v0[3])) + ((v1[0] * v1[0] + v1[1] * v1[1]) + (v1[2] * v1[2] + v1[3] * v1[3])); } }
;                     else if (TT >= 6) {
; #pragma unroll
;                         for (int j = 0; j < 4; ++j) { v0[j] = sigmoid_f(v0[j]); v1[j] = sigmoid_f(v1[j]); } }
;                     if (TT >= 6) { unsigned b0 = 0u, b1 = 0u;
; #pragma unroll
;                         for (int j = 0; j < 4; ++j) { b0 = __builtin_amdgcn_cvt_pk_u8_f32(__builtin_rintf(v0[j] * 255.0f), j, b0); b1 = __builtin_amdgcn_cvt_pk_u8_f32(__builtin_rintf(v1[j] * 255.0f), j, b1); }
;                         if (bj == 0) { gq.x = b0; gq.y = b1; } else { gq.z = b0; gq.w = b1; } }
;                     else { u32x4 w; w.x = cvt_pk_bf16(v0[0], v0[1]); w.y = cvt_pk_bf16(v0[2], v0[3]); w.z = cvt_pk_bf16(v1[0], v1[1]); w.w = cvt_pk_bf16(v1[2], v1[3]);
;                         *(u32x4*)(rowp + bj * HALF) = w; } }
;                 if (TT >= 6) *(u32x4*)((unsigned char*)base + (size_t)(row0 + ai * HALF + m * 16) * GATE_PITCH + hh * 256 + (wc * 4 + fq) * 16) = gq;
;                 if (TT == 5) { ps += __shfl_xor(ps, 16); pq += __shfl_xor(pq, 16); ps += __shfl_xor(ps, 32); pq += __shfl_xor(pq, 32);
;                     if (m == 0 || fq == m) { psm = ps; pqm = pq; }
;                     if (m == 3) *(f32x2*)(sgst + ((size_t)((row0 + ai * HALF + fq * 16) * 8 + hh) * 4 + wc) * 2) = (f32x2){psm, pqm}; } }
	v_mul_f32_e64 v207, v207, v215
	v_mul_f32_e64 v178, v178, v182
	v_mul_f32_e64 v179, v179, v183
	v_cndmask_b32_e64 v152, v176, v180, s[14:15]
	v_cmp_gt_f32_e64 s[14:15], 0, v143
	v_mul_f32_e64 v214, v190, v206
	v_mul_f32_e64 v215, v191, v207
	v_fma_f32 v206, -v190, v206, v190
	v_fma_f32 v207, -v191, v207, v191
	v_cndmask_b32_e64 v157, v205, v209, s[14:15]
	v_cmp_gt_f32_e64 s[14:15], 0, v155
	v_mul_f32_e64 v182, v138, v178
	v_mul_f32_e64 v183, v139, v179
	v_fma_f32 v178, -v138, v178, v138
	v_fma_f32 v179, -v139, v179, v139
	v_cndmask_b32_e64 v156, v177, v181, s[14:15]
	v_cmp_gt_f32_e64 s[14:15], 0, v190
	v_add_f32_e64 v176, v146, v160
	v_add_f32_e64 v177, v147, v161
	v_cvt_pk_bf16_f32 v143, v146, v160
	v_cndmask_b32_e64 v155, v206, v214, s[14:15]
	v_cmp_gt_f32_e64 s[14:15], 0, v138
	v_cvt_pk_bf16_f32 v142, v216, v184
	v_cvt_pk_bf16_f32 v144, v152, v156
	v_cndmask_b32_e64 v154, v178, v182, s[14:15]
	v_cmp_gt_f32_e64 s[14:15], 0, v191
	s_nop 1
	v_cndmask_b32_e64 v163, v207, v215, s[14:15]
	v_cmp_gt_f32_e64 s[14:15], 0, v139
	v_add_f32_e64 v138, v216, v184
	v_add_f32_e64 v139, v217, v185
	s_nop 0
	v_cndmask_b32_e64 v162, v179, v183, s[14:15]
	v_add_f32_e64 v138, v138, v176
	v_add_f32_e64 v139, v139, v177
	v_add_f32_e64 v176, v152, v156
	v_add_f32_e64 v177, v153, v157
	v_add_f32_e64 v178, v154, v162
	v_add_f32_e64 v179, v155, v163
	v_cvt_pk_bf16_f32 v145, v154, v162
	v_add_f32_e64 v176, v176, v178
	v_add_f32_e64 v177, v177, v179
	v_mul_f32_e64 v178, v162, v162
	v_mul_f32_e64 v179, v163, v163
	v_add_f32_e64 v138, v138, v176
	v_add_f32_e64 v139, v139, v177
	v_mul_f32_e64 v176, v160, v160
	v_mul_f32_e64 v177, v161, v161
	v_add_f32_e32 v138, 0, v138
	v_add_f32_e32 v180, v139, v138
	v_mul_f32_e64 v138, v184, v184
	v_mul_f32_e64 v139, v185, v185
	v_fma_f32 v176, v146, v146, v176
	v_fma_f32 v177, v147, v147, v177
	v_fma_f32 v138, v216, v216, v138
	v_fma_f32 v139, v217, v217, v139
	v_fma_f32 v178, v154, v154, v178
	v_fma_f32 v179, v155, v155, v179
	v_add_f32_e64 v138, v138, v176
	v_add_f32_e64 v139, v139, v177
	v_mul_f32_e64 v176, v156, v156
	v_mul_f32_e64 v177, v157, v157
	global_store_dwordx4 v[140:141], v[142:145], off
	v_fma_f32 v176, v152, v152, v176
	v_fma_f32 v177, v153, v153, v177
	s_nop 0
	v_add_f32_e64 v176, v176, v178
	v_add_f32_e64 v177, v177, v179
	v_cvt_pk_bf16_f32 v143, v147, v161
	v_add_f32_e64 v138, v138, v176
	v_add_f32_e64 v139, v139, v177
	v_cvt_pk_bf16_f32 v142, v217, v185
	v_add_f32_e32 v138, v138, v139
	ds_bpermute_b32 v146, v149, v138
	ds_bpermute_b32 v139, v149, v180
	v_cvt_pk_bf16_f32 v144, v153, v157
	v_cvt_pk_bf16_f32 v145, v155, v163
	global_store_dwordx4 v[140:141], v[142:145], off offset:256
	s_waitcnt lgkmcnt(0)
	v_add_f32_e32 v138, v138, v146
	v_add_f32_e32 v139, v180, v139
	ds_bpermute_b32 v147, v148, v138
	ds_bpermute_b32 v146, v148, v139
	s_waitcnt lgkmcnt(0)
	v_add_f32_e32 v138, v138, v147
	v_add_f32_e32 v140, v139, v146
	v_cndmask_b32_e32 v151, v151, v138, vcc
	ds_read2_b32 v[138:139], v199 offset0:96 offset1:112
	v_cndmask_b32_e32 v159, v159, v140, vcc
	v_add_u32_e32 v140, 0xa0, v150
	v_mad_i64_i32 v[140:141], s[2:3], v140, s81, v[134:135]
	s_waitcnt lgkmcnt(0)
	v_fma_f32 v144, v24, v138, 0
	v_fma_f32 v145, v25, v138, 0
	v_fma_f32 v188, v34, v138, 0
	v_fma_f32 v189, v35, v138, 0
	v_and_b32_e32 v143, 0x7fffffff, v145
	v_and_b32_e32 v142, 0x7fffffff, v144
	v_fma_f32 v142, v142, s4, 1.0
	v_fma_f32 v143, v143, s4, 1.0
	v_fma_f32 v152, v26, v138, 0
	v_fma_f32 v153, v27, v138, 0
	v_rcp_f32_e32 v146, v142
	v_rcp_f32_e32 v147, v143
	v_fma_f32 v142, v22, v138, 0
	v_fma_f32 v143, v23, v138, 0
	v_and_b32_e32 v205, 0x7fffffff, v189
	v_and_b32_e32 v183, 0x7fffffff, v143
	v_and_b32_e32 v182, 0x7fffffff, v142
	v_fma_f32 v182, v182, s4, 1.0
	v_fma_f32 v183, v183, s4, 1.0
	v_and_b32_e32 v204, 0x7fffffff, v188
	v_rcp_f32_e32 v182, v182
	v_rcp_f32_e32 v183, v183
	v_and_b32_e32 v163, 0x7fffffff, v153
	v_and_b32_e32 v162, 0x7fffffff, v152
	v_fma_f32 v204, v204, s4, 1.0
	v_fma_f32 v205, v205, s4, 1.0
	v_fma_f32 v184, v182, s46, v132
	v_fma_f32 v185, v183, s46, v132
	v_fma_f32 v162, v162, s4, 1.0
	v_fma_f32 v163, v163, s4, 1.0
	v_fma_f32 v184, v182, v184, s48
	v_fma_f32 v185, v183, v185, s48
	v_rcp_f32_e32 v204, v204
	v_fma_f32 v184, v182, v184, s50
	v_fma_f32 v185, v183, v185, s50
	v_rcp_f32_e32 v205, v205
	v_fma_f32 v184, v182, v184, s52
	v_fma_f32 v185, v183, v185, s52
	v_rcp_f32_e32 v162, v162
	v_mul_f32_e64 v182, v182, v184
	v_mul_f32_e64 v183, v183, v185
	v_fma_f32 v184, v32, v138, 0
	v_fma_f32 v185, v33, v138, 0
	v_rcp_f32_e32 v163, v163
	v_and_b32_e32 v187, 0x7fffffff, v185
	v_and_b32_e32 v186, 0x7fffffff, v184
	v_fma_f32 v186, v186, s4, 1.0
	v_fma_f32 v187, v187, s4, 1.0
	v_fma_f32 v190, v30, v138, 0
	v_fma_f32 v191, v31, v138, 0
	v_rcp_f32_e32 v186, v186
	v_rcp_f32_e32 v187, v187
	v_fma_f32 v206, v204, s46, v132
	v_fma_f32 v207, v205, s46, v132
	v_and_b32_e32 v217, 0x7fffffff, v191
	v_and_b32_e32 v216, 0x7fffffff, v190
	v_fma_f32 v176, v162, s46, v132
	v_fma_f32 v177, v163, s46, v132
	v_fma_f32 v206, v204, v206, s48
	v_fma_f32 v207, v205, v207, s48
	v_fma_f32 v216, v216, s4, 1.0
	v_fma_f32 v217, v217, s4, 1.0
	v_fma_f32 v176, v162, v176, s48
	v_fma_f32 v177, v163, v177, s48
	v_fma_f32 v194, v186, s46, v132
	v_fma_f32 v195, v187, s46, v132
	v_mul_f32_e64 v202, v184, v184
	v_mul_f32_e64 v203, v185, v185
	v_fma_f32 v206, v204, v206, s50
	v_fma_f32 v207, v205, v207, s50
	v_rcp_f32_e32 v216, v216
	v_rcp_f32_e32 v217, v217
	v_fma_f32 v156, v146, s46, v132
	v_fma_f32 v157, v147, s46, v132
	v_mul_f32_e64 v160, v144, v144
	v_mul_f32_e64 v161, v145, v145
	v_fma_f32 v176, v162, v176, s50
	v_fma_f32 v177, v163, v177, s50
; __device__ __forceinline__ float silu_f(float g) { return g * __builtin_amdgcn_rcpf(1.0f + __builtin_amdgcn_exp2f(-1.44269504f * g)); }
; __device__ __forceinline__ f32x2 gelu_pk(f32x2 v) {
;     const f32x2 av = __builtin_elementwise_abs(v), d = av * 0.2316418882f + 1.0f;
;     f32x2 t; t.x = __builtin_amdgcn_rcpf(d.x); t.y = __builtin_amdgcn_rcpf(d.y);
;     f32x2 q = t * 0.5307027145f + (-0.7265760135f); q = q * t + 0.7107068705f; q = q * t + (-0.142248368f); q = q * t + 0.127414796f; q = q * t;
;     const f32x2 s = (v * v) * (-0.72134752044f);
;     f32x2 e; e.x = __builtin_amdgcn_exp2f(s.x); e.y = __builtin_amdgcn_exp2f(s.y);
;     const f32x2 m = v * (q * e), r = v - m;
;     f32x2 o; o.x = v.x < 0.f ? m.x : r.x; o.y = v.y < 0.f ? m.y : r.y; return o;
;     template <int TT> __device__ __forceinline__ void other(const f32x4 (&acc)[2][2][4][2], bf16_t* base, int row0, int col0, PG8_LAS float* my, int t, int hh, int wc, int fq) const {
;     ...
;                 for (int bj = 0; bj < 2; ++bj) { f32x4 v0 = acc[ai][bj][m][0] * rs + bv[bj][0], v1 = acc[ai][bj][m][1] * rs + bv[bj][1];
;                     if (TT == 3) {
; #pragma unroll
;                         for (int j = 0; j < 4; ++j) { v0[j] = silu_f(v0[j]); v1[j] = silu_f(v1[j]); } }
;                     else if (TT == 4 || TT == 5) { f32x2 a = gelu_pk((f32x2){v0[0], v0[1]}), b = gelu_pk((f32x2){v0[2], v0[3]}), c = gelu_pk((f32x2){v1[0], v1[1]}), d = gelu_pk((f32x2){v1[2], v1[3]});
;                         v0 = (f32x4){a.x, a.y, b.x, b.y}; v1 = (f32x4){c.x, c.y, d.x, d.y};
;                         if (TT == 5) { ps += ((v0[0] + v0[1]) + (v0[2] + v0[3])) + ((v1[0] + v1[1]) + (v1[2] + v1[3]));
;                             pq += ((v0[0] * v0[0] + v0[1] * v0[1]) + (v0[2] * v0[2] + v0[3] * v0[3])) + ((v1[0] * v1[0] + v1[1] * v1[1]) + (v1[2] * v1[2] + v1[3] * v1[3])); } }
	v_fma_f32 v192, v28, v138, 0
	v_fma_f32 v193, v29, v138, 0
	v_fma_f32 v194, v186, v194, s48
	v_fma_f32 v195, v187, v195, s48
	v_mul_f32_e64 v202, v202, s54
	v_mul_f32_e64 v203, v203, s54
	v_fma_f32 v206, v204, v206, s52
	v_fma_f32 v207, v205, v207, s52
	v_fma_f32 v154, v20, v138, 0
	v_fma_f32 v155, v21, v138, 0
	v_fma_f32 v156, v146, v156, s48
	v_fma_f32 v157, v147, v157, s48
	v_mul_f32_e64 v160, v160, s54
	v_mul_f32_e64 v161, v161, s54
	v_fma_f32 v176, v162, v176, s52
	v_fma_f32 v177, v163, v177, s52
	v_fma_f32 v194, v186, v194, s50
	v_fma_f32 v195, v187, v195, s50
	v_exp_f32_e32 v202, v202
	v_exp_f32_e32 v203, v203
	v_mul_f32_e64 v204, v204, v206
	v_mul_f32_e64 v205, v205, v207
	v_and_b32_e32 v207, 0x7fffffff, v193
	v_and_b32_e32 v206, 0x7fffffff, v192
	v_fma_f32 v156, v146, v156, s50
	v_fma_f32 v157, v147, v157, s50
	v_exp_f32_e32 v160, v160
	v_exp_f32_e32 v161, v161
	v_mul_f32_e64 v162, v162, v176
	v_mul_f32_e64 v163, v163, v177
	v_and_b32_e32 v177, 0x7fffffff, v155
	v_and_b32_e32 v176, 0x7fffffff, v154
	v_fma_f32 v194, v186, v194, s52
	v_fma_f32 v195, v187, v195, s52
	v_fma_f32 v206, v206, s4, 1.0
	v_fma_f32 v207, v207, s4, 1.0
	v_fma_f32 v156, v146, v156, s52
	v_fma_f32 v157, v147, v157, s52
	v_fma_f32 v176, v176, s4, 1.0
	v_fma_f32 v177, v177, s4, 1.0
	v_mul_f32_e64 v186, v186, v194
	v_mul_f32_e64 v187, v187, v195
	v_mul_f32_e64 v194, v188, v188
	v_mul_f32_e64 v195, v189, v189
	v_rcp_f32_e32 v206, v206
	v_rcp_f32_e32 v207, v207
	v_fma_f32 v218, v216, s46, v132
	v_fma_f32 v219, v217, s46, v132
	v_mul_f32_e64 v146, v146, v156
	v_mul_f32_e64 v147, v147, v157
	v_mul_f32_e64 v156, v152, v152
	v_mul_f32_e64 v157, v153, v153
	v_rcp_f32_e32 v176, v176
	v_rcp_f32_e32 v177, v177
	v_mul_f32_e64 v194, v194, s54
	v_mul_f32_e64 v195, v195, s54
	v_fma_f32 v218, v216, v218, s48
	v_fma_f32 v219, v217, v219, s48
	v_mul_f32_e64 v156, v156, s54
	v_mul_f32_e64 v157, v157, s54
	v_mul_f32_e64 v186, v202, v186
	v_mul_f32_e64 v187, v203, v187
	v_exp_f32_e32 v194, v194
	v_exp_f32_e32 v195, v195
	v_fma_f32 v218, v216, v218, s50
	v_fma_f32 v219, v217, v219, s50
	v_mul_f32_e64 v146, v160, v146
	v_mul_f32_e64 v147, v161, v147
	v_exp_f32_e32 v156, v156
	v_exp_f32_e32 v157, v157
	v_mul_f32_e64 v202, v184, v186
	v_mul_f32_e64 v203, v185, v187
	v_fma_f32 v186, -v184, v186, v184
	v_fma_f32 v187, -v185, v187, v185
	v_fma_f32 v218, v216, v218, s52
	v_fma_f32 v219, v217, v219, s52
	v_cmp_gt_f32_e32 vcc, 0, v184
	v_mul_f32_e64 v160, v144, v146
	v_mul_f32_e64 v161, v145, v147
	v_fma_f32 v146, -v144, v146, v144
	v_fma_f32 v147, -v145, v147, v145
	v_fma_f32 v208, v206, s46, v132
	v_fma_f32 v209, v207, s46, v132
	v_mul_f32_e64 v214, v192, v192
	v_mul_f32_e64 v215, v193, v193
	v_mul_f32_e64 v216, v216, v218
	v_mul_f32_e64 v217, v217, v219
	v_cndmask_b32_e32 v219, v186, v202, vcc
	v_cmp_gt_f32_e32 vcc, 0, v144
	v_fma_f32 v178, v176, s46, v132
	v_fma_f32 v179, v177, s46, v132
	v_mul_f32_e64 v180, v154, v154
	v_mul_f32_e64 v181, v155, v155
	v_fma_f32 v208, v206, v208, s48
	v_fma_f32 v209, v207, v209, s48
	v_mul_f32_e64 v214, v214, s54
	v_mul_f32_e64 v215, v215, s54
	v_cndmask_b32_e32 v218, v146, v160, vcc
	v_cmp_gt_f32_e32 vcc, 0, v185
	v_fma_f32 v178, v176, v178, s48
	v_fma_f32 v179, v177, v179, s48
	v_mul_f32_e64 v180, v180, s54
	v_mul_f32_e64 v181, v181, s54
	v_mul_f32_e64 v194, v194, v204
	v_mul_f32_e64 v195, v195, v205
	v_fma_f32 v208, v206, v208, s50
	v_fma_f32 v209, v207, v209, s50
	v_exp_f32_e32 v214, v214
	v_exp_f32_e32 v215, v215
	v_cndmask_b32_e32 v185, v187, v203, vcc
	v_cmp_gt_f32_e32 vcc, 0, v145
	v_mul_f32_e64 v156, v156, v162
	v_mul_f32_e64 v157, v157, v163
	v_fma_f32 v178, v176, v178, s50
	v_fma_f32 v179, v177, v179, s50
	v_exp_f32_e32 v180, v180
	v_exp_f32_e32 v181, v181
	v_mul_f32_e64 v204, v188, v194
	v_mul_f32_e64 v205, v189, v195
	v_fma_f32 v194, -v188, v194, v188
	v_fma_f32 v195, -v189, v195, v189
	v_fma_f32 v208, v206, v208, s52
	v_fma_f32 v209, v207, v209, s52
	v_cndmask_b32_e32 v184, v147, v161, vcc
	v_cmp_gt_f32_e32 vcc, 0, v188
	v_mul_f32_e64 v162, v152, v156
	v_mul_f32_e64 v163, v153, v157
	v_fma_f32 v156, -v152, v156, v152
	v_fma_f32 v157, -v153, v157, v153
	v_fma_f32 v178, v176, v178, s52
	v_fma_f32 v179, v177, v179, s52
	v_mul_f32_e64 v206, v206, v208
	v_mul_f32_e64 v207, v207, v209
	v_mul_f32_e64 v208, v190, v190
	v_mul_f32_e64 v209, v191, v191
	v_cndmask_b32_e32 v147, v194, v204, vcc
	v_cmp_gt_f32_e32 vcc, 0, v152
	v_mul_f32_e64 v176, v176, v178
	v_mul_f32_e64 v177, v177, v179
	v_mul_f32_e64 v178, v142, v142
	v_mul_f32_e64 v179, v143, v143
	v_mul_f32_e64 v208, v208, s54
	v_mul_f32_e64 v209, v209, s54
	v_cndmask_b32_e32 v146, v156, v162, vcc
	v_cmp_gt_f32_e32 vcc, 0, v189
	v_mul_f32_e64 v178, v178, s54
	v_mul_f32_e64 v179, v179, s54
	v_mul_f32_e64 v206, v214, v206
	v_mul_f32_e64 v207, v215, v207
	v_exp_f32_e32 v208, v208
	v_exp_f32_e32 v209, v209
	v_cndmask_b32_e32 v161, v195, v205, vcc
	v_cmp_gt_f32_e32 vcc, 0, v153
	v_mul_f32_e64 v176, v180, v176
	v_mul_f32_e64 v177, v181, v177
	v_exp_f32_e32 v178, v178
	v_exp_f32_e32 v179, v179
	v_mul_f32_e64 v214, v192, v206
	v_mul_f32_e64 v215, v193, v207
	v_fma_f32 v206, -v192, v206, v192
	v_fma_f32 v207, -v193, v207, v193
	v_cndmask_b32_e32 v160, v157, v163, vcc
	v_cmp_gt_f32_e32 vcc, 0, v192
	v_mul_f32_e64 v180, v154, v176
	v_mul_f32_e64 v181, v155, v177
	v_fma_f32 v176, -v154, v176, v154
	v_fma_f32 v177, -v155, v177, v155
	v_cndmask_b32_e32 v153, v206, v214, vcc
	v_cmp_gt_f32_e32 vcc, 0, v154
	v_mul_f32_e64 v208, v208, v216
	v_mul_f32_e64 v209, v209, v217
	v_mul_f32_e64 v178, v178, v182
	v_mul_f32_e64 v179, v179, v183
	v_cndmask_b32_e32 v152, v176, v180, vcc
	v_cmp_gt_f32_e32 vcc, 0, v193
; __device__ __forceinline__ f32x2 gelu_pk(f32x2 v) {
;     const f32x2 av = __builtin_elementwise_abs(v), d = av * 0.2316418882f + 1.0f;
;     f32x2 t; t.x = __builtin_amdgcn_rcpf(d.x); t.y = __builtin_amdgcn_rcpf(d.y);
;     f32x2 q = t * 0.5307027145f + (-0.7265760135f); q = q * t + 0.7107068705f; q = q * t + (-0.142248368f); q = q * t + 0.127414796f; q = q * t;
;     const f32x2 s = (v * v) * (-0.72134752044f);
;     f32x2 e; e.x = __builtin_amdgcn_exp2f(s.x); e.y = __builtin_amdgcn_exp2f(s.y);
;     const f32x2 m = v * (q * e), r = v - m;
;     f32x2 o; o.x = v.x < 0.f ? m.x : r.x; o.y = v.y < 0.f ? m.y : r.y; return o;
;     template <int TT> __device__ __forceinline__ void other(const f32x4 (&acc)[2][2][4][2], bf16_t* base, int row0, int col0, PG8_LAS float* my, int t, int hh, int wc, int fq) const {
;     ...
;                     else if (TT == 4 || TT == 5) { f32x2 a = gelu_pk((f32x2){v0[0], v0[1]}), b = gelu_pk((f32x2){v0[2], v0[3]}), c = gelu_pk((f32x2){v1[0], v1[1]}), d = gelu_pk((f32x2){v1[2], v1[3]});
;                         v0 = (f32x4){a.x, a.y, b.x, b.y}; v1 = (f32x4){c.x, c.y, d.x, d.y};
;                         if (TT == 5) { ps += ((v0[0] + v0[1]) + (v0[2] + v0[3])) + ((v1[0] + v1[1]) + (v1[2] + v1[3]));
;                             pq += ((v0[0] * v0[0] + v0[1] * v0[1]) + (v0[2] * v0[2] + v0[3] * v0[3])) + ((v1[0] * v1[0] + v1[1] * v1[1]) + (v1[2] * v1[2] + v1[3] * v1[3])); } }
;                     else if (TT >= 6) {
; #pragma unroll
;                         for (int j = 0; j < 4; ++j) { v0[j] = sigmoid_f(v0[j]); v1[j] = sigmoid_f(v1[j]); } }
;                     if (TT >= 6) { unsigned b0 = 0u, b1 = 0u;
; #pragma unroll
;                         for (int j = 0; j < 4; ++j) { b0 = __builtin_amdgcn_cvt_pk_u8_f32(__builtin_rintf(v0[j] * 255.0f), j, b0); b1 = __builtin_amdgcn_cvt_pk_u8_f32(__builtin_rintf(v1[j] * 255.0f), j, b1); }
;                         if (bj == 0) { gq.x = b0; gq.y = b1; } else { gq.z = b0; gq.w = b1; } }
;                     else { u32x4 w; w.x = cvt_pk_bf16(v0[0], v0[1]); w.y = cvt_pk_bf16(v0[2], v0[3]); w.z = cvt_pk_bf16(v1[0], v1[1]); w.w = cvt_pk_bf16(v1[2], v1[3]);
;                         *(u32x4*)(rowp + bj * HALF) = w; } }
;                 if (TT >= 6) *(u32x4*)((unsigned char*)base + (size_t)(row0 + ai * HALF + m * 16) * GATE_PITCH + hh * 256 + (wc * 4 + fq) * 16) = gq;
	v_mul_f32_e64 v216, v190, v208
	v_mul_f32_e64 v217, v191, v209
	v_fma_f32 v208, -v190, v208, v190
	v_fma_f32 v209, -v191, v209, v191
	v_cndmask_b32_e32 v157, v207, v215, vcc
	v_cmp_gt_f32_e32 vcc, 0, v155
	v_mul_f32_e64 v182, v142, v178
	v_mul_f32_e64 v183, v143, v179
	v_fma_f32 v178, -v142, v178, v142
	v_fma_f32 v179, -v143, v179, v143
	v_cndmask_b32_e32 v156, v177, v181, vcc
	v_cmp_gt_f32_e32 vcc, 0, v190
	v_add_f32_e64 v176, v218, v184
	v_add_f32_e64 v177, v219, v185
	v_cvt_pk_bf16_f32 v144, v152, v156
	v_cndmask_b32_e32 v155, v208, v216, vcc
	v_cmp_gt_f32_e32 vcc, 0, v142
	v_cvt_pk_bf16_f32 v142, v218, v184
	s_nop 0
	v_cndmask_b32_e32 v154, v178, v182, vcc
	v_cmp_gt_f32_e32 vcc, 0, v191
	s_nop 1
	v_cndmask_b32_e32 v163, v209, v217, vcc
	v_cmp_gt_f32_e32 vcc, 0, v143
	v_cvt_pk_bf16_f32 v143, v146, v160
	s_nop 0
	v_cndmask_b32_e32 v162, v179, v183, vcc
	v_add_f32_e64 v178, v146, v160
	v_add_f32_e64 v179, v147, v161
	v_add_f32_e64 v180, v154, v162
	v_add_f32_e64 v181, v155, v163
	v_add_f32_e64 v176, v176, v178
	v_add_f32_e64 v177, v177, v179
	v_add_f32_e64 v178, v152, v156
	v_add_f32_e64 v179, v153, v157
	v_cvt_pk_bf16_f32 v145, v154, v162
	v_add_f32_e64 v178, v178, v180
	v_add_f32_e64 v179, v179, v181
	v_mul_f32_e64 v180, v162, v162
	v_mul_f32_e64 v181, v163, v163
	v_add_f32_e64 v176, v176, v178
	v_add_f32_e64 v177, v177, v179
	v_mul_f32_e64 v178, v160, v160
	v_mul_f32_e64 v179, v161, v161
	v_add_f32_e32 v138, 0, v176
	v_add_f32_e32 v138, v177, v138
	v_mul_f32_e64 v176, v184, v184
	v_mul_f32_e64 v177, v185, v185
	v_fma_f32 v178, v146, v146, v178
	v_fma_f32 v179, v147, v147, v179
	v_fma_f32 v176, v218, v218, v176
	v_fma_f32 v177, v219, v219, v177
	v_fma_f32 v180, v154, v154, v180
	v_fma_f32 v181, v155, v155, v181
	v_add_f32_e64 v176, v176, v178
	v_add_f32_e64 v177, v177, v179
	v_mul_f32_e64 v178, v156, v156
	v_mul_f32_e64 v179, v157, v157
	global_store_dwordx4 v[140:141], v[142:145], off
	v_fma_f32 v178, v152, v152, v178
	v_fma_f32 v179, v153, v153, v179
	ds_bpermute_b32 v152, v149, v138
	v_add_f32_e64 v178, v178, v180
	v_add_f32_e64 v179, v179, v181
	v_cvt_pk_bf16_f32 v143, v147, v161
	v_add_f32_e64 v176, v176, v178
	v_add_f32_e64 v177, v177, v179
	v_cvt_pk_bf16_f32 v142, v219, v185
	v_add_f32_e32 v146, v176, v177
	ds_bpermute_b32 v154, v149, v146
	s_waitcnt lgkmcnt(0)
	v_add_f32_e32 v138, v138, v152
	ds_bpermute_b32 v147, v148, v138
	v_cvt_pk_bf16_f32 v144, v153, v157
	v_cvt_pk_bf16_f32 v145, v155, v163
	v_add_f32_e32 v146, v146, v154
	ds_bpermute_b32 v152, v148, v146
	global_store_dwordx4 v[140:141], v[142:145], off offset:256
	s_waitcnt lgkmcnt(0)
	v_add_f32_e32 v138, v138, v147
	v_cndmask_b32_e64 v159, v159, v138, s[10:11]
	v_mov_b32_e32 v142, v139
	v_add_u32_e32 v138, 0xb0, v150
	v_fma_f32 v144, v8, v142, 0
	v_fma_f32 v145, v9, v142, 0
	v_mad_i64_i32 v[134:135], s[2:3], v138, s81, v[134:135]
	v_and_b32_e32 v139, 0x7fffffff, v145
	v_and_b32_e32 v138, 0x7fffffff, v144
	v_fma_f32 v138, v138, s4, 1.0
	v_fma_f32 v139, v139, s4, 1.0
	v_add_f32_e32 v140, v146, v152
	v_rcp_f32_e32 v146, v138
	v_rcp_f32_e32 v147, v139
	v_fma_f32 v138, v6, v142, 0
	v_fma_f32 v139, v7, v142, 0
	v_cndmask_b32_e64 v201, v151, v140, s[10:11]
	v_and_b32_e32 v179, 0x7fffffff, v139
	v_and_b32_e32 v178, 0x7fffffff, v138
	v_fma_f32 v178, v178, s4, 1.0
	v_fma_f32 v179, v179, s4, 1.0
	v_fma_f32 v150, v10, v142, 0
	v_fma_f32 v151, v11, v142, 0
	v_rcp_f32_e32 v178, v178
	v_rcp_f32_e32 v179, v179
	v_fma_f32 v184, v18, v142, 0
	v_fma_f32 v185, v19, v142, 0
	v_and_b32_e32 v157, 0x7fffffff, v151
	v_and_b32_e32 v156, 0x7fffffff, v150
	v_and_b32_e32 v193, 0x7fffffff, v185
	v_and_b32_e32 v192, 0x7fffffff, v184
	v_fma_f32 v156, v156, s4, 1.0
	v_fma_f32 v157, v157, s4, 1.0
	v_fma_f32 v180, v178, s46, v132
	v_fma_f32 v181, v179, s46, v132
	v_fma_f32 v192, v192, s4, 1.0
	v_fma_f32 v193, v193, s4, 1.0
	v_rcp_f32_e32 v156, v156
	v_rcp_f32_e32 v157, v157
	v_fma_f32 v180, v178, v180, s48
	v_fma_f32 v181, v179, v181, s48
	v_rcp_f32_e32 v192, v192
	v_rcp_f32_e32 v193, v193
	v_fma_f32 v180, v178, v180, s50
	v_fma_f32 v181, v179, v181, s50
	v_fma_f32 v160, v156, s46, v132
	v_fma_f32 v161, v157, s46, v132
	v_fma_f32 v180, v178, v180, s52
	v_fma_f32 v181, v179, v181, s52
	v_fma_f32 v194, v192, s46, v132
	v_fma_f32 v195, v193, s46, v132
	v_mul_f32_e64 v178, v178, v180
	v_mul_f32_e64 v179, v179, v181
	v_fma_f32 v180, v16, v142, 0
	v_fma_f32 v181, v17, v142, 0
	v_fma_f32 v160, v156, v160, s48
	v_fma_f32 v161, v157, v161, s48
	v_and_b32_e32 v183, 0x7fffffff, v181
	v_and_b32_e32 v182, 0x7fffffff, v180
	v_fma_f32 v182, v182, s4, 1.0
	v_fma_f32 v183, v183, s4, 1.0
	v_fma_f32 v194, v192, v194, s48
	v_fma_f32 v195, v193, v195, s48
	v_fma_f32 v160, v156, v160, s50
	v_fma_f32 v161, v157, v161, s50
	v_rcp_f32_e32 v182, v182
	v_rcp_f32_e32 v183, v183
	v_fma_f32 v194, v192, v194, s50
	v_fma_f32 v195, v193, v195, s50
	v_fma_f32 v140, v4, v142, 0
	v_fma_f32 v141, v5, v142, 0
	v_fma_f32 v160, v156, v160, s52
	v_fma_f32 v161, v157, v161, s52
	v_fma_f32 v186, v14, v142, 0
	v_fma_f32 v187, v15, v142, 0
	v_fma_f32 v143, v13, v142, 0
	v_fma_f32 v142, v12, v142, 0
	v_fma_f32 v194, v192, v194, s52
	v_fma_f32 v195, v193, v195, s52
	v_mul_f32_e64 v156, v156, v160
	v_mul_f32_e64 v157, v157, v161
	v_and_b32_e32 v161, 0x7fffffff, v141
	v_and_b32_e32 v160, 0x7fffffff, v140
	v_mul_f32_e64 v192, v192, v194
	v_mul_f32_e64 v193, v193, v195
	v_and_b32_e32 v195, 0x7fffffff, v143
	v_and_b32_e32 v194, 0x7fffffff, v142
	v_and_b32_e32 v207, 0x7fffffff, v187
	v_and_b32_e32 v206, 0x7fffffff, v186
	v_fma_f32 v160, v160, s4, 1.0
	v_fma_f32 v161, v161, s4, 1.0
	v_fma_f32 v194, v194, s4, 1.0
	v_fma_f32 v195, v195, s4, 1.0
; __device__ __forceinline__ float silu_f(float g) { return g * __builtin_amdgcn_rcpf(1.0f + __builtin_amdgcn_exp2f(-1.44269504f * g)); }
; __device__ __forceinline__ f32x2 gelu_pk(f32x2 v) {
;     const f32x2 av = __builtin_elementwise_abs(v), d = av * 0.2316418882f + 1.0f;
;     f32x2 t; t.x = __builtin_amdgcn_rcpf(d.x); t.y = __builtin_amdgcn_rcpf(d.y);
;     f32x2 q = t * 0.5307027145f + (-0.7265760135f); q = q * t + 0.7107068705f; q = q * t + (-0.142248368f); q = q * t + 0.127414796f; q = q * t;
;     const f32x2 s = (v * v) * (-0.72134752044f);
;     f32x2 e; e.x = __builtin_amdgcn_exp2f(s.x); e.y = __builtin_amdgcn_exp2f(s.y);
;     const f32x2 m = v * (q * e), r = v - m;
;     f32x2 o; o.x = v.x < 0.f ? m.x : r.x; o.y = v.y < 0.f ? m.y : r.y; return o;
;     template <int TT> __device__ __forceinline__ void other(const f32x4 (&acc)[2][2][4][2], bf16_t* base, int row0, int col0, PG8_LAS float* my, int t, int hh, int wc, int fq) const {
;     ...
;                 for (int bj = 0; bj < 2; ++bj) { f32x4 v0 = acc[ai][bj][m][0] * rs + bv[bj][0], v1 = acc[ai][bj][m][1] * rs + bv[bj][1];
;                     if (TT == 3) {
; #pragma unroll
;                         for (int j = 0; j < 4; ++j) { v0[j] = silu_f(v0[j]); v1[j] = silu_f(v1[j]); } }
;                     else if (TT == 4 || TT == 5) { f32x2 a = gelu_pk((f32x2){v0[0], v0[1]}), b = gelu_pk((f32x2){v0[2], v0[3]}), c = gelu_pk((f32x2){v1[0], v1[1]}), d = gelu_pk((f32x2){v1[2], v1[3]});
;                         v0 = (f32x4){a.x, a.y, b.x, b.y}; v1 = (f32x4){c.x, c.y, d.x, d.y};
	v_fma_f32 v206, v206, s4, 1.0
	v_fma_f32 v207, v207, s4, 1.0
	v_rcp_f32_e32 v160, v160
	v_rcp_f32_e32 v161, v161
	v_fma_f32 v188, v182, s46, v132
	v_fma_f32 v189, v183, s46, v132
	v_mul_f32_e64 v190, v180, v180
	v_mul_f32_e64 v191, v181, v181
	v_rcp_f32_e32 v194, v194
	v_rcp_f32_e32 v195, v195
	v_rcp_f32_e32 v206, v206
	v_rcp_f32_e32 v207, v207
	v_fma_f32 v152, v146, s46, v132
	v_fma_f32 v153, v147, s46, v132
	v_mul_f32_e64 v154, v144, v144
	v_mul_f32_e64 v155, v145, v145
	v_fma_f32 v188, v182, v188, s48
	v_fma_f32 v189, v183, v189, s48
	v_mul_f32_e64 v190, v190, s54
	v_mul_f32_e64 v191, v191, s54
	v_fma_f32 v152, v146, v152, s48
	v_fma_f32 v153, v147, v153, s48
	v_mul_f32_e64 v154, v154, s54
	v_mul_f32_e64 v155, v155, s54
	v_fma_f32 v188, v182, v188, s50
	v_fma_f32 v189, v183, v189, s50
	v_exp_f32_e32 v190, v190
	v_exp_f32_e32 v191, v191
	v_fma_f32 v152, v146, v152, s50
	v_fma_f32 v153, v147, v153, s50
	v_exp_f32_e32 v154, v154
	v_exp_f32_e32 v155, v155
	v_fma_f32 v188, v182, v188, s52
	v_fma_f32 v189, v183, v189, s52
	v_fma_f32 v152, v146, v152, s52
	v_fma_f32 v153, v147, v153, s52
	v_fma_f32 v162, v160, s46, v132
	v_fma_f32 v163, v161, s46, v132
	v_mul_f32_e64 v182, v182, v188
	v_mul_f32_e64 v183, v183, v189
	v_mul_f32_e64 v188, v184, v184
	v_mul_f32_e64 v189, v185, v185
	v_fma_f32 v202, v194, s46, v132
	v_fma_f32 v203, v195, s46, v132
	v_fma_f32 v133, v207, s46, v132
	v_fma_f32 v132, v206, s46, v132
	v_mul_f32_e64 v146, v146, v152
	v_mul_f32_e64 v147, v147, v153
	v_mul_f32_e64 v152, v150, v150
	v_mul_f32_e64 v153, v151, v151
	v_mul_f32_e64 v188, v188, s54
	v_mul_f32_e64 v189, v189, s54
	v_fma_f32 v132, v206, v132, s48
	v_fma_f32 v133, v207, v133, s48
	v_mul_f32_e64 v152, v152, s54
	v_mul_f32_e64 v153, v153, s54
	v_mul_f32_e64 v182, v190, v182
	v_mul_f32_e64 v183, v191, v183
	v_exp_f32_e32 v188, v188
	v_exp_f32_e32 v189, v189
	v_fma_f32 v132, v206, v132, s50
	v_fma_f32 v133, v207, v133, s50
	v_mul_f32_e64 v146, v154, v146
	v_mul_f32_e64 v147, v155, v147
	v_exp_f32_e32 v152, v152
	v_exp_f32_e32 v153, v153
	v_mul_f32_e64 v190, v180, v182
	v_mul_f32_e64 v191, v181, v183
	v_fma_f32 v182, -v180, v182, v180
	v_fma_f32 v183, -v181, v183, v181
	v_fma_f32 v132, v206, v132, s52
	v_fma_f32 v133, v207, v133, s52
	v_cmp_gt_f32_e32 vcc, 0, v180
	v_mul_f32_e64 v154, v144, v146
	v_mul_f32_e64 v155, v145, v147
	v_fma_f32 v146, -v144, v146, v144
	v_fma_f32 v147, -v145, v147, v145
	v_mul_f32_e64 v204, v142, v142
	v_mul_f32_e64 v205, v143, v143
	v_mul_f32_e64 v132, v206, v132
	v_mul_f32_e64 v133, v207, v133
	v_cndmask_b32_e32 v207, v182, v190, vcc
	v_cmp_gt_f32_e32 vcc, 0, v144
	v_mul_f32_e64 v176, v140, v140
	v_mul_f32_e64 v177, v141, v141
	v_fma_f32 v202, v194, v202, s48
	v_fma_f32 v203, v195, v203, s48
	v_mul_f32_e64 v204, v204, s54
	v_mul_f32_e64 v205, v205, s54
	v_cndmask_b32_e32 v206, v146, v154, vcc
	v_cmp_gt_f32_e32 vcc, 0, v181
	v_fma_f32 v162, v160, v162, s48
	v_fma_f32 v163, v161, v163, s48
	v_mul_f32_e64 v176, v176, s54
	v_mul_f32_e64 v177, v177, s54
	v_mul_f32_e64 v188, v188, v192
	v_mul_f32_e64 v189, v189, v193
	v_fma_f32 v202, v194, v202, s50
	v_fma_f32 v203, v195, v203, s50
	v_exp_f32_e32 v204, v204
	v_exp_f32_e32 v205, v205
	v_cndmask_b32_e32 v181, v183, v191, vcc
	v_cmp_gt_f32_e32 vcc, 0, v145
	v_mul_f32_e64 v152, v152, v156
	v_mul_f32_e64 v153, v153, v157
	v_fma_f32 v162, v160, v162, s50
	v_fma_f32 v163, v161, v163, s50
	v_exp_f32_e32 v176, v176
	v_exp_f32_e32 v177, v177
	v_mul_f32_e64 v192, v184, v188
	v_mul_f32_e64 v193, v185, v189
	v_fma_f32 v188, -v184, v188, v184
	v_fma_f32 v189, -v185, v189, v185
	v_fma_f32 v202, v194, v202, s52
	v_fma_f32 v203, v195, v203, s52
	v_cndmask_b32_e32 v180, v147, v155, vcc
	v_cmp_gt_f32_e32 vcc, 0, v184
	v_mul_f32_e64 v156, v150, v152
	v_mul_f32_e64 v157, v151, v153
	v_fma_f32 v152, -v150, v152, v150
	v_fma_f32 v153, -v151, v153, v151
	v_fma_f32 v162, v160, v162, s52
	v_fma_f32 v163, v161, v163, s52
	v_mul_f32_e64 v194, v194, v202
	v_mul_f32_e64 v195, v195, v203
	v_mul_f32_e64 v202, v186, v186
	v_mul_f32_e64 v203, v187, v187
	v_cndmask_b32_e32 v145, v188, v192, vcc
	v_cmp_gt_f32_e32 vcc, 0, v150
	v_mul_f32_e64 v160, v160, v162
; __device__ __forceinline__ unsigned cvt_pk_bf16(float lo, float hi) { f32x2_c v = {lo, hi}; bf16x2_c b = __builtin_convertvector(v, bf16x2_c); return __builtin_bit_cast(unsigned, b); }
; __device__ __forceinline__ float sigmoid_f(float g) { return __builtin_amdgcn_rcpf(1.0f + __builtin_amdgcn_exp2f(-1.44269504f * g)); }
;     template <int TT> __device__ __forceinline__ void other(const f32x4 (&acc)[2][2][4][2], bf16_t* base, int row0, int col0, PG8_LAS float* my, int t, int hh, int wc, int fq) const {
;     ...
;                         if (TT == 5) { ps += ((v0[0] + v0[1]) + (v0[2] + v0[3])) + ((v1[0] + v1[1]) + (v1[2] + v1[3]));
;                             pq += ((v0[0] * v0[0] + v0[1] * v0[1]) + (v0[2] * v0[2] + v0[3] * v0[3])) + ((v1[0] * v1[0] + v1[1] * v1[1]) + (v1[2] * v1[2] + v1[3] * v1[3])); } }
;                     else if (TT >= 6) {
; #pragma unroll
;                         for (int j = 0; j < 4; ++j) { v0[j] = sigmoid_f(v0[j]); v1[j] = sigmoid_f(v1[j]); } }
;                     if (TT >= 6) { unsigned b0 = 0u, b1 = 0u;
; #pragma unroll
;                         for (int j = 0; j < 4; ++j) { b0 = __builtin_amdgcn_cvt_pk_u8_f32(__builtin_rintf(v0[j] * 255.0f), j, b0); b1 = __builtin_amdgcn_cvt_pk_u8_f32(__builtin_rintf(v1[j] * 255.0f), j, b1); }
;                         if (bj == 0) { gq.x = b0; gq.y = b1; } else { gq.z = b0; gq.w = b1; } }
;                     else { u32x4 w; w.x = cvt_pk_bf16(v0[0], v0[1]); w.y = cvt_pk_bf16(v0[2], v0[3]); w.z = cvt_pk_bf16(v1[0], v1[1]); w.w = cvt_pk_bf16(v1[2], v1[3]);
;                         *(u32x4*)(rowp + bj * HALF) = w; } }
;                 if (TT >= 6) *(u32x4*)((unsigned char*)base + (size_t)(row0 + ai * HALF + m * 16) * GATE_PITCH + hh * 256 + (wc * 4 + fq) * 16) = gq;
;                 if (TT == 5) { ps += __shfl_xor(ps, 16); pq += __shfl_xor(pq, 16); ps += __shfl_xor(ps, 32); pq += __shfl_xor(pq, 32);
;                     if (m == 0 || fq == m) { psm = ps; pqm = pq; }
;                     if (m == 3) *(f32x2*)(sgst + ((size_t)((row0 + ai * HALF + fq * 16) * 8 + hh) * 4 + wc) * 2) = (f32x2){psm, pqm}; } }
	v_mul_f32_e64 v161, v161, v163
	v_mul_f32_e64 v162, v138, v138
	v_mul_f32_e64 v163, v139, v139
	v_mul_f32_e64 v202, v202, s54
	v_mul_f32_e64 v203, v203, s54
	v_cndmask_b32_e32 v144, v152, v156, vcc
	v_cmp_gt_f32_e32 vcc, 0, v185
	v_mul_f32_e64 v162, v162, s54
	v_mul_f32_e64 v163, v163, s54
	v_mul_f32_e64 v194, v204, v194
	v_mul_f32_e64 v195, v205, v195
	v_exp_f32_e32 v202, v202
	v_exp_f32_e32 v203, v203
	v_cndmask_b32_e32 v147, v189, v193, vcc
	v_cmp_gt_f32_e32 vcc, 0, v151
	v_mul_f32_e64 v160, v176, v160
	v_mul_f32_e64 v161, v177, v161
	v_exp_f32_e32 v162, v162
	v_exp_f32_e32 v163, v163
	v_mul_f32_e64 v204, v142, v194
	v_mul_f32_e64 v205, v143, v195
	v_fma_f32 v194, -v142, v194, v142
	v_fma_f32 v195, -v143, v195, v143
	v_cndmask_b32_e32 v146, v153, v157, vcc
	v_cmp_gt_f32_e32 vcc, 0, v142
	v_mul_f32_e64 v176, v140, v160
	v_mul_f32_e64 v177, v141, v161
	v_fma_f32 v160, -v140, v160, v140
	v_fma_f32 v161, -v141, v161, v141
	v_cndmask_b32_e32 v151, v194, v204, vcc
	v_cmp_gt_f32_e32 vcc, 0, v140
	v_mul_f32_e64 v132, v202, v132
	v_mul_f32_e64 v133, v203, v133
	v_mul_f32_e64 v162, v162, v178
	v_mul_f32_e64 v163, v163, v179
	v_cndmask_b32_e32 v150, v160, v176, vcc
	v_cmp_gt_f32_e32 vcc, 0, v143
	v_mul_f32_e64 v202, v186, v132
	v_mul_f32_e64 v203, v187, v133
	v_fma_f32 v132, -v186, v132, v186
	v_fma_f32 v133, -v187, v133, v187
	v_cndmask_b32_e32 v143, v195, v205, vcc
	v_cmp_gt_f32_e32 vcc, 0, v141
	v_mul_f32_e64 v178, v138, v162
	v_mul_f32_e64 v179, v139, v163
	v_fma_f32 v162, -v138, v162, v138
	v_fma_f32 v163, -v139, v163, v139
	v_cndmask_b32_e32 v142, v161, v177, vcc
	v_cmp_gt_f32_e32 vcc, 0, v186
	v_cvt_pk_bf16_f32 v140, v150, v142
	s_nop 0
	v_cndmask_b32_e32 v153, v132, v202, vcc
	v_cmp_gt_f32_e32 vcc, 0, v138
	v_cvt_pk_bf16_f32 v138, v206, v180
	s_nop 0
	v_cndmask_b32_e32 v152, v162, v178, vcc
	v_cmp_gt_f32_e32 vcc, 0, v187
	s_nop 1
	v_cndmask_b32_e32 v133, v133, v203, vcc
	v_cmp_gt_f32_e32 vcc, 0, v139
	v_cvt_pk_bf16_f32 v139, v144, v146
	s_nop 0
	v_cndmask_b32_e32 v132, v163, v179, vcc
	v_cvt_pk_bf16_f32 v141, v152, v132
	global_store_dwordx4 v[134:135], v[138:141], off
	v_add_f32_e64 v154, v152, v132
	v_add_f32_e64 v155, v153, v133
	s_nop 0
	v_add_f32_e64 v138, v206, v180
	v_add_f32_e64 v139, v207, v181
	v_add_f32_e64 v140, v144, v146
	v_add_f32_e64 v141, v145, v147
	s_nop 0
	v_add_f32_e64 v138, v138, v140
	v_add_f32_e64 v139, v139, v141
	v_add_f32_e64 v140, v150, v142
	v_add_f32_e64 v141, v151, v143
	s_nop 0
	v_add_f32_e64 v140, v140, v154
	v_add_f32_e64 v141, v141, v155
	v_mul_f32_e64 v154, v132, v132
	v_mul_f32_e64 v155, v133, v133
	v_add_f32_e64 v138, v138, v140
	v_add_f32_e64 v139, v139, v141
	v_mul_f32_e64 v140, v146, v146
	v_mul_f32_e64 v141, v147, v147
	v_add_f32_e32 v138, 0, v138
	v_add_f32_e32 v156, v139, v138
	v_mul_f32_e64 v138, v180, v180
	v_mul_f32_e64 v139, v181, v181
	v_fma_f32 v140, v144, v144, v140
	v_fma_f32 v141, v145, v145, v141
	v_fma_f32 v138, v206, v206, v138
	v_fma_f32 v139, v207, v207, v139
	v_fma_f32 v154, v152, v152, v154
	v_fma_f32 v155, v153, v153, v155
	v_add_f32_e64 v138, v138, v140
	v_add_f32_e64 v139, v139, v141
	v_mul_f32_e64 v140, v142, v142
	v_mul_f32_e64 v141, v143, v143
	s_nop 0
	v_fma_f32 v140, v150, v150, v140
	v_fma_f32 v141, v151, v151, v141
	s_nop 0
	v_add_f32_e64 v140, v140, v154
	v_add_f32_e64 v141, v141, v155
	s_nop 0
	v_add_f32_e64 v138, v138, v140
	v_add_f32_e64 v139, v139, v141
	ds_bpermute_b32 v141, v149, v156
	v_add_f32_e32 v132, v138, v139
	ds_bpermute_b32 v142, v149, v132
	v_cvt_pk_bf16_f32 v140, v151, v143
	v_cvt_pk_bf16_f32 v139, v145, v147
	s_waitcnt lgkmcnt(0)
	v_add_f32_e32 v143, v156, v141
	ds_bpermute_b32 v144, v148, v143
	v_add_f32_e32 v142, v132, v142
	ds_bpermute_b32 v145, v148, v142
	v_cvt_pk_bf16_f32 v138, v207, v181
	v_cvt_pk_bf16_f32 v141, v153, v133
	s_waitcnt lgkmcnt(0)
	v_add_f32_e32 v132, v143, v144
	global_store_dwordx4 v[134:135], v[138:141], off offset:256
	v_add_f32_e32 v133, v142, v145
	v_cndmask_b32_e64 v132, v159, v132, s[12:13]
	v_cndmask_b32_e64 v133, v201, v133, s[12:13]
	v_lshl_add_u64 v[134:135], s[20:21], 0, v[136:137]
	global_store_dwordx2 v[134:135], v[132:133], off

; __device__ __forceinline__ float silu_f(float g) { return g * __builtin_amdgcn_rcpf(1.0f + __builtin_amdgcn_exp2f(-1.44269504f * g)); }
; __device__ __forceinline__ f32x2 gelu_pk(f32x2 v) {
;     const f32x2 av = __builtin_elementwise_abs(v), d = av * 0.2316418882f + 1.0f;
;     f32x2 t; t.x = __builtin_amdgcn_rcpf(d.x); t.y = __builtin_amdgcn_rcpf(d.y);
;     f32x2 q = t * 0.5307027145f + (-0.7265760135f); q = q * t + 0.7107068705f; q = q * t + (-0.142248368f); q = q * t + 0.127414796f; q = q * t;
;     const f32x2 s = (v * v) * (-0.72134752044f);
;     f32x2 e; e.x = __builtin_amdgcn_exp2f(s.x); e.y = __builtin_amdgcn_exp2f(s.y);
;     const f32x2 m = v * (q * e), r = v - m;
;     f32x2 o; o.x = v.x < 0.f ? m.x : r.x; o.y = v.y < 0.f ? m.y : r.y; return o;
;     template <int TT> __device__ __forceinline__ void other(const f32x4 (&acc)[2][2][4][2], bf16_t* base, int row0, int col0, PG8_LAS float* my, int t, int hh, int wc, int fq) const {
;     ...
;             for (int m = 0; m < 4; ++m) { bf16_t* rowp = base + (size_t)(row0 + ai * HALF + m * 16) * LDT + col0;
;                 const float rs = my[(ai * 4 + m) * 16]; float ps = 0.f, pq = 0.f; u32x4 gq = {0u, 0u, 0u, 0u};
; #pragma unroll
;                 for (int bj = 0; bj < 2; ++bj) { f32x4 v0 = acc[ai][bj][m][0] * rs + bv[bj][0], v1 = acc[ai][bj][m][1] * rs + bv[bj][1];
;                     if (TT == 3) {
; #pragma unroll
;                         for (int j = 0; j < 4; ++j) { v0[j] = silu_f(v0[j]); v1[j] = silu_f(v1[j]); } }
;                     else if (TT == 4 || TT == 5) { f32x2 a = gelu_pk((f32x2){v0[0], v0[1]}), b = gelu_pk((f32x2){v0[2], v0[3]}), c = gelu_pk((f32x2){v1[0], v1[1]}), d = gelu_pk((f32x2){v1[2], v1[3]});
;                         v0 = (f32x4){a.x, a.y, b.x, b.y}; v1 = (f32x4){c.x, c.y, d.x, d.y};
;                         if (TT == 5) { ps += ((v0[0] + v0[1]) + (v0[2] + v0[3])) + ((v1[0] + v1[1]) + (v1[2] + v1[3]));
;                             pq += ((v0[0] * v0[0] + v0[1] * v0[1]) + (v0[2] * v0[2] + v0[3] * v0[3])) + ((v1[0] * v1[0] + v1[1] * v1[1]) + (v1[2] * v1[2] + v1[3] * v1[3])); } }
;                     else if (TT >= 6) {
; #pragma unroll
;                         for (int j = 0; j < 4; ++j) { v0[j] = sigmoid_f(v0[j]); v1[j] = sigmoid_f(v1[j]); } }
;                     if (TT >= 6) { unsigned b0 = 0u, b1 = 0u;
; #pragma unroll
.LBB0_357:
	s_andn2_b64 vcc, exec, s[4:5]
	s_cbranch_vccnz .LBB0_362
	s_cmp_gt_i32 s45, 0
	s_mov_b64 s[4:5], -1
	s_cbranch_scc0 .LBB0_360
	v_mov_b32_e32 v132, v158
	v_mov_b32_e32 v142, v174
	s_waitcnt lgkmcnt(0)
	v_mov_b32_e32 v133, v3
	ds_read2_b32 v[138:139], v199 offset1:16
	v_ashrrev_i32_e32 v133, 31, v132
	v_lshl_add_u64 v[134:135], v[132:133], 1, s[28:29]
	s_mov_b32 s4, 0x3e6d3388
	v_mad_i64_i32 v[136:137], s[2:3], v142, s81, v[134:135]
	s_waitcnt lgkmcnt(0)
	v_fma_f32 v146, v120, v138, 0
	v_fma_f32 v147, v121, v138, 0
	s_mov_b32 s2, 0xbf3a00e3
	v_and_b32_e32 v133, 0x7fffffff, v147
	v_and_b32_e32 v132, 0x7fffffff, v146
	v_fma_f32 v132, v132, s4, 1.0
	v_fma_f32 v133, v133, s4, 1.0
	s_mov_b32 s10, 0x3f07dc22
	v_rcp_f32_e32 v150, v132
	v_rcp_f32_e32 v151, v133
	v_mov_b64_e32 v[132:133], s[2:3]
	v_mul_f32_e64 v154, v146, v146
	v_mul_f32_e64 v155, v147, v147
	s_mov_b32 s48, 0xbf38aa3b
	v_fma_f32 v152, v150, s10, v132
	v_fma_f32 v153, v151, s10, v132
	s_mov_b32 s12, 0x3f35f0e3
	v_mul_f32_e64 v154, v154, s48
	v_mul_f32_e64 v155, v155, s48
	v_fma_f32 v152, v150, v152, s12
	v_fma_f32 v153, v151, v153, s12
	s_mov_b32 s14, 0xbe11a98e
	v_exp_f32_e32 v154, v154
	v_exp_f32_e32 v155, v155
	v_fma_f32 v152, v150, v152, s14
	v_fma_f32 v153, v151, v153, s14
	s_mov_b32 s46, 0x3e027906
	v_fma_f32 v152, v150, v152, s46
	v_fma_f32 v153, v151, v153, s46
	v_fma_f32 v144, v122, v138, 0
	v_fma_f32 v145, v123, v138, 0
	v_mul_f32_e64 v150, v150, v152
	v_mul_f32_e64 v151, v151, v153
	v_cmp_gt_f32_e32 vcc, 0, v146
	v_mul_f32_e64 v150, v154, v150
	v_mul_f32_e64 v151, v155, v151
	v_mul_f32_e64 v152, v144, v144
	v_mul_f32_e64 v153, v145, v145
	v_mul_f32_e64 v154, v146, v150
	v_mul_f32_e64 v155, v147, v151
	v_fma_f32 v150, -v146, v150, v146
	v_fma_f32 v151, -v147, v151, v147
	v_and_b32_e32 v146, 0x7fffffff, v144
	v_cndmask_b32_e32 v143, v150, v154, vcc
	v_cmp_gt_f32_e32 vcc, 0, v147
	v_and_b32_e32 v147, 0x7fffffff, v145
	v_fma_f32 v146, v146, s4, 1.0
	v_fma_f32 v147, v147, s4, 1.0
	v_cndmask_b32_e32 v154, v151, v155, vcc
	v_rcp_f32_e32 v146, v146
	v_rcp_f32_e32 v147, v147
	v_fma_f32 v148, v116, v138, 0
	v_fma_f32 v149, v117, v138, 0
	v_cmp_gt_f32_e32 vcc, 0, v144
	v_fma_f32 v140, v118, v138, 0
	v_fma_f32 v141, v119, v138, 0
	v_fma_f32 v150, v146, s10, v132
	v_fma_f32 v151, v147, s10, v132
	s_nop 0
	v_fma_f32 v150, v146, v150, s12
	v_fma_f32 v151, v147, v151, s12
	s_nop 0
	v_fma_f32 v150, v146, v150, s14
	v_fma_f32 v151, v147, v151, s14
	s_nop 0
	v_fma_f32 v150, v146, v150, s46
	v_fma_f32 v151, v147, v151, s46
	s_nop 0
	v_mul_f32_e64 v146, v146, v150
	v_mul_f32_e64 v147, v147, v151
	v_mul_f32_e64 v150, v152, s48
	v_mul_f32_e64 v151, v153, s48
	s_nop 0
	v_exp_f32_e32 v150, v150
	v_exp_f32_e32 v151, v151
	s_nop 0
	v_mul_f32_e64 v146, v150, v146
	v_mul_f32_e64 v147, v151, v147
	s_nop 0
	v_mul_f32_e64 v150, v144, v146
	v_mul_f32_e64 v151, v145, v147
	v_fma_f32 v146, -v144, v146, v144
	v_fma_f32 v147, -v145, v147, v145
	v_and_b32_e32 v144, 0x7fffffff, v148
	v_cndmask_b32_e32 v152, v146, v150, vcc
	v_cmp_gt_f32_e32 vcc, 0, v145
	v_and_b32_e32 v145, 0x7fffffff, v149
	v_fma_f32 v144, v144, s4, 1.0
	v_fma_f32 v145, v145, s4, 1.0
	v_cndmask_b32_e32 v153, v147, v151, vcc
	v_rcp_f32_e32 v144, v144
	v_rcp_f32_e32 v145, v145
	v_mul_f32_e64 v150, v148, v148
	v_mul_f32_e64 v151, v149, v149
	v_cmp_gt_f32_e32 vcc, 0, v148
	v_mul_f32_e64 v150, v150, s48
	v_mul_f32_e64 v151, v151, s48
	v_fma_f32 v146, v144, s10, v132
	v_fma_f32 v147, v145, s10, v132
	v_exp_f32_e32 v150, v150
	v_fma_f32 v146, v144, v146, s12
	v_fma_f32 v147, v145, v147, s12
	v_exp_f32_e32 v151, v151
	v_fma_f32 v146, v144, v146, s14
	v_fma_f32 v147, v145, v147, s14
	s_nop 0
	v_fma_f32 v146, v144, v146, s46
	v_fma_f32 v147, v145, v147, s46
	s_nop 0
	v_mul_f32_e64 v144, v144, v146
	v_mul_f32_e64 v145, v145, v147
	v_mul_f32_e64 v146, v140, v140
	v_mul_f32_e64 v147, v141, v141
	v_mul_f32_e64 v144, v150, v144
	v_mul_f32_e64 v145, v151, v145
	v_mul_f32_e64 v146, v146, s48
	v_mul_f32_e64 v147, v147, s48
	v_mul_f32_e64 v150, v148, v144
	v_mul_f32_e64 v151, v149, v145
	v_fma_f32 v144, -v148, v144, v148
	v_fma_f32 v145, -v149, v145, v149
	v_exp_f32_e32 v146, v146
	v_cndmask_b32_e32 v150, v144, v150, vcc
	v_cmp_gt_f32_e32 vcc, 0, v149
	v_and_b32_e32 v144, 0x7fffffff, v140
	v_exp_f32_e32 v147, v147
	v_cndmask_b32_e32 v151, v145, v151, vcc
	v_and_b32_e32 v145, 0x7fffffff, v141
	v_fma_f32 v144, v144, s4, 1.0
	v_fma_f32 v145, v145, s4, 1.0
	v_cmp_gt_f32_e32 vcc, 0, v140
	v_rcp_f32_e32 v144, v144
	v_rcp_f32_e32 v145, v145
	s_nop 0
	v_fma_f32 v148, v144, s10, v132
	v_fma_f32 v149, v145, s10, v132
	s_nop 0
	v_fma_f32 v148, v144, v148, s12
	v_fma_f32 v149, v145, v149, s12
	s_nop 0
	v_fma_f32 v148, v144, v148, s14
	v_fma_f32 v149, v145, v149, s14
	s_nop 0
	v_fma_f32 v148, v144, v148, s46
	v_fma_f32 v149, v145, v149, s46
	s_nop 0
	v_mul_f32_e64 v144, v144, v148
	v_mul_f32_e64 v145, v145, v149
	v_fma_f32 v148, v124, v138, 0
	v_fma_f32 v149, v125, v138, 0
	v_mul_f32_e64 v144, v146, v144
	v_mul_f32_e64 v145, v147, v145
	s_nop 0
	v_mul_f32_e64 v146, v140, v144
	v_mul_f32_e64 v147, v141, v145
	v_fma_f32 v144, -v140, v144, v140
	v_fma_f32 v145, -v141, v145, v141
	s_nop 0
	v_cndmask_b32_e32 v140, v144, v146, vcc
	v_cmp_gt_f32_e32 vcc, 0, v141
	v_cvt_pk_bf16_f32 v144, v143, v154
	v_cvt_pk_bf16_f32 v146, v150, v151
	v_cndmask_b32_e32 v141, v145, v147, vcc
	v_cvt_pk_bf16_f32 v145, v152, v153
	v_cvt_pk_bf16_f32 v147, v140, v141
	global_store_dwordx4 v[136:137], v[144:147], off
	v_fma_f32 v140, v126, v138, 0
	v_fma_f32 v141, v127, v138, 0
	s_nop 0
	v_fma_f32 v146, v128, v138, 0
	v_fma_f32 v147, v129, v138, 0
	v_fma_f32 v144, v130, v138, 0
; __device__ __forceinline__ f32x2 gelu_pk(f32x2 v) {
;     const f32x2 av = __builtin_elementwise_abs(v), d = av * 0.2316418882f + 1.0f;
;     f32x2 t; t.x = __builtin_amdgcn_rcpf(d.x); t.y = __builtin_amdgcn_rcpf(d.y);
;     f32x2 q = t * 0.5307027145f + (-0.7265760135f); q = q * t + 0.7107068705f; q = q * t + (-0.142248368f); q = q * t + 0.127414796f; q = q * t;
;     const f32x2 s = (v * v) * (-0.72134752044f);
;     f32x2 e; e.x = __builtin_amdgcn_exp2f(s.x); e.y = __builtin_amdgcn_exp2f(s.y);
;     const f32x2 m = v * (q * e), r = v - m;
;     f32x2 o; o.x = v.x < 0.f ? m.x : r.x; o.y = v.y < 0.f ? m.y : r.y; return o;
;     template <int TT> __device__ __forceinline__ void other(const f32x4 (&acc)[2][2][4][2], bf16_t* base, int row0, int col0, PG8_LAS float* my, int t, int hh, int wc, int fq) const {
;     ...
;                 for (int bj = 0; bj < 2; ++bj) { f32x4 v0 = acc[ai][bj][m][0] * rs + bv[bj][0], v1 = acc[ai][bj][m][1] * rs + bv[bj][1];
;                     if (TT == 3) {
; #pragma unroll
;                         for (int j = 0; j < 4; ++j) { v0[j] = silu_f(v0[j]); v1[j] = silu_f(v1[j]); } }
;                     else if (TT == 4 || TT == 5) { f32x2 a = gelu_pk((f32x2){v0[0], v0[1]}), b = gelu_pk((f32x2){v0[2], v0[3]}), c = gelu_pk((f32x2){v1[0], v1[1]}), d = gelu_pk((f32x2){v1[2], v1[3]});
;                         v0 = (f32x4){a.x, a.y, b.x, b.y}; v1 = (f32x4){c.x, c.y, d.x, d.y};
;                         if (TT == 5) { ps += ((v0[0] + v0[1]) + (v0[2] + v0[3])) + ((v1[0] + v1[1]) + (v1[2] + v1[3]));
;                             pq += ((v0[0] * v0[0] + v0[1] * v0[1]) + (v0[2] * v0[2] + v0[3] * v0[3])) + ((v1[0] * v1[0] + v1[1] * v1[1]) + (v1[2] * v1[2] + v1[3] * v1[3])); } }
;                     else if (TT >= 6) {
; #pragma unroll
;                         for (int j = 0; j < 4; ++j) { v0[j] = sigmoid_f(v0[j]); v1[j] = sigmoid_f(v1[j]); } }
;                     if (TT >= 6) { unsigned b0 = 0u, b1 = 0u;
; #pragma unroll
;                         for (int j = 0; j < 4; ++j) { b0 = __builtin_amdgcn_cvt_pk_u8_f32(__builtin_rintf(v0[j] * 255.0f), j, b0); b1 = __builtin_amdgcn_cvt_pk_u8_f32(__builtin_rintf(v1[j] * 255.0f), j, b1); }
;                         if (bj == 0) { gq.x = b0; gq.y = b1; } else { gq.z = b0; gq.w = b1; } }
	v_fma_f32 v145, v131, v138, 0
	v_and_b32_e32 v151, 0x7fffffff, v147
	v_and_b32_e32 v150, 0x7fffffff, v146
	v_fma_f32 v150, v150, s4, 1.0
	v_fma_f32 v151, v151, s4, 1.0
	v_mul_f32_e64 v154, v146, v146
	v_mul_f32_e64 v155, v147, v147
	v_rcp_f32_e32 v150, v150
	v_rcp_f32_e32 v151, v151
	v_mul_f32_e64 v154, v154, s48
	v_mul_f32_e64 v155, v155, s48
	v_cmp_gt_f32_e32 vcc, 0, v146
	v_exp_f32_e32 v154, v154
	v_fma_f32 v152, v150, s10, v132
	v_fma_f32 v153, v151, s10, v132
	v_exp_f32_e32 v155, v155
	v_fma_f32 v152, v150, v152, s12
	v_fma_f32 v153, v151, v153, s12
	s_nop 0
	v_fma_f32 v152, v150, v152, s14
	v_fma_f32 v153, v151, v153, s14
	s_nop 0
	v_fma_f32 v152, v150, v152, s46
	v_fma_f32 v153, v151, v153, s46
	s_nop 0
	v_mul_f32_e64 v150, v150, v152
	v_mul_f32_e64 v151, v151, v153
	v_mul_f32_e64 v152, v144, v144
	v_mul_f32_e64 v153, v145, v145
	v_mul_f32_e64 v150, v154, v150
	v_mul_f32_e64 v151, v155, v151
	s_nop 0
	v_mul_f32_e64 v154, v146, v150
	v_mul_f32_e64 v155, v147, v151
	v_fma_f32 v150, -v146, v150, v146
	v_fma_f32 v151, -v147, v151, v147
	v_and_b32_e32 v146, 0x7fffffff, v144
	v_cndmask_b32_e32 v138, v150, v154, vcc
	v_cmp_gt_f32_e32 vcc, 0, v147
	v_and_b32_e32 v147, 0x7fffffff, v145
	v_fma_f32 v146, v146, s4, 1.0
	v_fma_f32 v147, v147, s4, 1.0
	v_cndmask_b32_e32 v143, v151, v155, vcc
	v_rcp_f32_e32 v146, v146
	v_rcp_f32_e32 v147, v147
	v_cmp_gt_f32_e32 vcc, 0, v144
	v_fma_f32 v150, v146, s10, v132
	v_fma_f32 v151, v147, s10, v132
	s_nop 0
	v_fma_f32 v150, v146, v150, s12
	v_fma_f32 v151, v147, v151, s12
	s_nop 0
	v_fma_f32 v150, v146, v150, s14
	v_fma_f32 v151, v147, v151, s14
	s_nop 0
	v_fma_f32 v150, v146, v150, s46
	v_fma_f32 v151, v147, v151, s46
	s_nop 0
	v_mul_f32_e64 v146, v146, v150
	v_mul_f32_e64 v147, v147, v151
	v_mul_f32_e64 v150, v152, s48
	v_mul_f32_e64 v151, v153, s48
	s_nop 0
	v_exp_f32_e32 v150, v150
	v_exp_f32_e32 v151, v151
	s_nop 0
	v_mul_f32_e64 v146, v150, v146
	v_mul_f32_e64 v147, v151, v147
	s_nop 0
	v_mul_f32_e64 v150, v144, v146
	v_mul_f32_e64 v151, v145, v147
	v_fma_f32 v146, -v144, v146, v144
	v_fma_f32 v147, -v145, v147, v145
	v_and_b32_e32 v144, 0x7fffffff, v148
	v_cndmask_b32_e32 v152, v146, v150, vcc
	v_cmp_gt_f32_e32 vcc, 0, v145
	v_and_b32_e32 v145, 0x7fffffff, v149
	v_fma_f32 v144, v144, s4, 1.0
	v_fma_f32 v145, v145, s4, 1.0
	v_cndmask_b32_e32 v153, v147, v151, vcc
	v_rcp_f32_e32 v144, v144
	v_rcp_f32_e32 v145, v145
	v_mul_f32_e64 v150, v148, v148
	v_mul_f32_e64 v151, v149, v149
	v_cmp_gt_f32_e32 vcc, 0, v148
	v_mul_f32_e64 v150, v150, s48
	v_mul_f32_e64 v151, v151, s48
	v_fma_f32 v146, v144, s10, v132
	v_fma_f32 v147, v145, s10, v132
	v_exp_f32_e32 v150, v150
	v_fma_f32 v146, v144, v146, s12
	v_fma_f32 v147, v145, v147, s12
	v_exp_f32_e32 v151, v151
	v_fma_f32 v146, v144, v146, s14
	v_fma_f32 v147, v145, v147, s14
	s_nop 0
	v_fma_f32 v146, v144, v146, s46
	v_fma_f32 v147, v145, v147, s46
	s_nop 0
	v_mul_f32_e64 v144, v144, v146
	v_mul_f32_e64 v145, v145, v147
	v_mul_f32_e64 v146, v140, v140
	v_mul_f32_e64 v147, v141, v141
	v_mul_f32_e64 v144, v150, v144
	v_mul_f32_e64 v145, v151, v145
	v_mul_f32_e64 v146, v146, s48
	v_mul_f32_e64 v147, v147, s48
	v_mul_f32_e64 v150, v148, v144
	v_mul_f32_e64 v151, v149, v145
	v_fma_f32 v144, -v148, v144, v148
	v_fma_f32 v145, -v149, v145, v149
	v_exp_f32_e32 v146, v146
	v_cndmask_b32_e32 v150, v144, v150, vcc
	v_cmp_gt_f32_e32 vcc, 0, v149
	v_and_b32_e32 v144, 0x7fffffff, v140
	v_exp_f32_e32 v147, v147
	v_cndmask_b32_e32 v151, v145, v151, vcc
	v_and_b32_e32 v145, 0x7fffffff, v141
	v_fma_f32 v144, v144, s4, 1.0
	v_fma_f32 v145, v145, s4, 1.0
	v_cmp_gt_f32_e32 vcc, 0, v140
	v_rcp_f32_e32 v144, v144
	v_rcp_f32_e32 v145, v145
	s_nop 0
	v_fma_f32 v148, v144, s10, v132
	v_fma_f32 v149, v145, s10, v132
	s_nop 0
	v_fma_f32 v148, v144, v148, s12
	v_fma_f32 v149, v145, v149, s12
	s_nop 0
	v_fma_f32 v148, v144, v148, s14
	v_fma_f32 v149, v145, v149, s14
	s_nop 0
	v_fma_f32 v148, v144, v148, s46
	v_fma_f32 v149, v145, v149, s46
	s_nop 0
	v_mul_f32_e64 v144, v144, v148
	v_mul_f32_e64 v145, v145, v149
	s_nop 0
	v_mul_f32_e64 v144, v146, v144
	v_mul_f32_e64 v145, v147, v145
	s_nop 0
	v_mul_f32_e64 v146, v140, v144
	v_mul_f32_e64 v147, v141, v145
	v_fma_f32 v144, -v140, v144, v140
	v_fma_f32 v145, -v141, v145, v141
	s_nop 0
	v_cndmask_b32_e32 v140, v144, v146, vcc
	v_cmp_gt_f32_e32 vcc, 0, v141
	v_cvt_pk_bf16_f32 v144, v138, v143
	v_cvt_pk_bf16_f32 v146, v150, v151
	v_cndmask_b32_e32 v141, v145, v147, vcc
	v_cvt_pk_bf16_f32 v145, v152, v153
	v_cvt_pk_bf16_f32 v147, v140, v141
	v_mov_b32_e32 v138, v139
	global_store_dwordx4 v[136:137], v[144:147], off offset:256
	v_fma_f32 v140, v102, v138, 0
	v_fma_f32 v141, v103, v138, 0
	v_fma_f32 v148, v100, v138, 0
	v_fma_f32 v149, v101, v138, 0
	v_fma_f32 v146, v104, v138, 0
	v_fma_f32 v147, v105, v138, 0
	v_fma_f32 v144, v106, v138, 0
	v_fma_f32 v145, v107, v138, 0
	v_and_b32_e32 v151, 0x7fffffff, v147
	v_and_b32_e32 v150, 0x7fffffff, v146
	v_fma_f32 v150, v150, s4, 1.0
	v_fma_f32 v151, v151, s4, 1.0
	v_mul_f32_e64 v154, v146, v146
	v_mul_f32_e64 v155, v147, v147
	v_rcp_f32_e32 v150, v150
	v_rcp_f32_e32 v151, v151
	v_mul_f32_e64 v154, v154, s48
	v_mul_f32_e64 v155, v155, s48
	v_cmp_gt_f32_e32 vcc, 0, v146
	v_exp_f32_e32 v154, v154
	v_fma_f32 v152, v150, s10, v132
	v_fma_f32 v153, v151, s10, v132
	v_exp_f32_e32 v155, v155
	v_fma_f32 v152, v150, v152, s12
	v_fma_f32 v153, v151, v153, s12
	v_add_u32_e32 v136, 16, v142
	v_fma_f32 v152, v150, v152, s14
	v_fma_f32 v153, v151, v153, s14
	v_mad_i64_i32 v[136:137], s[2:3], v136, s81, v[134:135]
	v_fma_f32 v152, v150, v152, s46
	v_fma_f32 v153, v151, v153, s46
	s_nop 0
	v_mul_f32_e64 v150, v150, v152
; __device__ __forceinline__ f32x2 gelu_pk(f32x2 v) {
;     const f32x2 av = __builtin_elementwise_abs(v), d = av * 0.2316418882f + 1.0f;
;     f32x2 t; t.x = __builtin_amdgcn_rcpf(d.x); t.y = __builtin_amdgcn_rcpf(d.y);
;     f32x2 q = t * 0.5307027145f + (-0.7265760135f); q = q * t + 0.7107068705f; q = q * t + (-0.142248368f); q = q * t + 0.127414796f; q = q * t;
;     const f32x2 s = (v * v) * (-0.72134752044f);
;     f32x2 e; e.x = __builtin_amdgcn_exp2f(s.x); e.y = __builtin_amdgcn_exp2f(s.y);
;     const f32x2 m = v * (q * e), r = v - m;
;     f32x2 o; o.x = v.x < 0.f ? m.x : r.x; o.y = v.y < 0.f ? m.y : r.y; return o;
;     template <int TT> __device__ __forceinline__ void other(const f32x4 (&acc)[2][2][4][2], bf16_t* base, int row0, int col0, PG8_LAS float* my, int t, int hh, int wc, int fq) const {
;     ...
;                 for (int bj = 0; bj < 2; ++bj) { f32x4 v0 = acc[ai][bj][m][0] * rs + bv[bj][0], v1 = acc[ai][bj][m][1] * rs + bv[bj][1];
;                     if (TT == 3) {
; #pragma unroll
;                         for (int j = 0; j < 4; ++j) { v0[j] = silu_f(v0[j]); v1[j] = silu_f(v1[j]); } }
;                     else if (TT == 4 || TT == 5) { f32x2 a = gelu_pk((f32x2){v0[0], v0[1]}), b = gelu_pk((f32x2){v0[2], v0[3]}), c = gelu_pk((f32x2){v1[0], v1[1]}), d = gelu_pk((f32x2){v1[2], v1[3]});
;                         v0 = (f32x4){a.x, a.y, b.x, b.y}; v1 = (f32x4){c.x, c.y, d.x, d.y};
;                         if (TT == 5) { ps += ((v0[0] + v0[1]) + (v0[2] + v0[3])) + ((v1[0] + v1[1]) + (v1[2] + v1[3]));
;                             pq += ((v0[0] * v0[0] + v0[1] * v0[1]) + (v0[2] * v0[2] + v0[3] * v0[3])) + ((v1[0] * v1[0] + v1[1] * v1[1]) + (v1[2] * v1[2] + v1[3] * v1[3])); } }
;                     else if (TT >= 6) {
; #pragma unroll
;                         for (int j = 0; j < 4; ++j) { v0[j] = sigmoid_f(v0[j]); v1[j] = sigmoid_f(v1[j]); } }
;                     if (TT >= 6) { unsigned b0 = 0u, b1 = 0u;
; #pragma unroll
;                         for (int j = 0; j < 4; ++j) { b0 = __builtin_amdgcn_cvt_pk_u8_f32(__builtin_rintf(v0[j] * 255.0f), j, b0); b1 = __builtin_amdgcn_cvt_pk_u8_f32(__builtin_rintf(v1[j] * 255.0f), j, b1); }
;                         if (bj == 0) { gq.x = b0; gq.y = b1; } else { gq.z = b0; gq.w = b1; } }
	v_mul_f32_e64 v151, v151, v153
	v_mul_f32_e64 v152, v144, v144
	v_mul_f32_e64 v153, v145, v145
	v_mul_f32_e64 v150, v154, v150
	v_mul_f32_e64 v151, v155, v151
	s_nop 0
	v_mul_f32_e64 v154, v146, v150
	v_mul_f32_e64 v155, v147, v151
	v_fma_f32 v150, -v146, v150, v146
	v_fma_f32 v151, -v147, v151, v147
	v_and_b32_e32 v146, 0x7fffffff, v144
	v_cndmask_b32_e32 v139, v150, v154, vcc
	v_cmp_gt_f32_e32 vcc, 0, v147
	v_and_b32_e32 v147, 0x7fffffff, v145
	v_fma_f32 v146, v146, s4, 1.0
	v_fma_f32 v147, v147, s4, 1.0
	v_cndmask_b32_e32 v143, v151, v155, vcc
	v_rcp_f32_e32 v146, v146
	v_rcp_f32_e32 v147, v147
	v_cmp_gt_f32_e32 vcc, 0, v144
	v_fma_f32 v150, v146, s10, v132
	v_fma_f32 v151, v147, s10, v132
	s_nop 0
	v_fma_f32 v150, v146, v150, s12
	v_fma_f32 v151, v147, v151, s12
	s_nop 0
	v_fma_f32 v150, v146, v150, s14
	v_fma_f32 v151, v147, v151, s14
	s_nop 0
	v_fma_f32 v150, v146, v150, s46
	v_fma_f32 v151, v147, v151, s46
	s_nop 0
	v_mul_f32_e64 v146, v146, v150
	v_mul_f32_e64 v147, v147, v151
	v_mul_f32_e64 v150, v152, s48
	v_mul_f32_e64 v151, v153, s48
	s_nop 0
	v_exp_f32_e32 v150, v150
	v_exp_f32_e32 v151, v151
	s_nop 0
	v_mul_f32_e64 v146, v150, v146
	v_mul_f32_e64 v147, v151, v147
	s_nop 0
	v_mul_f32_e64 v150, v144, v146
	v_mul_f32_e64 v151, v145, v147
	v_fma_f32 v146, -v144, v146, v144
	v_fma_f32 v147, -v145, v147, v145
	v_and_b32_e32 v144, 0x7fffffff, v148
	v_cndmask_b32_e32 v152, v146, v150, vcc
	v_cmp_gt_f32_e32 vcc, 0, v145
	v_and_b32_e32 v145, 0x7fffffff, v149
	v_fma_f32 v144, v144, s4, 1.0
	v_fma_f32 v145, v145, s4, 1.0
	v_cndmask_b32_e32 v153, v147, v151, vcc
	v_rcp_f32_e32 v144, v144
	v_rcp_f32_e32 v145, v145
	v_mul_f32_e64 v150, v148, v148
	v_mul_f32_e64 v151, v149, v149
	v_cmp_gt_f32_e32 vcc, 0, v148
	v_mul_f32_e64 v150, v150, s48
	v_mul_f32_e64 v151, v151, s48
	v_fma_f32 v146, v144, s10, v132
	v_fma_f32 v147, v145, s10, v132
	v_exp_f32_e32 v150, v150
	v_fma_f32 v146, v144, v146, s12
	v_fma_f32 v147, v145, v147, s12
	v_exp_f32_e32 v151, v151
	v_fma_f32 v146, v144, v146, s14
	v_fma_f32 v147, v145, v147, s14
	s_nop 0
	v_fma_f32 v146, v144, v146, s46
	v_fma_f32 v147, v145, v147, s46
	s_nop 0
	v_mul_f32_e64 v144, v144, v146
	v_mul_f32_e64 v145, v145, v147
	v_mul_f32_e64 v146, v140, v140
	v_mul_f32_e64 v147, v141, v141
	v_mul_f32_e64 v144, v150, v144
	v_mul_f32_e64 v145, v151, v145
	v_mul_f32_e64 v146, v146, s48
	v_mul_f32_e64 v147, v147, s48
	v_mul_f32_e64 v150, v148, v144
	v_mul_f32_e64 v151, v149, v145
	v_fma_f32 v144, -v148, v144, v148
	v_fma_f32 v145, -v149, v145, v149
	v_exp_f32_e32 v146, v146
	v_cndmask_b32_e32 v150, v144, v150, vcc
	v_cmp_gt_f32_e32 vcc, 0, v149
	v_and_b32_e32 v144, 0x7fffffff, v140
	v_exp_f32_e32 v147, v147
	v_cndmask_b32_e32 v151, v145, v151, vcc
	v_and_b32_e32 v145, 0x7fffffff, v141
	v_fma_f32 v144, v144, s4, 1.0
	v_fma_f32 v145, v145, s4, 1.0
	v_cmp_gt_f32_e32 vcc, 0, v140
	v_rcp_f32_e32 v144, v144
	v_rcp_f32_e32 v145, v145
	s_nop 0
	v_fma_f32 v148, v144, s10, v132
	v_fma_f32 v149, v145, s10, v132
	s_nop 0
	v_fma_f32 v148, v144, v148, s12
	v_fma_f32 v149, v145, v149, s12
	s_nop 0
	v_fma_f32 v148, v144, v148, s14
	v_fma_f32 v149, v145, v149, s14
	s_nop 0
	v_fma_f32 v148, v144, v148, s46
	v_fma_f32 v149, v145, v149, s46
	s_nop 0
	v_mul_f32_e64 v144, v144, v148
	v_mul_f32_e64 v145, v145, v149
	s_nop 0
	v_mul_f32_e64 v144, v146, v144
	v_mul_f32_e64 v145, v147, v145
	s_nop 0
	v_mul_f32_e64 v146, v140, v144
	v_mul_f32_e64 v147, v141, v145
	v_fma_f32 v144, -v140, v144, v140
	v_fma_f32 v145, -v141, v145, v141
	s_nop 0
	v_cndmask_b32_e32 v140, v144, v146, vcc
	v_cmp_gt_f32_e32 vcc, 0, v141
	v_cvt_pk_bf16_f32 v144, v139, v143
	v_cvt_pk_bf16_f32 v146, v150, v151
	v_cndmask_b32_e32 v141, v145, v147, vcc
	v_cvt_pk_bf16_f32 v145, v152, v153
	v_cvt_pk_bf16_f32 v147, v140, v141
	global_store_dwordx4 v[136:137], v[144:147], off
	v_fma_f32 v140, v110, v138, 0
	v_fma_f32 v141, v111, v138, 0
	s_nop 0
	v_fma_f32 v146, v112, v138, 0
	v_fma_f32 v147, v113, v138, 0
	v_fma_f32 v144, v114, v138, 0
	v_fma_f32 v145, v115, v138, 0
	v_and_b32_e32 v149, 0x7fffffff, v147
	v_and_b32_e32 v148, 0x7fffffff, v146
	v_fma_f32 v148, v148, s4, 1.0
	v_fma_f32 v149, v149, s4, 1.0
	v_mul_f32_e64 v152, v146, v146
	v_mul_f32_e64 v153, v147, v147
	v_rcp_f32_e32 v148, v148
	v_rcp_f32_e32 v149, v149
	v_mul_f32_e64 v152, v152, s48
	v_mul_f32_e64 v153, v153, s48
	v_cmp_gt_f32_e32 vcc, 0, v146
	v_exp_f32_e32 v152, v152
	v_fma_f32 v150, v148, s10, v132
	v_fma_f32 v151, v149, s10, v132
	v_exp_f32_e32 v153, v153
	v_fma_f32 v150, v148, v150, s12
	v_fma_f32 v151, v149, v151, s12
	v_fma_f32 v139, v109, v138, 0
	v_fma_f32 v138, v108, v138, 0
	v_fma_f32 v150, v148, v150, s14
	v_fma_f32 v151, v149, v151, s14
	s_nop 0
	v_fma_f32 v150, v148, v150, s46
	v_fma_f32 v151, v149, v151, s46
	s_nop 0
	v_mul_f32_e64 v148, v148, v150
	v_mul_f32_e64 v149, v149, v151
	v_mul_f32_e64 v150, v144, v144
	v_mul_f32_e64 v151, v145, v145
	v_mul_f32_e64 v148, v152, v148
	v_mul_f32_e64 v149, v153, v149
	s_nop 0
	v_mul_f32_e64 v152, v146, v148
	v_mul_f32_e64 v153, v147, v149
	v_fma_f32 v148, -v146, v148, v146
	v_fma_f32 v149, -v147, v149, v147
	v_and_b32_e32 v146, 0x7fffffff, v144
	v_cndmask_b32_e32 v143, v148, v152, vcc
	v_cmp_gt_f32_e32 vcc, 0, v147
	v_and_b32_e32 v147, 0x7fffffff, v145
	v_fma_f32 v146, v146, s4, 1.0
	v_fma_f32 v147, v147, s4, 1.0
	v_cndmask_b32_e32 v152, v149, v153, vcc
	v_rcp_f32_e32 v146, v146
	v_rcp_f32_e32 v147, v147
	v_cmp_gt_f32_e32 vcc, 0, v144
	v_fma_f32 v148, v146, s10, v132
	v_fma_f32 v149, v147, s10, v132
	s_nop 0
	v_fma_f32 v148, v146, v148, s12
	v_fma_f32 v149, v147, v149, s12
	s_nop 0
	v_fma_f32 v148, v146, v148, s14
	v_fma_f32 v149, v147, v149, s14
; __device__ __forceinline__ float silu_f(float g) { return g * __builtin_amdgcn_rcpf(1.0f + __builtin_amdgcn_exp2f(-1.44269504f * g)); }
; __device__ __forceinline__ f32x2 gelu_pk(f32x2 v) {
;     const f32x2 av = __builtin_elementwise_abs(v), d = av * 0.2316418882f + 1.0f;
;     f32x2 t; t.x = __builtin_amdgcn_rcpf(d.x); t.y = __builtin_amdgcn_rcpf(d.y);
;     f32x2 q = t * 0.5307027145f + (-0.7265760135f); q = q * t + 0.7107068705f; q = q * t + (-0.142248368f); q = q * t + 0.127414796f; q = q * t;
;     const f32x2 s = (v * v) * (-0.72134752044f);
;     f32x2 e; e.x = __builtin_amdgcn_exp2f(s.x); e.y = __builtin_amdgcn_exp2f(s.y);
;     const f32x2 m = v * (q * e), r = v - m;
;     f32x2 o; o.x = v.x < 0.f ? m.x : r.x; o.y = v.y < 0.f ? m.y : r.y; return o;
;     template <int TT> __device__ __forceinline__ void other(const f32x4 (&acc)[2][2][4][2], bf16_t* base, int row0, int col0, PG8_LAS float* my, int t, int hh, int wc, int fq) const {
;     ...
;             for (int m = 0; m < 4; ++m) { bf16_t* rowp = base + (size_t)(row0 + ai * HALF + m * 16) * LDT + col0;
;                 const float rs = my[(ai * 4 + m) * 16]; float ps = 0.f, pq = 0.f; u32x4 gq = {0u, 0u, 0u, 0u};
; #pragma unroll
;                 for (int bj = 0; bj < 2; ++bj) { f32x4 v0 = acc[ai][bj][m][0] * rs + bv[bj][0], v1 = acc[ai][bj][m][1] * rs + bv[bj][1];
;                     if (TT == 3) {
; #pragma unroll
;                         for (int j = 0; j < 4; ++j) { v0[j] = silu_f(v0[j]); v1[j] = silu_f(v1[j]); } }
;                     else if (TT == 4 || TT == 5) { f32x2 a = gelu_pk((f32x2){v0[0], v0[1]}), b = gelu_pk((f32x2){v0[2], v0[3]}), c = gelu_pk((f32x2){v1[0], v1[1]}), d = gelu_pk((f32x2){v1[2], v1[3]});
;                         v0 = (f32x4){a.x, a.y, b.x, b.y}; v1 = (f32x4){c.x, c.y, d.x, d.y};
;                         if (TT == 5) { ps += ((v0[0] + v0[1]) + (v0[2] + v0[3])) + ((v1[0] + v1[1]) + (v1[2] + v1[3]));
;                             pq += ((v0[0] * v0[0] + v0[1] * v0[1]) + (v0[2] * v0[2] + v0[3] * v0[3])) + ((v1[0] * v1[0] + v1[1] * v1[1]) + (v1[2] * v1[2] + v1[3] * v1[3])); } }
;                     else if (TT >= 6) {
; #pragma unroll
;                         for (int j = 0; j < 4; ++j) { v0[j] = sigmoid_f(v0[j]); v1[j] = sigmoid_f(v1[j]); } }
;                     if (TT >= 6) { unsigned b0 = 0u, b1 = 0u;
; #pragma unroll
	s_nop 0
	v_fma_f32 v148, v146, v148, s46
	v_fma_f32 v149, v147, v149, s46
	s_nop 0
	v_mul_f32_e64 v146, v146, v148
	v_mul_f32_e64 v147, v147, v149
	v_mul_f32_e64 v148, v150, s48
	v_mul_f32_e64 v149, v151, s48
	s_nop 0
	v_exp_f32_e32 v148, v148
	v_exp_f32_e32 v149, v149
	s_nop 0
	v_mul_f32_e64 v146, v148, v146
	v_mul_f32_e64 v147, v149, v147
	s_nop 0
	v_mul_f32_e64 v148, v144, v146
	v_mul_f32_e64 v149, v145, v147
	v_fma_f32 v146, -v144, v146, v144
	v_fma_f32 v147, -v145, v147, v145
	v_and_b32_e32 v144, 0x7fffffff, v138
	v_cndmask_b32_e32 v150, v146, v148, vcc
	v_cmp_gt_f32_e32 vcc, 0, v145
	v_and_b32_e32 v145, 0x7fffffff, v139
	v_fma_f32 v144, v144, s4, 1.0
	v_fma_f32 v145, v145, s4, 1.0
	v_cndmask_b32_e32 v151, v147, v149, vcc
	v_rcp_f32_e32 v144, v144
	v_rcp_f32_e32 v145, v145
	v_mul_f32_e64 v148, v138, v138
	v_mul_f32_e64 v149, v139, v139
	v_cmp_gt_f32_e32 vcc, 0, v138
	v_mul_f32_e64 v148, v148, s48
	v_mul_f32_e64 v149, v149, s48
	v_fma_f32 v146, v144, s10, v132
	v_fma_f32 v147, v145, s10, v132
	v_exp_f32_e32 v148, v148
	v_fma_f32 v146, v144, v146, s12
	v_fma_f32 v147, v145, v147, s12
	v_exp_f32_e32 v149, v149
	v_fma_f32 v146, v144, v146, s14
	v_fma_f32 v147, v145, v147, s14
	s_nop 0
	v_fma_f32 v146, v144, v146, s46
	v_fma_f32 v147, v145, v147, s46
	s_nop 0
	v_mul_f32_e64 v144, v144, v146
	v_mul_f32_e64 v145, v145, v147
	v_mul_f32_e64 v146, v140, v140
	v_mul_f32_e64 v147, v141, v141
	v_mul_f32_e64 v144, v148, v144
	v_mul_f32_e64 v145, v149, v145
	s_nop 0
	v_mul_f32_e64 v148, v138, v144
	v_mul_f32_e64 v149, v139, v145
	v_fma_f32 v144, -v138, v144, v138
	v_fma_f32 v145, -v139, v145, v139
	v_and_b32_e32 v138, 0x7fffffff, v140
	v_cndmask_b32_e32 v148, v144, v148, vcc
	v_cmp_gt_f32_e32 vcc, 0, v139
	v_and_b32_e32 v139, 0x7fffffff, v141
	v_fma_f32 v138, v138, s4, 1.0
	v_fma_f32 v139, v139, s4, 1.0
	v_cndmask_b32_e32 v149, v145, v149, vcc
	v_rcp_f32_e32 v138, v138
	v_rcp_f32_e32 v139, v139
	v_cmp_gt_f32_e32 vcc, 0, v140
	v_fma_f32 v144, v138, s10, v132
	v_fma_f32 v145, v139, s10, v132
	s_nop 0
	v_fma_f32 v144, v138, v144, s12
	v_fma_f32 v145, v139, v145, s12
	s_nop 0
	v_fma_f32 v144, v138, v144, s14
	v_fma_f32 v145, v139, v145, s14
	s_nop 0
	v_fma_f32 v144, v138, v144, s46
	v_fma_f32 v145, v139, v145, s46
	s_nop 0
	v_mul_f32_e64 v138, v138, v144
	v_mul_f32_e64 v139, v139, v145
	v_mul_f32_e64 v144, v146, s48
	v_mul_f32_e64 v145, v147, s48
	s_nop 0
	v_exp_f32_e32 v144, v144
	v_exp_f32_e32 v145, v145
	s_nop 0
	v_mul_f32_e64 v138, v144, v138
	v_mul_f32_e64 v139, v145, v139
	s_nop 0
	v_mul_f32_e64 v144, v140, v138
	v_mul_f32_e64 v145, v141, v139
	v_fma_f32 v138, -v140, v138, v140
	v_fma_f32 v139, -v141, v139, v141
	v_cvt_pk_bf16_f32 v140, v148, v149
	v_cndmask_b32_e32 v144, v138, v144, vcc
	v_cmp_gt_f32_e32 vcc, 0, v141
	v_cvt_pk_bf16_f32 v138, v143, v152
	s_nop 0
	v_cndmask_b32_e32 v141, v139, v145, vcc
	v_cvt_pk_bf16_f32 v139, v150, v151
	v_cvt_pk_bf16_f32 v141, v144, v141
	global_store_dwordx4 v[136:137], v[138:141], off offset:256
	ds_read2_b32 v[138:139], v199 offset0:32 offset1:48
	v_add_u32_e32 v136, 32, v142
	v_mad_i64_i32 v[136:137], s[2:3], v136, s81, v[134:135]
	s_waitcnt lgkmcnt(0)
	v_fma_f32 v146, v88, v138, 0
	v_fma_f32 v147, v89, v138, 0
	s_nop 0
	v_and_b32_e32 v151, 0x7fffffff, v147
	v_and_b32_e32 v150, 0x7fffffff, v146
	v_fma_f32 v150, v150, s4, 1.0
	v_fma_f32 v151, v151, s4, 1.0
	v_mul_f32_e64 v154, v146, v146
	v_mul_f32_e64 v155, v147, v147
	v_rcp_f32_e32 v150, v150
	v_rcp_f32_e32 v151, v151
	v_mul_f32_e64 v154, v154, s48
	v_mul_f32_e64 v155, v155, s48
	v_fma_f32 v144, v90, v138, 0
	v_fma_f32 v145, v91, v138, 0
	v_exp_f32_e32 v154, v154
	v_fma_f32 v152, v150, s10, v132
	v_fma_f32 v153, v151, s10, v132
	v_exp_f32_e32 v155, v155
	v_fma_f32 v152, v150, v152, s12
	v_fma_f32 v153, v151, v153, s12
	v_cmp_gt_f32_e32 vcc, 0, v146
	v_fma_f32 v152, v150, v152, s14
	v_fma_f32 v153, v151, v153, s14
	v_fma_f32 v148, v84, v138, 0
	v_fma_f32 v149, v85, v138, 0
	v_fma_f32 v152, v150, v152, s46
	v_fma_f32 v153, v151, v153, s46
	v_fma_f32 v140, v86, v138, 0
	v_fma_f32 v141, v87, v138, 0
	v_mul_f32_e64 v150, v150, v152
	v_mul_f32_e64 v151, v151, v153
	v_mul_f32_e64 v152, v144, v144
	v_mul_f32_e64 v153, v145, v145
	v_mul_f32_e64 v150, v154, v150
	v_mul_f32_e64 v151, v155, v151
	s_nop 0
	v_mul_f32_e64 v154, v146, v150
	v_mul_f32_e64 v155, v147, v151
	v_fma_f32 v150, -v146, v150, v146
	v_fma_f32 v151, -v147, v151, v147
	v_and_b32_e32 v146, 0x7fffffff, v144
	v_cndmask_b32_e32 v143, v150, v154, vcc
	v_cmp_gt_f32_e32 vcc, 0, v147
	v_and_b32_e32 v147, 0x7fffffff, v145
	v_fma_f32 v146, v146, s4, 1.0
	v_fma_f32 v147, v147, s4, 1.0
	v_cndmask_b32_e32 v154, v151, v155, vcc
	v_rcp_f32_e32 v146, v146
	v_rcp_f32_e32 v147, v147
	v_cmp_gt_f32_e32 vcc, 0, v144
	v_fma_f32 v150, v146, s10, v132
	v_fma_f32 v151, v147, s10, v132
	s_nop 0
	v_fma_f32 v150, v146, v150, s12
	v_fma_f32 v151, v147, v151, s12
	s_nop 0
	v_fma_f32 v150, v146, v150, s14
	v_fma_f32 v151, v147, v151, s14
	s_nop 0
	v_fma_f32 v150, v146, v150, s46
	v_fma_f32 v151, v147, v151, s46
	s_nop 0
	v_mul_f32_e64 v146, v146, v150
	v_mul_f32_e64 v147, v147, v151
	v_mul_f32_e64 v150, v152, s48
	v_mul_f32_e64 v151, v153, s48
	s_nop 0
	v_exp_f32_e32 v150, v150
	v_exp_f32_e32 v151, v151
	s_nop 0
	v_mul_f32_e64 v146, v150, v146
	v_mul_f32_e64 v147, v151, v147
	s_nop 0
	v_mul_f32_e64 v150, v144, v146
	v_mul_f32_e64 v151, v145, v147
	v_fma_f32 v146, -v144, v146, v144
	v_fma_f32 v147, -v145, v147, v145
	v_and_b32_e32 v144, 0x7fffffff, v148
	v_cndmask_b32_e32 v152, v146, v150, vcc
	v_cmp_gt_f32_e32 vcc, 0, v145
	v_and_b32_e32 v145, 0x7fffffff, v149
	v_fma_f32 v144, v144, s4, 1.0
	v_fma_f32 v145, v145, s4, 1.0
; __device__ __forceinline__ f32x2 gelu_pk(f32x2 v) {
;     const f32x2 av = __builtin_elementwise_abs(v), d = av * 0.2316418882f + 1.0f;
;     f32x2 t; t.x = __builtin_amdgcn_rcpf(d.x); t.y = __builtin_amdgcn_rcpf(d.y);
;     f32x2 q = t * 0.5307027145f + (-0.7265760135f); q = q * t + 0.7107068705f; q = q * t + (-0.142248368f); q = q * t + 0.127414796f; q = q * t;
;     const f32x2 s = (v * v) * (-0.72134752044f);
;     f32x2 e; e.x = __builtin_amdgcn_exp2f(s.x); e.y = __builtin_amdgcn_exp2f(s.y);
;     const f32x2 m = v * (q * e), r = v - m;
;     f32x2 o; o.x = v.x < 0.f ? m.x : r.x; o.y = v.y < 0.f ? m.y : r.y; return o;
;     template <int TT> __device__ __forceinline__ void other(const f32x4 (&acc)[2][2][4][2], bf16_t* base, int row0, int col0, PG8_LAS float* my, int t, int hh, int wc, int fq) const {
;     ...
;                 for (int bj = 0; bj < 2; ++bj) { f32x4 v0 = acc[ai][bj][m][0] * rs + bv[bj][0], v1 = acc[ai][bj][m][1] * rs + bv[bj][1];
;                     if (TT == 3) {
; #pragma unroll
;                         for (int j = 0; j < 4; ++j) { v0[j] = silu_f(v0[j]); v1[j] = silu_f(v1[j]); } }
;                     else if (TT == 4 || TT == 5) { f32x2 a = gelu_pk((f32x2){v0[0], v0[1]}), b = gelu_pk((f32x2){v0[2], v0[3]}), c = gelu_pk((f32x2){v1[0], v1[1]}), d = gelu_pk((f32x2){v1[2], v1[3]});
;                         v0 = (f32x4){a.x, a.y, b.x, b.y}; v1 = (f32x4){c.x, c.y, d.x, d.y};
;                         if (TT == 5) { ps += ((v0[0] + v0[1]) + (v0[2] + v0[3])) + ((v1[0] + v1[1]) + (v1[2] + v1[3]));
;                             pq += ((v0[0] * v0[0] + v0[1] * v0[1]) + (v0[2] * v0[2] + v0[3] * v0[3])) + ((v1[0] * v1[0] + v1[1] * v1[1]) + (v1[2] * v1[2] + v1[3] * v1[3])); } }
;                     else if (TT >= 6) {
; #pragma unroll
;                         for (int j = 0; j < 4; ++j) { v0[j] = sigmoid_f(v0[j]); v1[j] = sigmoid_f(v1[j]); } }
;                     if (TT >= 6) { unsigned b0 = 0u, b1 = 0u;
; #pragma unroll
;                         for (int j = 0; j < 4; ++j) { b0 = __builtin_amdgcn_cvt_pk_u8_f32(__builtin_rintf(v0[j] * 255.0f), j, b0); b1 = __builtin_amdgcn_cvt_pk_u8_f32(__builtin_rintf(v1[j] * 255.0f), j, b1); }
;                         if (bj == 0) { gq.x = b0; gq.y = b1; } else { gq.z = b0; gq.w = b1; } }
	v_cndmask_b32_e32 v153, v147, v151, vcc
	v_rcp_f32_e32 v144, v144
	v_rcp_f32_e32 v145, v145
	v_mul_f32_e64 v150, v148, v148
	v_mul_f32_e64 v151, v149, v149
	v_cmp_gt_f32_e32 vcc, 0, v148
	v_mul_f32_e64 v150, v150, s48
	v_mul_f32_e64 v151, v151, s48
	v_fma_f32 v146, v144, s10, v132
	v_fma_f32 v147, v145, s10, v132
	v_exp_f32_e32 v150, v150
	v_fma_f32 v146, v144, v146, s12
	v_fma_f32 v147, v145, v147, s12
	v_exp_f32_e32 v151, v151
	v_fma_f32 v146, v144, v146, s14
	v_fma_f32 v147, v145, v147, s14
	s_nop 0
	v_fma_f32 v146, v144, v146, s46
	v_fma_f32 v147, v145, v147, s46
	s_nop 0
	v_mul_f32_e64 v144, v144, v146
	v_mul_f32_e64 v145, v145, v147
	v_mul_f32_e64 v146, v140, v140
	v_mul_f32_e64 v147, v141, v141
	v_mul_f32_e64 v144, v150, v144
	v_mul_f32_e64 v145, v151, v145
	v_mul_f32_e64 v146, v146, s48
	v_mul_f32_e64 v147, v147, s48
	v_mul_f32_e64 v150, v148, v144
	v_mul_f32_e64 v151, v149, v145
	v_fma_f32 v144, -v148, v144, v148
	v_fma_f32 v145, -v149, v145, v149
	v_exp_f32_e32 v146, v146
	v_cndmask_b32_e32 v150, v144, v150, vcc
	v_cmp_gt_f32_e32 vcc, 0, v149
	v_and_b32_e32 v144, 0x7fffffff, v140
	v_exp_f32_e32 v147, v147
	v_cndmask_b32_e32 v151, v145, v151, vcc
	v_and_b32_e32 v145, 0x7fffffff, v141
	v_fma_f32 v144, v144, s4, 1.0
	v_fma_f32 v145, v145, s4, 1.0
	v_cmp_gt_f32_e32 vcc, 0, v140
	v_rcp_f32_e32 v144, v144
	v_rcp_f32_e32 v145, v145
	s_nop 0
	v_fma_f32 v148, v144, s10, v132
	v_fma_f32 v149, v145, s10, v132
	s_nop 0
	v_fma_f32 v148, v144, v148, s12
	v_fma_f32 v149, v145, v149, s12
	s_nop 0
	v_fma_f32 v148, v144, v148, s14
	v_fma_f32 v149, v145, v149, s14
	s_nop 0
	v_fma_f32 v148, v144, v148, s46
	v_fma_f32 v149, v145, v149, s46
	s_nop 0
	v_mul_f32_e64 v144, v144, v148
	v_mul_f32_e64 v145, v145, v149
	v_fma_f32 v148, v92, v138, 0
	v_fma_f32 v149, v93, v138, 0
	v_mul_f32_e64 v144, v146, v144
	v_mul_f32_e64 v145, v147, v145
	s_nop 0
	v_mul_f32_e64 v146, v140, v144
	v_mul_f32_e64 v147, v141, v145
	v_fma_f32 v144, -v140, v144, v140
	v_fma_f32 v145, -v141, v145, v141
	s_nop 0
	v_cndmask_b32_e32 v140, v144, v146, vcc
	v_cmp_gt_f32_e32 vcc, 0, v141
	v_cvt_pk_bf16_f32 v144, v143, v154
	v_cvt_pk_bf16_f32 v146, v150, v151
	v_cndmask_b32_e32 v141, v145, v147, vcc
	v_cvt_pk_bf16_f32 v145, v152, v153
	v_cvt_pk_bf16_f32 v147, v140, v141
	global_store_dwordx4 v[136:137], v[144:147], off
	v_fma_f32 v140, v94, v138, 0
	v_fma_f32 v141, v95, v138, 0
	s_nop 0
	v_fma_f32 v146, v96, v138, 0
	v_fma_f32 v147, v97, v138, 0
	v_fma_f32 v144, v98, v138, 0
	v_fma_f32 v145, v99, v138, 0
	v_and_b32_e32 v151, 0x7fffffff, v147
	v_and_b32_e32 v150, 0x7fffffff, v146
	v_fma_f32 v150, v150, s4, 1.0
	v_fma_f32 v151, v151, s4, 1.0
	v_mul_f32_e64 v154, v146, v146
	v_mul_f32_e64 v155, v147, v147
	v_rcp_f32_e32 v150, v150
	v_rcp_f32_e32 v151, v151
	v_mul_f32_e64 v154, v154, s48
	v_mul_f32_e64 v155, v155, s48
	v_cmp_gt_f32_e32 vcc, 0, v146
	v_exp_f32_e32 v154, v154
	v_fma_f32 v152, v150, s10, v132
	v_fma_f32 v153, v151, s10, v132
	v_exp_f32_e32 v155, v155
	v_fma_f32 v152, v150, v152, s12
	v_fma_f32 v153, v151, v153, s12
	s_nop 0
	v_fma_f32 v152, v150, v152, s14
	v_fma_f32 v153, v151, v153, s14
	s_nop 0
	v_fma_f32 v152, v150, v152, s46
	v_fma_f32 v153, v151, v153, s46
	s_nop 0
	v_mul_f32_e64 v150, v150, v152
	v_mul_f32_e64 v151, v151, v153
	v_mul_f32_e64 v152, v144, v144
	v_mul_f32_e64 v153, v145, v145
	v_mul_f32_e64 v150, v154, v150
	v_mul_f32_e64 v151, v155, v151
	s_nop 0
	v_mul_f32_e64 v154, v146, v150
	v_mul_f32_e64 v155, v147, v151
	v_fma_f32 v150, -v146, v150, v146
	v_fma_f32 v151, -v147, v151, v147
	v_and_b32_e32 v146, 0x7fffffff, v144
	v_cndmask_b32_e32 v138, v150, v154, vcc
	v_cmp_gt_f32_e32 vcc, 0, v147
	v_and_b32_e32 v147, 0x7fffffff, v145
	v_fma_f32 v146, v146, s4, 1.0
	v_fma_f32 v147, v147, s4, 1.0
	v_cndmask_b32_e32 v143, v151, v155, vcc
	v_rcp_f32_e32 v146, v146
	v_rcp_f32_e32 v147, v147
	v_cmp_gt_f32_e32 vcc, 0, v144
	v_fma_f32 v150, v146, s10, v132
	v_fma_f32 v151, v147, s10, v132
	s_nop 0
	v_fma_f32 v150, v146, v150, s12
	v_fma_f32 v151, v147, v151, s12
	s_nop 0
	v_fma_f32 v150, v146, v150, s14
	v_fma_f32 v151, v147, v151, s14
	s_nop 0
	v_fma_f32 v150, v146, v150, s46
	v_fma_f32 v151, v147, v151, s46
	s_nop 0
	v_mul_f32_e64 v146, v146, v150
	v_mul_f32_e64 v147, v147, v151
	v_mul_f32_e64 v150, v152, s48
	v_mul_f32_e64 v151, v153, s48
	s_nop 0
	v_exp_f32_e32 v150, v150
	v_exp_f32_e32 v151, v151
	s_nop 0
	v_mul_f32_e64 v146, v150, v146
	v_mul_f32_e64 v147, v151, v147
	s_nop 0
	v_mul_f32_e64 v150, v144, v146
	v_mul_f32_e64 v151, v145, v147
	v_fma_f32 v146, -v144, v146, v144
	v_fma_f32 v147, -v145, v147, v145
	v_and_b32_e32 v144, 0x7fffffff, v148
	v_cndmask_b32_e32 v152, v146, v150, vcc
	v_cmp_gt_f32_e32 vcc, 0, v145
	v_and_b32_e32 v145, 0x7fffffff, v149
	v_fma_f32 v144, v144, s4, 1.0
	v_fma_f32 v145, v145, s4, 1.0
	v_cndmask_b32_e32 v153, v147, v151, vcc
	v_rcp_f32_e32 v144, v144
	v_rcp_f32_e32 v145, v145
	v_mul_f32_e64 v150, v148, v148
	v_mul_f32_e64 v151, v149, v149
	v_cmp_gt_f32_e32 vcc, 0, v148
	v_mul_f32_e64 v150, v150, s48
	v_mul_f32_e64 v151, v151, s48
	v_fma_f32 v146, v144, s10, v132
	v_fma_f32 v147, v145, s10, v132
	v_exp_f32_e32 v150, v150
	v_fma_f32 v146, v144, v146, s12
	v_fma_f32 v147, v145, v147, s12
	v_exp_f32_e32 v151, v151
	v_fma_f32 v146, v144, v146, s14
	v_fma_f32 v147, v145, v147, s14
	s_nop 0
	v_fma_f32 v146, v144, v146, s46
	v_fma_f32 v147, v145, v147, s46
	s_nop 0
	v_mul_f32_e64 v144, v144, v146
	v_mul_f32_e64 v145, v145, v147
	v_mul_f32_e64 v146, v140, v140
	v_mul_f32_e64 v147, v141, v141
	v_mul_f32_e64 v144, v150, v144
	v_mul_f32_e64 v145, v151, v145
	v_mul_f32_e64 v146, v146, s48
	v_mul_f32_e64 v147, v147, s48
	v_mul_f32_e64 v150, v148, v144
; __device__ __forceinline__ f32x2 gelu_pk(f32x2 v) {
;     const f32x2 av = __builtin_elementwise_abs(v), d = av * 0.2316418882f + 1.0f;
;     f32x2 t; t.x = __builtin_amdgcn_rcpf(d.x); t.y = __builtin_amdgcn_rcpf(d.y);
;     f32x2 q = t * 0.5307027145f + (-0.7265760135f); q = q * t + 0.7107068705f; q = q * t + (-0.142248368f); q = q * t + 0.127414796f; q = q * t;
;     const f32x2 s = (v * v) * (-0.72134752044f);
;     f32x2 e; e.x = __builtin_amdgcn_exp2f(s.x); e.y = __builtin_amdgcn_exp2f(s.y);
;     const f32x2 m = v * (q * e), r = v - m;
;     f32x2 o; o.x = v.x < 0.f ? m.x : r.x; o.y = v.y < 0.f ? m.y : r.y; return o;
;     template <int TT> __device__ __forceinline__ void other(const f32x4 (&acc)[2][2][4][2], bf16_t* base, int row0, int col0, PG8_LAS float* my, int t, int hh, int wc, int fq) const {
;     ...
;                 for (int bj = 0; bj < 2; ++bj) { f32x4 v0 = acc[ai][bj][m][0] * rs + bv[bj][0], v1 = acc[ai][bj][m][1] * rs + bv[bj][1];
;                     if (TT == 3) {
; #pragma unroll
;                         for (int j = 0; j < 4; ++j) { v0[j] = silu_f(v0[j]); v1[j] = silu_f(v1[j]); } }
;                     else if (TT == 4 || TT == 5) { f32x2 a = gelu_pk((f32x2){v0[0], v0[1]}), b = gelu_pk((f32x2){v0[2], v0[3]}), c = gelu_pk((f32x2){v1[0], v1[1]}), d = gelu_pk((f32x2){v1[2], v1[3]});
;                         v0 = (f32x4){a.x, a.y, b.x, b.y}; v1 = (f32x4){c.x, c.y, d.x, d.y};
;                         if (TT == 5) { ps += ((v0[0] + v0[1]) + (v0[2] + v0[3])) + ((v1[0] + v1[1]) + (v1[2] + v1[3]));
;                             pq += ((v0[0] * v0[0] + v0[1] * v0[1]) + (v0[2] * v0[2] + v0[3] * v0[3])) + ((v1[0] * v1[0] + v1[1] * v1[1]) + (v1[2] * v1[2] + v1[3] * v1[3])); } }
;                     else if (TT >= 6) {
; #pragma unroll
;                         for (int j = 0; j < 4; ++j) { v0[j] = sigmoid_f(v0[j]); v1[j] = sigmoid_f(v1[j]); } }
;                     if (TT >= 6) { unsigned b0 = 0u, b1 = 0u;
; #pragma unroll
;                         for (int j = 0; j < 4; ++j) { b0 = __builtin_amdgcn_cvt_pk_u8_f32(__builtin_rintf(v0[j] * 255.0f), j, b0); b1 = __builtin_amdgcn_cvt_pk_u8_f32(__builtin_rintf(v1[j] * 255.0f), j, b1); }
;                         if (bj == 0) { gq.x = b0; gq.y = b1; } else { gq.z = b0; gq.w = b1; } }
	v_mul_f32_e64 v151, v149, v145
	v_fma_f32 v144, -v148, v144, v148
	v_fma_f32 v145, -v149, v145, v149
	v_exp_f32_e32 v146, v146
	v_cndmask_b32_e32 v150, v144, v150, vcc
	v_cmp_gt_f32_e32 vcc, 0, v149
	v_and_b32_e32 v144, 0x7fffffff, v140
	v_exp_f32_e32 v147, v147
	v_cndmask_b32_e32 v151, v145, v151, vcc
	v_and_b32_e32 v145, 0x7fffffff, v141
	v_fma_f32 v144, v144, s4, 1.0
	v_fma_f32 v145, v145, s4, 1.0
	v_cmp_gt_f32_e32 vcc, 0, v140
	v_rcp_f32_e32 v144, v144
	v_rcp_f32_e32 v145, v145
	s_nop 0
	v_fma_f32 v148, v144, s10, v132
	v_fma_f32 v149, v145, s10, v132
	s_nop 0
	v_fma_f32 v148, v144, v148, s12
	v_fma_f32 v149, v145, v149, s12
	s_nop 0
	v_fma_f32 v148, v144, v148, s14
	v_fma_f32 v149, v145, v149, s14
	s_nop 0
	v_fma_f32 v148, v144, v148, s46
	v_fma_f32 v149, v145, v149, s46
	s_nop 0
	v_mul_f32_e64 v144, v144, v148
	v_mul_f32_e64 v145, v145, v149
	s_nop 0
	v_mul_f32_e64 v144, v146, v144
	v_mul_f32_e64 v145, v147, v145
	s_nop 0
	v_mul_f32_e64 v146, v140, v144
	v_mul_f32_e64 v147, v141, v145
	v_fma_f32 v144, -v140, v144, v140
	v_fma_f32 v145, -v141, v145, v141
	s_nop 0
	v_cndmask_b32_e32 v140, v144, v146, vcc
	v_cmp_gt_f32_e32 vcc, 0, v141
	v_cvt_pk_bf16_f32 v144, v138, v143
	v_cvt_pk_bf16_f32 v146, v150, v151
	v_cndmask_b32_e32 v141, v145, v147, vcc
	v_cvt_pk_bf16_f32 v145, v152, v153
	v_cvt_pk_bf16_f32 v147, v140, v141
	v_mov_b32_e32 v138, v139
	global_store_dwordx4 v[136:137], v[144:147], off offset:256
	v_fma_f32 v140, v70, v138, 0
	v_fma_f32 v141, v71, v138, 0
	v_fma_f32 v148, v68, v138, 0
	v_fma_f32 v149, v69, v138, 0
	v_fma_f32 v146, v72, v138, 0
	v_fma_f32 v147, v73, v138, 0
	v_fma_f32 v144, v74, v138, 0
	v_fma_f32 v145, v75, v138, 0
	v_and_b32_e32 v151, 0x7fffffff, v147
	v_and_b32_e32 v150, 0x7fffffff, v146
	v_fma_f32 v150, v150, s4, 1.0
	v_fma_f32 v151, v151, s4, 1.0
	v_mul_f32_e64 v154, v146, v146
	v_mul_f32_e64 v155, v147, v147
	v_rcp_f32_e32 v150, v150
	v_rcp_f32_e32 v151, v151
	v_mul_f32_e64 v154, v154, s48
	v_mul_f32_e64 v155, v155, s48
	v_cmp_gt_f32_e32 vcc, 0, v146
	v_exp_f32_e32 v154, v154
	v_fma_f32 v152, v150, s10, v132
	v_fma_f32 v153, v151, s10, v132
	v_exp_f32_e32 v155, v155
	v_fma_f32 v152, v150, v152, s12
	v_fma_f32 v153, v151, v153, s12
	v_add_u32_e32 v136, 48, v142
	v_fma_f32 v152, v150, v152, s14
	v_fma_f32 v153, v151, v153, s14
	v_mad_i64_i32 v[136:137], s[2:3], v136, s81, v[134:135]
	v_fma_f32 v152, v150, v152, s46
	v_fma_f32 v153, v151, v153, s46
	s_nop 0
	v_mul_f32_e64 v150, v150, v152
	v_mul_f32_e64 v151, v151, v153
	v_mul_f32_e64 v152, v144, v144
	v_mul_f32_e64 v153, v145, v145
	v_mul_f32_e64 v150, v154, v150
	v_mul_f32_e64 v151, v155, v151
	s_nop 0
	v_mul_f32_e64 v154, v146, v150
	v_mul_f32_e64 v155, v147, v151
	v_fma_f32 v150, -v146, v150, v146
	v_fma_f32 v151, -v147, v151, v147
	v_and_b32_e32 v146, 0x7fffffff, v144
	v_cndmask_b32_e32 v139, v150, v154, vcc
	v_cmp_gt_f32_e32 vcc, 0, v147
	v_and_b32_e32 v147, 0x7fffffff, v145
	v_fma_f32 v146, v146, s4, 1.0
	v_fma_f32 v147, v147, s4, 1.0
	v_cndmask_b32_e32 v143, v151, v155, vcc
	v_rcp_f32_e32 v146, v146
	v_rcp_f32_e32 v147, v147
	v_cmp_gt_f32_e32 vcc, 0, v144
	v_fma_f32 v150, v146, s10, v132
	v_fma_f32 v151, v147, s10, v132
	s_nop 0
	v_fma_f32 v150, v146, v150, s12
	v_fma_f32 v151, v147, v151, s12
	s_nop 0
	v_fma_f32 v150, v146, v150, s14
	v_fma_f32 v151, v147, v151, s14
	s_nop 0
	v_fma_f32 v150, v146, v150, s46
	v_fma_f32 v151, v147, v151, s46
	s_nop 0
	v_mul_f32_e64 v146, v146, v150
	v_mul_f32_e64 v147, v147, v151
	v_mul_f32_e64 v150, v152, s48
	v_mul_f32_e64 v151, v153, s48
	s_nop 0
	v_exp_f32_e32 v150, v150
	v_exp_f32_e32 v151, v151
	s_nop 0
	v_mul_f32_e64 v146, v150, v146
	v_mul_f32_e64 v147, v151, v147
	s_nop 0
	v_mul_f32_e64 v150, v144, v146
	v_mul_f32_e64 v151, v145, v147
	v_fma_f32 v146, -v144, v146, v144
	v_fma_f32 v147, -v145, v147, v145
	v_and_b32_e32 v144, 0x7fffffff, v148
	v_cndmask_b32_e32 v152, v146, v150, vcc
	v_cmp_gt_f32_e32 vcc, 0, v145
	v_and_b32_e32 v145, 0x7fffffff, v149
	v_fma_f32 v144, v144, s4, 1.0
	v_fma_f32 v145, v145, s4, 1.0
	v_cndmask_b32_e32 v153, v147, v151, vcc
	v_rcp_f32_e32 v144, v144
	v_rcp_f32_e32 v145, v145
	v_mul_f32_e64 v150, v148, v148
	v_mul_f32_e64 v151, v149, v149
	v_cmp_gt_f32_e32 vcc, 0, v148
	v_mul_f32_e64 v150, v150, s48
	v_mul_f32_e64 v151, v151, s48
	v_fma_f32 v146, v144, s10, v132
	v_fma_f32 v147, v145, s10, v132
	v_exp_f32_e32 v150, v150
	v_fma_f32 v146, v144, v146, s12
	v_fma_f32 v147, v145, v147, s12
	v_exp_f32_e32 v151, v151
	v_fma_f32 v146, v144, v146, s14
	v_fma_f32 v147, v145, v147, s14
	s_nop 0
	v_fma_f32 v146, v144, v146, s46
	v_fma_f32 v147, v145, v147, s46
	s_nop 0
	v_mul_f32_e64 v144, v144, v146
	v_mul_f32_e64 v145, v145, v147
	v_mul_f32_e64 v146, v140, v140
	v_mul_f32_e64 v147, v141, v141
	v_mul_f32_e64 v144, v150, v144
	v_mul_f32_e64 v145, v151, v145
	v_mul_f32_e64 v146, v146, s48
	v_mul_f32_e64 v147, v147, s48
	v_mul_f32_e64 v150, v148, v144
	v_mul_f32_e64 v151, v149, v145
	v_fma_f32 v144, -v148, v144, v148
	v_fma_f32 v145, -v149, v145, v149
	v_exp_f32_e32 v146, v146
	v_cndmask_b32_e32 v150, v144, v150, vcc
	v_cmp_gt_f32_e32 vcc, 0, v149
	v_and_b32_e32 v144, 0x7fffffff, v140
	v_exp_f32_e32 v147, v147
	v_cndmask_b32_e32 v151, v145, v151, vcc
	v_and_b32_e32 v145, 0x7fffffff, v141
	v_fma_f32 v144, v144, s4, 1.0
	v_fma_f32 v145, v145, s4, 1.0
	v_cmp_gt_f32_e32 vcc, 0, v140
	v_rcp_f32_e32 v144, v144
	v_rcp_f32_e32 v145, v145
	s_nop 0
	v_fma_f32 v148, v144, s10, v132
	v_fma_f32 v149, v145, s10, v132
	s_nop 0
	v_fma_f32 v148, v144, v148, s12
	v_fma_f32 v149, v145, v149, s12
	s_nop 0
	v_fma_f32 v148, v144, v148, s14
	v_fma_f32 v149, v145, v149, s14
	s_nop 0
	v_fma_f32 v148, v144, v148, s46
; __device__ __forceinline__ float silu_f(float g) { return g * __builtin_amdgcn_rcpf(1.0f + __builtin_amdgcn_exp2f(-1.44269504f * g)); }
; __device__ __forceinline__ f32x2 gelu_pk(f32x2 v) {
;     const f32x2 av = __builtin_elementwise_abs(v), d = av * 0.2316418882f + 1.0f;
;     f32x2 t; t.x = __builtin_amdgcn_rcpf(d.x); t.y = __builtin_amdgcn_rcpf(d.y);
;     f32x2 q = t * 0.5307027145f + (-0.7265760135f); q = q * t + 0.7107068705f; q = q * t + (-0.142248368f); q = q * t + 0.127414796f; q = q * t;
;     const f32x2 s = (v * v) * (-0.72134752044f);
;     f32x2 e; e.x = __builtin_amdgcn_exp2f(s.x); e.y = __builtin_amdgcn_exp2f(s.y);
;     const f32x2 m = v * (q * e), r = v - m;
;     f32x2 o; o.x = v.x < 0.f ? m.x : r.x; o.y = v.y < 0.f ? m.y : r.y; return o;
;     template <int TT> __device__ __forceinline__ void other(const f32x4 (&acc)[2][2][4][2], bf16_t* base, int row0, int col0, PG8_LAS float* my, int t, int hh, int wc, int fq) const {
;     ...
;             for (int m = 0; m < 4; ++m) { bf16_t* rowp = base + (size_t)(row0 + ai * HALF + m * 16) * LDT + col0;
;                 const float rs = my[(ai * 4 + m) * 16]; float ps = 0.f, pq = 0.f; u32x4 gq = {0u, 0u, 0u, 0u};
; #pragma unroll
;                 for (int bj = 0; bj < 2; ++bj) { f32x4 v0 = acc[ai][bj][m][0] * rs + bv[bj][0], v1 = acc[ai][bj][m][1] * rs + bv[bj][1];
;                     if (TT == 3) {
; #pragma unroll
;                         for (int j = 0; j < 4; ++j) { v0[j] = silu_f(v0[j]); v1[j] = silu_f(v1[j]); } }
;                     else if (TT == 4 || TT == 5) { f32x2 a = gelu_pk((f32x2){v0[0], v0[1]}), b = gelu_pk((f32x2){v0[2], v0[3]}), c = gelu_pk((f32x2){v1[0], v1[1]}), d = gelu_pk((f32x2){v1[2], v1[3]});
;                         v0 = (f32x4){a.x, a.y, b.x, b.y}; v1 = (f32x4){c.x, c.y, d.x, d.y};
;                         if (TT == 5) { ps += ((v0[0] + v0[1]) + (v0[2] + v0[3])) + ((v1[0] + v1[1]) + (v1[2] + v1[3]));
;                             pq += ((v0[0] * v0[0] + v0[1] * v0[1]) + (v0[2] * v0[2] + v0[3] * v0[3])) + ((v1[0] * v1[0] + v1[1] * v1[1]) + (v1[2] * v1[2] + v1[3] * v1[3])); } }
;                     else if (TT >= 6) {
; #pragma unroll
;                         for (int j = 0; j < 4; ++j) { v0[j] = sigmoid_f(v0[j]); v1[j] = sigmoid_f(v1[j]); } }
;                     if (TT >= 6) { unsigned b0 = 0u, b1 = 0u;
; #pragma unroll
	v_fma_f32 v149, v145, v149, s46
	s_nop 0
	v_mul_f32_e64 v144, v144, v148
	v_mul_f32_e64 v145, v145, v149
	s_nop 0
	v_mul_f32_e64 v144, v146, v144
	v_mul_f32_e64 v145, v147, v145
	s_nop 0
	v_mul_f32_e64 v146, v140, v144
	v_mul_f32_e64 v147, v141, v145
	v_fma_f32 v144, -v140, v144, v140
	v_fma_f32 v145, -v141, v145, v141
	s_nop 0
	v_cndmask_b32_e32 v140, v144, v146, vcc
	v_cmp_gt_f32_e32 vcc, 0, v141
	v_cvt_pk_bf16_f32 v144, v139, v143
	v_cvt_pk_bf16_f32 v146, v150, v151
	v_cndmask_b32_e32 v141, v145, v147, vcc
	v_cvt_pk_bf16_f32 v145, v152, v153
	v_cvt_pk_bf16_f32 v147, v140, v141
	global_store_dwordx4 v[136:137], v[144:147], off
	v_fma_f32 v140, v78, v138, 0
	v_fma_f32 v141, v79, v138, 0
	s_nop 0
	v_fma_f32 v146, v80, v138, 0
	v_fma_f32 v147, v81, v138, 0
	v_fma_f32 v144, v82, v138, 0
	v_fma_f32 v145, v83, v138, 0
	v_and_b32_e32 v149, 0x7fffffff, v147
	v_and_b32_e32 v148, 0x7fffffff, v146
	v_fma_f32 v148, v148, s4, 1.0
	v_fma_f32 v149, v149, s4, 1.0
	v_mul_f32_e64 v152, v146, v146
	v_mul_f32_e64 v153, v147, v147
	v_rcp_f32_e32 v148, v148
	v_rcp_f32_e32 v149, v149
	v_mul_f32_e64 v152, v152, s48
	v_mul_f32_e64 v153, v153, s48
	v_cmp_gt_f32_e32 vcc, 0, v146
	v_exp_f32_e32 v152, v152
	v_fma_f32 v150, v148, s10, v132
	v_fma_f32 v151, v149, s10, v132
	v_exp_f32_e32 v153, v153
	v_fma_f32 v150, v148, v150, s12
	v_fma_f32 v151, v149, v151, s12
	v_fma_f32 v139, v77, v138, 0
	v_fma_f32 v138, v76, v138, 0
	v_fma_f32 v150, v148, v150, s14
	v_fma_f32 v151, v149, v151, s14
	s_nop 0
	v_fma_f32 v150, v148, v150, s46
	v_fma_f32 v151, v149, v151, s46
	s_nop 0
	v_mul_f32_e64 v148, v148, v150
	v_mul_f32_e64 v149, v149, v151
	v_mul_f32_e64 v150, v144, v144
	v_mul_f32_e64 v151, v145, v145
	v_mul_f32_e64 v148, v152, v148
	v_mul_f32_e64 v149, v153, v149
	s_nop 0
	v_mul_f32_e64 v152, v146, v148
	v_mul_f32_e64 v153, v147, v149
	v_fma_f32 v148, -v146, v148, v146
	v_fma_f32 v149, -v147, v149, v147
	v_and_b32_e32 v146, 0x7fffffff, v144
	v_cndmask_b32_e32 v143, v148, v152, vcc
	v_cmp_gt_f32_e32 vcc, 0, v147
	v_and_b32_e32 v147, 0x7fffffff, v145
	v_fma_f32 v146, v146, s4, 1.0
	v_fma_f32 v147, v147, s4, 1.0
	v_cndmask_b32_e32 v152, v149, v153, vcc
	v_rcp_f32_e32 v146, v146
	v_rcp_f32_e32 v147, v147
	v_cmp_gt_f32_e32 vcc, 0, v144
	v_fma_f32 v148, v146, s10, v132
	v_fma_f32 v149, v147, s10, v132
	s_nop 0
	v_fma_f32 v148, v146, v148, s12
	v_fma_f32 v149, v147, v149, s12
	s_nop 0
	v_fma_f32 v148, v146, v148, s14
	v_fma_f32 v149, v147, v149, s14
	s_nop 0
	v_fma_f32 v148, v146, v148, s46
	v_fma_f32 v149, v147, v149, s46
	s_nop 0
	v_mul_f32_e64 v146, v146, v148
	v_mul_f32_e64 v147, v147, v149
	v_mul_f32_e64 v148, v150, s48
	v_mul_f32_e64 v149, v151, s48
	s_nop 0
	v_exp_f32_e32 v148, v148
	v_exp_f32_e32 v149, v149
	s_nop 0
	v_mul_f32_e64 v146, v148, v146
	v_mul_f32_e64 v147, v149, v147
	s_nop 0
	v_mul_f32_e64 v148, v144, v146
	v_mul_f32_e64 v149, v145, v147
	v_fma_f32 v146, -v144, v146, v144
	v_fma_f32 v147, -v145, v147, v145
	v_and_b32_e32 v144, 0x7fffffff, v138
	v_cndmask_b32_e32 v150, v146, v148, vcc
	v_cmp_gt_f32_e32 vcc, 0, v145
	v_and_b32_e32 v145, 0x7fffffff, v139
	v_fma_f32 v144, v144, s4, 1.0
	v_fma_f32 v145, v145, s4, 1.0
	v_cndmask_b32_e32 v151, v147, v149, vcc
	v_rcp_f32_e32 v144, v144
	v_rcp_f32_e32 v145, v145
	v_mul_f32_e64 v148, v138, v138
	v_mul_f32_e64 v149, v139, v139
	v_cmp_gt_f32_e32 vcc, 0, v138
	v_mul_f32_e64 v148, v148, s48
	v_mul_f32_e64 v149, v149, s48
	v_fma_f32 v146, v144, s10, v132
	v_fma_f32 v147, v145, s10, v132
	v_exp_f32_e32 v148, v148
	v_fma_f32 v146, v144, v146, s12
	v_fma_f32 v147, v145, v147, s12
	v_exp_f32_e32 v149, v149
	v_fma_f32 v146, v144, v146, s14
	v_fma_f32 v147, v145, v147, s14
	s_nop 0
	v_fma_f32 v146, v144, v146, s46
	v_fma_f32 v147, v145, v147, s46
	s_nop 0
	v_mul_f32_e64 v144, v144, v146
	v_mul_f32_e64 v145, v145, v147
	v_mul_f32_e64 v146, v140, v140
	v_mul_f32_e64 v147, v141, v141
	v_mul_f32_e64 v144, v148, v144
	v_mul_f32_e64 v145, v149, v145
	s_nop 0
	v_mul_f32_e64 v148, v138, v144
	v_mul_f32_e64 v149, v139, v145
	v_fma_f32 v144, -v138, v144, v138
	v_fma_f32 v145, -v139, v145, v139
	v_and_b32_e32 v138, 0x7fffffff, v140
	v_cndmask_b32_e32 v148, v144, v148, vcc
	v_cmp_gt_f32_e32 vcc, 0, v139
	v_and_b32_e32 v139, 0x7fffffff, v141
	v_fma_f32 v138, v138, s4, 1.0
	v_fma_f32 v139, v139, s4, 1.0
	v_cndmask_b32_e32 v149, v145, v149, vcc
	v_rcp_f32_e32 v138, v138
	v_rcp_f32_e32 v139, v139
	v_cmp_gt_f32_e32 vcc, 0, v140
	v_fma_f32 v144, v138, s10, v132
	v_fma_f32 v145, v139, s10, v132
	s_nop 0
	v_fma_f32 v144, v138, v144, s12
	v_fma_f32 v145, v139, v145, s12
	s_nop 0
	v_fma_f32 v144, v138, v144, s14
	v_fma_f32 v145, v139, v145, s14
	s_nop 0
	v_fma_f32 v144, v138, v144, s46
	v_fma_f32 v145, v139, v145, s46
	s_nop 0
	v_mul_f32_e64 v138, v138, v144
	v_mul_f32_e64 v139, v139, v145
	v_mul_f32_e64 v144, v146, s48
	v_mul_f32_e64 v145, v147, s48
	s_nop 0
	v_exp_f32_e32 v144, v144
	v_exp_f32_e32 v145, v145
	s_nop 0
	v_mul_f32_e64 v138, v144, v138
	v_mul_f32_e64 v139, v145, v139
	s_nop 0
	v_mul_f32_e64 v144, v140, v138
	v_mul_f32_e64 v145, v141, v139
	v_fma_f32 v138, -v140, v138, v140
	v_fma_f32 v139, -v141, v139, v141
	v_cvt_pk_bf16_f32 v140, v148, v149
	v_cndmask_b32_e32 v144, v138, v144, vcc
	v_cmp_gt_f32_e32 vcc, 0, v141
	v_cvt_pk_bf16_f32 v138, v143, v152
	s_nop 0
	v_cndmask_b32_e32 v141, v139, v145, vcc
	v_cvt_pk_bf16_f32 v139, v150, v151
	v_cvt_pk_bf16_f32 v141, v144, v141
	global_store_dwordx4 v[136:137], v[138:141], off offset:256
	ds_read2_b32 v[138:139], v199 offset0:64 offset1:80
	v_add_u32_e32 v136, 0x80, v142
	v_mad_i64_i32 v[136:137], s[2:3], v136, s81, v[134:135]
	s_waitcnt lgkmcnt(0)
; __device__ __forceinline__ f32x2 gelu_pk(f32x2 v) {
;     const f32x2 av = __builtin_elementwise_abs(v), d = av * 0.2316418882f + 1.0f;
;     f32x2 t; t.x = __builtin_amdgcn_rcpf(d.x); t.y = __builtin_amdgcn_rcpf(d.y);
;     f32x2 q = t * 0.5307027145f + (-0.7265760135f); q = q * t + 0.7107068705f; q = q * t + (-0.142248368f); q = q * t + 0.127414796f; q = q * t;
;     const f32x2 s = (v * v) * (-0.72134752044f);
;     f32x2 e; e.x = __builtin_amdgcn_exp2f(s.x); e.y = __builtin_amdgcn_exp2f(s.y);
;     const f32x2 m = v * (q * e), r = v - m;
;     f32x2 o; o.x = v.x < 0.f ? m.x : r.x; o.y = v.y < 0.f ? m.y : r.y; return o;
;     template <int TT> __device__ __forceinline__ void other(const f32x4 (&acc)[2][2][4][2], bf16_t* base, int row0, int col0, PG8_LAS float* my, int t, int hh, int wc, int fq) const {
;     ...
;                 for (int bj = 0; bj < 2; ++bj) { f32x4 v0 = acc[ai][bj][m][0] * rs + bv[bj][0], v1 = acc[ai][bj][m][1] * rs + bv[bj][1];
;                     if (TT == 3) {
; #pragma unroll
;                         for (int j = 0; j < 4; ++j) { v0[j] = silu_f(v0[j]); v1[j] = silu_f(v1[j]); } }
;                     else if (TT == 4 || TT == 5) { f32x2 a = gelu_pk((f32x2){v0[0], v0[1]}), b = gelu_pk((f32x2){v0[2], v0[3]}), c = gelu_pk((f32x2){v1[0], v1[1]}), d = gelu_pk((f32x2){v1[2], v1[3]});
;                         v0 = (f32x4){a.x, a.y, b.x, b.y}; v1 = (f32x4){c.x, c.y, d.x, d.y};
;                         if (TT == 5) { ps += ((v0[0] + v0[1]) + (v0[2] + v0[3])) + ((v1[0] + v1[1]) + (v1[2] + v1[3]));
;                             pq += ((v0[0] * v0[0] + v0[1] * v0[1]) + (v0[2] * v0[2] + v0[3] * v0[3])) + ((v1[0] * v1[0] + v1[1] * v1[1]) + (v1[2] * v1[2] + v1[3] * v1[3])); } }
;                     else if (TT >= 6) {
; #pragma unroll
;                         for (int j = 0; j < 4; ++j) { v0[j] = sigmoid_f(v0[j]); v1[j] = sigmoid_f(v1[j]); } }
;                     if (TT >= 6) { unsigned b0 = 0u, b1 = 0u;
; #pragma unroll
;                         for (int j = 0; j < 4; ++j) { b0 = __builtin_amdgcn_cvt_pk_u8_f32(__builtin_rintf(v0[j] * 255.0f), j, b0); b1 = __builtin_amdgcn_cvt_pk_u8_f32(__builtin_rintf(v1[j] * 255.0f), j, b1); }
;                         if (bj == 0) { gq.x = b0; gq.y = b1; } else { gq.z = b0; gq.w = b1; } }
	v_fma_f32 v146, v56, v138, 0
	v_fma_f32 v147, v57, v138, 0
	s_nop 0
	v_and_b32_e32 v151, 0x7fffffff, v147
	v_and_b32_e32 v150, 0x7fffffff, v146
	v_fma_f32 v150, v150, s4, 1.0
	v_fma_f32 v151, v151, s4, 1.0
	v_mul_f32_e64 v154, v146, v146
	v_mul_f32_e64 v155, v147, v147
	v_rcp_f32_e32 v150, v150
	v_rcp_f32_e32 v151, v151
	v_mul_f32_e64 v154, v154, s48
	v_mul_f32_e64 v155, v155, s48
	v_fma_f32 v144, v58, v138, 0
	v_fma_f32 v145, v59, v138, 0
	v_exp_f32_e32 v154, v154
	v_fma_f32 v152, v150, s10, v132
	v_fma_f32 v153, v151, s10, v132
	v_exp_f32_e32 v155, v155
	v_fma_f32 v152, v150, v152, s12
	v_fma_f32 v153, v151, v153, s12
	v_cmp_gt_f32_e32 vcc, 0, v146
	v_fma_f32 v152, v150, v152, s14
	v_fma_f32 v153, v151, v153, s14
	v_fma_f32 v148, v52, v138, 0
	v_fma_f32 v149, v53, v138, 0
	v_fma_f32 v152, v150, v152, s46
	v_fma_f32 v153, v151, v153, s46
	v_fma_f32 v140, v54, v138, 0
	v_fma_f32 v141, v55, v138, 0
	v_mul_f32_e64 v150, v150, v152
	v_mul_f32_e64 v151, v151, v153
	v_mul_f32_e64 v152, v144, v144
	v_mul_f32_e64 v153, v145, v145
	v_mul_f32_e64 v150, v154, v150
	v_mul_f32_e64 v151, v155, v151
	s_nop 0
	v_mul_f32_e64 v154, v146, v150
	v_mul_f32_e64 v155, v147, v151
	v_fma_f32 v150, -v146, v150, v146
	v_fma_f32 v151, -v147, v151, v147
	v_and_b32_e32 v146, 0x7fffffff, v144
	v_cndmask_b32_e32 v143, v150, v154, vcc
	v_cmp_gt_f32_e32 vcc, 0, v147
	v_and_b32_e32 v147, 0x7fffffff, v145
	v_fma_f32 v146, v146, s4, 1.0
	v_fma_f32 v147, v147, s4, 1.0
	v_cndmask_b32_e32 v154, v151, v155, vcc
	v_rcp_f32_e32 v146, v146
	v_rcp_f32_e32 v147, v147
	v_cmp_gt_f32_e32 vcc, 0, v144
	v_fma_f32 v150, v146, s10, v132
	v_fma_f32 v151, v147, s10, v132
	s_nop 0
	v_fma_f32 v150, v146, v150, s12
	v_fma_f32 v151, v147, v151, s12
	s_nop 0
	v_fma_f32 v150, v146, v150, s14
	v_fma_f32 v151, v147, v151, s14
	s_nop 0
	v_fma_f32 v150, v146, v150, s46
	v_fma_f32 v151, v147, v151, s46
	s_nop 0
	v_mul_f32_e64 v146, v146, v150
	v_mul_f32_e64 v147, v147, v151
	v_mul_f32_e64 v150, v152, s48
	v_mul_f32_e64 v151, v153, s48
	s_nop 0
	v_exp_f32_e32 v150, v150
	v_exp_f32_e32 v151, v151
	s_nop 0
	v_mul_f32_e64 v146, v150, v146
	v_mul_f32_e64 v147, v151, v147
	s_nop 0
	v_mul_f32_e64 v150, v144, v146
	v_mul_f32_e64 v151, v145, v147
	v_fma_f32 v146, -v144, v146, v144
	v_fma_f32 v147, -v145, v147, v145
	v_and_b32_e32 v144, 0x7fffffff, v148
	v_cndmask_b32_e32 v152, v146, v150, vcc
	v_cmp_gt_f32_e32 vcc, 0, v145
	v_and_b32_e32 v145, 0x7fffffff, v149
	v_fma_f32 v144, v144, s4, 1.0
	v_fma_f32 v145, v145, s4, 1.0
	v_cndmask_b32_e32 v153, v147, v151, vcc
	v_rcp_f32_e32 v144, v144
	v_rcp_f32_e32 v145, v145
	v_mul_f32_e64 v150, v148, v148
	v_mul_f32_e64 v151, v149, v149
	v_cmp_gt_f32_e32 vcc, 0, v148
	v_mul_f32_e64 v150, v150, s48
	v_mul_f32_e64 v151, v151, s48
	v_fma_f32 v146, v144, s10, v132
	v_fma_f32 v147, v145, s10, v132
	v_exp_f32_e32 v150, v150
	v_fma_f32 v146, v144, v146, s12
	v_fma_f32 v147, v145, v147, s12
	v_exp_f32_e32 v151, v151
	v_fma_f32 v146, v144, v146, s14
	v_fma_f32 v147, v145, v147, s14
	s_nop 0
	v_fma_f32 v146, v144, v146, s46
	v_fma_f32 v147, v145, v147, s46
	s_nop 0
	v_mul_f32_e64 v144, v144, v146
	v_mul_f32_e64 v145, v145, v147
	v_mul_f32_e64 v146, v140, v140
	v_mul_f32_e64 v147, v141, v141
	v_mul_f32_e64 v144, v150, v144
	v_mul_f32_e64 v145, v151, v145
	v_mul_f32_e64 v146, v146, s48
	v_mul_f32_e64 v147, v147, s48
	v_mul_f32_e64 v150, v148, v144
	v_mul_f32_e64 v151, v149, v145
	v_fma_f32 v144, -v148, v144, v148
	v_fma_f32 v145, -v149, v145, v149
	v_exp_f32_e32 v146, v146
	v_cndmask_b32_e32 v150, v144, v150, vcc
	v_cmp_gt_f32_e32 vcc, 0, v149
	v_and_b32_e32 v144, 0x7fffffff, v140
	v_exp_f32_e32 v147, v147
	v_cndmask_b32_e32 v151, v145, v151, vcc
	v_and_b32_e32 v145, 0x7fffffff, v141
	v_fma_f32 v144, v144, s4, 1.0
	v_fma_f32 v145, v145, s4, 1.0
	v_cmp_gt_f32_e32 vcc, 0, v140
	v_rcp_f32_e32 v144, v144
	v_rcp_f32_e32 v145, v145
	s_nop 0
	v_fma_f32 v148, v144, s10, v132
	v_fma_f32 v149, v145, s10, v132
	s_nop 0
	v_fma_f32 v148, v144, v148, s12
	v_fma_f32 v149, v145, v149, s12
	s_nop 0
	v_fma_f32 v148, v144, v148, s14
	v_fma_f32 v149, v145, v149, s14
	s_nop 0
	v_fma_f32 v148, v144, v148, s46
	v_fma_f32 v149, v145, v149, s46
	s_nop 0
	v_mul_f32_e64 v144, v144, v148
	v_mul_f32_e64 v145, v145, v149
	v_fma_f32 v148, v60, v138, 0
	v_fma_f32 v149, v61, v138, 0
	v_mul_f32_e64 v144, v146, v144
	v_mul_f32_e64 v145, v147, v145
	s_nop 0
	v_mul_f32_e64 v146, v140, v144
	v_mul_f32_e64 v147, v141, v145
	v_fma_f32 v144, -v140, v144, v140
	v_fma_f32 v145, -v141, v145, v141
	s_nop 0
	v_cndmask_b32_e32 v140, v144, v146, vcc
	v_cmp_gt_f32_e32 vcc, 0, v141
	v_cvt_pk_bf16_f32 v144, v143, v154
	v_cvt_pk_bf16_f32 v146, v150, v151
	v_cndmask_b32_e32 v141, v145, v147, vcc
	v_cvt_pk_bf16_f32 v145, v152, v153
	v_cvt_pk_bf16_f32 v147, v140, v141
	global_store_dwordx4 v[136:137], v[144:147], off
	v_fma_f32 v140, v62, v138, 0
	v_fma_f32 v141, v63, v138, 0
	s_nop 0
	v_fma_f32 v146, v64, v138, 0
	v_fma_f32 v147, v65, v138, 0
	v_fma_f32 v144, v66, v138, 0
	v_fma_f32 v145, v67, v138, 0
	v_and_b32_e32 v151, 0x7fffffff, v147
	v_and_b32_e32 v150, 0x7fffffff, v146
	v_fma_f32 v150, v150, s4, 1.0
	v_fma_f32 v151, v151, s4, 1.0
	v_mul_f32_e64 v154, v146, v146
	v_mul_f32_e64 v155, v147, v147
	v_rcp_f32_e32 v150, v150
	v_rcp_f32_e32 v151, v151
	v_mul_f32_e64 v154, v154, s48
	v_mul_f32_e64 v155, v155, s48
	v_cmp_gt_f32_e32 vcc, 0, v146
	v_exp_f32_e32 v154, v154
	v_fma_f32 v152, v150, s10, v132
	v_fma_f32 v153, v151, s10, v132
	v_exp_f32_e32 v155, v155
	v_fma_f32 v152, v150, v152, s12
	v_fma_f32 v153, v151, v153, s12
	s_nop 0
	v_fma_f32 v152, v150, v152, s14
	v_fma_f32 v153, v151, v153, s14
	s_nop 0
	v_fma_f32 v152, v150, v152, s46
; __device__ __forceinline__ f32x2 gelu_pk(f32x2 v) {
;     const f32x2 av = __builtin_elementwise_abs(v), d = av * 0.2316418882f + 1.0f;
;     f32x2 t; t.x = __builtin_amdgcn_rcpf(d.x); t.y = __builtin_amdgcn_rcpf(d.y);
;     f32x2 q = t * 0.5307027145f + (-0.7265760135f); q = q * t + 0.7107068705f; q = q * t + (-0.142248368f); q = q * t + 0.127414796f; q = q * t;
;     const f32x2 s = (v * v) * (-0.72134752044f);
;     f32x2 e; e.x = __builtin_amdgcn_exp2f(s.x); e.y = __builtin_amdgcn_exp2f(s.y);
;     const f32x2 m = v * (q * e), r = v - m;
;     f32x2 o; o.x = v.x < 0.f ? m.x : r.x; o.y = v.y < 0.f ? m.y : r.y; return o;
;     template <int TT> __device__ __forceinline__ void other(const f32x4 (&acc)[2][2][4][2], bf16_t* base, int row0, int col0, PG8_LAS float* my, int t, int hh, int wc, int fq) const {
;     ...
;                 for (int bj = 0; bj < 2; ++bj) { f32x4 v0 = acc[ai][bj][m][0] * rs + bv[bj][0], v1 = acc[ai][bj][m][1] * rs + bv[bj][1];
;                     if (TT == 3) {
; #pragma unroll
;                         for (int j = 0; j < 4; ++j) { v0[j] = silu_f(v0[j]); v1[j] = silu_f(v1[j]); } }
;                     else if (TT == 4 || TT == 5) { f32x2 a = gelu_pk((f32x2){v0[0], v0[1]}), b = gelu_pk((f32x2){v0[2], v0[3]}), c = gelu_pk((f32x2){v1[0], v1[1]}), d = gelu_pk((f32x2){v1[2], v1[3]});
;                         v0 = (f32x4){a.x, a.y, b.x, b.y}; v1 = (f32x4){c.x, c.y, d.x, d.y};
;                         if (TT == 5) { ps += ((v0[0] + v0[1]) + (v0[2] + v0[3])) + ((v1[0] + v1[1]) + (v1[2] + v1[3]));
;                             pq += ((v0[0] * v0[0] + v0[1] * v0[1]) + (v0[2] * v0[2] + v0[3] * v0[3])) + ((v1[0] * v1[0] + v1[1] * v1[1]) + (v1[2] * v1[2] + v1[3] * v1[3])); } }
;                     else if (TT >= 6) {
; #pragma unroll
;                         for (int j = 0; j < 4; ++j) { v0[j] = sigmoid_f(v0[j]); v1[j] = sigmoid_f(v1[j]); } }
;                     if (TT >= 6) { unsigned b0 = 0u, b1 = 0u;
; #pragma unroll
;                         for (int j = 0; j < 4; ++j) { b0 = __builtin_amdgcn_cvt_pk_u8_f32(__builtin_rintf(v0[j] * 255.0f), j, b0); b1 = __builtin_amdgcn_cvt_pk_u8_f32(__builtin_rintf(v1[j] * 255.0f), j, b1); }
;                         if (bj == 0) { gq.x = b0; gq.y = b1; } else { gq.z = b0; gq.w = b1; } }
	v_fma_f32 v153, v151, v153, s46
	s_nop 0
	v_mul_f32_e64 v150, v150, v152
	v_mul_f32_e64 v151, v151, v153
	v_mul_f32_e64 v152, v144, v144
	v_mul_f32_e64 v153, v145, v145
	v_mul_f32_e64 v150, v154, v150
	v_mul_f32_e64 v151, v155, v151
	s_nop 0
	v_mul_f32_e64 v154, v146, v150
	v_mul_f32_e64 v155, v147, v151
	v_fma_f32 v150, -v146, v150, v146
	v_fma_f32 v151, -v147, v151, v147
	v_and_b32_e32 v146, 0x7fffffff, v144
	v_cndmask_b32_e32 v138, v150, v154, vcc
	v_cmp_gt_f32_e32 vcc, 0, v147
	v_and_b32_e32 v147, 0x7fffffff, v145
	v_fma_f32 v146, v146, s4, 1.0
	v_fma_f32 v147, v147, s4, 1.0
	v_cndmask_b32_e32 v143, v151, v155, vcc
	v_rcp_f32_e32 v146, v146
	v_rcp_f32_e32 v147, v147
	v_cmp_gt_f32_e32 vcc, 0, v144
	v_fma_f32 v150, v146, s10, v132
	v_fma_f32 v151, v147, s10, v132
	s_nop 0
	v_fma_f32 v150, v146, v150, s12
	v_fma_f32 v151, v147, v151, s12
	s_nop 0
	v_fma_f32 v150, v146, v150, s14
	v_fma_f32 v151, v147, v151, s14
	s_nop 0
	v_fma_f32 v150, v146, v150, s46
	v_fma_f32 v151, v147, v151, s46
	s_nop 0
	v_mul_f32_e64 v146, v146, v150
	v_mul_f32_e64 v147, v147, v151
	v_mul_f32_e64 v150, v152, s48
	v_mul_f32_e64 v151, v153, s48
	s_nop 0
	v_exp_f32_e32 v150, v150
	v_exp_f32_e32 v151, v151
	s_nop 0
	v_mul_f32_e64 v146, v150, v146
	v_mul_f32_e64 v147, v151, v147
	s_nop 0
	v_mul_f32_e64 v150, v144, v146
	v_mul_f32_e64 v151, v145, v147
	v_fma_f32 v146, -v144, v146, v144
	v_fma_f32 v147, -v145, v147, v145
	v_and_b32_e32 v144, 0x7fffffff, v148
	v_cndmask_b32_e32 v152, v146, v150, vcc
	v_cmp_gt_f32_e32 vcc, 0, v145
	v_and_b32_e32 v145, 0x7fffffff, v149
	v_fma_f32 v144, v144, s4, 1.0
	v_fma_f32 v145, v145, s4, 1.0
	v_cndmask_b32_e32 v153, v147, v151, vcc
	v_rcp_f32_e32 v144, v144
	v_rcp_f32_e32 v145, v145
	v_mul_f32_e64 v150, v148, v148
	v_mul_f32_e64 v151, v149, v149
	v_cmp_gt_f32_e32 vcc, 0, v148
	v_mul_f32_e64 v150, v150, s48
	v_mul_f32_e64 v151, v151, s48
	v_fma_f32 v146, v144, s10, v132
	v_fma_f32 v147, v145, s10, v132
	v_exp_f32_e32 v150, v150
	v_fma_f32 v146, v144, v146, s12
	v_fma_f32 v147, v145, v147, s12
	v_exp_f32_e32 v151, v151
	v_fma_f32 v146, v144, v146, s14
	v_fma_f32 v147, v145, v147, s14
	s_nop 0
	v_fma_f32 v146, v144, v146, s46
	v_fma_f32 v147, v145, v147, s46
	s_nop 0
	v_mul_f32_e64 v144, v144, v146
	v_mul_f32_e64 v145, v145, v147
	v_mul_f32_e64 v146, v140, v140
	v_mul_f32_e64 v147, v141, v141
	v_mul_f32_e64 v144, v150, v144
	v_mul_f32_e64 v145, v151, v145
	v_mul_f32_e64 v146, v146, s48
	v_mul_f32_e64 v147, v147, s48
	v_mul_f32_e64 v150, v148, v144
	v_mul_f32_e64 v151, v149, v145
	v_fma_f32 v144, -v148, v144, v148
	v_fma_f32 v145, -v149, v145, v149
	v_exp_f32_e32 v146, v146
	v_cndmask_b32_e32 v150, v144, v150, vcc
	v_cmp_gt_f32_e32 vcc, 0, v149
	v_and_b32_e32 v144, 0x7fffffff, v140
	v_exp_f32_e32 v147, v147
	v_cndmask_b32_e32 v151, v145, v151, vcc
	v_and_b32_e32 v145, 0x7fffffff, v141
	v_fma_f32 v144, v144, s4, 1.0
	v_fma_f32 v145, v145, s4, 1.0
	v_cmp_gt_f32_e32 vcc, 0, v140
	v_rcp_f32_e32 v144, v144
	v_rcp_f32_e32 v145, v145
	s_nop 0
	v_fma_f32 v148, v144, s10, v132
	v_fma_f32 v149, v145, s10, v132
	s_nop 0
	v_fma_f32 v148, v144, v148, s12
	v_fma_f32 v149, v145, v149, s12
	s_nop 0
	v_fma_f32 v148, v144, v148, s14
	v_fma_f32 v149, v145, v149, s14
	s_nop 0
	v_fma_f32 v148, v144, v148, s46
	v_fma_f32 v149, v145, v149, s46
	s_nop 0
	v_mul_f32_e64 v144, v144, v148
	v_mul_f32_e64 v145, v145, v149
	s_nop 0
	v_mul_f32_e64 v144, v146, v144
	v_mul_f32_e64 v145, v147, v145
	s_nop 0
	v_mul_f32_e64 v146, v140, v144
	v_mul_f32_e64 v147, v141, v145
	v_fma_f32 v144, -v140, v144, v140
	v_fma_f32 v145, -v141, v145, v141
	s_nop 0
	v_cndmask_b32_e32 v140, v144, v146, vcc
	v_cmp_gt_f32_e32 vcc, 0, v141
	v_cvt_pk_bf16_f32 v144, v138, v143
	v_cvt_pk_bf16_f32 v146, v150, v151
	v_cndmask_b32_e32 v141, v145, v147, vcc
	v_cvt_pk_bf16_f32 v145, v152, v153
	v_cvt_pk_bf16_f32 v147, v140, v141
	v_mov_b32_e32 v138, v139
	global_store_dwordx4 v[136:137], v[144:147], off offset:256
	v_fma_f32 v140, v38, v138, 0
	v_fma_f32 v141, v39, v138, 0
	v_fma_f32 v148, v36, v138, 0
	v_fma_f32 v149, v37, v138, 0
	v_fma_f32 v146, v40, v138, 0
	v_fma_f32 v147, v41, v138, 0
	v_fma_f32 v144, v42, v138, 0
	v_fma_f32 v145, v43, v138, 0
	v_and_b32_e32 v151, 0x7fffffff, v147
	v_and_b32_e32 v150, 0x7fffffff, v146
	v_fma_f32 v150, v150, s4, 1.0
	v_fma_f32 v151, v151, s4, 1.0
	v_mul_f32_e64 v154, v146, v146
	v_mul_f32_e64 v155, v147, v147
	v_rcp_f32_e32 v150, v150
	v_rcp_f32_e32 v151, v151
	v_mul_f32_e64 v154, v154, s48
	v_mul_f32_e64 v155, v155, s48
	v_cmp_gt_f32_e32 vcc, 0, v146
	v_exp_f32_e32 v154, v154
	v_fma_f32 v152, v150, s10, v132
	v_fma_f32 v153, v151, s10, v132
	v_exp_f32_e32 v155, v155
	v_fma_f32 v152, v150, v152, s12
	v_fma_f32 v153, v151, v153, s12
	v_add_u32_e32 v136, 0x90, v142
	v_fma_f32 v152, v150, v152, s14
	v_fma_f32 v153, v151, v153, s14
	v_mad_i64_i32 v[136:137], s[2:3], v136, s81, v[134:135]
	v_fma_f32 v152, v150, v152, s46
	v_fma_f32 v153, v151, v153, s46
	s_nop 0
	v_mul_f32_e64 v150, v150, v152
	v_mul_f32_e64 v151, v151, v153
	v_mul_f32_e64 v152, v144, v144
	v_mul_f32_e64 v153, v145, v145
	v_mul_f32_e64 v150, v154, v150
	v_mul_f32_e64 v151, v155, v151
	s_nop 0
	v_mul_f32_e64 v154, v146, v150
	v_mul_f32_e64 v155, v147, v151
	v_fma_f32 v150, -v146, v150, v146
	v_fma_f32 v151, -v147, v151, v147
	v_and_b32_e32 v146, 0x7fffffff, v144
	v_cndmask_b32_e32 v139, v150, v154, vcc
	v_cmp_gt_f32_e32 vcc, 0, v147
	v_and_b32_e32 v147, 0x7fffffff, v145
	v_fma_f32 v146, v146, s4, 1.0
	v_fma_f32 v147, v147, s4, 1.0
	v_cndmask_b32_e32 v143, v151, v155, vcc
	v_rcp_f32_e32 v146, v146
	v_rcp_f32_e32 v147, v147
	v_cmp_gt_f32_e32 vcc, 0, v144
	v_fma_f32 v150, v146, s10, v132
; __device__ __forceinline__ float silu_f(float g) { return g * __builtin_amdgcn_rcpf(1.0f + __builtin_amdgcn_exp2f(-1.44269504f * g)); }
; __device__ __forceinline__ f32x2 gelu_pk(f32x2 v) {
;     const f32x2 av = __builtin_elementwise_abs(v), d = av * 0.2316418882f + 1.0f;
;     f32x2 t; t.x = __builtin_amdgcn_rcpf(d.x); t.y = __builtin_amdgcn_rcpf(d.y);
;     f32x2 q = t * 0.5307027145f + (-0.7265760135f); q = q * t + 0.7107068705f; q = q * t + (-0.142248368f); q = q * t + 0.127414796f; q = q * t;
;     const f32x2 s = (v * v) * (-0.72134752044f);
;     f32x2 e; e.x = __builtin_amdgcn_exp2f(s.x); e.y = __builtin_amdgcn_exp2f(s.y);
;     const f32x2 m = v * (q * e), r = v - m;
;     f32x2 o; o.x = v.x < 0.f ? m.x : r.x; o.y = v.y < 0.f ? m.y : r.y; return o;
; }
;     template <int TT> __device__ __forceinline__ void other(const f32x4 (&acc)[2][2][4][2], bf16_t* base, int row0, int col0, PG8_LAS float* my, int t, int hh, int wc, int fq) const {
;     ...
;             for (int m = 0; m < 4; ++m) { bf16_t* rowp = base + (size_t)(row0 + ai * HALF + m * 16) * LDT + col0;
;                 const float rs = my[(ai * 4 + m) * 16]; float ps = 0.f, pq = 0.f; u32x4 gq = {0u, 0u, 0u, 0u};
; #pragma unroll
;                 for (int bj = 0; bj < 2; ++bj) { f32x4 v0 = acc[ai][bj][m][0] * rs + bv[bj][0], v1 = acc[ai][bj][m][1] * rs + bv[bj][1];
;                     if (TT == 3) {
; #pragma unroll
;                         for (int j = 0; j < 4; ++j) { v0[j] = silu_f(v0[j]); v1[j] = silu_f(v1[j]); } }
;                     else if (TT == 4 || TT == 5) { f32x2 a = gelu_pk((f32x2){v0[0], v0[1]}), b = gelu_pk((f32x2){v0[2], v0[3]}), c = gelu_pk((f32x2){v1[0], v1[1]}), d = gelu_pk((f32x2){v1[2], v1[3]});
;                         v0 = (f32x4){a.x, a.y, b.x, b.y}; v1 = (f32x4){c.x, c.y, d.x, d.y};
;                         if (TT == 5) { ps += ((v0[0] + v0[1]) + (v0[2] + v0[3])) + ((v1[0] + v1[1]) + (v1[2] + v1[3]));
;                             pq += ((v0[0] * v0[0] + v0[1] * v0[1]) + (v0[2] * v0[2] + v0[3] * v0[3])) + ((v1[0] * v1[0] + v1[1] * v1[1]) + (v1[2] * v1[2] + v1[3] * v1[3])); } }
;                     else if (TT >= 6) {
; #pragma unroll
;                         for (int j = 0; j < 4; ++j) { v0[j] = sigmoid_f(v0[j]); v1[j] = sigmoid_f(v1[j]); } }
;                     if (TT >= 6) { unsigned b0 = 0u, b1 = 0u;
; #pragma unroll
	v_fma_f32 v151, v147, s10, v132
	s_nop 0
	v_fma_f32 v150, v146, v150, s12
	v_fma_f32 v151, v147, v151, s12
	s_nop 0
	v_fma_f32 v150, v146, v150, s14
	v_fma_f32 v151, v147, v151, s14
	s_nop 0
	v_fma_f32 v150, v146, v150, s46
	v_fma_f32 v151, v147, v151, s46
	s_nop 0
	v_mul_f32_e64 v146, v146, v150
	v_mul_f32_e64 v147, v147, v151
	v_mul_f32_e64 v150, v152, s48
	v_mul_f32_e64 v151, v153, s48
	s_nop 0
	v_exp_f32_e32 v150, v150
	v_exp_f32_e32 v151, v151
	s_nop 0
	v_mul_f32_e64 v146, v150, v146
	v_mul_f32_e64 v147, v151, v147
	s_nop 0
	v_mul_f32_e64 v150, v144, v146
	v_mul_f32_e64 v151, v145, v147
	v_fma_f32 v146, -v144, v146, v144
	v_fma_f32 v147, -v145, v147, v145
	v_and_b32_e32 v144, 0x7fffffff, v148
	v_cndmask_b32_e32 v152, v146, v150, vcc
	v_cmp_gt_f32_e32 vcc, 0, v145
	v_and_b32_e32 v145, 0x7fffffff, v149
	v_fma_f32 v144, v144, s4, 1.0
	v_fma_f32 v145, v145, s4, 1.0
	v_cndmask_b32_e32 v153, v147, v151, vcc
	v_rcp_f32_e32 v144, v144
	v_rcp_f32_e32 v145, v145
	v_mul_f32_e64 v150, v148, v148
	v_mul_f32_e64 v151, v149, v149
	v_cmp_gt_f32_e32 vcc, 0, v148
	v_mul_f32_e64 v150, v150, s48
	v_mul_f32_e64 v151, v151, s48
	v_fma_f32 v146, v144, s10, v132
	v_fma_f32 v147, v145, s10, v132
	v_exp_f32_e32 v150, v150
	v_fma_f32 v146, v144, v146, s12
	v_fma_f32 v147, v145, v147, s12
	v_exp_f32_e32 v151, v151
	v_fma_f32 v146, v144, v146, s14
	v_fma_f32 v147, v145, v147, s14
	s_nop 0
	v_fma_f32 v146, v144, v146, s46
	v_fma_f32 v147, v145, v147, s46
	s_nop 0
	v_mul_f32_e64 v144, v144, v146
	v_mul_f32_e64 v145, v145, v147
	v_mul_f32_e64 v146, v140, v140
	v_mul_f32_e64 v147, v141, v141
	v_mul_f32_e64 v144, v150, v144
	v_mul_f32_e64 v145, v151, v145
	v_mul_f32_e64 v146, v146, s48
	v_mul_f32_e64 v147, v147, s48
	v_mul_f32_e64 v150, v148, v144
	v_mul_f32_e64 v151, v149, v145
	v_fma_f32 v144, -v148, v144, v148
	v_fma_f32 v145, -v149, v145, v149
	v_exp_f32_e32 v146, v146
	v_cndmask_b32_e32 v150, v144, v150, vcc
	v_cmp_gt_f32_e32 vcc, 0, v149
	v_and_b32_e32 v144, 0x7fffffff, v140
	v_exp_f32_e32 v147, v147
	v_cndmask_b32_e32 v151, v145, v151, vcc
	v_and_b32_e32 v145, 0x7fffffff, v141
	v_fma_f32 v144, v144, s4, 1.0
	v_fma_f32 v145, v145, s4, 1.0
	v_cmp_gt_f32_e32 vcc, 0, v140
	v_rcp_f32_e32 v144, v144
	v_rcp_f32_e32 v145, v145
	s_nop 0
	v_fma_f32 v148, v144, s10, v132
	v_fma_f32 v149, v145, s10, v132
	s_nop 0
	v_fma_f32 v148, v144, v148, s12
	v_fma_f32 v149, v145, v149, s12
	s_nop 0
	v_fma_f32 v148, v144, v148, s14
	v_fma_f32 v149, v145, v149, s14
	s_nop 0
	v_fma_f32 v148, v144, v148, s46
	v_fma_f32 v149, v145, v149, s46
	s_nop 0
	v_mul_f32_e64 v144, v144, v148
	v_mul_f32_e64 v145, v145, v149
	s_nop 0
	v_mul_f32_e64 v144, v146, v144
	v_mul_f32_e64 v145, v147, v145
	s_nop 0
	v_mul_f32_e64 v146, v140, v144
	v_mul_f32_e64 v147, v141, v145
	v_fma_f32 v144, -v140, v144, v140
	v_fma_f32 v145, -v141, v145, v141
	s_nop 0
	v_cndmask_b32_e32 v140, v144, v146, vcc
	v_cmp_gt_f32_e32 vcc, 0, v141
	v_cvt_pk_bf16_f32 v144, v139, v143
	v_cvt_pk_bf16_f32 v146, v150, v151
	v_cndmask_b32_e32 v141, v145, v147, vcc
	v_cvt_pk_bf16_f32 v145, v152, v153
	v_cvt_pk_bf16_f32 v147, v140, v141
	global_store_dwordx4 v[136:137], v[144:147], off
	v_fma_f32 v140, v46, v138, 0
	v_fma_f32 v141, v47, v138, 0
	s_nop 0
	v_fma_f32 v146, v48, v138, 0
	v_fma_f32 v147, v49, v138, 0
	v_fma_f32 v144, v50, v138, 0
	v_fma_f32 v145, v51, v138, 0
	v_and_b32_e32 v149, 0x7fffffff, v147
	v_and_b32_e32 v148, 0x7fffffff, v146
	v_fma_f32 v148, v148, s4, 1.0
	v_fma_f32 v149, v149, s4, 1.0
	v_mul_f32_e64 v152, v146, v146
	v_mul_f32_e64 v153, v147, v147
	v_rcp_f32_e32 v148, v148
	v_rcp_f32_e32 v149, v149
	v_mul_f32_e64 v152, v152, s48
	v_mul_f32_e64 v153, v153, s48
	v_cmp_gt_f32_e32 vcc, 0, v146
	v_exp_f32_e32 v152, v152
	v_fma_f32 v150, v148, s10, v132
	v_fma_f32 v151, v149, s10, v132
	v_exp_f32_e32 v153, v153
	v_fma_f32 v150, v148, v150, s12
	v_fma_f32 v151, v149, v151, s12
	v_fma_f32 v139, v45, v138, 0
	v_fma_f32 v138, v44, v138, 0
	v_fma_f32 v150, v148, v150, s14
	v_fma_f32 v151, v149, v151, s14
	s_nop 0
	v_fma_f32 v150, v148, v150, s46
	v_fma_f32 v151, v149, v151, s46
	s_nop 0
	v_mul_f32_e64 v148, v148, v150
	v_mul_f32_e64 v149, v149, v151
	v_mul_f32_e64 v150, v144, v144
	v_mul_f32_e64 v151, v145, v145
	v_mul_f32_e64 v148, v152, v148
	v_mul_f32_e64 v149, v153, v149
	s_nop 0
	v_mul_f32_e64 v152, v146, v148
	v_mul_f32_e64 v153, v147, v149
	v_fma_f32 v148, -v146, v148, v146
	v_fma_f32 v149, -v147, v149, v147
	v_and_b32_e32 v146, 0x7fffffff, v144
	v_cndmask_b32_e32 v143, v148, v152, vcc
	v_cmp_gt_f32_e32 vcc, 0, v147
	v_and_b32_e32 v147, 0x7fffffff, v145
	v_fma_f32 v146, v146, s4, 1.0
	v_fma_f32 v147, v147, s4, 1.0
	v_cndmask_b32_e32 v152, v149, v153, vcc
	v_rcp_f32_e32 v146, v146
	v_rcp_f32_e32 v147, v147
	v_cmp_gt_f32_e32 vcc, 0, v144
	v_fma_f32 v148, v146, s10, v132
	v_fma_f32 v149, v147, s10, v132
	s_nop 0
	v_fma_f32 v148, v146, v148, s12
	v_fma_f32 v149, v147, v149, s12
	s_nop 0
	v_fma_f32 v148, v146, v148, s14
	v_fma_f32 v149, v147, v149, s14
	s_nop 0
	v_fma_f32 v148, v146, v148, s46
	v_fma_f32 v149, v147, v149, s46
	s_nop 0
	v_mul_f32_e64 v146, v146, v148
	v_mul_f32_e64 v147, v147, v149
	v_mul_f32_e64 v148, v150, s48
	v_mul_f32_e64 v149, v151, s48
	s_nop 0
	v_exp_f32_e32 v148, v148
	v_exp_f32_e32 v149, v149
	s_nop 0
	v_mul_f32_e64 v146, v148, v146
	v_mul_f32_e64 v147, v149, v147
	s_nop 0
	v_mul_f32_e64 v148, v144, v146
	v_mul_f32_e64 v149, v145, v147
	v_fma_f32 v146, -v144, v146, v144
	v_fma_f32 v147, -v145, v147, v145
	v_and_b32_e32 v144, 0x7fffffff, v138
	v_cndmask_b32_e32 v150, v146, v148, vcc
	v_cmp_gt_f32_e32 vcc, 0, v145
	v_and_b32_e32 v145, 0x7fffffff, v139
	v_fma_f32 v144, v144, s4, 1.0
	v_fma_f32 v145, v145, s4, 1.0
; __device__ __forceinline__ float silu_f(float g) { return g * __builtin_amdgcn_rcpf(1.0f + __builtin_amdgcn_exp2f(-1.44269504f * g)); }
; __device__ __forceinline__ f32x2 gelu_pk(f32x2 v) {
;     const f32x2 av = __builtin_elementwise_abs(v), d = av * 0.2316418882f + 1.0f;
;     f32x2 t; t.x = __builtin_amdgcn_rcpf(d.x); t.y = __builtin_amdgcn_rcpf(d.y);
;     f32x2 q = t * 0.5307027145f + (-0.7265760135f); q = q * t + 0.7107068705f; q = q * t + (-0.142248368f); q = q * t + 0.127414796f; q = q * t;
;     const f32x2 s = (v * v) * (-0.72134752044f);
;     f32x2 e; e.x = __builtin_amdgcn_exp2f(s.x); e.y = __builtin_amdgcn_exp2f(s.y);
;     const f32x2 m = v * (q * e), r = v - m;
;     f32x2 o; o.x = v.x < 0.f ? m.x : r.x; o.y = v.y < 0.f ? m.y : r.y; return o;
; }
;     template <int TT> __device__ __forceinline__ void other(const f32x4 (&acc)[2][2][4][2], bf16_t* base, int row0, int col0, PG8_LAS float* my, int t, int hh, int wc, int fq) const {
;     ...
;             for (int m = 0; m < 4; ++m) { bf16_t* rowp = base + (size_t)(row0 + ai * HALF + m * 16) * LDT + col0;
;                 const float rs = my[(ai * 4 + m) * 16]; float ps = 0.f, pq = 0.f; u32x4 gq = {0u, 0u, 0u, 0u};
; #pragma unroll
;                 for (int bj = 0; bj < 2; ++bj) { f32x4 v0 = acc[ai][bj][m][0] * rs + bv[bj][0], v1 = acc[ai][bj][m][1] * rs + bv[bj][1];
;                     if (TT == 3) {
; #pragma unroll
;                         for (int j = 0; j < 4; ++j) { v0[j] = silu_f(v0[j]); v1[j] = silu_f(v1[j]); } }
;                     else if (TT == 4 || TT == 5) { f32x2 a = gelu_pk((f32x2){v0[0], v0[1]}), b = gelu_pk((f32x2){v0[2], v0[3]}), c = gelu_pk((f32x2){v1[0], v1[1]}), d = gelu_pk((f32x2){v1[2], v1[3]});
;                         v0 = (f32x4){a.x, a.y, b.x, b.y}; v1 = (f32x4){c.x, c.y, d.x, d.y};
;                         if (TT == 5) { ps += ((v0[0] + v0[1]) + (v0[2] + v0[3])) + ((v1[0] + v1[1]) + (v1[2] + v1[3]));
;                             pq += ((v0[0] * v0[0] + v0[1] * v0[1]) + (v0[2] * v0[2] + v0[3] * v0[3])) + ((v1[0] * v1[0] + v1[1] * v1[1]) + (v1[2] * v1[2] + v1[3] * v1[3])); } }
;                     else if (TT >= 6) {
; #pragma unroll
;                         for (int j = 0; j < 4; ++j) { v0[j] = sigmoid_f(v0[j]); v1[j] = sigmoid_f(v1[j]); } }
;                     if (TT >= 6) { unsigned b0 = 0u, b1 = 0u;
; #pragma unroll
	v_cndmask_b32_e32 v151, v147, v149, vcc
	v_rcp_f32_e32 v144, v144
	v_rcp_f32_e32 v145, v145
	v_mul_f32_e64 v148, v138, v138
	v_mul_f32_e64 v149, v139, v139
	v_cmp_gt_f32_e32 vcc, 0, v138
	v_mul_f32_e64 v148, v148, s48
	v_mul_f32_e64 v149, v149, s48
	v_fma_f32 v146, v144, s10, v132
	v_fma_f32 v147, v145, s10, v132
	v_exp_f32_e32 v148, v148
	v_fma_f32 v146, v144, v146, s12
	v_fma_f32 v147, v145, v147, s12
	v_exp_f32_e32 v149, v149
	v_fma_f32 v146, v144, v146, s14
	v_fma_f32 v147, v145, v147, s14
	s_nop 0
	v_fma_f32 v146, v144, v146, s46
	v_fma_f32 v147, v145, v147, s46
	s_nop 0
	v_mul_f32_e64 v144, v144, v146
	v_mul_f32_e64 v145, v145, v147
	v_mul_f32_e64 v146, v140, v140
	v_mul_f32_e64 v147, v141, v141
	v_mul_f32_e64 v144, v148, v144
	v_mul_f32_e64 v145, v149, v145
	s_nop 0
	v_mul_f32_e64 v148, v138, v144
	v_mul_f32_e64 v149, v139, v145
	v_fma_f32 v144, -v138, v144, v138
	v_fma_f32 v145, -v139, v145, v139
	v_and_b32_e32 v138, 0x7fffffff, v140
	v_cndmask_b32_e32 v148, v144, v148, vcc
	v_cmp_gt_f32_e32 vcc, 0, v139
	v_and_b32_e32 v139, 0x7fffffff, v141
	v_fma_f32 v138, v138, s4, 1.0
	v_fma_f32 v139, v139, s4, 1.0
	v_cndmask_b32_e32 v149, v145, v149, vcc
	v_rcp_f32_e32 v138, v138
	v_rcp_f32_e32 v139, v139
	v_cmp_gt_f32_e32 vcc, 0, v140
	v_fma_f32 v144, v138, s10, v132
	v_fma_f32 v145, v139, s10, v132
	s_nop 0
	v_fma_f32 v144, v138, v144, s12
	v_fma_f32 v145, v139, v145, s12
	s_nop 0
	v_fma_f32 v144, v138, v144, s14
	v_fma_f32 v145, v139, v145, s14
	s_nop 0
	v_fma_f32 v144, v138, v144, s46
	v_fma_f32 v145, v139, v145, s46
	s_nop 0
	v_mul_f32_e64 v138, v138, v144
	v_mul_f32_e64 v139, v139, v145
	v_mul_f32_e64 v144, v146, s48
	v_mul_f32_e64 v145, v147, s48
	s_nop 0
	v_exp_f32_e32 v144, v144
	v_exp_f32_e32 v145, v145
	s_nop 0
	v_mul_f32_e64 v138, v144, v138
	v_mul_f32_e64 v139, v145, v139
	s_nop 0
	v_mul_f32_e64 v144, v140, v138
	v_mul_f32_e64 v145, v141, v139
	v_fma_f32 v138, -v140, v138, v140
	v_fma_f32 v139, -v141, v139, v141
	v_cvt_pk_bf16_f32 v140, v148, v149
	v_cndmask_b32_e32 v144, v138, v144, vcc
	v_cmp_gt_f32_e32 vcc, 0, v141
	v_cvt_pk_bf16_f32 v138, v143, v152
	s_nop 0
	v_cndmask_b32_e32 v141, v139, v145, vcc
	v_cvt_pk_bf16_f32 v139, v150, v151
	v_cvt_pk_bf16_f32 v141, v144, v141
	global_store_dwordx4 v[136:137], v[138:141], off offset:256
	ds_read2_b32 v[138:139], v199 offset0:96 offset1:112
	v_add_u32_e32 v136, 0xa0, v142
	v_mad_i64_i32 v[136:137], s[2:3], v136, s81, v[134:135]
	s_waitcnt lgkmcnt(0)
	v_fma_f32 v146, v24, v138, 0
	v_fma_f32 v147, v25, v138, 0
	s_nop 0
	v_and_b32_e32 v151, 0x7fffffff, v147
	v_and_b32_e32 v150, 0x7fffffff, v146
	v_fma_f32 v150, v150, s4, 1.0
	v_fma_f32 v151, v151, s4, 1.0
	v_mul_f32_e64 v154, v146, v146
	v_mul_f32_e64 v155, v147, v147
	v_rcp_f32_e32 v150, v150
	v_rcp_f32_e32 v151, v151
	v_mul_f32_e64 v154, v154, s48
	v_mul_f32_e64 v155, v155, s48
	v_fma_f32 v144, v26, v138, 0
	v_fma_f32 v145, v27, v138, 0
	v_exp_f32_e32 v154, v154
	v_fma_f32 v152, v150, s10, v132
	v_fma_f32 v153, v151, s10, v132
	v_exp_f32_e32 v155, v155
	v_fma_f32 v152, v150, v152, s12
	v_fma_f32 v153, v151, v153, s12
	v_cmp_gt_f32_e32 vcc, 0, v146
	v_fma_f32 v152, v150, v152, s14
	v_fma_f32 v153, v151, v153, s14
	v_fma_f32 v148, v20, v138, 0
	v_fma_f32 v149, v21, v138, 0
	v_fma_f32 v152, v150, v152, s46
	v_fma_f32 v153, v151, v153, s46
	v_fma_f32 v140, v22, v138, 0
	v_fma_f32 v141, v23, v138, 0
	v_mul_f32_e64 v150, v150, v152
	v_mul_f32_e64 v151, v151, v153
	v_mul_f32_e64 v152, v144, v144
	v_mul_f32_e64 v153, v145, v145
	v_mul_f32_e64 v150, v154, v150
	v_mul_f32_e64 v151, v155, v151
	s_nop 0
	v_mul_f32_e64 v154, v146, v150
	v_mul_f32_e64 v155, v147, v151
	v_fma_f32 v150, -v146, v150, v146
	v_fma_f32 v151, -v147, v151, v147
	v_and_b32_e32 v146, 0x7fffffff, v144
	v_cndmask_b32_e32 v143, v150, v154, vcc
	v_cmp_gt_f32_e32 vcc, 0, v147
	v_and_b32_e32 v147, 0x7fffffff, v145
	v_fma_f32 v146, v146, s4, 1.0
	v_fma_f32 v147, v147, s4, 1.0
	v_cndmask_b32_e32 v154, v151, v155, vcc
	v_rcp_f32_e32 v146, v146
	v_rcp_f32_e32 v147, v147
	v_cmp_gt_f32_e32 vcc, 0, v144
	v_fma_f32 v150, v146, s10, v132
	v_fma_f32 v151, v147, s10, v132
	s_nop 0
	v_fma_f32 v150, v146, v150, s12
	v_fma_f32 v151, v147, v151, s12
	s_nop 0
	v_fma_f32 v150, v146, v150, s14
	v_fma_f32 v151, v147, v151, s14
	s_nop 0
	v_fma_f32 v150, v146, v150, s46
	v_fma_f32 v151, v147, v151, s46
	s_nop 0
	v_mul_f32_e64 v146, v146, v150
	v_mul_f32_e64 v147, v147, v151
	v_mul_f32_e64 v150, v152, s48
	v_mul_f32_e64 v151, v153, s48
	s_nop 0
	v_exp_f32_e32 v150, v150
	v_exp_f32_e32 v151, v151
	s_nop 0
	v_mul_f32_e64 v146, v150, v146
	v_mul_f32_e64 v147, v151, v147
	s_nop 0
	v_mul_f32_e64 v150, v144, v146
	v_mul_f32_e64 v151, v145, v147
	v_fma_f32 v146, -v144, v146, v144
	v_fma_f32 v147, -v145, v147, v145
	v_and_b32_e32 v144, 0x7fffffff, v148
	v_cndmask_b32_e32 v152, v146, v150, vcc
	v_cmp_gt_f32_e32 vcc, 0, v145
	v_and_b32_e32 v145, 0x7fffffff, v149
	v_fma_f32 v144, v144, s4, 1.0
	v_fma_f32 v145, v145, s4, 1.0
	v_cndmask_b32_e32 v153, v147, v151, vcc
	v_rcp_f32_e32 v144, v144
	v_rcp_f32_e32 v145, v145
	v_mul_f32_e64 v150, v148, v148
	v_mul_f32_e64 v151, v149, v149
	v_cmp_gt_f32_e32 vcc, 0, v148
	v_mul_f32_e64 v150, v150, s48
	v_mul_f32_e64 v151, v151, s48
	v_fma_f32 v146, v144, s10, v132
	v_fma_f32 v147, v145, s10, v132
	v_exp_f32_e32 v150, v150
	v_fma_f32 v146, v144, v146, s12
	v_fma_f32 v147, v145, v147, s12
	v_exp_f32_e32 v151, v151
	v_fma_f32 v146, v144, v146, s14
	v_fma_f32 v147, v145, v147, s14
	s_nop 0
	v_fma_f32 v146, v144, v146, s46
	v_fma_f32 v147, v145, v147, s46
	s_nop 0
	v_mul_f32_e64 v144, v144, v146
	v_mul_f32_e64 v145, v145, v147
	v_mul_f32_e64 v146, v140, v140
	v_mul_f32_e64 v147, v141, v141
; __device__ __forceinline__ float silu_f(float g) { return g * __builtin_amdgcn_rcpf(1.0f + __builtin_amdgcn_exp2f(-1.44269504f * g)); }
; __device__ __forceinline__ f32x2 gelu_pk(f32x2 v) {
;     const f32x2 av = __builtin_elementwise_abs(v), d = av * 0.2316418882f + 1.0f;
;     f32x2 t; t.x = __builtin_amdgcn_rcpf(d.x); t.y = __builtin_amdgcn_rcpf(d.y);
;     f32x2 q = t * 0.5307027145f + (-0.7265760135f); q = q * t + 0.7107068705f; q = q * t + (-0.142248368f); q = q * t + 0.127414796f; q = q * t;
;     const f32x2 s = (v * v) * (-0.72134752044f);
;     f32x2 e; e.x = __builtin_amdgcn_exp2f(s.x); e.y = __builtin_amdgcn_exp2f(s.y);
;     const f32x2 m = v * (q * e), r = v - m;
;     f32x2 o; o.x = v.x < 0.f ? m.x : r.x; o.y = v.y < 0.f ? m.y : r.y; return o;
; }
;     template <int TT> __device__ __forceinline__ void other(const f32x4 (&acc)[2][2][4][2], bf16_t* base, int row0, int col0, PG8_LAS float* my, int t, int hh, int wc, int fq) const {
;     ...
;             for (int m = 0; m < 4; ++m) { bf16_t* rowp = base + (size_t)(row0 + ai * HALF + m * 16) * LDT + col0;
;                 const float rs = my[(ai * 4 + m) * 16]; float ps = 0.f, pq = 0.f; u32x4 gq = {0u, 0u, 0u, 0u};
; #pragma unroll
;                 for (int bj = 0; bj < 2; ++bj) { f32x4 v0 = acc[ai][bj][m][0] * rs + bv[bj][0], v1 = acc[ai][bj][m][1] * rs + bv[bj][1];
;                     if (TT == 3) {
; #pragma unroll
;                         for (int j = 0; j < 4; ++j) { v0[j] = silu_f(v0[j]); v1[j] = silu_f(v1[j]); } }
;                     else if (TT == 4 || TT == 5) { f32x2 a = gelu_pk((f32x2){v0[0], v0[1]}), b = gelu_pk((f32x2){v0[2], v0[3]}), c = gelu_pk((f32x2){v1[0], v1[1]}), d = gelu_pk((f32x2){v1[2], v1[3]});
;                         v0 = (f32x4){a.x, a.y, b.x, b.y}; v1 = (f32x4){c.x, c.y, d.x, d.y};
;                         if (TT == 5) { ps += ((v0[0] + v0[1]) + (v0[2] + v0[3])) + ((v1[0] + v1[1]) + (v1[2] + v1[3]));
;                             pq += ((v0[0] * v0[0] + v0[1] * v0[1]) + (v0[2] * v0[2] + v0[3] * v0[3])) + ((v1[0] * v1[0] + v1[1] * v1[1]) + (v1[2] * v1[2] + v1[3] * v1[3])); } }
;                     else if (TT >= 6) {
; #pragma unroll
;                         for (int j = 0; j < 4; ++j) { v0[j] = sigmoid_f(v0[j]); v1[j] = sigmoid_f(v1[j]); } }
;                     if (TT >= 6) { unsigned b0 = 0u, b1 = 0u;
; #pragma unroll
	v_mul_f32_e64 v144, v150, v144
	v_mul_f32_e64 v145, v151, v145
	v_mul_f32_e64 v146, v146, s48
	v_mul_f32_e64 v147, v147, s48
	v_mul_f32_e64 v150, v148, v144
	v_mul_f32_e64 v151, v149, v145
	v_fma_f32 v144, -v148, v144, v148
	v_fma_f32 v145, -v149, v145, v149
	v_exp_f32_e32 v146, v146
	v_cndmask_b32_e32 v150, v144, v150, vcc
	v_cmp_gt_f32_e32 vcc, 0, v149
	v_and_b32_e32 v144, 0x7fffffff, v140
	v_exp_f32_e32 v147, v147
	v_cndmask_b32_e32 v151, v145, v151, vcc
	v_and_b32_e32 v145, 0x7fffffff, v141
	v_fma_f32 v144, v144, s4, 1.0
	v_fma_f32 v145, v145, s4, 1.0
	v_cmp_gt_f32_e32 vcc, 0, v140
	v_rcp_f32_e32 v144, v144
	v_rcp_f32_e32 v145, v145
	s_nop 0
	v_fma_f32 v148, v144, s10, v132
	v_fma_f32 v149, v145, s10, v132
	s_nop 0
	v_fma_f32 v148, v144, v148, s12
	v_fma_f32 v149, v145, v149, s12
	s_nop 0
	v_fma_f32 v148, v144, v148, s14
	v_fma_f32 v149, v145, v149, s14
	s_nop 0
	v_fma_f32 v148, v144, v148, s46
	v_fma_f32 v149, v145, v149, s46
	s_nop 0
	v_mul_f32_e64 v144, v144, v148
	v_mul_f32_e64 v145, v145, v149
	v_fma_f32 v148, v28, v138, 0
	v_fma_f32 v149, v29, v138, 0
	v_mul_f32_e64 v144, v146, v144
	v_mul_f32_e64 v145, v147, v145
	s_nop 0
	v_mul_f32_e64 v146, v140, v144
	v_mul_f32_e64 v147, v141, v145
	v_fma_f32 v144, -v140, v144, v140
	v_fma_f32 v145, -v141, v145, v141
	s_nop 0
	v_cndmask_b32_e32 v140, v144, v146, vcc
	v_cmp_gt_f32_e32 vcc, 0, v141
	v_cvt_pk_bf16_f32 v144, v143, v154
	v_cvt_pk_bf16_f32 v146, v150, v151
	v_cndmask_b32_e32 v141, v145, v147, vcc
	v_cvt_pk_bf16_f32 v145, v152, v153
	v_cvt_pk_bf16_f32 v147, v140, v141
	global_store_dwordx4 v[136:137], v[144:147], off
	v_fma_f32 v140, v30, v138, 0
	v_fma_f32 v141, v31, v138, 0
	s_nop 0
	v_fma_f32 v146, v32, v138, 0
	v_fma_f32 v147, v33, v138, 0
	v_fma_f32 v144, v34, v138, 0
	v_fma_f32 v145, v35, v138, 0
	v_and_b32_e32 v151, 0x7fffffff, v147
	v_and_b32_e32 v150, 0x7fffffff, v146
	v_fma_f32 v150, v150, s4, 1.0
	v_fma_f32 v151, v151, s4, 1.0
	v_mul_f32_e64 v154, v146, v146
	v_mul_f32_e64 v155, v147, v147
	v_rcp_f32_e32 v150, v150
	v_rcp_f32_e32 v151, v151
	v_mul_f32_e64 v154, v154, s48
	v_mul_f32_e64 v155, v155, s48
	v_cmp_gt_f32_e32 vcc, 0, v146
	v_exp_f32_e32 v154, v154
	v_fma_f32 v152, v150, s10, v132
	v_fma_f32 v153, v151, s10, v132
	v_exp_f32_e32 v155, v155
	v_fma_f32 v152, v150, v152, s12
	v_fma_f32 v153, v151, v153, s12
	s_nop 0
	v_fma_f32 v152, v150, v152, s14
	v_fma_f32 v153, v151, v153, s14
	s_nop 0
	v_fma_f32 v152, v150, v152, s46
	v_fma_f32 v153, v151, v153, s46
	s_nop 0
	v_mul_f32_e64 v150, v150, v152
	v_mul_f32_e64 v151, v151, v153
	v_mul_f32_e64 v152, v144, v144
	v_mul_f32_e64 v153, v145, v145
	v_mul_f32_e64 v150, v154, v150
	v_mul_f32_e64 v151, v155, v151
	s_nop 0
	v_mul_f32_e64 v154, v146, v150
	v_mul_f32_e64 v155, v147, v151
	v_fma_f32 v150, -v146, v150, v146
	v_fma_f32 v151, -v147, v151, v147
	v_and_b32_e32 v146, 0x7fffffff, v144
	v_cndmask_b32_e32 v138, v150, v154, vcc
	v_cmp_gt_f32_e32 vcc, 0, v147
	v_and_b32_e32 v147, 0x7fffffff, v145
	v_fma_f32 v146, v146, s4, 1.0
	v_fma_f32 v147, v147, s4, 1.0
	v_cndmask_b32_e32 v143, v151, v155, vcc
	v_rcp_f32_e32 v146, v146
	v_rcp_f32_e32 v147, v147
	v_cmp_gt_f32_e32 vcc, 0, v144
	v_fma_f32 v150, v146, s10, v132
	v_fma_f32 v151, v147, s10, v132
	s_nop 0
	v_fma_f32 v150, v146, v150, s12
	v_fma_f32 v151, v147, v151, s12
	s_nop 0
	v_fma_f32 v150, v146, v150, s14
	v_fma_f32 v151, v147, v151, s14
	s_nop 0
	v_fma_f32 v150, v146, v150, s46
	v_fma_f32 v151, v147, v151, s46
	s_nop 0
	v_mul_f32_e64 v146, v146, v150
	v_mul_f32_e64 v147, v147, v151
	v_mul_f32_e64 v150, v152, s48
	v_mul_f32_e64 v151, v153, s48
	s_nop 0
	v_exp_f32_e32 v150, v150
	v_exp_f32_e32 v151, v151
	s_nop 0
	v_mul_f32_e64 v146, v150, v146
	v_mul_f32_e64 v147, v151, v147
	s_nop 0
	v_mul_f32_e64 v150, v144, v146
	v_mul_f32_e64 v151, v145, v147
	v_fma_f32 v146, -v144, v146, v144
	v_fma_f32 v147, -v145, v147, v145
	v_and_b32_e32 v144, 0x7fffffff, v148
	v_cndmask_b32_e32 v152, v146, v150, vcc
	v_cmp_gt_f32_e32 vcc, 0, v145
	v_and_b32_e32 v145, 0x7fffffff, v149
	v_fma_f32 v144, v144, s4, 1.0
	v_fma_f32 v145, v145, s4, 1.0
	v_cndmask_b32_e32 v153, v147, v151, vcc
	v_rcp_f32_e32 v144, v144
	v_rcp_f32_e32 v145, v145
	v_mul_f32_e64 v150, v148, v148
	v_mul_f32_e64 v151, v149, v149
	v_cmp_gt_f32_e32 vcc, 0, v148
	v_mul_f32_e64 v150, v150, s48
	v_mul_f32_e64 v151, v151, s48
	v_fma_f32 v146, v144, s10, v132
	v_fma_f32 v147, v145, s10, v132
	v_exp_f32_e32 v150, v150
	v_fma_f32 v146, v144, v146, s12
	v_fma_f32 v147, v145, v147, s12
	v_exp_f32_e32 v151, v151
	v_fma_f32 v146, v144, v146, s14
	v_fma_f32 v147, v145, v147, s14
	s_nop 0
	v_fma_f32 v146, v144, v146, s46
	v_fma_f32 v147, v145, v147, s46
	s_nop 0
	v_mul_f32_e64 v144, v144, v146
	v_mul_f32_e64 v145, v145, v147
	v_mul_f32_e64 v146, v140, v140
	v_mul_f32_e64 v147, v141, v141
	v_mul_f32_e64 v144, v150, v144
	v_mul_f32_e64 v145, v151, v145
	v_mul_f32_e64 v146, v146, s48
	v_mul_f32_e64 v147, v147, s48
	v_mul_f32_e64 v150, v148, v144
	v_mul_f32_e64 v151, v149, v145
	v_fma_f32 v144, -v148, v144, v148
	v_fma_f32 v145, -v149, v145, v149
	v_exp_f32_e32 v146, v146
	v_cndmask_b32_e32 v150, v144, v150, vcc
	v_cmp_gt_f32_e32 vcc, 0, v149
	v_and_b32_e32 v144, 0x7fffffff, v140
	v_exp_f32_e32 v147, v147
	v_cndmask_b32_e32 v151, v145, v151, vcc
	v_and_b32_e32 v145, 0x7fffffff, v141
	v_fma_f32 v144, v144, s4, 1.0
	v_fma_f32 v145, v145, s4, 1.0
	v_cmp_gt_f32_e32 vcc, 0, v140
	v_rcp_f32_e32 v144, v144
	v_rcp_f32_e32 v145, v145
	s_nop 0
	v_fma_f32 v148, v144, s10, v132
	v_fma_f32 v149, v145, s10, v132
	s_nop 0
	v_fma_f32 v148, v144, v148, s12
	v_fma_f32 v149, v145, v149, s12
	s_nop 0
	v_fma_f32 v148, v144, v148, s14
	v_fma_f32 v149, v145, v149, s14
; __device__ __forceinline__ float silu_f(float g) { return g * __builtin_amdgcn_rcpf(1.0f + __builtin_amdgcn_exp2f(-1.44269504f * g)); }
; __device__ __forceinline__ f32x2 gelu_pk(f32x2 v) {
;     const f32x2 av = __builtin_elementwise_abs(v), d = av * 0.2316418882f + 1.0f;
;     f32x2 t; t.x = __builtin_amdgcn_rcpf(d.x); t.y = __builtin_amdgcn_rcpf(d.y);
;     f32x2 q = t * 0.5307027145f + (-0.7265760135f); q = q * t + 0.7107068705f; q = q * t + (-0.142248368f); q = q * t + 0.127414796f; q = q * t;
;     const f32x2 s = (v * v) * (-0.72134752044f);
;     f32x2 e; e.x = __builtin_amdgcn_exp2f(s.x); e.y = __builtin_amdgcn_exp2f(s.y);
;     const f32x2 m = v * (q * e), r = v - m;
;     f32x2 o; o.x = v.x < 0.f ? m.x : r.x; o.y = v.y < 0.f ? m.y : r.y; return o;
; }
;     template <int TT> __device__ __forceinline__ void other(const f32x4 (&acc)[2][2][4][2], bf16_t* base, int row0, int col0, PG8_LAS float* my, int t, int hh, int wc, int fq) const {
;     ...
;             for (int m = 0; m < 4; ++m) { bf16_t* rowp = base + (size_t)(row0 + ai * HALF + m * 16) * LDT + col0;
;                 const float rs = my[(ai * 4 + m) * 16]; float ps = 0.f, pq = 0.f; u32x4 gq = {0u, 0u, 0u, 0u};
; #pragma unroll
;                 for (int bj = 0; bj < 2; ++bj) { f32x4 v0 = acc[ai][bj][m][0] * rs + bv[bj][0], v1 = acc[ai][bj][m][1] * rs + bv[bj][1];
;                     if (TT == 3) {
; #pragma unroll
;                         for (int j = 0; j < 4; ++j) { v0[j] = silu_f(v0[j]); v1[j] = silu_f(v1[j]); } }
;                     else if (TT == 4 || TT == 5) { f32x2 a = gelu_pk((f32x2){v0[0], v0[1]}), b = gelu_pk((f32x2){v0[2], v0[3]}), c = gelu_pk((f32x2){v1[0], v1[1]}), d = gelu_pk((f32x2){v1[2], v1[3]});
;                         v0 = (f32x4){a.x, a.y, b.x, b.y}; v1 = (f32x4){c.x, c.y, d.x, d.y};
;                         if (TT == 5) { ps += ((v0[0] + v0[1]) + (v0[2] + v0[3])) + ((v1[0] + v1[1]) + (v1[2] + v1[3]));
;                             pq += ((v0[0] * v0[0] + v0[1] * v0[1]) + (v0[2] * v0[2] + v0[3] * v0[3])) + ((v1[0] * v1[0] + v1[1] * v1[1]) + (v1[2] * v1[2] + v1[3] * v1[3])); } }
;                     else if (TT >= 6) {
; #pragma unroll
;                         for (int j = 0; j < 4; ++j) { v0[j] = sigmoid_f(v0[j]); v1[j] = sigmoid_f(v1[j]); } }
;                     if (TT >= 6) { unsigned b0 = 0u, b1 = 0u;
; #pragma unroll
	s_nop 0
	v_fma_f32 v148, v144, v148, s46
	v_fma_f32 v149, v145, v149, s46
	s_nop 0
	v_mul_f32_e64 v144, v144, v148
	v_mul_f32_e64 v145, v145, v149
	s_nop 0
	v_mul_f32_e64 v144, v146, v144
	v_mul_f32_e64 v145, v147, v145
	s_nop 0
	v_mul_f32_e64 v146, v140, v144
	v_mul_f32_e64 v147, v141, v145
	v_fma_f32 v144, -v140, v144, v140
	v_fma_f32 v145, -v141, v145, v141
	s_nop 0
	v_cndmask_b32_e32 v140, v144, v146, vcc
	v_cmp_gt_f32_e32 vcc, 0, v141
	v_cvt_pk_bf16_f32 v144, v138, v143
	v_cvt_pk_bf16_f32 v146, v150, v151
	v_cndmask_b32_e32 v141, v145, v147, vcc
	v_cvt_pk_bf16_f32 v145, v152, v153
	v_cvt_pk_bf16_f32 v147, v140, v141
	global_store_dwordx4 v[136:137], v[144:147], off offset:256
	v_add_u32_e32 v136, 0xb0, v142
	v_mad_i64_i32 v[134:135], s[2:3], v136, s81, v[134:135]
	v_mov_b32_e32 v136, v139
	v_fma_f32 v142, v8, v136, 0
	v_fma_f32 v143, v9, v136, 0
	v_fma_f32 v140, v10, v136, 0
	v_fma_f32 v141, v11, v136, 0
	v_and_b32_e32 v147, 0x7fffffff, v143
	v_and_b32_e32 v146, 0x7fffffff, v142
	v_fma_f32 v146, v146, s4, 1.0
	v_fma_f32 v147, v147, s4, 1.0
	v_mul_f32_e64 v150, v142, v142
	v_mul_f32_e64 v151, v143, v143
	v_rcp_f32_e32 v146, v146
	v_rcp_f32_e32 v147, v147
	v_mul_f32_e64 v150, v150, s48
	v_mul_f32_e64 v151, v151, s48
	v_cmp_gt_f32_e32 vcc, 0, v142
	v_exp_f32_e32 v150, v150
	v_fma_f32 v148, v146, s10, v132
	v_fma_f32 v149, v147, s10, v132
	v_exp_f32_e32 v151, v151
	v_fma_f32 v148, v146, v148, s12
	v_fma_f32 v149, v147, v149, s12
	v_fma_f32 v138, v6, v136, 0
	v_fma_f32 v139, v7, v136, 0
	v_fma_f32 v148, v146, v148, s14
	v_fma_f32 v149, v147, v149, s14
	v_fma_f32 v144, v4, v136, 0
	v_fma_f32 v145, v5, v136, 0
	v_fma_f32 v148, v146, v148, s46
	v_fma_f32 v149, v147, v149, s46
	s_nop 0
	v_mul_f32_e64 v146, v146, v148
	v_mul_f32_e64 v147, v147, v149
	v_mul_f32_e64 v148, v140, v140
	v_mul_f32_e64 v149, v141, v141
	v_mul_f32_e64 v146, v150, v146
	v_mul_f32_e64 v147, v151, v147
	s_nop 0
	v_mul_f32_e64 v150, v142, v146
	v_mul_f32_e64 v151, v143, v147
	v_fma_f32 v146, -v142, v146, v142
	v_fma_f32 v147, -v143, v147, v143
	v_and_b32_e32 v142, 0x7fffffff, v140
	v_cndmask_b32_e32 v137, v146, v150, vcc
	v_cmp_gt_f32_e32 vcc, 0, v143
	v_and_b32_e32 v143, 0x7fffffff, v141
	v_fma_f32 v142, v142, s4, 1.0
	v_fma_f32 v143, v143, s4, 1.0
	v_cndmask_b32_e32 v150, v147, v151, vcc
	v_rcp_f32_e32 v142, v142
	v_rcp_f32_e32 v143, v143
	v_cmp_gt_f32_e32 vcc, 0, v140
	v_fma_f32 v146, v142, s10, v132
	v_fma_f32 v147, v143, s10, v132
	s_nop 0
	v_fma_f32 v146, v142, v146, s12
	v_fma_f32 v147, v143, v147, s12
	s_nop 0
	v_fma_f32 v146, v142, v146, s14
	v_fma_f32 v147, v143, v147, s14
	s_nop 0
	v_fma_f32 v146, v142, v146, s46
	v_fma_f32 v147, v143, v147, s46
	s_nop 0
	v_mul_f32_e64 v142, v142, v146
	v_mul_f32_e64 v143, v143, v147
	v_mul_f32_e64 v146, v148, s48
	v_mul_f32_e64 v147, v149, s48
	s_nop 0
	v_exp_f32_e32 v146, v146
	v_exp_f32_e32 v147, v147
	s_nop 0
	v_mul_f32_e64 v142, v146, v142
	v_mul_f32_e64 v143, v147, v143
	s_nop 0
	v_mul_f32_e64 v146, v140, v142
	v_mul_f32_e64 v147, v141, v143
	v_fma_f32 v142, -v140, v142, v140
	v_fma_f32 v143, -v141, v143, v141
	v_and_b32_e32 v140, 0x7fffffff, v144
	v_cndmask_b32_e32 v148, v142, v146, vcc
	v_cmp_gt_f32_e32 vcc, 0, v141
	v_and_b32_e32 v141, 0x7fffffff, v145
	v_fma_f32 v140, v140, s4, 1.0
	v_fma_f32 v141, v141, s4, 1.0
	v_cndmask_b32_e32 v149, v143, v147, vcc
	v_rcp_f32_e32 v140, v140
	v_rcp_f32_e32 v141, v141
	v_mul_f32_e64 v146, v144, v144
	v_mul_f32_e64 v147, v145, v145
	v_cmp_gt_f32_e32 vcc, 0, v144
	v_mul_f32_e64 v146, v146, s48
	v_mul_f32_e64 v147, v147, s48
	v_fma_f32 v142, v140, s10, v132
	v_fma_f32 v143, v141, s10, v132
	v_exp_f32_e32 v146, v146
	v_fma_f32 v142, v140, v142, s12
	v_fma_f32 v143, v141, v143, s12
	v_exp_f32_e32 v147, v147
	v_fma_f32 v142, v140, v142, s14
	v_fma_f32 v143, v141, v143, s14
	s_nop 0
	v_fma_f32 v142, v140, v142, s46
	v_fma_f32 v143, v141, v143, s46
	s_nop 0
	v_mul_f32_e64 v140, v140, v142
	v_mul_f32_e64 v141, v141, v143
	v_mul_f32_e64 v142, v138, v138
	v_mul_f32_e64 v143, v139, v139
	v_mul_f32_e64 v140, v146, v140
	v_mul_f32_e64 v141, v147, v141
	v_mul_f32_e64 v142, v142, s48
	v_mul_f32_e64 v143, v143, s48
	v_mul_f32_e64 v146, v144, v140
	v_mul_f32_e64 v147, v145, v141
	v_fma_f32 v140, -v144, v140, v144
	v_fma_f32 v141, -v145, v141, v145
	v_exp_f32_e32 v142, v142
	v_cndmask_b32_e32 v146, v140, v146, vcc
	v_cmp_gt_f32_e32 vcc, 0, v145
	v_and_b32_e32 v140, 0x7fffffff, v138
	v_exp_f32_e32 v143, v143
	v_cndmask_b32_e32 v147, v141, v147, vcc
	v_and_b32_e32 v141, 0x7fffffff, v139
	v_fma_f32 v140, v140, s4, 1.0
	v_fma_f32 v141, v141, s4, 1.0
	v_cmp_gt_f32_e32 vcc, 0, v138
	v_rcp_f32_e32 v140, v140
	v_rcp_f32_e32 v141, v141
	s_nop 0
	v_fma_f32 v144, v140, s10, v132
	v_fma_f32 v145, v141, s10, v132
	s_nop 0
	v_fma_f32 v144, v140, v144, s12
	v_fma_f32 v145, v141, v145, s12
	s_nop 0
	v_fma_f32 v144, v140, v144, s14
	v_fma_f32 v145, v141, v145, s14
	s_nop 0
	v_fma_f32 v144, v140, v144, s46
	v_fma_f32 v145, v141, v145, s46
	s_nop 0
	v_mul_f32_e64 v140, v140, v144
	v_mul_f32_e64 v141, v141, v145
	s_nop 0
	v_mul_f32_e64 v140, v142, v140
	v_mul_f32_e64 v141, v143, v141
	s_nop 0
	v_mul_f32_e64 v142, v138, v140
	v_mul_f32_e64 v143, v139, v141
	v_fma_f32 v140, -v138, v140, v138
	v_fma_f32 v141, -v139, v141, v139
	v_cvt_pk_bf16_f32 v138, v137, v150
	v_cndmask_b32_e32 v142, v140, v142, vcc
	v_cmp_gt_f32_e32 vcc, 0, v139
	v_cvt_pk_bf16_f32 v139, v148, v149
	v_cvt_pk_bf16_f32 v140, v146, v147
	v_cndmask_b32_e32 v141, v141, v143, vcc
	v_cvt_pk_bf16_f32 v141, v142, v141
	v_fma_f32 v142, v16, v136, 0
	v_fma_f32 v143, v17, v136, 0
	global_store_dwordx4 v[134:135], v[138:141], off
	v_and_b32_e32 v145, 0x7fffffff, v143
; __device__ __forceinline__ float silu_f(float g) { return g * __builtin_amdgcn_rcpf(1.0f + __builtin_amdgcn_exp2f(-1.44269504f * g)); }
; __device__ __forceinline__ f32x2 gelu_pk(f32x2 v) {
;     const f32x2 av = __builtin_elementwise_abs(v), d = av * 0.2316418882f + 1.0f;
;     f32x2 t; t.x = __builtin_amdgcn_rcpf(d.x); t.y = __builtin_amdgcn_rcpf(d.y);
;     f32x2 q = t * 0.5307027145f + (-0.7265760135f); q = q * t + 0.7107068705f; q = q * t + (-0.142248368f); q = q * t + 0.127414796f; q = q * t;
;     const f32x2 s = (v * v) * (-0.72134752044f);
;     f32x2 e; e.x = __builtin_amdgcn_exp2f(s.x); e.y = __builtin_amdgcn_exp2f(s.y);
;     const f32x2 m = v * (q * e), r = v - m;
;     f32x2 o; o.x = v.x < 0.f ? m.x : r.x; o.y = v.y < 0.f ? m.y : r.y; return o;
; }
;     template <int TT> __device__ __forceinline__ void other(const f32x4 (&acc)[2][2][4][2], bf16_t* base, int row0, int col0, PG8_LAS float* my, int t, int hh, int wc, int fq) const {
;     ...
;             for (int m = 0; m < 4; ++m) { bf16_t* rowp = base + (size_t)(row0 + ai * HALF + m * 16) * LDT + col0;
;                 const float rs = my[(ai * 4 + m) * 16]; float ps = 0.f, pq = 0.f; u32x4 gq = {0u, 0u, 0u, 0u};
; #pragma unroll
;                 for (int bj = 0; bj < 2; ++bj) { f32x4 v0 = acc[ai][bj][m][0] * rs + bv[bj][0], v1 = acc[ai][bj][m][1] * rs + bv[bj][1];
;                     if (TT == 3) {
; #pragma unroll
;                         for (int j = 0; j < 4; ++j) { v0[j] = silu_f(v0[j]); v1[j] = silu_f(v1[j]); } }
;                     else if (TT == 4 || TT == 5) { f32x2 a = gelu_pk((f32x2){v0[0], v0[1]}), b = gelu_pk((f32x2){v0[2], v0[3]}), c = gelu_pk((f32x2){v1[0], v1[1]}), d = gelu_pk((f32x2){v1[2], v1[3]});
;                         v0 = (f32x4){a.x, a.y, b.x, b.y}; v1 = (f32x4){c.x, c.y, d.x, d.y};
;                         if (TT == 5) { ps += ((v0[0] + v0[1]) + (v0[2] + v0[3])) + ((v1[0] + v1[1]) + (v1[2] + v1[3]));
;                             pq += ((v0[0] * v0[0] + v0[1] * v0[1]) + (v0[2] * v0[2] + v0[3] * v0[3])) + ((v1[0] * v1[0] + v1[1] * v1[1]) + (v1[2] * v1[2] + v1[3] * v1[3])); } }
;                     else if (TT >= 6) {
; #pragma unroll
;                         for (int j = 0; j < 4; ++j) { v0[j] = sigmoid_f(v0[j]); v1[j] = sigmoid_f(v1[j]); } }
;                     if (TT >= 6) { unsigned b0 = 0u, b1 = 0u;
; #pragma unroll
	v_and_b32_e32 v144, 0x7fffffff, v142
	v_fma_f32 v144, v144, s4, 1.0
	v_fma_f32 v145, v145, s4, 1.0
	v_mul_f32_e64 v148, v142, v142
	v_mul_f32_e64 v149, v143, v143
	v_rcp_f32_e32 v144, v144
	v_rcp_f32_e32 v145, v145
	v_mul_f32_e64 v148, v148, s48
	v_mul_f32_e64 v149, v149, s48
	v_fma_f32 v140, v18, v136, 0
	v_fma_f32 v141, v19, v136, 0
	v_exp_f32_e32 v148, v148
	v_fma_f32 v146, v144, s10, v132
	v_fma_f32 v147, v145, s10, v132
	v_exp_f32_e32 v149, v149
	v_fma_f32 v146, v144, v146, s12
	v_fma_f32 v147, v145, v147, s12
	v_cmp_gt_f32_e32 vcc, 0, v142
	v_fma_f32 v146, v144, v146, s14
	v_fma_f32 v147, v145, v147, s14
	v_fma_f32 v138, v14, v136, 0
	v_fma_f32 v139, v15, v136, 0
	v_fma_f32 v146, v144, v146, s46
	v_fma_f32 v147, v145, v147, s46
	v_fma_f32 v137, v13, v136, 0
	v_fma_f32 v136, v12, v136, 0
	v_mul_f32_e64 v144, v144, v146
	v_mul_f32_e64 v145, v145, v147
	v_mul_f32_e64 v146, v140, v140
	v_mul_f32_e64 v147, v141, v141
	v_mul_f32_e64 v144, v148, v144
	v_mul_f32_e64 v145, v149, v145
	s_nop 0
	v_mul_f32_e64 v148, v142, v144
	v_mul_f32_e64 v149, v143, v145
	v_fma_f32 v144, -v142, v144, v142
	v_fma_f32 v145, -v143, v145, v143
	v_and_b32_e32 v142, 0x7fffffff, v140
	v_cndmask_b32_e32 v148, v144, v148, vcc
	v_cmp_gt_f32_e32 vcc, 0, v143
	v_and_b32_e32 v143, 0x7fffffff, v141
	v_fma_f32 v142, v142, s4, 1.0
	v_fma_f32 v143, v143, s4, 1.0
	v_cndmask_b32_e32 v149, v145, v149, vcc
	v_rcp_f32_e32 v142, v142
	v_rcp_f32_e32 v143, v143
	v_cmp_gt_f32_e32 vcc, 0, v140
	v_fma_f32 v144, v142, s10, v132
	v_fma_f32 v145, v143, s10, v132
	s_nop 0
	v_fma_f32 v144, v142, v144, s12
	v_fma_f32 v145, v143, v145, s12
	s_nop 0
	v_fma_f32 v144, v142, v144, s14
	v_fma_f32 v145, v143, v145, s14
	s_nop 0
	v_fma_f32 v144, v142, v144, s46
	v_fma_f32 v145, v143, v145, s46
	s_nop 0
	v_mul_f32_e64 v142, v142, v144
	v_mul_f32_e64 v143, v143, v145
	v_mul_f32_e64 v144, v146, s48
	v_mul_f32_e64 v145, v147, s48
	s_nop 0
	v_exp_f32_e32 v144, v144
	v_exp_f32_e32 v145, v145
	s_nop 0
	v_mul_f32_e64 v142, v144, v142
	v_mul_f32_e64 v143, v145, v143
	s_nop 0
	v_mul_f32_e64 v144, v140, v142
	v_mul_f32_e64 v145, v141, v143
	v_fma_f32 v142, -v140, v142, v140
	v_fma_f32 v143, -v141, v143, v141
	v_and_b32_e32 v140, 0x7fffffff, v136
	v_cndmask_b32_e32 v146, v142, v144, vcc
	v_cmp_gt_f32_e32 vcc, 0, v141
	v_and_b32_e32 v141, 0x7fffffff, v137
	v_fma_f32 v140, v140, s4, 1.0
	v_fma_f32 v141, v141, s4, 1.0
	v_cndmask_b32_e32 v147, v143, v145, vcc
	v_rcp_f32_e32 v140, v140
	v_rcp_f32_e32 v141, v141
	v_mul_f32_e64 v144, v136, v136
	v_mul_f32_e64 v145, v137, v137
	v_cmp_gt_f32_e32 vcc, 0, v136
	v_mul_f32_e64 v144, v144, s48
	v_mul_f32_e64 v145, v145, s48
	v_fma_f32 v142, v140, s10, v132
	v_fma_f32 v143, v141, s10, v132
	v_exp_f32_e32 v144, v144
	v_fma_f32 v142, v140, v142, s12
	v_fma_f32 v143, v141, v143, s12
	v_exp_f32_e32 v145, v145
	v_fma_f32 v142, v140, v142, s14
	v_fma_f32 v143, v141, v143, s14
	s_nop 0
	v_fma_f32 v142, v140, v142, s46
	v_fma_f32 v143, v141, v143, s46
	s_nop 0
	v_mul_f32_e64 v140, v140, v142
	v_mul_f32_e64 v141, v141, v143
	v_mul_f32_e64 v142, v138, v138
	v_mul_f32_e64 v143, v139, v139
	v_mul_f32_e64 v140, v144, v140
	v_mul_f32_e64 v141, v145, v141
	s_nop 0
	v_mul_f32_e64 v144, v136, v140
	v_mul_f32_e64 v145, v137, v141
	v_fma_f32 v140, -v136, v140, v136
	v_fma_f32 v141, -v137, v141, v137
	v_and_b32_e32 v136, 0x7fffffff, v138
	v_cndmask_b32_e32 v140, v140, v144, vcc
	v_cmp_gt_f32_e32 vcc, 0, v137
	v_and_b32_e32 v137, 0x7fffffff, v139
	v_fma_f32 v136, v136, s4, 1.0
	v_fma_f32 v137, v137, s4, 1.0
	v_cndmask_b32_e32 v141, v141, v145, vcc
	v_rcp_f32_e32 v136, v136
	v_rcp_f32_e32 v137, v137
	v_cmp_gt_f32_e32 vcc, 0, v138
	s_mov_b64 s[4:5], 0
	v_fma_f32 v133, v137, s10, v132
	v_fma_f32 v132, v136, s10, v132
	s_nop 0
	v_fma_f32 v132, v136, v132, s12
	v_fma_f32 v133, v137, v133, s12
	s_nop 0
	v_fma_f32 v132, v136, v132, s14
	v_fma_f32 v133, v137, v133, s14
	s_nop 0
	v_fma_f32 v132, v136, v132, s46
	v_fma_f32 v133, v137, v133, s46
	s_nop 0
	v_mul_f32_e64 v132, v136, v132
	v_mul_f32_e64 v133, v137, v133
	v_mul_f32_e64 v136, v142, s48
	v_mul_f32_e64 v137, v143, s48
	s_nop 0
	v_exp_f32_e32 v136, v136
	v_exp_f32_e32 v137, v137
	s_nop 0
	v_mul_f32_e64 v132, v136, v132
	v_mul_f32_e64 v133, v137, v133
	s_nop 0
	v_mul_f32_e64 v136, v138, v132
	v_mul_f32_e64 v137, v139, v133
	v_fma_f32 v132, -v138, v132, v138
	v_fma_f32 v133, -v139, v133, v139
	v_cvt_pk_bf16_f32 v138, v140, v141
	v_cndmask_b32_e32 v132, v132, v136, vcc
	v_cmp_gt_f32_e32 vcc, 0, v139
	v_cvt_pk_bf16_f32 v136, v148, v149
	s_nop 0
	v_cndmask_b32_e32 v133, v133, v137, vcc
	v_cvt_pk_bf16_f32 v137, v146, v147
	v_cvt_pk_bf16_f32 v139, v132, v133
	global_store_dwordx4 v[134:135], v[136:139], off offset:256
; __device__ __forceinline__ unsigned cvt_pk_bf16(float lo, float hi) { f32x2_c v = {lo, hi}; bf16x2_c b = __builtin_convertvector(v, bf16x2_c); return __builtin_bit_cast(unsigned, b); }
; __device__ __forceinline__ float silu_f(float g) { return g * __builtin_amdgcn_rcpf(1.0f + __builtin_amdgcn_exp2f(-1.44269504f * g)); }
;     template <int TT> __device__ __forceinline__ void other(const f32x4 (&acc)[2][2][4][2], bf16_t* base, int row0, int col0, PG8_LAS float* my, int t, int hh, int wc, int fq) const {
;     ...
;                 for (int bj = 0; bj < 2; ++bj) { f32x4 v0 = acc[ai][bj][m][0] * rs + bv[bj][0], v1 = acc[ai][bj][m][1] * rs + bv[bj][1];
;                     if (TT == 3) {
; #pragma unroll
;                         for (int j = 0; j < 4; ++j) { v0[j] = silu_f(v0[j]); v1[j] = silu_f(v1[j]); } }
;     ...
;                     else { u32x4 w; w.x = cvt_pk_bf16(v0[0], v0[1]); w.y = cvt_pk_bf16(v0[2], v0[3]); w.z = cvt_pk_bf16(v1[0], v1[1]); w.w = cvt_pk_bf16(v1[2], v1[3]);
;                         *(u32x4*)(rowp + bj * HALF) = w; } }
.LBB0_360:
	s_andn2_b64 vcc, exec, s[4:5]
	s_cbranch_vccnz .LBB0_362
	v_mov_b32_e32 v138, v174
	s_waitcnt lgkmcnt(0)
	v_mov_b32_e32 v133, v3
	v_mov_b32_e32 v132, v158
	ds_read2_b32 v[136:137], v199 offset1:16
	v_ashrrev_i32_e32 v133, 31, v132
	v_lshl_add_u64 v[132:133], v[132:133], 1, s[28:29]
	v_mad_i64_i32 v[134:135], s[2:3], v138, s81, v[132:133]
	s_waitcnt lgkmcnt(0)
	v_fma_f32 v142, v120, v136, 0
	v_fma_f32 v143, v121, v136, 0
	v_fma_f32 v146, v116, v136, 0
	v_fma_f32 v147, v117, v136, 0
	v_mul_f32_e32 v139, 0xbfb8aa3b, v142
	v_exp_f32_e32 v139, v139
	v_fma_f32 v140, v122, v136, 0
	v_fma_f32 v141, v123, v136, 0
	v_fma_f32 v144, v118, v136, 0
	v_fma_f32 v145, v119, v136, 0
	v_add_f32_e32 v139, 1.0, v139
	v_rcp_f32_e32 v148, v139
	v_mul_f32_e32 v139, 0xbfb8aa3b, v146
	v_exp_f32_e32 v139, v139
	s_nop 0
	v_add_f32_e32 v139, 1.0, v139
	v_rcp_f32_e32 v150, v139
	v_mul_f32_e32 v139, 0xbfb8aa3b, v143
	v_exp_f32_e32 v139, v139
	s_nop 0
	v_add_f32_e32 v139, 1.0, v139
	v_rcp_f32_e32 v149, v139
	v_mul_f32_e32 v139, 0xbfb8aa3b, v147
	v_exp_f32_e32 v139, v139
	v_mul_f32_e64 v142, v142, v148
	v_mul_f32_e64 v143, v143, v149
	v_add_f32_e32 v139, 1.0, v139
	v_rcp_f32_e32 v151, v139
	v_mul_f32_e32 v139, 0xbfb8aa3b, v140
	v_exp_f32_e32 v139, v139
	v_mul_f32_e64 v146, v146, v150
	v_mul_f32_e64 v147, v147, v151
	v_add_f32_e32 v139, 1.0, v139
	v_rcp_f32_e32 v148, v139
	v_mul_f32_e32 v139, 0xbfb8aa3b, v144
	v_exp_f32_e32 v139, v139
	s_nop 0
	v_add_f32_e32 v139, 1.0, v139
	v_rcp_f32_e32 v150, v139
	v_mul_f32_e32 v139, 0xbfb8aa3b, v141
	v_exp_f32_e32 v139, v139
	s_nop 0
	v_add_f32_e32 v139, 1.0, v139
	v_rcp_f32_e32 v149, v139
	v_mul_f32_e32 v139, 0xbfb8aa3b, v145
	v_exp_f32_e32 v139, v139
	v_mul_f32_e64 v148, v140, v148
	v_mul_f32_e64 v149, v141, v149
	v_cvt_pk_bf16_f32 v140, v142, v143
	v_add_f32_e32 v139, 1.0, v139
	v_rcp_f32_e32 v151, v139
	v_cvt_pk_bf16_f32 v141, v148, v149
	v_cvt_pk_bf16_f32 v142, v146, v147
	v_fma_f32 v146, v124, v136, 0
	v_fma_f32 v147, v125, v136, 0
	v_mul_f32_e64 v144, v144, v150
	v_mul_f32_e64 v145, v145, v151
	s_nop 0
	v_cvt_pk_bf16_f32 v143, v144, v145
	global_store_dwordx4 v[134:135], v[140:143], off
	v_fma_f32 v144, v126, v136, 0
	v_fma_f32 v145, v127, v136, 0
	s_nop 0
	v_fma_f32 v142, v128, v136, 0
	v_fma_f32 v143, v129, v136, 0
	v_fma_f32 v140, v130, v136, 0
	v_fma_f32 v141, v131, v136, 0
	v_mul_f32_e32 v136, 0xbfb8aa3b, v142
	v_exp_f32_e32 v136, v136
	s_nop 0
	v_add_f32_e32 v136, 1.0, v136
	v_rcp_f32_e32 v148, v136
	v_mul_f32_e32 v136, 0xbfb8aa3b, v146
	v_exp_f32_e32 v136, v136
	s_nop 0
	v_add_f32_e32 v136, 1.0, v136
	v_rcp_f32_e32 v150, v136
	v_mul_f32_e32 v136, 0xbfb8aa3b, v143
	v_exp_f32_e32 v136, v136
	s_nop 0
	v_add_f32_e32 v136, 1.0, v136
	v_rcp_f32_e32 v149, v136
	v_mul_f32_e32 v136, 0xbfb8aa3b, v147
	v_exp_f32_e32 v136, v136
	v_mul_f32_e64 v142, v142, v148
	v_mul_f32_e64 v143, v143, v149
	v_add_f32_e32 v136, 1.0, v136
	v_rcp_f32_e32 v151, v136
	v_mul_f32_e32 v136, 0xbfb8aa3b, v140
	v_exp_f32_e32 v136, v136
	v_mul_f32_e64 v146, v146, v150
	v_mul_f32_e64 v147, v147, v151
	v_add_f32_e32 v136, 1.0, v136
	v_rcp_f32_e32 v148, v136
	v_mul_f32_e32 v136, 0xbfb8aa3b, v144
	v_exp_f32_e32 v136, v136
	s_nop 0
	v_add_f32_e32 v136, 1.0, v136
	v_rcp_f32_e32 v150, v136
	v_mul_f32_e32 v136, 0xbfb8aa3b, v141
	v_exp_f32_e32 v136, v136
	s_nop 0
	v_add_f32_e32 v136, 1.0, v136
	v_rcp_f32_e32 v149, v136
	v_mul_f32_e32 v136, 0xbfb8aa3b, v145
	v_exp_f32_e32 v136, v136
	v_mul_f32_e64 v148, v140, v148
	v_mul_f32_e64 v149, v141, v149
	v_cvt_pk_bf16_f32 v140, v142, v143
	v_add_f32_e32 v136, 1.0, v136
	v_rcp_f32_e32 v151, v136
	v_cvt_pk_bf16_f32 v141, v148, v149
	v_cvt_pk_bf16_f32 v142, v146, v147
	v_mov_b32_e32 v136, v137
	v_mul_f32_e64 v144, v144, v150
	v_mul_f32_e64 v145, v145, v151
	v_fma_f32 v146, v100, v136, 0
	v_fma_f32 v147, v101, v136, 0
	v_cvt_pk_bf16_f32 v143, v144, v145
	global_store_dwordx4 v[134:135], v[140:143], off offset:256
	v_fma_f32 v144, v102, v136, 0
	v_fma_f32 v145, v103, v136, 0
	v_add_u32_e32 v134, 16, v138
	v_fma_f32 v142, v104, v136, 0
	v_fma_f32 v143, v105, v136, 0
	v_fma_f32 v140, v106, v136, 0
	v_fma_f32 v141, v107, v136, 0
	v_mul_f32_e32 v137, 0xbfb8aa3b, v142
	v_exp_f32_e32 v137, v137
	v_mad_i64_i32 v[134:135], s[2:3], v134, s81, v[132:133]
	v_add_f32_e32 v137, 1.0, v137
	v_rcp_f32_e32 v148, v137
	v_mul_f32_e32 v137, 0xbfb8aa3b, v146
	v_exp_f32_e32 v137, v137
	s_nop 0
	v_add_f32_e32 v137, 1.0, v137
	v_rcp_f32_e32 v150, v137
	v_mul_f32_e32 v137, 0xbfb8aa3b, v143
	v_exp_f32_e32 v137, v137
	s_nop 0
	v_add_f32_e32 v137, 1.0, v137
	v_rcp_f32_e32 v149, v137
	v_mul_f32_e32 v137, 0xbfb8aa3b, v147
	v_exp_f32_e32 v137, v137
	v_mul_f32_e64 v142, v142, v148
	v_mul_f32_e64 v143, v143, v149
	v_add_f32_e32 v137, 1.0, v137
	v_rcp_f32_e32 v151, v137
	v_mul_f32_e32 v137, 0xbfb8aa3b, v140
	v_exp_f32_e32 v137, v137
	v_mul_f32_e64 v146, v146, v150
	v_mul_f32_e64 v147, v147, v151
	v_add_f32_e32 v137, 1.0, v137
	v_rcp_f32_e32 v148, v137
	v_mul_f32_e32 v137, 0xbfb8aa3b, v144
	v_exp_f32_e32 v137, v137
	s_nop 0
	v_add_f32_e32 v137, 1.0, v137
	v_rcp_f32_e32 v150, v137
	v_mul_f32_e32 v137, 0xbfb8aa3b, v141
	v_exp_f32_e32 v137, v137
	s_nop 0
	v_add_f32_e32 v137, 1.0, v137
	v_rcp_f32_e32 v149, v137
	v_mul_f32_e32 v137, 0xbfb8aa3b, v145
	v_exp_f32_e32 v137, v137
	v_mul_f32_e64 v148, v140, v148
	v_mul_f32_e64 v149, v141, v149
	v_cvt_pk_bf16_f32 v140, v142, v143
	v_add_f32_e32 v137, 1.0, v137
	v_rcp_f32_e32 v151, v137
	v_cvt_pk_bf16_f32 v141, v148, v149
	v_cvt_pk_bf16_f32 v142, v146, v147
	v_mul_f32_e64 v144, v144, v150
	v_mul_f32_e64 v145, v145, v151
	s_nop 0
	v_cvt_pk_bf16_f32 v143, v144, v145
	global_store_dwordx4 v[134:135], v[140:143], off
; __device__ __forceinline__ unsigned cvt_pk_bf16(float lo, float hi) { f32x2_c v = {lo, hi}; bf16x2_c b = __builtin_convertvector(v, bf16x2_c); return __builtin_bit_cast(unsigned, b); }
; __device__ __forceinline__ float silu_f(float g) { return g * __builtin_amdgcn_rcpf(1.0f + __builtin_amdgcn_exp2f(-1.44269504f * g)); }
;     template <int TT> __device__ __forceinline__ void other(const f32x4 (&acc)[2][2][4][2], bf16_t* base, int row0, int col0, PG8_LAS float* my, int t, int hh, int wc, int fq) const {
;     ...
;                 for (int bj = 0; bj < 2; ++bj) { f32x4 v0 = acc[ai][bj][m][0] * rs + bv[bj][0], v1 = acc[ai][bj][m][1] * rs + bv[bj][1];
;                     if (TT == 3) {
; #pragma unroll
;                         for (int j = 0; j < 4; ++j) { v0[j] = silu_f(v0[j]); v1[j] = silu_f(v1[j]); } }
;     ...
;                     else { u32x4 w; w.x = cvt_pk_bf16(v0[0], v0[1]); w.y = cvt_pk_bf16(v0[2], v0[3]); w.z = cvt_pk_bf16(v1[0], v1[1]); w.w = cvt_pk_bf16(v1[2], v1[3]);
;                         *(u32x4*)(rowp + bj * HALF) = w; } }
	v_fma_f32 v144, v110, v136, 0
	v_fma_f32 v145, v111, v136, 0
	s_nop 0
	v_fma_f32 v142, v112, v136, 0
	v_fma_f32 v143, v113, v136, 0
	v_fma_f32 v140, v114, v136, 0
	v_fma_f32 v141, v115, v136, 0
	v_mul_f32_e32 v139, 0xbfb8aa3b, v142
	v_exp_f32_e32 v139, v139
	v_fma_f32 v137, v109, v136, 0
	v_fma_f32 v136, v108, v136, 0
	v_add_f32_e32 v139, 1.0, v139
	v_rcp_f32_e32 v146, v139
	v_mul_f32_e32 v139, 0xbfb8aa3b, v136
	v_exp_f32_e32 v139, v139
	s_nop 0
	v_add_f32_e32 v139, 1.0, v139
	v_rcp_f32_e32 v148, v139
	v_mul_f32_e32 v139, 0xbfb8aa3b, v143
	v_exp_f32_e32 v139, v139
	s_nop 0
	v_add_f32_e32 v139, 1.0, v139
	v_rcp_f32_e32 v147, v139
	v_mul_f32_e32 v139, 0xbfb8aa3b, v137
	v_exp_f32_e32 v139, v139
	v_mul_f32_e64 v142, v142, v146
	v_mul_f32_e64 v143, v143, v147
	v_add_f32_e32 v139, 1.0, v139
	v_rcp_f32_e32 v149, v139
	v_mul_f32_e32 v139, 0xbfb8aa3b, v140
	v_exp_f32_e32 v139, v139
	v_mul_f32_e64 v136, v136, v148
	v_mul_f32_e64 v137, v137, v149
	v_add_f32_e32 v139, 1.0, v139
	v_rcp_f32_e32 v146, v139
	v_mul_f32_e32 v139, 0xbfb8aa3b, v144
	v_exp_f32_e32 v139, v139
	s_nop 0
	v_add_f32_e32 v139, 1.0, v139
	v_rcp_f32_e32 v148, v139
	v_mul_f32_e32 v139, 0xbfb8aa3b, v141
	v_exp_f32_e32 v139, v139
	s_nop 0
	v_add_f32_e32 v139, 1.0, v139
	v_rcp_f32_e32 v147, v139
	v_mul_f32_e32 v139, 0xbfb8aa3b, v145
	v_exp_f32_e32 v139, v139
	v_mul_f32_e64 v146, v140, v146
	v_mul_f32_e64 v147, v141, v147
	v_cvt_pk_bf16_f32 v140, v142, v143
	v_add_f32_e32 v139, 1.0, v139
	v_rcp_f32_e32 v149, v139
	v_cvt_pk_bf16_f32 v142, v136, v137
	ds_read2_b32 v[136:137], v199 offset0:32 offset1:48
	v_cvt_pk_bf16_f32 v141, v146, v147
	v_mul_f32_e64 v144, v144, v148
	v_mul_f32_e64 v145, v145, v149
	s_waitcnt lgkmcnt(0)
	v_fma_f32 v146, v84, v136, 0
	v_fma_f32 v147, v85, v136, 0
	v_cvt_pk_bf16_f32 v143, v144, v145
	global_store_dwordx4 v[134:135], v[140:143], off offset:256
	v_fma_f32 v144, v86, v136, 0
	v_fma_f32 v145, v87, v136, 0
	v_add_u32_e32 v134, 32, v138
	v_fma_f32 v142, v88, v136, 0
	v_fma_f32 v143, v89, v136, 0
	v_fma_f32 v140, v90, v136, 0
	v_fma_f32 v141, v91, v136, 0
	v_mul_f32_e32 v139, 0xbfb8aa3b, v142
	v_exp_f32_e32 v139, v139
	v_mad_i64_i32 v[134:135], s[2:3], v134, s81, v[132:133]
	v_add_f32_e32 v139, 1.0, v139
	v_rcp_f32_e32 v148, v139
	v_mul_f32_e32 v139, 0xbfb8aa3b, v146
	v_exp_f32_e32 v139, v139
	s_nop 0
	v_add_f32_e32 v139, 1.0, v139
	v_rcp_f32_e32 v150, v139
	v_mul_f32_e32 v139, 0xbfb8aa3b, v143
	v_exp_f32_e32 v139, v139
	s_nop 0
	v_add_f32_e32 v139, 1.0, v139
	v_rcp_f32_e32 v149, v139
	v_mul_f32_e32 v139, 0xbfb8aa3b, v147
	v_exp_f32_e32 v139, v139
	v_mul_f32_e64 v142, v142, v148
	v_mul_f32_e64 v143, v143, v149
	v_add_f32_e32 v139, 1.0, v139
	v_rcp_f32_e32 v151, v139
	v_mul_f32_e32 v139, 0xbfb8aa3b, v140
	v_exp_f32_e32 v139, v139
	v_mul_f32_e64 v146, v146, v150
	v_mul_f32_e64 v147, v147, v151
	v_add_f32_e32 v139, 1.0, v139
	v_rcp_f32_e32 v148, v139
	v_mul_f32_e32 v139, 0xbfb8aa3b, v144
	v_exp_f32_e32 v139, v139
	s_nop 0
	v_add_f32_e32 v139, 1.0, v139
	v_rcp_f32_e32 v150, v139
	v_mul_f32_e32 v139, 0xbfb8aa3b, v141
	v_exp_f32_e32 v139, v139
	s_nop 0
	v_add_f32_e32 v139, 1.0, v139
	v_rcp_f32_e32 v149, v139
	v_mul_f32_e32 v139, 0xbfb8aa3b, v145
	v_exp_f32_e32 v139, v139
	v_mul_f32_e64 v148, v140, v148
	v_mul_f32_e64 v149, v141, v149
	v_cvt_pk_bf16_f32 v140, v142, v143
	v_add_f32_e32 v139, 1.0, v139
	v_rcp_f32_e32 v151, v139
	v_cvt_pk_bf16_f32 v141, v148, v149
	v_cvt_pk_bf16_f32 v142, v146, v147
	v_fma_f32 v146, v92, v136, 0
	v_fma_f32 v147, v93, v136, 0
	v_mul_f32_e64 v144, v144, v150
	v_mul_f32_e64 v145, v145, v151
	s_nop 0
	v_cvt_pk_bf16_f32 v143, v144, v145
	global_store_dwordx4 v[134:135], v[140:143], off
	v_fma_f32 v144, v94, v136, 0
	v_fma_f32 v145, v95, v136, 0
	s_nop 0
	v_fma_f32 v142, v96, v136, 0
	v_fma_f32 v143, v97, v136, 0
	v_fma_f32 v140, v98, v136, 0
	v_fma_f32 v141, v99, v136, 0
	v_mul_f32_e32 v136, 0xbfb8aa3b, v142
	v_exp_f32_e32 v136, v136
	s_nop 0
	v_add_f32_e32 v136, 1.0, v136
	v_rcp_f32_e32 v148, v136
	v_mul_f32_e32 v136, 0xbfb8aa3b, v146
	v_exp_f32_e32 v136, v136
	s_nop 0
	v_add_f32_e32 v136, 1.0, v136
	v_rcp_f32_e32 v150, v136
	v_mul_f32_e32 v136, 0xbfb8aa3b, v143
	v_exp_f32_e32 v136, v136
	s_nop 0
	v_add_f32_e32 v136, 1.0, v136
	v_rcp_f32_e32 v149, v136
	v_mul_f32_e32 v136, 0xbfb8aa3b, v147
	v_exp_f32_e32 v136, v136
	v_mul_f32_e64 v142, v142, v148
	v_mul_f32_e64 v143, v143, v149
	v_add_f32_e32 v136, 1.0, v136
	v_rcp_f32_e32 v151, v136
	v_mul_f32_e32 v136, 0xbfb8aa3b, v140
	v_exp_f32_e32 v136, v136
	v_mul_f32_e64 v146, v146, v150
	v_mul_f32_e64 v147, v147, v151
	v_add_f32_e32 v136, 1.0, v136
	v_rcp_f32_e32 v148, v136
	v_mul_f32_e32 v136, 0xbfb8aa3b, v144
	v_exp_f32_e32 v136, v136
	s_nop 0
	v_add_f32_e32 v136, 1.0, v136
	v_rcp_f32_e32 v150, v136
	v_mul_f32_e32 v136, 0xbfb8aa3b, v141
	v_exp_f32_e32 v136, v136
	s_nop 0
	v_add_f32_e32 v136, 1.0, v136
	v_rcp_f32_e32 v149, v136
	v_mul_f32_e32 v136, 0xbfb8aa3b, v145
	v_exp_f32_e32 v136, v136
	v_mul_f32_e64 v148, v140, v148
	v_mul_f32_e64 v149, v141, v149
	v_cvt_pk_bf16_f32 v140, v142, v143
	v_add_f32_e32 v136, 1.0, v136
	v_rcp_f32_e32 v151, v136
	v_cvt_pk_bf16_f32 v141, v148, v149
	v_cvt_pk_bf16_f32 v142, v146, v147
	v_mov_b32_e32 v136, v137
	v_mul_f32_e64 v144, v144, v150
	v_mul_f32_e64 v145, v145, v151
	v_fma_f32 v146, v68, v136, 0
	v_fma_f32 v147, v69, v136, 0
	v_cvt_pk_bf16_f32 v143, v144, v145
	global_store_dwordx4 v[134:135], v[140:143], off offset:256
	v_fma_f32 v144, v70, v136, 0
	v_fma_f32 v145, v71, v136, 0
	v_add_u32_e32 v134, 48, v138
	v_fma_f32 v142, v72, v136, 0
	v_fma_f32 v143, v73, v136, 0
	v_fma_f32 v140, v74, v136, 0
	v_fma_f32 v141, v75, v136, 0
	v_mul_f32_e32 v137, 0xbfb8aa3b, v142
; __device__ __forceinline__ unsigned cvt_pk_bf16(float lo, float hi) { f32x2_c v = {lo, hi}; bf16x2_c b = __builtin_convertvector(v, bf16x2_c); return __builtin_bit_cast(unsigned, b); }
; __device__ __forceinline__ float silu_f(float g) { return g * __builtin_amdgcn_rcpf(1.0f + __builtin_amdgcn_exp2f(-1.44269504f * g)); }
;     template <int TT> __device__ __forceinline__ void other(const f32x4 (&acc)[2][2][4][2], bf16_t* base, int row0, int col0, PG8_LAS float* my, int t, int hh, int wc, int fq) const {
;     ...
;                 for (int bj = 0; bj < 2; ++bj) { f32x4 v0 = acc[ai][bj][m][0] * rs + bv[bj][0], v1 = acc[ai][bj][m][1] * rs + bv[bj][1];
;                     if (TT == 3) {
; #pragma unroll
;                         for (int j = 0; j < 4; ++j) { v0[j] = silu_f(v0[j]); v1[j] = silu_f(v1[j]); } }
;     ...
;                     else { u32x4 w; w.x = cvt_pk_bf16(v0[0], v0[1]); w.y = cvt_pk_bf16(v0[2], v0[3]); w.z = cvt_pk_bf16(v1[0], v1[1]); w.w = cvt_pk_bf16(v1[2], v1[3]);
;                         *(u32x4*)(rowp + bj * HALF) = w; } }
	v_exp_f32_e32 v137, v137
	v_mad_i64_i32 v[134:135], s[2:3], v134, s81, v[132:133]
	v_add_f32_e32 v137, 1.0, v137
	v_rcp_f32_e32 v148, v137
	v_mul_f32_e32 v137, 0xbfb8aa3b, v146
	v_exp_f32_e32 v137, v137
	s_nop 0
	v_add_f32_e32 v137, 1.0, v137
	v_rcp_f32_e32 v150, v137
	v_mul_f32_e32 v137, 0xbfb8aa3b, v143
	v_exp_f32_e32 v137, v137
	s_nop 0
	v_add_f32_e32 v137, 1.0, v137
	v_rcp_f32_e32 v149, v137
	v_mul_f32_e32 v137, 0xbfb8aa3b, v147
	v_exp_f32_e32 v137, v137
	v_mul_f32_e64 v142, v142, v148
	v_mul_f32_e64 v143, v143, v149
	v_add_f32_e32 v137, 1.0, v137
	v_rcp_f32_e32 v151, v137
	v_mul_f32_e32 v137, 0xbfb8aa3b, v140
	v_exp_f32_e32 v137, v137
	v_mul_f32_e64 v146, v146, v150
	v_mul_f32_e64 v147, v147, v151
	v_add_f32_e32 v137, 1.0, v137
	v_rcp_f32_e32 v148, v137
	v_mul_f32_e32 v137, 0xbfb8aa3b, v144
	v_exp_f32_e32 v137, v137
	s_nop 0
	v_add_f32_e32 v137, 1.0, v137
	v_rcp_f32_e32 v150, v137
	v_mul_f32_e32 v137, 0xbfb8aa3b, v141
	v_exp_f32_e32 v137, v137
	s_nop 0
	v_add_f32_e32 v137, 1.0, v137
	v_rcp_f32_e32 v149, v137
	v_mul_f32_e32 v137, 0xbfb8aa3b, v145
	v_exp_f32_e32 v137, v137
	v_mul_f32_e64 v148, v140, v148
	v_mul_f32_e64 v149, v141, v149
	v_cvt_pk_bf16_f32 v140, v142, v143
	v_add_f32_e32 v137, 1.0, v137
	v_rcp_f32_e32 v151, v137
	v_cvt_pk_bf16_f32 v141, v148, v149
	v_cvt_pk_bf16_f32 v142, v146, v147
	v_mul_f32_e64 v144, v144, v150
	v_mul_f32_e64 v145, v145, v151
	s_nop 0
	v_cvt_pk_bf16_f32 v143, v144, v145
	global_store_dwordx4 v[134:135], v[140:143], off
	v_fma_f32 v144, v78, v136, 0
	v_fma_f32 v145, v79, v136, 0
	s_nop 0
	v_fma_f32 v142, v80, v136, 0
	v_fma_f32 v143, v81, v136, 0
	v_fma_f32 v140, v82, v136, 0
	v_fma_f32 v141, v83, v136, 0
	v_mul_f32_e32 v139, 0xbfb8aa3b, v142
	v_exp_f32_e32 v139, v139
	v_fma_f32 v137, v77, v136, 0
	v_fma_f32 v136, v76, v136, 0
	v_add_f32_e32 v139, 1.0, v139
	v_rcp_f32_e32 v146, v139
	v_mul_f32_e32 v139, 0xbfb8aa3b, v136
	v_exp_f32_e32 v139, v139
	s_nop 0
	v_add_f32_e32 v139, 1.0, v139
	v_rcp_f32_e32 v148, v139
	v_mul_f32_e32 v139, 0xbfb8aa3b, v143
	v_exp_f32_e32 v139, v139
	s_nop 0
	v_add_f32_e32 v139, 1.0, v139
	v_rcp_f32_e32 v147, v139
	v_mul_f32_e32 v139, 0xbfb8aa3b, v137
	v_exp_f32_e32 v139, v139
	v_mul_f32_e64 v142, v142, v146
	v_mul_f32_e64 v143, v143, v147
	v_add_f32_e32 v139, 1.0, v139
	v_rcp_f32_e32 v149, v139
	v_mul_f32_e32 v139, 0xbfb8aa3b, v140
	v_exp_f32_e32 v139, v139
	v_mul_f32_e64 v136, v136, v148
	v_mul_f32_e64 v137, v137, v149
	v_add_f32_e32 v139, 1.0, v139
	v_rcp_f32_e32 v146, v139
	v_mul_f32_e32 v139, 0xbfb8aa3b, v144
	v_exp_f32_e32 v139, v139
	s_nop 0
	v_add_f32_e32 v139, 1.0, v139
	v_rcp_f32_e32 v148, v139
	v_mul_f32_e32 v139, 0xbfb8aa3b, v141
	v_exp_f32_e32 v139, v139
	s_nop 0
	v_add_f32_e32 v139, 1.0, v139
	v_rcp_f32_e32 v147, v139
	v_mul_f32_e32 v139, 0xbfb8aa3b, v145
	v_exp_f32_e32 v139, v139
	v_mul_f32_e64 v146, v140, v146
	v_mul_f32_e64 v147, v141, v147
	v_cvt_pk_bf16_f32 v140, v142, v143
	v_add_f32_e32 v139, 1.0, v139
	v_rcp_f32_e32 v149, v139
	v_cvt_pk_bf16_f32 v142, v136, v137
	ds_read2_b32 v[136:137], v199 offset0:64 offset1:80
	v_cvt_pk_bf16_f32 v141, v146, v147
	v_mul_f32_e64 v144, v144, v148
	v_mul_f32_e64 v145, v145, v149
	s_waitcnt lgkmcnt(0)
	v_fma_f32 v146, v52, v136, 0
	v_fma_f32 v147, v53, v136, 0
	v_cvt_pk_bf16_f32 v143, v144, v145
	global_store_dwordx4 v[134:135], v[140:143], off offset:256
	v_fma_f32 v144, v54, v136, 0
	v_fma_f32 v145, v55, v136, 0
	v_add_u32_e32 v134, 0x80, v138
	v_fma_f32 v142, v56, v136, 0
	v_fma_f32 v143, v57, v136, 0
	v_fma_f32 v140, v58, v136, 0
	v_fma_f32 v141, v59, v136, 0
	v_mul_f32_e32 v139, 0xbfb8aa3b, v142
	v_exp_f32_e32 v139, v139
	v_mad_i64_i32 v[134:135], s[2:3], v134, s81, v[132:133]
	v_add_f32_e32 v139, 1.0, v139
	v_rcp_f32_e32 v148, v139
	v_mul_f32_e32 v139, 0xbfb8aa3b, v146
	v_exp_f32_e32 v139, v139
	s_nop 0
	v_add_f32_e32 v139, 1.0, v139
	v_rcp_f32_e32 v150, v139
	v_mul_f32_e32 v139, 0xbfb8aa3b, v143
	v_exp_f32_e32 v139, v139
	s_nop 0
	v_add_f32_e32 v139, 1.0, v139
	v_rcp_f32_e32 v149, v139
	v_mul_f32_e32 v139, 0xbfb8aa3b, v147
	v_exp_f32_e32 v139, v139
	v_mul_f32_e64 v142, v142, v148
	v_mul_f32_e64 v143, v143, v149
	v_add_f32_e32 v139, 1.0, v139
	v_rcp_f32_e32 v151, v139
	v_mul_f32_e32 v139, 0xbfb8aa3b, v140
	v_exp_f32_e32 v139, v139
	v_mul_f32_e64 v146, v146, v150
	v_mul_f32_e64 v147, v147, v151
	v_add_f32_e32 v139, 1.0, v139
	v_rcp_f32_e32 v148, v139
	v_mul_f32_e32 v139, 0xbfb8aa3b, v144
	v_exp_f32_e32 v139, v139
	s_nop 0
	v_add_f32_e32 v139, 1.0, v139
	v_rcp_f32_e32 v150, v139
	v_mul_f32_e32 v139, 0xbfb8aa3b, v141
	v_exp_f32_e32 v139, v139
	s_nop 0
	v_add_f32_e32 v139, 1.0, v139
	v_rcp_f32_e32 v149, v139
	v_mul_f32_e32 v139, 0xbfb8aa3b, v145
	v_exp_f32_e32 v139, v139
	v_mul_f32_e64 v148, v140, v148
	v_mul_f32_e64 v149, v141, v149
	v_cvt_pk_bf16_f32 v140, v142, v143
	v_add_f32_e32 v139, 1.0, v139
	v_rcp_f32_e32 v151, v139
	v_cvt_pk_bf16_f32 v141, v148, v149
	v_cvt_pk_bf16_f32 v142, v146, v147
	v_fma_f32 v146, v60, v136, 0
	v_fma_f32 v147, v61, v136, 0
	v_mul_f32_e64 v144, v144, v150
	v_mul_f32_e64 v145, v145, v151
	s_nop 0
	v_cvt_pk_bf16_f32 v143, v144, v145
	global_store_dwordx4 v[134:135], v[140:143], off
	v_fma_f32 v144, v62, v136, 0
	v_fma_f32 v145, v63, v136, 0
	s_nop 0
	v_fma_f32 v142, v64, v136, 0
	v_fma_f32 v143, v65, v136, 0
	v_fma_f32 v140, v66, v136, 0
	v_fma_f32 v141, v67, v136, 0
	v_mul_f32_e32 v136, 0xbfb8aa3b, v142
	v_exp_f32_e32 v136, v136
	s_nop 0
	v_add_f32_e32 v136, 1.0, v136
	v_rcp_f32_e32 v148, v136
	v_mul_f32_e32 v136, 0xbfb8aa3b, v146
	v_exp_f32_e32 v136, v136
	s_nop 0
	v_add_f32_e32 v136, 1.0, v136
	v_rcp_f32_e32 v150, v136
	v_mul_f32_e32 v136, 0xbfb8aa3b, v143
	v_exp_f32_e32 v136, v136
; __device__ __forceinline__ unsigned cvt_pk_bf16(float lo, float hi) { f32x2_c v = {lo, hi}; bf16x2_c b = __builtin_convertvector(v, bf16x2_c); return __builtin_bit_cast(unsigned, b); }
; __device__ __forceinline__ float silu_f(float g) { return g * __builtin_amdgcn_rcpf(1.0f + __builtin_amdgcn_exp2f(-1.44269504f * g)); }
;     template <int TT> __device__ __forceinline__ void other(const f32x4 (&acc)[2][2][4][2], bf16_t* base, int row0, int col0, PG8_LAS float* my, int t, int hh, int wc, int fq) const {
;     ...
;                 for (int bj = 0; bj < 2; ++bj) { f32x4 v0 = acc[ai][bj][m][0] * rs + bv[bj][0], v1 = acc[ai][bj][m][1] * rs + bv[bj][1];
;                     if (TT == 3) {
; #pragma unroll
;                         for (int j = 0; j < 4; ++j) { v0[j] = silu_f(v0[j]); v1[j] = silu_f(v1[j]); } }
;     ...
;                     else { u32x4 w; w.x = cvt_pk_bf16(v0[0], v0[1]); w.y = cvt_pk_bf16(v0[2], v0[3]); w.z = cvt_pk_bf16(v1[0], v1[1]); w.w = cvt_pk_bf16(v1[2], v1[3]);
;                         *(u32x4*)(rowp + bj * HALF) = w; } }
	s_nop 0
	v_add_f32_e32 v136, 1.0, v136
	v_rcp_f32_e32 v149, v136
	v_mul_f32_e32 v136, 0xbfb8aa3b, v147
	v_exp_f32_e32 v136, v136
	v_mul_f32_e64 v142, v142, v148
	v_mul_f32_e64 v143, v143, v149
	v_add_f32_e32 v136, 1.0, v136
	v_rcp_f32_e32 v151, v136
	v_mul_f32_e32 v136, 0xbfb8aa3b, v140
	v_exp_f32_e32 v136, v136
	v_mul_f32_e64 v146, v146, v150
	v_mul_f32_e64 v147, v147, v151
	v_add_f32_e32 v136, 1.0, v136
	v_rcp_f32_e32 v148, v136
	v_mul_f32_e32 v136, 0xbfb8aa3b, v144
	v_exp_f32_e32 v136, v136
	s_nop 0
	v_add_f32_e32 v136, 1.0, v136
	v_rcp_f32_e32 v150, v136
	v_mul_f32_e32 v136, 0xbfb8aa3b, v141
	v_exp_f32_e32 v136, v136
	s_nop 0
	v_add_f32_e32 v136, 1.0, v136
	v_rcp_f32_e32 v149, v136
	v_mul_f32_e32 v136, 0xbfb8aa3b, v145
	v_exp_f32_e32 v136, v136
	v_mul_f32_e64 v148, v140, v148
	v_mul_f32_e64 v149, v141, v149
	v_cvt_pk_bf16_f32 v140, v142, v143
	v_add_f32_e32 v136, 1.0, v136
	v_rcp_f32_e32 v151, v136
	v_cvt_pk_bf16_f32 v141, v148, v149
	v_cvt_pk_bf16_f32 v142, v146, v147
	v_mov_b32_e32 v136, v137
	v_mul_f32_e64 v144, v144, v150
	v_mul_f32_e64 v145, v145, v151
	v_fma_f32 v146, v36, v136, 0
	v_fma_f32 v147, v37, v136, 0
	v_cvt_pk_bf16_f32 v143, v144, v145
	global_store_dwordx4 v[134:135], v[140:143], off offset:256
	v_fma_f32 v144, v38, v136, 0
	v_fma_f32 v145, v39, v136, 0
	v_add_u32_e32 v134, 0x90, v138
	v_fma_f32 v142, v40, v136, 0
	v_fma_f32 v143, v41, v136, 0
	v_fma_f32 v140, v42, v136, 0
	v_fma_f32 v141, v43, v136, 0
	v_mul_f32_e32 v137, 0xbfb8aa3b, v142
	v_exp_f32_e32 v137, v137
	v_mad_i64_i32 v[134:135], s[2:3], v134, s81, v[132:133]
	v_add_f32_e32 v137, 1.0, v137
	v_rcp_f32_e32 v148, v137
	v_mul_f32_e32 v137, 0xbfb8aa3b, v146
	v_exp_f32_e32 v137, v137
	s_nop 0
	v_add_f32_e32 v137, 1.0, v137
	v_rcp_f32_e32 v150, v137
	v_mul_f32_e32 v137, 0xbfb8aa3b, v143
	v_exp_f32_e32 v137, v137
	s_nop 0
	v_add_f32_e32 v137, 1.0, v137
	v_rcp_f32_e32 v149, v137
	v_mul_f32_e32 v137, 0xbfb8aa3b, v147
	v_exp_f32_e32 v137, v137
	v_mul_f32_e64 v142, v142, v148
	v_mul_f32_e64 v143, v143, v149
	v_add_f32_e32 v137, 1.0, v137
	v_rcp_f32_e32 v151, v137
	v_mul_f32_e32 v137, 0xbfb8aa3b, v140
	v_exp_f32_e32 v137, v137
	v_mul_f32_e64 v146, v146, v150
	v_mul_f32_e64 v147, v147, v151
	v_add_f32_e32 v137, 1.0, v137
	v_rcp_f32_e32 v148, v137
	v_mul_f32_e32 v137, 0xbfb8aa3b, v144
	v_exp_f32_e32 v137, v137
	s_nop 0
	v_add_f32_e32 v137, 1.0, v137
	v_rcp_f32_e32 v150, v137
	v_mul_f32_e32 v137, 0xbfb8aa3b, v141
	v_exp_f32_e32 v137, v137
	s_nop 0
	v_add_f32_e32 v137, 1.0, v137
	v_rcp_f32_e32 v149, v137
	v_mul_f32_e32 v137, 0xbfb8aa3b, v145
	v_exp_f32_e32 v137, v137
	v_mul_f32_e64 v148, v140, v148
	v_mul_f32_e64 v149, v141, v149
	v_cvt_pk_bf16_f32 v140, v142, v143
	v_add_f32_e32 v137, 1.0, v137
	v_rcp_f32_e32 v151, v137
	v_cvt_pk_bf16_f32 v141, v148, v149
	v_cvt_pk_bf16_f32 v142, v146, v147
	v_mul_f32_e64 v144, v144, v150
	v_mul_f32_e64 v145, v145, v151
	s_nop 0
	v_cvt_pk_bf16_f32 v143, v144, v145
	global_store_dwordx4 v[134:135], v[140:143], off
	v_fma_f32 v144, v46, v136, 0
	v_fma_f32 v145, v47, v136, 0
	s_nop 0
	v_fma_f32 v142, v48, v136, 0
	v_fma_f32 v143, v49, v136, 0
	v_fma_f32 v140, v50, v136, 0
	v_fma_f32 v141, v51, v136, 0
	v_mul_f32_e32 v139, 0xbfb8aa3b, v142
	v_exp_f32_e32 v139, v139
	v_fma_f32 v137, v45, v136, 0
	v_fma_f32 v136, v44, v136, 0
	v_add_f32_e32 v139, 1.0, v139
	v_rcp_f32_e32 v146, v139
	v_mul_f32_e32 v139, 0xbfb8aa3b, v136
	v_exp_f32_e32 v139, v139
	s_nop 0
	v_add_f32_e32 v139, 1.0, v139
	v_rcp_f32_e32 v148, v139
	v_mul_f32_e32 v139, 0xbfb8aa3b, v143
	v_exp_f32_e32 v139, v139
	s_nop 0
	v_add_f32_e32 v139, 1.0, v139
	v_rcp_f32_e32 v147, v139
	v_mul_f32_e32 v139, 0xbfb8aa3b, v137
	v_exp_f32_e32 v139, v139
	v_mul_f32_e64 v142, v142, v146
	v_mul_f32_e64 v143, v143, v147
	v_add_f32_e32 v139, 1.0, v139
	v_rcp_f32_e32 v149, v139
	v_mul_f32_e32 v139, 0xbfb8aa3b, v140
	v_exp_f32_e32 v139, v139
	v_mul_f32_e64 v136, v136, v148
	v_mul_f32_e64 v137, v137, v149
	v_add_f32_e32 v139, 1.0, v139
	v_rcp_f32_e32 v146, v139
	v_mul_f32_e32 v139, 0xbfb8aa3b, v144
	v_exp_f32_e32 v139, v139
	s_nop 0
	v_add_f32_e32 v139, 1.0, v139
	v_rcp_f32_e32 v148, v139
	v_mul_f32_e32 v139, 0xbfb8aa3b, v141
	v_exp_f32_e32 v139, v139
	s_nop 0
	v_add_f32_e32 v139, 1.0, v139
	v_rcp_f32_e32 v147, v139
	v_mul_f32_e32 v139, 0xbfb8aa3b, v145
	v_exp_f32_e32 v139, v139
	v_mul_f32_e64 v146, v140, v146
	v_mul_f32_e64 v147, v141, v147
	v_cvt_pk_bf16_f32 v140, v142, v143
	v_add_f32_e32 v139, 1.0, v139
	v_rcp_f32_e32 v149, v139
	v_cvt_pk_bf16_f32 v142, v136, v137
	ds_read2_b32 v[136:137], v199 offset0:96 offset1:112
	v_cvt_pk_bf16_f32 v141, v146, v147
	v_mul_f32_e64 v144, v144, v148
	v_mul_f32_e64 v145, v145, v149
	s_waitcnt lgkmcnt(0)
; __device__ __forceinline__ unsigned cvt_pk_bf16(float lo, float hi) { f32x2_c v = {lo, hi}; bf16x2_c b = __builtin_convertvector(v, bf16x2_c); return __builtin_bit_cast(unsigned, b); }
; __device__ __forceinline__ float silu_f(float g) { return g * __builtin_amdgcn_rcpf(1.0f + __builtin_amdgcn_exp2f(-1.44269504f * g)); }
;     template <int TT> __device__ __forceinline__ void other(const f32x4 (&acc)[2][2][4][2], bf16_t* base, int row0, int col0, PG8_LAS float* my, int t, int hh, int wc, int fq) const {
;     ...
;                 for (int bj = 0; bj < 2; ++bj) { f32x4 v0 = acc[ai][bj][m][0] * rs + bv[bj][0], v1 = acc[ai][bj][m][1] * rs + bv[bj][1];
;                     if (TT == 3) {
; #pragma unroll
;                         for (int j = 0; j < 4; ++j) { v0[j] = silu_f(v0[j]); v1[j] = silu_f(v1[j]); } }
;     ...
;                     else { u32x4 w; w.x = cvt_pk_bf16(v0[0], v0[1]); w.y = cvt_pk_bf16(v0[2], v0[3]); w.z = cvt_pk_bf16(v1[0], v1[1]); w.w = cvt_pk_bf16(v1[2], v1[3]);
;                         *(u32x4*)(rowp + bj * HALF) = w; } }
	v_fma_f32 v146, v20, v136, 0
	v_fma_f32 v147, v21, v136, 0
	v_cvt_pk_bf16_f32 v143, v144, v145
	global_store_dwordx4 v[134:135], v[140:143], off offset:256
	v_fma_f32 v144, v22, v136, 0
	v_fma_f32 v145, v23, v136, 0
	v_add_u32_e32 v134, 0xa0, v138
	v_fma_f32 v142, v24, v136, 0
	v_fma_f32 v143, v25, v136, 0
	v_fma_f32 v140, v26, v136, 0
	v_fma_f32 v141, v27, v136, 0
	v_mul_f32_e32 v139, 0xbfb8aa3b, v142
	v_exp_f32_e32 v139, v139
	v_mad_i64_i32 v[134:135], s[2:3], v134, s81, v[132:133]
	v_add_f32_e32 v139, 1.0, v139
	v_rcp_f32_e32 v148, v139
	v_mul_f32_e32 v139, 0xbfb8aa3b, v146
	v_exp_f32_e32 v139, v139
	s_nop 0
	v_add_f32_e32 v139, 1.0, v139
	v_rcp_f32_e32 v150, v139
	v_mul_f32_e32 v139, 0xbfb8aa3b, v143
	v_exp_f32_e32 v139, v139
	s_nop 0
	v_add_f32_e32 v139, 1.0, v139
	v_rcp_f32_e32 v149, v139
	v_mul_f32_e32 v139, 0xbfb8aa3b, v147
	v_exp_f32_e32 v139, v139
	v_mul_f32_e64 v142, v142, v148
	v_mul_f32_e64 v143, v143, v149
	v_add_f32_e32 v139, 1.0, v139
	v_rcp_f32_e32 v151, v139
	v_mul_f32_e32 v139, 0xbfb8aa3b, v140
	v_exp_f32_e32 v139, v139
	v_mul_f32_e64 v146, v146, v150
	v_mul_f32_e64 v147, v147, v151
	v_add_f32_e32 v139, 1.0, v139
	v_rcp_f32_e32 v148, v139
	v_mul_f32_e32 v139, 0xbfb8aa3b, v144
	v_exp_f32_e32 v139, v139
	s_nop 0
	v_add_f32_e32 v139, 1.0, v139
	v_rcp_f32_e32 v150, v139
	v_mul_f32_e32 v139, 0xbfb8aa3b, v141
	v_exp_f32_e32 v139, v139
	s_nop 0
	v_add_f32_e32 v139, 1.0, v139
	v_rcp_f32_e32 v149, v139
	v_mul_f32_e32 v139, 0xbfb8aa3b, v145
	v_exp_f32_e32 v139, v139
	v_mul_f32_e64 v148, v140, v148
	v_mul_f32_e64 v149, v141, v149
	v_cvt_pk_bf16_f32 v140, v142, v143
	v_add_f32_e32 v139, 1.0, v139
	v_rcp_f32_e32 v151, v139
	v_cvt_pk_bf16_f32 v141, v148, v149
	v_cvt_pk_bf16_f32 v142, v146, v147
	v_fma_f32 v146, v28, v136, 0
	v_fma_f32 v147, v29, v136, 0
	v_mul_f32_e64 v144, v144, v150
	v_mul_f32_e64 v145, v145, v151
	s_nop 0
	v_cvt_pk_bf16_f32 v143, v144, v145
	global_store_dwordx4 v[134:135], v[140:143], off
	v_fma_f32 v144, v30, v136, 0
	v_fma_f32 v145, v31, v136, 0
	s_nop 0
	v_fma_f32 v142, v32, v136, 0
	v_fma_f32 v143, v33, v136, 0
	v_fma_f32 v140, v34, v136, 0
	v_fma_f32 v141, v35, v136, 0
	v_mul_f32_e32 v136, 0xbfb8aa3b, v142
	v_exp_f32_e32 v136, v136
	s_nop 0
	v_add_f32_e32 v136, 1.0, v136
	v_rcp_f32_e32 v148, v136
	v_mul_f32_e32 v136, 0xbfb8aa3b, v146
	v_exp_f32_e32 v136, v136
	s_nop 0
	v_add_f32_e32 v136, 1.0, v136
	v_rcp_f32_e32 v150, v136
	v_mul_f32_e32 v136, 0xbfb8aa3b, v143
	v_exp_f32_e32 v136, v136
	s_nop 0
	v_add_f32_e32 v136, 1.0, v136
	v_rcp_f32_e32 v149, v136
	v_mul_f32_e32 v136, 0xbfb8aa3b, v147
	v_exp_f32_e32 v136, v136
	v_mul_f32_e64 v142, v142, v148
	v_mul_f32_e64 v143, v143, v149
	v_add_f32_e32 v136, 1.0, v136
	v_rcp_f32_e32 v151, v136
	v_mul_f32_e32 v136, 0xbfb8aa3b, v140
	v_exp_f32_e32 v136, v136
	v_mul_f32_e64 v146, v146, v150
	v_mul_f32_e64 v147, v147, v151
	v_add_f32_e32 v136, 1.0, v136
	v_rcp_f32_e32 v148, v136
	v_mul_f32_e32 v136, 0xbfb8aa3b, v144
	v_exp_f32_e32 v136, v136
	s_nop 0
	v_add_f32_e32 v136, 1.0, v136
	v_rcp_f32_e32 v150, v136
	v_mul_f32_e32 v136, 0xbfb8aa3b, v141
	v_exp_f32_e32 v136, v136
	s_nop 0
	v_add_f32_e32 v136, 1.0, v136
	v_rcp_f32_e32 v149, v136
	v_mul_f32_e32 v136, 0xbfb8aa3b, v145
	v_exp_f32_e32 v136, v136
	v_mul_f32_e64 v148, v140, v148
	v_mul_f32_e64 v149, v141, v149
	v_cvt_pk_bf16_f32 v140, v142, v143
	v_add_f32_e32 v136, 1.0, v136
	v_rcp_f32_e32 v151, v136
	v_cvt_pk_bf16_f32 v141, v148, v149
	v_cvt_pk_bf16_f32 v142, v146, v147
	v_mul_f32_e64 v144, v144, v150
	v_mul_f32_e64 v145, v145, v151
	s_nop 0
	v_cvt_pk_bf16_f32 v143, v144, v145
; __device__ __forceinline__ unsigned cvt_pk_bf16(float lo, float hi) { f32x2_c v = {lo, hi}; bf16x2_c b = __builtin_convertvector(v, bf16x2_c); return __builtin_bit_cast(unsigned, b); }
; __device__ __forceinline__ float silu_f(float g) { return g * __builtin_amdgcn_rcpf(1.0f + __builtin_amdgcn_exp2f(-1.44269504f * g)); }
;     template <int TT> __device__ __forceinline__ void other(const f32x4 (&acc)[2][2][4][2], bf16_t* base, int row0, int col0, PG8_LAS float* my, int t, int hh, int wc, int fq) const {
;     ...
;                 for (int bj = 0; bj < 2; ++bj) { f32x4 v0 = acc[ai][bj][m][0] * rs + bv[bj][0], v1 = acc[ai][bj][m][1] * rs + bv[bj][1];
;                     if (TT == 3) {
; #pragma unroll
;                         for (int j = 0; j < 4; ++j) { v0[j] = silu_f(v0[j]); v1[j] = silu_f(v1[j]); } }
;     ...
;                     else { u32x4 w; w.x = cvt_pk_bf16(v0[0], v0[1]); w.y = cvt_pk_bf16(v0[2], v0[3]); w.z = cvt_pk_bf16(v1[0], v1[1]); w.w = cvt_pk_bf16(v1[2], v1[3]);
;                         *(u32x4*)(rowp + bj * HALF) = w; } }
	global_store_dwordx4 v[134:135], v[140:143], off offset:256
	v_add_u32_e32 v134, 0xb0, v138
	v_mov_b32_e32 v138, v137
	v_fma_f32 v136, v8, v138, 0
	v_fma_f32 v137, v9, v138, 0
	v_mad_i64_i32 v[132:133], s[2:3], v134, s81, v[132:133]
	v_fma_f32 v134, v10, v138, 0
	v_fma_f32 v135, v11, v138, 0
	v_fma_f32 v140, v6, v138, 0
	v_fma_f32 v141, v7, v138, 0
	v_fma_f32 v142, v4, v138, 0
	v_fma_f32 v143, v5, v138, 0
	v_mul_f32_e32 v139, 0xbfb8aa3b, v136
	v_exp_f32_e32 v139, v139
	s_nop 0
	v_add_f32_e32 v139, 1.0, v139
	v_rcp_f32_e32 v144, v139
	v_mul_f32_e32 v139, 0xbfb8aa3b, v142
	v_exp_f32_e32 v139, v139
	s_nop 0
	v_add_f32_e32 v139, 1.0, v139
	v_rcp_f32_e32 v146, v139
	v_mul_f32_e32 v139, 0xbfb8aa3b, v137
	v_exp_f32_e32 v139, v139
	s_nop 0
	v_add_f32_e32 v139, 1.0, v139
	v_rcp_f32_e32 v145, v139
	v_mul_f32_e32 v139, 0xbfb8aa3b, v143
	v_exp_f32_e32 v139, v139
	v_mul_f32_e64 v136, v136, v144
	v_mul_f32_e64 v137, v137, v145
	v_add_f32_e32 v139, 1.0, v139
	v_rcp_f32_e32 v147, v139
	v_mul_f32_e32 v139, 0xbfb8aa3b, v134
	v_exp_f32_e32 v139, v139
	v_mul_f32_e64 v142, v142, v146
	v_mul_f32_e64 v143, v143, v147
	v_add_f32_e32 v139, 1.0, v139
	v_rcp_f32_e32 v144, v139
	v_mul_f32_e32 v139, 0xbfb8aa3b, v140
	v_exp_f32_e32 v139, v139
	s_nop 0
	v_add_f32_e32 v139, 1.0, v139
	v_rcp_f32_e32 v146, v139
	v_mul_f32_e32 v139, 0xbfb8aa3b, v135
	v_exp_f32_e32 v139, v139
	s_nop 0
	v_add_f32_e32 v139, 1.0, v139
	v_rcp_f32_e32 v145, v139
	s_nop 0
	v_mul_f32_e64 v144, v134, v144
	v_mul_f32_e64 v145, v135, v145
	v_mul_f32_e32 v134, 0xbfb8aa3b, v141
	v_exp_f32_e32 v134, v134
	v_cvt_pk_bf16_f32 v135, v144, v145
	v_add_f32_e32 v134, 1.0, v134
	v_rcp_f32_e32 v147, v134
	v_cvt_pk_bf16_f32 v134, v136, v137
	v_cvt_pk_bf16_f32 v136, v142, v143
	v_mul_f32_e64 v140, v140, v146
	v_mul_f32_e64 v141, v141, v147
	s_nop 0
	v_cvt_pk_bf16_f32 v137, v140, v141
	global_store_dwordx4 v[132:133], v[134:137], off
	v_fma_f32 v140, v14, v138, 0
	v_fma_f32 v141, v15, v138, 0
	s_nop 0
	v_fma_f32 v134, v18, v138, 0
	v_fma_f32 v135, v19, v138, 0
	v_fma_f32 v136, v16, v138, 0
	v_fma_f32 v137, v17, v138, 0
	v_fma_f32 v139, v13, v138, 0
	v_fma_f32 v138, v12, v138, 0
	v_mul_f32_e32 v142, 0xbfb8aa3b, v136
	v_mul_f32_e32 v143, 0xbfb8aa3b, v138
	v_exp_f32_e32 v143, v143
	v_exp_f32_e32 v142, v142
	v_add_f32_e32 v143, 1.0, v143
	v_rcp_f32_e32 v144, v143
	v_mul_f32_e32 v143, 0xbfb8aa3b, v137
	v_exp_f32_e32 v143, v143
	v_add_f32_e32 v142, 1.0, v142
	v_rcp_f32_e32 v142, v142
	v_add_f32_e32 v143, 1.0, v143
	v_rcp_f32_e32 v143, v143
	s_nop 0
	v_mul_f32_e64 v136, v136, v142
	v_mul_f32_e64 v137, v137, v143
	v_mul_f32_e32 v142, 0xbfb8aa3b, v139
	v_exp_f32_e32 v142, v142
	v_mul_f32_e32 v143, 0xbfb8aa3b, v140
	v_exp_f32_e32 v143, v143
	v_add_f32_e32 v142, 1.0, v142
	v_rcp_f32_e32 v145, v142
	v_add_f32_e32 v143, 1.0, v143
	v_mul_f32_e32 v142, 0xbfb8aa3b, v134
	v_exp_f32_e32 v142, v142
	v_mul_f32_e64 v138, v138, v144
	v_mul_f32_e64 v139, v139, v145
	v_rcp_f32_e32 v144, v143
	v_mul_f32_e32 v143, 0xbfb8aa3b, v135
	v_exp_f32_e32 v143, v143
	v_add_f32_e32 v142, 1.0, v142
	v_rcp_f32_e32 v142, v142
	v_add_f32_e32 v143, 1.0, v143
	v_rcp_f32_e32 v143, v143
	s_nop 0
	v_mul_f32_e64 v142, v134, v142
	v_mul_f32_e64 v143, v135, v143
	v_mul_f32_e32 v134, 0xbfb8aa3b, v141
	v_exp_f32_e32 v134, v134
	v_cvt_pk_bf16_f32 v135, v142, v143
	v_add_f32_e32 v134, 1.0, v134
	v_rcp_f32_e32 v145, v134
	v_cvt_pk_bf16_f32 v134, v136, v137
	v_cvt_pk_bf16_f32 v136, v138, v139
	v_mul_f32_e64 v140, v140, v144
	v_mul_f32_e64 v141, v141, v145
	s_nop 0
	v_cvt_pk_bf16_f32 v137, v140, v141
	global_store_dwordx4 v[132:133], v[134:137], off offset:256

;     __device__ __forceinline__ void operator()(const f32x4 (&acc)[2][2][4][2], const Unit& u, int wr, int wc, int fr, int fq) const {
;     ...
;         if (t <= 1) {
;             const float sc = (t == 1) ? 0.0625f : 1.0f, lgs = (t == 1) ? -lg2_gamma_h(hh) : lg2_gamma_h(hh);
; #pragma unroll
;             for (int ai = 0; ai < 2; ++ai) {
;                 u32x4 cv[4][2];
; #pragma unroll
;                 for (int m = 0; m < 4; ++m) { const u32x4* cp = (const u32x4*)(cs + ((size_t)(row0 + ai * HALF + m * 16) * 128 + cw));
;                     cv[m][0] = cp[0]; cv[m][1] = cp[1]; }
; #pragma unroll
;                 for (int m = 0; m < 4; ++m) { const int row = row0 + ai * HALF + m * 16;
;                     int rl = row; asm volatile("" : "+v"(rl));
;                     const float rs = my[(ai * 4 + m) * 16] * sc * __builtin_amdgcn_exp2f((float)((rl & 127) + 1) * lgs);
;                     const f32x4 xa0 = acc[ai][0][m][0] * rs, xa1 = acc[ai][0][m][1] * rs, xb0 = acc[ai][1][m][0] * rs, xb1 = acc[ai][1][m][1] * rs;
;                     const unsigned cw8[8] = {cv[m][0].x, cv[m][0].y, cv[m][0].z, cv[m][0].w, cv[m][1].x, cv[m][1].y, cv[m][1].z, cv[m][1].w};
;                     float co[8], si[8];
; #pragma unroll
;                     for (int j = 0; j < 8; ++j) { const h2_t hv = __builtin_bit_cast(h2_t, cw8[j]); co[j] = (float)hv.x; si[j] = (float)hv.y; }
;                     const float x1[8] = {xa0[0], xa0[1], xa0[2], xa0[3], xa1[0], xa1[1], xa1[2], xa1[3]};
;                     const float x2[8] = {xb0[0], xb0[1], xb0[2], xb0[3], xb1[0], xb1[1], xb1[2], xb1[3]};
;                     float o1[8], o2[8];
; #pragma unroll
;                     for (int j = 0; j < 8; ++j) { o1[j] = x1[j] * co[j] - x2[j] * si[j]; o2[j] = x1[j] * si[j] + x2[j] * co[j]; }
;                     u32x4 w1, w2;
;                     w1.x = cvt_pk_bf16(o1[0], o1[1]); w1.y = cvt_pk_bf16(o1[2], o1[3]); w1.z = cvt_pk_bf16(o1[4], o1[5]); w1.w = cvt_pk_bf16(o1[6], o1[7]);
;                     w2.x = cvt_pk_bf16(o2[0], o2[1]); w2.y = cvt_pk_bf16(o2[2], o2[3]); w2.z = cvt_pk_bf16(o2[4], o2[5]); w2.w = cvt_pk_bf16(o2[6], o2[7]);
;                     bf16_t* rowp = base + (size_t)row * LDT + col0;
;                     *(u32x4*)rowp = w1; *(u32x4*)(rowp + HALF) = w2; }
;                 asm volatile("" ::: "memory"); }
.LBB0_363:
	s_and_b32 s2, s44, 56
	s_cmp_eq_u32 s2, 48
	s_cselect_b64 vcc, -1, 0
	v_mov_b32_e32 v132, 0x3d800000
	v_cndmask_b32_e32 v201, 1.0, v132, vcc
	v_cvt_f32_ubyte0_e32 v132, s23
	v_sub_f32_e32 v132, 0xc0a00000, v132
	v_exp_f32_e32 v132, v132
	s_waitcnt lgkmcnt(0)
	v_mov_b32_e32 v133, 0x3e4ccccd
	v_mov_b32_e32 v134, 0xbfb8aa3b
	v_or_b32_e32 v194, 16, v174
	v_fmamk_f32 v133, v132, 0x3e2aaaab, v133
	v_fmaak_f32 v133, v132, v133, 0x3e800000
	v_fmaak_f32 v133, v132, v133, 0x3eaaaaab
	v_fma_f32 v133, v132, v133, 0.5
	v_fma_f32 v133, v132, v133, 1.0
	v_mul_f32_e64 v132, v133, -v132
	v_mov_b32_e32 v133, 0x3fb8aa3b
	v_cndmask_b32_e32 v133, v133, v134, vcc
	v_mul_f32_e32 v202, v133, v132
	v_lshlrev_b32_e32 v132, 1, v158
	v_mov_b32_e32 v133, v2
	v_lshl_add_u64 v[176:177], s[28:29], 0, v[132:133]
	v_lshlrev_b64 v[132:133], 9, v[174:175]
	v_lshl_add_u64 v[132:133], v[170:171], 0, v[132:133]
	global_load_dwordx4 v[156:159], v[132:133], off offset:16
	global_load_dwordx4 v[160:163], v[132:133], off
	v_ashrrev_i32_e32 v195, 31, v194
	v_lshlrev_b64 v[132:133], 9, v[194:195]
	v_lshl_add_u64 v[132:133], v[170:171], 0, v[132:133]
	global_load_dwordx4 v[148:151], v[132:133], off offset:16
	global_load_dwordx4 v[152:155], v[132:133], off
	v_or_b32_e32 v180, 32, v174
	v_ashrrev_i32_e32 v181, 31, v180
	v_lshlrev_b64 v[132:133], 9, v[180:181]
	v_or_b32_e32 v178, 48, v174
	v_lshl_add_u64 v[132:133], v[170:171], 0, v[132:133]
	v_ashrrev_i32_e32 v179, 31, v178
	global_load_dwordx4 v[140:143], v[132:133], off offset:16
	global_load_dwordx4 v[144:147], v[132:133], off
	v_lshlrev_b64 v[132:133], 9, v[178:179]
	v_lshl_add_u64 v[136:137], v[170:171], 0, v[132:133]
	v_mov_b32_e32 v175, v174
	global_load_dwordx4 v[132:135], v[136:137], off offset:16
	s_nop 0
	global_load_dwordx4 v[136:139], v[136:137], off
	ds_read_b32 v179, v199
	v_and_b32_e32 v175, 0x7f, v175
	v_add_u32_e32 v175, 1, v175
	v_cvt_f32_ubyte0_e32 v175, v175
	v_mul_f32_e32 v175, v202, v175
	v_exp_f32_e32 v175, v175
	s_waitcnt lgkmcnt(0)
	v_mul_f32_e32 v179, v201, v179
	v_mul_f32_e32 v182, v179, v175
	v_mul_f32_e64 v122, v122, v182
	v_mul_f32_e64 v123, v123, v182
	v_mul_f32_e64 v120, v120, v182
	v_mul_f32_e64 v121, v121, v182
	v_mul_f32_e64 v118, v118, v182
	v_mul_f32_e64 v119, v119, v182
	v_mul_f32_e64 v116, v116, v182
	v_mul_f32_e64 v117, v117, v182
	v_mul_f32_e64 v130, v130, v182
	v_mul_f32_e64 v131, v131, v182
	v_mul_f32_e64 v128, v128, v182
	v_mul_f32_e64 v129, v129, v182
	v_mul_f32_e64 v126, v126, v182
	v_mul_f32_e64 v127, v127, v182
	v_mul_f32_e64 v124, v124, v182
	v_mul_f32_e64 v125, v125, v182
	s_waitcnt vmcnt(0)
	v_cvt_f32_f16_e32 v183, v161
	v_cvt_f32_f16_e32 v182, v160
	v_cvt_f32_f16_sdwa v161, v161 dst_sel:DWORD dst_unused:UNUSED_PAD src0_sel:WORD_1
	v_cvt_f32_f16_sdwa v160, v160 dst_sel:DWORD dst_unused:UNUSED_PAD src0_sel:WORD_1
	v_mul_f32_e64 v184, v128, v160
	v_mul_f32_e64 v185, v129, v161
	s_nop 0
	v_fma_f32 v184, v120, v182, -v184
	v_fma_f32 v185, v121, v183, -v185
	v_mul_f32_e64 v120, v120, v160
	v_mul_f32_e64 v121, v121, v161
	v_cvt_f32_f16_sdwa v161, v163 dst_sel:DWORD dst_unused:UNUSED_PAD src0_sel:WORD_1
	v_cvt_f32_f16_sdwa v160, v162 dst_sel:DWORD dst_unused:UNUSED_PAD src0_sel:WORD_1
	v_fma_f32 v120, v128, v182, v120
	v_fma_f32 v121, v129, v183, v121
	v_cvt_f32_f16_e32 v129, v163
	v_cvt_f32_f16_e32 v128, v162
	v_mul_f32_e64 v162, v130, v160
	v_mul_f32_e64 v163, v131, v161
	v_cvt_pk_bf16_f32 v120, v120, v121
	v_fma_f32 v162, v122, v128, -v162
	v_fma_f32 v163, v123, v129, -v163
	v_mul_f32_e64 v122, v122, v160
	v_mul_f32_e64 v123, v123, v161
	s_nop 0
	v_fma_f32 v122, v130, v128, v122
	v_fma_f32 v123, v131, v129, v123
	v_cvt_f32_f16_sdwa v131, v157 dst_sel:DWORD dst_unused:UNUSED_PAD src0_sel:WORD_1
	v_cvt_f32_f16_sdwa v130, v156 dst_sel:DWORD dst_unused:UNUSED_PAD src0_sel:WORD_1
	v_cvt_f32_f16_e32 v129, v157
	v_cvt_f32_f16_e32 v128, v156
	v_cvt_pk_bf16_f32 v121, v122, v123
	v_mul_f32_e64 v156, v124, v130
	v_mul_f32_e64 v157, v125, v131
	s_nop 0
	v_fma_f32 v156, v116, v128, -v156
	v_fma_f32 v157, v117, v129, -v157
	v_mul_f32_e64 v116, v116, v130
	v_mul_f32_e64 v117, v117, v131
	s_nop 0
	v_fma_f32 v124, v124, v128, v116
	v_fma_f32 v125, v125, v129, v117
	v_cvt_f32_f16_sdwa v129, v159 dst_sel:DWORD dst_unused:UNUSED_PAD src0_sel:WORD_1
	v_cvt_f32_f16_sdwa v128, v158 dst_sel:DWORD dst_unused:UNUSED_PAD src0_sel:WORD_1
	v_cvt_f32_f16_e32 v117, v159
	v_cvt_f32_f16_e32 v116, v158
	v_cvt_pk_bf16_f32 v122, v124, v125
	v_mul_f32_e64 v130, v126, v128
	v_mul_f32_e64 v131, v127, v129
	v_mad_i64_i32 v[124:125], s[2:3], v174, s81, v[176:177]
	v_fma_f32 v130, v118, v116, -v130
	v_fma_f32 v131, v119, v117, -v131
	v_mul_f32_e64 v118, v118, v128
	v_mul_f32_e64 v119, v119, v129
	s_nop 0
	v_fma_f32 v126, v126, v116, v118
	v_fma_f32 v127, v127, v117, v119
	v_cvt_pk_bf16_f32 v116, v184, v185
	v_cvt_pk_bf16_f32 v117, v162, v163
	v_cvt_pk_bf16_f32 v118, v156, v157
	v_cvt_pk_bf16_f32 v119, v130, v131
	v_cvt_pk_bf16_f32 v123, v126, v127
	global_store_dwordx4 v[124:125], v[116:119], off
	global_store_dwordx4 v[124:125], v[120:123], off offset:256
	s_nop 0
	v_mov_b32_e32 v116, v194
	ds_read_b32 v117, v199 offset:64
	v_and_b32_e32 v116, 0x7f, v116
	v_add_u32_e32 v116, 1, v116
	v_cvt_f32_ubyte0_e32 v116, v116
	v_mul_f32_e32 v116, v202, v116
	v_exp_f32_e32 v116, v116
	s_waitcnt lgkmcnt(0)
;     __device__ __forceinline__ void operator()(const f32x4 (&acc)[2][2][4][2], const Unit& u, int wr, int wc, int fr, int fq) const {
;     ...
;         if (t <= 1) {
;             const float sc = (t == 1) ? 0.0625f : 1.0f, lgs = (t == 1) ? -lg2_gamma_h(hh) : lg2_gamma_h(hh);
; #pragma unroll
;             for (int ai = 0; ai < 2; ++ai) {
;                 u32x4 cv[4][2];
; #pragma unroll
;                 for (int m = 0; m < 4; ++m) { const u32x4* cp = (const u32x4*)(cs + ((size_t)(row0 + ai * HALF + m * 16) * 128 + cw));
;                     cv[m][0] = cp[0]; cv[m][1] = cp[1]; }
; #pragma unroll
;                 for (int m = 0; m < 4; ++m) { const int row = row0 + ai * HALF + m * 16;
;                     int rl = row; asm volatile("" : "+v"(rl));
;                     const float rs = my[(ai * 4 + m) * 16] * sc * __builtin_amdgcn_exp2f((float)((rl & 127) + 1) * lgs);
;                     const f32x4 xa0 = acc[ai][0][m][0] * rs, xa1 = acc[ai][0][m][1] * rs, xb0 = acc[ai][1][m][0] * rs, xb1 = acc[ai][1][m][1] * rs;
;                     const unsigned cw8[8] = {cv[m][0].x, cv[m][0].y, cv[m][0].z, cv[m][0].w, cv[m][1].x, cv[m][1].y, cv[m][1].z, cv[m][1].w};
;                     float co[8], si[8];
; #pragma unroll
;                     for (int j = 0; j < 8; ++j) { const h2_t hv = __builtin_bit_cast(h2_t, cw8[j]); co[j] = (float)hv.x; si[j] = (float)hv.y; }
;                     const float x1[8] = {xa0[0], xa0[1], xa0[2], xa0[3], xa1[0], xa1[1], xa1[2], xa1[3]};
;                     const float x2[8] = {xb0[0], xb0[1], xb0[2], xb0[3], xb1[0], xb1[1], xb1[2], xb1[3]};
;                     float o1[8], o2[8];
; #pragma unroll
;                     for (int j = 0; j < 8; ++j) { o1[j] = x1[j] * co[j] - x2[j] * si[j]; o2[j] = x1[j] * si[j] + x2[j] * co[j]; }
;                     u32x4 w1, w2;
;                     w1.x = cvt_pk_bf16(o1[0], o1[1]); w1.y = cvt_pk_bf16(o1[2], o1[3]); w1.z = cvt_pk_bf16(o1[4], o1[5]); w1.w = cvt_pk_bf16(o1[6], o1[7]);
;                     w2.x = cvt_pk_bf16(o2[0], o2[1]); w2.y = cvt_pk_bf16(o2[2], o2[3]); w2.z = cvt_pk_bf16(o2[4], o2[5]); w2.w = cvt_pk_bf16(o2[6], o2[7]);
;                     bf16_t* rowp = base + (size_t)row * LDT + col0;
;                     *(u32x4*)rowp = w1; *(u32x4*)(rowp + HALF) = w2; }
;                 asm volatile("" ::: "memory"); }
	v_mul_f32_e32 v117, v201, v117
	v_cvt_f32_f16_sdwa v119, v153 dst_sel:DWORD dst_unused:UNUSED_PAD src0_sel:WORD_1
	v_cvt_f32_f16_sdwa v118, v152 dst_sel:DWORD dst_unused:UNUSED_PAD src0_sel:WORD_1
	v_mul_f32_e32 v116, v117, v116
	v_mul_f32_e64 v106, v106, v116
	v_mul_f32_e64 v107, v107, v116
	v_mul_f32_e64 v104, v104, v116
	v_mul_f32_e64 v105, v105, v116
	v_mul_f32_e64 v102, v102, v116
	v_mul_f32_e64 v103, v103, v116
	v_mul_f32_e64 v100, v100, v116
	v_mul_f32_e64 v101, v101, v116
	v_mul_f32_e64 v114, v114, v116
	v_mul_f32_e64 v115, v115, v116
	v_mul_f32_e64 v112, v112, v116
	v_mul_f32_e64 v113, v113, v116
	v_mul_f32_e64 v110, v110, v116
	v_mul_f32_e64 v111, v111, v116
	v_mul_f32_e64 v108, v108, v116
	v_mul_f32_e64 v109, v109, v116
	v_cvt_f32_f16_e32 v117, v153
	v_cvt_f32_f16_e32 v116, v152
	v_mul_f32_e64 v120, v112, v118
	v_mul_f32_e64 v121, v113, v119
	s_nop 0
	v_fma_f32 v120, v104, v116, -v120
	v_fma_f32 v121, v105, v117, -v121
	v_mul_f32_e64 v104, v104, v118
	v_mul_f32_e64 v105, v105, v119
	s_nop 0
	v_fma_f32 v104, v112, v116, v104
	v_fma_f32 v105, v113, v117, v105
	v_cvt_f32_f16_sdwa v117, v155 dst_sel:DWORD dst_unused:UNUSED_PAD src0_sel:WORD_1
	v_cvt_f32_f16_sdwa v116, v154 dst_sel:DWORD dst_unused:UNUSED_PAD src0_sel:WORD_1
	v_cvt_f32_f16_e32 v113, v155
	v_cvt_f32_f16_e32 v112, v154
	v_cvt_pk_bf16_f32 v104, v104, v105
	v_mul_f32_e64 v118, v114, v116
	v_mul_f32_e64 v119, v115, v117
	s_nop 0
	v_fma_f32 v118, v106, v112, -v118
	v_fma_f32 v119, v107, v113, -v119
	v_mul_f32_e64 v106, v106, v116
	v_mul_f32_e64 v107, v107, v117
	s_nop 0
	v_fma_f32 v106, v114, v112, v106
	v_fma_f32 v107, v115, v113, v107
	v_cvt_f32_f16_sdwa v115, v149 dst_sel:DWORD dst_unused:UNUSED_PAD src0_sel:WORD_1
	v_cvt_f32_f16_sdwa v114, v148 dst_sel:DWORD dst_unused:UNUSED_PAD src0_sel:WORD_1
	v_cvt_f32_f16_e32 v113, v149
	v_cvt_f32_f16_e32 v112, v148
	v_cvt_pk_bf16_f32 v105, v106, v107
	v_mul_f32_e64 v116, v108, v114
	v_mul_f32_e64 v117, v109, v115
	s_nop 0
	v_fma_f32 v116, v100, v112, -v116
	v_fma_f32 v117, v101, v113, -v117
	v_mul_f32_e64 v100, v100, v114
	v_mul_f32_e64 v101, v101, v115
	s_nop 0
	v_fma_f32 v108, v108, v112, v100
	v_fma_f32 v109, v109, v113, v101
	v_cvt_f32_f16_sdwa v113, v151 dst_sel:DWORD dst_unused:UNUSED_PAD src0_sel:WORD_1
	v_cvt_f32_f16_sdwa v112, v150 dst_sel:DWORD dst_unused:UNUSED_PAD src0_sel:WORD_1
	v_cvt_f32_f16_e32 v101, v151
	v_cvt_f32_f16_e32 v100, v150
	v_cvt_pk_bf16_f32 v106, v108, v109
	v_mul_f32_e64 v114, v110, v112
	v_mul_f32_e64 v115, v111, v113
	v_mad_i64_i32 v[108:109], s[2:3], v194, s81, v[176:177]
	v_fma_f32 v114, v102, v100, -v114
	v_fma_f32 v115, v103, v101, -v115
	v_mul_f32_e64 v102, v102, v112
	v_mul_f32_e64 v103, v103, v113
	s_nop 0
	v_fma_f32 v110, v110, v100, v102
	v_fma_f32 v111, v111, v101, v103
	v_cvt_pk_bf16_f32 v100, v120, v121
	v_cvt_pk_bf16_f32 v101, v118, v119
	v_cvt_pk_bf16_f32 v102, v116, v117
	v_cvt_pk_bf16_f32 v103, v114, v115
	v_cvt_pk_bf16_f32 v107, v110, v111
	global_store_dwordx4 v[108:109], v[100:103], off
	global_store_dwordx4 v[108:109], v[104:107], off offset:256
	s_nop 0
	v_mov_b32_e32 v100, v180
	ds_read_b32 v101, v199 offset:128
	v_and_b32_e32 v100, 0x7f, v100
	v_add_u32_e32 v100, 1, v100
	v_cvt_f32_ubyte0_e32 v100, v100
	v_mul_f32_e32 v100, v202, v100
	v_exp_f32_e32 v100, v100
	s_waitcnt lgkmcnt(0)
	v_mul_f32_e32 v101, v201, v101
	v_cvt_f32_f16_sdwa v103, v145 dst_sel:DWORD dst_unused:UNUSED_PAD src0_sel:WORD_1
	v_cvt_f32_f16_sdwa v102, v144 dst_sel:DWORD dst_unused:UNUSED_PAD src0_sel:WORD_1
	v_mul_f32_e32 v100, v101, v100
	v_mul_f32_e64 v90, v90, v100
	v_mul_f32_e64 v91, v91, v100
	v_mul_f32_e64 v88, v88, v100
	v_mul_f32_e64 v89, v89, v100
	v_mul_f32_e64 v86, v86, v100
	v_mul_f32_e64 v87, v87, v100
	v_mul_f32_e64 v84, v84, v100
	v_mul_f32_e64 v85, v85, v100
	v_mul_f32_e64 v98, v98, v100
	v_mul_f32_e64 v99, v99, v100
	v_mul_f32_e64 v96, v96, v100
	v_mul_f32_e64 v97, v97, v100
	v_mul_f32_e64 v94, v94, v100
	v_mul_f32_e64 v95, v95, v100
	v_mul_f32_e64 v92, v92, v100
	v_mul_f32_e64 v93, v93, v100
	v_cvt_f32_f16_e32 v101, v145
	v_cvt_f32_f16_e32 v100, v144
	v_mul_f32_e64 v104, v96, v102
	v_mul_f32_e64 v105, v97, v103
	v_add_u32_e32 v106, 0x80, v174
	v_ashrrev_i32_e32 v107, 31, v106
	v_fma_f32 v104, v88, v100, -v104
	v_fma_f32 v105, v89, v101, -v105
	v_mul_f32_e64 v88, v88, v102
	v_mul_f32_e64 v89, v89, v103
	s_nop 0
	v_fma_f32 v88, v96, v100, v88
	v_fma_f32 v89, v97, v101, v89
	v_cvt_f32_f16_sdwa v101, v147 dst_sel:DWORD dst_unused:UNUSED_PAD src0_sel:WORD_1
	v_cvt_f32_f16_sdwa v100, v146 dst_sel:DWORD dst_unused:UNUSED_PAD src0_sel:WORD_1
	v_cvt_f32_f16_e32 v97, v147
	v_cvt_f32_f16_e32 v96, v146
	v_cvt_pk_bf16_f32 v88, v88, v89
	v_mul_f32_e64 v102, v98, v100
	v_mul_f32_e64 v103, v99, v101
	s_nop 0
	v_fma_f32 v102, v90, v96, -v102
	v_fma_f32 v103, v91, v97, -v103
	v_mul_f32_e64 v90, v90, v100
	v_mul_f32_e64 v91, v91, v101
	s_nop 0
	v_fma_f32 v90, v98, v96, v90
	v_fma_f32 v91, v99, v97, v91
	v_cvt_f32_f16_sdwa v99, v141 dst_sel:DWORD dst_unused:UNUSED_PAD src0_sel:WORD_1
	v_cvt_f32_f16_sdwa v98, v140 dst_sel:DWORD dst_unused:UNUSED_PAD src0_sel:WORD_1
	v_cvt_f32_f16_e32 v97, v141
	v_cvt_f32_f16_e32 v96, v140
	v_cvt_pk_bf16_f32 v89, v90, v91
	v_mul_f32_e64 v100, v92, v98
	v_mul_f32_e64 v101, v93, v99
	s_nop 0
	v_fma_f32 v100, v84, v96, -v100
	v_fma_f32 v101, v85, v97, -v101
	v_mul_f32_e64 v84, v84, v98
	v_mul_f32_e64 v85, v85, v99
	s_nop 0
	v_fma_f32 v92, v92, v96, v84
	v_fma_f32 v93, v93, v97, v85
	v_cvt_f32_f16_sdwa v97, v143 dst_sel:DWORD dst_unused:UNUSED_PAD src0_sel:WORD_1
	v_cvt_f32_f16_sdwa v96, v142 dst_sel:DWORD dst_unused:UNUSED_PAD src0_sel:WORD_1
	v_cvt_f32_f16_e32 v85, v143
	v_cvt_f32_f16_e32 v84, v142
	v_cvt_pk_bf16_f32 v90, v92, v93
	v_mul_f32_e64 v98, v94, v96
	v_mul_f32_e64 v99, v95, v97
	v_mad_i64_i32 v[92:93], s[2:3], v180, s81, v[176:177]
	v_fma_f32 v98, v86, v84, -v98
	v_fma_f32 v99, v87, v85, -v99
	v_mul_f32_e64 v86, v86, v96
	v_mul_f32_e64 v87, v87, v97
	v_add_u32_e32 v96, 0x90, v174
	v_fma_f32 v94, v94, v84, v86
	v_fma_f32 v95, v95, v85, v87
	v_cvt_pk_bf16_f32 v84, v104, v105
	v_cvt_pk_bf16_f32 v85, v102, v103
	v_cvt_pk_bf16_f32 v86, v100, v101
	v_cvt_pk_bf16_f32 v87, v98, v99
	v_cvt_pk_bf16_f32 v91, v94, v95
	global_store_dwordx4 v[92:93], v[84:87], off
	global_store_dwordx4 v[92:93], v[88:91], off offset:256
	v_ashrrev_i32_e32 v97, 31, v96
	v_mov_b32_e32 v84, v178
	ds_read_b32 v85, v199 offset:192
	v_and_b32_e32 v84, 0x7f, v84
	v_add_u32_e32 v84, 1, v84
	v_cvt_f32_ubyte0_e32 v84, v84
	v_mul_f32_e32 v84, v202, v84
	v_exp_f32_e32 v84, v84
	s_waitcnt lgkmcnt(0)
;     __device__ __forceinline__ void operator()(const f32x4 (&acc)[2][2][4][2], const Unit& u, int wr, int wc, int fr, int fq) const {
;     ...
;         if (t <= 1) {
;             const float sc = (t == 1) ? 0.0625f : 1.0f, lgs = (t == 1) ? -lg2_gamma_h(hh) : lg2_gamma_h(hh);
; #pragma unroll
;             for (int ai = 0; ai < 2; ++ai) {
;                 u32x4 cv[4][2];
; #pragma unroll
;                 for (int m = 0; m < 4; ++m) { const u32x4* cp = (const u32x4*)(cs + ((size_t)(row0 + ai * HALF + m * 16) * 128 + cw));
;                     cv[m][0] = cp[0]; cv[m][1] = cp[1]; }
; #pragma unroll
;                 for (int m = 0; m < 4; ++m) { const int row = row0 + ai * HALF + m * 16;
;                     int rl = row; asm volatile("" : "+v"(rl));
;                     const float rs = my[(ai * 4 + m) * 16] * sc * __builtin_amdgcn_exp2f((float)((rl & 127) + 1) * lgs);
;                     const f32x4 xa0 = acc[ai][0][m][0] * rs, xa1 = acc[ai][0][m][1] * rs, xb0 = acc[ai][1][m][0] * rs, xb1 = acc[ai][1][m][1] * rs;
;                     const unsigned cw8[8] = {cv[m][0].x, cv[m][0].y, cv[m][0].z, cv[m][0].w, cv[m][1].x, cv[m][1].y, cv[m][1].z, cv[m][1].w};
;                     float co[8], si[8];
; #pragma unroll
;                     for (int j = 0; j < 8; ++j) { const h2_t hv = __builtin_bit_cast(h2_t, cw8[j]); co[j] = (float)hv.x; si[j] = (float)hv.y; }
;                     const float x1[8] = {xa0[0], xa0[1], xa0[2], xa0[3], xa1[0], xa1[1], xa1[2], xa1[3]};
;                     const float x2[8] = {xb0[0], xb0[1], xb0[2], xb0[3], xb1[0], xb1[1], xb1[2], xb1[3]};
;                     float o1[8], o2[8];
; #pragma unroll
;                     for (int j = 0; j < 8; ++j) { o1[j] = x1[j] * co[j] - x2[j] * si[j]; o2[j] = x1[j] * si[j] + x2[j] * co[j]; }
;                     u32x4 w1, w2;
;                     w1.x = cvt_pk_bf16(o1[0], o1[1]); w1.y = cvt_pk_bf16(o1[2], o1[3]); w1.z = cvt_pk_bf16(o1[4], o1[5]); w1.w = cvt_pk_bf16(o1[6], o1[7]);
;                     w2.x = cvt_pk_bf16(o2[0], o2[1]); w2.y = cvt_pk_bf16(o2[2], o2[3]); w2.z = cvt_pk_bf16(o2[4], o2[5]); w2.w = cvt_pk_bf16(o2[6], o2[7]);
;                     bf16_t* rowp = base + (size_t)row * LDT + col0;
;                     *(u32x4*)rowp = w1; *(u32x4*)(rowp + HALF) = w2; }
;                 asm volatile("" ::: "memory"); }
	v_mul_f32_e32 v85, v201, v85
	v_cvt_f32_f16_sdwa v87, v137 dst_sel:DWORD dst_unused:UNUSED_PAD src0_sel:WORD_1
	v_cvt_f32_f16_sdwa v86, v136 dst_sel:DWORD dst_unused:UNUSED_PAD src0_sel:WORD_1
	v_mul_f32_e32 v84, v85, v84
	v_mul_f32_e64 v74, v74, v84
	v_mul_f32_e64 v75, v75, v84
	v_mul_f32_e64 v72, v72, v84
	v_mul_f32_e64 v73, v73, v84
	v_mul_f32_e64 v70, v70, v84
	v_mul_f32_e64 v71, v71, v84
	v_mul_f32_e64 v68, v68, v84
	v_mul_f32_e64 v69, v69, v84
	v_mul_f32_e64 v82, v82, v84
	v_mul_f32_e64 v83, v83, v84
	v_mul_f32_e64 v80, v80, v84
	v_mul_f32_e64 v81, v81, v84
	v_mul_f32_e64 v78, v78, v84
	v_mul_f32_e64 v79, v79, v84
	v_mul_f32_e64 v76, v76, v84
	v_mul_f32_e64 v77, v77, v84
	v_cvt_f32_f16_e32 v85, v137
	v_cvt_f32_f16_e32 v84, v136
	v_mul_f32_e64 v88, v80, v86
	v_mul_f32_e64 v89, v81, v87
	v_add_u32_e32 v94, 0xa0, v174
	v_ashrrev_i32_e32 v95, 31, v94
	v_fma_f32 v88, v72, v84, -v88
	v_fma_f32 v89, v73, v85, -v89
	v_mul_f32_e64 v72, v72, v86
	v_mul_f32_e64 v73, v73, v87
	v_add_u32_e32 v92, 0xb0, v174
	v_fma_f32 v72, v80, v84, v72
	v_fma_f32 v73, v81, v85, v73
	v_cvt_f32_f16_sdwa v85, v139 dst_sel:DWORD dst_unused:UNUSED_PAD src0_sel:WORD_1
	v_cvt_f32_f16_sdwa v84, v138 dst_sel:DWORD dst_unused:UNUSED_PAD src0_sel:WORD_1
	v_cvt_f32_f16_e32 v81, v139
	v_cvt_f32_f16_e32 v80, v138
	v_cvt_pk_bf16_f32 v72, v72, v73
	v_mul_f32_e64 v86, v82, v84
	v_mul_f32_e64 v87, v83, v85
	v_ashrrev_i32_e32 v93, 31, v92
	v_fma_f32 v86, v74, v80, -v86
	v_fma_f32 v87, v75, v81, -v87
	v_mul_f32_e64 v74, v74, v84
	v_mul_f32_e64 v75, v75, v85
	s_nop 0
	v_fma_f32 v74, v82, v80, v74
	v_fma_f32 v75, v83, v81, v75
	v_cvt_f32_f16_sdwa v83, v133 dst_sel:DWORD dst_unused:UNUSED_PAD src0_sel:WORD_1
	v_cvt_f32_f16_sdwa v82, v132 dst_sel:DWORD dst_unused:UNUSED_PAD src0_sel:WORD_1
	v_cvt_f32_f16_e32 v81, v133
	v_cvt_f32_f16_e32 v80, v132
	v_cvt_pk_bf16_f32 v73, v74, v75
	v_mul_f32_e64 v84, v76, v82
	v_mul_f32_e64 v85, v77, v83
	s_nop 0
	v_fma_f32 v84, v68, v80, -v84
	v_fma_f32 v85, v69, v81, -v85
	v_mul_f32_e64 v68, v68, v82
	v_mul_f32_e64 v69, v69, v83
	s_nop 0
	v_fma_f32 v76, v76, v80, v68
	v_fma_f32 v77, v77, v81, v69
	v_cvt_f32_f16_sdwa v81, v135 dst_sel:DWORD dst_unused:UNUSED_PAD src0_sel:WORD_1
	v_cvt_f32_f16_sdwa v80, v134 dst_sel:DWORD dst_unused:UNUSED_PAD src0_sel:WORD_1
	v_cvt_f32_f16_e32 v69, v135
	v_cvt_f32_f16_e32 v68, v134
	v_cvt_pk_bf16_f32 v74, v76, v77
	v_mul_f32_e64 v82, v78, v80
	v_mul_f32_e64 v83, v79, v81
	v_mad_i64_i32 v[76:77], s[2:3], v178, s81, v[176:177]
	v_fma_f32 v82, v70, v68, -v82
	v_fma_f32 v83, v71, v69, -v83
	v_mul_f32_e64 v70, v70, v80
	v_mul_f32_e64 v71, v71, v81
	s_nop 0
	v_fma_f32 v78, v78, v68, v70
	v_fma_f32 v79, v79, v69, v71
	v_cvt_pk_bf16_f32 v68, v88, v89
	v_cvt_pk_bf16_f32 v69, v86, v87
	v_cvt_pk_bf16_f32 v70, v84, v85
	v_cvt_pk_bf16_f32 v71, v82, v83
	v_cvt_pk_bf16_f32 v75, v78, v79
	global_store_dwordx4 v[76:77], v[68:71], off
	global_store_dwordx4 v[76:77], v[72:75], off offset:256
	s_nop 0
	v_lshlrev_b64 v[68:69], 9, v[106:107]
	v_lshl_add_u64 v[68:69], v[170:171], 0, v[68:69]
	global_load_dwordx4 v[98:101], v[68:69], off offset:16
	global_load_dwordx4 v[102:105], v[68:69], off
	v_lshlrev_b64 v[68:69], 9, v[96:97]
	v_lshl_add_u64 v[68:69], v[170:171], 0, v[68:69]
	global_load_dwordx4 v[84:87], v[68:69], off offset:16
	global_load_dwordx4 v[88:91], v[68:69], off
	v_lshlrev_b64 v[68:69], 9, v[94:95]
	v_lshl_add_u64 v[68:69], v[170:171], 0, v[68:69]
	global_load_dwordx4 v[76:79], v[68:69], off offset:16
	global_load_dwordx4 v[80:83], v[68:69], off
	v_lshlrev_b64 v[68:69], 9, v[92:93]
	v_lshl_add_u64 v[72:73], v[170:171], 0, v[68:69]
	v_mov_b32_e32 v93, v106
	global_load_dwordx4 v[68:71], v[72:73], off offset:16
	s_nop 0
	global_load_dwordx4 v[72:75], v[72:73], off
	ds_read_b32 v95, v199 offset:256
	v_and_b32_e32 v93, 0x7f, v93
	v_add_u32_e32 v93, 1, v93
	v_cvt_f32_ubyte0_e32 v93, v93
	v_mul_f32_e32 v93, v202, v93
	v_exp_f32_e32 v93, v93
	s_waitcnt lgkmcnt(0)
	v_mul_f32_e32 v95, v201, v95
	v_mul_f32_e32 v108, v95, v93
	v_mul_f32_e64 v58, v58, v108
	v_mul_f32_e64 v59, v59, v108
	v_mul_f32_e64 v56, v56, v108
	v_mul_f32_e64 v57, v57, v108
	v_mul_f32_e64 v54, v54, v108
	v_mul_f32_e64 v55, v55, v108
	v_mul_f32_e64 v52, v52, v108
	v_mul_f32_e64 v53, v53, v108
	v_mul_f32_e64 v66, v66, v108
	v_mul_f32_e64 v67, v67, v108
	v_mul_f32_e64 v64, v64, v108
	v_mul_f32_e64 v65, v65, v108
	v_mul_f32_e64 v62, v62, v108
	v_mul_f32_e64 v63, v63, v108
	v_mul_f32_e64 v60, v60, v108
	v_mul_f32_e64 v61, v61, v108
	s_waitcnt vmcnt(6)
;     __device__ __forceinline__ void operator()(const f32x4 (&acc)[2][2][4][2], const Unit& u, int wr, int wc, int fr, int fq) const {
;     ...
;         if (t <= 1) {
;             const float sc = (t == 1) ? 0.0625f : 1.0f, lgs = (t == 1) ? -lg2_gamma_h(hh) : lg2_gamma_h(hh);
; #pragma unroll
;             for (int ai = 0; ai < 2; ++ai) {
;                 u32x4 cv[4][2];
; #pragma unroll
;                 for (int m = 0; m < 4; ++m) { const u32x4* cp = (const u32x4*)(cs + ((size_t)(row0 + ai * HALF + m * 16) * 128 + cw));
;                     cv[m][0] = cp[0]; cv[m][1] = cp[1]; }
; #pragma unroll
;                 for (int m = 0; m < 4; ++m) { const int row = row0 + ai * HALF + m * 16;
;                     int rl = row; asm volatile("" : "+v"(rl));
;                     const float rs = my[(ai * 4 + m) * 16] * sc * __builtin_amdgcn_exp2f((float)((rl & 127) + 1) * lgs);
;                     const f32x4 xa0 = acc[ai][0][m][0] * rs, xa1 = acc[ai][0][m][1] * rs, xb0 = acc[ai][1][m][0] * rs, xb1 = acc[ai][1][m][1] * rs;
;                     const unsigned cw8[8] = {cv[m][0].x, cv[m][0].y, cv[m][0].z, cv[m][0].w, cv[m][1].x, cv[m][1].y, cv[m][1].z, cv[m][1].w};
;                     float co[8], si[8];
; #pragma unroll
;                     for (int j = 0; j < 8; ++j) { const h2_t hv = __builtin_bit_cast(h2_t, cw8[j]); co[j] = (float)hv.x; si[j] = (float)hv.y; }
;                     const float x1[8] = {xa0[0], xa0[1], xa0[2], xa0[3], xa1[0], xa1[1], xa1[2], xa1[3]};
;                     const float x2[8] = {xb0[0], xb0[1], xb0[2], xb0[3], xb1[0], xb1[1], xb1[2], xb1[3]};
;                     float o1[8], o2[8];
; #pragma unroll
;                     for (int j = 0; j < 8; ++j) { o1[j] = x1[j] * co[j] - x2[j] * si[j]; o2[j] = x1[j] * si[j] + x2[j] * co[j]; }
;                     u32x4 w1, w2;
;                     w1.x = cvt_pk_bf16(o1[0], o1[1]); w1.y = cvt_pk_bf16(o1[2], o1[3]); w1.z = cvt_pk_bf16(o1[4], o1[5]); w1.w = cvt_pk_bf16(o1[6], o1[7]);
;                     w2.x = cvt_pk_bf16(o2[0], o2[1]); w2.y = cvt_pk_bf16(o2[2], o2[3]); w2.z = cvt_pk_bf16(o2[4], o2[5]); w2.w = cvt_pk_bf16(o2[6], o2[7]);
;                     bf16_t* rowp = base + (size_t)row * LDT + col0;
;                     *(u32x4*)rowp = w1; *(u32x4*)(rowp + HALF) = w2; }
;                 asm volatile("" ::: "memory"); }
	v_cvt_f32_f16_e32 v109, v103
	v_cvt_f32_f16_e32 v108, v102
	v_cvt_f32_f16_sdwa v103, v103 dst_sel:DWORD dst_unused:UNUSED_PAD src0_sel:WORD_1
	v_cvt_f32_f16_sdwa v102, v102 dst_sel:DWORD dst_unused:UNUSED_PAD src0_sel:WORD_1
	v_mul_f32_e64 v110, v64, v102
	v_mul_f32_e64 v111, v65, v103
	s_nop 0
	v_fma_f32 v110, v56, v108, -v110
	v_fma_f32 v111, v57, v109, -v111
	v_mul_f32_e64 v56, v56, v102
	v_mul_f32_e64 v57, v57, v103
	v_cvt_f32_f16_sdwa v103, v105 dst_sel:DWORD dst_unused:UNUSED_PAD src0_sel:WORD_1
	v_cvt_f32_f16_sdwa v102, v104 dst_sel:DWORD dst_unused:UNUSED_PAD src0_sel:WORD_1
	v_fma_f32 v56, v64, v108, v56
	v_fma_f32 v57, v65, v109, v57
	v_cvt_f32_f16_e32 v65, v105
	v_cvt_f32_f16_e32 v64, v104
	v_mul_f32_e64 v104, v66, v102
	v_mul_f32_e64 v105, v67, v103
	v_cvt_pk_bf16_f32 v56, v56, v57
	v_fma_f32 v104, v58, v64, -v104
	v_fma_f32 v105, v59, v65, -v105
	v_mul_f32_e64 v58, v58, v102
	v_mul_f32_e64 v59, v59, v103
	s_nop 0
	v_fma_f32 v58, v66, v64, v58
	v_fma_f32 v59, v67, v65, v59
	v_cvt_f32_f16_sdwa v67, v99 dst_sel:DWORD dst_unused:UNUSED_PAD src0_sel:WORD_1
	v_cvt_f32_f16_sdwa v66, v98 dst_sel:DWORD dst_unused:UNUSED_PAD src0_sel:WORD_1
	v_cvt_f32_f16_e32 v65, v99
	v_cvt_f32_f16_e32 v64, v98
	v_cvt_pk_bf16_f32 v57, v58, v59
	v_mul_f32_e64 v98, v60, v66
	v_mul_f32_e64 v99, v61, v67
	s_nop 0
	v_fma_f32 v98, v52, v64, -v98
	v_fma_f32 v99, v53, v65, -v99
	v_mul_f32_e64 v52, v52, v66
	v_mul_f32_e64 v53, v53, v67
	s_nop 0
	v_fma_f32 v60, v60, v64, v52
	v_fma_f32 v61, v61, v65, v53
	v_cvt_f32_f16_sdwa v65, v101 dst_sel:DWORD dst_unused:UNUSED_PAD src0_sel:WORD_1
	v_cvt_f32_f16_sdwa v64, v100 dst_sel:DWORD dst_unused:UNUSED_PAD src0_sel:WORD_1
	v_cvt_f32_f16_e32 v53, v101
	v_cvt_f32_f16_e32 v52, v100
	v_cvt_pk_bf16_f32 v58, v60, v61
	v_mul_f32_e64 v66, v62, v64
	v_mul_f32_e64 v67, v63, v65
	v_mad_i64_i32 v[60:61], s[2:3], v106, s81, v[176:177]
	v_fma_f32 v66, v54, v52, -v66
	v_fma_f32 v67, v55, v53, -v67
	v_mul_f32_e64 v54, v54, v64
	v_mul_f32_e64 v55, v55, v65
	s_nop 0
	v_fma_f32 v62, v62, v52, v54
	v_fma_f32 v63, v63, v53, v55
	v_cvt_pk_bf16_f32 v52, v110, v111
	v_cvt_pk_bf16_f32 v53, v104, v105
	v_cvt_pk_bf16_f32 v54, v98, v99
	v_cvt_pk_bf16_f32 v55, v66, v67
	v_cvt_pk_bf16_f32 v59, v62, v63
	global_store_dwordx4 v[60:61], v[52:55], off
	global_store_dwordx4 v[60:61], v[56:59], off offset:256
	s_nop 0
	v_mov_b32_e32 v52, v96
	ds_read_b32 v53, v199 offset:320
	v_and_b32_e32 v52, 0x7f, v52
	v_add_u32_e32 v52, 1, v52
	v_cvt_f32_ubyte0_e32 v52, v52
	v_mul_f32_e32 v52, v202, v52
	v_exp_f32_e32 v52, v52
	s_waitcnt lgkmcnt(0)
	v_mul_f32_e32 v53, v201, v53
	s_waitcnt vmcnt(6)
	v_cvt_f32_f16_sdwa v55, v89 dst_sel:DWORD dst_unused:UNUSED_PAD src0_sel:WORD_1
	v_cvt_f32_f16_sdwa v54, v88 dst_sel:DWORD dst_unused:UNUSED_PAD src0_sel:WORD_1
	v_mul_f32_e32 v52, v53, v52
	v_mul_f32_e64 v42, v42, v52
	v_mul_f32_e64 v43, v43, v52
	v_mul_f32_e64 v40, v40, v52
	v_mul_f32_e64 v41, v41, v52
	v_mul_f32_e64 v38, v38, v52
	v_mul_f32_e64 v39, v39, v52
	v_mul_f32_e64 v36, v36, v52
	v_mul_f32_e64 v37, v37, v52
	v_mul_f32_e64 v50, v50, v52
	v_mul_f32_e64 v51, v51, v52
	v_mul_f32_e64 v48, v48, v52
	v_mul_f32_e64 v49, v49, v52
	v_mul_f32_e64 v46, v46, v52
	v_mul_f32_e64 v47, v47, v52
	v_mul_f32_e64 v44, v44, v52
	v_mul_f32_e64 v45, v45, v52
	v_cvt_f32_f16_e32 v53, v89
	v_cvt_f32_f16_e32 v52, v88
	v_mul_f32_e64 v56, v48, v54
	v_mul_f32_e64 v57, v49, v55
	s_nop 0
	v_fma_f32 v56, v40, v52, -v56
	v_fma_f32 v57, v41, v53, -v57
	v_mul_f32_e64 v40, v40, v54
	v_mul_f32_e64 v41, v41, v55
	s_nop 0
	v_fma_f32 v40, v48, v52, v40
	v_fma_f32 v41, v49, v53, v41
	v_cvt_f32_f16_sdwa v53, v91 dst_sel:DWORD dst_unused:UNUSED_PAD src0_sel:WORD_1
	v_cvt_f32_f16_sdwa v52, v90 dst_sel:DWORD dst_unused:UNUSED_PAD src0_sel:WORD_1
	v_cvt_f32_f16_e32 v49, v91
	v_cvt_f32_f16_e32 v48, v90
	v_cvt_pk_bf16_f32 v40, v40, v41
	v_mul_f32_e64 v54, v50, v52
	v_mul_f32_e64 v55, v51, v53
	s_nop 0
	v_fma_f32 v54, v42, v48, -v54
	v_fma_f32 v55, v43, v49, -v55
	v_mul_f32_e64 v42, v42, v52
	v_mul_f32_e64 v43, v43, v53
	s_nop 0
	v_fma_f32 v42, v50, v48, v42
	v_fma_f32 v43, v51, v49, v43
	v_cvt_f32_f16_sdwa v51, v85 dst_sel:DWORD dst_unused:UNUSED_PAD src0_sel:WORD_1
	v_cvt_f32_f16_sdwa v50, v84 dst_sel:DWORD dst_unused:UNUSED_PAD src0_sel:WORD_1
	v_cvt_f32_f16_e32 v49, v85
	v_cvt_f32_f16_e32 v48, v84
	v_cvt_pk_bf16_f32 v41, v42, v43
	v_mul_f32_e64 v52, v44, v50
	v_mul_f32_e64 v53, v45, v51
	s_nop 0
	v_fma_f32 v52, v36, v48, -v52
	v_fma_f32 v53, v37, v49, -v53
	v_mul_f32_e64 v36, v36, v50
	v_mul_f32_e64 v37, v37, v51
	s_nop 0
	v_fma_f32 v44, v44, v48, v36
	v_fma_f32 v45, v45, v49, v37
	v_cvt_f32_f16_sdwa v49, v87 dst_sel:DWORD dst_unused:UNUSED_PAD src0_sel:WORD_1
	v_cvt_f32_f16_sdwa v48, v86 dst_sel:DWORD dst_unused:UNUSED_PAD src0_sel:WORD_1
	v_cvt_f32_f16_e32 v37, v87
	v_cvt_f32_f16_e32 v36, v86
	v_cvt_pk_bf16_f32 v42, v44, v45
	v_mul_f32_e64 v50, v46, v48
	v_mul_f32_e64 v51, v47, v49
	v_mad_i64_i32 v[44:45], s[2:3], v96, s81, v[176:177]
	v_fma_f32 v50, v38, v36, -v50
	v_fma_f32 v51, v39, v37, -v51
	v_mul_f32_e64 v38, v38, v48
	v_mul_f32_e64 v39, v39, v49
	s_nop 0
	v_fma_f32 v46, v46, v36, v38
	v_fma_f32 v47, v47, v37, v39
	v_cvt_pk_bf16_f32 v36, v56, v57
	v_cvt_pk_bf16_f32 v37, v54, v55
	v_cvt_pk_bf16_f32 v38, v52, v53
	v_cvt_pk_bf16_f32 v39, v50, v51
	v_cvt_pk_bf16_f32 v43, v46, v47
	global_store_dwordx4 v[44:45], v[36:39], off
	global_store_dwordx4 v[44:45], v[40:43], off offset:256
	s_nop 0
	v_mov_b32_e32 v36, v94
	ds_read_b32 v37, v199 offset:384
	v_and_b32_e32 v36, 0x7f, v36
	v_add_u32_e32 v36, 1, v36
	v_cvt_f32_ubyte0_e32 v36, v36
	v_mul_f32_e32 v36, v202, v36
	v_exp_f32_e32 v36, v36
	s_waitcnt lgkmcnt(0)
;     __device__ __forceinline__ void operator()(const f32x4 (&acc)[2][2][4][2], const Unit& u, int wr, int wc, int fr, int fq) const {
;     ...
;         if (t <= 1) {
;             const float sc = (t == 1) ? 0.0625f : 1.0f, lgs = (t == 1) ? -lg2_gamma_h(hh) : lg2_gamma_h(hh);
; #pragma unroll
;             for (int ai = 0; ai < 2; ++ai) {
;                 u32x4 cv[4][2];
; #pragma unroll
;                 for (int m = 0; m < 4; ++m) { const u32x4* cp = (const u32x4*)(cs + ((size_t)(row0 + ai * HALF + m * 16) * 128 + cw));
;                     cv[m][0] = cp[0]; cv[m][1] = cp[1]; }
; #pragma unroll
;                 for (int m = 0; m < 4; ++m) { const int row = row0 + ai * HALF + m * 16;
;                     int rl = row; asm volatile("" : "+v"(rl));
;                     const float rs = my[(ai * 4 + m) * 16] * sc * __builtin_amdgcn_exp2f((float)((rl & 127) + 1) * lgs);
;                     const f32x4 xa0 = acc[ai][0][m][0] * rs, xa1 = acc[ai][0][m][1] * rs, xb0 = acc[ai][1][m][0] * rs, xb1 = acc[ai][1][m][1] * rs;
;                     const unsigned cw8[8] = {cv[m][0].x, cv[m][0].y, cv[m][0].z, cv[m][0].w, cv[m][1].x, cv[m][1].y, cv[m][1].z, cv[m][1].w};
;                     float co[8], si[8];
; #pragma unroll
;                     for (int j = 0; j < 8; ++j) { const h2_t hv = __builtin_bit_cast(h2_t, cw8[j]); co[j] = (float)hv.x; si[j] = (float)hv.y; }
;                     const float x1[8] = {xa0[0], xa0[1], xa0[2], xa0[3], xa1[0], xa1[1], xa1[2], xa1[3]};
;                     const float x2[8] = {xb0[0], xb0[1], xb0[2], xb0[3], xb1[0], xb1[1], xb1[2], xb1[3]};
;                     float o1[8], o2[8];
; #pragma unroll
;                     for (int j = 0; j < 8; ++j) { o1[j] = x1[j] * co[j] - x2[j] * si[j]; o2[j] = x1[j] * si[j] + x2[j] * co[j]; }
;                     u32x4 w1, w2;
;                     w1.x = cvt_pk_bf16(o1[0], o1[1]); w1.y = cvt_pk_bf16(o1[2], o1[3]); w1.z = cvt_pk_bf16(o1[4], o1[5]); w1.w = cvt_pk_bf16(o1[6], o1[7]);
;                     w2.x = cvt_pk_bf16(o2[0], o2[1]); w2.y = cvt_pk_bf16(o2[2], o2[3]); w2.z = cvt_pk_bf16(o2[4], o2[5]); w2.w = cvt_pk_bf16(o2[6], o2[7]);
;                     bf16_t* rowp = base + (size_t)row * LDT + col0;
;                     *(u32x4*)rowp = w1; *(u32x4*)(rowp + HALF) = w2; }
;                 asm volatile("" ::: "memory"); }
	v_mul_f32_e32 v37, v201, v37
	s_waitcnt vmcnt(6)
	v_cvt_f32_f16_sdwa v39, v81 dst_sel:DWORD dst_unused:UNUSED_PAD src0_sel:WORD_1
	v_cvt_f32_f16_sdwa v38, v80 dst_sel:DWORD dst_unused:UNUSED_PAD src0_sel:WORD_1
	v_mul_f32_e32 v36, v37, v36
	v_mul_f32_e64 v26, v26, v36
	v_mul_f32_e64 v27, v27, v36
	v_mul_f32_e64 v24, v24, v36
	v_mul_f32_e64 v25, v25, v36
	v_mul_f32_e64 v22, v22, v36
	v_mul_f32_e64 v23, v23, v36
	v_mul_f32_e64 v20, v20, v36
	v_mul_f32_e64 v21, v21, v36
	v_mul_f32_e64 v34, v34, v36
	v_mul_f32_e64 v35, v35, v36
	v_mul_f32_e64 v32, v32, v36
	v_mul_f32_e64 v33, v33, v36
	v_mul_f32_e64 v30, v30, v36
	v_mul_f32_e64 v31, v31, v36
	v_mul_f32_e64 v28, v28, v36
	v_mul_f32_e64 v29, v29, v36
	v_cvt_f32_f16_e32 v37, v81
	v_cvt_f32_f16_e32 v36, v80
	v_mul_f32_e64 v40, v32, v38
	v_mul_f32_e64 v41, v33, v39
	s_nop 0
	v_fma_f32 v40, v24, v36, -v40
	v_fma_f32 v41, v25, v37, -v41
	v_mul_f32_e64 v24, v24, v38
	v_mul_f32_e64 v25, v25, v39
	s_nop 0
	v_fma_f32 v24, v32, v36, v24
	v_fma_f32 v25, v33, v37, v25
	v_cvt_f32_f16_sdwa v37, v83 dst_sel:DWORD dst_unused:UNUSED_PAD src0_sel:WORD_1
	v_cvt_f32_f16_sdwa v36, v82 dst_sel:DWORD dst_unused:UNUSED_PAD src0_sel:WORD_1
	v_cvt_f32_f16_e32 v33, v83
	v_cvt_f32_f16_e32 v32, v82
	v_cvt_pk_bf16_f32 v24, v24, v25
	v_mul_f32_e64 v38, v34, v36
	v_mul_f32_e64 v39, v35, v37
	s_nop 0
	v_fma_f32 v38, v26, v32, -v38
	v_fma_f32 v39, v27, v33, -v39
	v_mul_f32_e64 v26, v26, v36
	v_mul_f32_e64 v27, v27, v37
	s_nop 0
	v_fma_f32 v26, v34, v32, v26
	v_fma_f32 v27, v35, v33, v27
	v_cvt_f32_f16_sdwa v35, v77 dst_sel:DWORD dst_unused:UNUSED_PAD src0_sel:WORD_1
	v_cvt_f32_f16_sdwa v34, v76 dst_sel:DWORD dst_unused:UNUSED_PAD src0_sel:WORD_1
	v_cvt_f32_f16_e32 v33, v77
	v_cvt_f32_f16_e32 v32, v76
	v_cvt_pk_bf16_f32 v25, v26, v27
	v_mul_f32_e64 v36, v28, v34
	v_mul_f32_e64 v37, v29, v35
	s_nop 0
	v_fma_f32 v36, v20, v32, -v36
	v_fma_f32 v37, v21, v33, -v37
	v_mul_f32_e64 v20, v20, v34
	v_mul_f32_e64 v21, v21, v35
	s_nop 0
	v_fma_f32 v28, v28, v32, v20
	v_fma_f32 v29, v29, v33, v21
	v_cvt_f32_f16_sdwa v33, v79 dst_sel:DWORD dst_unused:UNUSED_PAD src0_sel:WORD_1
	v_cvt_f32_f16_sdwa v32, v78 dst_sel:DWORD dst_unused:UNUSED_PAD src0_sel:WORD_1
	v_cvt_f32_f16_e32 v21, v79
	v_cvt_f32_f16_e32 v20, v78
	v_cvt_pk_bf16_f32 v26, v28, v29
	v_mul_f32_e64 v34, v30, v32
	v_mul_f32_e64 v35, v31, v33
	v_mad_i64_i32 v[28:29], s[2:3], v94, s81, v[176:177]
	v_fma_f32 v34, v22, v20, -v34
	v_fma_f32 v35, v23, v21, -v35
	v_mul_f32_e64 v22, v22, v32
	v_mul_f32_e64 v23, v23, v33
	s_nop 0
	v_fma_f32 v30, v30, v20, v22
	v_fma_f32 v31, v31, v21, v23
	v_cvt_pk_bf16_f32 v20, v40, v41
	v_cvt_pk_bf16_f32 v21, v38, v39
	v_cvt_pk_bf16_f32 v22, v36, v37
	v_cvt_pk_bf16_f32 v23, v34, v35
	v_cvt_pk_bf16_f32 v27, v30, v31
	global_store_dwordx4 v[28:29], v[20:23], off
	global_store_dwordx4 v[28:29], v[24:27], off offset:256
	s_nop 0
	v_mov_b32_e32 v20, v92
	ds_read_b32 v21, v199 offset:448
	v_and_b32_e32 v20, 0x7f, v20
	v_add_u32_e32 v20, 1, v20
	v_cvt_f32_ubyte0_e32 v20, v20
	v_mul_f32_e32 v20, v202, v20
	v_exp_f32_e32 v20, v20
	s_waitcnt lgkmcnt(0)
	v_mul_f32_e32 v21, v201, v21
	s_waitcnt vmcnt(6)
	v_cvt_f32_f16_sdwa v23, v73 dst_sel:DWORD dst_unused:UNUSED_PAD src0_sel:WORD_1
	v_cvt_f32_f16_sdwa v22, v72 dst_sel:DWORD dst_unused:UNUSED_PAD src0_sel:WORD_1
	v_mul_f32_e32 v20, v21, v20
	v_mul_f32_e64 v10, v10, v20
	v_mul_f32_e64 v11, v11, v20
	v_mul_f32_e64 v8, v8, v20
	v_mul_f32_e64 v9, v9, v20
	v_mul_f32_e64 v6, v6, v20
	v_mul_f32_e64 v7, v7, v20
	v_mul_f32_e64 v4, v4, v20
	v_mul_f32_e64 v5, v5, v20
	v_mul_f32_e64 v18, v18, v20
	v_mul_f32_e64 v19, v19, v20
	v_mul_f32_e64 v16, v16, v20
	v_mul_f32_e64 v17, v17, v20
	v_mul_f32_e64 v14, v14, v20
	v_mul_f32_e64 v15, v15, v20
	v_mul_f32_e64 v12, v12, v20
	v_mul_f32_e64 v13, v13, v20
	v_cvt_f32_f16_e32 v21, v73
	v_cvt_f32_f16_e32 v20, v72
	v_mul_f32_e64 v24, v16, v22
	v_mul_f32_e64 v25, v17, v23
	s_nop 0
	v_fma_f32 v24, v8, v20, -v24
	v_fma_f32 v25, v9, v21, -v25
	v_mul_f32_e64 v8, v8, v22
	v_mul_f32_e64 v9, v9, v23
	s_nop 0
	v_fma_f32 v8, v16, v20, v8
	v_fma_f32 v9, v17, v21, v9
	v_cvt_f32_f16_sdwa v21, v75 dst_sel:DWORD dst_unused:UNUSED_PAD src0_sel:WORD_1
	v_cvt_f32_f16_sdwa v20, v74 dst_sel:DWORD dst_unused:UNUSED_PAD src0_sel:WORD_1
	v_cvt_f32_f16_e32 v17, v75
	v_cvt_f32_f16_e32 v16, v74
	v_cvt_pk_bf16_f32 v8, v8, v9
	v_mul_f32_e64 v22, v18, v20
	v_mul_f32_e64 v23, v19, v21
	s_nop 0
	v_fma_f32 v22, v10, v16, -v22
	v_fma_f32 v23, v11, v17, -v23
	v_mul_f32_e64 v10, v10, v20
	v_mul_f32_e64 v11, v11, v21
	s_nop 0
	v_fma_f32 v10, v18, v16, v10
	v_fma_f32 v11, v19, v17, v11
	v_cvt_f32_f16_sdwa v19, v69 dst_sel:DWORD dst_unused:UNUSED_PAD src0_sel:WORD_1
	v_cvt_f32_f16_sdwa v18, v68 dst_sel:DWORD dst_unused:UNUSED_PAD src0_sel:WORD_1
	v_cvt_f32_f16_e32 v17, v69
	v_cvt_f32_f16_e32 v16, v68
	v_cvt_pk_bf16_f32 v9, v10, v11
	v_mul_f32_e64 v20, v12, v18
	v_mul_f32_e64 v21, v13, v19
	s_nop 0
	v_fma_f32 v20, v4, v16, -v20
	v_fma_f32 v21, v5, v17, -v21
	v_mul_f32_e64 v4, v4, v18
	v_mul_f32_e64 v5, v5, v19
	s_nop 0
	v_fma_f32 v12, v12, v16, v4
	v_fma_f32 v13, v13, v17, v5
	v_cvt_f32_f16_sdwa v17, v71 dst_sel:DWORD dst_unused:UNUSED_PAD src0_sel:WORD_1
	v_cvt_f32_f16_sdwa v16, v70 dst_sel:DWORD dst_unused:UNUSED_PAD src0_sel:WORD_1
	v_cvt_f32_f16_e32 v5, v71
	v_cvt_f32_f16_e32 v4, v70
	v_cvt_pk_bf16_f32 v10, v12, v13
	v_mul_f32_e64 v18, v14, v16
	v_mul_f32_e64 v19, v15, v17
	v_mad_i64_i32 v[12:13], s[2:3], v92, s81, v[176:177]
	v_fma_f32 v18, v6, v4, -v18
	v_fma_f32 v19, v7, v5, -v19
	v_mul_f32_e64 v6, v6, v16
	v_mul_f32_e64 v7, v7, v17
	s_nop 0
	v_fma_f32 v14, v14, v4, v6
	v_fma_f32 v15, v15, v5, v7
	v_cvt_pk_bf16_f32 v4, v24, v25
	v_cvt_pk_bf16_f32 v5, v22, v23
	v_cvt_pk_bf16_f32 v6, v20, v21
	v_cvt_pk_bf16_f32 v7, v18, v19
	v_cvt_pk_bf16_f32 v11, v14, v15
	global_store_dwordx4 v[12:13], v[4:7], off
	global_store_dwordx4 v[12:13], v[8:11], off offset:256
	s_and_b64 vcc, exec, s[8:9]
	s_mov_b64 s[4:5], -1
	s_cbranch_vccnz .LBB0_314

;     __device__ bool next(int i, Unit& u) const { const int rounds = nwg / G; if (i >= rounds) return false; return StaticOrder::next(rounds - 1 - i, u); }
;     __device__ bool next(int i, Unit& u) const { const int rounds = nwg / G; if (i >= 2 * rounds) return false; const bool ok = StaticOrder::next(i >= rounds ? i - rounds : i, u); u.z = (i >= rounds) ? 1 : 0; return ok; }
; #define PG8_TRIP_HEAD(T) const int t = (T); const bool last = (t == nt - 2); \
;             const char* a1 = cA + (size_t)(t + 1) * kstep; \
;             const char* a2 = last ? nA : cA + (size_t)(t + 2) * kstep; const char* b2 = last ? nB : cB + (size_t)(t + 2) * kstep; \
;             const char* a3 = a2 + kstep; const char* b3 = b2 + kstep; \
;             if (last && has_next) S.a_ready(nxt);
; template <class Epi, class Sched, bool ALIGN_EPI = false, bool SP2 = false>
; __device__ __forceinline__ void gemm_phase(PG8_LAS unsigned char* lds, const Gemm g, const Sched& S, const Epi& E) {
;     ...
;         const bool has_next = S.next(ui + 1, nxt);
;         const char* nA = has_next ? (const char*)S.opA(g, nxt) + (size_t)nxt.pm * tstepA : cA; const char* nB = has_next ? (const char*)S.opB(g, nxt) + (size_t)nxt.pn * tstepB : cB;
;     ...
;         if constexpr (SP2) {
;             { PG8_TRIP_HEAD(0) PG8_TRIP_SP2(asm volatile("s_waitcnt vmcnt(%0)" :: "n"(8 + Epi::NST) : "memory"), PG8_MMAZ) }
.LBB0_593:
	v_readlane_b32 s18, v253, 7
	v_readlane_b32 s34, v254, 59
	s_cmp_eq_u32 s29, 0
	v_readlane_b32 s19, v253, 8
	v_readlane_b32 s35, v254, 60
	s_cselect_b32 s33, s35, s19
	s_cselect_b32 s34, s34, s18
	s_ashr_i32 s15, s14, 31
	s_lshl_b64 s[18:19], s[14:15], 20
	s_add_u32 s18, s34, s18
	s_addc_u32 s19, s33, s19
	s_and_b64 s[4:5], s[4:5], exec
	s_cselect_b32 s4, s19, s9
	s_cselect_b32 s5, s18, s8
	s_add_i32 s35, 0, 0x10000
	s_add_i32 s37, 0, 0x14000
	v_add_u32_e32 v116, s35, v219
	v_add_u32_e32 v117, s37, v219
	ds_read_b128 v[4:7], v116
	ds_read_b128 v[8:11], v116 offset:1024
	ds_read_b128 v[12:15], v116 offset:2048
	ds_read_b128 v[16:19], v116 offset:3072
	ds_read_b128 v[20:23], v117
	ds_read_b128 v[24:27], v117 offset:1024
	ds_read_b128 v[28:31], v117 offset:2048
	ds_read_b128 v[32:35], v117 offset:3072
	s_mov_b32 s15, 0
	v_lshl_add_u64 v[192:193], s[20:21], 0, v[196:197]
	s_mov_b64 s[38:39], 0x84080
	s_add_i32 s33, s23, 0xc000
	v_lshl_add_u64 v[68:69], v[192:193], 0, s[38:39]
	s_mov_b32 m0, s33
	s_mov_b64 s[38:39], 0xc6080
	s_add_i32 s34, s23, 0xe000
	ds_read_b128 v[36:39], v221
	ds_read_b128 v[40:43], v221 offset:1024
	ds_read_b128 v[44:47], v221 offset:2048
	ds_read_b128 v[48:51], v221 offset:3072
	ds_read_b128 v[52:55], v221 offset:4096
	ds_read_b128 v[56:59], v221 offset:5120
	ds_read_b128 v[60:63], v221 offset:6144
	ds_read_b128 v[64:67], v221 offset:7168
	global_load_lds_dwordx4 v[68:69], off
	v_lshl_add_u64 v[68:69], v[192:193], 0, s[38:39]
	s_mov_b32 m0, s34
	s_nop 0
	global_load_lds_dwordx4 v[68:69], off
	s_waitcnt vmcnt(8)
	s_waitcnt lgkmcnt(0)
	s_barrier
	s_setprio 1
	s_waitcnt lgkmcnt(0)
	v_mfma_f32_16x16x32_bf16 v[92:95], v[4:7], v[60:63], 0
	v_mfma_f32_16x16x32_bf16 v[68:71], v[4:7], v[36:39], 0
	v_mfma_f32_16x16x32_bf16 v[72:75], v[12:15], v[36:39], 0
	v_mfma_f32_16x16x32_bf16 v[76:79], v[4:7], v[44:47], 0
	v_mfma_f32_16x16x32_bf16 v[80:83], v[12:15], v[44:47], 0
	v_mfma_f32_16x16x32_bf16 v[84:87], v[4:7], v[52:55], 0
	v_mfma_f32_16x16x32_bf16 v[88:91], v[12:15], v[52:55], 0
	v_mfma_f32_16x16x32_bf16 v[100:103], v[8:11], v[64:67], v[92:95]
	v_mfma_f32_16x16x32_bf16 v[92:95], v[12:15], v[60:63], 0
	v_mfma_f32_16x16x32_bf16 v[68:71], v[8:11], v[40:43], v[68:71]
	v_mfma_f32_16x16x32_bf16 v[72:75], v[16:19], v[40:43], v[72:75]
	v_mfma_f32_16x16x32_bf16 v[76:79], v[8:11], v[48:51], v[76:79]
	v_mfma_f32_16x16x32_bf16 v[80:83], v[16:19], v[48:51], v[80:83]
	v_mfma_f32_16x16x32_bf16 v[84:87], v[8:11], v[56:59], v[84:87]
	v_mfma_f32_16x16x32_bf16 v[88:91], v[16:19], v[56:59], v[88:91]
	v_mfma_f32_16x16x32_bf16 v[104:107], v[16:19], v[64:67], v[92:95]
	s_setprio 0
	s_setprio 1
	v_mfma_f32_16x16x32_bf16 v[92:95], v[20:23], v[36:39], 0
	v_mfma_f32_16x16x32_bf16 v[36:39], v[28:31], v[36:39], 0
	v_mfma_f32_16x16x32_bf16 v[118:121], v[24:27], v[40:43], v[92:95]
	v_mfma_f32_16x16x32_bf16 v[36:39], v[32:35], v[40:43], v[36:39]
	v_mfma_f32_16x16x32_bf16 v[40:43], v[20:23], v[44:47], 0
	v_mfma_f32_16x16x32_bf16 v[44:47], v[28:31], v[44:47], 0
	v_mfma_f32_16x16x32_bf16 v[40:43], v[24:27], v[48:51], v[40:43]
	v_mfma_f32_16x16x32_bf16 v[44:47], v[32:35], v[48:51], v[44:47]
	v_mfma_f32_16x16x32_bf16 v[48:51], v[20:23], v[52:55], 0
	v_mfma_f32_16x16x32_bf16 v[52:55], v[28:31], v[52:55], 0
	v_mfma_f32_16x16x32_bf16 v[48:51], v[24:27], v[56:59], v[48:51]
	v_mfma_f32_16x16x32_bf16 v[52:55], v[32:35], v[56:59], v[52:55]
	v_mfma_f32_16x16x32_bf16 v[56:59], v[20:23], v[60:63], 0
	v_mfma_f32_16x16x32_bf16 v[60:63], v[28:31], v[60:63], 0
	v_mfma_f32_16x16x32_bf16 v[56:59], v[24:27], v[64:67], v[56:59]
	v_mfma_f32_16x16x32_bf16 v[60:63], v[32:35], v[64:67], v[60:63]
	s_setprio 0
	s_barrier
	v_lshl_add_u64 v[250:251], s[8:9], 0, v[194:195]
	s_mov_b64 s[40:41], 0x100
	s_add_i32 s35, s35, s22
	v_lshl_add_u64 v[134:135], v[250:251], 0, s[40:41]
	s_mov_b32 m0, s35
	s_mov_b64 s[38:39], 0x40100
	s_add_i32 s36, s35, 0x2000
	ds_read_b128 v[64:67], v221 offset:16384
	ds_read_b128 v[92:95], v221 offset:17408
	ds_read_b128 v[96:99], v221 offset:18432
	ds_read_b128 v[108:111], v221 offset:19456
	ds_read_b128 v[112:115], v221 offset:20480
	ds_read_b128 v[122:125], v221 offset:21504
	ds_read_b128 v[126:129], v221 offset:22528
	ds_read_b128 v[130:133], v221 offset:23552
	global_load_lds_dwordx4 v[134:135], off
	v_lshl_add_u64 v[134:135], v[250:251], 0, s[38:39]
	s_mov_b32 m0, s36
	s_mov_b64 s[38:39], 0x80100
	s_add_i32 s37, s37, s22
	global_load_lds_dwordx4 v[134:135], off
	v_lshl_add_u64 v[134:135], v[250:251], 0, s[38:39]
	s_mov_b32 m0, s37
	s_mov_b64 s[38:39], 0xc0100
	global_load_lds_dwordx4 v[134:135], off
	v_lshl_add_u64 v[134:135], v[250:251], 0, s[38:39]
	s_add_i32 s38, s37, 0x2000
	s_mov_b32 m0, s38
	s_nop 0
	global_load_lds_dwordx4 v[134:135], off
	v_lshl_add_u64 v[134:135], v[192:193], 0, s[40:41]
	s_mov_b32 m0, s23
	s_mov_b64 s[40:41], 0x42100
	global_load_lds_dwordx4 v[134:135], off
	v_lshl_add_u64 v[134:135], v[192:193], 0, s[40:41]
	s_mov_b32 m0, s24
	s_nop 0
	global_load_lds_dwordx4 v[134:135], off
	s_waitcnt vmcnt(8)
	s_waitcnt lgkmcnt(0)
	s_barrier
	s_setprio 1
	s_waitcnt lgkmcnt(0)
	v_mfma_f32_16x16x32_bf16 v[134:137], v[4:7], v[64:67], 0
	v_mfma_f32_16x16x32_bf16 v[144:147], v[4:7], v[96:99], 0
	v_mfma_f32_16x16x32_bf16 v[152:155], v[4:7], v[112:115], 0
	v_mfma_f32_16x16x32_bf16 v[4:7], v[4:7], v[126:129], 0
	v_mfma_f32_16x16x32_bf16 v[136:139], v[8:11], v[92:95], v[134:137]
	v_mfma_f32_16x16x32_bf16 v[144:147], v[8:11], v[108:111], v[144:147]
	v_mfma_f32_16x16x32_bf16 v[152:155], v[8:11], v[122:125], v[152:155]
	v_mfma_f32_16x16x32_bf16 v[4:7], v[8:11], v[130:133], v[4:7]
	v_mfma_f32_16x16x32_bf16 v[8:11], v[12:15], v[126:129], 0
	v_mfma_f32_16x16x32_bf16 v[140:143], v[12:15], v[64:67], 0
	v_mfma_f32_16x16x32_bf16 v[148:151], v[12:15], v[96:99], 0
	v_mfma_f32_16x16x32_bf16 v[156:159], v[12:15], v[112:115], 0
	v_mfma_f32_16x16x32_bf16 v[8:11], v[16:19], v[130:133], v[8:11]
	v_mfma_f32_16x16x32_bf16 v[140:143], v[16:19], v[92:95], v[140:143]
	v_mfma_f32_16x16x32_bf16 v[148:151], v[16:19], v[108:111], v[148:151]
	v_mfma_f32_16x16x32_bf16 v[156:159], v[16:19], v[122:125], v[156:159]
	s_setprio 0
	s_setprio 1
	v_mfma_f32_16x16x32_bf16 v[12:15], v[20:23], v[64:67], 0
	v_mfma_f32_16x16x32_bf16 v[160:163], v[24:27], v[92:95], v[12:15]
	v_mfma_f32_16x16x32_bf16 v[12:15], v[28:31], v[64:67], 0
	v_mfma_f32_16x16x32_bf16 v[164:167], v[32:35], v[92:95], v[12:15]
	v_mfma_f32_16x16x32_bf16 v[12:15], v[20:23], v[96:99], 0
	v_mfma_f32_16x16x32_bf16 v[168:171], v[24:27], v[108:111], v[12:15]
	v_mfma_f32_16x16x32_bf16 v[12:15], v[28:31], v[96:99], 0
	v_mfma_f32_16x16x32_bf16 v[172:175], v[32:35], v[108:111], v[12:15]
	v_mfma_f32_16x16x32_bf16 v[12:15], v[20:23], v[112:115], 0
	v_mfma_f32_16x16x32_bf16 v[176:179], v[24:27], v[122:125], v[12:15]
	v_mfma_f32_16x16x32_bf16 v[12:15], v[28:31], v[112:115], 0
	v_mfma_f32_16x16x32_bf16 v[180:183], v[32:35], v[122:125], v[12:15]
	v_mfma_f32_16x16x32_bf16 v[12:15], v[20:23], v[126:129], 0
	v_mfma_f32_16x16x32_bf16 v[184:187], v[24:27], v[130:133], v[12:15]
	v_mfma_f32_16x16x32_bf16 v[12:15], v[28:31], v[126:129], 0
	v_mfma_f32_16x16x32_bf16 v[188:191], v[32:35], v[130:133], v[12:15]
	s_setprio 0
	s_barrier
	s_add_i32 s39, 0, 0x18000
	s_add_i32 s41, 0, 0x1c000
	v_add_u32_e32 v134, s39, v219
	v_add_u32_e32 v135, s41, v219
	s_nop 0
	ds_read_b128 v[12:15], v134
	ds_read_b128 v[16:19], v134 offset:1024
	ds_read_b128 v[20:23], v134 offset:2048
	ds_read_b128 v[24:27], v134 offset:3072
	ds_read_b128 v[202:205], v135
	ds_read_b128 v[206:209], v135 offset:1024
	ds_read_b128 v[222:225], v135 offset:2048
	ds_read_b128 v[226:229], v135 offset:3072
	s_mov_b64 s[42:43], 0x84100
	s_mov_b32 m0, s25
	v_lshl_add_u64 v[92:93], v[192:193], 0, s[42:43]
	s_mov_b64 s[42:43], 0xc6100
	ds_read_b128 v[28:31], v221 offset:32768
	ds_read_b128 v[32:35], v221 offset:33792
	ds_read_b128 v[64:67], v221 offset:34816
	ds_read_b128 v[230:233], v221 offset:35840
	ds_read_b128 v[234:237], v221 offset:36864
	ds_read_b128 v[238:241], v221 offset:37888
	ds_read_b128 v[242:245], v221 offset:38912
	ds_read_b128 v[246:249], v221 offset:39936
	global_load_lds_dwordx4 v[92:93], off
	v_lshl_add_u64 v[92:93], v[192:193], 0, s[42:43]
	s_mov_b32 m0, s26
	s_nop 0
	global_load_lds_dwordx4 v[92:93], off
	s_waitcnt vmcnt(8)
	s_waitcnt lgkmcnt(0)
	s_barrier
	s_setprio 1
	s_waitcnt lgkmcnt(0)
	v_mfma_f32_16x16x32_bf16 v[68:71], v[12:15], v[28:31], v[68:71]
	v_mfma_f32_16x16x32_bf16 v[130:133], v[16:19], v[32:35], v[68:71]
	v_mfma_f32_16x16x32_bf16 v[68:71], v[20:23], v[28:31], v[72:75]
	v_mfma_f32_16x16x32_bf16 v[126:129], v[24:27], v[32:35], v[68:71]
	v_mfma_f32_16x16x32_bf16 v[68:71], v[12:15], v[64:67], v[76:79]
	v_mfma_f32_16x16x32_bf16 v[112:115], v[16:19], v[230:233], v[68:71]
	v_mfma_f32_16x16x32_bf16 v[68:71], v[20:23], v[64:67], v[80:83]
	v_mfma_f32_16x16x32_bf16 v[108:111], v[24:27], v[230:233], v[68:71]
	v_mfma_f32_16x16x32_bf16 v[68:71], v[12:15], v[234:237], v[84:87]
	v_mfma_f32_16x16x32_bf16 v[96:99], v[16:19], v[238:241], v[68:71]
	v_mfma_f32_16x16x32_bf16 v[68:71], v[20:23], v[234:237], v[88:91]
	v_mfma_f32_16x16x32_bf16 v[92:95], v[24:27], v[238:241], v[68:71]
	v_mfma_f32_16x16x32_bf16 v[68:71], v[12:15], v[242:245], v[100:103]
	v_mfma_f32_16x16x32_bf16 v[80:83], v[16:19], v[246:249], v[68:71]
	v_mfma_f32_16x16x32_bf16 v[68:71], v[20:23], v[242:245], v[104:107]
	v_mfma_f32_16x16x32_bf16 v[76:79], v[24:27], v[246:249], v[68:71]
	s_setprio 0
	s_setprio 1
	v_mfma_f32_16x16x32_bf16 v[68:71], v[202:205], v[28:31], v[118:121]
	v_mfma_f32_16x16x32_bf16 v[28:31], v[222:225], v[28:31], v[36:39]
	v_mfma_f32_16x16x32_bf16 v[118:121], v[226:229], v[32:35], v[28:31]
	v_mfma_f32_16x16x32_bf16 v[28:31], v[202:205], v[64:67], v[40:43]
	v_mfma_f32_16x16x32_bf16 v[104:107], v[206:209], v[230:233], v[28:31]
	v_mfma_f32_16x16x32_bf16 v[28:31], v[222:225], v[64:67], v[44:47]
	v_mfma_f32_16x16x32_bf16 v[100:103], v[226:229], v[230:233], v[28:31]
	v_mfma_f32_16x16x32_bf16 v[28:31], v[202:205], v[234:237], v[48:51]
	v_mfma_f32_16x16x32_bf16 v[88:91], v[206:209], v[238:241], v[28:31]
	v_mfma_f32_16x16x32_bf16 v[28:31], v[222:225], v[234:237], v[52:55]
	v_mfma_f32_16x16x32_bf16 v[84:87], v[226:229], v[238:241], v[28:31]
	v_mfma_f32_16x16x32_bf16 v[28:31], v[202:205], v[242:245], v[56:59]
	v_mfma_f32_16x16x32_bf16 v[72:75], v[206:209], v[246:249], v[28:31]
	v_mfma_f32_16x16x32_bf16 v[28:31], v[222:225], v[242:245], v[60:63]
	v_mfma_f32_16x16x32_bf16 v[122:125], v[206:209], v[32:35], v[68:71]
	v_mfma_f32_16x16x32_bf16 v[68:71], v[226:229], v[246:249], v[28:31]
	s_setprio 0
	s_barrier
; #define PG8_MMA(ai, bj, At, Bt) do { __builtin_amdgcn_s_setprio(1); _Pragma("unroll") for (int m = 0; m < 4; ++m) _Pragma("unroll") for (int n = 0; n < 2; ++n) _Pragma("unroll") for (int k = 0; k < 2; ++k) \
;         acc[ai][bj][m][n] = __builtin_amdgcn_mfma_f32_16x16x32_bf16(Bt[n][k], At[m][k], acc[ai][bj][m][n], 0, 0, 0); __builtin_amdgcn_s_setprio(0); } while (0)
; #define PG8_WAIT_V(n) asm volatile("s_waitcnt vmcnt(" #n ")" ::: "memory")
; #define PG8_TRIP_HEAD(T) const int t = (T); const bool last = (t == nt - 2); \
;             const char* a1 = cA + (size_t)(t + 1) * kstep; \
;             const char* a2 = last ? nA : cA + (size_t)(t + 2) * kstep; const char* b2 = last ? nB : cB + (size_t)(t + 2) * kstep; \
;             const char* a3 = a2 + kstep; const char* b3 = b2 + kstep; \
;             if (last && has_next) S.a_ready(nxt);
; template <class Epi, class Sched, bool ALIGN_EPI = false, bool SP2 = false>
; __device__ __forceinline__ void gemm_phase(PG8_LAS unsigned char* lds, const Gemm g, const Sched& S, const Epi& E) {
;     ...
;         if constexpr (SP2) {
;             { PG8_TRIP_HEAD(0) PG8_TRIP_SP2(asm volatile("s_waitcnt vmcnt(%0)" :: "n"(8 + Epi::NST) : "memory"), PG8_MMAZ) }
;             for (int tt = 2; tt < nt; tt += 2) { PG8_TRIP_HEAD(tt) PG8_TRIP_SP2(PG8_WAIT_V(8), PG8_MMA) }
	s_mov_b64 s[44:45], 0x180
	s_add_i32 s39, s39, s22
	s_nop 1
	v_lshl_add_u64 v[28:29], v[250:251], 0, s[44:45]
	s_mov_b32 m0, s39
	s_mov_b64 s[42:43], 0x40180
	s_add_i32 s40, s39, 0x2000
	ds_read_b128 v[36:39], v221 offset:49152
	ds_read_b128 v[40:43], v221 offset:50176
	ds_read_b128 v[230:233], v221 offset:51200
	ds_read_b128 v[234:237], v221 offset:52224
	ds_read_b128 v[238:241], v221 offset:53248
	ds_read_b128 v[242:245], v221 offset:54272
	ds_read_b128 v[246:249], v221 offset:55296
	ds_read_b128 v[214:217], v221 offset:56320
	global_load_lds_dwordx4 v[28:29], off
	v_lshl_add_u64 v[28:29], v[250:251], 0, s[42:43]
	s_mov_b32 m0, s40
	s_mov_b64 s[42:43], 0x80180
	s_add_i32 s41, s41, s22
	global_load_lds_dwordx4 v[28:29], off
	v_lshl_add_u64 v[28:29], v[250:251], 0, s[42:43]
	s_mov_b32 m0, s41
	s_mov_b64 s[42:43], 0xc0180
	global_load_lds_dwordx4 v[28:29], off
	v_lshl_add_u64 v[28:29], v[250:251], 0, s[42:43]
	s_add_i32 s42, s41, 0x2000
	s_mov_b32 m0, s42
	s_nop 0
	global_load_lds_dwordx4 v[28:29], off
	v_lshl_add_u64 v[28:29], v[192:193], 0, s[44:45]
	s_mov_b32 m0, s27
	s_mov_b64 s[44:45], 0x42180
	global_load_lds_dwordx4 v[28:29], off
	v_lshl_add_u64 v[28:29], v[192:193], 0, s[44:45]
	s_mov_b32 m0, s28
	s_nop 0
	global_load_lds_dwordx4 v[28:29], off
	s_waitcnt vmcnt(8)
	s_waitcnt lgkmcnt(0)
	s_barrier
	s_setprio 1
	s_waitcnt lgkmcnt(0)
	v_mfma_f32_16x16x32_bf16 v[28:31], v[12:15], v[36:39], v[136:139]
	v_mfma_f32_16x16x32_bf16 v[64:67], v[16:19], v[40:43], v[28:31]
	v_mfma_f32_16x16x32_bf16 v[28:31], v[20:23], v[36:39], v[140:143]
	v_mfma_f32_16x16x32_bf16 v[60:63], v[24:27], v[40:43], v[28:31]
	v_mfma_f32_16x16x32_bf16 v[28:31], v[12:15], v[230:233], v[144:147]
	v_mfma_f32_16x16x32_bf16 v[48:51], v[16:19], v[234:237], v[28:31]
	v_mfma_f32_16x16x32_bf16 v[28:31], v[20:23], v[230:233], v[148:151]
	v_mfma_f32_16x16x32_bf16 v[44:47], v[24:27], v[234:237], v[28:31]
	v_mfma_f32_16x16x32_bf16 v[28:31], v[12:15], v[238:241], v[152:155]
	v_mfma_f32_16x16x32_bf16 v[4:7], v[12:15], v[246:249], v[4:7]
	v_mfma_f32_16x16x32_bf16 v[32:35], v[16:19], v[242:245], v[28:31]
	v_mfma_f32_16x16x32_bf16 v[28:31], v[20:23], v[238:241], v[156:159]
	v_mfma_f32_16x16x32_bf16 v[16:19], v[16:19], v[214:217], v[4:7]
	v_mfma_f32_16x16x32_bf16 v[4:7], v[20:23], v[246:249], v[8:11]
	v_mfma_f32_16x16x32_bf16 v[28:31], v[24:27], v[242:245], v[28:31]
	v_mfma_f32_16x16x32_bf16 v[12:15], v[24:27], v[214:217], v[4:7]
	s_setprio 0
	s_setprio 1
	v_mfma_f32_16x16x32_bf16 v[4:7], v[202:205], v[36:39], v[160:163]
	v_mfma_f32_16x16x32_bf16 v[56:59], v[206:209], v[40:43], v[4:7]
	v_mfma_f32_16x16x32_bf16 v[4:7], v[222:225], v[36:39], v[164:167]
	v_mfma_f32_16x16x32_bf16 v[52:55], v[226:229], v[40:43], v[4:7]
	v_mfma_f32_16x16x32_bf16 v[4:7], v[202:205], v[230:233], v[168:171]
	v_mfma_f32_16x16x32_bf16 v[40:43], v[206:209], v[234:237], v[4:7]
	v_mfma_f32_16x16x32_bf16 v[4:7], v[222:225], v[230:233], v[172:175]
	v_mfma_f32_16x16x32_bf16 v[36:39], v[226:229], v[234:237], v[4:7]
	v_mfma_f32_16x16x32_bf16 v[4:7], v[202:205], v[238:241], v[176:179]
	v_mfma_f32_16x16x32_bf16 v[24:27], v[206:209], v[242:245], v[4:7]
	v_mfma_f32_16x16x32_bf16 v[4:7], v[222:225], v[238:241], v[180:183]
	v_mfma_f32_16x16x32_bf16 v[20:23], v[226:229], v[242:245], v[4:7]
	v_mfma_f32_16x16x32_bf16 v[4:7], v[202:205], v[246:249], v[184:187]
	v_mfma_f32_16x16x32_bf16 v[8:11], v[206:209], v[214:217], v[4:7]
	v_mfma_f32_16x16x32_bf16 v[4:7], v[222:225], v[246:249], v[188:191]
	v_mfma_f32_16x16x32_bf16 v[4:7], v[226:229], v[214:217], v[4:7]
	s_setprio 0
	s_barrier
	s_add_u32 s20, s20, 0x84180
	s_addc_u32 s21, s21, 0
	s_add_u32 s8, s8, 0x200
	s_addc_u32 s9, s9, 0
	s_mov_b64 s[48:49], 0x80000
	s_mov_b64 s[50:51], 0x80080
	s_mov_b64 s[52:53], 0xc0000
	s_mov_b64 s[54:55], 0xc0080
	s_mov_b64 s[56:57], 0xc6000

; __device__ __forceinline__ unsigned cvt_pk_bf16(float lo, float hi) { f32x2_c v = {lo, hi}; bf16x2_c b = __builtin_convertvector(v, bf16x2_c); return __builtin_bit_cast(unsigned, b); }
; __device__ __forceinline__ float bf_lo(unsigned u) { return __uint_as_float(u << 16); }
; __device__ __forceinline__ float bf_hi(unsigned u) { return __uint_as_float(u & 0xffff0000u); }
;     __device__ __forceinline__ void operator()(const f32x4 (&acc)[2][2][4][2], const Unit& u, int wr, int wc, int fr, int fq) const {
;     ...
;         for (int ai = 0; ai < 2; ++ai) {
;             u32x4 gv[4], pv[4][2];
; #pragma unroll
;             for (int m = 0; m < 4; ++m) { gv[m] = *(const u32x4*)((const unsigned char*)gt + (size_t)(row0 + ai * HALF + m * 16) * GATE_PITCH + u.pn * 256 + (wc * 4 + fq) * 16);
; #pragma unroll
;                 for (int bj = 0; bj < 2; ++bj) { const size_t off = (size_t)(row0 + ai * HALF + m * 16) * LDT + col0 + bj * HALF;
;                     pv[m][bj] = addp ? *(const u32x4*)(T + off) : (u32x4){0u, 0u, 0u, 0u}; } }
; #pragma unroll
;             for (int m = 0; m < 4; ++m)
; #pragma unroll
;                 for (int bj = 0; bj < 2; ++bj) { const size_t off = (size_t)(row0 + ai * HALF + m * 16) * LDT + col0 + bj * HALF; const unsigned g0 = bj ? gv[m].z : gv[m].x, g1 = bj ? gv[m].w : gv[m].y;
;                     const f32x4 a0 = acc[ai][bj][m][0] * (1.0f / 255.0f), a1 = acc[ai][bj][m][1] * (1.0f / 255.0f);
;                     float o[8] = {a0[0] * (float)(g0 & 255u), a0[1] * (float)((g0 >> 8) & 255u), a0[2] * (float)((g0 >> 16) & 255u), a0[3] * (float)(g0 >> 24), a1[0] * (float)(g1 & 255u), a1[1] * (float)((g1 >> 8) & 255u), a1[2] * (float)((g1 >> 16) & 255u), a1[3] * (float)(g1 >> 24)};
;                     { const u32x4 pw = pv[m][bj];
;                         o[0] += bf_lo(pw.x); o[1] += bf_hi(pw.x); o[2] += bf_lo(pw.y); o[3] += bf_hi(pw.y); o[4] += bf_lo(pw.z); o[5] += bf_hi(pw.z); o[6] += bf_lo(pw.w); o[7] += bf_hi(pw.w); }
;                     u32x4 w; w.x = cvt_pk_bf16(o[0], o[1]); w.y = cvt_pk_bf16(o[2], o[3]); w.z = cvt_pk_bf16(o[4], o[5]); w.w = cvt_pk_bf16(o[6], o[7]);
;                     *(u32x4*)(T + off) = w; }
.LBB0_613:
	s_mov_b32 s20, 0x3b808081
	v_mul_f32_e64 v130, v130, s20
	v_mul_f32_e64 v131, v131, s20
	s_waitcnt vmcnt(0)
	v_cvt_f32_ubyte1_e32 v183, v170
	v_cvt_f32_ubyte0_e32 v182, v170
	v_lshlrev_b32_e32 v184, 16, v178
	v_and_b32_e32 v185, 0xffff0000, v178
	v_mul_f32_e64 v132, v132, s20
	v_mul_f32_e64 v133, v133, s20
	v_fma_f32 v130, v130, v182, v184
	v_fma_f32 v131, v131, v183, v185
	v_cvt_f32_ubyte3_e32 v183, v170
	v_cvt_f32_ubyte2_e32 v182, v170
	v_lshlrev_b32_e32 v178, 16, v179
	v_and_b32_e32 v179, 0xffff0000, v179
	v_mul_f32_e64 v126, v126, s20
	v_mul_f32_e64 v127, v127, s20
	v_fma_f32 v132, v132, v182, v178
	v_fma_f32 v133, v133, v183, v179
	v_cvt_f32_ubyte1_e32 v179, v171
	v_cvt_f32_ubyte0_e32 v178, v171
	v_lshlrev_b32_e32 v182, 16, v180
	v_and_b32_e32 v183, 0xffff0000, v180
	v_mul_f32_e64 v128, v128, s20
	v_mul_f32_e64 v129, v129, s20
	v_fma_f32 v126, v126, v178, v182
	v_fma_f32 v127, v127, v179, v183
	v_cvt_f32_ubyte3_e32 v179, v171
	v_cvt_f32_ubyte2_e32 v178, v171
	v_lshlrev_b32_e32 v170, 16, v181
	v_and_b32_e32 v171, 0xffff0000, v181
	v_fma_f32 v128, v128, v178, v170
	v_fma_f32 v129, v129, v179, v171
	v_cvt_pk_bf16_f32 v130, v130, v131
	v_cvt_pk_bf16_f32 v131, v132, v133
	v_cvt_pk_bf16_f32 v133, v128, v129
	v_mov_b64_e32 v[128:129], s[94:95]
	v_cvt_pk_bf16_f32 v132, v126, v127
	v_mad_i64_i32 v[170:171], s[4:5], v222, s81, v[128:129]
	v_lshlrev_b64 v[126:127], 1, v[206:207]
	v_lshl_add_u64 v[170:171], v[170:171], 0, v[126:127]
	global_store_dwordx4 v[170:171], v[130:133], off
	v_mul_f32_e64 v122, v122, s20
	v_mul_f32_e64 v123, v123, s20
	v_mul_f32_e64 v124, v124, s20
	v_mul_f32_e64 v125, v125, s20
	v_cvt_f32_ubyte1_e32 v131, v172
	v_cvt_f32_ubyte0_e32 v130, v172
	v_lshlrev_b32_e32 v132, 16, v174
	v_and_b32_e32 v133, 0xffff0000, v174
	v_fma_f32 v122, v122, v130, v132
	v_fma_f32 v123, v123, v131, v133
	v_cvt_f32_ubyte3_e32 v131, v172
	v_cvt_f32_ubyte2_e32 v130, v172
	v_lshlrev_b32_e32 v132, 16, v175
	v_and_b32_e32 v133, 0xffff0000, v175
	v_mul_f32_e64 v118, v118, s20
	v_mul_f32_e64 v119, v119, s20
	v_fma_f32 v124, v124, v130, v132
	v_fma_f32 v125, v125, v131, v133
	v_cvt_f32_ubyte1_e32 v131, v173
	v_cvt_f32_ubyte0_e32 v130, v173
	v_lshlrev_b32_e32 v132, 16, v176
	v_and_b32_e32 v133, 0xffff0000, v176
	v_mul_f32_e64 v120, v120, s20
	v_mul_f32_e64 v121, v121, s20
	v_fma_f32 v130, v118, v130, v132
	v_fma_f32 v131, v119, v131, v133
	v_cvt_f32_ubyte3_e32 v119, v173
	v_cvt_f32_ubyte2_e32 v118, v173
	v_lshlrev_b32_e32 v132, 16, v177
	v_and_b32_e32 v133, 0xffff0000, v177
	v_fma_f32 v132, v120, v118, v132
	v_fma_f32 v133, v121, v119, v133
	v_cvt_pk_bf16_f32 v118, v122, v123
	v_cvt_pk_bf16_f32 v119, v124, v125
	v_cvt_pk_bf16_f32 v120, v130, v131
	v_cvt_pk_bf16_f32 v121, v132, v133
	global_store_dwordx4 v[170:171], v[118:121], off offset:256
	v_mul_f32_e64 v112, v112, s20
	v_mul_f32_e64 v113, v113, s20
	v_mul_f32_e64 v114, v114, s20
	v_mul_f32_e64 v115, v115, s20
	v_cvt_f32_ubyte1_e32 v119, v162
	v_cvt_f32_ubyte0_e32 v118, v162
	v_lshlrev_b32_e32 v120, 16, v158
	v_and_b32_e32 v121, 0xffff0000, v158
	v_fma_f32 v112, v112, v118, v120
	v_fma_f32 v113, v113, v119, v121
	v_cvt_f32_ubyte3_e32 v119, v162
	v_cvt_f32_ubyte2_e32 v118, v162
	v_lshlrev_b32_e32 v120, 16, v159
	v_and_b32_e32 v121, 0xffff0000, v159
	v_mul_f32_e64 v108, v108, s20
	v_mul_f32_e64 v109, v109, s20
	v_fma_f32 v114, v114, v118, v120
	v_fma_f32 v115, v115, v119, v121
	v_cvt_f32_ubyte1_e32 v119, v163
	v_cvt_f32_ubyte0_e32 v118, v163
	v_lshlrev_b32_e32 v120, 16, v160
	v_and_b32_e32 v121, 0xffff0000, v160
	v_mul_f32_e64 v110, v110, s20
	v_mul_f32_e64 v111, v111, s20
	v_fma_f32 v118, v108, v118, v120
	v_fma_f32 v119, v109, v119, v121
	v_cvt_f32_ubyte3_e32 v109, v163
	v_cvt_f32_ubyte2_e32 v108, v163
	v_lshlrev_b32_e32 v120, 16, v161
	v_and_b32_e32 v121, 0xffff0000, v161
	v_fma_f32 v120, v110, v108, v120
	v_fma_f32 v121, v111, v109, v121
	v_cvt_pk_bf16_f32 v108, v112, v113
	v_mad_i64_i32 v[112:113], s[4:5], v224, s81, v[128:129]
	v_cvt_pk_bf16_f32 v109, v114, v115
	v_cvt_pk_bf16_f32 v110, v118, v119
	v_cvt_pk_bf16_f32 v111, v120, v121
	v_lshl_add_u64 v[112:113], v[112:113], 0, v[126:127]
	global_store_dwordx4 v[112:113], v[108:111], off
	v_mul_f32_e64 v104, v104, s20
	v_mul_f32_e64 v105, v105, s20
	v_mul_f32_e64 v106, v106, s20
	v_mul_f32_e64 v107, v107, s20
	v_cvt_f32_ubyte1_e32 v109, v164
	v_cvt_f32_ubyte0_e32 v108, v164
	v_lshlrev_b32_e32 v110, 16, v166
	v_and_b32_e32 v111, 0xffff0000, v166
	v_fma_f32 v104, v104, v108, v110
	v_fma_f32 v105, v105, v109, v111
	v_cvt_f32_ubyte3_e32 v109, v164
	v_cvt_f32_ubyte2_e32 v108, v164
	v_lshlrev_b32_e32 v110, 16, v167
	v_and_b32_e32 v111, 0xffff0000, v167
	v_mul_f32_e64 v100, v100, s20
	v_mul_f32_e64 v101, v101, s20
	v_fma_f32 v106, v106, v108, v110
	v_fma_f32 v107, v107, v109, v111
	v_cvt_f32_ubyte1_e32 v109, v165
	v_cvt_f32_ubyte0_e32 v108, v165
	v_lshlrev_b32_e32 v110, 16, v168
	v_and_b32_e32 v111, 0xffff0000, v168
	v_mul_f32_e64 v102, v102, s20
	v_mul_f32_e64 v103, v103, s20
	v_fma_f32 v108, v100, v108, v110
	v_fma_f32 v109, v101, v109, v111
	v_cvt_f32_ubyte3_e32 v101, v165
	v_cvt_f32_ubyte2_e32 v100, v165
	v_lshlrev_b32_e32 v110, 16, v169
	v_and_b32_e32 v111, 0xffff0000, v169
	v_fma_f32 v110, v102, v100, v110
	v_fma_f32 v111, v103, v101, v111
	v_cvt_pk_bf16_f32 v100, v104, v105
	v_cvt_pk_bf16_f32 v101, v106, v107
	v_cvt_pk_bf16_f32 v102, v108, v109
	v_cvt_pk_bf16_f32 v103, v110, v111
; __device__ __forceinline__ unsigned cvt_pk_bf16(float lo, float hi) { f32x2_c v = {lo, hi}; bf16x2_c b = __builtin_convertvector(v, bf16x2_c); return __builtin_bit_cast(unsigned, b); }
; __device__ __forceinline__ float bf_lo(unsigned u) { return __uint_as_float(u << 16); }
; __device__ __forceinline__ float bf_hi(unsigned u) { return __uint_as_float(u & 0xffff0000u); }
;     __device__ __forceinline__ void operator()(const f32x4 (&acc)[2][2][4][2], const Unit& u, int wr, int wc, int fr, int fq) const {
;     ...
;         for (int ai = 0; ai < 2; ++ai) {
;             u32x4 gv[4], pv[4][2];
; #pragma unroll
;             for (int m = 0; m < 4; ++m) { gv[m] = *(const u32x4*)((const unsigned char*)gt + (size_t)(row0 + ai * HALF + m * 16) * GATE_PITCH + u.pn * 256 + (wc * 4 + fq) * 16);
; #pragma unroll
;                 for (int bj = 0; bj < 2; ++bj) { const size_t off = (size_t)(row0 + ai * HALF + m * 16) * LDT + col0 + bj * HALF;
;                     pv[m][bj] = addp ? *(const u32x4*)(T + off) : (u32x4){0u, 0u, 0u, 0u}; } }
; #pragma unroll
;             for (int m = 0; m < 4; ++m)
; #pragma unroll
;                 for (int bj = 0; bj < 2; ++bj) { const size_t off = (size_t)(row0 + ai * HALF + m * 16) * LDT + col0 + bj * HALF; const unsigned g0 = bj ? gv[m].z : gv[m].x, g1 = bj ? gv[m].w : gv[m].y;
;                     const f32x4 a0 = acc[ai][bj][m][0] * (1.0f / 255.0f), a1 = acc[ai][bj][m][1] * (1.0f / 255.0f);
;                     float o[8] = {a0[0] * (float)(g0 & 255u), a0[1] * (float)((g0 >> 8) & 255u), a0[2] * (float)((g0 >> 16) & 255u), a0[3] * (float)(g0 >> 24), a1[0] * (float)(g1 & 255u), a1[1] * (float)((g1 >> 8) & 255u), a1[2] * (float)((g1 >> 16) & 255u), a1[3] * (float)(g1 >> 24)};
;                     { const u32x4 pw = pv[m][bj];
;                         o[0] += bf_lo(pw.x); o[1] += bf_hi(pw.x); o[2] += bf_lo(pw.y); o[3] += bf_hi(pw.y); o[4] += bf_lo(pw.z); o[5] += bf_hi(pw.z); o[6] += bf_lo(pw.w); o[7] += bf_hi(pw.w); }
;                     u32x4 w; w.x = cvt_pk_bf16(o[0], o[1]); w.y = cvt_pk_bf16(o[2], o[3]); w.z = cvt_pk_bf16(o[4], o[5]); w.w = cvt_pk_bf16(o[6], o[7]);
;                     *(u32x4*)(T + off) = w; }
	global_store_dwordx4 v[112:113], v[100:103], off offset:256
	v_mul_f32_e64 v96, v96, s20
	v_mul_f32_e64 v97, v97, s20
	v_mul_f32_e64 v98, v98, s20
	v_mul_f32_e64 v99, v99, s20
	v_cvt_f32_ubyte1_e32 v101, v146
	v_cvt_f32_ubyte0_e32 v100, v146
	v_lshlrev_b32_e32 v102, 16, v150
	v_and_b32_e32 v103, 0xffff0000, v150
	v_fma_f32 v96, v96, v100, v102
	v_fma_f32 v97, v97, v101, v103
	v_cvt_f32_ubyte3_e32 v101, v146
	v_cvt_f32_ubyte2_e32 v100, v146
	v_lshlrev_b32_e32 v102, 16, v151
	v_and_b32_e32 v103, 0xffff0000, v151
	v_mul_f32_e64 v92, v92, s20
	v_mul_f32_e64 v93, v93, s20
	v_fma_f32 v98, v98, v100, v102
	v_fma_f32 v99, v99, v101, v103
	v_cvt_f32_ubyte1_e32 v101, v147
	v_cvt_f32_ubyte0_e32 v100, v147
	v_lshlrev_b32_e32 v102, 16, v152
	v_and_b32_e32 v103, 0xffff0000, v152
	v_mul_f32_e64 v94, v94, s20
	v_mul_f32_e64 v95, v95, s20
	v_fma_f32 v100, v92, v100, v102
	v_fma_f32 v101, v93, v101, v103
	v_cvt_f32_ubyte3_e32 v93, v147
	v_cvt_f32_ubyte2_e32 v92, v147
	v_lshlrev_b32_e32 v102, 16, v153
	v_and_b32_e32 v103, 0xffff0000, v153
	v_fma_f32 v102, v94, v92, v102
	v_fma_f32 v103, v95, v93, v103
	v_cvt_pk_bf16_f32 v92, v96, v97
	v_mad_i64_i32 v[96:97], s[4:5], v223, s81, v[128:129]
	v_cvt_pk_bf16_f32 v93, v98, v99
	v_cvt_pk_bf16_f32 v94, v100, v101
	v_cvt_pk_bf16_f32 v95, v102, v103
	v_lshl_add_u64 v[96:97], v[96:97], 0, v[126:127]
	global_store_dwordx4 v[96:97], v[92:95], off
	v_mul_f32_e64 v88, v88, s20
	v_mul_f32_e64 v89, v89, s20
	v_mul_f32_e64 v90, v90, s20
	v_mul_f32_e64 v91, v91, s20
	v_cvt_f32_ubyte1_e32 v93, v148
	v_cvt_f32_ubyte0_e32 v92, v148
	v_lshlrev_b32_e32 v94, 16, v154
	v_and_b32_e32 v95, 0xffff0000, v154
	v_fma_f32 v88, v88, v92, v94
	v_fma_f32 v89, v89, v93, v95
	v_cvt_f32_ubyte3_e32 v93, v148
	v_cvt_f32_ubyte2_e32 v92, v148
	v_lshlrev_b32_e32 v94, 16, v155
	v_and_b32_e32 v95, 0xffff0000, v155
	v_mul_f32_e64 v84, v84, s20
	v_mul_f32_e64 v85, v85, s20
	v_fma_f32 v90, v90, v92, v94
	v_fma_f32 v91, v91, v93, v95
	v_cvt_f32_ubyte1_e32 v93, v149
	v_cvt_f32_ubyte0_e32 v92, v149
	v_lshlrev_b32_e32 v94, 16, v156
	v_and_b32_e32 v95, 0xffff0000, v156
	v_mul_f32_e64 v86, v86, s20
	v_mul_f32_e64 v87, v87, s20
	v_fma_f32 v92, v84, v92, v94
	v_fma_f32 v93, v85, v93, v95
	v_cvt_f32_ubyte3_e32 v85, v149
	v_cvt_f32_ubyte2_e32 v84, v149
	v_lshlrev_b32_e32 v94, 16, v157
	v_and_b32_e32 v95, 0xffff0000, v157
	v_fma_f32 v94, v86, v84, v94
	v_fma_f32 v95, v87, v85, v95
	v_cvt_pk_bf16_f32 v84, v88, v89
	v_cvt_pk_bf16_f32 v85, v90, v91
	v_cvt_pk_bf16_f32 v86, v92, v93
	v_cvt_pk_bf16_f32 v87, v94, v95
	global_store_dwordx4 v[96:97], v[84:87], off offset:256
	v_mul_f32_e64 v80, v80, s20
	v_mul_f32_e64 v81, v81, s20
	v_mul_f32_e64 v82, v82, s20
	v_mul_f32_e64 v83, v83, s20
	v_cvt_f32_ubyte1_e32 v85, v134
	v_cvt_f32_ubyte0_e32 v84, v134
	v_lshlrev_b32_e32 v86, 16, v138
	v_and_b32_e32 v87, 0xffff0000, v138
	v_fma_f32 v80, v80, v84, v86
	v_fma_f32 v81, v81, v85, v87
	v_cvt_f32_ubyte3_e32 v85, v134
	v_cvt_f32_ubyte2_e32 v84, v134
	v_lshlrev_b32_e32 v86, 16, v139
	v_and_b32_e32 v87, 0xffff0000, v139
	v_mul_f32_e64 v76, v76, s20
	v_mul_f32_e64 v77, v77, s20
	v_fma_f32 v82, v82, v84, v86
	v_fma_f32 v83, v83, v85, v87
	v_cvt_f32_ubyte1_e32 v85, v135
	v_cvt_f32_ubyte0_e32 v84, v135
	v_lshlrev_b32_e32 v86, 16, v140
	v_and_b32_e32 v87, 0xffff0000, v140
	v_mul_f32_e64 v78, v78, s20
	v_mul_f32_e64 v79, v79, s20
	v_fma_f32 v84, v76, v84, v86
	v_fma_f32 v85, v77, v85, v87
	v_cvt_f32_ubyte3_e32 v77, v135
	v_cvt_f32_ubyte2_e32 v76, v135
	v_lshlrev_b32_e32 v86, 16, v141
	v_and_b32_e32 v87, 0xffff0000, v141
	v_fma_f32 v86, v78, v76, v86
	v_fma_f32 v87, v79, v77, v87
	v_cvt_pk_bf16_f32 v76, v80, v81
	v_mad_i64_i32 v[80:81], s[4:5], v117, s81, v[128:129]
	v_cvt_pk_bf16_f32 v77, v82, v83
	v_cvt_pk_bf16_f32 v78, v84, v85
	v_cvt_pk_bf16_f32 v79, v86, v87
	v_lshl_add_u64 v[80:81], v[80:81], 0, v[126:127]
	global_store_dwordx4 v[80:81], v[76:79], off
	v_mul_f32_e64 v72, v72, s20
	v_mul_f32_e64 v73, v73, s20
	v_mul_f32_e64 v74, v74, s20
	v_mul_f32_e64 v75, v75, s20
	v_cvt_f32_ubyte1_e32 v77, v136
	v_cvt_f32_ubyte0_e32 v76, v136
	v_lshlrev_b32_e32 v78, 16, v142
	v_and_b32_e32 v79, 0xffff0000, v142
	v_fma_f32 v72, v72, v76, v78
	v_fma_f32 v73, v73, v77, v79
	v_cvt_f32_ubyte3_e32 v77, v136
	v_cvt_f32_ubyte2_e32 v76, v136
	v_lshlrev_b32_e32 v78, 16, v143
	v_and_b32_e32 v79, 0xffff0000, v143
	v_mul_f32_e64 v68, v68, s20
	v_mul_f32_e64 v69, v69, s20
	v_fma_f32 v74, v74, v76, v78
	v_fma_f32 v75, v75, v77, v79
	v_cvt_f32_ubyte1_e32 v77, v137
	v_cvt_f32_ubyte0_e32 v76, v137
	v_lshlrev_b32_e32 v78, 16, v144
	v_and_b32_e32 v79, 0xffff0000, v144
	v_mul_f32_e64 v70, v70, s20
	v_mul_f32_e64 v71, v71, s20
	v_fma_f32 v76, v68, v76, v78
	v_fma_f32 v77, v69, v77, v79
	v_cvt_f32_ubyte3_e32 v69, v137
	v_cvt_f32_ubyte2_e32 v68, v137
	v_lshlrev_b32_e32 v78, 16, v145
	v_and_b32_e32 v79, 0xffff0000, v145
	v_fma_f32 v78, v70, v68, v78
	v_fma_f32 v79, v71, v69, v79
	v_cvt_pk_bf16_f32 v68, v72, v73
	v_cvt_pk_bf16_f32 v69, v74, v75
	v_cvt_pk_bf16_f32 v70, v76, v77
	v_cvt_pk_bf16_f32 v71, v78, v79
	global_store_dwordx4 v[80:81], v[68:71], off offset:256
	v_add_u32_e32 v121, 0x80, v222
	s_and_b64 vcc, exec, s[8:9]
	v_mad_i64_i32 v[68:69], s[4:5], v121, s0, v[202:203]
	global_load_dwordx4 v[104:107], v[68:69], off
	v_mad_i64_i32 v[68:69], s[4:5], v121, s81, v[204:205]
	v_mov_b32_e32 v117, 0
	v_mov_b32_e32 v118, 0
	v_mov_b32_e32 v119, 0
	s_cbranch_vccnz .LBB0_615
	global_load_dwordx4 v[116:119], v[68:69], off

; __device__ __forceinline__ unsigned cvt_pk_bf16(float lo, float hi) { f32x2_c v = {lo, hi}; bf16x2_c b = __builtin_convertvector(v, bf16x2_c); return __builtin_bit_cast(unsigned, b); }
; __device__ __forceinline__ float bf_lo(unsigned u) { return __uint_as_float(u << 16); }
; __device__ __forceinline__ float bf_hi(unsigned u) { return __uint_as_float(u & 0xffff0000u); }
;     __device__ __forceinline__ void operator()(const f32x4 (&acc)[2][2][4][2], const Unit& u, int wr, int wc, int fr, int fq) const {
;     ...
;         for (int ai = 0; ai < 2; ++ai) {
;             u32x4 gv[4], pv[4][2];
; #pragma unroll
;             for (int m = 0; m < 4; ++m) { gv[m] = *(const u32x4*)((const unsigned char*)gt + (size_t)(row0 + ai * HALF + m * 16) * GATE_PITCH + u.pn * 256 + (wc * 4 + fq) * 16);
; #pragma unroll
;                 for (int bj = 0; bj < 2; ++bj) { const size_t off = (size_t)(row0 + ai * HALF + m * 16) * LDT + col0 + bj * HALF;
;                     pv[m][bj] = addp ? *(const u32x4*)(T + off) : (u32x4){0u, 0u, 0u, 0u}; } }
; #pragma unroll
;             for (int m = 0; m < 4; ++m)
; #pragma unroll
;                 for (int bj = 0; bj < 2; ++bj) { const size_t off = (size_t)(row0 + ai * HALF + m * 16) * LDT + col0 + bj * HALF; const unsigned g0 = bj ? gv[m].z : gv[m].x, g1 = bj ? gv[m].w : gv[m].y;
;                     const f32x4 a0 = acc[ai][bj][m][0] * (1.0f / 255.0f), a1 = acc[ai][bj][m][1] * (1.0f / 255.0f);
;                     float o[8] = {a0[0] * (float)(g0 & 255u), a0[1] * (float)((g0 >> 8) & 255u), a0[2] * (float)((g0 >> 16) & 255u), a0[3] * (float)(g0 >> 24), a1[0] * (float)(g1 & 255u), a1[1] * (float)((g1 >> 8) & 255u), a1[2] * (float)((g1 >> 16) & 255u), a1[3] * (float)(g1 >> 24)};
;                     { const u32x4 pw = pv[m][bj];
;                         o[0] += bf_lo(pw.x); o[1] += bf_hi(pw.x); o[2] += bf_lo(pw.y); o[3] += bf_hi(pw.y); o[4] += bf_lo(pw.z); o[5] += bf_hi(pw.z); o[6] += bf_lo(pw.w); o[7] += bf_hi(pw.w); }
;                     u32x4 w; w.x = cvt_pk_bf16(o[0], o[1]); w.y = cvt_pk_bf16(o[2], o[3]); w.z = cvt_pk_bf16(o[4], o[5]); w.w = cvt_pk_bf16(o[6], o[7]);
;                     *(u32x4*)(T + off) = w; }
.LBB0_629:
	s_mov_b32 s0, 0x3b808081
	v_mul_f32_e64 v64, v64, s0
	v_mul_f32_e64 v65, v65, s0
	s_waitcnt vmcnt(3)
	v_cvt_f32_ubyte1_e32 v113, v104
	v_cvt_f32_ubyte0_e32 v112, v104
	v_lshlrev_b32_e32 v122, 16, v116
	v_and_b32_e32 v123, 0xffff0000, v116
	v_mul_f32_e64 v66, v66, s0
	v_mul_f32_e64 v67, v67, s0
	v_fma_f32 v64, v64, v112, v122
	v_fma_f32 v65, v65, v113, v123
	v_cvt_f32_ubyte3_e32 v113, v104
	v_cvt_f32_ubyte2_e32 v112, v104
	v_lshlrev_b32_e32 v116, 16, v117
	v_and_b32_e32 v117, 0xffff0000, v117
	v_mul_f32_e64 v60, v60, s0
	v_mul_f32_e64 v61, v61, s0
	v_fma_f32 v66, v66, v112, v116
	v_fma_f32 v67, v67, v113, v117
	v_cvt_f32_ubyte1_e32 v113, v105
	v_cvt_f32_ubyte0_e32 v112, v105
	v_lshlrev_b32_e32 v116, 16, v118
	v_and_b32_e32 v117, 0xffff0000, v118
	v_mul_f32_e64 v62, v62, s0
	v_mul_f32_e64 v63, v63, s0
	v_fma_f32 v60, v60, v112, v116
	v_fma_f32 v61, v61, v113, v117
	v_cvt_f32_ubyte3_e32 v113, v105
	v_cvt_f32_ubyte2_e32 v112, v105
	v_lshlrev_b32_e32 v104, 16, v119
	v_and_b32_e32 v105, 0xffff0000, v119
	v_fma_f32 v104, v62, v112, v104
	v_fma_f32 v105, v63, v113, v105
	v_cvt_pk_bf16_f32 v62, v64, v65
	v_cvt_pk_bf16_f32 v64, v60, v61
	v_mov_b64_e32 v[60:61], s[94:95]
	v_cvt_pk_bf16_f32 v63, v66, v67
	v_mad_i64_i32 v[66:67], s[4:5], v121, s81, v[60:61]
	v_cvt_pk_bf16_f32 v65, v104, v105
	v_lshl_add_u64 v[66:67], v[66:67], 0, v[126:127]
	global_store_dwordx4 v[66:67], v[62:65], off
	v_mul_f32_e64 v56, v56, s0
	v_mul_f32_e64 v57, v57, s0
	v_mul_f32_e64 v58, v58, s0
	v_mul_f32_e64 v59, v59, s0
	v_cvt_f32_ubyte1_e32 v63, v106
	v_cvt_f32_ubyte0_e32 v62, v106
	v_lshlrev_b32_e32 v64, 16, v108
	v_and_b32_e32 v65, 0xffff0000, v108
	v_fma_f32 v56, v56, v62, v64
	v_fma_f32 v57, v57, v63, v65
	v_cvt_f32_ubyte3_e32 v63, v106
	v_cvt_f32_ubyte2_e32 v62, v106
	v_lshlrev_b32_e32 v64, 16, v109
	v_and_b32_e32 v65, 0xffff0000, v109
	v_mul_f32_e64 v52, v52, s0
	v_mul_f32_e64 v53, v53, s0
	v_fma_f32 v58, v58, v62, v64
	v_fma_f32 v59, v59, v63, v65
	v_cvt_f32_ubyte1_e32 v63, v107
	v_cvt_f32_ubyte0_e32 v62, v107
	v_lshlrev_b32_e32 v64, 16, v110
	v_and_b32_e32 v65, 0xffff0000, v110
	v_mul_f32_e64 v54, v54, s0
	v_mul_f32_e64 v55, v55, s0
	v_fma_f32 v62, v52, v62, v64
	v_fma_f32 v63, v53, v63, v65
	v_cvt_f32_ubyte3_e32 v53, v107
	v_cvt_f32_ubyte2_e32 v52, v107
	v_lshlrev_b32_e32 v64, 16, v111
	v_and_b32_e32 v65, 0xffff0000, v111
	v_fma_f32 v64, v54, v52, v64
	v_fma_f32 v65, v55, v53, v65
	v_cvt_pk_bf16_f32 v52, v56, v57
	v_cvt_pk_bf16_f32 v53, v58, v59
	v_cvt_pk_bf16_f32 v54, v62, v63
	v_cvt_pk_bf16_f32 v55, v64, v65
	global_store_dwordx4 v[66:67], v[52:55], off offset:256
	v_mul_f32_e64 v48, v48, s0
	v_mul_f32_e64 v49, v49, s0
	v_mul_f32_e64 v50, v50, s0
	v_mul_f32_e64 v51, v51, s0
	s_waitcnt vmcnt(4)
	v_cvt_f32_ubyte1_e32 v53, v92
	v_cvt_f32_ubyte0_e32 v52, v92
	v_lshlrev_b32_e32 v54, 16, v96
	v_and_b32_e32 v55, 0xffff0000, v96
	v_fma_f32 v48, v48, v52, v54
	v_fma_f32 v49, v49, v53, v55
	v_cvt_f32_ubyte3_e32 v53, v92
	v_cvt_f32_ubyte2_e32 v52, v92
	v_lshlrev_b32_e32 v54, 16, v97
	v_and_b32_e32 v55, 0xffff0000, v97
	v_mul_f32_e64 v44, v44, s0
	v_mul_f32_e64 v45, v45, s0
	v_fma_f32 v50, v50, v52, v54
	v_fma_f32 v51, v51, v53, v55
	v_cvt_f32_ubyte1_e32 v53, v93
	v_cvt_f32_ubyte0_e32 v52, v93
	v_lshlrev_b32_e32 v54, 16, v98
	v_and_b32_e32 v55, 0xffff0000, v98
	v_mul_f32_e64 v46, v46, s0
	v_mul_f32_e64 v47, v47, s0
	v_fma_f32 v52, v44, v52, v54
	v_fma_f32 v53, v45, v53, v55
	v_cvt_f32_ubyte3_e32 v45, v93
	v_cvt_f32_ubyte2_e32 v44, v93
	v_lshlrev_b32_e32 v54, 16, v99
	v_and_b32_e32 v55, 0xffff0000, v99
	v_fma_f32 v54, v46, v44, v54
	v_fma_f32 v55, v47, v45, v55
	v_cvt_pk_bf16_f32 v44, v48, v49
	v_mad_i64_i32 v[48:49], s[4:5], v120, s81, v[60:61]
	v_cvt_pk_bf16_f32 v45, v50, v51
	v_cvt_pk_bf16_f32 v46, v52, v53
	v_cvt_pk_bf16_f32 v47, v54, v55
	v_lshl_add_u64 v[48:49], v[48:49], 0, v[126:127]
	global_store_dwordx4 v[48:49], v[44:47], off
	v_mul_f32_e64 v40, v40, s0
	v_mul_f32_e64 v41, v41, s0
	v_mul_f32_e64 v42, v42, s0
	v_mul_f32_e64 v43, v43, s0
	v_cvt_f32_ubyte1_e32 v45, v94
	v_cvt_f32_ubyte0_e32 v44, v94
	v_lshlrev_b32_e32 v46, 16, v100
	v_and_b32_e32 v47, 0xffff0000, v100
	v_fma_f32 v40, v40, v44, v46
	v_fma_f32 v41, v41, v45, v47
	v_cvt_f32_ubyte3_e32 v45, v94
	v_cvt_f32_ubyte2_e32 v44, v94
	v_lshlrev_b32_e32 v46, 16, v101
	v_and_b32_e32 v47, 0xffff0000, v101
	v_mul_f32_e64 v36, v36, s0
	v_mul_f32_e64 v37, v37, s0
	v_fma_f32 v42, v42, v44, v46
	v_fma_f32 v43, v43, v45, v47
	v_cvt_f32_ubyte1_e32 v45, v95
	v_cvt_f32_ubyte0_e32 v44, v95
	v_lshlrev_b32_e32 v46, 16, v102
	v_and_b32_e32 v47, 0xffff0000, v102
	v_mul_f32_e64 v38, v38, s0
	v_mul_f32_e64 v39, v39, s0
	v_fma_f32 v44, v36, v44, v46
	v_fma_f32 v45, v37, v45, v47
	v_cvt_f32_ubyte3_e32 v37, v95
	v_cvt_f32_ubyte2_e32 v36, v95
	v_lshlrev_b32_e32 v46, 16, v103
	v_and_b32_e32 v47, 0xffff0000, v103
	v_fma_f32 v46, v38, v36, v46
	v_fma_f32 v47, v39, v37, v47
	v_cvt_pk_bf16_f32 v36, v40, v41
	v_cvt_pk_bf16_f32 v37, v42, v43
	v_cvt_pk_bf16_f32 v38, v44, v45
	v_cvt_pk_bf16_f32 v39, v46, v47
	global_store_dwordx4 v[48:49], v[36:39], off offset:256
	v_mul_f32_e64 v32, v32, s0
	v_mul_f32_e64 v33, v33, s0
	v_mul_f32_e64 v34, v34, s0
	v_mul_f32_e64 v35, v35, s0
	s_waitcnt vmcnt(5)
; __device__ __forceinline__ float bf_lo(unsigned u) { return __uint_as_float(u << 16); }
;     __device__ __forceinline__ void operator()(const f32x4 (&acc)[2][2][4][2], const Unit& u, int wr, int wc, int fr, int fq) const {
;     ...
;         for (int ai = 0; ai < 2; ++ai) {
;             u32x4 gv[4], pv[4][2];
; #pragma unroll
;             for (int m = 0; m < 4; ++m) { gv[m] = *(const u32x4*)((const unsigned char*)gt + (size_t)(row0 + ai * HALF + m * 16) * GATE_PITCH + u.pn * 256 + (wc * 4 + fq) * 16);
; #pragma unroll
;                 for (int bj = 0; bj < 2; ++bj) { const size_t off = (size_t)(row0 + ai * HALF + m * 16) * LDT + col0 + bj * HALF;
;                     pv[m][bj] = addp ? *(const u32x4*)(T + off) : (u32x4){0u, 0u, 0u, 0u}; } }
; #pragma unroll
;             for (int m = 0; m < 4; ++m)
; #pragma unroll
;                 for (int bj = 0; bj < 2; ++bj) { const size_t off = (size_t)(row0 + ai * HALF + m * 16) * LDT + col0 + bj * HALF; const unsigned g0 = bj ? gv[m].z : gv[m].x, g1 = bj ? gv[m].w : gv[m].y;
;                     const f32x4 a0 = acc[ai][bj][m][0] * (1.0f / 255.0f), a1 = acc[ai][bj][m][1] * (1.0f / 255.0f);
;                     float o[8] = {a0[0] * (float)(g0 & 255u), a0[1] * (float)((g0 >> 8) & 255u), a0[2] * (float)((g0 >> 16) & 255u), a0[3] * (float)(g0 >> 24), a1[0] * (float)(g1 & 255u), a1[1] * (float)((g1 >> 8) & 255u), a1[2] * (float)((g1 >> 16) & 255u), a1[3] * (float)(g1 >> 24)};
;                     { const u32x4 pw = pv[m][bj];
;                         o[0] += bf_lo(pw.x); o[1] += bf_hi(pw.x); o[2] += bf_lo(pw.y); o[3] += bf_hi(pw.y); o[4] += bf_lo(pw.z); o[5] += bf_hi(pw.z); o[6] += bf_lo(pw.w); o[7] += bf_hi(pw.w); }
;                     u32x4 w; w.x = cvt_pk_bf16(o[0], o[1]); w.y = cvt_pk_bf16(o[2], o[3]); w.z = cvt_pk_bf16(o[4], o[5]); w.w = cvt_pk_bf16(o[6], o[7]);
;                     *(u32x4*)(T + off) = w; }
;             asm volatile("" ::: "memory"); }
;     }
; template <class Epi, class Sched, bool ALIGN_EPI = false, bool SP2 = false>
; __device__ __forceinline__ void gemm_phase(PG8_LAS unsigned char* lds, const Gemm g, const Sched& S, const Epi& E) {
;     ...
;         if (!has_next) break;
;         if constexpr (!SP2) {
; #pragma unroll
;         for (int a = 0; a < 2; ++a)
; #pragma unroll
;             for (int b = 0; b < 2; ++b)
; #pragma unroll
;                 for (int m = 0; m < 4; ++m)
; #pragma unroll
	v_cvt_f32_ubyte1_e32 v37, v80
	v_cvt_f32_ubyte0_e32 v36, v80
	v_lshlrev_b32_e32 v38, 16, v84
	v_and_b32_e32 v39, 0xffff0000, v84
	v_fma_f32 v32, v32, v36, v38
	v_fma_f32 v33, v33, v37, v39
	v_cvt_f32_ubyte3_e32 v37, v80
	v_cvt_f32_ubyte2_e32 v36, v80
	v_lshlrev_b32_e32 v38, 16, v85
	v_and_b32_e32 v39, 0xffff0000, v85
	v_mul_f32_e64 v28, v28, s0
	v_mul_f32_e64 v29, v29, s0
	v_fma_f32 v34, v34, v36, v38
	v_fma_f32 v35, v35, v37, v39
	v_cvt_f32_ubyte1_e32 v37, v81
	v_cvt_f32_ubyte0_e32 v36, v81
	v_lshlrev_b32_e32 v38, 16, v86
	v_and_b32_e32 v39, 0xffff0000, v86
	v_mul_f32_e64 v30, v30, s0
	v_mul_f32_e64 v31, v31, s0
	v_fma_f32 v36, v28, v36, v38
	v_fma_f32 v37, v29, v37, v39
	v_cvt_f32_ubyte3_e32 v29, v81
	v_cvt_f32_ubyte2_e32 v28, v81
	v_lshlrev_b32_e32 v38, 16, v87
	v_and_b32_e32 v39, 0xffff0000, v87
	v_fma_f32 v38, v30, v28, v38
	v_fma_f32 v39, v31, v29, v39
	v_cvt_pk_bf16_f32 v28, v32, v33
	v_mad_i64_i32 v[32:33], s[4:5], v115, s81, v[60:61]
	v_cvt_pk_bf16_f32 v29, v34, v35
	v_cvt_pk_bf16_f32 v30, v36, v37
	v_cvt_pk_bf16_f32 v31, v38, v39
	v_lshl_add_u64 v[32:33], v[32:33], 0, v[126:127]
	global_store_dwordx4 v[32:33], v[28:31], off
	v_mul_f32_e64 v24, v24, s0
	v_mul_f32_e64 v25, v25, s0
	v_mul_f32_e64 v26, v26, s0
	v_mul_f32_e64 v27, v27, s0
	v_cvt_f32_ubyte1_e32 v29, v82
	v_cvt_f32_ubyte0_e32 v28, v82
	v_lshlrev_b32_e32 v30, 16, v88
	v_and_b32_e32 v31, 0xffff0000, v88
	v_fma_f32 v24, v24, v28, v30
	v_fma_f32 v25, v25, v29, v31
	v_cvt_f32_ubyte3_e32 v29, v82
	v_cvt_f32_ubyte2_e32 v28, v82
	v_lshlrev_b32_e32 v30, 16, v89
	v_and_b32_e32 v31, 0xffff0000, v89
	v_mul_f32_e64 v20, v20, s0
	v_mul_f32_e64 v21, v21, s0
	v_fma_f32 v26, v26, v28, v30
	v_fma_f32 v27, v27, v29, v31
	v_cvt_f32_ubyte1_e32 v29, v83
	v_cvt_f32_ubyte0_e32 v28, v83
	v_lshlrev_b32_e32 v30, 16, v90
	v_and_b32_e32 v31, 0xffff0000, v90
	v_mul_f32_e64 v22, v22, s0
	v_mul_f32_e64 v23, v23, s0
	v_fma_f32 v28, v20, v28, v30
	v_fma_f32 v29, v21, v29, v31
	v_cvt_f32_ubyte3_e32 v21, v83
	v_cvt_f32_ubyte2_e32 v20, v83
	v_lshlrev_b32_e32 v30, 16, v91
	v_and_b32_e32 v31, 0xffff0000, v91
	v_fma_f32 v30, v22, v20, v30
	v_fma_f32 v31, v23, v21, v31
	v_cvt_pk_bf16_f32 v20, v24, v25
	v_cvt_pk_bf16_f32 v21, v26, v27
	v_cvt_pk_bf16_f32 v22, v28, v29
	v_cvt_pk_bf16_f32 v23, v30, v31
	global_store_dwordx4 v[32:33], v[20:23], off offset:256
	v_mul_f32_e64 v16, v16, s0
	v_mul_f32_e64 v17, v17, s0
	v_mul_f32_e64 v18, v18, s0
	v_mul_f32_e64 v19, v19, s0
	s_waitcnt vmcnt(6)
	v_cvt_f32_ubyte1_e32 v21, v68
	v_cvt_f32_ubyte0_e32 v20, v68
	v_lshlrev_b32_e32 v22, 16, v76
	v_and_b32_e32 v23, 0xffff0000, v76
	v_fma_f32 v16, v16, v20, v22
	v_fma_f32 v17, v17, v21, v23
	v_cvt_f32_ubyte3_e32 v21, v68
	v_cvt_f32_ubyte2_e32 v20, v68
	v_lshlrev_b32_e32 v22, 16, v77
	v_and_b32_e32 v23, 0xffff0000, v77
	v_mul_f32_e64 v12, v12, s0
	v_mul_f32_e64 v13, v13, s0
	v_fma_f32 v18, v18, v20, v22
	v_fma_f32 v19, v19, v21, v23
	v_cvt_f32_ubyte1_e32 v21, v69
	v_cvt_f32_ubyte0_e32 v20, v69
	v_lshlrev_b32_e32 v22, 16, v78
	v_and_b32_e32 v23, 0xffff0000, v78
	v_mul_f32_e64 v14, v14, s0
	v_mul_f32_e64 v15, v15, s0
	v_fma_f32 v20, v12, v20, v22
	v_fma_f32 v21, v13, v21, v23
	v_cvt_f32_ubyte3_e32 v13, v69
	v_cvt_f32_ubyte2_e32 v12, v69
	v_lshlrev_b32_e32 v22, 16, v79
	v_and_b32_e32 v23, 0xffff0000, v79
	v_fma_f32 v22, v14, v12, v22
	v_fma_f32 v23, v15, v13, v23
	v_cvt_pk_bf16_f32 v12, v16, v17
	v_mad_i64_i32 v[16:17], s[4:5], v114, s81, v[60:61]
	v_cvt_pk_bf16_f32 v13, v18, v19
	v_cvt_pk_bf16_f32 v14, v20, v21
	v_cvt_pk_bf16_f32 v15, v22, v23
	v_lshl_add_u64 v[16:17], v[16:17], 0, v[126:127]
	global_store_dwordx4 v[16:17], v[12:15], off
	v_mul_f32_e64 v8, v8, s0
	v_mul_f32_e64 v9, v9, s0
	v_mul_f32_e64 v10, v10, s0
	v_mul_f32_e64 v11, v11, s0
	v_cvt_f32_ubyte1_e32 v13, v70
	v_cvt_f32_ubyte0_e32 v12, v70
	v_lshlrev_b32_e32 v14, 16, v72
	v_and_b32_e32 v15, 0xffff0000, v72
	v_fma_f32 v8, v8, v12, v14
	v_fma_f32 v9, v9, v13, v15
	v_cvt_f32_ubyte3_e32 v13, v70
	v_cvt_f32_ubyte2_e32 v12, v70
	v_lshlrev_b32_e32 v14, 16, v73
	v_and_b32_e32 v15, 0xffff0000, v73
	v_mul_f32_e64 v4, v4, s0
	v_mul_f32_e64 v5, v5, s0
	v_fma_f32 v10, v10, v12, v14
	v_fma_f32 v11, v11, v13, v15
	v_cvt_f32_ubyte1_e32 v13, v71
	v_cvt_f32_ubyte0_e32 v12, v71
	v_lshlrev_b32_e32 v14, 16, v74
	v_and_b32_e32 v15, 0xffff0000, v74
	v_mul_f32_e64 v6, v6, s0
	v_mul_f32_e64 v7, v7, s0
	v_fma_f32 v12, v4, v12, v14
	v_fma_f32 v13, v5, v13, v15
	v_cvt_f32_ubyte3_e32 v5, v71
	v_cvt_f32_ubyte2_e32 v4, v71
	v_lshlrev_b32_e32 v14, 16, v75
	v_and_b32_e32 v15, 0xffff0000, v75
	v_fma_f32 v14, v6, v4, v14
	v_fma_f32 v15, v7, v5, v15
	v_cvt_pk_bf16_f32 v4, v8, v9
	v_cvt_pk_bf16_f32 v5, v10, v11
	v_cvt_pk_bf16_f32 v6, v12, v13
	v_cvt_pk_bf16_f32 v7, v14, v15
	global_store_dwordx4 v[16:17], v[4:7], off offset:256
	s_and_b64 vcc, exec, s[6:7]
	s_mov_b64 s[4:5], -1
	s_cbranch_vccnz .LBB0_582
	s_andn2_b64 vcc, exec, s[10:11]
	s_cbranch_vccnz .LBB0_581
	s_barrier
	s_branch .LBB0_581

;     __device__ bool next(int i, Unit& u) const { const int rounds = nwg / G; if (i >= rounds) return false; return StaticOrder::next(rounds - 1 - i, u); }
;     __device__ bool next(int i, Unit& u) const { const int rounds = nwg / G; if (i >= 2 * rounds) return false; const bool ok = StaticOrder::next(i >= rounds ? i - rounds : i, u); u.z = (i >= rounds) ? 1 : 0; return ok; }
; #define PG8_TRIP_HEAD(T) const int t = (T); const bool last = (t == nt - 2); \
;             const char* a1 = cA + (size_t)(t + 1) * kstep; \
;             const char* a2 = last ? nA : cA + (size_t)(t + 2) * kstep; const char* b2 = last ? nB : cB + (size_t)(t + 2) * kstep; \
;             const char* a3 = a2 + kstep; const char* b3 = b2 + kstep; \
;             if (last && has_next) S.a_ready(nxt);
; template <class Epi, class Sched, bool ALIGN_EPI = false, bool SP2 = false>
; __device__ __forceinline__ void gemm_phase(PG8_LAS unsigned char* lds, const Gemm g, const Sched& S, const Epi& E) {
;     ...
;         const bool has_next = S.next(ui + 1, nxt);
;         const char* nA = has_next ? (const char*)S.opA(g, nxt) + (size_t)nxt.pm * tstepA : cA; const char* nB = has_next ? (const char*)S.opB(g, nxt) + (size_t)nxt.pn * tstepB : cB;
;     ...
;         if constexpr (SP2) {
;             { PG8_TRIP_HEAD(0) PG8_TRIP_SP2(asm volatile("s_waitcnt vmcnt(%0)" :: "n"(8 + Epi::NST) : "memory"), PG8_MMAZ) }
.LBB0_699:
	s_ashr_i32 s19, s18, 31
	s_lshl_b64 s[4:5], s[18:19], 20
	v_readlane_b32 s22, v254, 33
	v_readlane_b32 s23, v254, 34
	s_add_u32 s22, s22, s4
	s_addc_u32 s23, s23, s5
	s_add_i32 s33, 0, 0x10000
	s_add_i32 s41, 0, 0x14000
	v_add_u32_e32 v116, s33, v176
	v_add_u32_e32 v117, s41, v176
	ds_read_b128 v[4:7], v116
	ds_read_b128 v[8:11], v116 offset:1024
	ds_read_b128 v[12:15], v116 offset:2048
	ds_read_b128 v[16:19], v116 offset:3072
	ds_read_b128 v[20:23], v117
	ds_read_b128 v[24:27], v117 offset:1024
	ds_read_b128 v[28:31], v117 offset:2048
	ds_read_b128 v[32:35], v117 offset:3072
	s_and_b64 s[4:5], s[10:11], exec
	s_cselect_b32 s3, s23, s25
	s_cselect_b32 s4, s22, s24
	v_lshl_add_u64 v[208:209], s[26:27], 0, v[162:163]
	s_mov_b64 s[10:11], 0x84080
	s_add_i32 s5, s29, 0xc000
	v_lshl_add_u64 v[68:69], v[208:209], 0, s[10:11]
	s_mov_b32 m0, s5
	s_mov_b64 s[10:11], 0xc6080
	s_add_i32 s19, s29, 0xe000
	ds_read_b128 v[36:39], v178
	ds_read_b128 v[40:43], v178 offset:1024
	ds_read_b128 v[44:47], v178 offset:2048
	ds_read_b128 v[48:51], v178 offset:3072
	ds_read_b128 v[52:55], v178 offset:4096
	ds_read_b128 v[56:59], v178 offset:5120
	ds_read_b128 v[60:63], v178 offset:6144
	ds_read_b128 v[64:67], v178 offset:7168
	global_load_lds_dwordx4 v[68:69], off
	v_lshl_add_u64 v[68:69], v[208:209], 0, s[10:11]
	s_mov_b32 m0, s19
	s_nop 0
	global_load_lds_dwordx4 v[68:69], off
	s_waitcnt vmcnt(16)
	s_waitcnt lgkmcnt(0)
	s_barrier
	s_setprio 1
	s_waitcnt lgkmcnt(0)
	v_mfma_f32_16x16x32_bf16 v[92:95], v[4:7], v[60:63], 0
	v_mfma_f32_16x16x32_bf16 v[68:71], v[4:7], v[36:39], 0
	v_mfma_f32_16x16x32_bf16 v[72:75], v[12:15], v[36:39], 0
	v_mfma_f32_16x16x32_bf16 v[76:79], v[4:7], v[44:47], 0
	v_mfma_f32_16x16x32_bf16 v[80:83], v[12:15], v[44:47], 0
	v_mfma_f32_16x16x32_bf16 v[84:87], v[4:7], v[52:55], 0
	v_mfma_f32_16x16x32_bf16 v[88:91], v[12:15], v[52:55], 0
	v_mfma_f32_16x16x32_bf16 v[100:103], v[8:11], v[64:67], v[92:95]
	v_mfma_f32_16x16x32_bf16 v[92:95], v[12:15], v[60:63], 0
	v_mfma_f32_16x16x32_bf16 v[68:71], v[8:11], v[40:43], v[68:71]
	v_mfma_f32_16x16x32_bf16 v[72:75], v[16:19], v[40:43], v[72:75]
	v_mfma_f32_16x16x32_bf16 v[76:79], v[8:11], v[48:51], v[76:79]
	v_mfma_f32_16x16x32_bf16 v[80:83], v[16:19], v[48:51], v[80:83]
	v_mfma_f32_16x16x32_bf16 v[84:87], v[8:11], v[56:59], v[84:87]
	v_mfma_f32_16x16x32_bf16 v[88:91], v[16:19], v[56:59], v[88:91]
	v_mfma_f32_16x16x32_bf16 v[104:107], v[16:19], v[64:67], v[92:95]
	s_setprio 0
	s_setprio 1
	v_mfma_f32_16x16x32_bf16 v[92:95], v[20:23], v[36:39], 0
	v_mfma_f32_16x16x32_bf16 v[36:39], v[28:31], v[36:39], 0
	v_mfma_f32_16x16x32_bf16 v[120:123], v[24:27], v[40:43], v[92:95]
	v_mfma_f32_16x16x32_bf16 v[36:39], v[32:35], v[40:43], v[36:39]
	v_mfma_f32_16x16x32_bf16 v[40:43], v[20:23], v[44:47], 0
	v_mfma_f32_16x16x32_bf16 v[44:47], v[28:31], v[44:47], 0
	v_mfma_f32_16x16x32_bf16 v[40:43], v[24:27], v[48:51], v[40:43]
	v_mfma_f32_16x16x32_bf16 v[44:47], v[32:35], v[48:51], v[44:47]
	v_mfma_f32_16x16x32_bf16 v[48:51], v[20:23], v[52:55], 0
	v_mfma_f32_16x16x32_bf16 v[52:55], v[28:31], v[52:55], 0
	v_mfma_f32_16x16x32_bf16 v[48:51], v[24:27], v[56:59], v[48:51]
	v_mfma_f32_16x16x32_bf16 v[52:55], v[32:35], v[56:59], v[52:55]
	v_mfma_f32_16x16x32_bf16 v[56:59], v[20:23], v[60:63], 0
	v_mfma_f32_16x16x32_bf16 v[60:63], v[28:31], v[60:63], 0
	v_mfma_f32_16x16x32_bf16 v[56:59], v[24:27], v[64:67], v[56:59]
	v_mfma_f32_16x16x32_bf16 v[60:63], v[32:35], v[64:67], v[60:63]
	s_setprio 0
	s_barrier
	v_lshl_add_u64 v[250:251], s[24:25], 0, v[160:161]
	s_mov_b64 s[10:11], 0x100
	s_add_i32 s33, s33, s28
	v_lshl_add_u64 v[118:119], v[250:251], 0, s[10:11]
	s_mov_b32 m0, s33
	s_mov_b64 s[42:43], 0x40100
	s_add_i32 s40, s33, 0x2000
	ds_read_b128 v[64:67], v178 offset:16384
	ds_read_b128 v[92:95], v178 offset:17408
	ds_read_b128 v[96:99], v178 offset:18432
	ds_read_b128 v[108:111], v178 offset:19456
	ds_read_b128 v[112:115], v178 offset:20480
	ds_read_b128 v[124:127], v178 offset:21504
	ds_read_b128 v[128:131], v178 offset:22528
	ds_read_b128 v[132:135], v178 offset:23552
	global_load_lds_dwordx4 v[118:119], off
	v_lshl_add_u64 v[118:119], v[250:251], 0, s[42:43]
	s_mov_b32 m0, s40
	s_mov_b64 s[42:43], 0x80100
	s_add_i32 s41, s41, s28
	global_load_lds_dwordx4 v[118:119], off
	v_lshl_add_u64 v[118:119], v[250:251], 0, s[42:43]
	s_mov_b32 m0, s41
	s_mov_b64 s[42:43], 0xc0100
	global_load_lds_dwordx4 v[118:119], off
	v_lshl_add_u64 v[118:119], v[250:251], 0, s[42:43]
	s_add_i32 s42, s41, 0x2000
	s_mov_b32 m0, s42
	s_nop 0
	global_load_lds_dwordx4 v[118:119], off
	v_lshl_add_u64 v[118:119], v[208:209], 0, s[10:11]
	s_mov_b32 m0, s29
	s_mov_b64 s[10:11], 0x42100
	global_load_lds_dwordx4 v[118:119], off
	v_lshl_add_u64 v[118:119], v[208:209], 0, s[10:11]
	s_mov_b32 m0, s30
	s_nop 0
	global_load_lds_dwordx4 v[118:119], off
	s_waitcnt vmcnt(16)
	s_waitcnt lgkmcnt(0)
	s_barrier
	s_setprio 1
	s_waitcnt lgkmcnt(0)
	v_mfma_f32_16x16x32_bf16 v[136:139], v[4:7], v[64:67], 0
	v_mfma_f32_16x16x32_bf16 v[144:147], v[8:11], v[92:95], v[136:139]
	v_mfma_f32_16x16x32_bf16 v[136:139], v[12:15], v[64:67], 0
	v_mfma_f32_16x16x32_bf16 v[148:151], v[16:19], v[92:95], v[136:139]
	v_mfma_f32_16x16x32_bf16 v[136:139], v[4:7], v[96:99], 0
	v_mfma_f32_16x16x32_bf16 v[152:155], v[8:11], v[108:111], v[136:139]
	v_mfma_f32_16x16x32_bf16 v[136:139], v[12:15], v[96:99], 0
	v_mfma_f32_16x16x32_bf16 v[156:159], v[16:19], v[108:111], v[136:139]
	v_mfma_f32_16x16x32_bf16 v[136:139], v[4:7], v[112:115], 0
	v_mfma_f32_16x16x32_bf16 v[4:7], v[4:7], v[128:131], 0
	v_mfma_f32_16x16x32_bf16 v[166:169], v[8:11], v[124:127], v[136:139]
	v_mfma_f32_16x16x32_bf16 v[4:7], v[8:11], v[132:135], v[4:7]
	v_mfma_f32_16x16x32_bf16 v[8:11], v[12:15], v[128:131], 0
	v_mfma_f32_16x16x32_bf16 v[136:139], v[12:15], v[112:115], 0
	v_mfma_f32_16x16x32_bf16 v[8:11], v[16:19], v[132:135], v[8:11]
	v_mfma_f32_16x16x32_bf16 v[170:173], v[16:19], v[124:127], v[136:139]
	s_setprio 0
	s_setprio 1
	v_mfma_f32_16x16x32_bf16 v[12:15], v[20:23], v[64:67], 0
	v_mfma_f32_16x16x32_bf16 v[180:183], v[24:27], v[92:95], v[12:15]
	v_mfma_f32_16x16x32_bf16 v[12:15], v[28:31], v[64:67], 0
	v_mfma_f32_16x16x32_bf16 v[184:187], v[32:35], v[92:95], v[12:15]
	v_mfma_f32_16x16x32_bf16 v[12:15], v[20:23], v[96:99], 0
	v_mfma_f32_16x16x32_bf16 v[188:191], v[24:27], v[108:111], v[12:15]
	v_mfma_f32_16x16x32_bf16 v[12:15], v[28:31], v[96:99], 0
	v_mfma_f32_16x16x32_bf16 v[192:195], v[32:35], v[108:111], v[12:15]
	v_mfma_f32_16x16x32_bf16 v[12:15], v[20:23], v[112:115], 0
	v_mfma_f32_16x16x32_bf16 v[196:199], v[24:27], v[124:127], v[12:15]
	v_mfma_f32_16x16x32_bf16 v[12:15], v[28:31], v[112:115], 0
	v_mfma_f32_16x16x32_bf16 v[200:203], v[32:35], v[124:127], v[12:15]
	v_mfma_f32_16x16x32_bf16 v[12:15], v[20:23], v[128:131], 0
	v_mfma_f32_16x16x32_bf16 v[204:207], v[24:27], v[132:135], v[12:15]
	v_mfma_f32_16x16x32_bf16 v[12:15], v[28:31], v[128:131], 0
	v_mfma_f32_16x16x32_bf16 v[132:135], v[32:35], v[132:135], v[12:15]
	s_setprio 0
	s_barrier
	s_add_i32 s43, 0, 0x18000
	s_add_i32 s45, 0, 0x1c000
	v_add_u32_e32 v118, s43, v176
	v_add_u32_e32 v119, s45, v176
	s_nop 0
	ds_read_b128 v[12:15], v118
	ds_read_b128 v[16:19], v118 offset:1024
	ds_read_b128 v[20:23], v118 offset:2048
	ds_read_b128 v[24:27], v118 offset:3072
	ds_read_b128 v[214:217], v119
	ds_read_b128 v[218:221], v119 offset:1024
	ds_read_b128 v[222:225], v119 offset:2048
	ds_read_b128 v[226:229], v119 offset:3072
	s_mov_b64 s[10:11], 0x84100
	s_mov_b32 m0, s31
	v_lshl_add_u64 v[92:93], v[208:209], 0, s[10:11]
	s_mov_b64 s[10:11], 0xc6100
	ds_read_b128 v[28:31], v178 offset:32768
	ds_read_b128 v[32:35], v178 offset:33792
	ds_read_b128 v[64:67], v178 offset:34816
	ds_read_b128 v[230:233], v178 offset:35840
	ds_read_b128 v[234:237], v178 offset:36864
	ds_read_b128 v[238:241], v178 offset:37888
	ds_read_b128 v[242:245], v178 offset:38912
	ds_read_b128 v[246:249], v178 offset:39936
	global_load_lds_dwordx4 v[92:93], off
	v_lshl_add_u64 v[92:93], v[208:209], 0, s[10:11]
	s_mov_b32 m0, s34
	s_nop 0
	global_load_lds_dwordx4 v[92:93], off
	s_waitcnt vmcnt(8)
	s_waitcnt lgkmcnt(0)
	s_barrier
	s_setprio 1
	s_waitcnt lgkmcnt(0)
	v_mfma_f32_16x16x32_bf16 v[68:71], v[12:15], v[28:31], v[68:71]
	v_mfma_f32_16x16x32_bf16 v[140:143], v[16:19], v[32:35], v[68:71]
	v_mfma_f32_16x16x32_bf16 v[68:71], v[20:23], v[28:31], v[72:75]
	v_mfma_f32_16x16x32_bf16 v[136:139], v[24:27], v[32:35], v[68:71]
	v_mfma_f32_16x16x32_bf16 v[68:71], v[12:15], v[64:67], v[76:79]
	v_mfma_f32_16x16x32_bf16 v[112:115], v[16:19], v[230:233], v[68:71]
	v_mfma_f32_16x16x32_bf16 v[68:71], v[20:23], v[64:67], v[80:83]
	v_mfma_f32_16x16x32_bf16 v[108:111], v[24:27], v[230:233], v[68:71]
	v_mfma_f32_16x16x32_bf16 v[68:71], v[12:15], v[234:237], v[84:87]
	v_mfma_f32_16x16x32_bf16 v[96:99], v[16:19], v[238:241], v[68:71]
	v_mfma_f32_16x16x32_bf16 v[68:71], v[20:23], v[234:237], v[88:91]
	v_mfma_f32_16x16x32_bf16 v[92:95], v[24:27], v[238:241], v[68:71]
	v_mfma_f32_16x16x32_bf16 v[68:71], v[12:15], v[242:245], v[100:103]
	v_mfma_f32_16x16x32_bf16 v[80:83], v[16:19], v[246:249], v[68:71]
	v_mfma_f32_16x16x32_bf16 v[68:71], v[20:23], v[242:245], v[104:107]
	v_mfma_f32_16x16x32_bf16 v[76:79], v[24:27], v[246:249], v[68:71]
	s_setprio 0
	s_setprio 1
	v_mfma_f32_16x16x32_bf16 v[68:71], v[214:217], v[28:31], v[120:123]
	v_mfma_f32_16x16x32_bf16 v[28:31], v[222:225], v[28:31], v[36:39]
	v_mfma_f32_16x16x32_bf16 v[124:127], v[226:229], v[32:35], v[28:31]
	v_mfma_f32_16x16x32_bf16 v[28:31], v[214:217], v[64:67], v[40:43]
	v_mfma_f32_16x16x32_bf16 v[104:107], v[218:221], v[230:233], v[28:31]
	v_mfma_f32_16x16x32_bf16 v[28:31], v[222:225], v[64:67], v[44:47]
	v_mfma_f32_16x16x32_bf16 v[100:103], v[226:229], v[230:233], v[28:31]
	v_mfma_f32_16x16x32_bf16 v[28:31], v[214:217], v[234:237], v[48:51]
	v_mfma_f32_16x16x32_bf16 v[88:91], v[218:221], v[238:241], v[28:31]
	v_mfma_f32_16x16x32_bf16 v[28:31], v[222:225], v[234:237], v[52:55]
	v_mfma_f32_16x16x32_bf16 v[84:87], v[226:229], v[238:241], v[28:31]
	v_mfma_f32_16x16x32_bf16 v[28:31], v[214:217], v[242:245], v[56:59]
	v_mfma_f32_16x16x32_bf16 v[72:75], v[218:221], v[246:249], v[28:31]
	v_mfma_f32_16x16x32_bf16 v[28:31], v[222:225], v[242:245], v[60:63]
	v_mfma_f32_16x16x32_bf16 v[128:131], v[218:221], v[32:35], v[68:71]
	v_mfma_f32_16x16x32_bf16 v[68:71], v[226:229], v[246:249], v[28:31]
	s_setprio 0
	s_barrier
; #define PG8_MMA(ai, bj, At, Bt) do { __builtin_amdgcn_s_setprio(1); _Pragma("unroll") for (int m = 0; m < 4; ++m) _Pragma("unroll") for (int n = 0; n < 2; ++n) _Pragma("unroll") for (int k = 0; k < 2; ++k) \
;         acc[ai][bj][m][n] = __builtin_amdgcn_mfma_f32_16x16x32_bf16(Bt[n][k], At[m][k], acc[ai][bj][m][n], 0, 0, 0); __builtin_amdgcn_s_setprio(0); } while (0)
; #define PG8_WAIT_V(n) asm volatile("s_waitcnt vmcnt(" #n ")" ::: "memory")
; #define PG8_TRIP_HEAD(T) const int t = (T); const bool last = (t == nt - 2); \
;             const char* a1 = cA + (size_t)(t + 1) * kstep; \
;             const char* a2 = last ? nA : cA + (size_t)(t + 2) * kstep; const char* b2 = last ? nB : cB + (size_t)(t + 2) * kstep; \
;             const char* a3 = a2 + kstep; const char* b3 = b2 + kstep; \
;             if (last && has_next) S.a_ready(nxt);
; template <class Epi, class Sched, bool ALIGN_EPI = false, bool SP2 = false>
; __device__ __forceinline__ void gemm_phase(PG8_LAS unsigned char* lds, const Gemm g, const Sched& S, const Epi& E) {
;     ...
;         if constexpr (SP2) {
;             { PG8_TRIP_HEAD(0) PG8_TRIP_SP2(asm volatile("s_waitcnt vmcnt(%0)" :: "n"(8 + Epi::NST) : "memory"), PG8_MMAZ) }
;             for (int tt = 2; tt < nt; tt += 2) { PG8_TRIP_HEAD(tt) PG8_TRIP_SP2(PG8_WAIT_V(8), PG8_MMA) }
	s_mov_b64 s[10:11], 0x180
	s_add_i32 s43, s43, s28
	s_nop 1
	v_lshl_add_u64 v[28:29], v[250:251], 0, s[10:11]
	s_mov_b32 m0, s43
	s_mov_b64 s[46:47], 0x40180
	s_add_i32 s44, s43, 0x2000
	ds_read_b128 v[36:39], v178 offset:49152
	ds_read_b128 v[40:43], v178 offset:50176
	ds_read_b128 v[120:123], v178 offset:51200
	ds_read_b128 v[230:233], v178 offset:52224
	ds_read_b128 v[234:237], v178 offset:53248
	ds_read_b128 v[238:241], v178 offset:54272
	ds_read_b128 v[242:245], v178 offset:55296
	ds_read_b128 v[246:249], v178 offset:56320
	global_load_lds_dwordx4 v[28:29], off
	v_lshl_add_u64 v[28:29], v[250:251], 0, s[46:47]
	s_mov_b32 m0, s44
	s_mov_b64 s[46:47], 0x80180
	s_add_i32 s45, s45, s28
	global_load_lds_dwordx4 v[28:29], off
	v_lshl_add_u64 v[28:29], v[250:251], 0, s[46:47]
	s_mov_b32 m0, s45
	s_mov_b64 s[46:47], 0xc0180
	global_load_lds_dwordx4 v[28:29], off
	v_lshl_add_u64 v[28:29], v[250:251], 0, s[46:47]
	s_add_i32 s46, s45, 0x2000
	s_mov_b32 m0, s46
	s_nop 0
	global_load_lds_dwordx4 v[28:29], off
	v_lshl_add_u64 v[28:29], v[208:209], 0, s[10:11]
	s_mov_b32 m0, s36
	s_mov_b64 s[10:11], 0x42180
	global_load_lds_dwordx4 v[28:29], off
	v_lshl_add_u64 v[28:29], v[208:209], 0, s[10:11]
	s_mov_b32 m0, s37
	s_nop 0
	global_load_lds_dwordx4 v[28:29], off
	s_waitcnt vmcnt(8)
	s_waitcnt lgkmcnt(0)
	s_barrier
	s_setprio 1
	s_waitcnt lgkmcnt(0)
	v_mfma_f32_16x16x32_bf16 v[28:31], v[12:15], v[36:39], v[144:147]
	v_mfma_f32_16x16x32_bf16 v[56:59], v[16:19], v[40:43], v[28:31]
	v_mfma_f32_16x16x32_bf16 v[28:31], v[20:23], v[36:39], v[148:151]
	v_mfma_f32_16x16x32_bf16 v[52:55], v[24:27], v[40:43], v[28:31]
	v_mfma_f32_16x16x32_bf16 v[28:31], v[12:15], v[120:123], v[152:155]
	v_mfma_f32_16x16x32_bf16 v[48:51], v[16:19], v[230:233], v[28:31]
	v_mfma_f32_16x16x32_bf16 v[28:31], v[20:23], v[120:123], v[156:159]
	v_mfma_f32_16x16x32_bf16 v[44:47], v[24:27], v[230:233], v[28:31]
	v_mfma_f32_16x16x32_bf16 v[28:31], v[12:15], v[234:237], v[166:169]
	v_mfma_f32_16x16x32_bf16 v[4:7], v[12:15], v[242:245], v[4:7]
	v_mfma_f32_16x16x32_bf16 v[32:35], v[16:19], v[238:241], v[28:31]
	v_mfma_f32_16x16x32_bf16 v[28:31], v[20:23], v[234:237], v[170:173]
	v_mfma_f32_16x16x32_bf16 v[16:19], v[16:19], v[246:249], v[4:7]
	v_mfma_f32_16x16x32_bf16 v[4:7], v[20:23], v[242:245], v[8:11]
	v_mfma_f32_16x16x32_bf16 v[28:31], v[24:27], v[238:241], v[28:31]
	v_mfma_f32_16x16x32_bf16 v[12:15], v[24:27], v[246:249], v[4:7]
	s_setprio 0
	s_setprio 1
	v_mfma_f32_16x16x32_bf16 v[4:7], v[214:217], v[36:39], v[180:183]
	v_mfma_f32_16x16x32_bf16 v[64:67], v[218:221], v[40:43], v[4:7]
	v_mfma_f32_16x16x32_bf16 v[4:7], v[222:225], v[36:39], v[184:187]
	v_mfma_f32_16x16x32_bf16 v[60:63], v[226:229], v[40:43], v[4:7]
	v_mfma_f32_16x16x32_bf16 v[4:7], v[214:217], v[120:123], v[188:191]
	v_mfma_f32_16x16x32_bf16 v[40:43], v[218:221], v[230:233], v[4:7]
	v_mfma_f32_16x16x32_bf16 v[4:7], v[222:225], v[120:123], v[192:195]
	v_mfma_f32_16x16x32_bf16 v[36:39], v[226:229], v[230:233], v[4:7]
	v_mfma_f32_16x16x32_bf16 v[4:7], v[214:217], v[234:237], v[196:199]
	v_mfma_f32_16x16x32_bf16 v[24:27], v[218:221], v[238:241], v[4:7]
	v_mfma_f32_16x16x32_bf16 v[4:7], v[222:225], v[234:237], v[200:203]
	v_mfma_f32_16x16x32_bf16 v[20:23], v[226:229], v[238:241], v[4:7]
	v_mfma_f32_16x16x32_bf16 v[4:7], v[214:217], v[242:245], v[204:207]
	v_mfma_f32_16x16x32_bf16 v[8:11], v[218:221], v[246:249], v[4:7]
	v_mfma_f32_16x16x32_bf16 v[4:7], v[222:225], v[242:245], v[132:135]
	v_mfma_f32_16x16x32_bf16 v[4:7], v[226:229], v[246:249], v[4:7]
	s_setprio 0
	s_barrier
	s_add_u32 s10, s26, 0x84180
	s_addc_u32 s11, s27, 0
	s_add_u32 s24, s24, 0x200
	s_addc_u32 s25, s25, 0
	s_mov_b32 s26, 0
	s_mov_b64 s[52:53], 0x80000
	s_mov_b64 s[54:55], 0x80080
	s_mov_b64 s[56:57], 0xc0000
	s_mov_b64 s[60:61], 0xc0080
	s_mov_b64 s[62:63], 0xc6000

; __device__ __forceinline__ unsigned cvt_pk_bf16(float lo, float hi) { f32x2_c v = {lo, hi}; bf16x2_c b = __builtin_convertvector(v, bf16x2_c); return __builtin_bit_cast(unsigned, b); }
; __device__ __forceinline__ float bf_lo(unsigned u) { return __uint_as_float(u << 16); }
; __device__ __forceinline__ float bf_hi(unsigned u) { return __uint_as_float(u & 0xffff0000u); }
;     __device__ __forceinline__ void operator()(const f32x4 (&acc)[2][2][4][2], const Unit& u, int wr, int wc, int fr, int fq) const {
;     ...
;         for (int ai = 0; ai < 2; ++ai) {
;             u32x4 xv[4][2];
; #pragma unroll
;             for (int m = 0; m < 4; ++m)
; #pragma unroll
;                 for (int bj = 0; bj < 2; ++bj) xv[m][bj] = *(const u32x4*)(Hx + (size_t)(row0 + ai * HALF + m * 16) * LDT + col0 + bj * HALF);
;             float ssm[4];
; #pragma unroll
;             for (int m = 0; m < 4; ++m) { const int row = row0 + ai * HALF + m * 16; bf16_t* hp = Hx + (size_t)row * LDT + col0;
;                 float ss = 0.f;
; #pragma unroll
;                 for (int bj = 0; bj < 2; ++bj) { const u32x4 x = xv[m][bj]; const f32x4 a0 = acc[ai][bj][m][0], a1 = acc[ai][bj][m][1];
;                     const float y0 = bf_lo(x.x) + a0[0] * scale, y1 = bf_hi(x.x) + a0[1] * scale, y2 = bf_lo(x.y) + a0[2] * scale, y3 = bf_hi(x.y) + a0[3] * scale;
;                     const float y4 = bf_lo(x.z) + a1[0] * scale, y5 = bf_hi(x.z) + a1[1] * scale, y6 = bf_lo(x.w) + a1[2] * scale, y7 = bf_hi(x.w) + a1[3] * scale;
;                     ss += ((y0 * y0 + y1 * y1) + (y2 * y2 + y3 * y3)) + ((y4 * y4 + y5 * y5) + (y6 * y6 + y7 * y7));
;                     u32x4 w; w.x = cvt_pk_bf16(y0, y1); w.y = cvt_pk_bf16(y2, y3); w.z = cvt_pk_bf16(y4, y5); w.w = cvt_pk_bf16(y6, y7);
;                     *(u32x4*)(hp + bj * HALF) = w; }
;                 ss += __shfl_xor(ss, 16); ss += __shfl_xor(ss, 32); ssm[m] = ss; }
.LBB0_703:
	v_lshl_or_b32 v116, s0, 8, v177
	v_ashrrev_i32_e32 v117, 31, v116
	v_readlane_b32 s4, v254, 23
	v_lshlrev_b64 v[166:167], 1, v[116:117]
	v_readlane_b32 s5, v254, 24
	v_lshl_add_u32 v181, s2, 8, v174
	v_or_b32_e32 v196, 16, v181
	v_lshl_add_u64 v[168:169], s[4:5], 0, v[166:167]
	v_mad_i64_i32 v[116:117], s[2:3], v181, s81, v[168:169]
	global_load_dwordx4 v[182:185], v[116:117], off
	global_load_dwordx4 v[156:159], v[116:117], off offset:256
	v_mad_i64_i32 v[116:117], s[2:3], v196, s81, v[168:169]
	global_load_dwordx4 v[152:155], v[116:117], off
	global_load_dwordx4 v[148:151], v[116:117], off offset:256
	v_or_b32_e32 v195, 32, v181
	v_mad_i64_i32 v[116:117], s[2:3], v195, s81, v[168:169]
	global_load_dwordx4 v[144:147], v[116:117], off
	global_load_dwordx4 v[132:135], v[116:117], off offset:256
	v_and_b32_e32 v119, 64, v210
	v_xor_b32_e32 v118, 16, v210
	v_add_u32_e32 v119, 64, v119
	v_cmp_lt_i32_e32 vcc, v118, v119
	v_or_b32_e32 v194, 48, v181
	v_mad_i64_i32 v[116:117], s[2:3], v194, s81, v[168:169]
	v_cndmask_b32_e32 v118, v210, v118, vcc
	v_lshlrev_b32_e32 v180, 2, v118
	v_xor_b32_e32 v118, 32, v210
	v_cmp_lt_i32_e32 vcc, v118, v119
	v_mov_b64_e32 v[170:171], s[4:5]
	v_mad_i64_i32 v[172:173], s[2:3], v181, s81, v[170:171]
	v_cndmask_b32_e32 v118, v210, v118, vcc
	v_lshlrev_b32_e32 v179, 2, v118
	global_load_dwordx4 v[120:123], v[116:117], off
	s_nop 0
	global_load_dwordx4 v[116:119], v[116:117], off offset:256
	v_lshl_add_u64 v[172:173], v[172:173], 0, v[166:167]
	v_cmp_lt_i32_e32 vcc, 0, v3
	s_waitcnt vmcnt(0)
	v_lshlrev_b32_e32 v186, 16, v182
	v_and_b32_e32 v187, 0xffff0000, v182
	v_lshlrev_b32_e32 v182, 16, v183
	v_and_b32_e32 v183, 0xffff0000, v183
	v_add_f32_e64 v142, v142, v182
	v_add_f32_e64 v143, v143, v183
	v_lshlrev_b32_e32 v182, 16, v184
	v_and_b32_e32 v183, 0xffff0000, v184
	v_add_f32_e64 v182, v136, v182
	v_add_f32_e64 v183, v137, v183
	v_lshlrev_b32_e32 v136, 16, v185
	v_and_b32_e32 v137, 0xffff0000, v185
	v_add_f32_e64 v140, v140, v186
	v_add_f32_e64 v141, v141, v187
	v_add_f32_e64 v184, v138, v136
	v_add_f32_e64 v185, v139, v137
	v_cvt_pk_bf16_f32 v136, v140, v141
	v_cvt_pk_bf16_f32 v137, v142, v143
	v_cvt_pk_bf16_f32 v138, v182, v183
	v_cvt_pk_bf16_f32 v139, v184, v185
	global_store_dwordx4 v[172:173], v[136:139], off
	v_mul_f32_e64 v190, v182, v182
	v_mul_f32_e64 v191, v183, v183
	v_mul_f32_e64 v192, v184, v184
	v_mul_f32_e64 v193, v185, v185
	v_lshlrev_b32_e32 v136, 16, v156
	v_and_b32_e32 v137, 0xffff0000, v156
	v_add_f32_e64 v128, v128, v136
	v_add_f32_e64 v129, v129, v137
	v_lshlrev_b32_e32 v136, 16, v157
	v_and_b32_e32 v137, 0xffff0000, v157
	v_add_f32_e64 v130, v130, v136
	v_add_f32_e64 v131, v131, v137
	v_lshlrev_b32_e32 v136, 16, v158
	v_and_b32_e32 v137, 0xffff0000, v158
	v_add_f32_e64 v136, v124, v136
	v_add_f32_e64 v137, v125, v137
	v_lshlrev_b32_e32 v124, 16, v159
	v_and_b32_e32 v125, 0xffff0000, v159
	v_add_f32_e64 v138, v126, v124
	v_add_f32_e64 v139, v127, v125
	v_mul_f32_e64 v124, v128, v128
	v_mul_f32_e64 v125, v129, v129
	v_mul_f32_e64 v126, v130, v130
	v_mul_f32_e64 v127, v131, v131
	v_add_f32_e32 v124, v124, v125
	v_add_f32_e32 v126, v126, v127
	v_mul_f32_e64 v186, v140, v140
	v_mul_f32_e64 v187, v141, v141
	v_mul_f32_e64 v188, v142, v142
	v_mul_f32_e64 v189, v143, v143
	v_mul_f32_e64 v140, v136, v136
	v_mul_f32_e64 v141, v137, v137
	v_mul_f32_e64 v142, v138, v138
	v_mul_f32_e64 v143, v139, v139
	v_add_f32_e32 v124, v124, v126
	v_add_f32_e32 v125, v192, v193
	v_add_f32_e32 v126, v190, v191
	v_add_f32_e32 v142, v142, v143
	v_add_f32_e32 v140, v140, v141
	v_add_f32_e32 v125, v126, v125
	v_add_f32_e32 v126, v188, v189
	v_add_f32_e32 v127, v186, v187
	v_add_f32_e32 v140, v140, v142
	v_add_f32_e32 v126, v127, v126
	v_add_f32_e32 v124, v124, v140
	v_add_f32_e32 v125, v126, v125
	v_add_f32_e32 v140, v125, v124
	v_cvt_pk_bf16_f32 v124, v128, v129
	v_lshlrev_b32_e32 v128, 16, v152
	v_and_b32_e32 v129, 0xffff0000, v152
	v_add_f32_e64 v112, v112, v128
	v_add_f32_e64 v113, v113, v129
	v_lshlrev_b32_e32 v128, 16, v153
	v_and_b32_e32 v129, 0xffff0000, v153
	v_add_f32_e64 v114, v114, v128
	v_add_f32_e64 v115, v115, v129
	v_lshlrev_b32_e32 v128, 16, v154
	v_and_b32_e32 v129, 0xffff0000, v154
	v_cvt_pk_bf16_f32 v125, v130, v131
	v_cvt_pk_bf16_f32 v126, v136, v137
	v_cvt_pk_bf16_f32 v127, v138, v139
	v_add_f32_e64 v128, v108, v128
	v_add_f32_e64 v129, v109, v129
	v_lshlrev_b32_e32 v108, 16, v155
	v_and_b32_e32 v109, 0xffff0000, v155
	global_store_dwordx4 v[172:173], v[124:127], off offset:256
	v_add_f32_e64 v130, v110, v108
	v_add_f32_e64 v131, v111, v109
	v_cvt_pk_bf16_f32 v108, v112, v113
	v_mad_i64_i32 v[126:127], s[2:3], v196, s81, v[170:171]
	v_lshl_add_u64 v[126:127], v[126:127], 0, v[166:167]
	v_cvt_pk_bf16_f32 v109, v114, v115
	v_cvt_pk_bf16_f32 v110, v128, v129
	v_cvt_pk_bf16_f32 v111, v130, v131
	ds_bpermute_b32 v124, v180, v140
	global_store_dwordx4 v[126:127], v[108:111], off
	v_mul_f32_e64 v142, v130, v130
	v_mul_f32_e64 v143, v131, v131
	v_mul_f32_e64 v136, v112, v112
	v_mul_f32_e64 v137, v113, v113
	v_lshlrev_b32_e32 v108, 16, v148
	v_and_b32_e32 v109, 0xffff0000, v148
	v_add_f32_e64 v104, v104, v108
	v_add_f32_e64 v105, v105, v109
	v_lshlrev_b32_e32 v108, 16, v149
	v_and_b32_e32 v109, 0xffff0000, v149
	v_add_f32_e64 v106, v106, v108
	v_add_f32_e64 v107, v107, v109
	v_lshlrev_b32_e32 v108, 16, v150
	v_and_b32_e32 v109, 0xffff0000, v150
	v_add_f32_e64 v108, v100, v108
	v_add_f32_e64 v109, v101, v109
	v_lshlrev_b32_e32 v100, 16, v151
	v_and_b32_e32 v101, 0xffff0000, v151
	v_add_f32_e64 v110, v102, v100
	v_add_f32_e64 v111, v103, v101
	v_mul_f32_e64 v100, v104, v104
	v_mul_f32_e64 v101, v105, v105
	v_mul_f32_e64 v102, v106, v106
	v_mul_f32_e64 v103, v107, v107
	s_waitcnt lgkmcnt(0)
; __device__ __forceinline__ unsigned cvt_pk_bf16(float lo, float hi) { f32x2_c v = {lo, hi}; bf16x2_c b = __builtin_convertvector(v, bf16x2_c); return __builtin_bit_cast(unsigned, b); }
; __device__ __forceinline__ float bf_lo(unsigned u) { return __uint_as_float(u << 16); }
; __device__ __forceinline__ float bf_hi(unsigned u) { return __uint_as_float(u & 0xffff0000u); }
;     __device__ __forceinline__ void operator()(const f32x4 (&acc)[2][2][4][2], const Unit& u, int wr, int wc, int fr, int fq) const {
;     ...
;                 for (int bj = 0; bj < 2; ++bj) xv[m][bj] = *(const u32x4*)(Hx + (size_t)(row0 + ai * HALF + m * 16) * LDT + col0 + bj * HALF);
;             float ssm[4];
; #pragma unroll
;             for (int m = 0; m < 4; ++m) { const int row = row0 + ai * HALF + m * 16; bf16_t* hp = Hx + (size_t)row * LDT + col0;
;                 float ss = 0.f;
; #pragma unroll
;                 for (int bj = 0; bj < 2; ++bj) { const u32x4 x = xv[m][bj]; const f32x4 a0 = acc[ai][bj][m][0], a1 = acc[ai][bj][m][1];
;                     const float y0 = bf_lo(x.x) + a0[0] * scale, y1 = bf_hi(x.x) + a0[1] * scale, y2 = bf_lo(x.y) + a0[2] * scale, y3 = bf_hi(x.y) + a0[3] * scale;
;                     const float y4 = bf_lo(x.z) + a1[0] * scale, y5 = bf_hi(x.z) + a1[1] * scale, y6 = bf_lo(x.w) + a1[2] * scale, y7 = bf_hi(x.w) + a1[3] * scale;
;                     ss += ((y0 * y0 + y1 * y1) + (y2 * y2 + y3 * y3)) + ((y4 * y4 + y5 * y5) + (y6 * y6 + y7 * y7));
;                     u32x4 w; w.x = cvt_pk_bf16(y0, y1); w.y = cvt_pk_bf16(y2, y3); w.z = cvt_pk_bf16(y4, y5); w.w = cvt_pk_bf16(y6, y7);
;                     *(u32x4*)(hp + bj * HALF) = w; }
;                 ss += __shfl_xor(ss, 16); ss += __shfl_xor(ss, 32); ssm[m] = ss; }
;             { const float sv = (fq == 0) ? ssm[0] : (fq == 1) ? ssm[1] : (fq == 2) ? ssm[2] : ssm[3];
	v_add_f32_e32 v124, v140, v124
	v_mul_f32_e64 v140, v128, v128
	v_mul_f32_e64 v141, v129, v129
	v_add_f32_e32 v102, v102, v103
	v_add_f32_e32 v100, v100, v101
	v_mul_f32_e64 v138, v114, v114
	v_mul_f32_e64 v139, v115, v115
	v_mul_f32_e64 v112, v108, v108
	v_mul_f32_e64 v113, v109, v109
	v_mul_f32_e64 v114, v110, v110
	v_mul_f32_e64 v115, v111, v111
	v_add_f32_e32 v100, v100, v102
	v_add_f32_e32 v101, v142, v143
	v_add_f32_e32 v102, v140, v141
	v_add_f32_e32 v114, v114, v115
	v_add_f32_e32 v112, v112, v113
	v_add_f32_e32 v101, v102, v101
	v_add_f32_e32 v102, v138, v139
	v_add_f32_e32 v103, v136, v137
	v_add_f32_e32 v112, v112, v114
	v_add_f32_e32 v102, v103, v102
	v_add_f32_e32 v100, v100, v112
	v_add_f32_e32 v101, v102, v101
	v_add_f32_e32 v112, v101, v100
	v_cvt_pk_bf16_f32 v100, v104, v105
	v_lshlrev_b32_e32 v104, 16, v144
	v_and_b32_e32 v105, 0xffff0000, v144
	v_add_f32_e64 v96, v96, v104
	v_add_f32_e64 v97, v97, v105
	v_lshlrev_b32_e32 v104, 16, v145
	v_and_b32_e32 v105, 0xffff0000, v145
	v_add_f32_e64 v98, v98, v104
	v_add_f32_e64 v99, v99, v105
	v_lshlrev_b32_e32 v104, 16, v146
	v_and_b32_e32 v105, 0xffff0000, v146
	v_cvt_pk_bf16_f32 v101, v106, v107
	v_cvt_pk_bf16_f32 v102, v108, v109
	v_cvt_pk_bf16_f32 v103, v110, v111
	v_add_f32_e64 v104, v92, v104
	v_add_f32_e64 v105, v93, v105
	v_lshlrev_b32_e32 v92, 16, v147
	v_and_b32_e32 v93, 0xffff0000, v147
	global_store_dwordx4 v[126:127], v[100:103], off offset:256
	v_add_f32_e64 v106, v94, v92
	v_add_f32_e64 v107, v95, v93
	v_cvt_pk_bf16_f32 v92, v96, v97
	v_mad_i64_i32 v[102:103], s[2:3], v195, s81, v[170:171]
	v_lshl_add_u64 v[102:103], v[102:103], 0, v[166:167]
	v_cvt_pk_bf16_f32 v93, v98, v99
	v_cvt_pk_bf16_f32 v94, v104, v105
	v_cvt_pk_bf16_f32 v95, v106, v107
	ds_bpermute_b32 v100, v180, v112
	global_store_dwordx4 v[102:103], v[92:95], off
	v_mul_f32_e64 v114, v106, v106
	v_mul_f32_e64 v115, v107, v107
	v_mul_f32_e64 v108, v96, v96
	v_mul_f32_e64 v109, v97, v97
	v_lshlrev_b32_e32 v92, 16, v132
	v_and_b32_e32 v93, 0xffff0000, v132
	v_add_f32_e64 v88, v88, v92
	v_add_f32_e64 v89, v89, v93
	v_lshlrev_b32_e32 v92, 16, v133
	v_and_b32_e32 v93, 0xffff0000, v133
	v_add_f32_e64 v90, v90, v92
	v_add_f32_e64 v91, v91, v93
	v_lshlrev_b32_e32 v92, 16, v134
	v_and_b32_e32 v93, 0xffff0000, v134
	v_add_f32_e64 v92, v84, v92
	v_add_f32_e64 v93, v85, v93
	v_lshlrev_b32_e32 v84, 16, v135
	v_and_b32_e32 v85, 0xffff0000, v135
	v_add_f32_e64 v94, v86, v84
	v_add_f32_e64 v95, v87, v85
	v_mul_f32_e64 v84, v88, v88
	v_mul_f32_e64 v85, v89, v89
	v_mul_f32_e64 v86, v90, v90
	v_mul_f32_e64 v87, v91, v91
	s_waitcnt lgkmcnt(0)
	v_add_f32_e32 v100, v112, v100
	v_mul_f32_e64 v112, v104, v104
	v_mul_f32_e64 v113, v105, v105
	v_add_f32_e32 v86, v86, v87
	v_add_f32_e32 v84, v84, v85
	v_mul_f32_e64 v110, v98, v98
	v_mul_f32_e64 v111, v99, v99
	v_mul_f32_e64 v96, v92, v92
	v_mul_f32_e64 v97, v93, v93
	v_mul_f32_e64 v98, v94, v94
	v_mul_f32_e64 v99, v95, v95
	v_add_f32_e32 v84, v84, v86
	v_add_f32_e32 v85, v114, v115
	v_add_f32_e32 v86, v112, v113
	v_add_f32_e32 v98, v98, v99
	v_add_f32_e32 v96, v96, v97
	v_add_f32_e32 v85, v86, v85
	v_add_f32_e32 v86, v110, v111
	v_add_f32_e32 v87, v108, v109
	v_add_f32_e32 v96, v96, v98
	v_add_f32_e32 v86, v87, v86
	v_add_f32_e32 v84, v84, v96
	v_add_f32_e32 v85, v86, v85
	v_add_f32_e32 v96, v85, v84
	v_cvt_pk_bf16_f32 v84, v88, v89
	v_lshlrev_b32_e32 v88, 16, v120
	v_and_b32_e32 v89, 0xffff0000, v120
	v_add_f32_e64 v80, v80, v88
	v_add_f32_e64 v81, v81, v89
	v_lshlrev_b32_e32 v88, 16, v121
	v_and_b32_e32 v89, 0xffff0000, v121
	v_add_f32_e64 v82, v82, v88
	v_add_f32_e64 v83, v83, v89
	v_lshlrev_b32_e32 v88, 16, v122
	v_and_b32_e32 v89, 0xffff0000, v122
	v_cvt_pk_bf16_f32 v85, v90, v91
	v_cvt_pk_bf16_f32 v86, v92, v93
	v_cvt_pk_bf16_f32 v87, v94, v95
	v_add_f32_e64 v88, v76, v88
	v_add_f32_e64 v89, v77, v89
	v_lshlrev_b32_e32 v76, 16, v123
	v_and_b32_e32 v77, 0xffff0000, v123
	global_store_dwordx4 v[102:103], v[84:87], off offset:256
	v_add_f32_e64 v90, v78, v76
	v_add_f32_e64 v91, v79, v77
	v_cvt_pk_bf16_f32 v76, v80, v81
	v_mad_i64_i32 v[86:87], s[2:3], v194, s81, v[170:171]
	v_lshl_add_u64 v[86:87], v[86:87], 0, v[166:167]
	v_cvt_pk_bf16_f32 v77, v82, v83
	v_cvt_pk_bf16_f32 v78, v88, v89
	v_cvt_pk_bf16_f32 v79, v90, v91
	ds_bpermute_b32 v84, v180, v96
	global_store_dwordx4 v[86:87], v[76:79], off
	v_mul_f32_e64 v98, v90, v90
	v_mul_f32_e64 v99, v91, v91
	v_mul_f32_e64 v92, v80, v80
	v_mul_f32_e64 v93, v81, v81
	v_lshlrev_b32_e32 v76, 16, v116
	v_and_b32_e32 v77, 0xffff0000, v116
	v_add_f32_e64 v72, v72, v76
	v_add_f32_e64 v73, v73, v77
	v_lshlrev_b32_e32 v76, 16, v117
	v_and_b32_e32 v77, 0xffff0000, v117
	v_add_f32_e64 v74, v74, v76
	v_add_f32_e64 v75, v75, v77
	v_lshlrev_b32_e32 v76, 16, v118
	v_and_b32_e32 v77, 0xffff0000, v118
	v_add_f32_e64 v76, v68, v76
	v_add_f32_e64 v77, v69, v77
	v_lshlrev_b32_e32 v68, 16, v119
	v_and_b32_e32 v69, 0xffff0000, v119
	v_add_f32_e64 v78, v70, v68
	v_add_f32_e64 v79, v71, v69
	v_mul_f32_e64 v68, v72, v72
	v_mul_f32_e64 v69, v73, v73
	v_mul_f32_e64 v70, v74, v74
	v_mul_f32_e64 v71, v75, v75
	s_waitcnt lgkmcnt(0)
	v_add_f32_e32 v84, v96, v84
	v_mul_f32_e64 v96, v88, v88
	v_mul_f32_e64 v97, v89, v89
	v_add_f32_e32 v70, v70, v71
	v_add_f32_e32 v68, v68, v69
	v_mul_f32_e64 v94, v82, v82
	v_mul_f32_e64 v95, v83, v83
	v_mul_f32_e64 v80, v76, v76
	v_mul_f32_e64 v81, v77, v77
	v_mul_f32_e64 v82, v78, v78
	v_mul_f32_e64 v83, v79, v79
	v_add_f32_e32 v68, v68, v70
	v_add_f32_e32 v69, v98, v99
	v_add_f32_e32 v70, v96, v97
	v_add_f32_e32 v82, v82, v83
	v_add_f32_e32 v80, v80, v81
	v_add_f32_e32 v69, v70, v69
	v_add_f32_e32 v70, v94, v95
	v_add_f32_e32 v71, v92, v93
	v_add_f32_e32 v80, v80, v82
	v_add_f32_e32 v70, v71, v70
	v_add_f32_e32 v68, v68, v80
	v_add_f32_e32 v69, v70, v69
	v_add_f32_e32 v80, v69, v68
	v_cvt_pk_bf16_f32 v68, v72, v73
	v_cvt_pk_bf16_f32 v69, v74, v75
	v_cvt_pk_bf16_f32 v70, v76, v77
	v_cvt_pk_bf16_f32 v71, v78, v79
	global_store_dwordx4 v[86:87], v[68:71], off offset:256
	ds_bpermute_b32 v68, v180, v80
	ds_bpermute_b32 v125, v179, v124
	ds_bpermute_b32 v101, v179, v100
	ds_bpermute_b32 v85, v179, v84
	s_waitcnt lgkmcnt(3)
	v_add_f32_e32 v69, v80, v68
	ds_bpermute_b32 v70, v179, v69
	s_and_saveexec_b64 s[2:3], vcc
	s_xor_b64 s[4:5], exec, s[2:3]
	s_cbranch_execz .LBB0_709
	v_cmp_ne_u32_e32 vcc, 1, v3
	s_and_saveexec_b64 s[2:3], vcc
	s_xor_b64 s[10:11], exec, s[2:3]
	s_cbranch_execz .LBB0_706
	s_waitcnt lgkmcnt(0)
	v_add_f32_e32 v68, v69, v70
	v_add_f32_e32 v69, v84, v85
	v_cndmask_b32_e64 v68, v68, v69, s[6:7]

; __device__ __forceinline__ unsigned cvt_pk_bf16(float lo, float hi) { f32x2_c v = {lo, hi}; bf16x2_c b = __builtin_convertvector(v, bf16x2_c); return __builtin_bit_cast(unsigned, b); }
; __device__ __forceinline__ float bf_lo(unsigned u) { return __uint_as_float(u << 16); }
; __device__ __forceinline__ float bf_hi(unsigned u) { return __uint_as_float(u & 0xffff0000u); }
;     __device__ __forceinline__ void operator()(const f32x4 (&acc)[2][2][4][2], const Unit& u, int wr, int wc, int fr, int fq) const {
;     ...
;                 for (int bj = 0; bj < 2; ++bj) xv[m][bj] = *(const u32x4*)(Hx + (size_t)(row0 + ai * HALF + m * 16) * LDT + col0 + bj * HALF);
;             float ssm[4];
; #pragma unroll
;             for (int m = 0; m < 4; ++m) { const int row = row0 + ai * HALF + m * 16; bf16_t* hp = Hx + (size_t)row * LDT + col0;
;                 float ss = 0.f;
; #pragma unroll
;                 for (int bj = 0; bj < 2; ++bj) { const u32x4 x = xv[m][bj]; const f32x4 a0 = acc[ai][bj][m][0], a1 = acc[ai][bj][m][1];
;                     const float y0 = bf_lo(x.x) + a0[0] * scale, y1 = bf_hi(x.x) + a0[1] * scale, y2 = bf_lo(x.y) + a0[2] * scale, y3 = bf_hi(x.y) + a0[3] * scale;
;                     const float y4 = bf_lo(x.z) + a1[0] * scale, y5 = bf_hi(x.z) + a1[1] * scale, y6 = bf_lo(x.w) + a1[2] * scale, y7 = bf_hi(x.w) + a1[3] * scale;
;                     ss += ((y0 * y0 + y1 * y1) + (y2 * y2 + y3 * y3)) + ((y4 * y4 + y5 * y5) + (y6 * y6 + y7 * y7));
;                     u32x4 w; w.x = cvt_pk_bf16(y0, y1); w.y = cvt_pk_bf16(y2, y3); w.z = cvt_pk_bf16(y4, y5); w.w = cvt_pk_bf16(y6, y7);
;                     *(u32x4*)(hp + bj * HALF) = w; }
;                 ss += __shfl_xor(ss, 16); ss += __shfl_xor(ss, 32); ssm[m] = ss; }
;             { const float sv = (fq == 0) ? ssm[0] : (fq == 1) ? ssm[1] : (fq == 2) ? ssm[2] : ssm[3];
;               ssq[(size_t)(row0 + ai * HALF + fq * 16) * 32 + u.pn * 4 + wc] = sv; }
.LBB0_711:
	s_or_b64 exec, exec, s[4:5]
	v_or_b32_e32 v92, v181, v175
	v_ashrrev_i32_e32 v93, 31, v92
	s_lshl_b32 s10, s0, 2
	s_waitcnt lgkmcnt(0)
	v_lshlrev_b64 v[70:71], 7, v[92:93]
	s_ashr_i32 s11, s10, 31
	v_lshl_add_u64 v[70:71], s[14:15], 0, v[70:71]
	v_lshl_add_u64 v[70:71], s[10:11], 2, v[70:71]
	s_lshl_b32 s0, s35, 2
	v_lshl_add_u64 v[70:71], v[70:71], 0, s[0:1]
	global_store_dword v[70:71], v68, off
	v_add_u32_e32 v97, 0x80, v181
	v_mad_i64_i32 v[68:69], s[2:3], v97, s81, v[168:169]
	global_load_dwordx4 v[98:101], v[68:69], off
	global_load_dwordx4 v[102:105], v[68:69], off offset:256
	v_add_u32_e32 v116, 0x90, v181
	v_mad_i64_i32 v[68:69], s[2:3], v116, s81, v[168:169]
	global_load_dwordx4 v[88:91], v[68:69], off
	global_load_dwordx4 v[84:87], v[68:69], off offset:256
	v_add_u32_e32 v96, 0xa0, v181
	v_mad_i64_i32 v[68:69], s[2:3], v96, s81, v[168:169]
	global_load_dwordx4 v[80:83], v[68:69], off
	global_load_dwordx4 v[76:79], v[68:69], off offset:256
	v_add_u32_e32 v93, 0xb0, v181
	v_mad_i64_i32 v[68:69], s[2:3], v93, s81, v[168:169]
	global_load_dwordx4 v[72:75], v[68:69], off
	s_nop 0
	global_load_dwordx4 v[68:71], v[68:69], off offset:256
	v_readlane_b32 s2, v254, 23
	v_readlane_b32 s3, v254, 24
	v_cmp_lt_i32_e32 vcc, 0, v3
	s_waitcnt vmcnt(7)
	v_lshlrev_b32_e32 v108, 16, v98
	v_and_b32_e32 v109, 0xffff0000, v98
	v_lshlrev_b32_e32 v98, 16, v99
	v_and_b32_e32 v99, 0xffff0000, v99
	v_add_f32_e64 v58, v58, v98
	v_add_f32_e64 v59, v59, v99
	v_lshlrev_b32_e32 v98, 16, v100
	v_and_b32_e32 v99, 0xffff0000, v100
	v_mov_b64_e32 v[94:95], s[2:3]
	v_add_f32_e64 v98, v52, v98
	v_add_f32_e64 v99, v53, v99
	v_lshlrev_b32_e32 v52, 16, v101
	v_and_b32_e32 v53, 0xffff0000, v101
	v_mad_i64_i32 v[106:107], s[2:3], v97, s81, v[94:95]
	v_add_f32_e64 v56, v56, v108
	v_add_f32_e64 v57, v57, v109
	v_add_f32_e64 v100, v54, v52
	v_add_f32_e64 v101, v55, v53
	v_lshl_add_u64 v[106:107], v[106:107], 0, v[166:167]
	v_cvt_pk_bf16_f32 v52, v56, v57
	v_cvt_pk_bf16_f32 v53, v58, v59
	v_cvt_pk_bf16_f32 v54, v98, v99
	v_cvt_pk_bf16_f32 v55, v100, v101
	global_store_dwordx4 v[106:107], v[52:55], off
	v_mul_f32_e64 v108, v56, v56
	v_mul_f32_e64 v109, v57, v57
	v_mul_f32_e64 v110, v58, v58
	v_mul_f32_e64 v111, v59, v59
	s_waitcnt vmcnt(7)
	v_lshlrev_b32_e32 v52, 16, v102
	v_and_b32_e32 v53, 0xffff0000, v102
	v_lshlrev_b32_e32 v54, 16, v103
	v_and_b32_e32 v55, 0xffff0000, v103
	v_add_f32_e64 v52, v64, v52
	v_add_f32_e64 v53, v65, v53
	v_add_f32_e64 v54, v66, v54
	v_add_f32_e64 v55, v67, v55
	v_lshlrev_b32_e32 v56, 16, v104
	v_and_b32_e32 v57, 0xffff0000, v104
	v_lshlrev_b32_e32 v58, 16, v105
	v_and_b32_e32 v59, 0xffff0000, v105
	v_add_f32_e64 v56, v60, v56
	v_add_f32_e64 v57, v61, v57
	v_add_f32_e64 v58, v62, v58
	v_add_f32_e64 v59, v63, v59
	v_mul_f32_e64 v60, v52, v52
	v_mul_f32_e64 v61, v53, v53
	v_mul_f32_e64 v62, v54, v54
	v_mul_f32_e64 v63, v55, v55
	v_mul_f32_e64 v112, v98, v98
	v_mul_f32_e64 v113, v99, v99
	v_mul_f32_e64 v114, v100, v100
	v_mul_f32_e64 v115, v101, v101
	v_add_f32_e32 v62, v62, v63
	v_add_f32_e32 v60, v60, v61
	v_mul_f32_e64 v64, v56, v56
	v_mul_f32_e64 v65, v57, v57
	v_mul_f32_e64 v66, v58, v58
	v_mul_f32_e64 v67, v59, v59
	v_add_f32_e32 v60, v60, v62
	v_add_f32_e32 v61, v114, v115
	v_add_f32_e32 v62, v112, v113
	v_add_f32_e32 v66, v66, v67
	v_add_f32_e32 v64, v64, v65
	v_add_f32_e32 v61, v62, v61
	v_add_f32_e32 v62, v110, v111
	v_add_f32_e32 v63, v108, v109
	v_add_f32_e32 v64, v64, v66
	v_add_f32_e32 v62, v63, v62
	v_add_f32_e32 v60, v60, v64
	v_add_f32_e32 v61, v62, v61
	v_add_f32_e32 v60, v61, v60
	v_cvt_pk_bf16_f32 v52, v52, v53
	v_cvt_pk_bf16_f32 v53, v54, v55
	v_cvt_pk_bf16_f32 v54, v56, v57
	v_cvt_pk_bf16_f32 v55, v58, v59
	global_store_dwordx4 v[106:107], v[52:55], off offset:256
	ds_bpermute_b32 v52, v180, v60
	s_waitcnt vmcnt(7)
	v_lshlrev_b32_e32 v56, 16, v88
	v_and_b32_e32 v57, 0xffff0000, v88
	v_add_f32_e64 v48, v48, v56
	v_add_f32_e64 v49, v49, v57
	v_lshlrev_b32_e32 v56, 16, v89
	v_and_b32_e32 v57, 0xffff0000, v89
	v_add_f32_e64 v50, v50, v56
	v_add_f32_e64 v51, v51, v57
	v_lshlrev_b32_e32 v56, 16, v90
	v_and_b32_e32 v57, 0xffff0000, v90
	v_add_f32_e64 v56, v44, v56
	v_add_f32_e64 v57, v45, v57
	v_lshlrev_b32_e32 v44, 16, v91
	v_and_b32_e32 v45, 0xffff0000, v91
	s_waitcnt lgkmcnt(0)
	v_add_f32_e32 v54, v60, v52
	v_mad_i64_i32 v[52:53], s[2:3], v116, s81, v[94:95]
	v_add_f32_e64 v58, v46, v44
	v_add_f32_e64 v59, v47, v45
	v_lshl_add_u64 v[52:53], v[52:53], 0, v[166:167]
	v_cvt_pk_bf16_f32 v44, v48, v49
	v_cvt_pk_bf16_f32 v45, v50, v51
	v_cvt_pk_bf16_f32 v46, v56, v57
	v_cvt_pk_bf16_f32 v47, v58, v59
	global_store_dwordx4 v[52:53], v[44:47], off
	v_mul_f32_e64 v64, v56, v56
	v_mul_f32_e64 v65, v57, v57
	v_mul_f32_e64 v66, v58, v58
	v_mul_f32_e64 v67, v59, v59
	s_waitcnt vmcnt(7)
	v_lshlrev_b32_e32 v44, 16, v84
	v_and_b32_e32 v45, 0xffff0000, v84
	v_add_f32_e64 v40, v40, v44
	v_add_f32_e64 v41, v41, v45
	v_lshlrev_b32_e32 v44, 16, v85
	v_and_b32_e32 v45, 0xffff0000, v85
	v_add_f32_e64 v42, v42, v44
	v_add_f32_e64 v43, v43, v45
	v_lshlrev_b32_e32 v44, 16, v86
	v_and_b32_e32 v45, 0xffff0000, v86
	v_add_f32_e64 v44, v36, v44
	v_add_f32_e64 v45, v37, v45
	v_lshlrev_b32_e32 v36, 16, v87
	v_and_b32_e32 v37, 0xffff0000, v87
	v_add_f32_e64 v46, v38, v36
	v_add_f32_e64 v47, v39, v37
	v_mul_f32_e64 v36, v40, v40
	v_mul_f32_e64 v37, v41, v41
	v_mul_f32_e64 v38, v42, v42
	v_mul_f32_e64 v39, v43, v43
	v_add_f32_e32 v36, v36, v37
	v_add_f32_e32 v38, v38, v39
	v_mul_f32_e64 v60, v48, v48
	v_mul_f32_e64 v61, v49, v49
	v_mul_f32_e64 v62, v50, v50
	v_mul_f32_e64 v63, v51, v51
	v_mul_f32_e64 v48, v44, v44
	v_mul_f32_e64 v49, v45, v45
	v_mul_f32_e64 v50, v46, v46
	v_mul_f32_e64 v51, v47, v47
	v_add_f32_e32 v36, v36, v38
	v_add_f32_e32 v37, v66, v67
	v_add_f32_e32 v38, v64, v65
	v_add_f32_e32 v50, v50, v51
	v_add_f32_e32 v48, v48, v49
	v_add_f32_e32 v37, v38, v37
	v_add_f32_e32 v38, v62, v63
	v_add_f32_e32 v39, v60, v61
	v_add_f32_e32 v48, v48, v50
	v_add_f32_e32 v38, v39, v38
	v_add_f32_e32 v36, v36, v48
	v_add_f32_e32 v37, v38, v37
	v_add_f32_e32 v48, v37, v36
	v_cvt_pk_bf16_f32 v36, v40, v41
	s_waitcnt vmcnt(6)
; __device__ __forceinline__ unsigned cvt_pk_bf16(float lo, float hi) { f32x2_c v = {lo, hi}; bf16x2_c b = __builtin_convertvector(v, bf16x2_c); return __builtin_bit_cast(unsigned, b); }
; __device__ __forceinline__ float bf_lo(unsigned u) { return __uint_as_float(u << 16); }
; __device__ __forceinline__ float bf_hi(unsigned u) { return __uint_as_float(u & 0xffff0000u); }
;     __device__ __forceinline__ void operator()(const f32x4 (&acc)[2][2][4][2], const Unit& u, int wr, int wc, int fr, int fq) const {
;     ...
;             for (int m = 0; m < 4; ++m) { const int row = row0 + ai * HALF + m * 16; bf16_t* hp = Hx + (size_t)row * LDT + col0;
;                 float ss = 0.f;
; #pragma unroll
;                 for (int bj = 0; bj < 2; ++bj) { const u32x4 x = xv[m][bj]; const f32x4 a0 = acc[ai][bj][m][0], a1 = acc[ai][bj][m][1];
;                     const float y0 = bf_lo(x.x) + a0[0] * scale, y1 = bf_hi(x.x) + a0[1] * scale, y2 = bf_lo(x.y) + a0[2] * scale, y3 = bf_hi(x.y) + a0[3] * scale;
;                     const float y4 = bf_lo(x.z) + a1[0] * scale, y5 = bf_hi(x.z) + a1[1] * scale, y6 = bf_lo(x.w) + a1[2] * scale, y7 = bf_hi(x.w) + a1[3] * scale;
;                     ss += ((y0 * y0 + y1 * y1) + (y2 * y2 + y3 * y3)) + ((y4 * y4 + y5 * y5) + (y6 * y6 + y7 * y7));
;                     u32x4 w; w.x = cvt_pk_bf16(y0, y1); w.y = cvt_pk_bf16(y2, y3); w.z = cvt_pk_bf16(y4, y5); w.w = cvt_pk_bf16(y6, y7);
;                     *(u32x4*)(hp + bj * HALF) = w; }
;                 ss += __shfl_xor(ss, 16); ss += __shfl_xor(ss, 32); ssm[m] = ss; }
;             { const float sv = (fq == 0) ? ssm[0] : (fq == 1) ? ssm[1] : (fq == 2) ? ssm[2] : ssm[3];
	v_lshlrev_b32_e32 v40, 16, v80
	v_and_b32_e32 v41, 0xffff0000, v80
	v_add_f32_e64 v32, v32, v40
	v_add_f32_e64 v33, v33, v41
	v_lshlrev_b32_e32 v40, 16, v81
	v_and_b32_e32 v41, 0xffff0000, v81
	v_add_f32_e64 v34, v34, v40
	v_add_f32_e64 v35, v35, v41
	v_lshlrev_b32_e32 v40, 16, v82
	v_and_b32_e32 v41, 0xffff0000, v82
	v_cvt_pk_bf16_f32 v37, v42, v43
	v_cvt_pk_bf16_f32 v38, v44, v45
	v_cvt_pk_bf16_f32 v39, v46, v47
	v_add_f32_e64 v40, v28, v40
	v_add_f32_e64 v41, v29, v41
	v_lshlrev_b32_e32 v28, 16, v83
	v_and_b32_e32 v29, 0xffff0000, v83
	global_store_dwordx4 v[52:53], v[36:39], off offset:256
	v_add_f32_e64 v42, v30, v28
	v_add_f32_e64 v43, v31, v29
	v_cvt_pk_bf16_f32 v28, v32, v33
	v_mad_i64_i32 v[38:39], s[2:3], v96, s81, v[94:95]
	v_lshl_add_u64 v[38:39], v[38:39], 0, v[166:167]
	v_cvt_pk_bf16_f32 v29, v34, v35
	v_cvt_pk_bf16_f32 v30, v40, v41
	v_cvt_pk_bf16_f32 v31, v42, v43
	ds_bpermute_b32 v36, v180, v48
	global_store_dwordx4 v[38:39], v[28:31], off
	v_mul_f32_e64 v50, v42, v42
	v_mul_f32_e64 v51, v43, v43
	v_mul_f32_e64 v44, v32, v32
	v_mul_f32_e64 v45, v33, v33
	s_waitcnt vmcnt(7)
	v_lshlrev_b32_e32 v28, 16, v76
	v_and_b32_e32 v29, 0xffff0000, v76
	v_add_f32_e64 v24, v24, v28
	v_add_f32_e64 v25, v25, v29
	v_lshlrev_b32_e32 v28, 16, v77
	v_and_b32_e32 v29, 0xffff0000, v77
	v_add_f32_e64 v26, v26, v28
	v_add_f32_e64 v27, v27, v29
	v_lshlrev_b32_e32 v28, 16, v78
	v_and_b32_e32 v29, 0xffff0000, v78
	v_add_f32_e64 v28, v20, v28
	v_add_f32_e64 v29, v21, v29
	v_lshlrev_b32_e32 v20, 16, v79
	v_and_b32_e32 v21, 0xffff0000, v79
	v_add_f32_e64 v30, v22, v20
	v_add_f32_e64 v31, v23, v21
	v_mul_f32_e64 v20, v24, v24
	v_mul_f32_e64 v21, v25, v25
	v_mul_f32_e64 v22, v26, v26
	v_mul_f32_e64 v23, v27, v27
	s_waitcnt lgkmcnt(0)
	v_add_f32_e32 v36, v48, v36
	v_mul_f32_e64 v48, v40, v40
	v_mul_f32_e64 v49, v41, v41
	v_add_f32_e32 v22, v22, v23
	v_add_f32_e32 v20, v20, v21
	v_mul_f32_e64 v46, v34, v34
	v_mul_f32_e64 v47, v35, v35
	v_mul_f32_e64 v32, v28, v28
	v_mul_f32_e64 v33, v29, v29
	v_mul_f32_e64 v34, v30, v30
	v_mul_f32_e64 v35, v31, v31
	v_add_f32_e32 v20, v20, v22
	v_add_f32_e32 v21, v50, v51
	v_add_f32_e32 v22, v48, v49
	v_add_f32_e32 v34, v34, v35
	v_add_f32_e32 v32, v32, v33
	v_add_f32_e32 v21, v22, v21
	v_add_f32_e32 v22, v46, v47
	v_add_f32_e32 v23, v44, v45
	v_add_f32_e32 v32, v32, v34
	v_add_f32_e32 v22, v23, v22
	v_add_f32_e32 v20, v20, v32
	v_add_f32_e32 v21, v22, v21
	v_add_f32_e32 v32, v21, v20
	v_cvt_pk_bf16_f32 v20, v24, v25
	s_waitcnt vmcnt(6)
	v_lshlrev_b32_e32 v24, 16, v72
	v_and_b32_e32 v25, 0xffff0000, v72
	v_add_f32_e64 v16, v16, v24
	v_add_f32_e64 v17, v17, v25
	v_lshlrev_b32_e32 v24, 16, v73
	v_and_b32_e32 v25, 0xffff0000, v73
	v_add_f32_e64 v18, v18, v24
	v_add_f32_e64 v19, v19, v25
	v_lshlrev_b32_e32 v24, 16, v74
	v_and_b32_e32 v25, 0xffff0000, v74
	v_cvt_pk_bf16_f32 v21, v26, v27
	v_cvt_pk_bf16_f32 v22, v28, v29
	v_cvt_pk_bf16_f32 v23, v30, v31
	v_add_f32_e64 v24, v12, v24
	v_add_f32_e64 v25, v13, v25
	v_lshlrev_b32_e32 v12, 16, v75
	v_and_b32_e32 v13, 0xffff0000, v75
	global_store_dwordx4 v[38:39], v[20:23], off offset:256
	v_add_f32_e64 v26, v14, v12
	v_add_f32_e64 v27, v15, v13
	v_cvt_pk_bf16_f32 v12, v16, v17
	v_mad_i64_i32 v[22:23], s[2:3], v93, s81, v[94:95]
	v_lshl_add_u64 v[22:23], v[22:23], 0, v[166:167]
	v_cvt_pk_bf16_f32 v13, v18, v19
	v_cvt_pk_bf16_f32 v14, v24, v25
	v_cvt_pk_bf16_f32 v15, v26, v27
	ds_bpermute_b32 v20, v180, v32
	global_store_dwordx4 v[22:23], v[12:15], off
	v_mul_f32_e64 v34, v26, v26
	v_mul_f32_e64 v35, v27, v27
	v_mul_f32_e64 v28, v16, v16
	v_mul_f32_e64 v29, v17, v17
	s_waitcnt vmcnt(7)
	v_lshlrev_b32_e32 v12, 16, v68
	v_and_b32_e32 v13, 0xffff0000, v68
	v_add_f32_e64 v8, v8, v12
	v_add_f32_e64 v9, v9, v13
	v_lshlrev_b32_e32 v12, 16, v69
	v_and_b32_e32 v13, 0xffff0000, v69
	v_add_f32_e64 v10, v10, v12
	v_add_f32_e64 v11, v11, v13
	v_lshlrev_b32_e32 v12, 16, v70
	v_and_b32_e32 v13, 0xffff0000, v70
	v_add_f32_e64 v12, v4, v12
	v_add_f32_e64 v13, v5, v13
	v_lshlrev_b32_e32 v4, 16, v71
	v_and_b32_e32 v5, 0xffff0000, v71
	v_add_f32_e64 v14, v6, v4
	v_add_f32_e64 v15, v7, v5
	v_mul_f32_e64 v4, v8, v8
	v_mul_f32_e64 v5, v9, v9
	v_mul_f32_e64 v6, v10, v10
	v_mul_f32_e64 v7, v11, v11
	s_waitcnt lgkmcnt(0)
	v_add_f32_e32 v20, v32, v20
	v_mul_f32_e64 v32, v24, v24
	v_mul_f32_e64 v33, v25, v25
	v_add_f32_e32 v6, v6, v7
	v_add_f32_e32 v4, v4, v5
	v_mul_f32_e64 v30, v18, v18
	v_mul_f32_e64 v31, v19, v19
	v_mul_f32_e64 v16, v12, v12
	v_mul_f32_e64 v17, v13, v13
	v_mul_f32_e64 v18, v14, v14
	v_mul_f32_e64 v19, v15, v15
	v_add_f32_e32 v4, v4, v6
	v_add_f32_e32 v5, v34, v35
	v_add_f32_e32 v6, v32, v33
	v_add_f32_e32 v18, v18, v19
	v_add_f32_e32 v16, v16, v17
	v_add_f32_e32 v5, v6, v5
	v_add_f32_e32 v6, v30, v31
	v_add_f32_e32 v7, v28, v29
	v_add_f32_e32 v16, v16, v18
	v_add_f32_e32 v6, v7, v6
	v_add_f32_e32 v4, v4, v16
	v_add_f32_e32 v5, v6, v5
	v_add_f32_e32 v16, v5, v4
	v_cvt_pk_bf16_f32 v4, v8, v9
	v_cvt_pk_bf16_f32 v5, v10, v11
	v_cvt_pk_bf16_f32 v6, v12, v13
	v_cvt_pk_bf16_f32 v7, v14, v15
	global_store_dwordx4 v[22:23], v[4:7], off offset:256
	ds_bpermute_b32 v4, v180, v16
	ds_bpermute_b32 v55, v179, v54
	ds_bpermute_b32 v37, v179, v36
	ds_bpermute_b32 v21, v179, v20
	s_waitcnt lgkmcnt(3)
	v_add_f32_e32 v5, v16, v4
	ds_bpermute_b32 v6, v179, v5
	s_and_saveexec_b64 s[2:3], vcc
	s_xor_b64 s[4:5], exec, s[2:3]
	s_cbranch_execz .LBB0_717
	v_cmp_ne_u32_e32 vcc, 1, v3
	s_and_saveexec_b64 s[2:3], vcc
	s_xor_b64 s[24:25], exec, s[2:3]
	s_cbranch_execz .LBB0_714
	s_waitcnt lgkmcnt(0)
	v_add_f32_e32 v4, v5, v6
	v_add_f32_e32 v5, v20, v21
	v_cndmask_b32_e64 v4, v4, v5, s[6:7]
